# every packed f32 op (v_pk_fma/mul/add_f32) split into two scalar f32 ops, bit-identical math; on top of QK double-buffer, merge-loop fix, unscaled fp8 MFMA
# baseline (speedup 1.0000x reference)
; __device__ __forceinline__ void tjob_store(const TJob& J, int wave, int lane, const f32x4 (&R)[8]) {
;     ...
;     f32x4 s0 = (f32x4){1.f, 1.f, 1.f, 1.f}, s1 = s0;
;     if (J.scale) { s0 = *(const f32x4*)(J.scale + k); s1 = *(const f32x4*)(J.scale + k + 4); }
;     if (J.f8) {
;         s0 *= W8_SCALE; s1 *= W8_SCALE;
; #pragma unroll
;         for (int c = 0; c < 4; ++c)
;             __builtin_nontemporal_store(pack_fp8x8(R[0][c] * s0[0], R[1][c] * s0[1], R[2][c] * s0[2], R[3][c] * s0[3], R[4][c] * s1[0], R[5][c] * s1[1], R[6][c] * s1[2], R[7][c] * s1[3]),
;                                         (u32x2*)((unsigned char*)J.dst + (size_t)(n + c) * J.K + k));
;         return;
.LBB0_280:
	v_add_u32_e32 v119, s53, v108
	v_cmp_ne_u32_e32 vcc, 0, v110
	v_add_u32_e32 v118, 1, v119
	v_add_u32_e32 v117, 2, v119
	v_add_u32_e32 v33, 3, v119
	s_cbranch_vccz .LBB0_299
	s_waitcnt vmcnt(1)
	v_mul_f32_e64 v122, v100, s16
	v_mul_f32_e64 v123, v101, s16
	s_waitcnt vmcnt(0)
	v_mul_f32_e64 v126, v104, s16
	v_mul_f32_e64 v127, v105, s16
	v_mul_f32_e32 v129, v0, v122
	v_mul_f32_e32 v130, v4, v123
	v_mov_b32_e32 v128, v32
	v_mul_f32_e32 v133, v16, v126
	v_mul_f32_e32 v134, v20, v127
	v_cvt_pk_fp8_f32 v128, v129, v130
	v_mov_b32_e32 v129, v32
	v_cvt_pk_fp8_f32 v129, v133, v134
	v_mul_f32_e64 v120, v102, s16
	v_mul_f32_e64 v121, v103, s16
	v_mul_f32_e64 v124, v106, s16
	v_mul_f32_e64 v125, v107, s16
	v_mul_f32_e32 v131, v8, v120
	v_mul_f32_e32 v132, v12, v121
	v_mul_f32_e32 v130, v24, v124
	v_mul_f32_e32 v133, v28, v125
	v_cvt_pk_fp8_f32 v128, v131, v132 op_sel:[0,0,1]
	v_cvt_pk_fp8_f32 v129, v130, v133 op_sel:[0,0,1]
	v_mov_b64_e32 v[130:131], s[10:11]
	v_mad_i64_i32 v[132:133], s[34:35], s55, v119, v[130:131]
	v_lshl_add_u64 v[132:133], v[132:133], 0, v[34:35]
	global_store_dwordx2 v[132:133], v[128:129], off nt
	v_mul_f32_e32 v129, v1, v122
	v_mul_f32_e32 v132, v5, v123
	v_mov_b32_e32 v128, v32
	v_mul_f32_e32 v135, v17, v126
	v_mul_f32_e32 v136, v21, v127
	v_cvt_pk_fp8_f32 v128, v129, v132
	v_mov_b32_e32 v129, v32
	v_cvt_pk_fp8_f32 v129, v135, v136
	v_mul_f32_e32 v133, v9, v120
	v_mul_f32_e32 v134, v13, v121
	v_mul_f32_e32 v132, v25, v124
	v_mul_f32_e32 v135, v29, v125
	v_cvt_pk_fp8_f32 v128, v133, v134 op_sel:[0,0,1]
	v_cvt_pk_fp8_f32 v129, v132, v135 op_sel:[0,0,1]
	v_mad_i64_i32 v[132:133], s[34:35], v118, s55, v[130:131]
	v_lshl_add_u64 v[132:133], v[132:133], 0, v[34:35]
	global_store_dwordx2 v[132:133], v[128:129], off nt
	v_mul_f32_e32 v129, v2, v122
	v_mul_f32_e32 v132, v6, v123
	v_mov_b32_e32 v128, v32
	v_mul_f32_e32 v135, v18, v126
	v_mul_f32_e32 v136, v22, v127
	v_cvt_pk_fp8_f32 v128, v129, v132
	v_mov_b32_e32 v129, v32
	v_cvt_pk_fp8_f32 v129, v135, v136
	v_mul_f32_e32 v133, v10, v120
	v_mul_f32_e32 v134, v14, v121
	v_mul_f32_e32 v132, v26, v124
	v_mul_f32_e32 v135, v30, v125
	v_cvt_pk_fp8_f32 v128, v133, v134 op_sel:[0,0,1]
	v_cvt_pk_fp8_f32 v129, v132, v135 op_sel:[0,0,1]
	v_mad_i64_i32 v[132:133], s[34:35], v117, s55, v[130:131]
	v_lshl_add_u64 v[132:133], v[132:133], 0, v[34:35]
	global_store_dwordx2 v[132:133], v[128:129], off nt
	v_mul_f32_e32 v122, v3, v122
	v_mul_f32_e32 v123, v7, v123
	v_mul_f32_e32 v128, v11, v120
	v_mul_f32_e32 v129, v15, v121
	v_mul_f32_e32 v126, v19, v126
	v_mul_f32_e32 v127, v23, v127
	v_mov_b32_e32 v120, v32
	v_mov_b32_e32 v121, v32
	v_cvt_pk_fp8_f32 v120, v122, v123
	v_cvt_pk_fp8_f32 v121, v126, v127
	v_mul_f32_e32 v122, v27, v124
	v_mul_f32_e32 v123, v31, v125
	v_cvt_pk_fp8_f32 v120, v128, v129 op_sel:[0,0,1]
	v_cvt_pk_fp8_f32 v121, v122, v123 op_sel:[0,0,1]
	v_mad_i64_i32 v[122:123], s[34:35], v33, s55, v[130:131]
	v_lshl_add_u64 v[122:123], v[122:123], 0, v[34:35]
	global_store_dwordx2 v[122:123], v[120:121], off nt
	s_cbranch_execnz .LBB0_283

; __device__ __forceinline__ void tjob_store(const TJob& J, int wave, int lane, const f32x4 (&R)[8]) {
;     ...
;     f32x4 s0 = (f32x4){1.f, 1.f, 1.f, 1.f}, s1 = s0;
;     if (J.scale) { s0 = *(const f32x4*)(J.scale + k); s1 = *(const f32x4*)(J.scale + k + 4); }
;     if (J.f8) {
;         s0 *= W8_SCALE; s1 *= W8_SCALE;
; #pragma unroll
;         for (int c = 0; c < 4; ++c)
;             __builtin_nontemporal_store(pack_fp8x8(R[0][c] * s0[0], R[1][c] * s0[1], R[2][c] * s0[2], R[3][c] * s0[3], R[4][c] * s1[0], R[5][c] * s1[1], R[6][c] * s1[2], R[7][c] * s1[3]),
;                                         (u32x2*)((unsigned char*)J.dst + (size_t)(n + c) * J.K + k));
;         return;
.LBB0_384:
	v_add_u32_e32 v119, s56, v108
	v_cmp_eq_u32_e32 vcc, 0, v111
	v_add_u32_e32 v118, 1, v119
	v_add_u32_e32 v117, 2, v119
	v_add_u32_e32 v33, 3, v119
	s_cbranch_vccnz .LBB0_388
	s_waitcnt vmcnt(1)
	v_mul_f32_e64 v122, v100, s16
	v_mul_f32_e64 v123, v101, s16
	s_waitcnt vmcnt(0)
	v_mul_f32_e64 v126, v104, s16
	v_mul_f32_e64 v127, v105, s16
	v_mul_f32_e32 v129, v36, v122
	v_mul_f32_e32 v130, v40, v123
	v_mov_b32_e32 v128, v32
	v_mul_f32_e32 v133, v52, v126
	v_mul_f32_e32 v134, v56, v127
	v_cvt_pk_fp8_f32 v128, v129, v130
	v_mov_b32_e32 v129, v32
	v_cvt_pk_fp8_f32 v129, v133, v134
	v_mul_f32_e64 v120, v102, s16
	v_mul_f32_e64 v121, v103, s16
	v_mul_f32_e64 v124, v106, s16
	v_mul_f32_e64 v125, v107, s16
	v_mul_f32_e32 v131, v44, v120
	v_mul_f32_e32 v132, v48, v121
	v_mul_f32_e32 v130, v60, v124
	v_mul_f32_e32 v133, v64, v125
	v_cvt_pk_fp8_f32 v128, v131, v132 op_sel:[0,0,1]
	v_cvt_pk_fp8_f32 v129, v130, v133 op_sel:[0,0,1]
	v_mov_b64_e32 v[130:131], s[14:15]
	v_mad_i64_i32 v[132:133], s[34:35], s58, v119, v[130:131]
	v_lshl_add_u64 v[132:133], v[132:133], 0, v[34:35]
	global_store_dwordx2 v[132:133], v[128:129], off nt
	v_mul_f32_e32 v129, v37, v122
	v_mul_f32_e32 v132, v41, v123
	v_mov_b32_e32 v128, v32
	v_mul_f32_e32 v135, v53, v126
	v_mul_f32_e32 v136, v57, v127
	v_cvt_pk_fp8_f32 v128, v129, v132
	v_mov_b32_e32 v129, v32
	v_cvt_pk_fp8_f32 v129, v135, v136
	v_mul_f32_e32 v133, v45, v120
	v_mul_f32_e32 v134, v49, v121
	v_mul_f32_e32 v132, v61, v124
	v_mul_f32_e32 v135, v65, v125
	v_cvt_pk_fp8_f32 v128, v133, v134 op_sel:[0,0,1]
	v_cvt_pk_fp8_f32 v129, v132, v135 op_sel:[0,0,1]
	v_mad_i64_i32 v[132:133], s[34:35], v118, s58, v[130:131]
	v_lshl_add_u64 v[132:133], v[132:133], 0, v[34:35]
	global_store_dwordx2 v[132:133], v[128:129], off nt
	v_mul_f32_e32 v129, v38, v122
	v_mul_f32_e32 v132, v42, v123
	v_mov_b32_e32 v128, v32
	v_mul_f32_e32 v135, v54, v126
	v_mul_f32_e32 v136, v58, v127
	v_cvt_pk_fp8_f32 v128, v129, v132
	v_mov_b32_e32 v129, v32
	v_cvt_pk_fp8_f32 v129, v135, v136
	v_mul_f32_e32 v133, v46, v120
	v_mul_f32_e32 v134, v50, v121
	v_mul_f32_e32 v132, v62, v124
	v_mul_f32_e32 v135, v66, v125
	v_cvt_pk_fp8_f32 v128, v133, v134 op_sel:[0,0,1]
	v_cvt_pk_fp8_f32 v129, v132, v135 op_sel:[0,0,1]
	v_mad_i64_i32 v[132:133], s[34:35], v117, s58, v[130:131]
	v_lshl_add_u64 v[132:133], v[132:133], 0, v[34:35]
	global_store_dwordx2 v[132:133], v[128:129], off nt
	v_mul_f32_e32 v122, v39, v122
	v_mul_f32_e32 v123, v43, v123
	v_mul_f32_e32 v128, v47, v120
	v_mul_f32_e32 v129, v51, v121
	v_mul_f32_e32 v126, v55, v126
	v_mul_f32_e32 v127, v59, v127
	v_mov_b32_e32 v120, v32
	v_mov_b32_e32 v121, v32
	v_cvt_pk_fp8_f32 v120, v122, v123
	v_cvt_pk_fp8_f32 v121, v126, v127
	v_mul_f32_e32 v122, v63, v124
	v_mul_f32_e32 v123, v67, v125
	v_cvt_pk_fp8_f32 v120, v128, v129 op_sel:[0,0,1]
	v_cvt_pk_fp8_f32 v121, v122, v123 op_sel:[0,0,1]
	v_mad_i64_i32 v[122:123], s[34:35], v33, s58, v[130:131]
	v_lshl_add_u64 v[122:123], v[122:123], 0, v[34:35]
	global_store_dwordx2 v[122:123], v[120:121], off nt
	s_cbranch_execnz .LBB0_387

; __device__ __forceinline__ void tjob_store(const TJob& J, int wave, int lane, const f32x4 (&R)[8]) {
;     ...
;     f32x4 s0 = (f32x4){1.f, 1.f, 1.f, 1.f}, s1 = s0;
;     if (J.scale) { s0 = *(const f32x4*)(J.scale + k); s1 = *(const f32x4*)(J.scale + k + 4); }
;     if (J.f8) {
;         s0 *= W8_SCALE; s1 *= W8_SCALE;
; #pragma unroll
;         for (int c = 0; c < 4; ++c)
;             __builtin_nontemporal_store(pack_fp8x8(R[0][c] * s0[0], R[1][c] * s0[1], R[2][c] * s0[2], R[3][c] * s0[3], R[4][c] * s1[0], R[5][c] * s1[1], R[6][c] * s1[2], R[7][c] * s1[3]),
;                                         (u32x2*)((unsigned char*)J.dst + (size_t)(n + c) * J.K + k));
;         return;
.LBB0_468:
	v_add_u32_e32 v119, s65, v108
	v_cmp_eq_u32_e32 vcc, 0, v116
	v_add_u32_e32 v118, 1, v119
	v_add_u32_e32 v117, 2, v119
	v_add_u32_e32 v33, 3, v119
	s_cbranch_vccnz .LBB0_470
	s_waitcnt vmcnt(1)
	v_mul_f32_e64 v122, v100, s16
	v_mul_f32_e64 v123, v101, s16
	s_waitcnt vmcnt(0)
	v_mul_f32_e64 v126, v104, s16
	v_mul_f32_e64 v127, v105, s16
	v_mul_f32_e32 v129, v72, v122
	v_mul_f32_e32 v130, v76, v123
	v_mov_b32_e32 v128, v32
	v_mul_f32_e32 v133, v84, v126
	v_mul_f32_e32 v134, v88, v127
	v_cvt_pk_fp8_f32 v128, v129, v130
	v_mov_b32_e32 v129, v32
	v_cvt_pk_fp8_f32 v129, v133, v134
	v_mul_f32_e64 v120, v102, s16
	v_mul_f32_e64 v121, v103, s16
	v_mul_f32_e64 v124, v106, s16
	v_mul_f32_e64 v125, v107, s16
	v_mul_f32_e32 v131, v68, v120
	v_mul_f32_e32 v132, v80, v121
	v_mul_f32_e32 v130, v96, v124
	v_mul_f32_e32 v133, v92, v125
	v_cvt_pk_fp8_f32 v128, v131, v132 op_sel:[0,0,1]
	v_cvt_pk_fp8_f32 v129, v130, v133 op_sel:[0,0,1]
	v_mov_b64_e32 v[130:131], s[30:31]
	v_mad_i64_i32 v[132:133], s[34:35], s67, v119, v[130:131]
	v_lshl_add_u64 v[132:133], v[132:133], 0, v[34:35]
	global_store_dwordx2 v[132:133], v[128:129], off nt
	v_mul_f32_e32 v129, v73, v122
	v_mul_f32_e32 v132, v77, v123
	v_mov_b32_e32 v128, v32
	v_mul_f32_e32 v135, v85, v126
	v_mul_f32_e32 v136, v89, v127
	v_cvt_pk_fp8_f32 v128, v129, v132
	v_mov_b32_e32 v129, v32
	v_cvt_pk_fp8_f32 v129, v135, v136
	v_mul_f32_e32 v133, v69, v120
	v_mul_f32_e32 v134, v81, v121
	v_mul_f32_e32 v132, v97, v124
	v_mul_f32_e32 v135, v93, v125
	v_cvt_pk_fp8_f32 v128, v133, v134 op_sel:[0,0,1]
	v_cvt_pk_fp8_f32 v129, v132, v135 op_sel:[0,0,1]
	v_mad_i64_i32 v[132:133], s[34:35], v118, s67, v[130:131]
	v_lshl_add_u64 v[132:133], v[132:133], 0, v[34:35]
	global_store_dwordx2 v[132:133], v[128:129], off nt
	v_mul_f32_e32 v129, v74, v122
	v_mul_f32_e32 v132, v78, v123
	v_mov_b32_e32 v128, v32
	v_mul_f32_e32 v135, v86, v126
	v_mul_f32_e32 v136, v90, v127
	v_cvt_pk_fp8_f32 v128, v129, v132
	v_mov_b32_e32 v129, v32
	v_cvt_pk_fp8_f32 v129, v135, v136
	v_mul_f32_e32 v133, v70, v120
	v_mul_f32_e32 v134, v82, v121
	v_mul_f32_e32 v132, v98, v124
	v_mul_f32_e32 v135, v94, v125
	v_cvt_pk_fp8_f32 v128, v133, v134 op_sel:[0,0,1]
	v_cvt_pk_fp8_f32 v129, v132, v135 op_sel:[0,0,1]
	v_mad_i64_i32 v[132:133], s[34:35], v117, s67, v[130:131]
	v_lshl_add_u64 v[132:133], v[132:133], 0, v[34:35]
	global_store_dwordx2 v[132:133], v[128:129], off nt
	v_mul_f32_e32 v122, v75, v122
	v_mul_f32_e32 v123, v79, v123
	v_mul_f32_e32 v128, v71, v120
	v_mul_f32_e32 v129, v83, v121
	v_mul_f32_e32 v126, v87, v126
	v_mul_f32_e32 v127, v91, v127
	v_mov_b32_e32 v120, v32
	v_mov_b32_e32 v121, v32
	v_cvt_pk_fp8_f32 v120, v122, v123
	v_cvt_pk_fp8_f32 v121, v126, v127
	v_mul_f32_e32 v122, v99, v124
	v_mul_f32_e32 v123, v95, v125
	v_cvt_pk_fp8_f32 v120, v128, v129 op_sel:[0,0,1]
	v_cvt_pk_fp8_f32 v121, v122, v123 op_sel:[0,0,1]
	v_mad_i64_i32 v[122:123], s[34:35], v33, s67, v[130:131]
	v_lshl_add_u64 v[122:123], v[122:123], 0, v[34:35]
	s_mov_b64 s[34:35], 0
	global_store_dwordx2 v[122:123], v[120:121], off nt

; __device__ __forceinline__ f32x4 sigmoid4(const f32x4& x, float s) {
;     f32x4 z = x * (s * -1.4426950408889634f), e;
; #pragma unroll
;     for (int j = 0; j < 4; ++j) e[j] = __builtin_amdgcn_exp2f(z[j]);
;     e = e + 1.0f;
; #pragma unroll
;     for (int j = 0; j < 4; ++j) e[j] = __builtin_amdgcn_rcpf(e[j]);
;     return e;
; }
;     __device__ __forceinline__ void operator()(const f32x4 (&acc)[2][2][4][2], const Unit& u, int wr, int wc, int fr, int fq, const Pre&) const {
;     ...
;                 } else if (kind == KD_G) {
; #pragma unroll
;                     for (int bj = 0; bj < 2; ++bj)
;                         st_bf16x8(gabuf + (size_t)row * DM + 256 * (pn - TL_G) + 128 * bj + cw, sigmoid4(acc[ai][bj][m][0], rs), sigmoid4(acc[ai][bj][m][1], rs));
.LBB0_596:
	s_cmp_eq_u32 s55, 3
	s_cselect_b64 s[80:81], -1, 0
	s_lshl_b32 s8, s4, 8
	s_lshl_b32 s76, s4, 7
	s_add_i32 s90, s8, 0xffffe000
	s_add_i32 s84, s76, 0xfffff800
	v_lshlrev_b32_e32 v38, 3, v33
	v_readlane_b32 s2, v249, 59
	s_ashr_i32 s91, s90, 31
	s_ashr_i32 s85, s84, 31
	v_add_u32_e32 v36, s2, v38
	s_cmp_lg_u32 s55, 5
	s_waitcnt vmcnt(0)
	v_mul_f32_e32 v52, 0x3c800000, v32
	v_cmp_gt_i32_e64 s[2:3], 2, v33
	v_ashrrev_i32_e32 v37, 31, v36
	s_cselect_b64 s[82:83], -1, 0
	s_mov_b64 s[86:87], -1
	s_mov_b64 s[4:5], 0
	s_cmp_lt_i32 s55, 1
	s_mov_b64 s[92:93], 0
	s_cbranch_scc1 .LBB0_604
	s_cmp_gt_i32 s55, 1
	s_cbranch_scc0 .LBB0_601
	s_cmp_eq_u32 s55, 2
	s_mov_b64 s[92:93], -1
	s_cbranch_scc0 .LBB0_600
	v_readlane_b32 s86, v249, 46
	v_lshlrev_b64 v[32:33], 12, v[40:41]
	v_readlane_b32 s87, v249, 47
	v_mul_f32_e32 v39, 0xbfb8aa3b, v52
	v_mul_f32_e32 v34, v190, v39
	v_lshl_add_u64 v[32:33], s[86:87], 0, v[32:33]
	v_lshl_add_u64 v[32:33], s[90:91], 1, v[32:33]
	v_mul_f32_e32 v35, v191, v39
	v_lshl_add_u64 v[54:55], v[36:37], 1, v[32:33]
	v_mul_f32_e32 v32, v188, v39
	v_mul_f32_e32 v33, v189, v39
	v_exp_f32_e32 v34, v34
	v_exp_f32_e32 v35, v35
	v_exp_f32_e32 v32, v32
	v_exp_f32_e32 v33, v33
	s_mov_b64 s[92:93], 0
	v_add_f32_e64 v34, v34, 1.0
	v_add_f32_e64 v35, v35, 1.0
	v_add_f32_e64 v32, v32, 1.0
	v_add_f32_e64 v33, v33, 1.0
	v_rcp_f32_e32 v51, v34
	v_rcp_f32_e32 v53, v35
	v_mul_f32_e32 v34, v182, v39
	v_mul_f32_e32 v35, v183, v39
	v_rcp_f32_e32 v47, v32
	v_rcp_f32_e32 v49, v33
	v_mul_f32_e32 v32, v180, v39
	v_mul_f32_e32 v33, v181, v39
	v_exp_f32_e32 v34, v34
	v_exp_f32_e32 v35, v35
	v_exp_f32_e32 v32, v32
	v_exp_f32_e32 v33, v33
	v_add_f32_e64 v34, v34, 1.0
	v_add_f32_e64 v35, v35, 1.0
	s_nop 0
	v_rcp_f32_e32 v35, v35
	v_add_f32_e64 v32, v32, 1.0
	v_add_f32_e64 v33, v33, 1.0
	v_rcp_f32_e32 v58, v34
	v_rcp_f32_e32 v56, v32
	v_rcp_f32_e32 v57, v33
	v_cvt_pk_bf16_f32 v32, v47, v49
	v_cvt_pk_bf16_f32 v33, v51, v53
	v_cvt_pk_bf16_f32 v34, v56, v57
	v_cvt_pk_bf16_f32 v35, v58, v35
	global_store_dwordx4 v[54:55], v[32:35], off
	s_nop 1
	v_mul_f32_e32 v34, v186, v39
	v_mul_f32_e32 v35, v187, v39
	v_mul_f32_e32 v32, v184, v39
	v_mul_f32_e32 v33, v185, v39
	v_exp_f32_e32 v34, v34
	v_exp_f32_e32 v35, v35
	v_exp_f32_e32 v32, v32
	v_exp_f32_e32 v33, v33
	v_add_f32_e64 v34, v34, 1.0
	v_add_f32_e64 v35, v35, 1.0
	s_nop 0
	v_rcp_f32_e32 v51, v34
	v_add_f32_e64 v32, v32, 1.0
	v_add_f32_e64 v33, v33, 1.0
	v_rcp_f32_e32 v53, v35
	v_mul_f32_e32 v34, v178, v39
	v_mul_f32_e32 v35, v179, v39
	v_rcp_f32_e32 v47, v32
	v_rcp_f32_e32 v49, v33
	v_mul_f32_e32 v32, v176, v39
	v_mul_f32_e32 v33, v177, v39
	v_exp_f32_e32 v34, v34
	v_exp_f32_e32 v35, v35
	v_exp_f32_e32 v32, v32
	v_exp_f32_e32 v33, v33
	v_add_f32_e64 v34, v34, 1.0
	v_add_f32_e64 v35, v35, 1.0
	s_nop 0
	v_rcp_f32_e32 v35, v35
	v_add_f32_e64 v32, v32, 1.0
	v_add_f32_e64 v33, v33, 1.0
	v_rcp_f32_e32 v57, v34
	v_rcp_f32_e32 v39, v32
	v_rcp_f32_e32 v56, v33
	v_cvt_pk_bf16_f32 v32, v47, v49
	v_cvt_pk_bf16_f32 v33, v51, v53
	v_cvt_pk_bf16_f32 v34, v39, v56
	v_cvt_pk_bf16_f32 v35, v57, v35
	global_store_dwordx4 v[54:55], v[32:35], off offset:256

;     __device__ __forceinline__ void operator()(const f32x4 (&acc)[2][2][4][2], const Unit& u, int wr, int wc, int fr, int fq, const Pre&) const {
;     ...
;                 } else if (kind == KD_P) {
;                     const float r2 = rs * rs;
;                     st_bf16x8(pbuf + (size_t)row * DM + 128 * (pn - TL_P) + cw, acc[ai][0][m][0] * acc[ai][1][m][0] * r2, acc[ai][0][m][1] * acc[ai][1][m][1] * r2);
.LBB0_601:
	s_and_b64 vcc, exec, s[86:87]
	s_cbranch_vccz .LBB0_603
	v_readlane_b32 s50, v249, 44
	v_lshlrev_b64 v[34:35], 12, v[40:41]
	v_readlane_b32 s51, v249, 45
	v_mul_f32_e32 v32, v52, v52
	v_mul_f32_e64 v56, v188, v184
	v_mul_f32_e64 v57, v189, v185
	v_lshl_add_u64 v[34:35], s[50:51], 0, v[34:35]
	v_lshl_add_u64 v[34:35], s[84:85], 1, v[34:35]
	v_lshl_add_u64 v[54:55], v[36:37], 1, v[34:35]
	v_mul_f32_e64 v34, v190, v186
	v_mul_f32_e64 v35, v191, v187
	v_mul_f32_e64 v58, v182, v178
	v_mul_f32_e64 v59, v183, v179
	v_mul_f32_e64 v34, v34, v32
	v_mul_f32_e64 v35, v35, v32
	v_mul_f32_e64 v60, v180, v176
	v_mul_f32_e64 v61, v181, v177
	v_mul_f32_e64 v56, v56, v32
	v_mul_f32_e64 v57, v57, v32
	v_mul_f32_e64 v58, v58, v32
	v_mul_f32_e64 v59, v59, v32
	v_mul_f32_e64 v60, v60, v32
	v_mul_f32_e64 v61, v61, v32
	v_cvt_pk_bf16_f32 v32, v56, v57
	v_cvt_pk_bf16_f32 v33, v34, v35
	s_nop 0
	v_cvt_pk_bf16_f32 v34, v60, v61
	v_cvt_pk_bf16_f32 v35, v58, v59
	global_store_dwordx4 v[54:55], v[32:35], off

;     __device__ __forceinline__ void operator()(const f32x4 (&acc)[2][2][4][2], const Unit& u, int wr, int wc, int fr, int fq, const Pre&) const {
;     ...
;                 } else {
;                     const f32x4 x1 = acc[ai][0][m][0] * rs, x2 = acc[ai][0][m][1] * rs;
;                     if (wc < 2) {
;                         if (roti) st_bf16x8(kib + (size_t)row * 64 + cw, x1 * cs[q] - x2 * sn[q], x2 * cs[q] + x1 * sn[q]);
;                         else st_bf16x8(kib + (size_t)row * 64 + cw, x1, x2);
;                     } else if (wc == 2 && fq < 2) {
;                         *(f32x4*)(wib + (size_t)row * 16 + 8 * fq) = x1 * 0.03125f; *(f32x4*)(wib + (size_t)row * 16 + 8 * fq + 4) = x2 * 0.03125f;
;                     }
.LBB0_606:
	s_add_i32 s86, s8, 0xffffce00
	s_add_i32 s57, s8, 0xffffd000
	s_addk_i32 s8, 0xd800
	s_and_b64 s[88:89], s[94:95], s[2:3]
	v_ashrrev_i32_e32 v39, 31, v38
	s_ashr_i32 s87, s86, 31
	s_ashr_i32 s45, s57, 31
	s_andn2_b64 vcc, exec, s[92:93]
	s_ashr_i32 s54, s8, 31
	s_cbranch_vccnz .LBB0_630
	s_mov_b64 s[2:3], -1
	s_and_b64 vcc, exec, s[36:37]
	s_cbranch_vccz .LBB0_619
	s_and_b64 vcc, exec, s[82:83]
	s_cbranch_vccz .LBB0_616
	v_mul_f32_e64 v32, v190, v52
	v_mul_f32_e64 v33, v191, v52
	v_mul_f32_e64 v56, v188, v52
	v_mul_f32_e64 v57, v189, v52
	v_mul_f32_e64 v34, v182, v52
	v_mul_f32_e64 v35, v183, v52
	v_mul_f32_e64 v54, v180, v52
	v_mul_f32_e64 v55, v181, v52
	s_and_b64 vcc, exec, s[34:35]
	s_cbranch_vccz .LBB0_613
	s_and_saveexec_b64 s[2:3], s[88:89]
	s_cbranch_execz .LBB0_612
	v_readlane_b32 s4, v249, 56
	v_lshlrev_b64 v[58:59], 6, v[40:41]
	v_readlane_b32 s5, v249, 57
	v_mul_f32_e64 v240, v32, s38
	v_mul_f32_e64 v241, v33, s38
	v_mul_f32_e64 v238, v56, s38
	v_mul_f32_e64 v239, v57, s38
	v_lshl_add_u64 v[58:59], s[4:5], 0, v[58:59]
	v_lshl_add_u64 v[62:63], v[38:39], 2, v[58:59]
	v_mul_f32_e64 v60, v34, s38
	v_mul_f32_e64 v61, v35, s38
	v_mul_f32_e64 v58, v54, s38
	v_mul_f32_e64 v59, v55, s38
	global_store_dwordx4 v[62:63], v[238:241], off
	global_store_dwordx4 v[62:63], v[58:61], off offset:16

;     __device__ __forceinline__ void operator()(const f32x4 (&acc)[2][2][4][2], const Unit& u, int wr, int wc, int fr, int fq, const Pre&) const {
;     ...
;                 } else if (kind == KD_V) {
; #pragma unroll
;                     for (int bj = 0; bj < 2; ++bj) st_bf16x8(vb + (size_t)row * 512 + 256 * (pn - TL_V) + 128 * bj + cw, acc[ai][bj][m][0] * rs, acc[ai][bj][m][1] * rs);
.LBB0_616:
	s_andn2_b64 vcc, exec, s[2:3]
	s_cbranch_vccnz .LBB0_618
	v_readlane_b32 s2, v249, 52
	v_lshlrev_b64 v[32:33], 10, v[40:41]
	v_readlane_b32 s3, v249, 53
	v_mul_f32_e64 v34, v190, v52
	v_mul_f32_e64 v35, v191, v52
	v_mul_f32_e64 v56, v182, v52
	v_mul_f32_e64 v57, v183, v52
	v_lshl_add_u64 v[32:33], s[2:3], 0, v[32:33]
	v_lshl_add_u64 v[32:33], s[86:87], 1, v[32:33]
	v_lshl_add_u64 v[54:55], v[36:37], 1, v[32:33]
	v_mul_f32_e64 v32, v188, v52
	v_mul_f32_e64 v33, v189, v52
	v_mul_f32_e64 v58, v180, v52
	v_mul_f32_e64 v59, v181, v52
	v_cvt_pk_bf16_f32 v32, v32, v33
	v_cvt_pk_bf16_f32 v33, v34, v35
	s_nop 0
	v_cvt_pk_bf16_f32 v34, v58, v59
	v_cvt_pk_bf16_f32 v35, v56, v57
	global_store_dwordx4 v[54:55], v[32:35], off
	v_mul_f32_e64 v56, v178, v52
	v_mul_f32_e64 v57, v179, v52
	v_mul_f32_e64 v58, v176, v52
	v_mul_f32_e64 v59, v177, v52
	v_mul_f32_e64 v34, v186, v52
	v_mul_f32_e64 v35, v187, v52
	v_mul_f32_e64 v32, v184, v52
	v_mul_f32_e64 v33, v185, v52
	s_nop 0
	v_cvt_pk_bf16_f32 v32, v32, v33
	v_cvt_pk_bf16_f32 v33, v34, v35
	v_cvt_pk_bf16_f32 v34, v58, v59
	v_cvt_pk_bf16_f32 v35, v56, v57
	global_store_dwordx4 v[54:55], v[32:35], off offset:256

;     __device__ __forceinline__ void operator()(const f32x4 (&acc)[2][2][4][2], const Unit& u, int wr, int wc, int fr, int fq, const Pre&) const {
;     ...
;                 } else if (kind == KD_Q || kind == KD_K) {
;                     bf16_t* o = (kind == KD_Q) ? qb + (size_t)row * DM + 256 * (pn - TL_Q) + cw : kb + (size_t)row * 512 + 256 * (pn - TL_K) + cw;
; #pragma unroll
;                     for (int bj = 0; bj < 2; ++bj) {
;                         const f32x4 x1 = acc[ai][bj][m][0] * rs, x2 = acc[ai][bj][m][1] * rs;
;                         if (rotqk) st_bf16x8(o + 128 * bj, x1 * cs[q] - x2 * sn[q], x2 * cs[q] + x1 * sn[q]);
;                         else st_bf16x8(o + 128 * bj, x1, x2);
;                     }
.LBB0_619:
	s_andn2_b64 vcc, exec, s[2:3]
	s_cbranch_vccnz .LBB0_629
	v_mul_f32_e64 v54, v190, v52
	v_mul_f32_e64 v55, v191, v52
	v_mul_f32_e64 v56, v188, v52
	v_mul_f32_e64 v57, v189, v52
	v_mul_f32_e64 v58, v182, v52
	v_mul_f32_e64 v59, v183, v52
	v_mul_f32_e64 v60, v180, v52
	v_mul_f32_e64 v61, v181, v52
	s_mov_b64 s[2:3], -1
	s_and_b64 vcc, exec, s[78:79]
	s_cbranch_vccz .LBB0_622
	v_cvt_pk_bf16_f32 v32, v56, v57
	v_cvt_pk_bf16_f32 v33, v54, v55
	v_cvt_pk_bf16_f32 v34, v60, v61
	v_cvt_pk_bf16_f32 v35, v58, v59
	s_mov_b64 s[2:3], 0
.LBB0_622:
	s_andn2_b64 vcc, exec, s[2:3]
	s_cbranch_vccnz .LBB0_624
	v_mul_f32_e64 v32, v58, v26
	v_mul_f32_e64 v33, v59, v27
	v_mul_f32_e64 v34, v60, v24
	v_mul_f32_e64 v35, v61, v25
	v_fma_f32 v62, v54, v30, -v32
	v_fma_f32 v63, v55, v31, -v33
	v_fma_f32 v32, v56, v28, -v34
	v_fma_f32 v33, v57, v29, -v35
	v_mul_f32_e64 v34, v58, v30
	v_mul_f32_e64 v35, v59, v31
	v_mul_f32_e64 v58, v60, v28
	v_mul_f32_e64 v59, v61, v29
	v_fma_f32 v54, v54, v26, v34
	v_fma_f32 v55, v55, v27, v35
	v_fma_f32 v34, v56, v24, v58
	v_fma_f32 v35, v57, v25, v59
	v_cvt_pk_bf16_f32 v32, v32, v33
	v_cvt_pk_bf16_f32 v33, v62, v63
	s_nop 0
	v_cvt_pk_bf16_f32 v34, v34, v35
	v_cvt_pk_bf16_f32 v35, v54, v55
.LBB0_624:
	s_and_b64 s[2:3], s[80:81], exec
	v_readlane_b32 s2, v249, 49
	v_readlane_b32 s3, v249, 51
	s_cselect_b32 s3, s2, s3
	v_readlane_b32 s2, v249, 48
	v_readlane_b32 s4, v249, 50
	s_cselect_b32 s77, 12, 10
	s_cselect_b32 s2, s2, s4
	v_lshlrev_b64 v[54:55], s77, v[40:41]
	s_cselect_b32 s5, s54, s45
	s_cselect_b32 s4, s8, s57
	v_lshl_add_u64 v[54:55], s[2:3], 0, v[54:55]
	v_lshl_add_u64 v[54:55], s[4:5], 1, v[54:55]
	v_lshl_add_u64 v[54:55], v[36:37], 1, v[54:55]
	v_mov_b32_e32 v53, v52
	global_store_dwordx4 v[54:55], v[32:35], off
	v_mul_f32_e64 v58, v184, v52
	v_mul_f32_e64 v59, v185, v53
	v_mul_f32_e64 v62, v176, v52
	v_mul_f32_e64 v63, v177, v53
	v_mov_b32_e32 v32, v52
	v_mov_b32_e32 v33, v52
	v_mul_f32_e64 v56, v186, v32
	v_mul_f32_e64 v57, v187, v33
	v_mul_f32_e64 v60, v178, v32
	v_mul_f32_e64 v61, v179, v33
	s_andn2_b64 vcc, exec, s[78:79]
	s_mov_b64 s[2:3], -1
	s_cbranch_vccnz .LBB0_626
	s_mov_b64 s[2:3], 0
	v_cvt_pk_bf16_f32 v32, v58, v59
	v_cvt_pk_bf16_f32 v33, v56, v57
	v_cvt_pk_bf16_f32 v34, v62, v63
	v_cvt_pk_bf16_f32 v35, v60, v61
.LBB0_626:
	s_andn2_b64 vcc, exec, s[2:3]
	s_cbranch_vccnz .LBB0_628
	v_mul_f32_e64 v32, v60, v26
	v_mul_f32_e64 v33, v61, v27
	v_mul_f32_e64 v34, v62, v24
	v_mul_f32_e64 v35, v63, v25
	v_fma_f32 v238, v56, v30, -v32
	v_fma_f32 v239, v57, v31, -v33
	v_fma_f32 v32, v58, v28, -v34
	v_fma_f32 v33, v59, v29, -v35
	v_mul_f32_e64 v30, v60, v30
	v_mul_f32_e64 v31, v61, v31
	v_mul_f32_e64 v28, v62, v28
	v_mul_f32_e64 v29, v63, v29
	v_fma_f32 v26, v56, v26, v30
	v_fma_f32 v27, v57, v27, v31
	v_fma_f32 v24, v58, v24, v28
	v_fma_f32 v25, v59, v25, v29
	v_cvt_pk_bf16_f32 v32, v32, v33
	v_cvt_pk_bf16_f32 v33, v238, v239
	s_nop 0
	v_cvt_pk_bf16_f32 v34, v24, v25
	v_cvt_pk_bf16_f32 v35, v26, v27

; __device__ __forceinline__ f32x4 sigmoid4(const f32x4& x, float s) {
;     f32x4 z = x * (s * -1.4426950408889634f), e;
; #pragma unroll
;     for (int j = 0; j < 4; ++j) e[j] = __builtin_amdgcn_exp2f(z[j]);
;     e = e + 1.0f;
; #pragma unroll
;     for (int j = 0; j < 4; ++j) e[j] = __builtin_amdgcn_rcpf(e[j]);
;     return e;
; }
;     __device__ __forceinline__ void operator()(const f32x4 (&acc)[2][2][4][2], const Unit& u, int wr, int wc, int fr, int fq, const Pre&) const {
;     ...
; #pragma unroll
;             for (int m = 0; m < 4; ++m) {
;                 const int row = rowb + ai * 128 + m * 16, q = m;
;                 const float rs = rsv[ai * 4 + m];
;                 if (kind == KD_KVX) {
;                     bf16_t* o = (pn < 2 ? kx : vx) + (size_t)row * 512 + 256 * (pn & 1) + cw;
; #pragma unroll
;                     for (int bj = 0; bj < 2; ++bj) st_bf16x8(o + 128 * bj, acc[ai][bj][m][0] * rs, acc[ai][bj][m][1] * rs);
;                 } else if (kind == KD_A) {
;                     st_bf16x8(abuf + (size_t)row * DM + 128 * (pn - TL_A) + cw, acc[ai][0][m][0] * rs * sigmoid4(acc[ai][1][m][0], rs), acc[ai][0][m][1] * rs * sigmoid4(acc[ai][1][m][1], rs));
;                 } else if (kind == KD_P) {
;                     const float r2 = rs * rs;
;                     st_bf16x8(pbuf + (size_t)row * DM + 128 * (pn - TL_P) + cw, acc[ai][0][m][0] * acc[ai][1][m][0] * r2, acc[ai][0][m][1] * acc[ai][1][m][1] * r2);
;                 } else if (kind == KD_G) {
; #pragma unroll
;                     for (int bj = 0; bj < 2; ++bj)
;                         st_bf16x8(gabuf + (size_t)row * DM + 256 * (pn - TL_G) + 128 * bj + cw, sigmoid4(acc[ai][bj][m][0], rs), sigmoid4(acc[ai][bj][m][1], rs));
.LBB0_630:
	s_andn2_b64 vcc, exec, s[4:5]
	s_ashr_i32 s77, s76, 31
	s_cbranch_vccnz .LBB0_632
	v_lshlrev_b64 v[24:25], 12, v[40:41]
	v_lshl_add_u64 v[24:25], s[12:13], 0, v[24:25]
	v_lshl_add_u64 v[24:25], s[76:77], 1, v[24:25]
	v_mul_f32_e32 v35, 0xbfb8aa3b, v52
	v_lshl_add_u64 v[28:29], v[36:37], 1, v[24:25]
	v_mul_f32_e32 v24, v184, v35
	v_mul_f32_e32 v25, v185, v35
	v_mul_f32_e32 v26, v186, v35
	v_mul_f32_e32 v27, v187, v35
	v_exp_f32_e32 v24, v24
	v_exp_f32_e32 v26, v26
	v_exp_f32_e32 v27, v27
	v_exp_f32_e32 v25, v25
	v_mul_f32_e32 v34, v176, v35
	v_mul_f32_e32 v41, v177, v35
	v_add_f32_e64 v26, v26, 1.0
	v_add_f32_e64 v27, v27, 1.0
	v_add_f32_e64 v24, v24, 1.0
	v_add_f32_e64 v25, v25, 1.0
	v_mul_f32_e32 v47, v178, v35
	v_mul_f32_e32 v35, v179, v35
	v_rcp_f32_e32 v24, v24
	v_rcp_f32_e32 v25, v25
	v_rcp_f32_e32 v26, v26
	v_rcp_f32_e32 v27, v27
	v_exp_f32_e32 v34, v34
	v_exp_f32_e32 v54, v47
	v_exp_f32_e32 v55, v35
	v_exp_f32_e32 v35, v41
	v_mul_f32_e64 v30, v190, v52
	v_mul_f32_e64 v31, v191, v52
	v_mul_f32_e64 v32, v188, v52
	v_mul_f32_e64 v33, v189, v52
	v_mul_f32_e64 v26, v30, v26
	v_mul_f32_e64 v27, v31, v27
	v_mul_f32_e64 v24, v32, v24
	v_mul_f32_e64 v25, v33, v25
	v_add_f32_e64 v30, v54, 1.0
	v_add_f32_e64 v31, v55, 1.0
	v_add_f32_e64 v32, v34, 1.0
	v_add_f32_e64 v33, v35, 1.0
	v_rcp_f32_e32 v30, v30
	v_rcp_f32_e32 v32, v32
	v_rcp_f32_e32 v31, v31
	v_rcp_f32_e32 v33, v33
	v_mul_f32_e64 v34, v182, v52
	v_mul_f32_e64 v35, v183, v52
	v_mul_f32_e64 v53, v181, v52
	v_mul_f32_e64 v52, v180, v52
	v_mul_f32_e64 v30, v34, v30
	v_mul_f32_e64 v31, v35, v31
	v_mul_f32_e64 v32, v52, v32
	v_mul_f32_e64 v33, v53, v33
	v_cvt_pk_bf16_f32 v24, v24, v25
	v_cvt_pk_bf16_f32 v25, v26, v27
	s_nop 0
	v_cvt_pk_bf16_f32 v26, v32, v33
	v_cvt_pk_bf16_f32 v27, v30, v31
	global_store_dwordx4 v[28:29], v[24:27], off
.LBB0_632:
	v_mul_f32_e32 v28, 0x3c800000, v228
	s_mov_b64 s[92:93], -1
	s_mov_b64 s[4:5], 0
	s_cmp_lt_i32 s55, 1
	s_mov_b64 s[2:3], 0
	s_cbranch_scc1 .LBB0_664
	s_cmp_gt_i32 s55, 1
	s_cbranch_scc0 .LBB0_637
	s_cmp_eq_u32 s55, 2
	s_mov_b64 s[2:3], -1
	s_cbranch_scc0 .LBB0_636
	v_ashrrev_i32_e32 v51, 31, v50
	v_readlane_b32 s2, v249, 46
	v_lshlrev_b64 v[24:25], 12, v[50:51]
	v_readlane_b32 s3, v249, 47
	v_mul_f32_e32 v29, 0xbfb8aa3b, v28
	v_mul_f32_e32 v26, v174, v29
	v_lshl_add_u64 v[24:25], s[2:3], 0, v[24:25]
	v_lshl_add_u64 v[24:25], s[90:91], 1, v[24:25]
	v_mul_f32_e32 v27, v175, v29
	v_lshl_add_u64 v[30:31], v[36:37], 1, v[24:25]
	v_mul_f32_e32 v24, v172, v29
	v_mul_f32_e32 v25, v173, v29
	v_exp_f32_e32 v26, v26
	v_exp_f32_e32 v27, v27
	v_exp_f32_e32 v24, v24
	v_exp_f32_e32 v25, v25
	s_mov_b64 s[2:3], 0
	v_add_f32_e64 v26, v26, 1.0
	v_add_f32_e64 v27, v27, 1.0
	v_add_f32_e64 v24, v24, 1.0
	v_add_f32_e64 v25, v25, 1.0
	v_rcp_f32_e32 v34, v26
	v_rcp_f32_e32 v35, v27
	v_mul_f32_e32 v26, v166, v29
	v_mul_f32_e32 v27, v167, v29
	v_rcp_f32_e32 v32, v24
	v_rcp_f32_e32 v33, v25
	v_mul_f32_e32 v24, v164, v29
	v_mul_f32_e32 v25, v165, v29
	v_exp_f32_e32 v26, v26
	v_exp_f32_e32 v27, v27
	v_exp_f32_e32 v24, v24
	v_exp_f32_e32 v25, v25
	v_add_f32_e64 v26, v26, 1.0
	v_add_f32_e64 v27, v27, 1.0
	s_nop 0
	v_rcp_f32_e32 v27, v27
	v_add_f32_e64 v24, v24, 1.0
	v_add_f32_e64 v25, v25, 1.0
	v_rcp_f32_e32 v49, v26
	v_rcp_f32_e32 v41, v24
	v_rcp_f32_e32 v47, v25
	v_cvt_pk_bf16_f32 v24, v32, v33
	v_cvt_pk_bf16_f32 v25, v34, v35
	v_cvt_pk_bf16_f32 v26, v41, v47
	v_cvt_pk_bf16_f32 v27, v49, v27
	global_store_dwordx4 v[30:31], v[24:27], off
	s_nop 1
	v_mul_f32_e32 v26, v170, v29
	v_mul_f32_e32 v27, v171, v29
	v_mul_f32_e32 v24, v168, v29
	v_mul_f32_e32 v25, v169, v29
	v_exp_f32_e32 v26, v26
	v_exp_f32_e32 v27, v27
	v_exp_f32_e32 v24, v24
	v_exp_f32_e32 v25, v25
	v_add_f32_e64 v26, v26, 1.0
	v_add_f32_e64 v27, v27, 1.0
	s_nop 0
	v_rcp_f32_e32 v34, v26
	v_add_f32_e64 v24, v24, 1.0
	v_add_f32_e64 v25, v25, 1.0
	v_rcp_f32_e32 v35, v27
	v_mul_f32_e32 v26, v162, v29
	v_mul_f32_e32 v27, v163, v29
	v_rcp_f32_e32 v32, v24
	v_rcp_f32_e32 v33, v25
	v_mul_f32_e32 v24, v160, v29
	v_mul_f32_e32 v25, v161, v29
	v_exp_f32_e32 v26, v26
	v_exp_f32_e32 v27, v27
	v_exp_f32_e32 v24, v24
	v_exp_f32_e32 v25, v25
	v_add_f32_e64 v26, v26, 1.0
	v_add_f32_e64 v27, v27, 1.0
	s_nop 0
	v_rcp_f32_e32 v27, v27
	v_add_f32_e64 v24, v24, 1.0
	v_add_f32_e64 v25, v25, 1.0
	v_rcp_f32_e32 v47, v26
	v_rcp_f32_e32 v29, v24
	v_rcp_f32_e32 v41, v25
	v_cvt_pk_bf16_f32 v24, v32, v33
	v_cvt_pk_bf16_f32 v25, v34, v35
	v_cvt_pk_bf16_f32 v26, v29, v41
	v_cvt_pk_bf16_f32 v27, v47, v27
	global_store_dwordx4 v[30:31], v[24:27], off offset:256

;     __device__ __forceinline__ void operator()(const f32x4 (&acc)[2][2][4][2], const Unit& u, int wr, int wc, int fr, int fq, const Pre&) const {
;     ...
;                 } else if (kind == KD_P) {
;                     const float r2 = rs * rs;
;                     st_bf16x8(pbuf + (size_t)row * DM + 128 * (pn - TL_P) + cw, acc[ai][0][m][0] * acc[ai][1][m][0] * r2, acc[ai][0][m][1] * acc[ai][1][m][1] * r2);
.LBB0_637:
	s_and_b64 vcc, exec, s[92:93]
	s_cbranch_vccz .LBB0_639
	v_ashrrev_i32_e32 v51, 31, v50
	v_readlane_b32 s50, v249, 44
	v_lshlrev_b64 v[26:27], 12, v[50:51]
	v_readlane_b32 s51, v249, 45
	v_mul_f32_e32 v24, v28, v28
	v_mul_f32_e64 v32, v172, v168
	v_mul_f32_e64 v33, v173, v169
	v_lshl_add_u64 v[26:27], s[50:51], 0, v[26:27]
	v_lshl_add_u64 v[26:27], s[84:85], 1, v[26:27]
	v_lshl_add_u64 v[30:31], v[36:37], 1, v[26:27]
	v_mul_f32_e64 v26, v174, v170
	v_mul_f32_e64 v27, v175, v171
	v_mul_f32_e64 v34, v166, v162
	v_mul_f32_e64 v35, v167, v163
	v_mul_f32_e64 v26, v26, v24
	v_mul_f32_e64 v27, v27, v24
	v_mul_f32_e64 v52, v164, v160
	v_mul_f32_e64 v53, v165, v161
	v_mul_f32_e64 v32, v32, v24
	v_mul_f32_e64 v33, v33, v24
	v_mul_f32_e64 v34, v34, v24
	v_mul_f32_e64 v35, v35, v24
	v_mul_f32_e64 v52, v52, v24
	v_mul_f32_e64 v53, v53, v24
	v_cvt_pk_bf16_f32 v24, v32, v33
	v_cvt_pk_bf16_f32 v25, v26, v27
	s_nop 0
	v_cvt_pk_bf16_f32 v26, v52, v53
	v_cvt_pk_bf16_f32 v27, v34, v35
	global_store_dwordx4 v[30:31], v[24:27], off

;     __device__ __forceinline__ void operator()(const f32x4 (&acc)[2][2][4][2], const Unit& u, int wr, int wc, int fr, int fq, const Pre&) const {
;     ...
;                 } else {
;                     const f32x4 x1 = acc[ai][0][m][0] * rs, x2 = acc[ai][0][m][1] * rs;
;                     if (wc < 2) {
;                         if (roti) st_bf16x8(kib + (size_t)row * 64 + cw, x1 * cs[q] - x2 * sn[q], x2 * cs[q] + x1 * sn[q]);
;                         else st_bf16x8(kib + (size_t)row * 64 + cw, x1, x2);
;                     } else if (wc == 2 && fq < 2) {
;                         *(f32x4*)(wib + (size_t)row * 16 + 8 * fq) = x1 * 0.03125f; *(f32x4*)(wib + (size_t)row * 16 + 8 * fq + 4) = x2 * 0.03125f;
;                     }
.LBB0_641:
	s_and_b64 vcc, exec, s[2:3]
	s_mov_b64 s[4:5], -1
	s_cbranch_vccnz .LBB0_653
	s_andn2_b64 vcc, exec, s[82:83]
	s_cbranch_vccnz .LBB0_650
	v_mul_f32_e64 v26, v174, v28
	v_mul_f32_e64 v27, v175, v28
	v_mul_f32_e64 v32, v172, v28
	v_mul_f32_e64 v33, v173, v28
	v_mul_f32_e64 v24, v166, v28
	v_mul_f32_e64 v25, v167, v28
	v_mul_f32_e64 v30, v164, v28
	v_mul_f32_e64 v31, v165, v28
	s_andn2_b64 vcc, exec, s[34:35]
	s_cbranch_vccnz .LBB0_647
	s_and_saveexec_b64 s[4:5], s[88:89]
	s_cbranch_execz .LBB0_646
	v_ashrrev_i32_e32 v51, 31, v50
	v_readlane_b32 s36, v249, 56
	v_lshlrev_b64 v[34:35], 6, v[50:51]
	v_readlane_b32 s37, v249, 57
	v_mul_f32_e64 v54, v26, s38
	v_mul_f32_e64 v55, v27, s38
	v_mul_f32_e64 v52, v32, s38
	v_mul_f32_e64 v53, v33, s38
	v_lshl_add_u64 v[34:35], s[36:37], 0, v[34:35]
	v_lshl_add_u64 v[34:35], v[38:39], 2, v[34:35]
	global_store_dwordx4 v[34:35], v[52:55], off
	s_nop 1
	v_mul_f32_e64 v54, v24, s38
	v_mul_f32_e64 v55, v25, s38
	v_mul_f32_e64 v52, v30, s38
	v_mul_f32_e64 v53, v31, s38
	global_store_dwordx4 v[34:35], v[52:55], off offset:16

;     __device__ __forceinline__ void operator()(const f32x4 (&acc)[2][2][4][2], const Unit& u, int wr, int wc, int fr, int fq, const Pre&) const {
;     ...
;                 } else if (kind == KD_V) {
; #pragma unroll
;                     for (int bj = 0; bj < 2; ++bj) st_bf16x8(vb + (size_t)row * 512 + 256 * (pn - TL_V) + 128 * bj + cw, acc[ai][bj][m][0] * rs, acc[ai][bj][m][1] * rs);
.LBB0_650:
	s_andn2_b64 vcc, exec, s[4:5]
	s_cbranch_vccnz .LBB0_652
	v_ashrrev_i32_e32 v51, 31, v50
	v_readlane_b32 s4, v249, 52
	v_lshlrev_b64 v[24:25], 10, v[50:51]
	v_readlane_b32 s5, v249, 53
	v_mul_f32_e64 v26, v174, v28
	v_mul_f32_e64 v27, v175, v28
	v_mul_f32_e64 v32, v166, v28
	v_mul_f32_e64 v33, v167, v28
	v_lshl_add_u64 v[24:25], s[4:5], 0, v[24:25]
	v_lshl_add_u64 v[24:25], s[86:87], 1, v[24:25]
	v_lshl_add_u64 v[30:31], v[36:37], 1, v[24:25]
	v_mul_f32_e64 v24, v172, v28
	v_mul_f32_e64 v25, v173, v28
	v_mul_f32_e64 v34, v164, v28
	v_mul_f32_e64 v35, v165, v28
	v_cvt_pk_bf16_f32 v24, v24, v25
	v_cvt_pk_bf16_f32 v25, v26, v27
	s_nop 0
	v_cvt_pk_bf16_f32 v26, v34, v35
	v_cvt_pk_bf16_f32 v27, v32, v33
	global_store_dwordx4 v[30:31], v[24:27], off
	v_mul_f32_e64 v32, v162, v28
	v_mul_f32_e64 v33, v163, v28
	v_mul_f32_e64 v34, v160, v28
	v_mul_f32_e64 v35, v161, v28
	v_mul_f32_e64 v26, v170, v28
	v_mul_f32_e64 v27, v171, v28
	v_mul_f32_e64 v24, v168, v28
	v_mul_f32_e64 v25, v169, v28
	s_nop 0
	v_cvt_pk_bf16_f32 v24, v24, v25
	v_cvt_pk_bf16_f32 v25, v26, v27
	v_cvt_pk_bf16_f32 v26, v34, v35
	v_cvt_pk_bf16_f32 v27, v32, v33
	global_store_dwordx4 v[30:31], v[24:27], off offset:256

;     __device__ __forceinline__ void operator()(const f32x4 (&acc)[2][2][4][2], const Unit& u, int wr, int wc, int fr, int fq, const Pre&) const {
;     ...
;                 } else if (kind == KD_Q || kind == KD_K) {
;                     bf16_t* o = (kind == KD_Q) ? qb + (size_t)row * DM + 256 * (pn - TL_Q) + cw : kb + (size_t)row * 512 + 256 * (pn - TL_K) + cw;
; #pragma unroll
;                     for (int bj = 0; bj < 2; ++bj) {
;                         const f32x4 x1 = acc[ai][bj][m][0] * rs, x2 = acc[ai][bj][m][1] * rs;
;                         if (rotqk) st_bf16x8(o + 128 * bj, x1 * cs[q] - x2 * sn[q], x2 * cs[q] + x1 * sn[q]);
;                         else st_bf16x8(o + 128 * bj, x1, x2);
;                     }
.LBB0_653:
	s_andn2_b64 vcc, exec, s[4:5]
	s_cbranch_vccnz .LBB0_663
	v_cndmask_b32_e64 v24, 0, 1, s[78:79]
	v_mul_f32_e64 v30, v174, v28
	v_mul_f32_e64 v31, v175, v28
	v_mul_f32_e64 v32, v172, v28
	v_mul_f32_e64 v33, v173, v28
	v_mul_f32_e64 v34, v166, v28
	v_mul_f32_e64 v35, v167, v28
	v_mul_f32_e64 v52, v164, v28
	v_mul_f32_e64 v53, v165, v28
	v_cmp_ne_u32_e64 s[4:5], 1, v24
	s_andn2_b64 vcc, exec, s[78:79]
	s_mov_b64 s[36:37], -1
	s_cbranch_vccnz .LBB0_656
	s_mov_b64 s[36:37], 0
	v_cvt_pk_bf16_f32 v24, v32, v33
	v_cvt_pk_bf16_f32 v25, v30, v31
	v_cvt_pk_bf16_f32 v26, v52, v53
	v_cvt_pk_bf16_f32 v27, v34, v35
.LBB0_656:
	s_andn2_b64 vcc, exec, s[36:37]
	s_cbranch_vccnz .LBB0_658
	v_mul_f32_e64 v24, v34, v18
	v_mul_f32_e64 v25, v35, v19
	v_mul_f32_e64 v26, v52, v16
	v_mul_f32_e64 v27, v53, v17
	v_fma_f32 v54, v30, v22, -v24
	v_fma_f32 v55, v31, v23, -v25
	v_fma_f32 v24, v32, v20, -v26
	v_fma_f32 v25, v33, v21, -v27
	v_mul_f32_e64 v26, v34, v22
	v_mul_f32_e64 v27, v35, v23
	v_mul_f32_e64 v34, v52, v20
	v_mul_f32_e64 v35, v53, v21
	v_fma_f32 v30, v30, v18, v26
	v_fma_f32 v31, v31, v19, v27
	v_fma_f32 v26, v32, v16, v34
	v_fma_f32 v27, v33, v17, v35
	v_cvt_pk_bf16_f32 v24, v24, v25
	v_cvt_pk_bf16_f32 v25, v54, v55
	s_nop 0
	v_cvt_pk_bf16_f32 v26, v26, v27
	v_cvt_pk_bf16_f32 v27, v30, v31
.LBB0_658:
	s_and_b64 s[36:37], s[80:81], exec
	v_readlane_b32 s36, v249, 49
	v_readlane_b32 s37, v249, 51
	v_ashrrev_i32_e32 v51, 31, v50
	s_cselect_b32 s37, s36, s37
	v_readlane_b32 s36, v249, 48
	v_readlane_b32 s92, v249, 50
	s_cselect_b32 vcc_lo, 12, 10
	s_cselect_b32 s36, s36, s92
	v_lshlrev_b64 v[30:31], vcc_lo, v[50:51]
	s_cselect_b32 s93, s54, s45
	s_cselect_b32 s92, s8, s57
	v_lshl_add_u64 v[30:31], s[36:37], 0, v[30:31]
	v_lshl_add_u64 v[30:31], s[92:93], 1, v[30:31]
	v_lshl_add_u64 v[30:31], v[36:37], 1, v[30:31]
	v_mov_b32_e32 v29, v28
	global_store_dwordx4 v[30:31], v[24:27], off
	v_mul_f32_e64 v34, v168, v28
	v_mul_f32_e64 v35, v169, v29
	v_mul_f32_e64 v54, v160, v28
	v_mul_f32_e64 v55, v161, v29
	v_mov_b32_e32 v24, v28
	v_mov_b32_e32 v25, v28
	v_mul_f32_e64 v32, v170, v24
	v_mul_f32_e64 v33, v171, v25
	v_mul_f32_e64 v52, v162, v24
	v_mul_f32_e64 v53, v163, v25
	s_and_b64 vcc, exec, s[4:5]
	s_mov_b64 s[4:5], -1
	s_cbranch_vccnz .LBB0_660
	s_mov_b64 s[4:5], 0
	v_cvt_pk_bf16_f32 v24, v34, v35
	v_cvt_pk_bf16_f32 v25, v32, v33
	v_cvt_pk_bf16_f32 v26, v54, v55
	v_cvt_pk_bf16_f32 v27, v52, v53
.LBB0_660:
	s_andn2_b64 vcc, exec, s[4:5]
	s_cbranch_vccnz .LBB0_662
	v_mul_f32_e64 v24, v52, v18
	v_mul_f32_e64 v25, v53, v19
	v_mul_f32_e64 v26, v54, v16
	v_mul_f32_e64 v27, v55, v17
	v_fma_f32 v56, v32, v22, -v24
	v_fma_f32 v57, v33, v23, -v25
	v_fma_f32 v24, v34, v20, -v26
	v_fma_f32 v25, v35, v21, -v27
	v_mul_f32_e64 v22, v52, v22
	v_mul_f32_e64 v23, v53, v23
	v_mul_f32_e64 v20, v54, v20
	v_mul_f32_e64 v21, v55, v21
	v_fma_f32 v18, v32, v18, v22
	v_fma_f32 v19, v33, v19, v23
	v_fma_f32 v16, v34, v16, v20
	v_fma_f32 v17, v35, v17, v21
	v_cvt_pk_bf16_f32 v24, v24, v25
	v_cvt_pk_bf16_f32 v25, v56, v57
	s_nop 0
	v_cvt_pk_bf16_f32 v26, v16, v17
	v_cvt_pk_bf16_f32 v27, v18, v19

; __device__ __forceinline__ f32x4 sigmoid4(const f32x4& x, float s) {
;     f32x4 z = x * (s * -1.4426950408889634f), e;
; #pragma unroll
;     for (int j = 0; j < 4; ++j) e[j] = __builtin_amdgcn_exp2f(z[j]);
;     e = e + 1.0f;
; #pragma unroll
;     for (int j = 0; j < 4; ++j) e[j] = __builtin_amdgcn_rcpf(e[j]);
;     return e;
; }
;     __device__ __forceinline__ void operator()(const f32x4 (&acc)[2][2][4][2], const Unit& u, int wr, int wc, int fr, int fq, const Pre&) const {
;     ...
; #pragma unroll
;             for (int m = 0; m < 4; ++m) {
;                 const int row = rowb + ai * 128 + m * 16, q = m;
;                 const float rs = rsv[ai * 4 + m];
;                 if (kind == KD_KVX) {
;                     bf16_t* o = (pn < 2 ? kx : vx) + (size_t)row * 512 + 256 * (pn & 1) + cw;
; #pragma unroll
;                     for (int bj = 0; bj < 2; ++bj) st_bf16x8(o + 128 * bj, acc[ai][bj][m][0] * rs, acc[ai][bj][m][1] * rs);
;                 } else if (kind == KD_A) {
;                     st_bf16x8(abuf + (size_t)row * DM + 128 * (pn - TL_A) + cw, acc[ai][0][m][0] * rs * sigmoid4(acc[ai][1][m][0], rs), acc[ai][0][m][1] * rs * sigmoid4(acc[ai][1][m][1], rs));
;                 } else if (kind == KD_P) {
;                     const float r2 = rs * rs;
;                     st_bf16x8(pbuf + (size_t)row * DM + 128 * (pn - TL_P) + cw, acc[ai][0][m][0] * acc[ai][1][m][0] * r2, acc[ai][0][m][1] * acc[ai][1][m][1] * r2);
;                 } else if (kind == KD_G) {
; #pragma unroll
;                     for (int bj = 0; bj < 2; ++bj)
;                         st_bf16x8(gabuf + (size_t)row * DM + 256 * (pn - TL_G) + 128 * bj + cw, sigmoid4(acc[ai][bj][m][0], rs), sigmoid4(acc[ai][bj][m][1], rs));
.LBB0_667:
	v_ashrrev_i32_e32 v51, 31, v50
	v_lshlrev_b64 v[16:17], 12, v[50:51]
	v_lshl_add_u64 v[16:17], s[12:13], 0, v[16:17]
	v_lshl_add_u64 v[16:17], s[76:77], 1, v[16:17]
	v_mul_f32_e32 v27, 0xbfb8aa3b, v28
	v_lshl_add_u64 v[20:21], v[36:37], 1, v[16:17]
	v_mul_f32_e32 v16, v168, v27
	v_mul_f32_e32 v17, v169, v27
	v_mul_f32_e32 v18, v170, v27
	v_mul_f32_e32 v19, v171, v27
	v_exp_f32_e32 v16, v16
	v_exp_f32_e32 v18, v18
	v_exp_f32_e32 v19, v19
	v_exp_f32_e32 v17, v17
	v_mul_f32_e64 v22, v174, v28
	v_mul_f32_e64 v23, v175, v28
	v_mul_f32_e64 v24, v172, v28
	v_mul_f32_e64 v25, v173, v28
	v_add_f32_e64 v18, v18, 1.0
	v_add_f32_e64 v19, v19, 1.0
	v_add_f32_e64 v16, v16, 1.0
	v_add_f32_e64 v17, v17, 1.0
	v_mul_f32_e32 v26, v160, v27
	v_mul_f32_e32 v29, v161, v27
	v_mul_f32_e32 v30, v162, v27
	v_mul_f32_e32 v27, v163, v27
	v_rcp_f32_e32 v16, v16
	v_rcp_f32_e32 v17, v17
	v_rcp_f32_e32 v18, v18
	v_rcp_f32_e32 v19, v19
	v_exp_f32_e32 v26, v26
	v_exp_f32_e32 v30, v30
	v_exp_f32_e32 v31, v27
	v_exp_f32_e32 v27, v29
	v_mul_f32_e64 v18, v22, v18
	v_mul_f32_e64 v19, v23, v19
	v_mul_f32_e64 v16, v24, v16
	v_mul_f32_e64 v17, v25, v17
	v_add_f32_e64 v22, v30, 1.0
	v_add_f32_e64 v23, v31, 1.0
	v_add_f32_e64 v24, v26, 1.0
	v_add_f32_e64 v25, v27, 1.0
	v_rcp_f32_e32 v22, v22
	v_rcp_f32_e32 v24, v24
	v_rcp_f32_e32 v23, v23
	v_rcp_f32_e32 v25, v25
	v_mul_f32_e64 v26, v166, v28
	v_mul_f32_e64 v27, v167, v28
	v_mul_f32_e64 v29, v165, v28
	v_mul_f32_e64 v28, v164, v28
	v_mul_f32_e64 v22, v26, v22
	v_mul_f32_e64 v23, v27, v23
	v_mul_f32_e64 v24, v28, v24
	v_mul_f32_e64 v25, v29, v25
	v_cvt_pk_bf16_f32 v16, v16, v17
	v_cvt_pk_bf16_f32 v17, v18, v19
	s_nop 0
	v_cvt_pk_bf16_f32 v18, v24, v25
	v_cvt_pk_bf16_f32 v19, v22, v23
	global_store_dwordx4 v[20:21], v[16:19], off
.LBB0_668:
	v_mul_f32_e32 v20, 0x3c800000, v227
	s_mov_b64 s[92:93], -1
	s_mov_b64 s[4:5], 0
	s_cmp_lt_i32 s55, 1
	s_mov_b64 s[36:37], 0
	s_cbranch_scc1 .LBB0_700
	s_cmp_gt_i32 s55, 1
	s_cbranch_scc0 .LBB0_673
	s_cmp_eq_u32 s55, 2
	s_mov_b64 s[36:37], -1
	s_cbranch_scc0 .LBB0_672
	v_ashrrev_i32_e32 v49, 31, v48
	v_readlane_b32 s36, v249, 46
	v_lshlrev_b64 v[16:17], 12, v[48:49]
	v_readlane_b32 s37, v249, 47
	v_mul_f32_e32 v21, 0xbfb8aa3b, v20
	v_mul_f32_e32 v18, v158, v21
	v_lshl_add_u64 v[16:17], s[36:37], 0, v[16:17]
	v_lshl_add_u64 v[16:17], s[90:91], 1, v[16:17]
	v_mul_f32_e32 v19, v159, v21
	v_lshl_add_u64 v[22:23], v[36:37], 1, v[16:17]
	v_mul_f32_e32 v16, v156, v21
	v_mul_f32_e32 v17, v157, v21
	v_exp_f32_e32 v18, v18
	v_exp_f32_e32 v19, v19
	v_exp_f32_e32 v16, v16
	v_exp_f32_e32 v17, v17
	s_mov_b64 s[36:37], 0
	v_add_f32_e64 v18, v18, 1.0
	v_add_f32_e64 v19, v19, 1.0
	v_add_f32_e64 v16, v16, 1.0
	v_add_f32_e64 v17, v17, 1.0
	v_rcp_f32_e32 v26, v18
	v_rcp_f32_e32 v27, v19
	v_mul_f32_e32 v18, v150, v21
	v_mul_f32_e32 v19, v151, v21
	v_rcp_f32_e32 v24, v16
	v_rcp_f32_e32 v25, v17
	v_mul_f32_e32 v16, v148, v21
	v_mul_f32_e32 v17, v149, v21
	v_exp_f32_e32 v18, v18
	v_exp_f32_e32 v19, v19
	v_exp_f32_e32 v16, v16
	v_exp_f32_e32 v17, v17
	v_add_f32_e64 v18, v18, 1.0
	v_add_f32_e64 v19, v19, 1.0
	s_nop 0
	v_rcp_f32_e32 v19, v19
	v_add_f32_e64 v16, v16, 1.0
	v_add_f32_e64 v17, v17, 1.0
	v_rcp_f32_e32 v30, v18
	v_rcp_f32_e32 v28, v16
	v_rcp_f32_e32 v29, v17
	v_cvt_pk_bf16_f32 v16, v24, v25
	v_cvt_pk_bf16_f32 v17, v26, v27
	v_cvt_pk_bf16_f32 v18, v28, v29
	v_cvt_pk_bf16_f32 v19, v30, v19
	global_store_dwordx4 v[22:23], v[16:19], off
	s_nop 1
	v_mul_f32_e32 v18, v154, v21
	v_mul_f32_e32 v19, v155, v21
	v_mul_f32_e32 v16, v152, v21
	v_mul_f32_e32 v17, v153, v21
	v_exp_f32_e32 v18, v18
	v_exp_f32_e32 v19, v19
	v_exp_f32_e32 v16, v16
	v_exp_f32_e32 v17, v17
	v_add_f32_e64 v18, v18, 1.0
	v_add_f32_e64 v19, v19, 1.0
	s_nop 0
	v_rcp_f32_e32 v26, v18
	v_add_f32_e64 v16, v16, 1.0
	v_add_f32_e64 v17, v17, 1.0
	v_rcp_f32_e32 v27, v19
	v_mul_f32_e32 v18, v146, v21
	v_mul_f32_e32 v19, v147, v21
	v_rcp_f32_e32 v24, v16
	v_rcp_f32_e32 v25, v17
	v_mul_f32_e32 v16, v144, v21
	v_mul_f32_e32 v17, v145, v21
	v_exp_f32_e32 v18, v18
	v_exp_f32_e32 v19, v19
	v_exp_f32_e32 v16, v16
	v_exp_f32_e32 v17, v17
	v_add_f32_e64 v18, v18, 1.0
	v_add_f32_e64 v19, v19, 1.0
	s_nop 0
	v_rcp_f32_e32 v19, v19
	v_add_f32_e64 v16, v16, 1.0
	v_add_f32_e64 v17, v17, 1.0
	v_rcp_f32_e32 v29, v18
	v_rcp_f32_e32 v21, v16
	v_rcp_f32_e32 v28, v17
	v_cvt_pk_bf16_f32 v16, v24, v25
	v_cvt_pk_bf16_f32 v17, v26, v27
	v_cvt_pk_bf16_f32 v18, v21, v28
	v_cvt_pk_bf16_f32 v19, v29, v19
	global_store_dwordx4 v[22:23], v[16:19], off offset:256

;     __device__ __forceinline__ void operator()(const f32x4 (&acc)[2][2][4][2], const Unit& u, int wr, int wc, int fr, int fq, const Pre&) const {
;     ...
;                 } else if (kind == KD_P) {
;                     const float r2 = rs * rs;
;                     st_bf16x8(pbuf + (size_t)row * DM + 128 * (pn - TL_P) + cw, acc[ai][0][m][0] * acc[ai][1][m][0] * r2, acc[ai][0][m][1] * acc[ai][1][m][1] * r2);
.LBB0_673:
	s_and_b64 vcc, exec, s[92:93]
	s_cbranch_vccz .LBB0_675
	v_ashrrev_i32_e32 v49, 31, v48
	v_readlane_b32 s50, v249, 44
	v_lshlrev_b64 v[18:19], 12, v[48:49]
	v_readlane_b32 s51, v249, 45
	v_mul_f32_e32 v16, v20, v20
	v_mul_f32_e64 v24, v156, v152
	v_mul_f32_e64 v25, v157, v153
	v_lshl_add_u64 v[18:19], s[50:51], 0, v[18:19]
	v_lshl_add_u64 v[18:19], s[84:85], 1, v[18:19]
	v_lshl_add_u64 v[22:23], v[36:37], 1, v[18:19]
	v_mul_f32_e64 v18, v158, v154
	v_mul_f32_e64 v19, v159, v155
	v_mul_f32_e64 v26, v150, v146
	v_mul_f32_e64 v27, v151, v147
	v_mul_f32_e64 v18, v18, v16
	v_mul_f32_e64 v19, v19, v16
	v_mul_f32_e64 v28, v148, v144
	v_mul_f32_e64 v29, v149, v145
	v_mul_f32_e64 v24, v24, v16
	v_mul_f32_e64 v25, v25, v16
	v_mul_f32_e64 v26, v26, v16
	v_mul_f32_e64 v27, v27, v16
	v_mul_f32_e64 v28, v28, v16
	v_mul_f32_e64 v29, v29, v16
	v_cvt_pk_bf16_f32 v16, v24, v25
	v_cvt_pk_bf16_f32 v17, v18, v19
	s_nop 0
	v_cvt_pk_bf16_f32 v18, v28, v29
	v_cvt_pk_bf16_f32 v19, v26, v27
	global_store_dwordx4 v[22:23], v[16:19], off

;     __device__ __forceinline__ void operator()(const f32x4 (&acc)[2][2][4][2], const Unit& u, int wr, int wc, int fr, int fq, const Pre&) const {
;     ...
;                 } else {
;                     const f32x4 x1 = acc[ai][0][m][0] * rs, x2 = acc[ai][0][m][1] * rs;
;                     if (wc < 2) {
;                         if (roti) st_bf16x8(kib + (size_t)row * 64 + cw, x1 * cs[q] - x2 * sn[q], x2 * cs[q] + x1 * sn[q]);
;                         else st_bf16x8(kib + (size_t)row * 64 + cw, x1, x2);
;                     } else if (wc == 2 && fq < 2) {
;                         *(f32x4*)(wib + (size_t)row * 16 + 8 * fq) = x1 * 0.03125f; *(f32x4*)(wib + (size_t)row * 16 + 8 * fq + 4) = x2 * 0.03125f;
;                     }
.LBB0_677:
	s_and_b64 vcc, exec, s[2:3]
	s_mov_b64 s[4:5], -1
	s_cbranch_vccnz .LBB0_689
	s_andn2_b64 vcc, exec, s[82:83]
	s_cbranch_vccnz .LBB0_686
	v_mul_f32_e64 v18, v158, v20
	v_mul_f32_e64 v19, v159, v20
	v_mul_f32_e64 v24, v156, v20
	v_mul_f32_e64 v25, v157, v20
	v_mul_f32_e64 v16, v150, v20
	v_mul_f32_e64 v17, v151, v20
	v_mul_f32_e64 v22, v148, v20
	v_mul_f32_e64 v23, v149, v20
	s_andn2_b64 vcc, exec, s[34:35]
	s_cbranch_vccnz .LBB0_683
	s_and_saveexec_b64 s[4:5], s[88:89]
	s_cbranch_execz .LBB0_682
	v_ashrrev_i32_e32 v49, 31, v48
	v_readlane_b32 s36, v249, 56
	v_lshlrev_b64 v[30:31], 6, v[48:49]
	v_readlane_b32 s37, v249, 57
	v_mul_f32_e64 v28, v18, s38
	v_mul_f32_e64 v29, v19, s38
	v_mul_f32_e64 v26, v24, s38
	v_mul_f32_e64 v27, v25, s38
	v_lshl_add_u64 v[30:31], s[36:37], 0, v[30:31]
	v_lshl_add_u64 v[30:31], v[38:39], 2, v[30:31]
	global_store_dwordx4 v[30:31], v[26:29], off
	s_nop 1
	v_mul_f32_e64 v28, v16, s38
	v_mul_f32_e64 v29, v17, s38
	v_mul_f32_e64 v26, v22, s38
	v_mul_f32_e64 v27, v23, s38
	global_store_dwordx4 v[30:31], v[26:29], off offset:16

;     __device__ __forceinline__ void operator()(const f32x4 (&acc)[2][2][4][2], const Unit& u, int wr, int wc, int fr, int fq, const Pre&) const {
;     ...
;                 } else if (kind == KD_V) {
; #pragma unroll
;                     for (int bj = 0; bj < 2; ++bj) st_bf16x8(vb + (size_t)row * 512 + 256 * (pn - TL_V) + 128 * bj + cw, acc[ai][bj][m][0] * rs, acc[ai][bj][m][1] * rs);
.LBB0_686:
	s_andn2_b64 vcc, exec, s[4:5]
	s_cbranch_vccnz .LBB0_688
	v_ashrrev_i32_e32 v49, 31, v48
	v_readlane_b32 s4, v249, 52
	v_lshlrev_b64 v[16:17], 10, v[48:49]
	v_readlane_b32 s5, v249, 53
	v_mul_f32_e64 v18, v158, v20
	v_mul_f32_e64 v19, v159, v20
	v_mul_f32_e64 v24, v150, v20
	v_mul_f32_e64 v25, v151, v20
	v_lshl_add_u64 v[16:17], s[4:5], 0, v[16:17]
	v_lshl_add_u64 v[16:17], s[86:87], 1, v[16:17]
	v_lshl_add_u64 v[22:23], v[36:37], 1, v[16:17]
	v_mul_f32_e64 v16, v156, v20
	v_mul_f32_e64 v17, v157, v20
	v_mul_f32_e64 v26, v148, v20
	v_mul_f32_e64 v27, v149, v20
	v_cvt_pk_bf16_f32 v16, v16, v17
	v_cvt_pk_bf16_f32 v17, v18, v19
	s_nop 0
	v_cvt_pk_bf16_f32 v18, v26, v27
	v_cvt_pk_bf16_f32 v19, v24, v25
	global_store_dwordx4 v[22:23], v[16:19], off
	v_mul_f32_e64 v24, v146, v20
	v_mul_f32_e64 v25, v147, v20
	v_mul_f32_e64 v26, v144, v20
	v_mul_f32_e64 v27, v145, v20
	v_mul_f32_e64 v18, v154, v20
	v_mul_f32_e64 v19, v155, v20
	v_mul_f32_e64 v16, v152, v20
	v_mul_f32_e64 v17, v153, v20
	s_nop 0
	v_cvt_pk_bf16_f32 v16, v16, v17
	v_cvt_pk_bf16_f32 v17, v18, v19
	v_cvt_pk_bf16_f32 v18, v26, v27
	v_cvt_pk_bf16_f32 v19, v24, v25
	global_store_dwordx4 v[22:23], v[16:19], off offset:256

;     __device__ __forceinline__ void operator()(const f32x4 (&acc)[2][2][4][2], const Unit& u, int wr, int wc, int fr, int fq, const Pre&) const {
;     ...
;                 } else if (kind == KD_Q || kind == KD_K) {
;                     bf16_t* o = (kind == KD_Q) ? qb + (size_t)row * DM + 256 * (pn - TL_Q) + cw : kb + (size_t)row * 512 + 256 * (pn - TL_K) + cw;
; #pragma unroll
;                     for (int bj = 0; bj < 2; ++bj) {
;                         const f32x4 x1 = acc[ai][bj][m][0] * rs, x2 = acc[ai][bj][m][1] * rs;
;                         if (rotqk) st_bf16x8(o + 128 * bj, x1 * cs[q] - x2 * sn[q], x2 * cs[q] + x1 * sn[q]);
;                         else st_bf16x8(o + 128 * bj, x1, x2);
;                     }
.LBB0_689:
	s_andn2_b64 vcc, exec, s[4:5]
	s_cbranch_vccnz .LBB0_699
	v_cndmask_b32_e64 v16, 0, 1, s[78:79]
	v_mul_f32_e64 v22, v158, v20
	v_mul_f32_e64 v23, v159, v20
	v_mul_f32_e64 v24, v156, v20
	v_mul_f32_e64 v25, v157, v20
	v_mul_f32_e64 v26, v150, v20
	v_mul_f32_e64 v27, v151, v20
	v_mul_f32_e64 v28, v148, v20
	v_mul_f32_e64 v29, v149, v20
	v_cmp_ne_u32_e64 s[4:5], 1, v16
	s_andn2_b64 vcc, exec, s[78:79]
	s_mov_b64 s[36:37], -1
	s_cbranch_vccnz .LBB0_692
	s_mov_b64 s[36:37], 0
	v_cvt_pk_bf16_f32 v16, v24, v25
	v_cvt_pk_bf16_f32 v17, v22, v23
	v_cvt_pk_bf16_f32 v18, v28, v29
	v_cvt_pk_bf16_f32 v19, v26, v27
.LBB0_692:
	s_andn2_b64 vcc, exec, s[36:37]
	s_cbranch_vccnz .LBB0_694
	v_mul_f32_e64 v16, v26, v10
	v_mul_f32_e64 v17, v27, v11
	v_mul_f32_e64 v18, v28, v8
	v_mul_f32_e64 v19, v29, v9
	v_fma_f32 v30, v22, v14, -v16
	v_fma_f32 v31, v23, v15, -v17
	v_fma_f32 v16, v24, v12, -v18
	v_fma_f32 v17, v25, v13, -v19
	v_mul_f32_e64 v18, v26, v14
	v_mul_f32_e64 v19, v27, v15
	v_mul_f32_e64 v26, v28, v12
	v_mul_f32_e64 v27, v29, v13
	v_fma_f32 v22, v22, v10, v18
	v_fma_f32 v23, v23, v11, v19
	v_fma_f32 v18, v24, v8, v26
	v_fma_f32 v19, v25, v9, v27
	v_cvt_pk_bf16_f32 v16, v16, v17
	v_cvt_pk_bf16_f32 v17, v30, v31
	s_nop 0
	v_cvt_pk_bf16_f32 v18, v18, v19
	v_cvt_pk_bf16_f32 v19, v22, v23
.LBB0_694:
	s_and_b64 s[36:37], s[80:81], exec
	v_readlane_b32 s36, v249, 49
	v_readlane_b32 s37, v249, 51
	v_ashrrev_i32_e32 v49, 31, v48
	s_cselect_b32 s37, s36, s37
	v_readlane_b32 s36, v249, 48
	v_readlane_b32 s92, v249, 50
	s_cselect_b32 vcc_lo, 12, 10
	s_cselect_b32 s36, s36, s92
	v_lshlrev_b64 v[22:23], vcc_lo, v[48:49]
	s_cselect_b32 s93, s54, s45
	s_cselect_b32 s92, s8, s57
	v_lshl_add_u64 v[22:23], s[36:37], 0, v[22:23]
	v_lshl_add_u64 v[22:23], s[92:93], 1, v[22:23]
	v_lshl_add_u64 v[22:23], v[36:37], 1, v[22:23]
	v_mov_b32_e32 v21, v20
	global_store_dwordx4 v[22:23], v[16:19], off
	v_mul_f32_e64 v26, v152, v20
	v_mul_f32_e64 v27, v153, v21
	v_mul_f32_e64 v30, v144, v20
	v_mul_f32_e64 v31, v145, v21
	v_mov_b32_e32 v16, v20
	v_mov_b32_e32 v17, v20
	v_mul_f32_e64 v24, v154, v16
	v_mul_f32_e64 v25, v155, v17
	v_mul_f32_e64 v28, v146, v16
	v_mul_f32_e64 v29, v147, v17
	s_and_b64 vcc, exec, s[4:5]
	s_mov_b64 s[4:5], -1
	s_cbranch_vccnz .LBB0_696
	s_mov_b64 s[4:5], 0
	v_cvt_pk_bf16_f32 v16, v26, v27
	v_cvt_pk_bf16_f32 v17, v24, v25
	v_cvt_pk_bf16_f32 v18, v30, v31
	v_cvt_pk_bf16_f32 v19, v28, v29
.LBB0_696:
	s_andn2_b64 vcc, exec, s[4:5]
	s_cbranch_vccnz .LBB0_698
	v_mul_f32_e64 v16, v28, v10
	v_mul_f32_e64 v17, v29, v11
	v_mul_f32_e64 v18, v30, v8
	v_mul_f32_e64 v19, v31, v9
	v_fma_f32 v32, v24, v14, -v16
	v_fma_f32 v33, v25, v15, -v17
	v_fma_f32 v16, v26, v12, -v18
	v_fma_f32 v17, v27, v13, -v19
	v_mul_f32_e64 v14, v28, v14
	v_mul_f32_e64 v15, v29, v15
	v_mul_f32_e64 v12, v30, v12
	v_mul_f32_e64 v13, v31, v13
	v_fma_f32 v10, v24, v10, v14
	v_fma_f32 v11, v25, v11, v15
	v_fma_f32 v8, v26, v8, v12
	v_fma_f32 v9, v27, v9, v13
	v_cvt_pk_bf16_f32 v16, v16, v17
	v_cvt_pk_bf16_f32 v17, v32, v33
	s_nop 0
	v_cvt_pk_bf16_f32 v18, v8, v9
	v_cvt_pk_bf16_f32 v19, v10, v11

; __device__ __forceinline__ f32x4 sigmoid4(const f32x4& x, float s) {
;     f32x4 z = x * (s * -1.4426950408889634f), e;
; #pragma unroll
;     for (int j = 0; j < 4; ++j) e[j] = __builtin_amdgcn_exp2f(z[j]);
;     e = e + 1.0f;
; #pragma unroll
;     for (int j = 0; j < 4; ++j) e[j] = __builtin_amdgcn_rcpf(e[j]);
;     return e;
; }
;     __device__ __forceinline__ void operator()(const f32x4 (&acc)[2][2][4][2], const Unit& u, int wr, int wc, int fr, int fq, const Pre&) const {
;     ...
; #pragma unroll
;             for (int m = 0; m < 4; ++m) {
;                 const int row = rowb + ai * 128 + m * 16, q = m;
;                 const float rs = rsv[ai * 4 + m];
;                 if (kind == KD_KVX) {
;                     bf16_t* o = (pn < 2 ? kx : vx) + (size_t)row * 512 + 256 * (pn & 1) + cw;
; #pragma unroll
;                     for (int bj = 0; bj < 2; ++bj) st_bf16x8(o + 128 * bj, acc[ai][bj][m][0] * rs, acc[ai][bj][m][1] * rs);
;                 } else if (kind == KD_A) {
;                     st_bf16x8(abuf + (size_t)row * DM + 128 * (pn - TL_A) + cw, acc[ai][0][m][0] * rs * sigmoid4(acc[ai][1][m][0], rs), acc[ai][0][m][1] * rs * sigmoid4(acc[ai][1][m][1], rs));
;                 } else if (kind == KD_P) {
;                     const float r2 = rs * rs;
;                     st_bf16x8(pbuf + (size_t)row * DM + 128 * (pn - TL_P) + cw, acc[ai][0][m][0] * acc[ai][1][m][0] * r2, acc[ai][0][m][1] * acc[ai][1][m][1] * r2);
;                 } else if (kind == KD_G) {
; #pragma unroll
;                     for (int bj = 0; bj < 2; ++bj)
;                         st_bf16x8(gabuf + (size_t)row * DM + 256 * (pn - TL_G) + 128 * bj + cw, sigmoid4(acc[ai][bj][m][0], rs), sigmoid4(acc[ai][bj][m][1], rs));
.LBB0_703:
	v_ashrrev_i32_e32 v49, 31, v48
	v_lshlrev_b64 v[8:9], 12, v[48:49]
	v_lshl_add_u64 v[8:9], s[12:13], 0, v[8:9]
	v_lshl_add_u64 v[8:9], s[76:77], 1, v[8:9]
	v_mul_f32_e32 v19, 0xbfb8aa3b, v20
	v_lshl_add_u64 v[12:13], v[36:37], 1, v[8:9]
	v_mul_f32_e32 v8, v152, v19
	v_mul_f32_e32 v9, v153, v19
	v_mul_f32_e32 v10, v154, v19
	v_mul_f32_e32 v11, v155, v19
	v_exp_f32_e32 v8, v8
	v_exp_f32_e32 v10, v10
	v_exp_f32_e32 v11, v11
	v_exp_f32_e32 v9, v9
	v_mul_f32_e64 v14, v158, v20
	v_mul_f32_e64 v15, v159, v20
	v_mul_f32_e64 v16, v156, v20
	v_mul_f32_e64 v17, v157, v20
	v_add_f32_e64 v10, v10, 1.0
	v_add_f32_e64 v11, v11, 1.0
	v_add_f32_e64 v8, v8, 1.0
	v_add_f32_e64 v9, v9, 1.0
	v_mul_f32_e32 v18, v144, v19
	v_mul_f32_e32 v21, v145, v19
	v_mul_f32_e32 v22, v146, v19
	v_mul_f32_e32 v19, v147, v19
	v_rcp_f32_e32 v8, v8
	v_rcp_f32_e32 v9, v9
	v_rcp_f32_e32 v10, v10
	v_rcp_f32_e32 v11, v11
	v_exp_f32_e32 v18, v18
	v_exp_f32_e32 v22, v22
	v_exp_f32_e32 v23, v19
	v_exp_f32_e32 v19, v21
	v_mul_f32_e64 v10, v14, v10
	v_mul_f32_e64 v11, v15, v11
	v_mul_f32_e64 v8, v16, v8
	v_mul_f32_e64 v9, v17, v9
	v_add_f32_e64 v14, v22, 1.0
	v_add_f32_e64 v15, v23, 1.0
	v_add_f32_e64 v16, v18, 1.0
	v_add_f32_e64 v17, v19, 1.0
	v_rcp_f32_e32 v14, v14
	v_rcp_f32_e32 v16, v16
	v_rcp_f32_e32 v15, v15
	v_rcp_f32_e32 v17, v17
	v_mul_f32_e64 v18, v150, v20
	v_mul_f32_e64 v19, v151, v20
	v_mul_f32_e64 v21, v149, v20
	v_mul_f32_e64 v20, v148, v20
	v_mul_f32_e64 v14, v18, v14
	v_mul_f32_e64 v15, v19, v15
	v_mul_f32_e64 v16, v20, v16
	v_mul_f32_e64 v17, v21, v17
	v_cvt_pk_bf16_f32 v8, v8, v9
	v_cvt_pk_bf16_f32 v9, v10, v11
	s_nop 0
	v_cvt_pk_bf16_f32 v10, v16, v17
	v_cvt_pk_bf16_f32 v11, v14, v15
	global_store_dwordx4 v[12:13], v[8:11], off
.LBB0_704:
	v_mul_f32_e32 v12, 0x3c800000, v226
	s_mov_b64 s[92:93], -1
	s_mov_b64 s[4:5], 0
	s_cmp_lt_i32 s55, 1
	s_mov_b64 s[36:37], 0
	s_cbranch_scc1 .LBB0_738
	s_cmp_gt_i32 s55, 1
	s_cbranch_scc0 .LBB0_709
	s_cmp_eq_u32 s55, 2
	s_mov_b64 s[36:37], -1
	s_cbranch_scc0 .LBB0_708
	v_ashrrev_i32_e32 v47, 31, v46
	v_readlane_b32 s36, v249, 46
	v_lshlrev_b64 v[8:9], 12, v[46:47]
	v_readlane_b32 s37, v249, 47
	v_mul_f32_e32 v13, 0xbfb8aa3b, v12
	v_mul_f32_e32 v10, v142, v13
	v_lshl_add_u64 v[8:9], s[36:37], 0, v[8:9]
	v_lshl_add_u64 v[8:9], s[90:91], 1, v[8:9]
	v_mul_f32_e32 v11, v143, v13
	v_lshl_add_u64 v[14:15], v[36:37], 1, v[8:9]
	v_mul_f32_e32 v8, v140, v13
	v_mul_f32_e32 v9, v141, v13
	v_exp_f32_e32 v10, v10
	v_exp_f32_e32 v11, v11
	v_exp_f32_e32 v8, v8
	v_exp_f32_e32 v9, v9
	s_mov_b64 s[36:37], 0
	v_add_f32_e64 v10, v10, 1.0
	v_add_f32_e64 v11, v11, 1.0
	v_add_f32_e64 v8, v8, 1.0
	v_add_f32_e64 v9, v9, 1.0
	v_rcp_f32_e32 v18, v10
	v_rcp_f32_e32 v19, v11
	v_mul_f32_e32 v10, v134, v13
	v_mul_f32_e32 v11, v135, v13
	v_rcp_f32_e32 v16, v8
	v_rcp_f32_e32 v17, v9
	v_mul_f32_e32 v8, v132, v13
	v_mul_f32_e32 v9, v133, v13
	v_exp_f32_e32 v10, v10
	v_exp_f32_e32 v11, v11
	v_exp_f32_e32 v8, v8
	v_exp_f32_e32 v9, v9
	v_add_f32_e64 v10, v10, 1.0
	v_add_f32_e64 v11, v11, 1.0
	s_nop 0
	v_rcp_f32_e32 v11, v11
	v_add_f32_e64 v8, v8, 1.0
	v_add_f32_e64 v9, v9, 1.0
	v_rcp_f32_e32 v22, v10
	v_rcp_f32_e32 v20, v8
	v_rcp_f32_e32 v21, v9
	v_cvt_pk_bf16_f32 v8, v16, v17
	v_cvt_pk_bf16_f32 v9, v18, v19
	v_cvt_pk_bf16_f32 v10, v20, v21
	v_cvt_pk_bf16_f32 v11, v22, v11
	global_store_dwordx4 v[14:15], v[8:11], off
	s_nop 1
	v_mul_f32_e32 v10, v138, v13
	v_mul_f32_e32 v11, v139, v13
	v_mul_f32_e32 v8, v136, v13
	v_mul_f32_e32 v9, v137, v13
	v_exp_f32_e32 v10, v10
	v_exp_f32_e32 v11, v11
	v_exp_f32_e32 v8, v8
	v_exp_f32_e32 v9, v9
	v_add_f32_e64 v10, v10, 1.0
	v_add_f32_e64 v11, v11, 1.0
	s_nop 0
	v_rcp_f32_e32 v18, v10
	v_add_f32_e64 v8, v8, 1.0
	v_add_f32_e64 v9, v9, 1.0
	v_rcp_f32_e32 v19, v11
	v_mul_f32_e32 v10, v130, v13
	v_mul_f32_e32 v11, v131, v13
	v_rcp_f32_e32 v16, v8
	v_rcp_f32_e32 v17, v9
	v_mul_f32_e32 v8, v128, v13
	v_mul_f32_e32 v9, v129, v13
	v_exp_f32_e32 v10, v10
	v_exp_f32_e32 v11, v11
	v_exp_f32_e32 v8, v8
	v_exp_f32_e32 v9, v9
	v_add_f32_e64 v10, v10, 1.0
	v_add_f32_e64 v11, v11, 1.0
	s_nop 0
	v_rcp_f32_e32 v11, v11
	v_add_f32_e64 v8, v8, 1.0
	v_add_f32_e64 v9, v9, 1.0
	v_rcp_f32_e32 v21, v10
	v_rcp_f32_e32 v13, v8
	v_rcp_f32_e32 v20, v9
	v_cvt_pk_bf16_f32 v8, v16, v17
	v_cvt_pk_bf16_f32 v9, v18, v19
	v_cvt_pk_bf16_f32 v10, v13, v20
	v_cvt_pk_bf16_f32 v11, v21, v11
	global_store_dwordx4 v[14:15], v[8:11], off offset:256

;     __device__ __forceinline__ void operator()(const f32x4 (&acc)[2][2][4][2], const Unit& u, int wr, int wc, int fr, int fq, const Pre&) const {
;     ...
;                 } else if (kind == KD_P) {
;                     const float r2 = rs * rs;
;                     st_bf16x8(pbuf + (size_t)row * DM + 128 * (pn - TL_P) + cw, acc[ai][0][m][0] * acc[ai][1][m][0] * r2, acc[ai][0][m][1] * acc[ai][1][m][1] * r2);
.LBB0_709:
	s_and_b64 vcc, exec, s[92:93]
	s_cbranch_vccz .LBB0_711
	v_ashrrev_i32_e32 v47, 31, v46
	v_readlane_b32 s50, v249, 44
	v_lshlrev_b64 v[10:11], 12, v[46:47]
	v_readlane_b32 s51, v249, 45
	v_mul_f32_e32 v8, v12, v12
	v_mul_f32_e64 v16, v140, v136
	v_mul_f32_e64 v17, v141, v137
	v_lshl_add_u64 v[10:11], s[50:51], 0, v[10:11]
	v_lshl_add_u64 v[10:11], s[84:85], 1, v[10:11]
	v_lshl_add_u64 v[14:15], v[36:37], 1, v[10:11]
	v_mul_f32_e64 v10, v142, v138
	v_mul_f32_e64 v11, v143, v139
	v_mul_f32_e64 v18, v134, v130
	v_mul_f32_e64 v19, v135, v131
	v_mul_f32_e64 v10, v10, v8
	v_mul_f32_e64 v11, v11, v8
	v_mul_f32_e64 v20, v132, v128
	v_mul_f32_e64 v21, v133, v129
	v_mul_f32_e64 v16, v16, v8
	v_mul_f32_e64 v17, v17, v8
	v_mul_f32_e64 v18, v18, v8
	v_mul_f32_e64 v19, v19, v8
	v_mul_f32_e64 v20, v20, v8
	v_mul_f32_e64 v21, v21, v8
	v_cvt_pk_bf16_f32 v8, v16, v17
	v_cvt_pk_bf16_f32 v9, v10, v11
	s_nop 0
	v_cvt_pk_bf16_f32 v10, v20, v21
	v_cvt_pk_bf16_f32 v11, v18, v19
	global_store_dwordx4 v[14:15], v[8:11], off

;     __device__ __forceinline__ void operator()(const f32x4 (&acc)[2][2][4][2], const Unit& u, int wr, int wc, int fr, int fq, const Pre&) const {
;     ...
;                 } else {
;                     const f32x4 x1 = acc[ai][0][m][0] * rs, x2 = acc[ai][0][m][1] * rs;
;                     if (wc < 2) {
;                         if (roti) st_bf16x8(kib + (size_t)row * 64 + cw, x1 * cs[q] - x2 * sn[q], x2 * cs[q] + x1 * sn[q]);
;                         else st_bf16x8(kib + (size_t)row * 64 + cw, x1, x2);
;                     } else if (wc == 2 && fq < 2) {
;                         *(f32x4*)(wib + (size_t)row * 16 + 8 * fq) = x1 * 0.03125f; *(f32x4*)(wib + (size_t)row * 16 + 8 * fq + 4) = x2 * 0.03125f;
;                     }
.LBB0_713:
	s_and_b64 vcc, exec, s[2:3]
	s_mov_b64 s[4:5], -1
	s_cbranch_vccnz .LBB0_725
	s_andn2_b64 vcc, exec, s[82:83]
	s_cbranch_vccnz .LBB0_722
	v_mul_f32_e64 v10, v142, v12
	v_mul_f32_e64 v11, v143, v12
	v_mul_f32_e64 v16, v140, v12
	v_mul_f32_e64 v17, v141, v12
	v_mul_f32_e64 v8, v134, v12
	v_mul_f32_e64 v9, v135, v12
	v_mul_f32_e64 v14, v132, v12
	v_mul_f32_e64 v15, v133, v12
	s_andn2_b64 vcc, exec, s[34:35]
	s_cbranch_vccnz .LBB0_719
	s_and_saveexec_b64 s[4:5], s[88:89]
	s_cbranch_execz .LBB0_718
	v_ashrrev_i32_e32 v47, 31, v46
	v_readlane_b32 s36, v249, 56
	v_lshlrev_b64 v[22:23], 6, v[46:47]
	v_readlane_b32 s37, v249, 57
	v_mul_f32_e64 v20, v10, s38
	v_mul_f32_e64 v21, v11, s38
	v_mul_f32_e64 v18, v16, s38
	v_mul_f32_e64 v19, v17, s38
	v_lshl_add_u64 v[22:23], s[36:37], 0, v[22:23]
	v_lshl_add_u64 v[22:23], v[38:39], 2, v[22:23]
	global_store_dwordx4 v[22:23], v[18:21], off
	s_nop 1
	v_mul_f32_e64 v20, v8, s38
	v_mul_f32_e64 v21, v9, s38
	v_mul_f32_e64 v18, v14, s38
	v_mul_f32_e64 v19, v15, s38
	global_store_dwordx4 v[22:23], v[18:21], off offset:16

;     __device__ __forceinline__ void operator()(const f32x4 (&acc)[2][2][4][2], const Unit& u, int wr, int wc, int fr, int fq, const Pre&) const {
;     ...
;                 } else if (kind == KD_V) {
; #pragma unroll
;                     for (int bj = 0; bj < 2; ++bj) st_bf16x8(vb + (size_t)row * 512 + 256 * (pn - TL_V) + 128 * bj + cw, acc[ai][bj][m][0] * rs, acc[ai][bj][m][1] * rs);
.LBB0_722:
	s_andn2_b64 vcc, exec, s[4:5]
	s_cbranch_vccnz .LBB0_724
	v_ashrrev_i32_e32 v47, 31, v46
	v_readlane_b32 s4, v249, 52
	v_lshlrev_b64 v[8:9], 10, v[46:47]
	v_readlane_b32 s5, v249, 53
	v_mul_f32_e64 v10, v142, v12
	v_mul_f32_e64 v11, v143, v12
	v_mul_f32_e64 v16, v134, v12
	v_mul_f32_e64 v17, v135, v12
	v_lshl_add_u64 v[8:9], s[4:5], 0, v[8:9]
	v_lshl_add_u64 v[8:9], s[86:87], 1, v[8:9]
	v_lshl_add_u64 v[14:15], v[36:37], 1, v[8:9]
	v_mul_f32_e64 v8, v140, v12
	v_mul_f32_e64 v9, v141, v12
	v_mul_f32_e64 v18, v132, v12
	v_mul_f32_e64 v19, v133, v12
	v_cvt_pk_bf16_f32 v8, v8, v9
	v_cvt_pk_bf16_f32 v9, v10, v11
	s_nop 0
	v_cvt_pk_bf16_f32 v10, v18, v19
	v_cvt_pk_bf16_f32 v11, v16, v17
	global_store_dwordx4 v[14:15], v[8:11], off
	v_mul_f32_e64 v16, v130, v12
	v_mul_f32_e64 v17, v131, v12
	v_mul_f32_e64 v18, v128, v12
	v_mul_f32_e64 v19, v129, v12
	v_mul_f32_e64 v10, v138, v12
	v_mul_f32_e64 v11, v139, v12
	v_mul_f32_e64 v8, v136, v12
	v_mul_f32_e64 v9, v137, v12
	s_nop 0
	v_cvt_pk_bf16_f32 v8, v8, v9
	v_cvt_pk_bf16_f32 v9, v10, v11
	v_cvt_pk_bf16_f32 v10, v18, v19
	v_cvt_pk_bf16_f32 v11, v16, v17
	global_store_dwordx4 v[14:15], v[8:11], off offset:256

;     __device__ __forceinline__ void operator()(const f32x4 (&acc)[2][2][4][2], const Unit& u, int wr, int wc, int fr, int fq, const Pre&) const {
;     ...
;                 } else if (kind == KD_Q || kind == KD_K) {
;                     bf16_t* o = (kind == KD_Q) ? qb + (size_t)row * DM + 256 * (pn - TL_Q) + cw : kb + (size_t)row * 512 + 256 * (pn - TL_K) + cw;
; #pragma unroll
;                     for (int bj = 0; bj < 2; ++bj) {
;                         const f32x4 x1 = acc[ai][bj][m][0] * rs, x2 = acc[ai][bj][m][1] * rs;
;                         if (rotqk) st_bf16x8(o + 128 * bj, x1 * cs[q] - x2 * sn[q], x2 * cs[q] + x1 * sn[q]);
;                         else st_bf16x8(o + 128 * bj, x1, x2);
;                     }
.LBB0_725:
	s_andn2_b64 vcc, exec, s[4:5]
	s_cbranch_vccnz .LBB0_735
	v_cndmask_b32_e64 v8, 0, 1, s[78:79]
	v_mul_f32_e64 v14, v142, v12
	v_mul_f32_e64 v15, v143, v12
	v_mul_f32_e64 v16, v140, v12
	v_mul_f32_e64 v17, v141, v12
	v_mul_f32_e64 v18, v134, v12
	v_mul_f32_e64 v19, v135, v12
	v_mul_f32_e64 v20, v132, v12
	v_mul_f32_e64 v21, v133, v12
	v_cmp_ne_u32_e64 s[4:5], 1, v8
	s_andn2_b64 vcc, exec, s[78:79]
	s_mov_b64 s[36:37], -1
	s_cbranch_vccnz .LBB0_728
	s_mov_b64 s[36:37], 0
	v_cvt_pk_bf16_f32 v8, v16, v17
	v_cvt_pk_bf16_f32 v9, v14, v15
	v_cvt_pk_bf16_f32 v10, v20, v21
	v_cvt_pk_bf16_f32 v11, v18, v19
.LBB0_728:
	s_andn2_b64 vcc, exec, s[36:37]
	s_cbranch_vccnz .LBB0_730
	v_mul_f32_e64 v8, v18, v2
	v_mul_f32_e64 v9, v19, v3
	v_mul_f32_e64 v10, v20, v0
	v_mul_f32_e64 v11, v21, v1
	v_fma_f32 v22, v14, v6, -v8
	v_fma_f32 v23, v15, v7, -v9
	v_fma_f32 v8, v16, v4, -v10
	v_fma_f32 v9, v17, v5, -v11
	v_mul_f32_e64 v10, v18, v6
	v_mul_f32_e64 v11, v19, v7
	v_mul_f32_e64 v18, v20, v4
	v_mul_f32_e64 v19, v21, v5
	v_fma_f32 v14, v14, v2, v10
	v_fma_f32 v15, v15, v3, v11
	v_fma_f32 v10, v16, v0, v18
	v_fma_f32 v11, v17, v1, v19
	v_cvt_pk_bf16_f32 v8, v8, v9
	v_cvt_pk_bf16_f32 v9, v22, v23
	s_nop 0
	v_cvt_pk_bf16_f32 v10, v10, v11
	v_cvt_pk_bf16_f32 v11, v14, v15
.LBB0_730:
	s_and_b64 s[36:37], s[80:81], exec
	v_readlane_b32 s36, v249, 49
	v_readlane_b32 s37, v249, 51
	v_ashrrev_i32_e32 v47, 31, v46
	s_cselect_b32 s37, s36, s37
	v_readlane_b32 s36, v249, 48
	v_readlane_b32 s92, v249, 50
	s_cselect_b32 vcc_lo, 12, 10
	s_cselect_b32 s36, s36, s92
	v_lshlrev_b64 v[14:15], vcc_lo, v[46:47]
	s_cselect_b32 s93, s54, s45
	s_cselect_b32 s92, s8, s57
	v_lshl_add_u64 v[14:15], s[36:37], 0, v[14:15]
	v_lshl_add_u64 v[14:15], s[92:93], 1, v[14:15]
	v_lshl_add_u64 v[14:15], v[36:37], 1, v[14:15]
	v_mov_b32_e32 v13, v12
	global_store_dwordx4 v[14:15], v[8:11], off
	v_mul_f32_e64 v18, v136, v12
	v_mul_f32_e64 v19, v137, v13
	v_mul_f32_e64 v22, v128, v12
	v_mul_f32_e64 v23, v129, v13
	v_mov_b32_e32 v8, v12
	v_mov_b32_e32 v9, v12
	v_mul_f32_e64 v16, v138, v8
	v_mul_f32_e64 v17, v139, v9
	v_mul_f32_e64 v20, v130, v8
	v_mul_f32_e64 v21, v131, v9
	s_and_b64 vcc, exec, s[4:5]
	s_mov_b64 s[4:5], -1
	s_cbranch_vccnz .LBB0_732
	s_mov_b64 s[4:5], 0
	v_cvt_pk_bf16_f32 v8, v18, v19
	v_cvt_pk_bf16_f32 v9, v16, v17
	v_cvt_pk_bf16_f32 v10, v22, v23
	v_cvt_pk_bf16_f32 v11, v20, v21
.LBB0_732:
	s_andn2_b64 vcc, exec, s[4:5]
	s_cbranch_vccnz .LBB0_734
	v_mul_f32_e64 v8, v20, v2
	v_mul_f32_e64 v9, v21, v3
	v_mul_f32_e64 v10, v22, v0
	v_mul_f32_e64 v11, v23, v1
	v_fma_f32 v24, v16, v6, -v8
	v_fma_f32 v25, v17, v7, -v9
	v_fma_f32 v8, v18, v4, -v10
	v_fma_f32 v9, v19, v5, -v11
	v_mul_f32_e64 v6, v20, v6
	v_mul_f32_e64 v7, v21, v7
	v_mul_f32_e64 v4, v22, v4
	v_mul_f32_e64 v5, v23, v5
	v_fma_f32 v2, v16, v2, v6
	v_fma_f32 v3, v17, v3, v7
	v_fma_f32 v0, v18, v0, v4
	v_fma_f32 v1, v19, v1, v5
	v_cvt_pk_bf16_f32 v8, v8, v9
	v_cvt_pk_bf16_f32 v9, v24, v25
	s_nop 0
	v_cvt_pk_bf16_f32 v10, v0, v1
	v_cvt_pk_bf16_f32 v11, v2, v3

; __device__ __forceinline__ f32x4 sigmoid4(const f32x4& x, float s) {
;     f32x4 z = x * (s * -1.4426950408889634f), e;
; #pragma unroll
;     for (int j = 0; j < 4; ++j) e[j] = __builtin_amdgcn_exp2f(z[j]);
;     e = e + 1.0f;
; #pragma unroll
;     for (int j = 0; j < 4; ++j) e[j] = __builtin_amdgcn_rcpf(e[j]);
;     return e;
; }
;     __device__ __forceinline__ void operator()(const f32x4 (&acc)[2][2][4][2], const Unit& u, int wr, int wc, int fr, int fq, const Pre&) const {
;     ...
;                 } else if (kind == KD_A) {
;                     st_bf16x8(abuf + (size_t)row * DM + 128 * (pn - TL_A) + cw, acc[ai][0][m][0] * rs * sigmoid4(acc[ai][1][m][0], rs), acc[ai][0][m][1] * rs * sigmoid4(acc[ai][1][m][1], rs));
.LBB0_741:
	v_ashrrev_i32_e32 v47, 31, v46
	v_lshlrev_b64 v[0:1], 12, v[46:47]
	v_lshl_add_u64 v[0:1], s[12:13], 0, v[0:1]
	v_lshl_add_u64 v[0:1], s[76:77], 1, v[0:1]
	v_mul_f32_e32 v11, 0xbfb8aa3b, v12
	v_lshl_add_u64 v[4:5], v[36:37], 1, v[0:1]
	v_mul_f32_e32 v0, v136, v11
	v_mul_f32_e32 v1, v137, v11
	v_mul_f32_e32 v2, v138, v11
	v_mul_f32_e32 v3, v139, v11
	v_exp_f32_e32 v0, v0
	v_exp_f32_e32 v2, v2
	v_exp_f32_e32 v3, v3
	v_exp_f32_e32 v1, v1
	v_mul_f32_e64 v6, v142, v12
	v_mul_f32_e64 v7, v143, v12
	v_mul_f32_e64 v8, v140, v12
	v_mul_f32_e64 v9, v141, v12
	v_add_f32_e64 v2, v2, 1.0
	v_add_f32_e64 v3, v3, 1.0
	v_add_f32_e64 v0, v0, 1.0
	v_add_f32_e64 v1, v1, 1.0
	v_mul_f32_e32 v10, v128, v11
	v_mul_f32_e32 v13, v129, v11
	v_mul_f32_e32 v14, v130, v11
	v_mul_f32_e32 v11, v131, v11
	v_rcp_f32_e32 v0, v0
	v_rcp_f32_e32 v1, v1
	v_rcp_f32_e32 v2, v2
	v_rcp_f32_e32 v3, v3
	v_exp_f32_e32 v10, v10
	v_exp_f32_e32 v14, v14
	v_exp_f32_e32 v15, v11
	v_exp_f32_e32 v11, v13
	v_mul_f32_e64 v2, v6, v2
	v_mul_f32_e64 v3, v7, v3
	v_mul_f32_e64 v0, v8, v0
	v_mul_f32_e64 v1, v9, v1
	v_add_f32_e64 v6, v14, 1.0
	v_add_f32_e64 v7, v15, 1.0
	v_add_f32_e64 v8, v10, 1.0
	v_add_f32_e64 v9, v11, 1.0
	v_rcp_f32_e32 v6, v6
	v_rcp_f32_e32 v8, v8
	v_rcp_f32_e32 v7, v7
	v_rcp_f32_e32 v9, v9
	v_mul_f32_e64 v10, v134, v12
	v_mul_f32_e64 v11, v135, v12
	v_mul_f32_e64 v13, v133, v12
	v_mul_f32_e64 v12, v132, v12
	v_mul_f32_e64 v6, v10, v6
	v_mul_f32_e64 v7, v11, v7
	v_mul_f32_e64 v8, v12, v8
	v_mul_f32_e64 v9, v13, v9
	v_cvt_pk_bf16_f32 v0, v0, v1
	v_cvt_pk_bf16_f32 v1, v2, v3
	s_nop 0
	v_cvt_pk_bf16_f32 v2, v8, v9
	v_cvt_pk_bf16_f32 v3, v6, v7
	global_store_dwordx4 v[4:5], v[0:3], off
	v_add_u32_e32 v46, 0x80, v40
	s_andn2_b64 vcc, exec, s[16:17]
	v_ashrrev_i32_e32 v47, 31, v46
	s_cbranch_vccz .LBB0_737

;     __device__ __forceinline__ void operator()(const f32x4 (&acc)[2][2][4][2], const Unit& u, int wr, int wc, int fr, int fq, const Pre&) const {
;     ...
; #pragma unroll
;             for (int m = 0; m < 4; ++m) {
;                 const int row = rowb + ai * 128 + m * 16, q = m;
;                 const float rs = rsv[ai * 4 + m];
;     ...
;                 } else if (kind == KD_G) {
; #pragma unroll
;                     for (int bj = 0; bj < 2; ++bj)
;                         st_bf16x8(gabuf + (size_t)row * DM + 256 * (pn - TL_G) + 128 * bj + cw, sigmoid4(acc[ai][bj][m][0], rs), sigmoid4(acc[ai][bj][m][1], rs));
.LBB0_743:
	v_mul_f32_e32 v42, 0x3c800000, v225
	s_mov_b64 s[36:37], -1
	s_mov_b64 s[4:5], 0
	s_cmp_lt_i32 s55, 1
	s_mov_b64 s[16:17], 0
	s_cbranch_scc1 .LBB0_775
	s_cmp_gt_i32 s55, 1
	s_cbranch_scc0 .LBB0_748
	s_cmp_eq_u32 s55, 2
	s_mov_b64 s[16:17], -1
	s_cbranch_scc0 .LBB0_747
	v_readlane_b32 s16, v249, 46
	v_lshlrev_b64 v[32:33], 12, v[46:47]
	v_readlane_b32 s17, v249, 47
	v_mul_f32_e32 v41, 0xbfb8aa3b, v42
	v_mul_f32_e32 v34, v118, v41
	v_lshl_add_u64 v[32:33], s[16:17], 0, v[32:33]
	v_lshl_add_u64 v[32:33], s[90:91], 1, v[32:33]
	v_mul_f32_e32 v35, v119, v41
	v_lshl_add_u64 v[44:45], v[36:37], 1, v[32:33]
	v_mul_f32_e32 v32, v116, v41
	v_mul_f32_e32 v33, v117, v41
	v_exp_f32_e32 v34, v34
	v_exp_f32_e32 v35, v35
	v_exp_f32_e32 v32, v32
	v_exp_f32_e32 v33, v33
	s_mov_b64 s[16:17], 0
	v_add_f32_e64 v34, v34, 1.0
	v_add_f32_e64 v35, v35, 1.0
	v_add_f32_e64 v32, v32, 1.0
	v_add_f32_e64 v33, v33, 1.0
	v_rcp_f32_e32 v49, v34
	v_rcp_f32_e32 v50, v35
	v_mul_f32_e32 v34, v114, v41
	v_mul_f32_e32 v35, v115, v41
	v_rcp_f32_e32 v43, v32
	v_rcp_f32_e32 v48, v33
	v_mul_f32_e32 v32, v112, v41
	v_mul_f32_e32 v33, v113, v41
	v_exp_f32_e32 v34, v34
	v_exp_f32_e32 v35, v35
	v_exp_f32_e32 v32, v32
	v_exp_f32_e32 v33, v33
	v_add_f32_e64 v34, v34, 1.0
	v_add_f32_e64 v35, v35, 1.0
	s_nop 0
	v_rcp_f32_e32 v35, v35
	v_add_f32_e64 v32, v32, 1.0
	v_add_f32_e64 v33, v33, 1.0
	v_rcp_f32_e32 v53, v34
	v_rcp_f32_e32 v51, v32
	v_rcp_f32_e32 v52, v33
	v_cvt_pk_bf16_f32 v32, v43, v48
	v_cvt_pk_bf16_f32 v33, v49, v50
	v_cvt_pk_bf16_f32 v34, v51, v52
	v_cvt_pk_bf16_f32 v35, v53, v35
	global_store_dwordx4 v[44:45], v[32:35], off
	s_nop 1
	v_mul_f32_e32 v34, v126, v41
	v_mul_f32_e32 v35, v127, v41
	v_mul_f32_e32 v32, v124, v41
	v_mul_f32_e32 v33, v125, v41
	v_exp_f32_e32 v34, v34
	v_exp_f32_e32 v35, v35
	v_exp_f32_e32 v32, v32
	v_exp_f32_e32 v33, v33
	v_add_f32_e64 v34, v34, 1.0
	v_add_f32_e64 v35, v35, 1.0
	s_nop 0
	v_rcp_f32_e32 v49, v34
	v_add_f32_e64 v32, v32, 1.0
	v_add_f32_e64 v33, v33, 1.0
	v_rcp_f32_e32 v50, v35
	v_mul_f32_e32 v34, v122, v41
	v_mul_f32_e32 v35, v123, v41
	v_rcp_f32_e32 v43, v32
	v_rcp_f32_e32 v48, v33
	v_mul_f32_e32 v32, v120, v41
	v_mul_f32_e32 v33, v121, v41
	v_exp_f32_e32 v34, v34
	v_exp_f32_e32 v35, v35
	v_exp_f32_e32 v32, v32
	v_exp_f32_e32 v33, v33
	v_add_f32_e64 v34, v34, 1.0
	v_add_f32_e64 v35, v35, 1.0
	s_nop 0
	v_rcp_f32_e32 v35, v35
	v_add_f32_e64 v32, v32, 1.0
	v_add_f32_e64 v33, v33, 1.0
	v_rcp_f32_e32 v52, v34
	v_rcp_f32_e32 v41, v32
	v_rcp_f32_e32 v51, v33
	v_cvt_pk_bf16_f32 v32, v43, v48
	v_cvt_pk_bf16_f32 v33, v49, v50
	v_cvt_pk_bf16_f32 v34, v41, v51
	v_cvt_pk_bf16_f32 v35, v52, v35
	global_store_dwordx4 v[44:45], v[32:35], off offset:256

;     __device__ __forceinline__ void operator()(const f32x4 (&acc)[2][2][4][2], const Unit& u, int wr, int wc, int fr, int fq, const Pre&) const {
;     ...
;                 } else if (kind == KD_P) {
;                     const float r2 = rs * rs;
;                     st_bf16x8(pbuf + (size_t)row * DM + 128 * (pn - TL_P) + cw, acc[ai][0][m][0] * acc[ai][1][m][0] * r2, acc[ai][0][m][1] * acc[ai][1][m][1] * r2);
.LBB0_748:
	s_and_b64 vcc, exec, s[36:37]
	s_cbranch_vccz .LBB0_750
	v_readlane_b32 s36, v249, 44
	v_lshlrev_b64 v[34:35], 12, v[46:47]
	v_readlane_b32 s37, v249, 45
	v_mul_f32_e32 v32, v42, v42
	v_mul_f32_e64 v48, v116, v124
	v_mul_f32_e64 v49, v117, v125
	v_lshl_add_u64 v[34:35], s[36:37], 0, v[34:35]
	v_lshl_add_u64 v[34:35], s[84:85], 1, v[34:35]
	v_lshl_add_u64 v[44:45], v[36:37], 1, v[34:35]
	v_mul_f32_e64 v34, v118, v126
	v_mul_f32_e64 v35, v119, v127
	v_mul_f32_e64 v50, v114, v122
	v_mul_f32_e64 v51, v115, v123
	v_mul_f32_e64 v34, v34, v32
	v_mul_f32_e64 v35, v35, v32
	v_mul_f32_e64 v52, v112, v120
	v_mul_f32_e64 v53, v113, v121
	v_mul_f32_e64 v48, v48, v32
	v_mul_f32_e64 v49, v49, v32
	v_mul_f32_e64 v50, v50, v32
	v_mul_f32_e64 v51, v51, v32
	v_mul_f32_e64 v52, v52, v32
	v_mul_f32_e64 v53, v53, v32
	v_cvt_pk_bf16_f32 v32, v48, v49
	v_cvt_pk_bf16_f32 v33, v34, v35
	s_nop 0
	v_cvt_pk_bf16_f32 v34, v52, v53
	v_cvt_pk_bf16_f32 v35, v50, v51
	global_store_dwordx4 v[44:45], v[32:35], off

;     __device__ __forceinline__ void operator()(const f32x4 (&acc)[2][2][4][2], const Unit& u, int wr, int wc, int fr, int fq, const Pre&) const {
;     ...
;                 } else {
;                     const f32x4 x1 = acc[ai][0][m][0] * rs, x2 = acc[ai][0][m][1] * rs;
;                     if (wc < 2) {
;                         if (roti) st_bf16x8(kib + (size_t)row * 64 + cw, x1 * cs[q] - x2 * sn[q], x2 * cs[q] + x1 * sn[q]);
;                         else st_bf16x8(kib + (size_t)row * 64 + cw, x1, x2);
;                     } else if (wc == 2 && fq < 2) {
;                         *(f32x4*)(wib + (size_t)row * 16 + 8 * fq) = x1 * 0.03125f; *(f32x4*)(wib + (size_t)row * 16 + 8 * fq + 4) = x2 * 0.03125f;
;                     }
.LBB0_752:
	s_and_b64 vcc, exec, s[2:3]
	s_mov_b64 s[4:5], -1
	s_cbranch_vccnz .LBB0_764
	s_andn2_b64 vcc, exec, s[82:83]
	s_cbranch_vccnz .LBB0_761
	v_mul_f32_e64 v32, v118, v42
	v_mul_f32_e64 v33, v119, v42
	v_mul_f32_e64 v48, v116, v42
	v_mul_f32_e64 v49, v117, v42
	v_mul_f32_e64 v34, v114, v42
	v_mul_f32_e64 v35, v115, v42
	v_mul_f32_e64 v44, v112, v42
	v_mul_f32_e64 v45, v113, v42
	s_andn2_b64 vcc, exec, s[34:35]
	s_cbranch_vccnz .LBB0_758
	s_and_saveexec_b64 s[4:5], s[88:89]
	s_cbranch_execz .LBB0_757
	v_readlane_b32 s16, v249, 56
	v_lshlrev_b64 v[50:51], 6, v[46:47]
	v_readlane_b32 s17, v249, 57
	v_mul_f32_e64 v56, v32, s38
	v_mul_f32_e64 v57, v33, s38
	v_mul_f32_e64 v54, v48, s38
	v_mul_f32_e64 v55, v49, s38
	v_lshl_add_u64 v[50:51], s[16:17], 0, v[50:51]
	v_lshl_add_u64 v[58:59], v[38:39], 2, v[50:51]
	v_mul_f32_e64 v52, v34, s38
	v_mul_f32_e64 v53, v35, s38
	v_mul_f32_e64 v50, v44, s38
	v_mul_f32_e64 v51, v45, s38
	global_store_dwordx4 v[58:59], v[54:57], off
	global_store_dwordx4 v[58:59], v[50:53], off offset:16

;     __device__ __forceinline__ void operator()(const f32x4 (&acc)[2][2][4][2], const Unit& u, int wr, int wc, int fr, int fq, const Pre&) const {
;     ...
;                 } else if (kind == KD_V) {
; #pragma unroll
;                     for (int bj = 0; bj < 2; ++bj) st_bf16x8(vb + (size_t)row * 512 + 256 * (pn - TL_V) + 128 * bj + cw, acc[ai][bj][m][0] * rs, acc[ai][bj][m][1] * rs);
.LBB0_761:
	s_andn2_b64 vcc, exec, s[4:5]
	s_cbranch_vccnz .LBB0_763
	v_readlane_b32 s4, v249, 52
	v_lshlrev_b64 v[32:33], 10, v[46:47]
	v_readlane_b32 s5, v249, 53
	v_mul_f32_e64 v34, v118, v42
	v_mul_f32_e64 v35, v119, v42
	v_mul_f32_e64 v48, v114, v42
	v_mul_f32_e64 v49, v115, v42
	v_lshl_add_u64 v[32:33], s[4:5], 0, v[32:33]
	v_lshl_add_u64 v[32:33], s[86:87], 1, v[32:33]
	v_lshl_add_u64 v[44:45], v[36:37], 1, v[32:33]
	v_mul_f32_e64 v32, v116, v42
	v_mul_f32_e64 v33, v117, v42
	v_mul_f32_e64 v50, v112, v42
	v_mul_f32_e64 v51, v113, v42
	v_cvt_pk_bf16_f32 v32, v32, v33
	v_cvt_pk_bf16_f32 v33, v34, v35
	s_nop 0
	v_cvt_pk_bf16_f32 v34, v50, v51
	v_cvt_pk_bf16_f32 v35, v48, v49
	global_store_dwordx4 v[44:45], v[32:35], off
	v_mul_f32_e64 v48, v122, v42
	v_mul_f32_e64 v49, v123, v42
	v_mul_f32_e64 v50, v120, v42
	v_mul_f32_e64 v51, v121, v42
	v_mul_f32_e64 v34, v126, v42
	v_mul_f32_e64 v35, v127, v42
	v_mul_f32_e64 v32, v124, v42
	v_mul_f32_e64 v33, v125, v42
	s_nop 0
	v_cvt_pk_bf16_f32 v32, v32, v33
	v_cvt_pk_bf16_f32 v33, v34, v35
	v_cvt_pk_bf16_f32 v34, v50, v51
	v_cvt_pk_bf16_f32 v35, v48, v49
	global_store_dwordx4 v[44:45], v[32:35], off offset:256

;     __device__ __forceinline__ void operator()(const f32x4 (&acc)[2][2][4][2], const Unit& u, int wr, int wc, int fr, int fq, const Pre&) const {
;     ...
;                 } else if (kind == KD_Q || kind == KD_K) {
;                     bf16_t* o = (kind == KD_Q) ? qb + (size_t)row * DM + 256 * (pn - TL_Q) + cw : kb + (size_t)row * 512 + 256 * (pn - TL_K) + cw;
; #pragma unroll
;                     for (int bj = 0; bj < 2; ++bj) {
;                         const f32x4 x1 = acc[ai][bj][m][0] * rs, x2 = acc[ai][bj][m][1] * rs;
;                         if (rotqk) st_bf16x8(o + 128 * bj, x1 * cs[q] - x2 * sn[q], x2 * cs[q] + x1 * sn[q]);
;                         else st_bf16x8(o + 128 * bj, x1, x2);
;                     }
.LBB0_764:
	s_andn2_b64 vcc, exec, s[4:5]
	s_cbranch_vccnz .LBB0_774
	v_cndmask_b32_e64 v32, 0, 1, s[78:79]
	v_mul_f32_e64 v44, v118, v42
	v_mul_f32_e64 v45, v119, v42
	v_mul_f32_e64 v48, v116, v42
	v_mul_f32_e64 v49, v117, v42
	v_mul_f32_e64 v50, v114, v42
	v_mul_f32_e64 v51, v115, v42
	v_mul_f32_e64 v52, v112, v42
	v_mul_f32_e64 v53, v113, v42
	v_cmp_ne_u32_e64 s[4:5], 1, v32
	s_andn2_b64 vcc, exec, s[78:79]
	s_mov_b64 s[16:17], -1
	s_cbranch_vccnz .LBB0_767
	s_mov_b64 s[16:17], 0
	v_cvt_pk_bf16_f32 v32, v48, v49
	v_cvt_pk_bf16_f32 v33, v44, v45
	v_cvt_pk_bf16_f32 v34, v52, v53
	v_cvt_pk_bf16_f32 v35, v50, v51
.LBB0_767:
	s_andn2_b64 vcc, exec, s[16:17]
	s_cbranch_vccnz .LBB0_769
	s_waitcnt vmcnt(0)
	v_mul_f32_e64 v32, v50, v26
	v_mul_f32_e64 v33, v51, v27
	v_mul_f32_e64 v34, v52, v24
	v_mul_f32_e64 v35, v53, v25
	v_fma_f32 v54, v44, v30, -v32
	v_fma_f32 v55, v45, v31, -v33
	v_fma_f32 v32, v48, v28, -v34
	v_fma_f32 v33, v49, v29, -v35
	v_mul_f32_e64 v34, v50, v30
	v_mul_f32_e64 v35, v51, v31
	v_mul_f32_e64 v50, v52, v28
	v_mul_f32_e64 v51, v53, v29
	v_fma_f32 v44, v44, v26, v34
	v_fma_f32 v45, v45, v27, v35
	v_fma_f32 v34, v48, v24, v50
	v_fma_f32 v35, v49, v25, v51
	v_cvt_pk_bf16_f32 v32, v32, v33
	v_cvt_pk_bf16_f32 v33, v54, v55
	s_nop 0
	v_cvt_pk_bf16_f32 v34, v34, v35
	v_cvt_pk_bf16_f32 v35, v44, v45
.LBB0_769:
	s_and_b64 s[16:17], s[80:81], exec
	v_readlane_b32 s16, v249, 49
	v_readlane_b32 s17, v249, 51
	s_cselect_b32 s17, s16, s17
	v_readlane_b32 s16, v249, 48
	v_readlane_b32 s36, v249, 50
	s_cselect_b32 s92, 12, 10
	s_cselect_b32 s16, s16, s36
	v_lshlrev_b64 v[44:45], s92, v[46:47]
	s_cselect_b32 s37, s54, s45
	s_cselect_b32 s36, s8, s57
	v_lshl_add_u64 v[44:45], s[16:17], 0, v[44:45]
	v_lshl_add_u64 v[44:45], s[36:37], 1, v[44:45]
	v_lshl_add_u64 v[44:45], v[36:37], 1, v[44:45]
	v_mov_b32_e32 v43, v42
	global_store_dwordx4 v[44:45], v[32:35], off
	v_mul_f32_e64 v50, v124, v42
	v_mul_f32_e64 v51, v125, v43
	v_mul_f32_e64 v54, v120, v42
	v_mul_f32_e64 v55, v121, v43
	v_mov_b32_e32 v32, v42
	v_mov_b32_e32 v33, v42
	v_mul_f32_e64 v48, v126, v32
	v_mul_f32_e64 v49, v127, v33
	v_mul_f32_e64 v52, v122, v32
	v_mul_f32_e64 v53, v123, v33
	s_and_b64 vcc, exec, s[4:5]
	s_mov_b64 s[4:5], -1
	s_cbranch_vccnz .LBB0_771
	s_mov_b64 s[4:5], 0
	v_cvt_pk_bf16_f32 v32, v50, v51
	v_cvt_pk_bf16_f32 v33, v48, v49
	v_cvt_pk_bf16_f32 v34, v54, v55
	v_cvt_pk_bf16_f32 v35, v52, v53
.LBB0_771:
	s_andn2_b64 vcc, exec, s[4:5]
	s_cbranch_vccnz .LBB0_773
	s_waitcnt vmcnt(0)
	v_mul_f32_e64 v32, v52, v26
	v_mul_f32_e64 v33, v53, v27
	v_mul_f32_e64 v34, v54, v24
	v_mul_f32_e64 v35, v55, v25
	v_fma_f32 v56, v48, v30, -v32
	v_fma_f32 v57, v49, v31, -v33
	v_fma_f32 v32, v50, v28, -v34
	v_fma_f32 v33, v51, v29, -v35
	v_mul_f32_e64 v30, v52, v30
	v_mul_f32_e64 v31, v53, v31
	v_mul_f32_e64 v28, v54, v28
	v_mul_f32_e64 v29, v55, v29
	v_fma_f32 v26, v48, v26, v30
	v_fma_f32 v27, v49, v27, v31
	v_fma_f32 v24, v50, v24, v28
	v_fma_f32 v25, v51, v25, v29
	v_cvt_pk_bf16_f32 v32, v32, v33
	v_cvt_pk_bf16_f32 v33, v56, v57
	s_nop 0
	v_cvt_pk_bf16_f32 v34, v24, v25
	v_cvt_pk_bf16_f32 v35, v26, v27

; __device__ __forceinline__ f32x4 sigmoid4(const f32x4& x, float s) {
;     f32x4 z = x * (s * -1.4426950408889634f), e;
; #pragma unroll
;     for (int j = 0; j < 4; ++j) e[j] = __builtin_amdgcn_exp2f(z[j]);
;     e = e + 1.0f;
; #pragma unroll
;     for (int j = 0; j < 4; ++j) e[j] = __builtin_amdgcn_rcpf(e[j]);
;     return e;
; }
;     __device__ __forceinline__ void operator()(const f32x4 (&acc)[2][2][4][2], const Unit& u, int wr, int wc, int fr, int fq, const Pre&) const {
;     ...
;                 } else if (kind == KD_A) {
;                     st_bf16x8(abuf + (size_t)row * DM + 128 * (pn - TL_A) + cw, acc[ai][0][m][0] * rs * sigmoid4(acc[ai][1][m][0], rs), acc[ai][0][m][1] * rs * sigmoid4(acc[ai][1][m][1], rs));
;                 } else if (kind == KD_P) {
;                     const float r2 = rs * rs;
;                     st_bf16x8(pbuf + (size_t)row * DM + 128 * (pn - TL_P) + cw, acc[ai][0][m][0] * acc[ai][1][m][0] * r2, acc[ai][0][m][1] * acc[ai][1][m][1] * r2);
;                 } else if (kind == KD_G) {
; #pragma unroll
;                     for (int bj = 0; bj < 2; ++bj)
;                         st_bf16x8(gabuf + (size_t)row * DM + 256 * (pn - TL_G) + 128 * bj + cw, sigmoid4(acc[ai][bj][m][0], rs), sigmoid4(acc[ai][bj][m][1], rs));
.LBB0_778:
	s_waitcnt vmcnt(0)
	v_lshlrev_b64 v[24:25], 12, v[46:47]
	v_lshl_add_u64 v[24:25], s[12:13], 0, v[24:25]
	v_lshl_add_u64 v[24:25], s[76:77], 1, v[24:25]
	v_mul_f32_e32 v35, 0xbfb8aa3b, v42
	v_lshl_add_u64 v[28:29], v[36:37], 1, v[24:25]
	v_mul_f32_e32 v24, v124, v35
	v_mul_f32_e32 v25, v125, v35
	v_mul_f32_e32 v26, v126, v35
	v_mul_f32_e32 v27, v127, v35
	v_exp_f32_e32 v24, v24
	v_exp_f32_e32 v26, v26
	v_exp_f32_e32 v27, v27
	v_exp_f32_e32 v25, v25
	v_mul_f32_e64 v30, v118, v42
	v_mul_f32_e64 v31, v119, v42
	v_mul_f32_e64 v32, v116, v42
	v_mul_f32_e64 v33, v117, v42
	v_add_f32_e64 v26, v26, 1.0
	v_add_f32_e64 v27, v27, 1.0
	v_add_f32_e64 v24, v24, 1.0
	v_add_f32_e64 v25, v25, 1.0
	v_mul_f32_e32 v34, v120, v35
	v_mul_f32_e32 v41, v121, v35
	v_mul_f32_e32 v43, v122, v35
	v_mul_f32_e32 v35, v123, v35
	v_rcp_f32_e32 v24, v24
	v_rcp_f32_e32 v25, v25
	v_rcp_f32_e32 v26, v26
	v_rcp_f32_e32 v27, v27
	v_exp_f32_e32 v34, v34
	v_exp_f32_e32 v44, v43
	v_exp_f32_e32 v45, v35
	v_exp_f32_e32 v35, v41
	v_mul_f32_e64 v26, v30, v26
	v_mul_f32_e64 v27, v31, v27
	v_mul_f32_e64 v24, v32, v24
	v_mul_f32_e64 v25, v33, v25
	v_add_f32_e64 v30, v44, 1.0
	v_add_f32_e64 v31, v45, 1.0
	v_add_f32_e64 v32, v34, 1.0
	v_add_f32_e64 v33, v35, 1.0
	v_rcp_f32_e32 v30, v30
	v_rcp_f32_e32 v32, v32
	v_rcp_f32_e32 v31, v31
	v_rcp_f32_e32 v33, v33
	v_mul_f32_e64 v34, v114, v42
	v_mul_f32_e64 v35, v115, v42
	v_mul_f32_e64 v43, v113, v42
	v_mul_f32_e64 v42, v112, v42
	v_mul_f32_e64 v30, v34, v30
	v_mul_f32_e64 v31, v35, v31
	v_mul_f32_e64 v32, v42, v32
	v_mul_f32_e64 v33, v43, v33
	v_cvt_pk_bf16_f32 v24, v24, v25
	v_cvt_pk_bf16_f32 v25, v26, v27
	s_nop 0
	v_cvt_pk_bf16_f32 v26, v32, v33
	v_cvt_pk_bf16_f32 v27, v30, v31
	global_store_dwordx4 v[28:29], v[24:27], off
.LBB0_779:
	s_waitcnt vmcnt(0)
	v_add_u32_e32 v30, 0x90, v40
	v_mul_f32_e32 v28, 0x3c800000, v224
	s_mov_b64 s[36:37], -1
	s_mov_b64 s[4:5], 0
	s_cmp_lt_i32 s55, 1
	s_mov_b64 s[16:17], 0
	s_cbranch_scc1 .LBB0_811
	s_cmp_gt_i32 s55, 1
	s_cbranch_scc0 .LBB0_784
	s_cmp_eq_u32 s55, 2
	s_mov_b64 s[16:17], -1
	s_cbranch_scc0 .LBB0_783
	v_ashrrev_i32_e32 v31, 31, v30
	v_readlane_b32 s16, v249, 46
	v_lshlrev_b64 v[24:25], 12, v[30:31]
	v_readlane_b32 s17, v249, 47
	v_mul_f32_e32 v29, 0xbfb8aa3b, v28
	v_mul_f32_e32 v26, v102, v29
	v_lshl_add_u64 v[24:25], s[16:17], 0, v[24:25]
	v_lshl_add_u64 v[24:25], s[90:91], 1, v[24:25]
	v_mul_f32_e32 v27, v103, v29
	v_lshl_add_u64 v[32:33], v[36:37], 1, v[24:25]
	v_mul_f32_e32 v24, v100, v29
	v_mul_f32_e32 v25, v101, v29
	v_exp_f32_e32 v26, v26
	v_exp_f32_e32 v27, v27
	v_exp_f32_e32 v24, v24
	v_exp_f32_e32 v25, v25
	s_mov_b64 s[16:17], 0
	v_add_f32_e64 v26, v26, 1.0
	v_add_f32_e64 v27, v27, 1.0
	v_add_f32_e64 v24, v24, 1.0
	v_add_f32_e64 v25, v25, 1.0
	v_rcp_f32_e32 v35, v26
	v_rcp_f32_e32 v41, v27
	v_mul_f32_e32 v26, v98, v29
	v_mul_f32_e32 v27, v99, v29
	v_rcp_f32_e32 v31, v24
	v_rcp_f32_e32 v34, v25
	v_mul_f32_e32 v24, v96, v29
	v_mul_f32_e32 v25, v97, v29
	v_exp_f32_e32 v26, v26
	v_exp_f32_e32 v27, v27
	v_exp_f32_e32 v24, v24
	v_exp_f32_e32 v25, v25
	v_add_f32_e64 v26, v26, 1.0
	v_add_f32_e64 v27, v27, 1.0
	s_nop 0
	v_rcp_f32_e32 v27, v27
	v_add_f32_e64 v24, v24, 1.0
	v_add_f32_e64 v25, v25, 1.0
	v_rcp_f32_e32 v44, v26
	v_rcp_f32_e32 v42, v24
	v_rcp_f32_e32 v43, v25
	v_cvt_pk_bf16_f32 v24, v31, v34
	v_cvt_pk_bf16_f32 v25, v35, v41
	v_cvt_pk_bf16_f32 v26, v42, v43
	v_cvt_pk_bf16_f32 v27, v44, v27
	global_store_dwordx4 v[32:33], v[24:27], off
	s_nop 1
	v_mul_f32_e32 v26, v110, v29
	v_mul_f32_e32 v27, v111, v29
	v_mul_f32_e32 v24, v108, v29
	v_mul_f32_e32 v25, v109, v29
	v_exp_f32_e32 v26, v26
	v_exp_f32_e32 v27, v27
	v_exp_f32_e32 v24, v24
	v_exp_f32_e32 v25, v25
	v_add_f32_e64 v26, v26, 1.0
	v_add_f32_e64 v27, v27, 1.0
	s_nop 0
	v_rcp_f32_e32 v35, v26
	v_add_f32_e64 v24, v24, 1.0
	v_add_f32_e64 v25, v25, 1.0
	v_rcp_f32_e32 v41, v27
	v_mul_f32_e32 v26, v106, v29
	v_mul_f32_e32 v27, v107, v29
	v_rcp_f32_e32 v31, v24
	v_rcp_f32_e32 v34, v25
	v_mul_f32_e32 v24, v104, v29
	v_mul_f32_e32 v25, v105, v29
	v_exp_f32_e32 v26, v26
	v_exp_f32_e32 v27, v27
	v_exp_f32_e32 v24, v24
	v_exp_f32_e32 v25, v25
	v_add_f32_e64 v26, v26, 1.0
	v_add_f32_e64 v27, v27, 1.0
	s_nop 0
	v_rcp_f32_e32 v27, v27
	v_add_f32_e64 v24, v24, 1.0
	v_add_f32_e64 v25, v25, 1.0
	v_rcp_f32_e32 v43, v26
	v_rcp_f32_e32 v29, v24
	v_rcp_f32_e32 v42, v25
	v_cvt_pk_bf16_f32 v24, v31, v34
	v_cvt_pk_bf16_f32 v25, v35, v41
	v_cvt_pk_bf16_f32 v26, v29, v42
	v_cvt_pk_bf16_f32 v27, v43, v27
	global_store_dwordx4 v[32:33], v[24:27], off offset:256

;     __device__ __forceinline__ void operator()(const f32x4 (&acc)[2][2][4][2], const Unit& u, int wr, int wc, int fr, int fq, const Pre&) const {
;     ...
;                 } else if (kind == KD_P) {
;                     const float r2 = rs * rs;
;                     st_bf16x8(pbuf + (size_t)row * DM + 128 * (pn - TL_P) + cw, acc[ai][0][m][0] * acc[ai][1][m][0] * r2, acc[ai][0][m][1] * acc[ai][1][m][1] * r2);
.LBB0_784:
	s_and_b64 vcc, exec, s[36:37]
	s_cbranch_vccz .LBB0_786
	v_ashrrev_i32_e32 v31, 31, v30
	v_readlane_b32 s36, v249, 44
	v_lshlrev_b64 v[26:27], 12, v[30:31]
	v_readlane_b32 s37, v249, 45
	v_mul_f32_e32 v24, v28, v28
	v_mul_f32_e64 v34, v100, v108
	v_mul_f32_e64 v35, v101, v109
	v_lshl_add_u64 v[26:27], s[36:37], 0, v[26:27]
	v_lshl_add_u64 v[26:27], s[84:85], 1, v[26:27]
	v_lshl_add_u64 v[32:33], v[36:37], 1, v[26:27]
	v_mul_f32_e64 v26, v102, v110
	v_mul_f32_e64 v27, v103, v111
	v_mul_f32_e64 v42, v98, v106
	v_mul_f32_e64 v43, v99, v107
	v_mul_f32_e64 v26, v26, v24
	v_mul_f32_e64 v27, v27, v24
	v_mul_f32_e64 v44, v96, v104
	v_mul_f32_e64 v45, v97, v105
	v_mul_f32_e64 v34, v34, v24
	v_mul_f32_e64 v35, v35, v24
	v_mul_f32_e64 v42, v42, v24
	v_mul_f32_e64 v43, v43, v24
	v_mul_f32_e64 v44, v44, v24
	v_mul_f32_e64 v45, v45, v24
	v_cvt_pk_bf16_f32 v24, v34, v35
	v_cvt_pk_bf16_f32 v25, v26, v27
	s_nop 0
	v_cvt_pk_bf16_f32 v26, v44, v45
	v_cvt_pk_bf16_f32 v27, v42, v43
	global_store_dwordx4 v[32:33], v[24:27], off

;     __device__ __forceinline__ void operator()(const f32x4 (&acc)[2][2][4][2], const Unit& u, int wr, int wc, int fr, int fq, const Pre&) const {
;     ...
;                 } else {
;                     const f32x4 x1 = acc[ai][0][m][0] * rs, x2 = acc[ai][0][m][1] * rs;
;                     if (wc < 2) {
;                         if (roti) st_bf16x8(kib + (size_t)row * 64 + cw, x1 * cs[q] - x2 * sn[q], x2 * cs[q] + x1 * sn[q]);
;                         else st_bf16x8(kib + (size_t)row * 64 + cw, x1, x2);
;                     } else if (wc == 2 && fq < 2) {
;                         *(f32x4*)(wib + (size_t)row * 16 + 8 * fq) = x1 * 0.03125f; *(f32x4*)(wib + (size_t)row * 16 + 8 * fq + 4) = x2 * 0.03125f;
;                     }
.LBB0_788:
	s_and_b64 vcc, exec, s[2:3]
	s_mov_b64 s[4:5], -1
	s_cbranch_vccnz .LBB0_800
	s_andn2_b64 vcc, exec, s[82:83]
	s_cbranch_vccnz .LBB0_797
	v_mul_f32_e64 v26, v102, v28
	v_mul_f32_e64 v27, v103, v28
	v_mul_f32_e64 v34, v100, v28
	v_mul_f32_e64 v35, v101, v28
	v_mul_f32_e64 v24, v98, v28
	v_mul_f32_e64 v25, v99, v28
	v_mul_f32_e64 v32, v96, v28
	v_mul_f32_e64 v33, v97, v28
	s_andn2_b64 vcc, exec, s[34:35]
	s_cbranch_vccnz .LBB0_794
	s_and_saveexec_b64 s[4:5], s[88:89]
	s_cbranch_execz .LBB0_793
	v_ashrrev_i32_e32 v31, 31, v30
	v_readlane_b32 s16, v249, 56
	v_lshlrev_b64 v[46:47], 6, v[30:31]
	v_readlane_b32 s17, v249, 57
	v_mul_f32_e64 v44, v26, s38
	v_mul_f32_e64 v45, v27, s38
	v_mul_f32_e64 v42, v34, s38
	v_mul_f32_e64 v43, v35, s38
	v_lshl_add_u64 v[46:47], s[16:17], 0, v[46:47]
	v_lshl_add_u64 v[46:47], v[38:39], 2, v[46:47]
	global_store_dwordx4 v[46:47], v[42:45], off
	s_nop 1
	v_mul_f32_e64 v44, v24, s38
	v_mul_f32_e64 v45, v25, s38
	v_mul_f32_e64 v42, v32, s38
	v_mul_f32_e64 v43, v33, s38
	global_store_dwordx4 v[46:47], v[42:45], off offset:16

;     __device__ __forceinline__ void operator()(const f32x4 (&acc)[2][2][4][2], const Unit& u, int wr, int wc, int fr, int fq, const Pre&) const {
;     ...
;                 } else if (kind == KD_V) {
; #pragma unroll
;                     for (int bj = 0; bj < 2; ++bj) st_bf16x8(vb + (size_t)row * 512 + 256 * (pn - TL_V) + 128 * bj + cw, acc[ai][bj][m][0] * rs, acc[ai][bj][m][1] * rs);
.LBB0_797:
	s_andn2_b64 vcc, exec, s[4:5]
	s_cbranch_vccnz .LBB0_799
	v_ashrrev_i32_e32 v31, 31, v30
	v_readlane_b32 s4, v249, 52
	v_lshlrev_b64 v[24:25], 10, v[30:31]
	v_readlane_b32 s5, v249, 53
	v_mul_f32_e64 v26, v102, v28
	v_mul_f32_e64 v27, v103, v28
	v_mul_f32_e64 v34, v98, v28
	v_mul_f32_e64 v35, v99, v28
	v_lshl_add_u64 v[24:25], s[4:5], 0, v[24:25]
	v_lshl_add_u64 v[24:25], s[86:87], 1, v[24:25]
	v_lshl_add_u64 v[32:33], v[36:37], 1, v[24:25]
	v_mul_f32_e64 v24, v100, v28
	v_mul_f32_e64 v25, v101, v28
	v_mul_f32_e64 v42, v96, v28
	v_mul_f32_e64 v43, v97, v28
	v_cvt_pk_bf16_f32 v24, v24, v25
	v_cvt_pk_bf16_f32 v25, v26, v27
	s_nop 0
	v_cvt_pk_bf16_f32 v26, v42, v43
	v_cvt_pk_bf16_f32 v27, v34, v35
	global_store_dwordx4 v[32:33], v[24:27], off
	v_mul_f32_e64 v34, v106, v28
	v_mul_f32_e64 v35, v107, v28
	v_mul_f32_e64 v42, v104, v28
	v_mul_f32_e64 v43, v105, v28
	v_mul_f32_e64 v26, v110, v28
	v_mul_f32_e64 v27, v111, v28
	v_mul_f32_e64 v24, v108, v28
	v_mul_f32_e64 v25, v109, v28
	s_nop 0
	v_cvt_pk_bf16_f32 v24, v24, v25
	v_cvt_pk_bf16_f32 v25, v26, v27
	v_cvt_pk_bf16_f32 v26, v42, v43
	v_cvt_pk_bf16_f32 v27, v34, v35
	global_store_dwordx4 v[32:33], v[24:27], off offset:256

;     __device__ __forceinline__ void operator()(const f32x4 (&acc)[2][2][4][2], const Unit& u, int wr, int wc, int fr, int fq, const Pre&) const {
;     ...
;                 } else if (kind == KD_Q || kind == KD_K) {
;                     bf16_t* o = (kind == KD_Q) ? qb + (size_t)row * DM + 256 * (pn - TL_Q) + cw : kb + (size_t)row * 512 + 256 * (pn - TL_K) + cw;
; #pragma unroll
;                     for (int bj = 0; bj < 2; ++bj) {
;                         const f32x4 x1 = acc[ai][bj][m][0] * rs, x2 = acc[ai][bj][m][1] * rs;
;                         if (rotqk) st_bf16x8(o + 128 * bj, x1 * cs[q] - x2 * sn[q], x2 * cs[q] + x1 * sn[q]);
;                         else st_bf16x8(o + 128 * bj, x1, x2);
;                     }
.LBB0_800:
	s_andn2_b64 vcc, exec, s[4:5]
	s_cbranch_vccnz .LBB0_810
	v_cndmask_b32_e64 v24, 0, 1, s[78:79]
	v_mul_f32_e64 v32, v102, v28
	v_mul_f32_e64 v33, v103, v28
	v_mul_f32_e64 v34, v100, v28
	v_mul_f32_e64 v35, v101, v28
	v_mul_f32_e64 v42, v98, v28
	v_mul_f32_e64 v43, v99, v28
	v_mul_f32_e64 v44, v96, v28
	v_mul_f32_e64 v45, v97, v28
	v_cmp_ne_u32_e64 s[4:5], 1, v24
	s_andn2_b64 vcc, exec, s[78:79]
	s_mov_b64 s[16:17], -1
	s_cbranch_vccnz .LBB0_803
	s_mov_b64 s[16:17], 0
	v_cvt_pk_bf16_f32 v24, v34, v35
	v_cvt_pk_bf16_f32 v25, v32, v33
	v_cvt_pk_bf16_f32 v26, v44, v45
	v_cvt_pk_bf16_f32 v27, v42, v43
.LBB0_803:
	s_andn2_b64 vcc, exec, s[16:17]
	s_cbranch_vccnz .LBB0_805
	v_mul_f32_e64 v24, v42, v18
	v_mul_f32_e64 v25, v43, v19
	v_mul_f32_e64 v26, v44, v16
	v_mul_f32_e64 v27, v45, v17
	v_fma_f32 v46, v32, v22, -v24
	v_fma_f32 v47, v33, v23, -v25
	v_fma_f32 v24, v34, v20, -v26
	v_fma_f32 v25, v35, v21, -v27
	v_mul_f32_e64 v26, v42, v22
	v_mul_f32_e64 v27, v43, v23
	v_mul_f32_e64 v42, v44, v20
	v_mul_f32_e64 v43, v45, v21
	v_fma_f32 v32, v32, v18, v26
	v_fma_f32 v33, v33, v19, v27
	v_fma_f32 v26, v34, v16, v42
	v_fma_f32 v27, v35, v17, v43
	v_cvt_pk_bf16_f32 v24, v24, v25
	v_cvt_pk_bf16_f32 v25, v46, v47
	s_nop 0
	v_cvt_pk_bf16_f32 v26, v26, v27
	v_cvt_pk_bf16_f32 v27, v32, v33
.LBB0_805:
	s_and_b64 s[16:17], s[80:81], exec
	v_readlane_b32 s16, v249, 49
	v_readlane_b32 s17, v249, 51
	v_ashrrev_i32_e32 v31, 31, v30
	s_cselect_b32 s17, s16, s17
	v_readlane_b32 s16, v249, 48
	v_readlane_b32 s36, v249, 50
	s_cselect_b32 s92, 12, 10
	s_cselect_b32 s16, s16, s36
	v_lshlrev_b64 v[32:33], s92, v[30:31]
	s_cselect_b32 s37, s54, s45
	s_cselect_b32 s36, s8, s57
	v_lshl_add_u64 v[32:33], s[16:17], 0, v[32:33]
	v_lshl_add_u64 v[32:33], s[36:37], 1, v[32:33]
	v_lshl_add_u64 v[32:33], v[36:37], 1, v[32:33]
	v_mov_b32_e32 v29, v28
	global_store_dwordx4 v[32:33], v[24:27], off
	v_mul_f32_e64 v42, v108, v28
	v_mul_f32_e64 v43, v109, v29
	v_mul_f32_e64 v46, v104, v28
	v_mul_f32_e64 v47, v105, v29
	v_mov_b32_e32 v24, v28
	v_mov_b32_e32 v25, v28
	v_mul_f32_e64 v34, v110, v24
	v_mul_f32_e64 v35, v111, v25
	v_mul_f32_e64 v44, v106, v24
	v_mul_f32_e64 v45, v107, v25
	s_and_b64 vcc, exec, s[4:5]
	s_mov_b64 s[4:5], -1
	s_cbranch_vccnz .LBB0_807
	s_mov_b64 s[4:5], 0
	v_cvt_pk_bf16_f32 v24, v42, v43
	v_cvt_pk_bf16_f32 v25, v34, v35
	v_cvt_pk_bf16_f32 v26, v46, v47
	v_cvt_pk_bf16_f32 v27, v44, v45
.LBB0_807:
	s_andn2_b64 vcc, exec, s[4:5]
	s_cbranch_vccnz .LBB0_809
	v_mul_f32_e64 v24, v44, v18
	v_mul_f32_e64 v25, v45, v19
	v_mul_f32_e64 v26, v46, v16
	v_mul_f32_e64 v27, v47, v17
	v_fma_f32 v48, v34, v22, -v24
	v_fma_f32 v49, v35, v23, -v25
	v_fma_f32 v24, v42, v20, -v26
	v_fma_f32 v25, v43, v21, -v27
	v_mul_f32_e64 v22, v44, v22
	v_mul_f32_e64 v23, v45, v23
	v_mul_f32_e64 v20, v46, v20
	v_mul_f32_e64 v21, v47, v21
	v_fma_f32 v18, v34, v18, v22
	v_fma_f32 v19, v35, v19, v23
	v_fma_f32 v16, v42, v16, v20
	v_fma_f32 v17, v43, v17, v21
	v_cvt_pk_bf16_f32 v24, v24, v25
	v_cvt_pk_bf16_f32 v25, v48, v49
	s_nop 0
	v_cvt_pk_bf16_f32 v26, v16, v17
	v_cvt_pk_bf16_f32 v27, v18, v19

; __device__ __forceinline__ f32x4 sigmoid4(const f32x4& x, float s) {
;     f32x4 z = x * (s * -1.4426950408889634f), e;
; #pragma unroll
;     for (int j = 0; j < 4; ++j) e[j] = __builtin_amdgcn_exp2f(z[j]);
;     e = e + 1.0f;
; #pragma unroll
;     for (int j = 0; j < 4; ++j) e[j] = __builtin_amdgcn_rcpf(e[j]);
;     return e;
; }
;     __device__ __forceinline__ void operator()(const f32x4 (&acc)[2][2][4][2], const Unit& u, int wr, int wc, int fr, int fq, const Pre&) const {
;     ...
;                 } else if (kind == KD_A) {
;                     st_bf16x8(abuf + (size_t)row * DM + 128 * (pn - TL_A) + cw, acc[ai][0][m][0] * rs * sigmoid4(acc[ai][1][m][0], rs), acc[ai][0][m][1] * rs * sigmoid4(acc[ai][1][m][1], rs));
;                 } else if (kind == KD_P) {
;                     const float r2 = rs * rs;
;                     st_bf16x8(pbuf + (size_t)row * DM + 128 * (pn - TL_P) + cw, acc[ai][0][m][0] * acc[ai][1][m][0] * r2, acc[ai][0][m][1] * acc[ai][1][m][1] * r2);
;                 } else if (kind == KD_G) {
; #pragma unroll
;                     for (int bj = 0; bj < 2; ++bj)
;                         st_bf16x8(gabuf + (size_t)row * DM + 256 * (pn - TL_G) + 128 * bj + cw, sigmoid4(acc[ai][bj][m][0], rs), sigmoid4(acc[ai][bj][m][1], rs));
.LBB0_814:
	v_ashrrev_i32_e32 v31, 31, v30
	v_lshlrev_b64 v[16:17], 12, v[30:31]
	v_lshl_add_u64 v[16:17], s[12:13], 0, v[16:17]
	v_lshl_add_u64 v[16:17], s[76:77], 1, v[16:17]
	v_mul_f32_e32 v27, 0xbfb8aa3b, v28
	v_lshl_add_u64 v[20:21], v[36:37], 1, v[16:17]
	v_mul_f32_e32 v16, v108, v27
	v_mul_f32_e32 v17, v109, v27
	v_mul_f32_e32 v18, v110, v27
	v_mul_f32_e32 v19, v111, v27
	v_exp_f32_e32 v16, v16
	v_exp_f32_e32 v18, v18
	v_exp_f32_e32 v19, v19
	v_exp_f32_e32 v17, v17
	v_mul_f32_e64 v22, v102, v28
	v_mul_f32_e64 v23, v103, v28
	v_mul_f32_e64 v24, v100, v28
	v_mul_f32_e64 v25, v101, v28
	v_add_f32_e64 v18, v18, 1.0
	v_add_f32_e64 v19, v19, 1.0
	v_add_f32_e64 v16, v16, 1.0
	v_add_f32_e64 v17, v17, 1.0
	v_mul_f32_e32 v26, v104, v27
	v_mul_f32_e32 v29, v105, v27
	v_mul_f32_e32 v30, v106, v27
	v_mul_f32_e32 v27, v107, v27
	v_rcp_f32_e32 v16, v16
	v_rcp_f32_e32 v17, v17
	v_rcp_f32_e32 v18, v18
	v_rcp_f32_e32 v19, v19
	v_exp_f32_e32 v26, v26
	v_exp_f32_e32 v30, v30
	v_exp_f32_e32 v31, v27
	v_exp_f32_e32 v27, v29
	v_mul_f32_e64 v18, v22, v18
	v_mul_f32_e64 v19, v23, v19
	v_mul_f32_e64 v16, v24, v16
	v_mul_f32_e64 v17, v25, v17
	v_add_f32_e64 v22, v30, 1.0
	v_add_f32_e64 v23, v31, 1.0
	v_add_f32_e64 v24, v26, 1.0
	v_add_f32_e64 v25, v27, 1.0
	v_rcp_f32_e32 v22, v22
	v_rcp_f32_e32 v24, v24
	v_rcp_f32_e32 v23, v23
	v_rcp_f32_e32 v25, v25
	v_mul_f32_e64 v26, v98, v28
	v_mul_f32_e64 v27, v99, v28
	v_mul_f32_e64 v29, v97, v28
	v_mul_f32_e64 v28, v96, v28
	v_mul_f32_e64 v22, v26, v22
	v_mul_f32_e64 v23, v27, v23
	v_mul_f32_e64 v24, v28, v24
	v_mul_f32_e64 v25, v29, v25
	v_cvt_pk_bf16_f32 v16, v16, v17
	v_cvt_pk_bf16_f32 v17, v18, v19
	s_nop 0
	v_cvt_pk_bf16_f32 v18, v24, v25
	v_cvt_pk_bf16_f32 v19, v22, v23
	global_store_dwordx4 v[20:21], v[16:19], off
.LBB0_815:
	v_add_u32_e32 v22, 0xa0, v40
	v_mul_f32_e32 v20, 0x3c800000, v223
	s_mov_b64 s[36:37], -1
	s_mov_b64 s[4:5], 0
	s_cmp_lt_i32 s55, 1
	s_mov_b64 s[16:17], 0
	s_cbranch_scc1 .LBB0_847
	s_cmp_gt_i32 s55, 1
	s_cbranch_scc0 .LBB0_820
	s_cmp_eq_u32 s55, 2
	s_mov_b64 s[16:17], -1
	s_cbranch_scc0 .LBB0_819
	v_ashrrev_i32_e32 v23, 31, v22
	v_readlane_b32 s16, v249, 46
	v_lshlrev_b64 v[16:17], 12, v[22:23]
	v_readlane_b32 s17, v249, 47
	v_mul_f32_e32 v21, 0xbfb8aa3b, v20
	v_mul_f32_e32 v18, v86, v21
	v_lshl_add_u64 v[16:17], s[16:17], 0, v[16:17]
	v_lshl_add_u64 v[16:17], s[90:91], 1, v[16:17]
	v_mul_f32_e32 v19, v87, v21
	v_lshl_add_u64 v[24:25], v[36:37], 1, v[16:17]
	v_mul_f32_e32 v16, v84, v21
	v_mul_f32_e32 v17, v85, v21
	v_exp_f32_e32 v18, v18
	v_exp_f32_e32 v19, v19
	v_exp_f32_e32 v16, v16
	v_exp_f32_e32 v17, v17
	s_mov_b64 s[16:17], 0
	v_add_f32_e64 v18, v18, 1.0
	v_add_f32_e64 v19, v19, 1.0
	v_add_f32_e64 v16, v16, 1.0
	v_add_f32_e64 v17, v17, 1.0
	v_rcp_f32_e32 v27, v18
	v_rcp_f32_e32 v28, v19
	v_mul_f32_e32 v18, v82, v21
	v_mul_f32_e32 v19, v83, v21
	v_rcp_f32_e32 v23, v16
	v_rcp_f32_e32 v26, v17
	v_mul_f32_e32 v16, v80, v21
	v_mul_f32_e32 v17, v81, v21
	v_exp_f32_e32 v18, v18
	v_exp_f32_e32 v19, v19
	v_exp_f32_e32 v16, v16
	v_exp_f32_e32 v17, v17
	v_add_f32_e64 v18, v18, 1.0
	v_add_f32_e64 v19, v19, 1.0
	s_nop 0
	v_rcp_f32_e32 v19, v19
	v_add_f32_e64 v16, v16, 1.0
	v_add_f32_e64 v17, v17, 1.0
	v_rcp_f32_e32 v31, v18
	v_rcp_f32_e32 v29, v16
	v_rcp_f32_e32 v30, v17
	v_cvt_pk_bf16_f32 v16, v23, v26
	v_cvt_pk_bf16_f32 v17, v27, v28
	v_cvt_pk_bf16_f32 v18, v29, v30
	v_cvt_pk_bf16_f32 v19, v31, v19
	global_store_dwordx4 v[24:25], v[16:19], off
	s_nop 1
	v_mul_f32_e32 v18, v94, v21
	v_mul_f32_e32 v19, v95, v21
	v_mul_f32_e32 v16, v92, v21
	v_mul_f32_e32 v17, v93, v21
	v_exp_f32_e32 v18, v18
	v_exp_f32_e32 v19, v19
	v_exp_f32_e32 v16, v16
	v_exp_f32_e32 v17, v17
	v_add_f32_e64 v18, v18, 1.0
	v_add_f32_e64 v19, v19, 1.0
	s_nop 0
	v_rcp_f32_e32 v27, v18
	v_add_f32_e64 v16, v16, 1.0
	v_add_f32_e64 v17, v17, 1.0
	v_rcp_f32_e32 v28, v19
	v_mul_f32_e32 v18, v90, v21
	v_mul_f32_e32 v19, v91, v21
	v_rcp_f32_e32 v23, v16
	v_rcp_f32_e32 v26, v17
	v_mul_f32_e32 v16, v88, v21
	v_mul_f32_e32 v17, v89, v21
	v_exp_f32_e32 v18, v18
	v_exp_f32_e32 v19, v19
	v_exp_f32_e32 v16, v16
	v_exp_f32_e32 v17, v17
	v_add_f32_e64 v18, v18, 1.0
	v_add_f32_e64 v19, v19, 1.0
	s_nop 0
	v_rcp_f32_e32 v19, v19
	v_add_f32_e64 v16, v16, 1.0
	v_add_f32_e64 v17, v17, 1.0
	v_rcp_f32_e32 v30, v18
	v_rcp_f32_e32 v21, v16
	v_rcp_f32_e32 v29, v17
	v_cvt_pk_bf16_f32 v16, v23, v26
	v_cvt_pk_bf16_f32 v17, v27, v28
	v_cvt_pk_bf16_f32 v18, v21, v29
	v_cvt_pk_bf16_f32 v19, v30, v19
	global_store_dwordx4 v[24:25], v[16:19], off offset:256

;     __device__ __forceinline__ void operator()(const f32x4 (&acc)[2][2][4][2], const Unit& u, int wr, int wc, int fr, int fq, const Pre&) const {
;     ...
;                 } else if (kind == KD_P) {
;                     const float r2 = rs * rs;
;                     st_bf16x8(pbuf + (size_t)row * DM + 128 * (pn - TL_P) + cw, acc[ai][0][m][0] * acc[ai][1][m][0] * r2, acc[ai][0][m][1] * acc[ai][1][m][1] * r2);
.LBB0_820:
	s_and_b64 vcc, exec, s[36:37]
	s_cbranch_vccz .LBB0_822
	v_ashrrev_i32_e32 v23, 31, v22
	v_readlane_b32 s36, v249, 44
	v_lshlrev_b64 v[18:19], 12, v[22:23]
	v_readlane_b32 s37, v249, 45
	v_mul_f32_e32 v16, v20, v20
	v_mul_f32_e64 v26, v84, v92
	v_mul_f32_e64 v27, v85, v93
	v_lshl_add_u64 v[18:19], s[36:37], 0, v[18:19]
	v_lshl_add_u64 v[18:19], s[84:85], 1, v[18:19]
	v_lshl_add_u64 v[24:25], v[36:37], 1, v[18:19]
	v_mul_f32_e64 v18, v86, v94
	v_mul_f32_e64 v19, v87, v95
	v_mul_f32_e64 v28, v82, v90
	v_mul_f32_e64 v29, v83, v91
	v_mul_f32_e64 v18, v18, v16
	v_mul_f32_e64 v19, v19, v16
	v_mul_f32_e64 v30, v80, v88
	v_mul_f32_e64 v31, v81, v89
	v_mul_f32_e64 v26, v26, v16
	v_mul_f32_e64 v27, v27, v16
	v_mul_f32_e64 v28, v28, v16
	v_mul_f32_e64 v29, v29, v16
	v_mul_f32_e64 v30, v30, v16
	v_mul_f32_e64 v31, v31, v16
	v_cvt_pk_bf16_f32 v16, v26, v27
	v_cvt_pk_bf16_f32 v17, v18, v19
	s_nop 0
	v_cvt_pk_bf16_f32 v18, v30, v31
	v_cvt_pk_bf16_f32 v19, v28, v29
	global_store_dwordx4 v[24:25], v[16:19], off

;     __device__ __forceinline__ void operator()(const f32x4 (&acc)[2][2][4][2], const Unit& u, int wr, int wc, int fr, int fq, const Pre&) const {
;     ...
;                 } else {
;                     const f32x4 x1 = acc[ai][0][m][0] * rs, x2 = acc[ai][0][m][1] * rs;
;                     if (wc < 2) {
;                         if (roti) st_bf16x8(kib + (size_t)row * 64 + cw, x1 * cs[q] - x2 * sn[q], x2 * cs[q] + x1 * sn[q]);
;                         else st_bf16x8(kib + (size_t)row * 64 + cw, x1, x2);
;                     } else if (wc == 2 && fq < 2) {
;                         *(f32x4*)(wib + (size_t)row * 16 + 8 * fq) = x1 * 0.03125f; *(f32x4*)(wib + (size_t)row * 16 + 8 * fq + 4) = x2 * 0.03125f;
;                     }
.LBB0_824:
	s_and_b64 vcc, exec, s[2:3]
	s_mov_b64 s[4:5], -1
	s_cbranch_vccnz .LBB0_836
	s_andn2_b64 vcc, exec, s[82:83]
	s_cbranch_vccnz .LBB0_833
	v_mul_f32_e64 v18, v86, v20
	v_mul_f32_e64 v19, v87, v20
	v_mul_f32_e64 v26, v84, v20
	v_mul_f32_e64 v27, v85, v20
	v_mul_f32_e64 v16, v82, v20
	v_mul_f32_e64 v17, v83, v20
	v_mul_f32_e64 v24, v80, v20
	v_mul_f32_e64 v25, v81, v20
	s_andn2_b64 vcc, exec, s[34:35]
	s_cbranch_vccnz .LBB0_830
	s_and_saveexec_b64 s[4:5], s[88:89]
	s_cbranch_execz .LBB0_829
	v_ashrrev_i32_e32 v23, 31, v22
	v_readlane_b32 s16, v249, 56
	v_lshlrev_b64 v[32:33], 6, v[22:23]
	v_readlane_b32 s17, v249, 57
	v_mul_f32_e64 v30, v18, s38
	v_mul_f32_e64 v31, v19, s38
	v_mul_f32_e64 v28, v26, s38
	v_mul_f32_e64 v29, v27, s38
	v_lshl_add_u64 v[32:33], s[16:17], 0, v[32:33]
	v_lshl_add_u64 v[32:33], v[38:39], 2, v[32:33]
	global_store_dwordx4 v[32:33], v[28:31], off
	s_nop 1
	v_mul_f32_e64 v30, v16, s38
	v_mul_f32_e64 v31, v17, s38
	v_mul_f32_e64 v28, v24, s38
	v_mul_f32_e64 v29, v25, s38
	global_store_dwordx4 v[32:33], v[28:31], off offset:16

;     __device__ __forceinline__ void operator()(const f32x4 (&acc)[2][2][4][2], const Unit& u, int wr, int wc, int fr, int fq, const Pre&) const {
;     ...
;                 } else if (kind == KD_V) {
; #pragma unroll
;                     for (int bj = 0; bj < 2; ++bj) st_bf16x8(vb + (size_t)row * 512 + 256 * (pn - TL_V) + 128 * bj + cw, acc[ai][bj][m][0] * rs, acc[ai][bj][m][1] * rs);
.LBB0_833:
	s_andn2_b64 vcc, exec, s[4:5]
	s_cbranch_vccnz .LBB0_835
	v_ashrrev_i32_e32 v23, 31, v22
	v_readlane_b32 s4, v249, 52
	v_lshlrev_b64 v[16:17], 10, v[22:23]
	v_readlane_b32 s5, v249, 53
	v_mul_f32_e64 v18, v86, v20
	v_mul_f32_e64 v19, v87, v20
	v_mul_f32_e64 v26, v82, v20
	v_mul_f32_e64 v27, v83, v20
	v_lshl_add_u64 v[16:17], s[4:5], 0, v[16:17]
	v_lshl_add_u64 v[16:17], s[86:87], 1, v[16:17]
	v_lshl_add_u64 v[24:25], v[36:37], 1, v[16:17]
	v_mul_f32_e64 v16, v84, v20
	v_mul_f32_e64 v17, v85, v20
	v_mul_f32_e64 v28, v80, v20
	v_mul_f32_e64 v29, v81, v20
	v_cvt_pk_bf16_f32 v16, v16, v17
	v_cvt_pk_bf16_f32 v17, v18, v19
	s_nop 0
	v_cvt_pk_bf16_f32 v18, v28, v29
	v_cvt_pk_bf16_f32 v19, v26, v27
	global_store_dwordx4 v[24:25], v[16:19], off
	v_mul_f32_e64 v26, v90, v20
	v_mul_f32_e64 v27, v91, v20
	v_mul_f32_e64 v28, v88, v20
	v_mul_f32_e64 v29, v89, v20
	v_mul_f32_e64 v18, v94, v20
	v_mul_f32_e64 v19, v95, v20
	v_mul_f32_e64 v16, v92, v20
	v_mul_f32_e64 v17, v93, v20
	s_nop 0
	v_cvt_pk_bf16_f32 v16, v16, v17
	v_cvt_pk_bf16_f32 v17, v18, v19
	v_cvt_pk_bf16_f32 v18, v28, v29
	v_cvt_pk_bf16_f32 v19, v26, v27
	global_store_dwordx4 v[24:25], v[16:19], off offset:256

;     __device__ __forceinline__ void operator()(const f32x4 (&acc)[2][2][4][2], const Unit& u, int wr, int wc, int fr, int fq, const Pre&) const {
;     ...
;                 } else if (kind == KD_Q || kind == KD_K) {
;                     bf16_t* o = (kind == KD_Q) ? qb + (size_t)row * DM + 256 * (pn - TL_Q) + cw : kb + (size_t)row * 512 + 256 * (pn - TL_K) + cw;
; #pragma unroll
;                     for (int bj = 0; bj < 2; ++bj) {
;                         const f32x4 x1 = acc[ai][bj][m][0] * rs, x2 = acc[ai][bj][m][1] * rs;
;                         if (rotqk) st_bf16x8(o + 128 * bj, x1 * cs[q] - x2 * sn[q], x2 * cs[q] + x1 * sn[q]);
;                         else st_bf16x8(o + 128 * bj, x1, x2);
;                     }
.LBB0_836:
	s_andn2_b64 vcc, exec, s[4:5]
	s_cbranch_vccnz .LBB0_846
	v_cndmask_b32_e64 v16, 0, 1, s[78:79]
	v_mul_f32_e64 v24, v86, v20
	v_mul_f32_e64 v25, v87, v20
	v_mul_f32_e64 v26, v84, v20
	v_mul_f32_e64 v27, v85, v20
	v_mul_f32_e64 v28, v82, v20
	v_mul_f32_e64 v29, v83, v20
	v_mul_f32_e64 v30, v80, v20
	v_mul_f32_e64 v31, v81, v20
	v_cmp_ne_u32_e64 s[4:5], 1, v16
	s_andn2_b64 vcc, exec, s[78:79]
	s_mov_b64 s[16:17], -1
	s_cbranch_vccnz .LBB0_839
	s_mov_b64 s[16:17], 0
	v_cvt_pk_bf16_f32 v16, v26, v27
	v_cvt_pk_bf16_f32 v17, v24, v25
	v_cvt_pk_bf16_f32 v18, v30, v31
	v_cvt_pk_bf16_f32 v19, v28, v29
.LBB0_839:
	s_andn2_b64 vcc, exec, s[16:17]
	s_cbranch_vccnz .LBB0_841
	v_mul_f32_e64 v16, v28, v10
	v_mul_f32_e64 v17, v29, v11
	v_mul_f32_e64 v18, v30, v8
	v_mul_f32_e64 v19, v31, v9
	v_fma_f32 v32, v24, v14, -v16
	v_fma_f32 v33, v25, v15, -v17
	v_fma_f32 v16, v26, v12, -v18
	v_fma_f32 v17, v27, v13, -v19
	v_mul_f32_e64 v18, v28, v14
	v_mul_f32_e64 v19, v29, v15
	v_mul_f32_e64 v28, v30, v12
	v_mul_f32_e64 v29, v31, v13
	v_fma_f32 v24, v24, v10, v18
	v_fma_f32 v25, v25, v11, v19
	v_fma_f32 v18, v26, v8, v28
	v_fma_f32 v19, v27, v9, v29
	v_cvt_pk_bf16_f32 v16, v16, v17
	v_cvt_pk_bf16_f32 v17, v32, v33
	s_nop 0
	v_cvt_pk_bf16_f32 v18, v18, v19
	v_cvt_pk_bf16_f32 v19, v24, v25
.LBB0_841:
	s_and_b64 s[16:17], s[80:81], exec
	v_readlane_b32 s16, v249, 49
	v_readlane_b32 s17, v249, 51
	v_ashrrev_i32_e32 v23, 31, v22
	s_cselect_b32 s17, s16, s17
	v_readlane_b32 s16, v249, 48
	v_readlane_b32 s36, v249, 50
	s_cselect_b32 s92, 12, 10
	s_cselect_b32 s16, s16, s36
	v_lshlrev_b64 v[24:25], s92, v[22:23]
	s_cselect_b32 s37, s54, s45
	s_cselect_b32 s36, s8, s57
	v_lshl_add_u64 v[24:25], s[16:17], 0, v[24:25]
	v_lshl_add_u64 v[24:25], s[36:37], 1, v[24:25]
	v_lshl_add_u64 v[24:25], v[36:37], 1, v[24:25]
	v_mov_b32_e32 v21, v20
	global_store_dwordx4 v[24:25], v[16:19], off
	v_mul_f32_e64 v28, v92, v20
	v_mul_f32_e64 v29, v93, v21
	v_mul_f32_e64 v32, v88, v20
	v_mul_f32_e64 v33, v89, v21
	v_mov_b32_e32 v16, v20
	v_mov_b32_e32 v17, v20
	v_mul_f32_e64 v26, v94, v16
	v_mul_f32_e64 v27, v95, v17
	v_mul_f32_e64 v30, v90, v16
	v_mul_f32_e64 v31, v91, v17
	s_and_b64 vcc, exec, s[4:5]
	s_mov_b64 s[4:5], -1
	s_cbranch_vccnz .LBB0_843
	s_mov_b64 s[4:5], 0
	v_cvt_pk_bf16_f32 v16, v28, v29
	v_cvt_pk_bf16_f32 v17, v26, v27
	v_cvt_pk_bf16_f32 v18, v32, v33
	v_cvt_pk_bf16_f32 v19, v30, v31
.LBB0_843:
	s_andn2_b64 vcc, exec, s[4:5]
	s_cbranch_vccnz .LBB0_845
	v_mul_f32_e64 v16, v30, v10
	v_mul_f32_e64 v17, v31, v11
	v_mul_f32_e64 v18, v32, v8
	v_mul_f32_e64 v19, v33, v9
	v_fma_f32 v34, v26, v14, -v16
	v_fma_f32 v35, v27, v15, -v17
	v_fma_f32 v16, v28, v12, -v18
	v_fma_f32 v17, v29, v13, -v19
	v_mul_f32_e64 v14, v30, v14
	v_mul_f32_e64 v15, v31, v15
	v_mul_f32_e64 v12, v32, v12
	v_mul_f32_e64 v13, v33, v13
	v_fma_f32 v10, v26, v10, v14
	v_fma_f32 v11, v27, v11, v15
	v_fma_f32 v8, v28, v8, v12
	v_fma_f32 v9, v29, v9, v13
	v_cvt_pk_bf16_f32 v16, v16, v17
	v_cvt_pk_bf16_f32 v17, v34, v35
	s_nop 0
	v_cvt_pk_bf16_f32 v18, v8, v9
	v_cvt_pk_bf16_f32 v19, v10, v11

; __device__ __forceinline__ f32x4 sigmoid4(const f32x4& x, float s) {
;     f32x4 z = x * (s * -1.4426950408889634f), e;
; #pragma unroll
;     for (int j = 0; j < 4; ++j) e[j] = __builtin_amdgcn_exp2f(z[j]);
;     e = e + 1.0f;
; #pragma unroll
;     for (int j = 0; j < 4; ++j) e[j] = __builtin_amdgcn_rcpf(e[j]);
;     return e;
; }
;     __device__ __forceinline__ void operator()(const f32x4 (&acc)[2][2][4][2], const Unit& u, int wr, int wc, int fr, int fq, const Pre&) const {
;     ...
;                 } else if (kind == KD_A) {
;                     st_bf16x8(abuf + (size_t)row * DM + 128 * (pn - TL_A) + cw, acc[ai][0][m][0] * rs * sigmoid4(acc[ai][1][m][0], rs), acc[ai][0][m][1] * rs * sigmoid4(acc[ai][1][m][1], rs));
;                 } else if (kind == KD_P) {
;                     const float r2 = rs * rs;
;                     st_bf16x8(pbuf + (size_t)row * DM + 128 * (pn - TL_P) + cw, acc[ai][0][m][0] * acc[ai][1][m][0] * r2, acc[ai][0][m][1] * acc[ai][1][m][1] * r2);
;                 } else if (kind == KD_G) {
; #pragma unroll
;                     for (int bj = 0; bj < 2; ++bj)
;                         st_bf16x8(gabuf + (size_t)row * DM + 256 * (pn - TL_G) + 128 * bj + cw, sigmoid4(acc[ai][bj][m][0], rs), sigmoid4(acc[ai][bj][m][1], rs));
.LBB0_850:
	v_ashrrev_i32_e32 v23, 31, v22
	v_lshlrev_b64 v[8:9], 12, v[22:23]
	v_lshl_add_u64 v[8:9], s[12:13], 0, v[8:9]
	v_lshl_add_u64 v[8:9], s[76:77], 1, v[8:9]
	v_mul_f32_e32 v19, 0xbfb8aa3b, v20
	v_lshl_add_u64 v[12:13], v[36:37], 1, v[8:9]
	v_mul_f32_e32 v8, v92, v19
	v_mul_f32_e32 v9, v93, v19
	v_mul_f32_e32 v10, v94, v19
	v_mul_f32_e32 v11, v95, v19
	v_exp_f32_e32 v8, v8
	v_exp_f32_e32 v10, v10
	v_exp_f32_e32 v11, v11
	v_exp_f32_e32 v9, v9
	v_mul_f32_e64 v14, v86, v20
	v_mul_f32_e64 v15, v87, v20
	v_mul_f32_e64 v16, v84, v20
	v_mul_f32_e64 v17, v85, v20
	v_add_f32_e64 v10, v10, 1.0
	v_add_f32_e64 v11, v11, 1.0
	v_add_f32_e64 v8, v8, 1.0
	v_add_f32_e64 v9, v9, 1.0
	v_mul_f32_e32 v18, v88, v19
	v_mul_f32_e32 v21, v89, v19
	v_mul_f32_e32 v22, v90, v19
	v_mul_f32_e32 v19, v91, v19
	v_rcp_f32_e32 v8, v8
	v_rcp_f32_e32 v9, v9
	v_rcp_f32_e32 v10, v10
	v_rcp_f32_e32 v11, v11
	v_exp_f32_e32 v18, v18
	v_exp_f32_e32 v22, v22
	v_exp_f32_e32 v23, v19
	v_exp_f32_e32 v19, v21
	v_mul_f32_e64 v10, v14, v10
	v_mul_f32_e64 v11, v15, v11
	v_mul_f32_e64 v8, v16, v8
	v_mul_f32_e64 v9, v17, v9
	v_add_f32_e64 v14, v22, 1.0
	v_add_f32_e64 v15, v23, 1.0
	v_add_f32_e64 v16, v18, 1.0
	v_add_f32_e64 v17, v19, 1.0
	v_rcp_f32_e32 v14, v14
	v_rcp_f32_e32 v16, v16
	v_rcp_f32_e32 v15, v15
	v_rcp_f32_e32 v17, v17
	v_mul_f32_e64 v18, v82, v20
	v_mul_f32_e64 v19, v83, v20
	v_mul_f32_e64 v21, v81, v20
	v_mul_f32_e64 v20, v80, v20
	v_mul_f32_e64 v14, v18, v14
	v_mul_f32_e64 v15, v19, v15
	v_mul_f32_e64 v16, v20, v16
	v_mul_f32_e64 v17, v21, v17
	v_cvt_pk_bf16_f32 v8, v8, v9
	v_cvt_pk_bf16_f32 v9, v10, v11
	s_nop 0
	v_cvt_pk_bf16_f32 v10, v16, v17
	v_cvt_pk_bf16_f32 v11, v14, v15
	global_store_dwordx4 v[12:13], v[8:11], off
.LBB0_851:
	v_add_u32_e32 v14, 0xb0, v40
	v_mul_f32_e32 v12, 0x3c800000, v222
	s_mov_b64 s[36:37], -1
	s_mov_b64 s[4:5], 0
	s_cmp_lt_i32 s55, 1
	s_mov_b64 s[16:17], 0
	s_cbranch_scc1 .LBB0_884
	s_cmp_gt_i32 s55, 1
	s_cbranch_scc0 .LBB0_856
	s_cmp_eq_u32 s55, 2
	s_mov_b64 s[16:17], -1
	s_cbranch_scc0 .LBB0_855
	v_ashrrev_i32_e32 v15, 31, v14
	v_readlane_b32 s16, v249, 46
	v_lshlrev_b64 v[8:9], 12, v[14:15]
	v_readlane_b32 s17, v249, 47
	v_mul_f32_e32 v13, 0xbfb8aa3b, v12
	v_mul_f32_e32 v10, v70, v13
	v_lshl_add_u64 v[8:9], s[16:17], 0, v[8:9]
	v_lshl_add_u64 v[8:9], s[90:91], 1, v[8:9]
	v_mul_f32_e32 v11, v71, v13
	v_lshl_add_u64 v[16:17], v[36:37], 1, v[8:9]
	v_mul_f32_e32 v8, v68, v13
	v_mul_f32_e32 v9, v69, v13
	v_exp_f32_e32 v10, v10
	v_exp_f32_e32 v11, v11
	v_exp_f32_e32 v8, v8
	v_exp_f32_e32 v9, v9
	s_mov_b64 s[16:17], 0
	v_add_f32_e64 v10, v10, 1.0
	v_add_f32_e64 v11, v11, 1.0
	v_add_f32_e64 v8, v8, 1.0
	v_add_f32_e64 v9, v9, 1.0
	v_rcp_f32_e32 v19, v10
	v_rcp_f32_e32 v20, v11
	v_mul_f32_e32 v10, v66, v13
	v_mul_f32_e32 v11, v67, v13
	v_rcp_f32_e32 v15, v8
	v_rcp_f32_e32 v18, v9
	v_mul_f32_e32 v8, v64, v13
	v_mul_f32_e32 v9, v65, v13
	v_exp_f32_e32 v10, v10
	v_exp_f32_e32 v11, v11
	v_exp_f32_e32 v8, v8
	v_exp_f32_e32 v9, v9
	v_add_f32_e64 v10, v10, 1.0
	v_add_f32_e64 v11, v11, 1.0
	s_nop 0
	v_rcp_f32_e32 v11, v11
	v_add_f32_e64 v8, v8, 1.0
	v_add_f32_e64 v9, v9, 1.0
	v_rcp_f32_e32 v23, v10
	v_rcp_f32_e32 v21, v8
	v_rcp_f32_e32 v22, v9
	v_cvt_pk_bf16_f32 v8, v15, v18
	v_cvt_pk_bf16_f32 v9, v19, v20
	v_cvt_pk_bf16_f32 v10, v21, v22
	v_cvt_pk_bf16_f32 v11, v23, v11
	global_store_dwordx4 v[16:17], v[8:11], off
	s_nop 1
	v_mul_f32_e32 v10, v78, v13
	v_mul_f32_e32 v11, v79, v13
	v_mul_f32_e32 v8, v76, v13
	v_mul_f32_e32 v9, v77, v13
	v_exp_f32_e32 v10, v10
	v_exp_f32_e32 v11, v11
	v_exp_f32_e32 v8, v8
	v_exp_f32_e32 v9, v9
	v_add_f32_e64 v10, v10, 1.0
	v_add_f32_e64 v11, v11, 1.0
	s_nop 0
	v_rcp_f32_e32 v19, v10
	v_add_f32_e64 v8, v8, 1.0
	v_add_f32_e64 v9, v9, 1.0
	v_rcp_f32_e32 v20, v11
	v_mul_f32_e32 v10, v74, v13
	v_mul_f32_e32 v11, v75, v13
	v_rcp_f32_e32 v15, v8
	v_rcp_f32_e32 v18, v9
	v_mul_f32_e32 v8, v72, v13
	v_mul_f32_e32 v9, v73, v13
	v_exp_f32_e32 v10, v10
	v_exp_f32_e32 v11, v11
	v_exp_f32_e32 v8, v8
	v_exp_f32_e32 v9, v9
	v_add_f32_e64 v10, v10, 1.0
	v_add_f32_e64 v11, v11, 1.0
	s_nop 0
	v_rcp_f32_e32 v11, v11
	v_add_f32_e64 v8, v8, 1.0
	v_add_f32_e64 v9, v9, 1.0
	v_rcp_f32_e32 v22, v10
	v_rcp_f32_e32 v13, v8
	v_rcp_f32_e32 v21, v9
	v_cvt_pk_bf16_f32 v8, v15, v18
	v_cvt_pk_bf16_f32 v9, v19, v20
	v_cvt_pk_bf16_f32 v10, v13, v21
	v_cvt_pk_bf16_f32 v11, v22, v11
	global_store_dwordx4 v[16:17], v[8:11], off offset:256

;     __device__ __forceinline__ void operator()(const f32x4 (&acc)[2][2][4][2], const Unit& u, int wr, int wc, int fr, int fq, const Pre&) const {
;     ...
;                 } else if (kind == KD_P) {
;                     const float r2 = rs * rs;
;                     st_bf16x8(pbuf + (size_t)row * DM + 128 * (pn - TL_P) + cw, acc[ai][0][m][0] * acc[ai][1][m][0] * r2, acc[ai][0][m][1] * acc[ai][1][m][1] * r2);
.LBB0_856:
	s_and_b64 vcc, exec, s[36:37]
	s_cbranch_vccz .LBB0_858
	v_ashrrev_i32_e32 v15, 31, v14
	v_readlane_b32 s36, v249, 44
	v_lshlrev_b64 v[10:11], 12, v[14:15]
	v_readlane_b32 s37, v249, 45
	v_mul_f32_e32 v8, v12, v12
	v_mul_f32_e64 v18, v68, v76
	v_mul_f32_e64 v19, v69, v77
	v_lshl_add_u64 v[10:11], s[36:37], 0, v[10:11]
	v_lshl_add_u64 v[10:11], s[84:85], 1, v[10:11]
	v_lshl_add_u64 v[16:17], v[36:37], 1, v[10:11]
	v_mul_f32_e64 v10, v70, v78
	v_mul_f32_e64 v11, v71, v79
	v_mul_f32_e64 v20, v66, v74
	v_mul_f32_e64 v21, v67, v75
	v_mul_f32_e64 v10, v10, v8
	v_mul_f32_e64 v11, v11, v8
	v_mul_f32_e64 v22, v64, v72
	v_mul_f32_e64 v23, v65, v73
	v_mul_f32_e64 v18, v18, v8
	v_mul_f32_e64 v19, v19, v8
	v_mul_f32_e64 v20, v20, v8
	v_mul_f32_e64 v21, v21, v8
	v_mul_f32_e64 v22, v22, v8
	v_mul_f32_e64 v23, v23, v8
	v_cvt_pk_bf16_f32 v8, v18, v19
	v_cvt_pk_bf16_f32 v9, v10, v11
	s_nop 0
	v_cvt_pk_bf16_f32 v10, v22, v23
	v_cvt_pk_bf16_f32 v11, v20, v21
	global_store_dwordx4 v[16:17], v[8:11], off

;     __device__ __forceinline__ void operator()(const f32x4 (&acc)[2][2][4][2], const Unit& u, int wr, int wc, int fr, int fq, const Pre&) const {
;     ...
;                 } else {
;                     const f32x4 x1 = acc[ai][0][m][0] * rs, x2 = acc[ai][0][m][1] * rs;
;                     if (wc < 2) {
;                         if (roti) st_bf16x8(kib + (size_t)row * 64 + cw, x1 * cs[q] - x2 * sn[q], x2 * cs[q] + x1 * sn[q]);
;                         else st_bf16x8(kib + (size_t)row * 64 + cw, x1, x2);
;                     } else if (wc == 2 && fq < 2) {
;                         *(f32x4*)(wib + (size_t)row * 16 + 8 * fq) = x1 * 0.03125f; *(f32x4*)(wib + (size_t)row * 16 + 8 * fq + 4) = x2 * 0.03125f;
;                     }
.LBB0_860:
	s_and_b64 vcc, exec, s[2:3]
	s_mov_b64 s[2:3], -1
	s_cbranch_vccnz .LBB0_872
	s_andn2_b64 vcc, exec, s[82:83]
	s_cbranch_vccnz .LBB0_869
	v_mul_f32_e64 v10, v70, v12
	v_mul_f32_e64 v11, v71, v12
	v_mul_f32_e64 v18, v68, v12
	v_mul_f32_e64 v19, v69, v12
	v_mul_f32_e64 v8, v66, v12
	v_mul_f32_e64 v9, v67, v12
	v_mul_f32_e64 v16, v64, v12
	v_mul_f32_e64 v17, v65, v12
	s_andn2_b64 vcc, exec, s[34:35]
	s_cbranch_vccnz .LBB0_866
	s_and_saveexec_b64 s[2:3], s[88:89]
	s_cbranch_execz .LBB0_865
	v_ashrrev_i32_e32 v15, 31, v14
	v_readlane_b32 s4, v249, 56
	v_lshlrev_b64 v[24:25], 6, v[14:15]
	v_readlane_b32 s5, v249, 57
	v_mul_f32_e64 v22, v10, s38
	v_mul_f32_e64 v23, v11, s38
	v_mul_f32_e64 v20, v18, s38
	v_mul_f32_e64 v21, v19, s38
	v_lshl_add_u64 v[24:25], s[4:5], 0, v[24:25]
	v_lshl_add_u64 v[24:25], v[38:39], 2, v[24:25]
	global_store_dwordx4 v[24:25], v[20:23], off
	s_nop 1
	v_mul_f32_e64 v22, v8, s38
	v_mul_f32_e64 v23, v9, s38
	v_mul_f32_e64 v20, v16, s38
	v_mul_f32_e64 v21, v17, s38
	global_store_dwordx4 v[24:25], v[20:23], off offset:16

;     __device__ __forceinline__ void operator()(const f32x4 (&acc)[2][2][4][2], const Unit& u, int wr, int wc, int fr, int fq, const Pre&) const {
;     ...
;                 } else if (kind == KD_V) {
; #pragma unroll
;                     for (int bj = 0; bj < 2; ++bj) st_bf16x8(vb + (size_t)row * 512 + 256 * (pn - TL_V) + 128 * bj + cw, acc[ai][bj][m][0] * rs, acc[ai][bj][m][1] * rs);
.LBB0_869:
	s_andn2_b64 vcc, exec, s[2:3]
	s_cbranch_vccnz .LBB0_871
	v_ashrrev_i32_e32 v15, 31, v14
	v_readlane_b32 s2, v249, 52
	v_lshlrev_b64 v[8:9], 10, v[14:15]
	v_readlane_b32 s3, v249, 53
	v_mul_f32_e64 v10, v70, v12
	v_mul_f32_e64 v11, v71, v12
	v_mul_f32_e64 v18, v66, v12
	v_mul_f32_e64 v19, v67, v12
	v_lshl_add_u64 v[8:9], s[2:3], 0, v[8:9]
	v_lshl_add_u64 v[8:9], s[86:87], 1, v[8:9]
	v_lshl_add_u64 v[16:17], v[36:37], 1, v[8:9]
	v_mul_f32_e64 v8, v68, v12
	v_mul_f32_e64 v9, v69, v12
	v_mul_f32_e64 v20, v64, v12
	v_mul_f32_e64 v21, v65, v12
	v_cvt_pk_bf16_f32 v8, v8, v9
	v_cvt_pk_bf16_f32 v9, v10, v11
	s_nop 0
	v_cvt_pk_bf16_f32 v10, v20, v21
	v_cvt_pk_bf16_f32 v11, v18, v19
	global_store_dwordx4 v[16:17], v[8:11], off
	v_mul_f32_e64 v18, v74, v12
	v_mul_f32_e64 v19, v75, v12
	v_mul_f32_e64 v20, v72, v12
	v_mul_f32_e64 v21, v73, v12
	v_mul_f32_e64 v10, v78, v12
	v_mul_f32_e64 v11, v79, v12
	v_mul_f32_e64 v8, v76, v12
	v_mul_f32_e64 v9, v77, v12
	s_nop 0
	v_cvt_pk_bf16_f32 v8, v8, v9
	v_cvt_pk_bf16_f32 v9, v10, v11
	v_cvt_pk_bf16_f32 v10, v20, v21
	v_cvt_pk_bf16_f32 v11, v18, v19
	global_store_dwordx4 v[16:17], v[8:11], off offset:256

;     __device__ __forceinline__ void operator()(const f32x4 (&acc)[2][2][4][2], const Unit& u, int wr, int wc, int fr, int fq, const Pre&) const {
;     ...
;                 } else if (kind == KD_Q || kind == KD_K) {
;                     bf16_t* o = (kind == KD_Q) ? qb + (size_t)row * DM + 256 * (pn - TL_Q) + cw : kb + (size_t)row * 512 + 256 * (pn - TL_K) + cw;
; #pragma unroll
;                     for (int bj = 0; bj < 2; ++bj) {
;                         const f32x4 x1 = acc[ai][bj][m][0] * rs, x2 = acc[ai][bj][m][1] * rs;
;                         if (rotqk) st_bf16x8(o + 128 * bj, x1 * cs[q] - x2 * sn[q], x2 * cs[q] + x1 * sn[q]);
;                         else st_bf16x8(o + 128 * bj, x1, x2);
;                     }
.LBB0_872:
	s_andn2_b64 vcc, exec, s[2:3]
	s_cbranch_vccnz .LBB0_882
	v_cndmask_b32_e64 v8, 0, 1, s[78:79]
	v_mul_f32_e64 v16, v70, v12
	v_mul_f32_e64 v17, v71, v12
	v_mul_f32_e64 v18, v68, v12
	v_mul_f32_e64 v19, v69, v12
	v_mul_f32_e64 v20, v66, v12
	v_mul_f32_e64 v21, v67, v12
	v_mul_f32_e64 v22, v64, v12
	v_mul_f32_e64 v23, v65, v12
	v_cmp_ne_u32_e64 s[2:3], 1, v8
	s_andn2_b64 vcc, exec, s[78:79]
	s_mov_b64 s[4:5], -1
	s_cbranch_vccnz .LBB0_875
	s_mov_b64 s[4:5], 0
	v_cvt_pk_bf16_f32 v8, v18, v19
	v_cvt_pk_bf16_f32 v9, v16, v17
	v_cvt_pk_bf16_f32 v10, v22, v23
	v_cvt_pk_bf16_f32 v11, v20, v21
.LBB0_875:
	s_andn2_b64 vcc, exec, s[4:5]
	s_cbranch_vccnz .LBB0_877
	v_mul_f32_e64 v8, v20, v2
	v_mul_f32_e64 v9, v21, v3
	v_mul_f32_e64 v10, v22, v0
	v_mul_f32_e64 v11, v23, v1
	v_fma_f32 v24, v16, v6, -v8
	v_fma_f32 v25, v17, v7, -v9
	v_fma_f32 v8, v18, v4, -v10
	v_fma_f32 v9, v19, v5, -v11
	v_mul_f32_e64 v10, v20, v6
	v_mul_f32_e64 v11, v21, v7
	v_mul_f32_e64 v20, v22, v4
	v_mul_f32_e64 v21, v23, v5
	v_fma_f32 v16, v16, v2, v10
	v_fma_f32 v17, v17, v3, v11
	v_fma_f32 v10, v18, v0, v20
	v_fma_f32 v11, v19, v1, v21
	v_cvt_pk_bf16_f32 v8, v8, v9
	v_cvt_pk_bf16_f32 v9, v24, v25
	s_nop 0
	v_cvt_pk_bf16_f32 v10, v10, v11
	v_cvt_pk_bf16_f32 v11, v16, v17
.LBB0_877:
	s_and_b64 s[4:5], s[80:81], exec
	v_readlane_b32 s4, v249, 49
	v_readlane_b32 s5, v249, 51
	s_cselect_b32 s5, s4, s5
	v_readlane_b32 s4, v249, 48
	v_readlane_b32 s16, v249, 50
	v_ashrrev_i32_e32 v15, 31, v14
	s_cselect_b32 s4, s4, s16
	s_cselect_b32 s16, s8, s57
	s_cselect_b32 s8, 12, 10
	v_lshlrev_b64 v[16:17], s8, v[14:15]
	s_cselect_b32 s17, s54, s45
	v_lshl_add_u64 v[16:17], s[4:5], 0, v[16:17]
	v_lshl_add_u64 v[16:17], s[16:17], 1, v[16:17]
	v_lshl_add_u64 v[16:17], v[36:37], 1, v[16:17]
	v_mov_b32_e32 v13, v12
	global_store_dwordx4 v[16:17], v[8:11], off
	v_mul_f32_e64 v20, v76, v12
	v_mul_f32_e64 v21, v77, v13
	v_mul_f32_e64 v24, v72, v12
	v_mul_f32_e64 v25, v73, v13
	v_mov_b32_e32 v8, v12
	v_mov_b32_e32 v9, v12
	v_mul_f32_e64 v18, v78, v8
	v_mul_f32_e64 v19, v79, v9
	v_mul_f32_e64 v22, v74, v8
	v_mul_f32_e64 v23, v75, v9
	s_and_b64 vcc, exec, s[2:3]
	s_mov_b64 s[2:3], -1
	s_cbranch_vccnz .LBB0_879
	s_mov_b64 s[2:3], 0
	v_cvt_pk_bf16_f32 v8, v20, v21
	v_cvt_pk_bf16_f32 v9, v18, v19
	v_cvt_pk_bf16_f32 v10, v24, v25
	v_cvt_pk_bf16_f32 v11, v22, v23
.LBB0_879:
	s_andn2_b64 vcc, exec, s[2:3]
	s_cbranch_vccnz .LBB0_881
	v_mul_f32_e64 v8, v22, v2
	v_mul_f32_e64 v9, v23, v3
	v_mul_f32_e64 v10, v24, v0
	v_mul_f32_e64 v11, v25, v1
	v_fma_f32 v26, v18, v6, -v8
	v_fma_f32 v27, v19, v7, -v9
	v_fma_f32 v8, v20, v4, -v10
	v_fma_f32 v9, v21, v5, -v11
	v_mul_f32_e64 v6, v22, v6
	v_mul_f32_e64 v7, v23, v7
	v_mul_f32_e64 v4, v24, v4
	v_mul_f32_e64 v5, v25, v5
	v_fma_f32 v2, v18, v2, v6
	v_fma_f32 v3, v19, v3, v7
	v_fma_f32 v0, v20, v0, v4
	v_fma_f32 v1, v21, v1, v5
	v_cvt_pk_bf16_f32 v8, v8, v9
	v_cvt_pk_bf16_f32 v9, v26, v27
	s_nop 0
	v_cvt_pk_bf16_f32 v10, v0, v1
	v_cvt_pk_bf16_f32 v11, v2, v3

; __device__ __forceinline__ f32x4 sigmoid4(const f32x4& x, float s) {
;     f32x4 z = x * (s * -1.4426950408889634f), e;
; #pragma unroll
;     for (int j = 0; j < 4; ++j) e[j] = __builtin_amdgcn_exp2f(z[j]);
;     e = e + 1.0f;
; #pragma unroll
;     for (int j = 0; j < 4; ++j) e[j] = __builtin_amdgcn_rcpf(e[j]);
;     return e;
; }
;     __device__ __forceinline__ void operator()(const f32x4 (&acc)[2][2][4][2], const Unit& u, int wr, int wc, int fr, int fq, const Pre&) const {
;     ...
;                 } else if (kind == KD_A) {
;                     st_bf16x8(abuf + (size_t)row * DM + 128 * (pn - TL_A) + cw, acc[ai][0][m][0] * rs * sigmoid4(acc[ai][1][m][0], rs), acc[ai][0][m][1] * rs * sigmoid4(acc[ai][1][m][1], rs));
.LBB0_887:
	v_ashrrev_i32_e32 v15, 31, v14
	v_lshlrev_b64 v[0:1], 12, v[14:15]
	v_lshl_add_u64 v[0:1], s[12:13], 0, v[0:1]
	v_lshl_add_u64 v[0:1], s[76:77], 1, v[0:1]
	v_mul_f32_e32 v11, 0xbfb8aa3b, v12
	v_lshl_add_u64 v[4:5], v[36:37], 1, v[0:1]
	v_mul_f32_e32 v0, v76, v11
	v_mul_f32_e32 v1, v77, v11
	v_mul_f32_e32 v2, v78, v11
	v_mul_f32_e32 v3, v79, v11
	v_exp_f32_e32 v0, v0
	v_exp_f32_e32 v2, v2
	v_exp_f32_e32 v3, v3
	v_exp_f32_e32 v1, v1
	v_mul_f32_e64 v6, v70, v12
	v_mul_f32_e64 v7, v71, v12
	v_mul_f32_e64 v8, v68, v12
	v_mul_f32_e64 v9, v69, v12
	v_add_f32_e64 v2, v2, 1.0
	v_add_f32_e64 v3, v3, 1.0
	v_add_f32_e64 v0, v0, 1.0
	v_add_f32_e64 v1, v1, 1.0
	v_mul_f32_e32 v10, v72, v11
	v_mul_f32_e32 v13, v73, v11
	v_mul_f32_e32 v14, v74, v11
	v_mul_f32_e32 v11, v75, v11
	v_rcp_f32_e32 v0, v0
	v_rcp_f32_e32 v1, v1
	v_rcp_f32_e32 v2, v2
	v_rcp_f32_e32 v3, v3
	v_exp_f32_e32 v10, v10
	v_exp_f32_e32 v14, v14
	v_exp_f32_e32 v15, v11
	v_exp_f32_e32 v11, v13
	v_mul_f32_e64 v2, v6, v2
	v_mul_f32_e64 v3, v7, v3
	v_mul_f32_e64 v0, v8, v0
	v_mul_f32_e64 v1, v9, v1
	v_add_f32_e64 v6, v14, 1.0
	v_add_f32_e64 v7, v15, 1.0
	v_add_f32_e64 v8, v10, 1.0
	v_add_f32_e64 v9, v11, 1.0
	v_rcp_f32_e32 v6, v6
	v_rcp_f32_e32 v8, v8
	v_rcp_f32_e32 v7, v7
	v_rcp_f32_e32 v9, v9
	v_mul_f32_e64 v10, v66, v12
	v_mul_f32_e64 v11, v67, v12
	v_mul_f32_e64 v13, v65, v12
	v_mul_f32_e64 v12, v64, v12
	v_mul_f32_e64 v6, v10, v6
	v_mul_f32_e64 v7, v11, v7
	v_mul_f32_e64 v8, v12, v8
	v_mul_f32_e64 v9, v13, v9
	v_cvt_pk_bf16_f32 v0, v0, v1
	v_cvt_pk_bf16_f32 v1, v2, v3
	s_nop 0
	v_cvt_pk_bf16_f32 v2, v8, v9
	v_cvt_pk_bf16_f32 v3, v6, v7
	global_store_dwordx4 v[4:5], v[0:3], off
	s_and_b64 vcc, exec, s[64:65]
	s_cbranch_vccnz .LBB0_889

;     __device__ __forceinline__ void operator()(const f32x4 (&acc)[2][2][4][2], const Unit& u, int wr, int wc, int fr, int fq, const Pre&) const {
;         const int kind = u.kind, pn = u.pn;
;         const int cw = 32 * wc + 8 * fq;
;         const int rowb = u.pm * 256 + wr * 64 + fr;
;         float rsv[8];
;         { const float* rsp = (kind == KD_KVX) ? rsmem : rs0;
; #pragma unroll
;           for (int q = 0; q < 8; ++q) rsv[q] = rsp[rowb + (q >> 2) * 128 + (q & 3) * 16] * sc; }
;         const bool rotqk = (kind == KD_Q || kind == KD_K) && (wc == 0);
;         const bool roti = (kind == KD_QI && ((wc & 1) == 0) && fq < 2) || (kind == KD_KI && wc == 0 && fq < 2);
;     ...
;                 } else if (kind == KD_G) {
; #pragma unroll
;                     for (int bj = 0; bj < 2; ++bj)
;                         st_bf16x8(gabuf + (size_t)row * DM + 256 * (pn - TL_G) + 128 * bj + cw, sigmoid4(acc[ai][bj][m][0], rs), sigmoid4(acc[ai][bj][m][1], rs));
.LBB0_932:
	s_or_b64 exec, exec, s[30:31]
	s_xor_b64 s[0:1], s[0:1], -1
	v_writelane_b32 v248, s0, 11
	s_xor_b64 s[92:93], s[16:17], -1
	v_lshlrev_b32_e32 v174, 3, v160
	v_writelane_b32 v248, s1, 12
	s_xor_b64 s[0:1], s[28:29], -1
	s_cmp_eq_u32 s7, 3
	s_cselect_b64 s[90:91], -1, 0
	s_lshl_b32 s4, s2, 8
	s_lshl_b32 s88, s2, 7
	v_writelane_b32 v248, s0, 9
	s_add_i32 s38, s4, 0xffffe000
	s_add_i32 s42, s88, 0xfffff800
	v_writelane_b32 v248, s1, 10
	v_readlane_b32 s0, v249, 59
	s_ashr_i32 s39, s38, 31
	s_ashr_i32 s43, s42, 31
	s_ashr_i32 s89, s88, 31
	v_add_u32_e32 v172, s0, v174
	s_cmp_lg_u32 s7, 5
	v_readlane_b32 s0, v248, 26
	s_cselect_b64 s[58:59], -1, 0
	v_readlane_b32 s1, v248, 27
	s_add_i32 s28, s4, 0xffffcc00
	s_add_i32 s94, s4, 0xffffce00
	s_add_i32 s81, s4, 0xffffd000
	s_add_i32 s31, s4, 0xffffd800
	s_and_b64 s[0:1], s[0:1], vcc
	s_ashr_i32 s29, s28, 31
	s_ashr_i32 s95, s94, 31
	s_ashr_i32 s30, s81, 31
	s_ashr_i32 s34, s31, 31
	v_writelane_b32 v248, s0, 7
	s_cmp_lt_i32 s2, 2
	v_ashrrev_i32_e32 v173, 31, v172
	v_writelane_b32 v248, s1, 8
	v_ashrrev_i32_e32 v175, 31, v174
	s_cselect_b64 s[86:87], -1, 0
	s_mov_b64 s[0:1], -1
	s_and_b64 vcc, exec, s[56:57]
	s_cbranch_vccz .LBB0_986
	s_mov_b64 vcc, -1
	s_mov_b64 s[0:1], 0
	s_cmp_lt_i32 s7, 1
	s_mov_b64 s[2:3], 0
	s_cbranch_scc1 .LBB0_981
	s_cmp_gt_i32 s7, 1
	s_cbranch_scc0 .LBB0_938
	s_cmp_eq_u32 s7, 2
	s_mov_b64 s[2:3], -1
	s_cbranch_scc0 .LBB0_937
	v_readlane_b32 s2, v249, 46
	v_lshlrev_b64 v[160:161], 12, v[184:185]
	v_readlane_b32 s3, v249, 47
	s_waitcnt vmcnt(0)
	v_mul_f32_e32 v166, 0xbfb8aa3b, v198
	v_mul_f32_e32 v162, v150, v166
	v_lshl_add_u64 v[160:161], s[2:3], 0, v[160:161]
	v_lshl_add_u64 v[160:161], s[38:39], 1, v[160:161]
	v_mul_f32_e32 v163, v151, v166
	v_lshl_add_u64 v[164:165], v[172:173], 1, v[160:161]
	v_mul_f32_e32 v160, v148, v166
	v_mul_f32_e32 v161, v149, v166
	v_exp_f32_e32 v162, v162
	v_exp_f32_e32 v163, v163
	v_exp_f32_e32 v160, v160
	v_exp_f32_e32 v161, v161
	s_mov_b64 s[2:3], 0
	v_add_f32_e64 v162, v162, 1.0
	v_add_f32_e64 v163, v163, 1.0
	v_add_f32_e64 v160, v160, 1.0
	v_add_f32_e64 v161, v161, 1.0
	v_rcp_f32_e32 v169, v162
	v_rcp_f32_e32 v171, v163
	v_mul_f32_e32 v162, v146, v166
	v_mul_f32_e32 v163, v147, v166
	v_rcp_f32_e32 v167, v160
	v_rcp_f32_e32 v168, v161
	v_mul_f32_e32 v160, v144, v166
	v_mul_f32_e32 v161, v145, v166
	v_exp_f32_e32 v162, v162
	v_exp_f32_e32 v163, v163
	v_exp_f32_e32 v160, v160
	v_exp_f32_e32 v161, v161
	v_add_f32_e64 v162, v162, 1.0
	v_add_f32_e64 v163, v163, 1.0
	s_nop 0
	v_rcp_f32_e32 v163, v163
	v_add_f32_e64 v160, v160, 1.0
	v_add_f32_e64 v161, v161, 1.0
	v_rcp_f32_e32 v181, v162
	v_rcp_f32_e32 v177, v160
	v_rcp_f32_e32 v179, v161
	v_cvt_pk_bf16_f32 v160, v167, v168
	v_cvt_pk_bf16_f32 v161, v169, v171
	v_cvt_pk_bf16_f32 v162, v177, v179
	v_cvt_pk_bf16_f32 v163, v181, v163
	global_store_dwordx4 v[164:165], v[160:163], off
	s_nop 1
	v_mul_f32_e32 v162, v142, v166
	v_mul_f32_e32 v163, v143, v166
	v_mul_f32_e32 v160, v140, v166
	v_mul_f32_e32 v161, v141, v166
	v_exp_f32_e32 v162, v162
	v_exp_f32_e32 v163, v163
	v_exp_f32_e32 v160, v160
	v_exp_f32_e32 v161, v161
	v_add_f32_e64 v162, v162, 1.0
	v_add_f32_e64 v163, v163, 1.0
	s_nop 0
	v_rcp_f32_e32 v169, v162
	v_add_f32_e64 v160, v160, 1.0
	v_add_f32_e64 v161, v161, 1.0
	v_rcp_f32_e32 v171, v163
	v_mul_f32_e32 v162, v138, v166
	v_mul_f32_e32 v163, v139, v166
	v_rcp_f32_e32 v167, v160
	v_rcp_f32_e32 v168, v161
	v_mul_f32_e32 v160, v136, v166
	v_mul_f32_e32 v161, v137, v166
	v_exp_f32_e32 v162, v162
	v_exp_f32_e32 v163, v163
	v_exp_f32_e32 v160, v160
	v_exp_f32_e32 v161, v161
	v_add_f32_e64 v162, v162, 1.0
	v_add_f32_e64 v163, v163, 1.0
	s_nop 0
	v_rcp_f32_e32 v163, v163
	v_add_f32_e64 v160, v160, 1.0
	v_add_f32_e64 v161, v161, 1.0
	v_rcp_f32_e32 v179, v162
	v_rcp_f32_e32 v166, v160
	v_rcp_f32_e32 v177, v161
	v_cvt_pk_bf16_f32 v160, v167, v168
	v_cvt_pk_bf16_f32 v161, v169, v171
	v_cvt_pk_bf16_f32 v162, v166, v177
	v_cvt_pk_bf16_f32 v163, v179, v163
	global_store_dwordx4 v[164:165], v[160:163], off offset:256

;     __device__ __forceinline__ void operator()(const f32x4 (&acc)[2][2][4][2], const Unit& u, int wr, int wc, int fr, int fq, const Pre&) const {
;     ...
;                 } else if (kind == KD_P) {
;                     const float r2 = rs * rs;
;                     st_bf16x8(pbuf + (size_t)row * DM + 128 * (pn - TL_P) + cw, acc[ai][0][m][0] * acc[ai][1][m][0] * r2, acc[ai][0][m][1] * acc[ai][1][m][1] * r2);
.LBB0_938:
	s_and_b64 vcc, exec, vcc
	s_cbranch_vccz .LBB0_940
	v_readlane_b32 vcc_lo, v249, 44
	v_lshlrev_b64 v[162:163], 12, v[184:185]
	v_readlane_b32 vcc_hi, v249, 45
	s_waitcnt vmcnt(0)
	v_mul_f32_e32 v160, v198, v198
	v_mul_f32_e64 v166, v148, v140
	v_mul_f32_e64 v167, v149, v141
	v_lshl_add_u64 v[162:163], vcc, 0, v[162:163]
	v_lshl_add_u64 v[162:163], s[42:43], 1, v[162:163]
	v_lshl_add_u64 v[164:165], v[172:173], 1, v[162:163]
	v_mul_f32_e64 v162, v150, v142
	v_mul_f32_e64 v163, v151, v143
	v_mul_f32_e64 v168, v146, v138
	v_mul_f32_e64 v169, v147, v139
	v_mul_f32_e64 v162, v162, v160
	v_mul_f32_e64 v163, v163, v160
	v_mul_f32_e64 v230, v144, v136
	v_mul_f32_e64 v231, v145, v137
	v_mul_f32_e64 v166, v166, v160
	v_mul_f32_e64 v167, v167, v160
	v_mul_f32_e64 v168, v168, v160
	v_mul_f32_e64 v169, v169, v160
	v_mul_f32_e64 v230, v230, v160
	v_mul_f32_e64 v231, v231, v160
	v_cvt_pk_bf16_f32 v160, v166, v167
	v_cvt_pk_bf16_f32 v161, v162, v163
	s_nop 0
	v_cvt_pk_bf16_f32 v162, v230, v231
	v_cvt_pk_bf16_f32 v163, v168, v169
	global_store_dwordx4 v[164:165], v[160:163], off

;     __device__ __forceinline__ void operator()(const f32x4 (&acc)[2][2][4][2], const Unit& u, int wr, int wc, int fr, int fq, const Pre&) const {
;     ...
;                 } else if (kind == KD_QI) {
; #pragma unroll
;                     for (int bj = 0; bj < 2; ++bj) {
;                         const f32x4 x1 = acc[ai][bj][m][0] * rs, x2 = acc[ai][bj][m][1] * rs;
;                         bf16_t* o = qib + (size_t)row * 1024 + 256 * (pn - TL_QI) + 128 * bj + cw;
;                         if (roti) st_bf16x8(o, x1 * cs[q] - x2 * sn[q], x2 * cs[q] + x1 * sn[q]); else st_bf16x8(o, x1, x2);
;                     }
;                 } else {
;                     const f32x4 x1 = acc[ai][0][m][0] * rs, x2 = acc[ai][0][m][1] * rs;
;                     if (wc < 2) {
;                         if (roti) st_bf16x8(kib + (size_t)row * 64 + cw, x1 * cs[q] - x2 * sn[q], x2 * cs[q] + x1 * sn[q]);
;                         else st_bf16x8(kib + (size_t)row * 64 + cw, x1, x2);
;                     } else if (wc == 2 && fq < 2) {
;                         *(f32x4*)(wib + (size_t)row * 16 + 8 * fq) = x1 * 0.03125f; *(f32x4*)(wib + (size_t)row * 16 + 8 * fq + 4) = x2 * 0.03125f;
;                     }
.LBB0_942:
	s_mov_b64 s[0:1], -1
	s_and_b64 vcc, exec, s[64:65]
	s_cbranch_vccz .LBB0_970
	s_and_b64 vcc, exec, s[58:59]
	s_cbranch_vccz .LBB0_967
	v_readlane_b32 s2, v249, 63
	s_waitcnt vmcnt(0)
	v_mov_b32_e32 v199, v198
	v_readlane_b32 s3, v248, 0
	s_and_b64 vcc, exec, s[2:3]
	v_mul_f32_e64 v162, v148, v198
	v_mul_f32_e64 v163, v149, v199
	v_mul_f32_e64 v160, v144, v198
	v_mul_f32_e64 v161, v145, v199
	s_cbranch_vccz .LBB0_956
	v_readlane_b32 s2, v248, 24
	v_mov_b32_e32 v164, v198
	v_mov_b32_e32 v165, v198
	v_readlane_b32 s3, v248, 25
	v_mul_f32_e64 v166, v150, v164
	v_mul_f32_e64 v167, v151, v165
	v_mul_f32_e64 v164, v146, v164
	v_mul_f32_e64 v165, v147, v165
	s_and_b64 vcc, exec, s[2:3]
	s_cbranch_vccz .LBB0_949
	s_mov_b64 s[0:1], exec
	v_readlane_b32 s2, v248, 7
	v_readlane_b32 s3, v248, 8
	s_and_b64 s[2:3], s[0:1], s[2:3]
	s_mov_b64 exec, s[2:3]
	s_cbranch_execz .LBB0_948
	v_readlane_b32 s2, v249, 56
	v_lshlrev_b64 v[168:169], 6, v[184:185]
	v_readlane_b32 s3, v249, 57
	s_nop 1
	v_lshl_add_u64 v[168:169], s[2:3], 0, v[168:169]
	s_mov_b32 s2, 0x3d000000
	v_lshl_add_u64 v[168:169], v[174:175], 2, v[168:169]
	v_mul_f32_e64 v246, v166, s2
	v_mul_f32_e64 v247, v167, s2
	v_mul_f32_e64 v244, v162, s2
	v_mul_f32_e64 v245, v163, s2
	v_mul_f32_e64 v232, v164, s2
	v_mul_f32_e64 v233, v165, s2
	v_mul_f32_e64 v230, v160, s2
	v_mul_f32_e64 v231, v161, s2
	global_store_dwordx4 v[168:169], v[244:247], off
	global_store_dwordx4 v[168:169], v[230:233], off offset:16

;     __device__ __forceinline__ void operator()(const f32x4 (&acc)[2][2][4][2], const Unit& u, int wr, int wc, int fr, int fq, const Pre&) const {
;     ...
;                 } else {
;                     const f32x4 x1 = acc[ai][0][m][0] * rs, x2 = acc[ai][0][m][1] * rs;
;                     if (wc < 2) {
;                         if (roti) st_bf16x8(kib + (size_t)row * 64 + cw, x1 * cs[q] - x2 * sn[q], x2 * cs[q] + x1 * sn[q]);
;                         else st_bf16x8(kib + (size_t)row * 64 + cw, x1, x2);
.LBB0_952:
	s_andn2_saveexec_b64 s[0:1], s[0:1]
	s_cbranch_execz .LBB0_954
	v_mul_f32_e64 v230, v164, v154
	v_mul_f32_e64 v231, v165, v155
	v_mul_f32_e64 v164, v164, v158
	v_mul_f32_e64 v165, v165, v159
	v_mul_f32_e64 v234, v160, v156
	v_mul_f32_e64 v235, v161, v157
	v_mul_f32_e64 v232, v160, v152
	v_mul_f32_e64 v233, v161, v153
	v_fma_f32 v230, v166, v158, -v230
	v_fma_f32 v231, v167, v159, -v231
	v_fma_f32 v244, v166, v154, v164
	v_fma_f32 v245, v167, v155, v165
	v_fma_f32 v166, v162, v152, v234
	v_fma_f32 v167, v163, v153, v235
	v_fma_f32 v232, v162, v156, -v232
	v_fma_f32 v233, v163, v157, -v233
	s_nop 0
	v_cvt_pk_bf16_f32 v164, v232, v233
	v_cvt_pk_bf16_f32 v165, v230, v231
	v_cvt_pk_bf16_f32 v166, v166, v167
	v_cvt_pk_bf16_f32 v167, v244, v245
	global_store_dwordx4 v[168:169], v[164:167], off

;     __device__ __forceinline__ void operator()(const f32x4 (&acc)[2][2][4][2], const Unit& u, int wr, int wc, int fr, int fq, const Pre&) const {
;     ...
;                 } else if (kind == KD_QI) {
; #pragma unroll
;                     for (int bj = 0; bj < 2; ++bj) {
;                         const f32x4 x1 = acc[ai][bj][m][0] * rs, x2 = acc[ai][bj][m][1] * rs;
;                         bf16_t* o = qib + (size_t)row * 1024 + 256 * (pn - TL_QI) + 128 * bj + cw;
;                         if (roti) st_bf16x8(o, x1 * cs[q] - x2 * sn[q], x2 * cs[q] + x1 * sn[q]); else st_bf16x8(o, x1, x2);
;                     }
.LBB0_956:
	s_andn2_b64 vcc, exec, s[0:1]
	s_cbranch_vccnz .LBB0_966
	v_mov_b32_e32 v164, v198
	v_mov_b32_e32 v165, v198
	v_readlane_b32 vcc_lo, v248, 9
	v_mul_f32_e64 v232, v150, v164
	v_mul_f32_e64 v233, v151, v165
	v_mul_f32_e64 v230, v146, v164
	v_mul_f32_e64 v231, v147, v165
	v_readlane_b32 vcc_hi, v248, 10
	s_and_saveexec_b64 s[0:1], vcc
	s_xor_b64 s[0:1], exec, s[0:1]
	s_cbranch_execz .LBB0_959
	v_cvt_pk_bf16_f32 v166, v162, v163
	v_cvt_pk_bf16_f32 v167, v232, v233
	v_cvt_pk_bf16_f32 v168, v160, v161
	v_cvt_pk_bf16_f32 v169, v230, v231
.LBB0_959:
	s_andn2_saveexec_b64 s[0:1], s[0:1]
	s_cbranch_execz .LBB0_961
	v_mul_f32_e64 v166, v160, v152
	v_mul_f32_e64 v167, v161, v153
	v_mul_f32_e64 v164, v230, v154
	v_mul_f32_e64 v165, v231, v155
	v_fma_f32 v166, v162, v156, -v166
	v_fma_f32 v167, v163, v157, -v167
	v_mul_f32_e64 v168, v230, v158
	v_mul_f32_e64 v169, v231, v159
	v_mul_f32_e64 v160, v160, v156
	v_mul_f32_e64 v161, v161, v157
	v_fma_f32 v164, v232, v158, -v164
	v_fma_f32 v165, v233, v159, -v165
	v_fma_f32 v230, v232, v154, v168
	v_fma_f32 v231, v233, v155, v169
	v_fma_f32 v160, v162, v152, v160
	v_fma_f32 v161, v163, v153, v161
	v_cvt_pk_bf16_f32 v166, v166, v167
	v_cvt_pk_bf16_f32 v167, v164, v165
	s_nop 0
	v_cvt_pk_bf16_f32 v168, v160, v161
	v_cvt_pk_bf16_f32 v169, v230, v231
.LBB0_961:
	s_or_b64 exec, exec, s[0:1]
	v_readlane_b32 s0, v248, 18
	v_lshlrev_b64 v[160:161], 11, v[184:185]
	v_readlane_b32 s1, v248, 19
	v_mul_f32_e64 v164, v136, v198
	v_mul_f32_e64 v165, v137, v199
	s_nop 0
	v_lshl_add_u64 v[160:161], s[0:1], 0, v[160:161]
	v_lshl_add_u64 v[160:161], s[28:29], 1, v[160:161]
	v_lshl_add_u64 v[230:231], v[172:173], 1, v[160:161]
	v_mov_b32_e32 v160, v198
	v_mov_b32_e32 v161, v198
	global_store_dwordx4 v[230:231], v[166:169], off
	v_mul_f32_e64 v234, v142, v160
	v_mul_f32_e64 v235, v143, v161
	v_mul_f32_e64 v232, v138, v160
	v_mul_f32_e64 v233, v139, v161
	v_mul_f32_e64 v166, v140, v198
	v_mul_f32_e64 v167, v141, v199
	s_and_saveexec_b64 s[0:1], vcc
	s_xor_b64 s[0:1], exec, s[0:1]
	s_cbranch_execz .LBB0_963
	v_cvt_pk_bf16_f32 v160, v166, v167
	v_cvt_pk_bf16_f32 v161, v234, v235
	v_cvt_pk_bf16_f32 v162, v164, v165
	v_cvt_pk_bf16_f32 v163, v232, v233
.LBB0_963:
	s_andn2_saveexec_b64 s[0:1], s[0:1]
	s_cbranch_execz .LBB0_965
	v_mul_f32_e64 v160, v232, v154
	v_mul_f32_e64 v161, v233, v155
	v_mul_f32_e64 v162, v164, v152
	v_mul_f32_e64 v163, v165, v153
	v_fma_f32 v168, v234, v158, -v160
	v_fma_f32 v169, v235, v159, -v161
	v_fma_f32 v160, v166, v156, -v162
	v_fma_f32 v161, v167, v157, -v163
	v_mul_f32_e64 v162, v232, v158
	v_mul_f32_e64 v163, v233, v159
	v_mul_f32_e64 v164, v164, v156
	v_mul_f32_e64 v165, v165, v157
	v_fma_f32 v232, v234, v154, v162
	v_fma_f32 v233, v235, v155, v163
	v_fma_f32 v162, v166, v152, v164
	v_fma_f32 v163, v167, v153, v165
	v_cvt_pk_bf16_f32 v160, v160, v161
	v_cvt_pk_bf16_f32 v161, v168, v169
	s_nop 0
	v_cvt_pk_bf16_f32 v162, v162, v163
	v_cvt_pk_bf16_f32 v163, v232, v233

;     __device__ __forceinline__ void operator()(const f32x4 (&acc)[2][2][4][2], const Unit& u, int wr, int wc, int fr, int fq, const Pre&) const {
;     ...
;                 } else if (kind == KD_V) {
; #pragma unroll
;                     for (int bj = 0; bj < 2; ++bj) st_bf16x8(vb + (size_t)row * 512 + 256 * (pn - TL_V) + 128 * bj + cw, acc[ai][bj][m][0] * rs, acc[ai][bj][m][1] * rs);
.LBB0_967:
	s_andn2_b64 vcc, exec, s[0:1]
	s_cbranch_vccnz .LBB0_969
	v_readlane_b32 s0, v249, 52
	v_lshlrev_b64 v[160:161], 10, v[184:185]
	v_readlane_b32 s1, v249, 53
	s_waitcnt vmcnt(0)
	v_mul_f32_e64 v162, v150, v198
	v_mul_f32_e64 v163, v151, v198
	v_mul_f32_e64 v166, v146, v198
	v_mul_f32_e64 v167, v147, v198
	v_lshl_add_u64 v[160:161], s[0:1], 0, v[160:161]
	v_lshl_add_u64 v[160:161], s[94:95], 1, v[160:161]
	v_lshl_add_u64 v[164:165], v[172:173], 1, v[160:161]
	v_mul_f32_e64 v160, v148, v198
	v_mul_f32_e64 v161, v149, v198
	v_mul_f32_e64 v168, v144, v198
	v_mul_f32_e64 v169, v145, v198
	v_cvt_pk_bf16_f32 v160, v160, v161
	v_cvt_pk_bf16_f32 v161, v162, v163
	s_nop 0
	v_cvt_pk_bf16_f32 v162, v168, v169
	v_cvt_pk_bf16_f32 v163, v166, v167
	global_store_dwordx4 v[164:165], v[160:163], off
	v_mul_f32_e64 v166, v138, v198
	v_mul_f32_e64 v167, v139, v198
	v_mul_f32_e64 v168, v136, v198
	v_mul_f32_e64 v169, v137, v198
	v_mul_f32_e64 v162, v142, v198
	v_mul_f32_e64 v163, v143, v198
	v_mul_f32_e64 v160, v140, v198
	v_mul_f32_e64 v161, v141, v198
	s_nop 0
	v_cvt_pk_bf16_f32 v160, v160, v161
	v_cvt_pk_bf16_f32 v161, v162, v163
	v_cvt_pk_bf16_f32 v162, v168, v169
	v_cvt_pk_bf16_f32 v163, v166, v167
	global_store_dwordx4 v[164:165], v[160:163], off offset:256

;     __device__ __forceinline__ void operator()(const f32x4 (&acc)[2][2][4][2], const Unit& u, int wr, int wc, int fr, int fq, const Pre&) const {
;     ...
;                 } else if (kind == KD_Q || kind == KD_K) {
;                     bf16_t* o = (kind == KD_Q) ? qb + (size_t)row * DM + 256 * (pn - TL_Q) + cw : kb + (size_t)row * 512 + 256 * (pn - TL_K) + cw;
; #pragma unroll
;                     for (int bj = 0; bj < 2; ++bj) {
;                         const f32x4 x1 = acc[ai][bj][m][0] * rs, x2 = acc[ai][bj][m][1] * rs;
;                         if (rotqk) st_bf16x8(o + 128 * bj, x1 * cs[q] - x2 * sn[q], x2 * cs[q] + x1 * sn[q]);
;                         else st_bf16x8(o + 128 * bj, x1, x2);
;                     }
.LBB0_970:
	s_andn2_b64 vcc, exec, s[0:1]
	s_cbranch_vccnz .LBB0_980
	s_waitcnt vmcnt(0)
	v_mul_f32_e64 v164, v150, v198
	v_mul_f32_e64 v165, v151, v198
	v_mul_f32_e64 v166, v148, v198
	v_mul_f32_e64 v167, v149, v198
	v_mul_f32_e64 v168, v146, v198
	v_mul_f32_e64 v169, v147, v198
	v_mul_f32_e64 v230, v144, v198
	v_mul_f32_e64 v231, v145, v198
	s_mov_b64 s[0:1], -1
	s_and_b64 vcc, exec, s[92:93]
	s_cbranch_vccz .LBB0_973
	v_cvt_pk_bf16_f32 v160, v166, v167
	v_cvt_pk_bf16_f32 v161, v164, v165
	v_cvt_pk_bf16_f32 v162, v230, v231
	v_cvt_pk_bf16_f32 v163, v168, v169
	s_mov_b64 s[0:1], 0
.LBB0_973:
	s_andn2_b64 vcc, exec, s[0:1]
	s_cbranch_vccnz .LBB0_975
	v_mul_f32_e64 v160, v168, v154
	v_mul_f32_e64 v161, v169, v155
	v_mul_f32_e64 v162, v230, v152
	v_mul_f32_e64 v163, v231, v153
	v_fma_f32 v232, v164, v158, -v160
	v_fma_f32 v233, v165, v159, -v161
	v_fma_f32 v160, v166, v156, -v162
	v_fma_f32 v161, v167, v157, -v163
	v_mul_f32_e64 v162, v168, v158
	v_mul_f32_e64 v163, v169, v159
	v_mul_f32_e64 v168, v230, v156
	v_mul_f32_e64 v169, v231, v157
	v_fma_f32 v164, v164, v154, v162
	v_fma_f32 v165, v165, v155, v163
	v_fma_f32 v162, v166, v152, v168
	v_fma_f32 v163, v167, v153, v169
	v_cvt_pk_bf16_f32 v160, v160, v161
	v_cvt_pk_bf16_f32 v161, v232, v233
	s_nop 0
	v_cvt_pk_bf16_f32 v162, v162, v163
	v_cvt_pk_bf16_f32 v163, v164, v165
.LBB0_975:
	s_and_b64 s[0:1], s[90:91], exec
	v_readlane_b32 s0, v249, 49
	v_readlane_b32 s1, v249, 51
	s_cselect_b32 s1, s0, s1
	v_readlane_b32 s0, v249, 48
	v_readlane_b32 s2, v249, 50
	s_cselect_b32 s35, 12, 10
	s_cselect_b32 s0, s0, s2
	v_lshlrev_b64 v[164:165], s35, v[184:185]
	s_cselect_b32 s3, s34, s30
	s_cselect_b32 s2, s31, s81
	v_lshl_add_u64 v[164:165], s[0:1], 0, v[164:165]
	v_lshl_add_u64 v[164:165], s[2:3], 1, v[164:165]
	v_lshl_add_u64 v[164:165], v[172:173], 1, v[164:165]
	v_mov_b32_e32 v199, v198
	global_store_dwordx4 v[164:165], v[160:163], off
	v_mul_f32_e64 v168, v140, v198
	v_mul_f32_e64 v169, v141, v199
	v_mul_f32_e64 v232, v136, v198
	v_mul_f32_e64 v233, v137, v199
	v_mov_b32_e32 v160, v198
	v_mov_b32_e32 v161, v198
	v_mul_f32_e64 v166, v142, v160
	v_mul_f32_e64 v167, v143, v161
	v_mul_f32_e64 v230, v138, v160
	v_mul_f32_e64 v231, v139, v161
	s_andn2_b64 vcc, exec, s[92:93]
	s_mov_b64 s[0:1], -1
	s_cbranch_vccnz .LBB0_977
	s_mov_b64 s[0:1], 0
	v_cvt_pk_bf16_f32 v160, v168, v169
	v_cvt_pk_bf16_f32 v161, v166, v167
	v_cvt_pk_bf16_f32 v162, v232, v233
	v_cvt_pk_bf16_f32 v163, v230, v231
.LBB0_977:
	s_andn2_b64 vcc, exec, s[0:1]
	s_cbranch_vccnz .LBB0_979
	v_mul_f32_e64 v160, v230, v154
	v_mul_f32_e64 v161, v231, v155
	v_mul_f32_e64 v162, v232, v152
	v_mul_f32_e64 v163, v233, v153
	v_fma_f32 v234, v166, v158, -v160
	v_fma_f32 v235, v167, v159, -v161
	v_fma_f32 v160, v168, v156, -v162
	v_fma_f32 v161, v169, v157, -v163
	v_mul_f32_e64 v158, v230, v158
	v_mul_f32_e64 v159, v231, v159
	v_mul_f32_e64 v156, v232, v156
	v_mul_f32_e64 v157, v233, v157
	v_fma_f32 v154, v166, v154, v158
	v_fma_f32 v155, v167, v155, v159
	v_fma_f32 v152, v168, v152, v156
	v_fma_f32 v153, v169, v153, v157
	v_cvt_pk_bf16_f32 v160, v160, v161
	v_cvt_pk_bf16_f32 v161, v234, v235
	s_nop 0
	v_cvt_pk_bf16_f32 v162, v152, v153
	v_cvt_pk_bf16_f32 v163, v154, v155

; __device__ __forceinline__ f32x4 sigmoid4(const f32x4& x, float s) {
;     f32x4 z = x * (s * -1.4426950408889634f), e;
; #pragma unroll
;     for (int j = 0; j < 4; ++j) e[j] = __builtin_amdgcn_exp2f(z[j]);
;     e = e + 1.0f;
; #pragma unroll
;     for (int j = 0; j < 4; ++j) e[j] = __builtin_amdgcn_rcpf(e[j]);
;     return e;
; }
;     __device__ __forceinline__ void operator()(const f32x4 (&acc)[2][2][4][2], const Unit& u, int wr, int wc, int fr, int fq, const Pre&) const {
;     ...
;                 } else if (kind == KD_A) {
;                     st_bf16x8(abuf + (size_t)row * DM + 128 * (pn - TL_A) + cw, acc[ai][0][m][0] * rs * sigmoid4(acc[ai][1][m][0], rs), acc[ai][0][m][1] * rs * sigmoid4(acc[ai][1][m][1], rs));
.LBB0_984:
	s_waitcnt vmcnt(0)
	v_lshlrev_b64 v[152:153], 12, v[184:185]
	v_lshl_add_u64 v[152:153], s[12:13], 0, v[152:153]
	v_lshl_add_u64 v[152:153], s[88:89], 1, v[152:153]
	v_mul_f32_e32 v163, 0xbfb8aa3b, v198
	v_lshl_add_u64 v[156:157], v[172:173], 1, v[152:153]
	v_mul_f32_e32 v152, v140, v163
	v_mul_f32_e32 v153, v141, v163
	v_mul_f32_e32 v154, v142, v163
	v_mul_f32_e32 v155, v143, v163
	v_exp_f32_e32 v152, v152
	v_exp_f32_e32 v154, v154
	v_exp_f32_e32 v155, v155
	v_exp_f32_e32 v153, v153
	v_mul_f32_e32 v162, v136, v163
	v_mul_f32_e32 v166, v137, v163
	v_add_f32_e64 v154, v154, 1.0
	v_add_f32_e64 v155, v155, 1.0
	v_add_f32_e64 v152, v152, 1.0
	v_add_f32_e64 v153, v153, 1.0
	v_mul_f32_e32 v164, v138, v163
	v_mul_f32_e32 v163, v139, v163
	v_rcp_f32_e32 v152, v152
	v_rcp_f32_e32 v153, v153
	v_rcp_f32_e32 v154, v154
	v_rcp_f32_e32 v155, v155
	v_exp_f32_e32 v162, v162
	v_exp_f32_e32 v164, v164
	v_exp_f32_e32 v165, v163
	v_exp_f32_e32 v163, v166
	v_mul_f32_e64 v158, v150, v198
	v_mul_f32_e64 v159, v151, v198
	v_mul_f32_e64 v160, v148, v198
	v_mul_f32_e64 v161, v149, v198
	v_mul_f32_e64 v154, v158, v154
	v_mul_f32_e64 v155, v159, v155
	v_mul_f32_e64 v152, v160, v152
	v_mul_f32_e64 v153, v161, v153
	v_add_f32_e64 v158, v164, 1.0
	v_add_f32_e64 v159, v165, 1.0
	v_add_f32_e64 v160, v162, 1.0
	v_add_f32_e64 v161, v163, 1.0
	v_rcp_f32_e32 v158, v158
	v_rcp_f32_e32 v160, v160
	v_rcp_f32_e32 v159, v159
	v_rcp_f32_e32 v161, v161
	v_mul_f32_e64 v162, v146, v198
	v_mul_f32_e64 v163, v147, v198
	v_mul_f32_e64 v164, v144, v198
	v_mul_f32_e64 v165, v145, v198
	v_mul_f32_e64 v158, v162, v158
	v_mul_f32_e64 v159, v163, v159
	v_mul_f32_e64 v160, v164, v160
	v_mul_f32_e64 v161, v165, v161
	v_cvt_pk_bf16_f32 v152, v152, v153
	v_cvt_pk_bf16_f32 v153, v154, v155
	s_nop 0
	v_cvt_pk_bf16_f32 v154, v160, v161
	v_cvt_pk_bf16_f32 v155, v158, v159
	global_store_dwordx4 v[156:157], v[152:155], off

;     __device__ __forceinline__ void operator()(const f32x4 (&acc)[2][2][4][2], const Unit& u, int wr, int wc, int fr, int fq, const Pre&) const {
;     ...
;                 if (kind == KD_KVX) {
;                     bf16_t* o = (pn < 2 ? kx : vx) + (size_t)row * 512 + 256 * (pn & 1) + cw;
; #pragma unroll
;                     for (int bj = 0; bj < 2; ++bj) st_bf16x8(o + 128 * bj, acc[ai][bj][m][0] * rs, acc[ai][bj][m][1] * rs);
;     ...
;                 } else if (kind == KD_G) {
; #pragma unroll
;                     for (int bj = 0; bj < 2; ++bj)
;                         st_bf16x8(gabuf + (size_t)row * DM + 256 * (pn - TL_G) + 128 * bj + cw, sigmoid4(acc[ai][bj][m][0], rs), sigmoid4(acc[ai][bj][m][1], rs));
.LBB0_986:
	s_and_b32 s35, s4, 0x100
	s_and_b64 vcc, exec, s[0:1]
	s_cbranch_vccz .LBB0_988
	s_and_b64 s[0:1], s[86:87], exec
	s_cselect_b32 s1, s11, s15
	s_cselect_b32 s0, s10, s14
	s_waitcnt vmcnt(0)
	v_lshlrev_b64 v[152:153], 10, v[184:185]
	v_lshl_add_u64 v[152:153], s[0:1], 0, v[152:153]
	s_lshl_b32 s4, s35, 1
	v_lshl_add_u64 v[152:153], v[152:153], 0, s[4:5]
	v_lshl_add_u64 v[152:153], v[172:173], 1, v[152:153]
	v_mul_f32_e64 v150, v150, v198
	v_mul_f32_e64 v151, v151, v198
	v_mul_f32_e64 v148, v148, v198
	v_mul_f32_e64 v149, v149, v198
	v_mul_f32_e64 v154, v146, v198
	v_mul_f32_e64 v155, v147, v198
	v_mul_f32_e64 v146, v144, v198
	v_mul_f32_e64 v147, v145, v198
	v_cvt_pk_bf16_f32 v144, v148, v149
	v_cvt_pk_bf16_f32 v145, v150, v151
	v_mul_f32_e64 v142, v142, v198
	v_mul_f32_e64 v143, v143, v198
	v_cvt_pk_bf16_f32 v146, v146, v147
	v_cvt_pk_bf16_f32 v147, v154, v155
	global_store_dwordx4 v[152:153], v[144:147], off
	v_mul_f32_e64 v140, v140, v198
	v_mul_f32_e64 v141, v141, v198
	s_nop 0
	v_mul_f32_e64 v144, v138, v198
	v_mul_f32_e64 v145, v139, v198
	v_mul_f32_e64 v138, v136, v198
	v_mul_f32_e64 v139, v137, v198
	v_cvt_pk_bf16_f32 v136, v140, v141
	v_cvt_pk_bf16_f32 v137, v142, v143
	s_nop 0
	v_cvt_pk_bf16_f32 v138, v138, v139
	v_cvt_pk_bf16_f32 v139, v144, v145
	global_store_dwordx4 v[152:153], v[136:139], off offset:256
.LBB0_988:
	s_nop 1
	v_cndmask_b32_e64 v136, 0, 1, s[56:57]
	v_cmp_ne_u32_e64 s[0:1], 1, v136
	s_andn2_b64 vcc, exec, s[56:57]
	s_mov_b64 s[2:3], -1
	s_cbranch_vccnz .LBB0_1037
	s_mov_b64 vcc, -1
	s_mov_b64 s[2:3], 0
	s_cmp_lt_i32 s7, 1
	s_mov_b64 s[56:57], 0
	s_cbranch_scc1 .LBB0_1104
	s_cmp_gt_i32 s7, 1
	s_cbranch_scc0 .LBB0_994
	s_cmp_eq_u32 s7, 2
	s_mov_b64 s[56:57], -1
	s_cbranch_scc0 .LBB0_993
	v_ashrrev_i32_e32 v197, 31, v196
	v_readlane_b32 s56, v249, 46
	v_lshlrev_b64 v[136:137], 12, v[196:197]
	v_readlane_b32 s57, v249, 47
	s_waitcnt vmcnt(0)
	v_mul_f32_e32 v142, 0xbfb8aa3b, v194
	v_mul_f32_e32 v138, v126, v142
	v_lshl_add_u64 v[136:137], s[56:57], 0, v[136:137]
	v_lshl_add_u64 v[136:137], s[38:39], 1, v[136:137]
	v_mul_f32_e32 v139, v127, v142
	v_lshl_add_u64 v[140:141], v[172:173], 1, v[136:137]
	v_mul_f32_e32 v136, v124, v142
	v_mul_f32_e32 v137, v125, v142
	v_exp_f32_e32 v138, v138
	v_exp_f32_e32 v139, v139
	v_exp_f32_e32 v136, v136
	v_exp_f32_e32 v137, v137
	s_mov_b64 s[56:57], 0
	v_add_f32_e64 v138, v138, 1.0
	v_add_f32_e64 v139, v139, 1.0
	v_add_f32_e64 v136, v136, 1.0
	v_add_f32_e64 v137, v137, 1.0
	v_rcp_f32_e32 v145, v138
	v_rcp_f32_e32 v146, v139
	v_mul_f32_e32 v138, v122, v142
	v_mul_f32_e32 v139, v123, v142
	v_rcp_f32_e32 v143, v136
	v_rcp_f32_e32 v144, v137
	v_mul_f32_e32 v136, v120, v142
	v_mul_f32_e32 v137, v121, v142
	v_exp_f32_e32 v138, v138
	v_exp_f32_e32 v139, v139
	v_exp_f32_e32 v136, v136
	v_exp_f32_e32 v137, v137
	v_add_f32_e64 v138, v138, 1.0
	v_add_f32_e64 v139, v139, 1.0
	s_nop 0
	v_rcp_f32_e32 v139, v139
	v_add_f32_e64 v136, v136, 1.0
	v_add_f32_e64 v137, v137, 1.0
	v_rcp_f32_e32 v149, v138
	v_rcp_f32_e32 v147, v136
	v_rcp_f32_e32 v148, v137
	v_cvt_pk_bf16_f32 v136, v143, v144
	v_cvt_pk_bf16_f32 v137, v145, v146
	v_cvt_pk_bf16_f32 v138, v147, v148
	v_cvt_pk_bf16_f32 v139, v149, v139
	global_store_dwordx4 v[140:141], v[136:139], off
	s_nop 1
	v_mul_f32_e32 v138, v118, v142
	v_mul_f32_e32 v139, v119, v142
	v_mul_f32_e32 v136, v116, v142
	v_mul_f32_e32 v137, v117, v142
	v_exp_f32_e32 v138, v138
	v_exp_f32_e32 v139, v139
	v_exp_f32_e32 v136, v136
	v_exp_f32_e32 v137, v137
	v_add_f32_e64 v138, v138, 1.0
	v_add_f32_e64 v139, v139, 1.0
	s_nop 0
	v_rcp_f32_e32 v145, v138
	v_add_f32_e64 v136, v136, 1.0
	v_add_f32_e64 v137, v137, 1.0
	v_rcp_f32_e32 v146, v139
	v_mul_f32_e32 v138, v114, v142
	v_mul_f32_e32 v139, v115, v142
	v_rcp_f32_e32 v143, v136
	v_rcp_f32_e32 v144, v137
	v_mul_f32_e32 v136, v112, v142
	v_mul_f32_e32 v137, v113, v142
	v_exp_f32_e32 v138, v138
	v_exp_f32_e32 v139, v139
	v_exp_f32_e32 v136, v136
	v_exp_f32_e32 v137, v137
	v_add_f32_e64 v138, v138, 1.0
	v_add_f32_e64 v139, v139, 1.0
	s_nop 0
	v_rcp_f32_e32 v139, v139
	v_add_f32_e64 v136, v136, 1.0
	v_add_f32_e64 v137, v137, 1.0
	v_rcp_f32_e32 v148, v138
	v_rcp_f32_e32 v142, v136
	v_rcp_f32_e32 v147, v137
	v_cvt_pk_bf16_f32 v136, v143, v144
	v_cvt_pk_bf16_f32 v137, v145, v146
	v_cvt_pk_bf16_f32 v138, v142, v147
	v_cvt_pk_bf16_f32 v139, v148, v139
	global_store_dwordx4 v[140:141], v[136:139], off offset:256

;     __device__ __forceinline__ void operator()(const f32x4 (&acc)[2][2][4][2], const Unit& u, int wr, int wc, int fr, int fq, const Pre&) const {
;     ...
;                 } else if (kind == KD_P) {
;                     const float r2 = rs * rs;
;                     st_bf16x8(pbuf + (size_t)row * DM + 128 * (pn - TL_P) + cw, acc[ai][0][m][0] * acc[ai][1][m][0] * r2, acc[ai][0][m][1] * acc[ai][1][m][1] * r2);
.LBB0_994:
	s_and_b64 vcc, exec, vcc
	s_cbranch_vccz .LBB0_996
	v_ashrrev_i32_e32 v197, 31, v196
	v_readlane_b32 vcc_lo, v249, 44
	v_lshlrev_b64 v[138:139], 12, v[196:197]
	v_readlane_b32 vcc_hi, v249, 45
	s_waitcnt vmcnt(0)
	v_mul_f32_e32 v136, v194, v194
	v_mul_f32_e64 v142, v124, v116
	v_mul_f32_e64 v143, v125, v117
	v_lshl_add_u64 v[138:139], vcc, 0, v[138:139]
	v_lshl_add_u64 v[138:139], s[42:43], 1, v[138:139]
	v_lshl_add_u64 v[140:141], v[172:173], 1, v[138:139]
	v_mul_f32_e64 v138, v126, v118
	v_mul_f32_e64 v139, v127, v119
	v_mul_f32_e64 v144, v122, v114
	v_mul_f32_e64 v145, v123, v115
	v_mul_f32_e64 v138, v138, v136
	v_mul_f32_e64 v139, v139, v136
	v_mul_f32_e64 v146, v120, v112
	v_mul_f32_e64 v147, v121, v113
	v_mul_f32_e64 v142, v142, v136
	v_mul_f32_e64 v143, v143, v136
	v_mul_f32_e64 v144, v144, v136
	v_mul_f32_e64 v145, v145, v136
	v_mul_f32_e64 v146, v146, v136
	v_mul_f32_e64 v147, v147, v136
	v_cvt_pk_bf16_f32 v136, v142, v143
	v_cvt_pk_bf16_f32 v137, v138, v139
	s_nop 0
	v_cvt_pk_bf16_f32 v138, v146, v147
	v_cvt_pk_bf16_f32 v139, v144, v145
	global_store_dwordx4 v[140:141], v[136:139], off

;     __device__ __forceinline__ void operator()(const f32x4 (&acc)[2][2][4][2], const Unit& u, int wr, int wc, int fr, int fq, const Pre&) const {
;     ...
;                 } else {
;                     const f32x4 x1 = acc[ai][0][m][0] * rs, x2 = acc[ai][0][m][1] * rs;
;                     if (wc < 2) {
;                         if (roti) st_bf16x8(kib + (size_t)row * 64 + cw, x1 * cs[q] - x2 * sn[q], x2 * cs[q] + x1 * sn[q]);
;                         else st_bf16x8(kib + (size_t)row * 64 + cw, x1, x2);
;                     } else if (wc == 2 && fq < 2) {
;                         *(f32x4*)(wib + (size_t)row * 16 + 8 * fq) = x1 * 0.03125f; *(f32x4*)(wib + (size_t)row * 16 + 8 * fq + 4) = x2 * 0.03125f;
;                     }
.LBB0_998:
	s_andn2_b64 vcc, exec, s[64:65]
	s_mov_b64 s[2:3], -1
	s_cbranch_vccnz .LBB0_1026
	s_andn2_b64 vcc, exec, s[58:59]
	s_cbranch_vccnz .LBB0_1023
	v_readlane_b32 s56, v249, 63
	s_waitcnt vmcnt(0)
	v_mov_b32_e32 v195, v194
	v_readlane_b32 s57, v248, 0
	s_andn2_b64 vcc, exec, s[56:57]
	v_mul_f32_e64 v138, v124, v194
	v_mul_f32_e64 v139, v125, v195
	v_mul_f32_e64 v136, v120, v194
	v_mul_f32_e64 v137, v121, v195
	s_cbranch_vccnz .LBB0_1012
	v_readlane_b32 s2, v248, 24
	v_mov_b32_e32 v140, v194
	v_mov_b32_e32 v141, v194
	v_readlane_b32 s3, v248, 25
	v_mul_f32_e64 v142, v126, v140
	v_mul_f32_e64 v143, v127, v141
	v_mul_f32_e64 v140, v122, v140
	v_mul_f32_e64 v141, v123, v141
	s_andn2_b64 vcc, exec, s[2:3]
	s_mov_b64 s[2:3], -1
	s_cbranch_vccnz .LBB0_1005
	s_mov_b64 s[2:3], exec
	v_readlane_b32 s56, v248, 7
	v_readlane_b32 s57, v248, 8
	s_and_b64 s[56:57], s[2:3], s[56:57]
	s_mov_b64 exec, s[56:57]
	s_cbranch_execz .LBB0_1004
	v_ashrrev_i32_e32 v197, 31, v196
	v_readlane_b32 s56, v249, 56
	v_lshlrev_b64 v[148:149], 6, v[196:197]
	v_readlane_b32 s57, v249, 57
	s_mov_b32 s4, 0x3d000000
	v_mul_f32_e64 v146, v142, s4
	v_mul_f32_e64 v147, v143, s4
	v_lshl_add_u64 v[148:149], s[56:57], 0, v[148:149]
	v_mul_f32_e64 v144, v138, s4
	v_mul_f32_e64 v145, v139, s4
	v_lshl_add_u64 v[148:149], v[174:175], 2, v[148:149]
	global_store_dwordx4 v[148:149], v[144:147], off
	s_nop 1
	v_mul_f32_e64 v146, v140, s4
	v_mul_f32_e64 v147, v141, s4
	v_mul_f32_e64 v144, v136, s4
	v_mul_f32_e64 v145, v137, s4
	global_store_dwordx4 v[148:149], v[144:147], off offset:16

;     __device__ __forceinline__ void operator()(const f32x4 (&acc)[2][2][4][2], const Unit& u, int wr, int wc, int fr, int fq, const Pre&) const {
;     ...
;                 } else {
;                     const f32x4 x1 = acc[ai][0][m][0] * rs, x2 = acc[ai][0][m][1] * rs;
;                     if (wc < 2) {
;                         if (roti) st_bf16x8(kib + (size_t)row * 64 + cw, x1 * cs[q] - x2 * sn[q], x2 * cs[q] + x1 * sn[q]);
;                         else st_bf16x8(kib + (size_t)row * 64 + cw, x1, x2);
.LBB0_1008:
	s_andn2_saveexec_b64 s[2:3], s[2:3]
	s_cbranch_execz .LBB0_1010
	v_mul_f32_e64 v146, v140, v130
	v_mul_f32_e64 v147, v141, v131
	v_mul_f32_e64 v140, v140, v134
	v_mul_f32_e64 v141, v141, v135
	v_mul_f32_e64 v150, v136, v132
	v_mul_f32_e64 v151, v137, v133
	v_mul_f32_e64 v148, v136, v128
	v_mul_f32_e64 v149, v137, v129
	v_fma_f32 v146, v142, v134, -v146
	v_fma_f32 v147, v143, v135, -v147
	v_fma_f32 v152, v142, v130, v140
	v_fma_f32 v153, v143, v131, v141
	v_fma_f32 v142, v138, v128, v150
	v_fma_f32 v143, v139, v129, v151
	v_fma_f32 v148, v138, v132, -v148
	v_fma_f32 v149, v139, v133, -v149
	s_nop 0
	v_cvt_pk_bf16_f32 v140, v148, v149
	v_cvt_pk_bf16_f32 v141, v146, v147
	v_cvt_pk_bf16_f32 v142, v142, v143
	v_cvt_pk_bf16_f32 v143, v152, v153
	global_store_dwordx4 v[144:145], v[140:143], off

;     __device__ __forceinline__ void operator()(const f32x4 (&acc)[2][2][4][2], const Unit& u, int wr, int wc, int fr, int fq, const Pre&) const {
;     ...
;                 } else if (kind == KD_QI) {
; #pragma unroll
;                     for (int bj = 0; bj < 2; ++bj) {
;                         const f32x4 x1 = acc[ai][bj][m][0] * rs, x2 = acc[ai][bj][m][1] * rs;
;                         bf16_t* o = qib + (size_t)row * 1024 + 256 * (pn - TL_QI) + 128 * bj + cw;
;                         if (roti) st_bf16x8(o, x1 * cs[q] - x2 * sn[q], x2 * cs[q] + x1 * sn[q]); else st_bf16x8(o, x1, x2);
;                     }
.LBB0_1012:
	s_andn2_b64 vcc, exec, s[2:3]
	s_cbranch_vccnz .LBB0_1022
	v_mov_b32_e32 v140, v194
	v_mov_b32_e32 v141, v194
	v_readlane_b32 vcc_lo, v248, 9
	v_mul_f32_e64 v148, v126, v140
	v_mul_f32_e64 v149, v127, v141
	v_mul_f32_e64 v146, v122, v140
	v_mul_f32_e64 v147, v123, v141
	v_readlane_b32 vcc_hi, v248, 10
	s_and_saveexec_b64 s[2:3], vcc
	s_xor_b64 s[2:3], exec, s[2:3]
	s_cbranch_execz .LBB0_1015
	v_cvt_pk_bf16_f32 v142, v138, v139
	v_cvt_pk_bf16_f32 v143, v148, v149
	v_cvt_pk_bf16_f32 v144, v136, v137
	v_cvt_pk_bf16_f32 v145, v146, v147
.LBB0_1015:
	s_andn2_saveexec_b64 s[2:3], s[2:3]
	s_cbranch_execz .LBB0_1017
	v_mul_f32_e64 v142, v136, v128
	v_mul_f32_e64 v143, v137, v129
	v_mul_f32_e64 v140, v146, v130
	v_mul_f32_e64 v141, v147, v131
	v_fma_f32 v142, v138, v132, -v142
	v_fma_f32 v143, v139, v133, -v143
	v_mul_f32_e64 v144, v146, v134
	v_mul_f32_e64 v145, v147, v135
	v_mul_f32_e64 v136, v136, v132
	v_mul_f32_e64 v137, v137, v133
	v_fma_f32 v140, v148, v134, -v140
	v_fma_f32 v141, v149, v135, -v141
	v_fma_f32 v146, v148, v130, v144
	v_fma_f32 v147, v149, v131, v145
	v_fma_f32 v136, v138, v128, v136
	v_fma_f32 v137, v139, v129, v137
	v_cvt_pk_bf16_f32 v142, v142, v143
	v_cvt_pk_bf16_f32 v143, v140, v141
	s_nop 0
	v_cvt_pk_bf16_f32 v144, v136, v137
	v_cvt_pk_bf16_f32 v145, v146, v147
.LBB0_1017:
	s_or_b64 exec, exec, s[2:3]
	v_ashrrev_i32_e32 v197, 31, v196
	v_readlane_b32 s2, v248, 18
	v_lshlrev_b64 v[136:137], 11, v[196:197]
	v_readlane_b32 s3, v248, 19
	v_mul_f32_e64 v140, v112, v194
	v_mul_f32_e64 v141, v113, v195
	s_nop 0
	v_lshl_add_u64 v[136:137], s[2:3], 0, v[136:137]
	v_lshl_add_u64 v[136:137], s[28:29], 1, v[136:137]
	v_lshl_add_u64 v[146:147], v[172:173], 1, v[136:137]
	v_mov_b32_e32 v136, v194
	v_mov_b32_e32 v137, v194
	global_store_dwordx4 v[146:147], v[142:145], off
	v_mul_f32_e64 v150, v118, v136
	v_mul_f32_e64 v151, v119, v137
	v_mul_f32_e64 v148, v114, v136
	v_mul_f32_e64 v149, v115, v137
	v_mul_f32_e64 v142, v116, v194
	v_mul_f32_e64 v143, v117, v195
	s_and_saveexec_b64 s[2:3], vcc
	s_xor_b64 s[2:3], exec, s[2:3]
	s_cbranch_execz .LBB0_1019
	v_cvt_pk_bf16_f32 v136, v142, v143
	v_cvt_pk_bf16_f32 v137, v150, v151
	v_cvt_pk_bf16_f32 v138, v140, v141
	v_cvt_pk_bf16_f32 v139, v148, v149
.LBB0_1019:
	s_andn2_saveexec_b64 s[2:3], s[2:3]
	s_cbranch_execz .LBB0_1021
	v_mul_f32_e64 v136, v148, v130
	v_mul_f32_e64 v137, v149, v131
	v_mul_f32_e64 v138, v140, v128
	v_mul_f32_e64 v139, v141, v129
	v_fma_f32 v144, v150, v134, -v136
	v_fma_f32 v145, v151, v135, -v137
	v_fma_f32 v136, v142, v132, -v138
	v_fma_f32 v137, v143, v133, -v139
	v_mul_f32_e64 v138, v148, v134
	v_mul_f32_e64 v139, v149, v135
	v_mul_f32_e64 v140, v140, v132
	v_mul_f32_e64 v141, v141, v133
	v_fma_f32 v148, v150, v130, v138
	v_fma_f32 v149, v151, v131, v139
	v_fma_f32 v138, v142, v128, v140
	v_fma_f32 v139, v143, v129, v141
	v_cvt_pk_bf16_f32 v136, v136, v137
	v_cvt_pk_bf16_f32 v137, v144, v145
	s_nop 0
	v_cvt_pk_bf16_f32 v138, v138, v139
	v_cvt_pk_bf16_f32 v139, v148, v149

;     __device__ __forceinline__ void operator()(const f32x4 (&acc)[2][2][4][2], const Unit& u, int wr, int wc, int fr, int fq, const Pre&) const {
;     ...
;                 } else if (kind == KD_V) {
; #pragma unroll
;                     for (int bj = 0; bj < 2; ++bj) st_bf16x8(vb + (size_t)row * 512 + 256 * (pn - TL_V) + 128 * bj + cw, acc[ai][bj][m][0] * rs, acc[ai][bj][m][1] * rs);
.LBB0_1023:
	s_andn2_b64 vcc, exec, s[2:3]
	s_cbranch_vccnz .LBB0_1025
	v_ashrrev_i32_e32 v197, 31, v196
	v_readlane_b32 s2, v249, 52
	v_lshlrev_b64 v[136:137], 10, v[196:197]
	v_readlane_b32 s3, v249, 53
	s_waitcnt vmcnt(0)
	v_mul_f32_e64 v138, v126, v194
	v_mul_f32_e64 v139, v127, v194
	v_mul_f32_e64 v142, v122, v194
	v_mul_f32_e64 v143, v123, v194
	v_lshl_add_u64 v[136:137], s[2:3], 0, v[136:137]
	v_lshl_add_u64 v[136:137], s[94:95], 1, v[136:137]
	v_lshl_add_u64 v[140:141], v[172:173], 1, v[136:137]
	v_mul_f32_e64 v136, v124, v194
	v_mul_f32_e64 v137, v125, v194
	v_mul_f32_e64 v144, v120, v194
	v_mul_f32_e64 v145, v121, v194
	v_cvt_pk_bf16_f32 v136, v136, v137
	v_cvt_pk_bf16_f32 v137, v138, v139
	s_nop 0
	v_cvt_pk_bf16_f32 v138, v144, v145
	v_cvt_pk_bf16_f32 v139, v142, v143
	global_store_dwordx4 v[140:141], v[136:139], off
	v_mul_f32_e64 v142, v114, v194
	v_mul_f32_e64 v143, v115, v194
	v_mul_f32_e64 v144, v112, v194
	v_mul_f32_e64 v145, v113, v194
	v_mul_f32_e64 v138, v118, v194
	v_mul_f32_e64 v139, v119, v194
	v_mul_f32_e64 v136, v116, v194
	v_mul_f32_e64 v137, v117, v194
	s_nop 0
	v_cvt_pk_bf16_f32 v136, v136, v137
	v_cvt_pk_bf16_f32 v137, v138, v139
	v_cvt_pk_bf16_f32 v138, v144, v145
	v_cvt_pk_bf16_f32 v139, v142, v143
	global_store_dwordx4 v[140:141], v[136:139], off offset:256

;     __device__ __forceinline__ void operator()(const f32x4 (&acc)[2][2][4][2], const Unit& u, int wr, int wc, int fr, int fq, const Pre&) const {
;     ...
;                 } else if (kind == KD_Q || kind == KD_K) {
;                     bf16_t* o = (kind == KD_Q) ? qb + (size_t)row * DM + 256 * (pn - TL_Q) + cw : kb + (size_t)row * 512 + 256 * (pn - TL_K) + cw;
; #pragma unroll
;                     for (int bj = 0; bj < 2; ++bj) {
;                         const f32x4 x1 = acc[ai][bj][m][0] * rs, x2 = acc[ai][bj][m][1] * rs;
;                         if (rotqk) st_bf16x8(o + 128 * bj, x1 * cs[q] - x2 * sn[q], x2 * cs[q] + x1 * sn[q]);
;                         else st_bf16x8(o + 128 * bj, x1, x2);
;                     }
.LBB0_1026:
	s_andn2_b64 vcc, exec, s[2:3]
	s_cbranch_vccnz .LBB0_1036
	v_cndmask_b32_e64 v136, 0, 1, s[92:93]
	s_waitcnt vmcnt(0)
	v_mul_f32_e64 v140, v126, v194
	v_mul_f32_e64 v141, v127, v194
	v_mul_f32_e64 v142, v124, v194
	v_mul_f32_e64 v143, v125, v194
	v_mul_f32_e64 v144, v122, v194
	v_mul_f32_e64 v145, v123, v194
	v_mul_f32_e64 v146, v120, v194
	v_mul_f32_e64 v147, v121, v194
	v_cmp_ne_u32_e64 s[2:3], 1, v136
	s_andn2_b64 vcc, exec, s[92:93]
	s_mov_b64 s[56:57], -1
	s_cbranch_vccnz .LBB0_1029
	s_mov_b64 s[56:57], 0
	v_cvt_pk_bf16_f32 v136, v142, v143
	v_cvt_pk_bf16_f32 v137, v140, v141
	v_cvt_pk_bf16_f32 v138, v146, v147
	v_cvt_pk_bf16_f32 v139, v144, v145
.LBB0_1029:
	s_andn2_b64 vcc, exec, s[56:57]
	s_cbranch_vccnz .LBB0_1031
	v_mul_f32_e64 v136, v144, v130
	v_mul_f32_e64 v137, v145, v131
	v_mul_f32_e64 v138, v146, v128
	v_mul_f32_e64 v139, v147, v129
	v_fma_f32 v148, v140, v134, -v136
	v_fma_f32 v149, v141, v135, -v137
	v_fma_f32 v136, v142, v132, -v138
	v_fma_f32 v137, v143, v133, -v139
	v_mul_f32_e64 v138, v144, v134
	v_mul_f32_e64 v139, v145, v135
	v_mul_f32_e64 v144, v146, v132
	v_mul_f32_e64 v145, v147, v133
	v_fma_f32 v140, v140, v130, v138
	v_fma_f32 v141, v141, v131, v139
	v_fma_f32 v138, v142, v128, v144
	v_fma_f32 v139, v143, v129, v145
	v_cvt_pk_bf16_f32 v136, v136, v137
	v_cvt_pk_bf16_f32 v137, v148, v149
	s_nop 0
	v_cvt_pk_bf16_f32 v138, v138, v139
	v_cvt_pk_bf16_f32 v139, v140, v141
.LBB0_1031:
	s_and_b64 s[56:57], s[90:91], exec
	v_readlane_b32 s4, v249, 49
	v_readlane_b32 s56, v249, 51
	s_cselect_b32 s57, s4, s56
	v_readlane_b32 s4, v249, 48
	v_readlane_b32 s56, v249, 50
	v_ashrrev_i32_e32 v197, 31, v196
	s_cselect_b32 s56, s4, s56
	s_cselect_b32 s4, 12, 10
	v_lshlrev_b64 v[140:141], s4, v[196:197]
	s_cselect_b32 vcc_hi, s34, s30
	s_cselect_b32 vcc_lo, s31, s81
	v_lshl_add_u64 v[140:141], s[56:57], 0, v[140:141]
	v_lshl_add_u64 v[140:141], vcc, 1, v[140:141]
	v_lshl_add_u64 v[140:141], v[172:173], 1, v[140:141]
	v_mov_b32_e32 v195, v194
	global_store_dwordx4 v[140:141], v[136:139], off
	v_mul_f32_e64 v144, v116, v194
	v_mul_f32_e64 v145, v117, v195
	v_mul_f32_e64 v148, v112, v194
	v_mul_f32_e64 v149, v113, v195
	v_mov_b32_e32 v136, v194
	v_mov_b32_e32 v137, v194
	v_mul_f32_e64 v142, v118, v136
	v_mul_f32_e64 v143, v119, v137
	v_mul_f32_e64 v146, v114, v136
	v_mul_f32_e64 v147, v115, v137
	s_and_b64 vcc, exec, s[2:3]
	s_mov_b64 s[2:3], -1
	s_cbranch_vccnz .LBB0_1033
	s_mov_b64 s[2:3], 0
	v_cvt_pk_bf16_f32 v136, v144, v145
	v_cvt_pk_bf16_f32 v137, v142, v143
	v_cvt_pk_bf16_f32 v138, v148, v149
	v_cvt_pk_bf16_f32 v139, v146, v147
.LBB0_1033:
	s_andn2_b64 vcc, exec, s[2:3]
	s_cbranch_vccnz .LBB0_1035
	v_mul_f32_e64 v136, v146, v130
	v_mul_f32_e64 v137, v147, v131
	v_mul_f32_e64 v138, v148, v128
	v_mul_f32_e64 v139, v149, v129
	v_fma_f32 v150, v142, v134, -v136
	v_fma_f32 v151, v143, v135, -v137
	v_fma_f32 v136, v144, v132, -v138
	v_fma_f32 v137, v145, v133, -v139
	v_mul_f32_e64 v134, v146, v134
	v_mul_f32_e64 v135, v147, v135
	v_mul_f32_e64 v132, v148, v132
	v_mul_f32_e64 v133, v149, v133
	v_fma_f32 v130, v142, v130, v134
	v_fma_f32 v131, v143, v131, v135
	v_fma_f32 v128, v144, v128, v132
	v_fma_f32 v129, v145, v129, v133
	v_cvt_pk_bf16_f32 v136, v136, v137
	v_cvt_pk_bf16_f32 v137, v150, v151
	s_nop 0
	v_cvt_pk_bf16_f32 v138, v128, v129
	v_cvt_pk_bf16_f32 v139, v130, v131

;     __device__ __forceinline__ void operator()(const f32x4 (&acc)[2][2][4][2], const Unit& u, int wr, int wc, int fr, int fq, const Pre&) const {
;     ...
;                 if (kind == KD_KVX) {
;                     bf16_t* o = (pn < 2 ? kx : vx) + (size_t)row * 512 + 256 * (pn & 1) + cw;
; #pragma unroll
;                     for (int bj = 0; bj < 2; ++bj) st_bf16x8(o + 128 * bj, acc[ai][bj][m][0] * rs, acc[ai][bj][m][1] * rs);
.LBB0_1037:
	s_and_b64 vcc, exec, s[2:3]
	s_cbranch_vccz .LBB0_1109
	s_and_b64 s[2:3], s[86:87], exec
	v_ashrrev_i32_e32 v197, 31, v196
	s_cselect_b32 s3, s11, s15
	s_cselect_b32 s2, s10, s14
	s_waitcnt vmcnt(0)
	v_lshlrev_b64 v[128:129], 10, v[196:197]
	v_lshl_add_u64 v[128:129], s[2:3], 0, v[128:129]
	s_lshl_b32 s4, s35, 1
	v_lshl_add_u64 v[128:129], v[128:129], 0, s[4:5]
	v_lshl_add_u64 v[128:129], v[172:173], 1, v[128:129]
	v_mul_f32_e64 v126, v126, v194
	v_mul_f32_e64 v127, v127, v194
	v_mul_f32_e64 v124, v124, v194
	v_mul_f32_e64 v125, v125, v194
	v_mul_f32_e64 v130, v122, v194
	v_mul_f32_e64 v131, v123, v194
	v_mul_f32_e64 v122, v120, v194
	v_mul_f32_e64 v123, v121, v194
	v_cvt_pk_bf16_f32 v120, v124, v125
	v_cvt_pk_bf16_f32 v121, v126, v127
	v_mul_f32_e64 v118, v118, v194
	v_mul_f32_e64 v119, v119, v194
	v_cvt_pk_bf16_f32 v122, v122, v123
	v_cvt_pk_bf16_f32 v123, v130, v131
	global_store_dwordx4 v[128:129], v[120:123], off
	v_mul_f32_e64 v116, v116, v194
	v_mul_f32_e64 v117, v117, v194
	s_nop 0
	v_mul_f32_e64 v120, v114, v194
	v_mul_f32_e64 v121, v115, v194
	v_mul_f32_e64 v114, v112, v194
	v_mul_f32_e64 v115, v113, v194
	v_cvt_pk_bf16_f32 v112, v116, v117
	v_cvt_pk_bf16_f32 v113, v118, v119
	s_nop 0
	v_cvt_pk_bf16_f32 v114, v114, v115
	v_cvt_pk_bf16_f32 v115, v120, v121
	global_store_dwordx4 v[128:129], v[112:115], off offset:256
	s_and_b64 vcc, exec, s[0:1]
	s_mov_b64 s[2:3], -1
	s_cbranch_vccz .LBB0_1110
.LBB0_1039:
	s_and_b64 vcc, exec, s[2:3]
	s_cbranch_vccz .LBB0_1217
	s_and_b64 s[2:3], s[86:87], exec
	v_ashrrev_i32_e32 v193, 31, v192
	s_cselect_b32 s3, s11, s15
	s_cselect_b32 s2, s10, s14
	s_waitcnt vmcnt(0)
	v_lshlrev_b64 v[104:105], 10, v[192:193]
	v_lshl_add_u64 v[104:105], s[2:3], 0, v[104:105]
	s_lshl_b32 s4, s35, 1
	v_lshl_add_u64 v[104:105], v[104:105], 0, s[4:5]
	v_lshl_add_u64 v[104:105], v[172:173], 1, v[104:105]
	v_mul_f32_e64 v102, v102, v190
	v_mul_f32_e64 v103, v103, v190
	v_mul_f32_e64 v100, v100, v190
	v_mul_f32_e64 v101, v101, v190
	v_mul_f32_e64 v106, v98, v190
	v_mul_f32_e64 v107, v99, v190
	v_mul_f32_e64 v98, v96, v190
	v_mul_f32_e64 v99, v97, v190
	v_cvt_pk_bf16_f32 v96, v100, v101
	v_cvt_pk_bf16_f32 v97, v102, v103
	v_mul_f32_e64 v94, v94, v190
	v_mul_f32_e64 v95, v95, v190
	v_cvt_pk_bf16_f32 v98, v98, v99
	v_cvt_pk_bf16_f32 v99, v106, v107
	global_store_dwordx4 v[104:105], v[96:99], off
	v_mul_f32_e64 v92, v92, v190
	v_mul_f32_e64 v93, v93, v190
	s_nop 0
	v_mul_f32_e64 v96, v90, v190
	v_mul_f32_e64 v97, v91, v190
	v_mul_f32_e64 v90, v88, v190
	v_mul_f32_e64 v91, v89, v190
	v_cvt_pk_bf16_f32 v88, v92, v93
	v_cvt_pk_bf16_f32 v89, v94, v95
	s_nop 0
	v_cvt_pk_bf16_f32 v90, v90, v91
	v_cvt_pk_bf16_f32 v91, v96, v97
	global_store_dwordx4 v[104:105], v[88:91], off offset:256
	s_and_b64 vcc, exec, s[0:1]
	s_mov_b64 s[2:3], -1
	s_cbranch_vccz .LBB0_1218
.LBB0_1041:
	s_and_b64 vcc, exec, s[2:3]
	s_cbranch_vccz .LBB0_1043
	s_and_b64 s[2:3], s[86:87], exec
	v_ashrrev_i32_e32 v189, 31, v188
	s_cselect_b32 s3, s11, s15
	s_cselect_b32 s2, s10, s14
	s_waitcnt vmcnt(0)
	v_lshlrev_b64 v[80:81], 10, v[188:189]
	v_lshl_add_u64 v[80:81], s[2:3], 0, v[80:81]
	s_lshl_b32 s4, s35, 1
	v_lshl_add_u64 v[80:81], v[80:81], 0, s[4:5]
	v_lshl_add_u64 v[80:81], v[172:173], 1, v[80:81]
	v_mul_f32_e64 v78, v78, v186
	v_mul_f32_e64 v79, v79, v186
	v_mul_f32_e64 v76, v76, v186
	v_mul_f32_e64 v77, v77, v186
	v_mul_f32_e64 v82, v74, v186
	v_mul_f32_e64 v83, v75, v186
	v_mul_f32_e64 v74, v72, v186
	v_mul_f32_e64 v75, v73, v186
	v_cvt_pk_bf16_f32 v72, v76, v77
	v_cvt_pk_bf16_f32 v73, v78, v79
	v_mul_f32_e64 v70, v70, v186
	v_mul_f32_e64 v71, v71, v186
	v_cvt_pk_bf16_f32 v74, v74, v75
	v_cvt_pk_bf16_f32 v75, v82, v83
	global_store_dwordx4 v[80:81], v[72:75], off
	v_mul_f32_e64 v68, v68, v186
	v_mul_f32_e64 v69, v69, v186
	s_nop 0
	v_mul_f32_e64 v72, v66, v186
	v_mul_f32_e64 v73, v67, v186
	v_mul_f32_e64 v66, v64, v186
	v_mul_f32_e64 v67, v65, v186
	v_cvt_pk_bf16_f32 v64, v68, v69
	v_cvt_pk_bf16_f32 v65, v70, v71
	s_nop 0
	v_cvt_pk_bf16_f32 v66, v66, v67
	v_cvt_pk_bf16_f32 v67, v72, v73
	global_store_dwordx4 v[80:81], v[64:67], off offset:256

;     __device__ __forceinline__ void operator()(const f32x4 (&acc)[2][2][4][2], const Unit& u, int wr, int wc, int fr, int fq, const Pre&) const {
;     ...
;                 if (kind == KD_KVX) {
;                     bf16_t* o = (pn < 2 ? kx : vx) + (size_t)row * 512 + 256 * (pn & 1) + cw;
; #pragma unroll
;                     for (int bj = 0; bj < 2; ++bj) st_bf16x8(o + 128 * bj, acc[ai][bj][m][0] * rs, acc[ai][bj][m][1] * rs);
.LBB0_1045:
	s_and_b64 vcc, exec, s[2:3]
	s_cbranch_vccz .LBB0_1163
	s_and_b64 s[2:3], s[86:87], exec
	s_cselect_b32 s3, s11, s15
	s_cselect_b32 s2, s10, s14
	s_waitcnt vmcnt(0)
	v_lshlrev_b64 v[88:89], 10, v[112:113]
	v_lshl_add_u64 v[88:89], s[2:3], 0, v[88:89]
	s_lshl_b32 s4, s35, 1
	v_lshl_add_u64 v[88:89], v[88:89], 0, s[4:5]
	v_lshl_add_u64 v[88:89], v[172:173], 1, v[88:89]
	v_mul_f32_e64 v90, v58, v180
	v_mul_f32_e64 v91, v59, v180
	v_mul_f32_e64 v58, v56, v180
	v_mul_f32_e64 v59, v57, v180
	v_mul_f32_e64 v50, v50, v180
	v_mul_f32_e64 v51, v51, v180
	v_mul_f32_e64 v48, v48, v180
	v_mul_f32_e64 v49, v49, v180
	v_mul_f32_e64 v62, v62, v180
	v_mul_f32_e64 v63, v63, v180
	v_mul_f32_e64 v60, v60, v180
	v_mul_f32_e64 v61, v61, v180
	v_mul_f32_e64 v54, v54, v180
	v_mul_f32_e64 v55, v55, v180
	v_cvt_pk_bf16_f32 v56, v60, v61
	v_cvt_pk_bf16_f32 v57, v62, v63
	v_cvt_pk_bf16_f32 v58, v58, v59
	v_cvt_pk_bf16_f32 v59, v90, v91
	global_store_dwordx4 v[88:89], v[56:59], off
	v_mul_f32_e64 v52, v52, v180
	v_mul_f32_e64 v53, v53, v180
	v_cvt_pk_bf16_f32 v48, v48, v49
	v_cvt_pk_bf16_f32 v49, v50, v51
	s_nop 0
	v_cvt_pk_bf16_f32 v50, v52, v53
	v_cvt_pk_bf16_f32 v51, v54, v55
	global_store_dwordx4 v[88:89], v[48:51], off offset:256
	s_and_b64 vcc, exec, s[0:1]
	s_mov_b64 s[2:3], -1
	s_cbranch_vccz .LBB0_1164
.LBB0_1047:
	s_and_b64 vcc, exec, s[2:3]
	s_cbranch_vccz .LBB0_1271
	s_and_b64 s[2:3], s[86:87], exec
	v_ashrrev_i32_e32 v111, 31, v110
	s_cselect_b32 s3, s11, s15
	s_cselect_b32 s2, s10, s14
	v_lshlrev_b64 v[48:49], 10, v[110:111]
	v_lshl_add_u64 v[48:49], s[2:3], 0, v[48:49]
	s_lshl_b32 s4, s35, 1
	v_lshl_add_u64 v[48:49], v[48:49], 0, s[4:5]
	v_mul_f32_e64 v50, v34, v178
	v_mul_f32_e64 v51, v35, v178
	v_mul_f32_e64 v34, v32, v178
	v_mul_f32_e64 v35, v33, v178
	v_lshl_add_u64 v[48:49], v[172:173], 1, v[48:49]
	v_mul_f32_e64 v38, v38, v178
	v_mul_f32_e64 v39, v39, v178
	v_mul_f32_e64 v36, v36, v178
	v_mul_f32_e64 v37, v37, v178
	s_nop 0
	v_cvt_pk_bf16_f32 v32, v36, v37
	v_cvt_pk_bf16_f32 v33, v38, v39
	v_cvt_pk_bf16_f32 v34, v34, v35
	v_cvt_pk_bf16_f32 v35, v50, v51
	global_store_dwordx4 v[48:49], v[32:35], off
	v_mul_f32_e64 v36, v46, v178
	v_mul_f32_e64 v37, v47, v178
	v_mul_f32_e64 v38, v44, v178
	v_mul_f32_e64 v39, v45, v178
	v_mul_f32_e64 v34, v42, v178
	v_mul_f32_e64 v35, v43, v178
	v_mul_f32_e64 v32, v40, v178
	v_mul_f32_e64 v33, v41, v178
	s_nop 0
	v_cvt_pk_bf16_f32 v32, v32, v33
	v_cvt_pk_bf16_f32 v33, v34, v35
	v_cvt_pk_bf16_f32 v34, v38, v39
	v_cvt_pk_bf16_f32 v35, v36, v37
	global_store_dwordx4 v[48:49], v[32:35], off offset:256
	s_and_b64 vcc, exec, s[0:1]
	s_mov_b64 s[2:3], -1
	s_cbranch_vccz .LBB0_1272
.LBB0_1049:
	s_and_b64 vcc, exec, s[2:3]
	s_cbranch_vccz .LBB0_1330
	s_and_b64 s[2:3], s[86:87], exec
	v_ashrrev_i32_e32 v109, 31, v108
	s_cselect_b32 s3, s11, s15
	s_cselect_b32 s2, s10, s14
	v_lshlrev_b64 v[32:33], 10, v[108:109]
	v_lshl_add_u64 v[32:33], s[2:3], 0, v[32:33]
	s_lshl_b32 s4, s35, 1
	v_lshl_add_u64 v[32:33], v[32:33], 0, s[4:5]
	v_mul_f32_e64 v34, v18, v176
	v_mul_f32_e64 v35, v19, v176
	v_mul_f32_e64 v18, v16, v176
	v_mul_f32_e64 v19, v17, v176
	v_lshl_add_u64 v[32:33], v[172:173], 1, v[32:33]
	v_mul_f32_e64 v22, v22, v176
	v_mul_f32_e64 v23, v23, v176
	v_mul_f32_e64 v20, v20, v176
	v_mul_f32_e64 v21, v21, v176
	s_nop 0
	v_cvt_pk_bf16_f32 v16, v20, v21
	v_cvt_pk_bf16_f32 v17, v22, v23
	v_cvt_pk_bf16_f32 v18, v18, v19
	v_cvt_pk_bf16_f32 v19, v34, v35
	global_store_dwordx4 v[32:33], v[16:19], off
	v_mul_f32_e64 v20, v30, v176
	v_mul_f32_e64 v21, v31, v176
	v_mul_f32_e64 v22, v28, v176
	v_mul_f32_e64 v23, v29, v176
	v_mul_f32_e64 v18, v26, v176
	v_mul_f32_e64 v19, v27, v176
	v_mul_f32_e64 v16, v24, v176
	v_mul_f32_e64 v17, v25, v176
	s_nop 0
	v_cvt_pk_bf16_f32 v16, v16, v17
	v_cvt_pk_bf16_f32 v17, v18, v19
	v_cvt_pk_bf16_f32 v18, v22, v23
	v_cvt_pk_bf16_f32 v19, v20, v21
	global_store_dwordx4 v[32:33], v[16:19], off offset:256
	s_and_b64 vcc, exec, s[0:1]
	s_mov_b64 s[0:1], -1
	s_cbranch_vccz .LBB0_1331
.LBB0_1051:
	s_and_b64 vcc, exec, s[0:1]
	s_cbranch_vccz .LBB0_1053
	s_and_b64 s[0:1], s[86:87], exec
	v_ashrrev_i32_e32 v107, 31, v106
	s_cselect_b32 s1, s11, s15
	s_cselect_b32 s0, s10, s14
	v_lshlrev_b64 v[16:17], 10, v[106:107]
	v_lshl_add_u64 v[16:17], s[0:1], 0, v[16:17]
	s_lshl_b32 s4, s35, 1
	v_lshl_add_u64 v[16:17], v[16:17], 0, s[4:5]
	v_mul_f32_e64 v18, v2, v170
	v_mul_f32_e64 v19, v3, v170
	v_mul_f32_e64 v2, v0, v170
	v_mul_f32_e64 v3, v1, v170
	v_lshl_add_u64 v[16:17], v[172:173], 1, v[16:17]
	v_mul_f32_e64 v6, v6, v170
	v_mul_f32_e64 v7, v7, v170
	v_mul_f32_e64 v4, v4, v170
	v_mul_f32_e64 v5, v5, v170
	s_nop 0
	v_cvt_pk_bf16_f32 v0, v4, v5
	v_cvt_pk_bf16_f32 v1, v6, v7
	v_cvt_pk_bf16_f32 v2, v2, v3
	v_cvt_pk_bf16_f32 v3, v18, v19
	global_store_dwordx4 v[16:17], v[0:3], off
	v_mul_f32_e64 v4, v14, v170
	v_mul_f32_e64 v5, v15, v170
	v_mul_f32_e64 v6, v12, v170
	v_mul_f32_e64 v7, v13, v170
	v_mul_f32_e64 v2, v10, v170
	v_mul_f32_e64 v3, v11, v170
	v_mul_f32_e64 v0, v8, v170
	v_mul_f32_e64 v1, v9, v170
	s_nop 0
	v_cvt_pk_bf16_f32 v0, v0, v1
	v_cvt_pk_bf16_f32 v1, v2, v3
	v_cvt_pk_bf16_f32 v2, v6, v7
	v_cvt_pk_bf16_f32 v3, v4, v5
	global_store_dwordx4 v[16:17], v[0:3], off offset:256

; __device__ __forceinline__ f32x4 sigmoid4(const f32x4& x, float s) {
;     f32x4 z = x * (s * -1.4426950408889634f), e;
; #pragma unroll
;     for (int j = 0; j < 4; ++j) e[j] = __builtin_amdgcn_exp2f(z[j]);
;     e = e + 1.0f;
; #pragma unroll
;     for (int j = 0; j < 4; ++j) e[j] = __builtin_amdgcn_rcpf(e[j]);
;     return e;
; }
;     __device__ __forceinline__ void operator()(const f32x4 (&acc)[2][2][4][2], const Unit& u, int wr, int wc, int fr, int fq, const Pre&) const {
;     ...
;                 } else if (kind == KD_G) {
; #pragma unroll
;                     for (int bj = 0; bj < 2; ++bj)
;                         st_bf16x8(gabuf + (size_t)row * DM + 256 * (pn - TL_G) + 128 * bj + cw, sigmoid4(acc[ai][bj][m][0], rs), sigmoid4(acc[ai][bj][m][1], rs));
.LBB0_1056:
	s_mov_b64 s[36:37], -1
	s_mov_b64 s[2:3], 0
	s_cmp_lt_i32 s7, 1
	s_mov_b64 s[16:17], 0
	s_cbranch_scc1 .LBB0_1158
	s_cmp_gt_i32 s7, 1
	s_cbranch_scc0 .LBB0_1061
	s_cmp_eq_u32 s7, 2
	s_mov_b64 s[16:17], -1
	s_cbranch_scc0 .LBB0_1060
	v_readlane_b32 s16, v249, 46
	v_lshlrev_b64 v[96:97], 12, v[112:113]
	v_readlane_b32 s17, v249, 47
	v_mul_f32_e32 v102, 0xbfb8aa3b, v180
	v_mul_f32_e32 v98, v62, v102
	v_lshl_add_u64 v[96:97], s[16:17], 0, v[96:97]
	v_lshl_add_u64 v[96:97], s[38:39], 1, v[96:97]
	v_mul_f32_e32 v99, v63, v102
	v_lshl_add_u64 v[100:101], v[172:173], 1, v[96:97]
	v_mul_f32_e32 v96, v60, v102
	v_mul_f32_e32 v97, v61, v102
	v_exp_f32_e32 v98, v98
	v_exp_f32_e32 v99, v99
	v_exp_f32_e32 v96, v96
	v_exp_f32_e32 v97, v97
	s_mov_b64 s[16:17], 0
	v_add_f32_e64 v98, v98, 1.0
	v_add_f32_e64 v99, v99, 1.0
	v_add_f32_e64 v96, v96, 1.0
	v_add_f32_e64 v97, v97, 1.0
	v_rcp_f32_e32 v105, v98
	v_rcp_f32_e32 v107, v99
	v_mul_f32_e32 v98, v58, v102
	v_mul_f32_e32 v99, v59, v102
	v_rcp_f32_e32 v103, v96
	v_rcp_f32_e32 v104, v97
	v_mul_f32_e32 v96, v56, v102
	v_mul_f32_e32 v97, v57, v102
	v_exp_f32_e32 v98, v98
	v_exp_f32_e32 v99, v99
	v_exp_f32_e32 v96, v96
	v_exp_f32_e32 v97, v97
	v_add_f32_e64 v98, v98, 1.0
	v_add_f32_e64 v99, v99, 1.0
	s_nop 0
	v_rcp_f32_e32 v99, v99
	v_add_f32_e64 v96, v96, 1.0
	v_add_f32_e64 v97, v97, 1.0
	v_rcp_f32_e32 v114, v98
	v_rcp_f32_e32 v109, v96
	v_rcp_f32_e32 v111, v97
	v_cvt_pk_bf16_f32 v96, v103, v104
	v_cvt_pk_bf16_f32 v97, v105, v107
	v_cvt_pk_bf16_f32 v98, v109, v111
	v_cvt_pk_bf16_f32 v99, v114, v99
	global_store_dwordx4 v[100:101], v[96:99], off
	s_nop 1
	v_mul_f32_e32 v98, v50, v102
	v_mul_f32_e32 v99, v51, v102
	v_mul_f32_e32 v96, v48, v102
	v_mul_f32_e32 v97, v49, v102
	v_exp_f32_e32 v98, v98
	v_exp_f32_e32 v99, v99
	v_exp_f32_e32 v96, v96
	v_exp_f32_e32 v97, v97
	v_add_f32_e64 v98, v98, 1.0
	v_add_f32_e64 v99, v99, 1.0
	s_nop 0
	v_rcp_f32_e32 v105, v98
	v_add_f32_e64 v96, v96, 1.0
	v_add_f32_e64 v97, v97, 1.0
	v_rcp_f32_e32 v107, v99
	v_mul_f32_e32 v98, v54, v102
	v_mul_f32_e32 v99, v55, v102
	v_rcp_f32_e32 v103, v96
	v_rcp_f32_e32 v104, v97
	v_mul_f32_e32 v96, v52, v102
	v_mul_f32_e32 v97, v53, v102
	v_exp_f32_e32 v98, v98
	v_exp_f32_e32 v99, v99
	v_exp_f32_e32 v96, v96
	v_exp_f32_e32 v97, v97
	v_add_f32_e64 v98, v98, 1.0
	v_add_f32_e64 v99, v99, 1.0
	s_nop 0
	v_rcp_f32_e32 v99, v99
	v_add_f32_e64 v96, v96, 1.0
	v_add_f32_e64 v97, v97, 1.0
	v_rcp_f32_e32 v111, v98
	v_rcp_f32_e32 v102, v96
	v_rcp_f32_e32 v109, v97
	v_cvt_pk_bf16_f32 v96, v103, v104
	v_cvt_pk_bf16_f32 v97, v105, v107
	v_cvt_pk_bf16_f32 v98, v102, v109
	v_cvt_pk_bf16_f32 v99, v111, v99
	global_store_dwordx4 v[100:101], v[96:99], off offset:256

;     __device__ __forceinline__ void operator()(const f32x4 (&acc)[2][2][4][2], const Unit& u, int wr, int wc, int fr, int fq, const Pre&) const {
;     ...
;                 } else if (kind == KD_P) {
;                     const float r2 = rs * rs;
;                     st_bf16x8(pbuf + (size_t)row * DM + 128 * (pn - TL_P) + cw, acc[ai][0][m][0] * acc[ai][1][m][0] * r2, acc[ai][0][m][1] * acc[ai][1][m][1] * r2);
.LBB0_1061:
	s_and_b64 vcc, exec, s[36:37]
	s_cbranch_vccz .LBB0_1063
	v_readlane_b32 s36, v249, 44
	v_lshlrev_b64 v[98:99], 12, v[112:113]
	v_readlane_b32 s37, v249, 45
	v_mul_f32_e32 v96, v180, v180
	v_mul_f32_e64 v102, v60, v48
	v_mul_f32_e64 v103, v61, v49
	v_lshl_add_u64 v[98:99], s[36:37], 0, v[98:99]
	v_lshl_add_u64 v[98:99], s[42:43], 1, v[98:99]
	v_lshl_add_u64 v[100:101], v[172:173], 1, v[98:99]
	v_mul_f32_e64 v98, v62, v50
	v_mul_f32_e64 v99, v63, v51
	v_mul_f32_e64 v104, v58, v54
	v_mul_f32_e64 v105, v59, v55
	v_mul_f32_e64 v98, v98, v96
	v_mul_f32_e64 v99, v99, v96
	v_mul_f32_e64 v114, v56, v52
	v_mul_f32_e64 v115, v57, v53
	v_mul_f32_e64 v102, v102, v96
	v_mul_f32_e64 v103, v103, v96
	v_mul_f32_e64 v104, v104, v96
	v_mul_f32_e64 v105, v105, v96
	v_mul_f32_e64 v114, v114, v96
	v_mul_f32_e64 v115, v115, v96
	v_cvt_pk_bf16_f32 v96, v102, v103
	v_cvt_pk_bf16_f32 v97, v98, v99
	s_nop 0
	v_cvt_pk_bf16_f32 v98, v114, v115
	v_cvt_pk_bf16_f32 v99, v104, v105
	global_store_dwordx4 v[100:101], v[96:99], off

;     __device__ __forceinline__ void operator()(const f32x4 (&acc)[2][2][4][2], const Unit& u, int wr, int wc, int fr, int fq, const Pre&) const {
;     ...
;                 } else {
;                     const f32x4 x1 = acc[ai][0][m][0] * rs, x2 = acc[ai][0][m][1] * rs;
;                     if (wc < 2) {
;                         if (roti) st_bf16x8(kib + (size_t)row * 64 + cw, x1 * cs[q] - x2 * sn[q], x2 * cs[q] + x1 * sn[q]);
;                         else st_bf16x8(kib + (size_t)row * 64 + cw, x1, x2);
;                     } else if (wc == 2 && fq < 2) {
;                         *(f32x4*)(wib + (size_t)row * 16 + 8 * fq) = x1 * 0.03125f; *(f32x4*)(wib + (size_t)row * 16 + 8 * fq + 4) = x2 * 0.03125f;
;                     }
.LBB0_1065:
	s_andn2_b64 vcc, exec, s[64:65]
	s_mov_b64 s[2:3], -1
	s_cbranch_vccnz .LBB0_1093
	s_andn2_b64 vcc, exec, s[58:59]
	s_cbranch_vccnz .LBB0_1090
	v_readlane_b32 s16, v249, 63
	v_mov_b32_e32 v181, v180
	v_readlane_b32 s17, v248, 0
	s_andn2_b64 vcc, exec, s[16:17]
	v_mul_f32_e64 v98, v60, v180
	v_mul_f32_e64 v99, v61, v181
	v_mul_f32_e64 v96, v56, v180
	v_mul_f32_e64 v97, v57, v181
	s_cbranch_vccnz .LBB0_1079
	v_readlane_b32 s2, v248, 24
	v_mov_b32_e32 v100, v180
	v_mov_b32_e32 v101, v180
	v_readlane_b32 s3, v248, 25
	v_mul_f32_e64 v102, v62, v100
	v_mul_f32_e64 v103, v63, v101
	v_mul_f32_e64 v100, v58, v100
	v_mul_f32_e64 v101, v59, v101
	s_andn2_b64 vcc, exec, s[2:3]
	s_mov_b64 s[2:3], -1
	s_cbranch_vccnz .LBB0_1072
	s_mov_b64 s[2:3], exec
	v_readlane_b32 s16, v248, 7
	v_readlane_b32 s17, v248, 8
	s_and_b64 s[16:17], s[2:3], s[16:17]
	s_mov_b64 exec, s[16:17]
	s_cbranch_execz .LBB0_1071
	v_readlane_b32 s16, v249, 56
	v_lshlrev_b64 v[104:105], 6, v[112:113]
	v_readlane_b32 s17, v249, 57
	s_mov_b32 s4, 0x3d000000
	v_mul_f32_e64 v120, v102, s4
	v_mul_f32_e64 v121, v103, s4
	v_lshl_add_u64 v[104:105], s[16:17], 0, v[104:105]
	v_lshl_add_u64 v[104:105], v[174:175], 2, v[104:105]
	v_mul_f32_e64 v118, v98, s4
	v_mul_f32_e64 v119, v99, s4
	v_mul_f32_e64 v116, v100, s4
	v_mul_f32_e64 v117, v101, s4
	v_mul_f32_e64 v114, v96, s4
	v_mul_f32_e64 v115, v97, s4
	global_store_dwordx4 v[104:105], v[118:121], off
	global_store_dwordx4 v[104:105], v[114:117], off offset:16

;     __device__ __forceinline__ void operator()(const f32x4 (&acc)[2][2][4][2], const Unit& u, int wr, int wc, int fr, int fq, const Pre&) const {
;     ...
;                 } else {
;                     const f32x4 x1 = acc[ai][0][m][0] * rs, x2 = acc[ai][0][m][1] * rs;
;                     if (wc < 2) {
;                         if (roti) st_bf16x8(kib + (size_t)row * 64 + cw, x1 * cs[q] - x2 * sn[q], x2 * cs[q] + x1 * sn[q]);
;                         else st_bf16x8(kib + (size_t)row * 64 + cw, x1, x2);
.LBB0_1075:
	s_andn2_saveexec_b64 s[2:3], s[2:3]
	s_cbranch_execz .LBB0_1077
	s_waitcnt vmcnt(0)
	v_mul_f32_e64 v114, v100, v90
	v_mul_f32_e64 v115, v101, v91
	v_mul_f32_e64 v100, v100, v94
	v_mul_f32_e64 v101, v101, v95
	v_mul_f32_e64 v118, v96, v92
	v_mul_f32_e64 v119, v97, v93
	v_mul_f32_e64 v116, v96, v88
	v_mul_f32_e64 v117, v97, v89
	v_fma_f32 v114, v102, v94, -v114
	v_fma_f32 v115, v103, v95, -v115
	v_fma_f32 v120, v102, v90, v100
	v_fma_f32 v121, v103, v91, v101
	v_fma_f32 v102, v98, v88, v118
	v_fma_f32 v103, v99, v89, v119
	v_fma_f32 v116, v98, v92, -v116
	v_fma_f32 v117, v99, v93, -v117
	s_nop 0
	v_cvt_pk_bf16_f32 v100, v116, v117
	v_cvt_pk_bf16_f32 v101, v114, v115
	v_cvt_pk_bf16_f32 v102, v102, v103
	v_cvt_pk_bf16_f32 v103, v120, v121
	global_store_dwordx4 v[104:105], v[100:103], off

;     __device__ __forceinline__ void operator()(const f32x4 (&acc)[2][2][4][2], const Unit& u, int wr, int wc, int fr, int fq, const Pre&) const {
;     ...
;                 } else if (kind == KD_QI) {
; #pragma unroll
;                     for (int bj = 0; bj < 2; ++bj) {
;                         const f32x4 x1 = acc[ai][bj][m][0] * rs, x2 = acc[ai][bj][m][1] * rs;
;                         bf16_t* o = qib + (size_t)row * 1024 + 256 * (pn - TL_QI) + 128 * bj + cw;
;                         if (roti) st_bf16x8(o, x1 * cs[q] - x2 * sn[q], x2 * cs[q] + x1 * sn[q]); else st_bf16x8(o, x1, x2);
;                     }
.LBB0_1079:
	s_andn2_b64 vcc, exec, s[2:3]
	s_cbranch_vccnz .LBB0_1089
	v_mov_b32_e32 v100, v180
	v_mov_b32_e32 v101, v180
	v_readlane_b32 s36, v248, 9
	v_mul_f32_e64 v116, v62, v100
	v_mul_f32_e64 v117, v63, v101
	v_mul_f32_e64 v114, v58, v100
	v_mul_f32_e64 v115, v59, v101
	v_readlane_b32 s37, v248, 10
	s_and_saveexec_b64 s[2:3], s[36:37]
	s_xor_b64 s[2:3], exec, s[2:3]
	s_cbranch_execz .LBB0_1082
	v_cvt_pk_bf16_f32 v102, v98, v99
	v_cvt_pk_bf16_f32 v103, v116, v117
	v_cvt_pk_bf16_f32 v104, v96, v97
	v_cvt_pk_bf16_f32 v105, v114, v115
.LBB0_1082:
	s_andn2_saveexec_b64 s[2:3], s[2:3]
	s_cbranch_execz .LBB0_1084
	s_waitcnt vmcnt(0)
	v_mul_f32_e64 v102, v96, v88
	v_mul_f32_e64 v103, v97, v89
	v_mul_f32_e64 v100, v114, v90
	v_mul_f32_e64 v101, v115, v91
	v_fma_f32 v102, v98, v92, -v102
	v_fma_f32 v103, v99, v93, -v103
	v_mul_f32_e64 v104, v114, v94
	v_mul_f32_e64 v105, v115, v95
	v_mul_f32_e64 v96, v96, v92
	v_mul_f32_e64 v97, v97, v93
	v_fma_f32 v100, v116, v94, -v100
	v_fma_f32 v101, v117, v95, -v101
	v_fma_f32 v114, v116, v90, v104
	v_fma_f32 v115, v117, v91, v105
	v_fma_f32 v96, v98, v88, v96
	v_fma_f32 v97, v99, v89, v97
	v_cvt_pk_bf16_f32 v102, v102, v103
	v_cvt_pk_bf16_f32 v103, v100, v101
	s_nop 0
	v_cvt_pk_bf16_f32 v104, v96, v97
	v_cvt_pk_bf16_f32 v105, v114, v115
.LBB0_1084:
	s_or_b64 exec, exec, s[2:3]
	v_readlane_b32 s2, v248, 18
	v_lshlrev_b64 v[96:97], 11, v[112:113]
	v_readlane_b32 s3, v248, 19
	v_mul_f32_e64 v100, v52, v180
	v_mul_f32_e64 v101, v53, v181
	s_nop 0
	v_lshl_add_u64 v[96:97], s[2:3], 0, v[96:97]
	v_lshl_add_u64 v[96:97], s[28:29], 1, v[96:97]
	v_lshl_add_u64 v[114:115], v[172:173], 1, v[96:97]
	v_mov_b32_e32 v96, v180
	v_mov_b32_e32 v97, v180
	global_store_dwordx4 v[114:115], v[102:105], off
	v_mul_f32_e64 v118, v50, v96
	v_mul_f32_e64 v119, v51, v97
	v_mul_f32_e64 v116, v54, v96
	v_mul_f32_e64 v117, v55, v97
	v_mul_f32_e64 v102, v48, v180
	v_mul_f32_e64 v103, v49, v181
	s_and_saveexec_b64 s[2:3], s[36:37]
	s_xor_b64 s[2:3], exec, s[2:3]
	s_cbranch_execz .LBB0_1086
	v_cvt_pk_bf16_f32 v96, v102, v103
	v_cvt_pk_bf16_f32 v97, v118, v119
	v_cvt_pk_bf16_f32 v98, v100, v101
	v_cvt_pk_bf16_f32 v99, v116, v117
.LBB0_1086:
	s_andn2_saveexec_b64 s[2:3], s[2:3]
	s_cbranch_execz .LBB0_1088
	s_waitcnt vmcnt(0)
	v_mul_f32_e64 v96, v116, v90
	v_mul_f32_e64 v97, v117, v91
	v_mul_f32_e64 v98, v100, v88
	v_mul_f32_e64 v99, v101, v89
	v_fma_f32 v104, v118, v94, -v96
	v_fma_f32 v105, v119, v95, -v97
	v_fma_f32 v96, v102, v92, -v98
	v_fma_f32 v97, v103, v93, -v99
	v_mul_f32_e64 v98, v116, v94
	v_mul_f32_e64 v99, v117, v95
	v_mul_f32_e64 v100, v100, v92
	v_mul_f32_e64 v101, v101, v93
	v_fma_f32 v116, v118, v90, v98
	v_fma_f32 v117, v119, v91, v99
	v_fma_f32 v98, v102, v88, v100
	v_fma_f32 v99, v103, v89, v101
	v_cvt_pk_bf16_f32 v96, v96, v97
	v_cvt_pk_bf16_f32 v97, v104, v105
	s_nop 0
	v_cvt_pk_bf16_f32 v98, v98, v99
	v_cvt_pk_bf16_f32 v99, v116, v117

;     __device__ __forceinline__ void operator()(const f32x4 (&acc)[2][2][4][2], const Unit& u, int wr, int wc, int fr, int fq, const Pre&) const {
;     ...
;                 } else if (kind == KD_V) {
; #pragma unroll
;                     for (int bj = 0; bj < 2; ++bj) st_bf16x8(vb + (size_t)row * 512 + 256 * (pn - TL_V) + 128 * bj + cw, acc[ai][bj][m][0] * rs, acc[ai][bj][m][1] * rs);
.LBB0_1090:
	s_andn2_b64 vcc, exec, s[2:3]
	s_cbranch_vccnz .LBB0_1092
	v_readlane_b32 s2, v249, 52
	v_lshlrev_b64 v[96:97], 10, v[112:113]
	v_readlane_b32 s3, v249, 53
	v_mul_f32_e64 v98, v62, v180
	v_mul_f32_e64 v99, v63, v180
	v_mul_f32_e64 v102, v58, v180
	v_mul_f32_e64 v103, v59, v180
	v_lshl_add_u64 v[96:97], s[2:3], 0, v[96:97]
	v_lshl_add_u64 v[96:97], s[94:95], 1, v[96:97]
	v_lshl_add_u64 v[100:101], v[172:173], 1, v[96:97]
	v_mul_f32_e64 v96, v60, v180
	v_mul_f32_e64 v97, v61, v180
	v_mul_f32_e64 v104, v56, v180
	v_mul_f32_e64 v105, v57, v180
	v_cvt_pk_bf16_f32 v96, v96, v97
	v_cvt_pk_bf16_f32 v97, v98, v99
	s_nop 0
	v_cvt_pk_bf16_f32 v98, v104, v105
	v_cvt_pk_bf16_f32 v99, v102, v103
	global_store_dwordx4 v[100:101], v[96:99], off
	v_mul_f32_e64 v102, v54, v180
	v_mul_f32_e64 v103, v55, v180
	v_mul_f32_e64 v104, v52, v180
	v_mul_f32_e64 v105, v53, v180
	v_mul_f32_e64 v98, v50, v180
	v_mul_f32_e64 v99, v51, v180
	v_mul_f32_e64 v96, v48, v180
	v_mul_f32_e64 v97, v49, v180
	s_nop 0
	v_cvt_pk_bf16_f32 v96, v96, v97
	v_cvt_pk_bf16_f32 v97, v98, v99
	v_cvt_pk_bf16_f32 v98, v104, v105
	v_cvt_pk_bf16_f32 v99, v102, v103
	global_store_dwordx4 v[100:101], v[96:99], off offset:256

;     __device__ __forceinline__ void operator()(const f32x4 (&acc)[2][2][4][2], const Unit& u, int wr, int wc, int fr, int fq, const Pre&) const {
;     ...
;                 } else if (kind == KD_Q || kind == KD_K) {
;                     bf16_t* o = (kind == KD_Q) ? qb + (size_t)row * DM + 256 * (pn - TL_Q) + cw : kb + (size_t)row * 512 + 256 * (pn - TL_K) + cw;
; #pragma unroll
;                     for (int bj = 0; bj < 2; ++bj) {
;                         const f32x4 x1 = acc[ai][bj][m][0] * rs, x2 = acc[ai][bj][m][1] * rs;
;                         if (rotqk) st_bf16x8(o + 128 * bj, x1 * cs[q] - x2 * sn[q], x2 * cs[q] + x1 * sn[q]);
;                         else st_bf16x8(o + 128 * bj, x1, x2);
;                     }
.LBB0_1093:
	s_andn2_b64 vcc, exec, s[2:3]
	s_cbranch_vccnz .LBB0_1103
	v_cndmask_b32_e64 v96, 0, 1, s[92:93]
	v_mul_f32_e64 v100, v62, v180
	v_mul_f32_e64 v101, v63, v180
	v_mul_f32_e64 v102, v60, v180
	v_mul_f32_e64 v103, v61, v180
	v_mul_f32_e64 v104, v58, v180
	v_mul_f32_e64 v105, v59, v180
	v_mul_f32_e64 v114, v56, v180
	v_mul_f32_e64 v115, v57, v180
	v_cmp_ne_u32_e64 s[2:3], 1, v96
	s_andn2_b64 vcc, exec, s[92:93]
	s_mov_b64 s[16:17], -1
	s_cbranch_vccnz .LBB0_1096
	s_mov_b64 s[16:17], 0
	v_cvt_pk_bf16_f32 v96, v102, v103
	v_cvt_pk_bf16_f32 v97, v100, v101
	v_cvt_pk_bf16_f32 v98, v114, v115
	v_cvt_pk_bf16_f32 v99, v104, v105
.LBB0_1096:
	s_andn2_b64 vcc, exec, s[16:17]
	s_cbranch_vccnz .LBB0_1098
	s_waitcnt vmcnt(0)
	v_mul_f32_e64 v96, v104, v90
	v_mul_f32_e64 v97, v105, v91
	v_mul_f32_e64 v98, v114, v88
	v_mul_f32_e64 v99, v115, v89
	v_fma_f32 v116, v100, v94, -v96
	v_fma_f32 v117, v101, v95, -v97
	v_fma_f32 v96, v102, v92, -v98
	v_fma_f32 v97, v103, v93, -v99
	v_mul_f32_e64 v98, v104, v94
	v_mul_f32_e64 v99, v105, v95
	v_mul_f32_e64 v104, v114, v92
	v_mul_f32_e64 v105, v115, v93
	v_fma_f32 v100, v100, v90, v98
	v_fma_f32 v101, v101, v91, v99
	v_fma_f32 v98, v102, v88, v104
	v_fma_f32 v99, v103, v89, v105
	v_cvt_pk_bf16_f32 v96, v96, v97
	v_cvt_pk_bf16_f32 v97, v116, v117
	s_nop 0
	v_cvt_pk_bf16_f32 v98, v98, v99
	v_cvt_pk_bf16_f32 v99, v100, v101
.LBB0_1098:
	s_and_b64 s[16:17], s[90:91], exec
	v_readlane_b32 s4, v249, 49
	v_readlane_b32 s16, v249, 51
	s_cselect_b32 s17, s4, s16
	v_readlane_b32 s4, v249, 48
	v_readlane_b32 s16, v249, 50
	s_cselect_b32 s16, s4, s16
	s_cselect_b32 s4, 12, 10
	v_lshlrev_b64 v[100:101], s4, v[112:113]
	s_cselect_b32 s37, s34, s30
	s_cselect_b32 s36, s31, s81
	v_lshl_add_u64 v[100:101], s[16:17], 0, v[100:101]
	v_lshl_add_u64 v[100:101], s[36:37], 1, v[100:101]
	v_lshl_add_u64 v[100:101], v[172:173], 1, v[100:101]
	v_mov_b32_e32 v181, v180
	global_store_dwordx4 v[100:101], v[96:99], off
	v_mul_f32_e64 v104, v48, v180
	v_mul_f32_e64 v105, v49, v181
	v_mul_f32_e64 v116, v52, v180
	v_mul_f32_e64 v117, v53, v181
	v_mov_b32_e32 v96, v180
	v_mov_b32_e32 v97, v180
	v_mul_f32_e64 v102, v50, v96
	v_mul_f32_e64 v103, v51, v97
	v_mul_f32_e64 v114, v54, v96
	v_mul_f32_e64 v115, v55, v97
	s_and_b64 vcc, exec, s[2:3]
	s_mov_b64 s[2:3], -1
	s_cbranch_vccnz .LBB0_1100
	s_mov_b64 s[2:3], 0
	v_cvt_pk_bf16_f32 v96, v104, v105
	v_cvt_pk_bf16_f32 v97, v102, v103
	v_cvt_pk_bf16_f32 v98, v116, v117
	v_cvt_pk_bf16_f32 v99, v114, v115
.LBB0_1100:
	s_andn2_b64 vcc, exec, s[2:3]
	s_cbranch_vccnz .LBB0_1102
	s_waitcnt vmcnt(0)
	v_mul_f32_e64 v96, v114, v90
	v_mul_f32_e64 v97, v115, v91
	v_mul_f32_e64 v98, v116, v88
	v_mul_f32_e64 v99, v117, v89
	v_fma_f32 v118, v102, v94, -v96
	v_fma_f32 v119, v103, v95, -v97
	v_fma_f32 v96, v104, v92, -v98
	v_fma_f32 v97, v105, v93, -v99
	v_mul_f32_e64 v94, v114, v94
	v_mul_f32_e64 v95, v115, v95
	v_mul_f32_e64 v92, v116, v92
	v_mul_f32_e64 v93, v117, v93
	v_fma_f32 v90, v102, v90, v94
	v_fma_f32 v91, v103, v91, v95
	v_fma_f32 v88, v104, v88, v92
	v_fma_f32 v89, v105, v89, v93
	v_cvt_pk_bf16_f32 v96, v96, v97
	v_cvt_pk_bf16_f32 v97, v118, v119
	s_nop 0
	v_cvt_pk_bf16_f32 v98, v88, v89
	v_cvt_pk_bf16_f32 v99, v90, v91

; __device__ __forceinline__ f32x4 sigmoid4(const f32x4& x, float s) {
;     f32x4 z = x * (s * -1.4426950408889634f), e;
; #pragma unroll
;     for (int j = 0; j < 4; ++j) e[j] = __builtin_amdgcn_exp2f(z[j]);
;     e = e + 1.0f;
; #pragma unroll
;     for (int j = 0; j < 4; ++j) e[j] = __builtin_amdgcn_rcpf(e[j]);
;     return e;
; }
;     __device__ __forceinline__ void operator()(const f32x4 (&acc)[2][2][4][2], const Unit& u, int wr, int wc, int fr, int fq, const Pre&) const {
;     ...
;                 } else if (kind == KD_A) {
;                     st_bf16x8(abuf + (size_t)row * DM + 128 * (pn - TL_A) + cw, acc[ai][0][m][0] * rs * sigmoid4(acc[ai][1][m][0], rs), acc[ai][0][m][1] * rs * sigmoid4(acc[ai][1][m][1], rs));
.LBB0_1107:
	v_ashrrev_i32_e32 v197, 31, v196
	s_waitcnt vmcnt(0)
	v_lshlrev_b64 v[128:129], 12, v[196:197]
	v_lshl_add_u64 v[128:129], s[12:13], 0, v[128:129]
	v_lshl_add_u64 v[128:129], s[88:89], 1, v[128:129]
	v_mul_f32_e32 v139, 0xbfb8aa3b, v194
	v_lshl_add_u64 v[132:133], v[172:173], 1, v[128:129]
	v_mul_f32_e32 v128, v116, v139
	v_mul_f32_e32 v129, v117, v139
	v_mul_f32_e32 v130, v118, v139
	v_mul_f32_e32 v131, v119, v139
	v_exp_f32_e32 v128, v128
	v_exp_f32_e32 v130, v130
	v_exp_f32_e32 v131, v131
	v_exp_f32_e32 v129, v129
	v_mul_f32_e32 v138, v112, v139
	v_mul_f32_e32 v142, v113, v139
	v_add_f32_e64 v130, v130, 1.0
	v_add_f32_e64 v131, v131, 1.0
	v_add_f32_e64 v128, v128, 1.0
	v_add_f32_e64 v129, v129, 1.0
	v_mul_f32_e32 v140, v114, v139
	v_mul_f32_e32 v139, v115, v139
	v_rcp_f32_e32 v128, v128
	v_rcp_f32_e32 v129, v129
	v_rcp_f32_e32 v130, v130
	v_rcp_f32_e32 v131, v131
	v_exp_f32_e32 v138, v138
	v_exp_f32_e32 v140, v140
	v_exp_f32_e32 v141, v139
	v_exp_f32_e32 v139, v142
	v_mul_f32_e64 v134, v126, v194
	v_mul_f32_e64 v135, v127, v194
	v_mul_f32_e64 v136, v124, v194
	v_mul_f32_e64 v137, v125, v194
	v_mul_f32_e64 v130, v134, v130
	v_mul_f32_e64 v131, v135, v131
	v_mul_f32_e64 v128, v136, v128
	v_mul_f32_e64 v129, v137, v129
	v_add_f32_e64 v134, v140, 1.0
	v_add_f32_e64 v135, v141, 1.0
	v_add_f32_e64 v136, v138, 1.0
	v_add_f32_e64 v137, v139, 1.0
	v_rcp_f32_e32 v134, v134
	v_rcp_f32_e32 v136, v136
	v_rcp_f32_e32 v135, v135
	v_rcp_f32_e32 v137, v137
	v_mul_f32_e64 v138, v122, v194
	v_mul_f32_e64 v139, v123, v194
	v_mul_f32_e64 v140, v120, v194
	v_mul_f32_e64 v141, v121, v194
	v_mul_f32_e64 v134, v138, v134
	v_mul_f32_e64 v135, v139, v135
	v_mul_f32_e64 v136, v140, v136
	v_mul_f32_e64 v137, v141, v137
	v_cvt_pk_bf16_f32 v128, v128, v129
	v_cvt_pk_bf16_f32 v129, v130, v131
	s_nop 0
	v_cvt_pk_bf16_f32 v130, v136, v137
	v_cvt_pk_bf16_f32 v131, v134, v135
	global_store_dwordx4 v[132:133], v[128:131], off

; __device__ __forceinline__ f32x4 sigmoid4(const f32x4& x, float s) {
;     f32x4 z = x * (s * -1.4426950408889634f), e;
; #pragma unroll
;     for (int j = 0; j < 4; ++j) e[j] = __builtin_amdgcn_exp2f(z[j]);
;     e = e + 1.0f;
; #pragma unroll
;     for (int j = 0; j < 4; ++j) e[j] = __builtin_amdgcn_rcpf(e[j]);
;     return e;
; }
;     __device__ __forceinline__ void operator()(const f32x4 (&acc)[2][2][4][2], const Unit& u, int wr, int wc, int fr, int fq, const Pre&) const {
;     ...
;                 } else if (kind == KD_G) {
; #pragma unroll
;                     for (int bj = 0; bj < 2; ++bj)
;                         st_bf16x8(gabuf + (size_t)row * DM + 256 * (pn - TL_G) + 128 * bj + cw, sigmoid4(acc[ai][bj][m][0], rs), sigmoid4(acc[ai][bj][m][1], rs));
.LBB0_1110:
	s_mov_b64 vcc, -1
	s_mov_b64 s[2:3], 0
	s_cmp_lt_i32 s7, 1
	s_mov_b64 s[56:57], 0
	s_cbranch_scc1 .LBB0_1212
	s_cmp_gt_i32 s7, 1
	s_cbranch_scc0 .LBB0_1115
	s_cmp_eq_u32 s7, 2
	s_mov_b64 s[56:57], -1
	s_cbranch_scc0 .LBB0_1114
	v_ashrrev_i32_e32 v193, 31, v192
	v_readlane_b32 s56, v249, 46
	v_lshlrev_b64 v[112:113], 12, v[192:193]
	v_readlane_b32 s57, v249, 47
	s_waitcnt vmcnt(0)
	v_mul_f32_e32 v118, 0xbfb8aa3b, v190
	v_mul_f32_e32 v114, v102, v118
	v_lshl_add_u64 v[112:113], s[56:57], 0, v[112:113]
	v_lshl_add_u64 v[112:113], s[38:39], 1, v[112:113]
	v_mul_f32_e32 v115, v103, v118
	v_lshl_add_u64 v[116:117], v[172:173], 1, v[112:113]
	v_mul_f32_e32 v112, v100, v118
	v_mul_f32_e32 v113, v101, v118
	v_exp_f32_e32 v114, v114
	v_exp_f32_e32 v115, v115
	v_exp_f32_e32 v112, v112
	v_exp_f32_e32 v113, v113
	s_mov_b64 s[56:57], 0
	v_add_f32_e64 v114, v114, 1.0
	v_add_f32_e64 v115, v115, 1.0
	v_add_f32_e64 v112, v112, 1.0
	v_add_f32_e64 v113, v113, 1.0
	v_rcp_f32_e32 v121, v114
	v_rcp_f32_e32 v122, v115
	v_mul_f32_e32 v114, v98, v118
	v_mul_f32_e32 v115, v99, v118
	v_rcp_f32_e32 v119, v112
	v_rcp_f32_e32 v120, v113
	v_mul_f32_e32 v112, v96, v118
	v_mul_f32_e32 v113, v97, v118
	v_exp_f32_e32 v114, v114
	v_exp_f32_e32 v115, v115
	v_exp_f32_e32 v112, v112
	v_exp_f32_e32 v113, v113
	v_add_f32_e64 v114, v114, 1.0
	v_add_f32_e64 v115, v115, 1.0
	s_nop 0
	v_rcp_f32_e32 v115, v115
	v_add_f32_e64 v112, v112, 1.0
	v_add_f32_e64 v113, v113, 1.0
	v_rcp_f32_e32 v125, v114
	v_rcp_f32_e32 v123, v112
	v_rcp_f32_e32 v124, v113
	v_cvt_pk_bf16_f32 v112, v119, v120
	v_cvt_pk_bf16_f32 v113, v121, v122
	v_cvt_pk_bf16_f32 v114, v123, v124
	v_cvt_pk_bf16_f32 v115, v125, v115
	global_store_dwordx4 v[116:117], v[112:115], off
	s_nop 1
	v_mul_f32_e32 v114, v94, v118
	v_mul_f32_e32 v115, v95, v118
	v_mul_f32_e32 v112, v92, v118
	v_mul_f32_e32 v113, v93, v118
	v_exp_f32_e32 v114, v114
	v_exp_f32_e32 v115, v115
	v_exp_f32_e32 v112, v112
	v_exp_f32_e32 v113, v113
	v_add_f32_e64 v114, v114, 1.0
	v_add_f32_e64 v115, v115, 1.0
	s_nop 0
	v_rcp_f32_e32 v121, v114
	v_add_f32_e64 v112, v112, 1.0
	v_add_f32_e64 v113, v113, 1.0
	v_rcp_f32_e32 v122, v115
	v_mul_f32_e32 v114, v90, v118
	v_mul_f32_e32 v115, v91, v118
	v_rcp_f32_e32 v119, v112
	v_rcp_f32_e32 v120, v113
	v_mul_f32_e32 v112, v88, v118
	v_mul_f32_e32 v113, v89, v118
	v_exp_f32_e32 v114, v114
	v_exp_f32_e32 v115, v115
	v_exp_f32_e32 v112, v112
	v_exp_f32_e32 v113, v113
	v_add_f32_e64 v114, v114, 1.0
	v_add_f32_e64 v115, v115, 1.0
	s_nop 0
	v_rcp_f32_e32 v115, v115
	v_add_f32_e64 v112, v112, 1.0
	v_add_f32_e64 v113, v113, 1.0
	v_rcp_f32_e32 v124, v114
	v_rcp_f32_e32 v118, v112
	v_rcp_f32_e32 v123, v113
	v_cvt_pk_bf16_f32 v112, v119, v120
	v_cvt_pk_bf16_f32 v113, v121, v122
	v_cvt_pk_bf16_f32 v114, v118, v123
	v_cvt_pk_bf16_f32 v115, v124, v115
	global_store_dwordx4 v[116:117], v[112:115], off offset:256

;     __device__ __forceinline__ void operator()(const f32x4 (&acc)[2][2][4][2], const Unit& u, int wr, int wc, int fr, int fq, const Pre&) const {
;     ...
;                 } else if (kind == KD_P) {
;                     const float r2 = rs * rs;
;                     st_bf16x8(pbuf + (size_t)row * DM + 128 * (pn - TL_P) + cw, acc[ai][0][m][0] * acc[ai][1][m][0] * r2, acc[ai][0][m][1] * acc[ai][1][m][1] * r2);
.LBB0_1115:
	s_and_b64 vcc, exec, vcc
	s_cbranch_vccz .LBB0_1117
	v_ashrrev_i32_e32 v193, 31, v192
	v_readlane_b32 vcc_lo, v249, 44
	v_lshlrev_b64 v[114:115], 12, v[192:193]
	v_readlane_b32 vcc_hi, v249, 45
	s_waitcnt vmcnt(0)
	v_mul_f32_e32 v112, v190, v190
	v_mul_f32_e64 v118, v100, v92
	v_mul_f32_e64 v119, v101, v93
	v_lshl_add_u64 v[114:115], vcc, 0, v[114:115]
	v_lshl_add_u64 v[114:115], s[42:43], 1, v[114:115]
	v_lshl_add_u64 v[116:117], v[172:173], 1, v[114:115]
	v_mul_f32_e64 v114, v102, v94
	v_mul_f32_e64 v115, v103, v95
	v_mul_f32_e64 v120, v98, v90
	v_mul_f32_e64 v121, v99, v91
	v_mul_f32_e64 v114, v114, v112
	v_mul_f32_e64 v115, v115, v112
	v_mul_f32_e64 v122, v96, v88
	v_mul_f32_e64 v123, v97, v89
	v_mul_f32_e64 v118, v118, v112
	v_mul_f32_e64 v119, v119, v112
	v_mul_f32_e64 v120, v120, v112
	v_mul_f32_e64 v121, v121, v112
	v_mul_f32_e64 v122, v122, v112
	v_mul_f32_e64 v123, v123, v112
	v_cvt_pk_bf16_f32 v112, v118, v119
	v_cvt_pk_bf16_f32 v113, v114, v115
	s_nop 0
	v_cvt_pk_bf16_f32 v114, v122, v123
	v_cvt_pk_bf16_f32 v115, v120, v121
	global_store_dwordx4 v[116:117], v[112:115], off

;     __device__ __forceinline__ void operator()(const f32x4 (&acc)[2][2][4][2], const Unit& u, int wr, int wc, int fr, int fq, const Pre&) const {
;     ...
;                 } else {
;                     const f32x4 x1 = acc[ai][0][m][0] * rs, x2 = acc[ai][0][m][1] * rs;
;                     if (wc < 2) {
;                         if (roti) st_bf16x8(kib + (size_t)row * 64 + cw, x1 * cs[q] - x2 * sn[q], x2 * cs[q] + x1 * sn[q]);
;                         else st_bf16x8(kib + (size_t)row * 64 + cw, x1, x2);
;                     } else if (wc == 2 && fq < 2) {
;                         *(f32x4*)(wib + (size_t)row * 16 + 8 * fq) = x1 * 0.03125f; *(f32x4*)(wib + (size_t)row * 16 + 8 * fq + 4) = x2 * 0.03125f;
;                     }
.LBB0_1119:
	s_andn2_b64 vcc, exec, s[64:65]
	s_mov_b64 s[2:3], -1
	s_cbranch_vccnz .LBB0_1147
	s_andn2_b64 vcc, exec, s[58:59]
	s_cbranch_vccnz .LBB0_1144
	v_readlane_b32 s56, v249, 63
	s_waitcnt vmcnt(0)
	v_mov_b32_e32 v191, v190
	v_readlane_b32 s57, v248, 0
	s_andn2_b64 vcc, exec, s[56:57]
	v_mul_f32_e64 v114, v100, v190
	v_mul_f32_e64 v115, v101, v191
	v_mul_f32_e64 v112, v96, v190
	v_mul_f32_e64 v113, v97, v191
	s_cbranch_vccnz .LBB0_1133
	v_readlane_b32 s2, v248, 24
	v_mov_b32_e32 v116, v190
	v_mov_b32_e32 v117, v190
	v_readlane_b32 s3, v248, 25
	v_mul_f32_e64 v118, v102, v116
	v_mul_f32_e64 v119, v103, v117
	v_mul_f32_e64 v116, v98, v116
	v_mul_f32_e64 v117, v99, v117
	s_andn2_b64 vcc, exec, s[2:3]
	s_mov_b64 s[2:3], -1
	s_cbranch_vccnz .LBB0_1126
	s_mov_b64 s[2:3], exec
	v_readlane_b32 s56, v248, 7
	v_readlane_b32 s57, v248, 8
	s_and_b64 s[56:57], s[2:3], s[56:57]
	s_mov_b64 exec, s[56:57]
	s_cbranch_execz .LBB0_1125
	v_ashrrev_i32_e32 v193, 31, v192
	v_readlane_b32 s56, v249, 56
	v_lshlrev_b64 v[124:125], 6, v[192:193]
	v_readlane_b32 s57, v249, 57
	s_mov_b32 s4, 0x3d000000
	v_mul_f32_e64 v122, v118, s4
	v_mul_f32_e64 v123, v119, s4
	v_lshl_add_u64 v[124:125], s[56:57], 0, v[124:125]
	v_mul_f32_e64 v120, v114, s4
	v_mul_f32_e64 v121, v115, s4
	v_lshl_add_u64 v[124:125], v[174:175], 2, v[124:125]
	global_store_dwordx4 v[124:125], v[120:123], off
	s_nop 1
	v_mul_f32_e64 v122, v116, s4
	v_mul_f32_e64 v123, v117, s4
	v_mul_f32_e64 v120, v112, s4
	v_mul_f32_e64 v121, v113, s4
	global_store_dwordx4 v[124:125], v[120:123], off offset:16

;     __device__ __forceinline__ void operator()(const f32x4 (&acc)[2][2][4][2], const Unit& u, int wr, int wc, int fr, int fq, const Pre&) const {
;     ...
;                     const f32x4 x1 = acc[ai][0][m][0] * rs, x2 = acc[ai][0][m][1] * rs;
;                     if (wc < 2) {
;                         if (roti) st_bf16x8(kib + (size_t)row * 64 + cw, x1 * cs[q] - x2 * sn[q], x2 * cs[q] + x1 * sn[q]);
;                         else st_bf16x8(kib + (size_t)row * 64 + cw, x1, x2);
.LBB0_1129:
	s_andn2_saveexec_b64 s[2:3], s[2:3]
	s_cbranch_execz .LBB0_1131
	v_mul_f32_e64 v122, v116, v106
	v_mul_f32_e64 v123, v117, v107
	v_mul_f32_e64 v116, v116, v110
	v_mul_f32_e64 v117, v117, v111
	v_mul_f32_e64 v126, v112, v108
	v_mul_f32_e64 v127, v113, v109
	v_mul_f32_e64 v124, v112, v104
	v_mul_f32_e64 v125, v113, v105
	v_fma_f32 v122, v118, v110, -v122
	v_fma_f32 v123, v119, v111, -v123
	v_fma_f32 v128, v118, v106, v116
	v_fma_f32 v129, v119, v107, v117
	v_fma_f32 v118, v114, v104, v126
	v_fma_f32 v119, v115, v105, v127
	v_fma_f32 v124, v114, v108, -v124
	v_fma_f32 v125, v115, v109, -v125
	s_nop 0
	v_cvt_pk_bf16_f32 v116, v124, v125
	v_cvt_pk_bf16_f32 v117, v122, v123
	v_cvt_pk_bf16_f32 v118, v118, v119
	v_cvt_pk_bf16_f32 v119, v128, v129
	global_store_dwordx4 v[120:121], v[116:119], off

;     __device__ __forceinline__ void operator()(const f32x4 (&acc)[2][2][4][2], const Unit& u, int wr, int wc, int fr, int fq, const Pre&) const {
;     ...
;                 } else if (kind == KD_QI) {
; #pragma unroll
;                     for (int bj = 0; bj < 2; ++bj) {
;                         const f32x4 x1 = acc[ai][bj][m][0] * rs, x2 = acc[ai][bj][m][1] * rs;
;                         bf16_t* o = qib + (size_t)row * 1024 + 256 * (pn - TL_QI) + 128 * bj + cw;
;                         if (roti) st_bf16x8(o, x1 * cs[q] - x2 * sn[q], x2 * cs[q] + x1 * sn[q]); else st_bf16x8(o, x1, x2);
;                     }
.LBB0_1133:
	s_andn2_b64 vcc, exec, s[2:3]
	s_cbranch_vccnz .LBB0_1143
	v_mov_b32_e32 v116, v190
	v_mov_b32_e32 v117, v190
	v_readlane_b32 vcc_lo, v248, 9
	v_mul_f32_e64 v124, v102, v116
	v_mul_f32_e64 v125, v103, v117
	v_mul_f32_e64 v122, v98, v116
	v_mul_f32_e64 v123, v99, v117
	v_readlane_b32 vcc_hi, v248, 10
	s_and_saveexec_b64 s[2:3], vcc
	s_xor_b64 s[2:3], exec, s[2:3]
	s_cbranch_execz .LBB0_1136
	v_cvt_pk_bf16_f32 v118, v114, v115
	v_cvt_pk_bf16_f32 v119, v124, v125
	v_cvt_pk_bf16_f32 v120, v112, v113
	v_cvt_pk_bf16_f32 v121, v122, v123
.LBB0_1136:
	s_andn2_saveexec_b64 s[2:3], s[2:3]
	s_cbranch_execz .LBB0_1138
	v_mul_f32_e64 v118, v112, v104
	v_mul_f32_e64 v119, v113, v105
	v_mul_f32_e64 v116, v122, v106
	v_mul_f32_e64 v117, v123, v107
	v_fma_f32 v118, v114, v108, -v118
	v_fma_f32 v119, v115, v109, -v119
	v_mul_f32_e64 v120, v122, v110
	v_mul_f32_e64 v121, v123, v111
	v_mul_f32_e64 v112, v112, v108
	v_mul_f32_e64 v113, v113, v109
	v_fma_f32 v116, v124, v110, -v116
	v_fma_f32 v117, v125, v111, -v117
	v_fma_f32 v122, v124, v106, v120
	v_fma_f32 v123, v125, v107, v121
	v_fma_f32 v112, v114, v104, v112
	v_fma_f32 v113, v115, v105, v113
	v_cvt_pk_bf16_f32 v118, v118, v119
	v_cvt_pk_bf16_f32 v119, v116, v117
	s_nop 0
	v_cvt_pk_bf16_f32 v120, v112, v113
	v_cvt_pk_bf16_f32 v121, v122, v123
.LBB0_1138:
	s_or_b64 exec, exec, s[2:3]
	v_ashrrev_i32_e32 v193, 31, v192
	v_readlane_b32 s2, v248, 18
	v_lshlrev_b64 v[112:113], 11, v[192:193]
	v_readlane_b32 s3, v248, 19
	v_mul_f32_e64 v116, v88, v190
	v_mul_f32_e64 v117, v89, v191
	s_nop 0
	v_lshl_add_u64 v[112:113], s[2:3], 0, v[112:113]
	v_lshl_add_u64 v[112:113], s[28:29], 1, v[112:113]
	v_lshl_add_u64 v[122:123], v[172:173], 1, v[112:113]
	v_mov_b32_e32 v112, v190
	v_mov_b32_e32 v113, v190
	global_store_dwordx4 v[122:123], v[118:121], off
	v_mul_f32_e64 v126, v94, v112
	v_mul_f32_e64 v127, v95, v113
	v_mul_f32_e64 v124, v90, v112
	v_mul_f32_e64 v125, v91, v113
	v_mul_f32_e64 v118, v92, v190
	v_mul_f32_e64 v119, v93, v191
	s_and_saveexec_b64 s[2:3], vcc
	s_xor_b64 s[2:3], exec, s[2:3]
	s_cbranch_execz .LBB0_1140
	v_cvt_pk_bf16_f32 v112, v118, v119
	v_cvt_pk_bf16_f32 v113, v126, v127
	v_cvt_pk_bf16_f32 v114, v116, v117
	v_cvt_pk_bf16_f32 v115, v124, v125
.LBB0_1140:
	s_andn2_saveexec_b64 s[2:3], s[2:3]
	s_cbranch_execz .LBB0_1142
	v_mul_f32_e64 v112, v124, v106
	v_mul_f32_e64 v113, v125, v107
	v_mul_f32_e64 v114, v116, v104
	v_mul_f32_e64 v115, v117, v105
	v_fma_f32 v120, v126, v110, -v112
	v_fma_f32 v121, v127, v111, -v113
	v_fma_f32 v112, v118, v108, -v114
	v_fma_f32 v113, v119, v109, -v115
	v_mul_f32_e64 v114, v124, v110
	v_mul_f32_e64 v115, v125, v111
	v_mul_f32_e64 v116, v116, v108
	v_mul_f32_e64 v117, v117, v109
	v_fma_f32 v124, v126, v106, v114
	v_fma_f32 v125, v127, v107, v115
	v_fma_f32 v114, v118, v104, v116
	v_fma_f32 v115, v119, v105, v117
	v_cvt_pk_bf16_f32 v112, v112, v113
	v_cvt_pk_bf16_f32 v113, v120, v121
	s_nop 0
	v_cvt_pk_bf16_f32 v114, v114, v115
	v_cvt_pk_bf16_f32 v115, v124, v125

;     __device__ __forceinline__ void operator()(const f32x4 (&acc)[2][2][4][2], const Unit& u, int wr, int wc, int fr, int fq, const Pre&) const {
;     ...
;                 } else if (kind == KD_V) {
; #pragma unroll
;                     for (int bj = 0; bj < 2; ++bj) st_bf16x8(vb + (size_t)row * 512 + 256 * (pn - TL_V) + 128 * bj + cw, acc[ai][bj][m][0] * rs, acc[ai][bj][m][1] * rs);
.LBB0_1144:
	s_andn2_b64 vcc, exec, s[2:3]
	s_cbranch_vccnz .LBB0_1146
	v_ashrrev_i32_e32 v193, 31, v192
	v_readlane_b32 s2, v249, 52
	v_lshlrev_b64 v[112:113], 10, v[192:193]
	v_readlane_b32 s3, v249, 53
	s_waitcnt vmcnt(0)
	v_mul_f32_e64 v114, v102, v190
	v_mul_f32_e64 v115, v103, v190
	v_mul_f32_e64 v118, v98, v190
	v_mul_f32_e64 v119, v99, v190
	v_lshl_add_u64 v[112:113], s[2:3], 0, v[112:113]
	v_lshl_add_u64 v[112:113], s[94:95], 1, v[112:113]
	v_lshl_add_u64 v[116:117], v[172:173], 1, v[112:113]
	v_mul_f32_e64 v112, v100, v190
	v_mul_f32_e64 v113, v101, v190
	v_mul_f32_e64 v120, v96, v190
	v_mul_f32_e64 v121, v97, v190
	v_cvt_pk_bf16_f32 v112, v112, v113
	v_cvt_pk_bf16_f32 v113, v114, v115
	s_nop 0
	v_cvt_pk_bf16_f32 v114, v120, v121
	v_cvt_pk_bf16_f32 v115, v118, v119
	global_store_dwordx4 v[116:117], v[112:115], off
	v_mul_f32_e64 v118, v90, v190
	v_mul_f32_e64 v119, v91, v190
	v_mul_f32_e64 v120, v88, v190
	v_mul_f32_e64 v121, v89, v190
	v_mul_f32_e64 v114, v94, v190
	v_mul_f32_e64 v115, v95, v190
	v_mul_f32_e64 v112, v92, v190
	v_mul_f32_e64 v113, v93, v190
	s_nop 0
	v_cvt_pk_bf16_f32 v112, v112, v113
	v_cvt_pk_bf16_f32 v113, v114, v115
	v_cvt_pk_bf16_f32 v114, v120, v121
	v_cvt_pk_bf16_f32 v115, v118, v119
	global_store_dwordx4 v[116:117], v[112:115], off offset:256

;     __device__ __forceinline__ void operator()(const f32x4 (&acc)[2][2][4][2], const Unit& u, int wr, int wc, int fr, int fq, const Pre&) const {
;     ...
;                 } else if (kind == KD_Q || kind == KD_K) {
;                     bf16_t* o = (kind == KD_Q) ? qb + (size_t)row * DM + 256 * (pn - TL_Q) + cw : kb + (size_t)row * 512 + 256 * (pn - TL_K) + cw;
; #pragma unroll
;                     for (int bj = 0; bj < 2; ++bj) {
;                         const f32x4 x1 = acc[ai][bj][m][0] * rs, x2 = acc[ai][bj][m][1] * rs;
;                         if (rotqk) st_bf16x8(o + 128 * bj, x1 * cs[q] - x2 * sn[q], x2 * cs[q] + x1 * sn[q]);
;                         else st_bf16x8(o + 128 * bj, x1, x2);
;                     }
.LBB0_1147:
	s_andn2_b64 vcc, exec, s[2:3]
	s_cbranch_vccnz .LBB0_1157
	v_cndmask_b32_e64 v112, 0, 1, s[92:93]
	s_waitcnt vmcnt(0)
	v_mul_f32_e64 v116, v102, v190
	v_mul_f32_e64 v117, v103, v190
	v_mul_f32_e64 v118, v100, v190
	v_mul_f32_e64 v119, v101, v190
	v_mul_f32_e64 v120, v98, v190
	v_mul_f32_e64 v121, v99, v190
	v_mul_f32_e64 v122, v96, v190
	v_mul_f32_e64 v123, v97, v190
	v_cmp_ne_u32_e64 s[2:3], 1, v112
	s_andn2_b64 vcc, exec, s[92:93]
	s_mov_b64 s[56:57], -1
	s_cbranch_vccnz .LBB0_1150
	s_mov_b64 s[56:57], 0
	v_cvt_pk_bf16_f32 v112, v118, v119
	v_cvt_pk_bf16_f32 v113, v116, v117
	v_cvt_pk_bf16_f32 v114, v122, v123
	v_cvt_pk_bf16_f32 v115, v120, v121
.LBB0_1150:
	s_andn2_b64 vcc, exec, s[56:57]
	s_cbranch_vccnz .LBB0_1152
	v_mul_f32_e64 v112, v120, v106
	v_mul_f32_e64 v113, v121, v107
	v_mul_f32_e64 v114, v122, v104
	v_mul_f32_e64 v115, v123, v105
	v_fma_f32 v124, v116, v110, -v112
	v_fma_f32 v125, v117, v111, -v113
	v_fma_f32 v112, v118, v108, -v114
	v_fma_f32 v113, v119, v109, -v115
	v_mul_f32_e64 v114, v120, v110
	v_mul_f32_e64 v115, v121, v111
	v_mul_f32_e64 v120, v122, v108
	v_mul_f32_e64 v121, v123, v109
	v_fma_f32 v116, v116, v106, v114
	v_fma_f32 v117, v117, v107, v115
	v_fma_f32 v114, v118, v104, v120
	v_fma_f32 v115, v119, v105, v121
	v_cvt_pk_bf16_f32 v112, v112, v113
	v_cvt_pk_bf16_f32 v113, v124, v125
	s_nop 0
	v_cvt_pk_bf16_f32 v114, v114, v115
	v_cvt_pk_bf16_f32 v115, v116, v117
.LBB0_1152:
	s_and_b64 s[56:57], s[90:91], exec
	v_readlane_b32 s4, v249, 49
	v_readlane_b32 s56, v249, 51
	s_cselect_b32 s57, s4, s56
	v_readlane_b32 s4, v249, 48
	v_readlane_b32 s56, v249, 50
	v_ashrrev_i32_e32 v193, 31, v192
	s_cselect_b32 s56, s4, s56
	s_cselect_b32 s4, 12, 10
	v_lshlrev_b64 v[116:117], s4, v[192:193]
	s_cselect_b32 vcc_hi, s34, s30
	s_cselect_b32 vcc_lo, s31, s81
	v_lshl_add_u64 v[116:117], s[56:57], 0, v[116:117]
	v_lshl_add_u64 v[116:117], vcc, 1, v[116:117]
	v_lshl_add_u64 v[116:117], v[172:173], 1, v[116:117]
	v_mov_b32_e32 v191, v190
	global_store_dwordx4 v[116:117], v[112:115], off
	v_mul_f32_e64 v120, v92, v190
	v_mul_f32_e64 v121, v93, v191
	v_mul_f32_e64 v124, v88, v190
	v_mul_f32_e64 v125, v89, v191
	v_mov_b32_e32 v112, v190
	v_mov_b32_e32 v113, v190
	v_mul_f32_e64 v118, v94, v112
	v_mul_f32_e64 v119, v95, v113
	v_mul_f32_e64 v122, v90, v112
	v_mul_f32_e64 v123, v91, v113
	s_and_b64 vcc, exec, s[2:3]
	s_mov_b64 s[2:3], -1
	s_cbranch_vccnz .LBB0_1154
	s_mov_b64 s[2:3], 0
	v_cvt_pk_bf16_f32 v112, v120, v121
	v_cvt_pk_bf16_f32 v113, v118, v119
	v_cvt_pk_bf16_f32 v114, v124, v125
	v_cvt_pk_bf16_f32 v115, v122, v123
.LBB0_1154:
	s_andn2_b64 vcc, exec, s[2:3]
	s_cbranch_vccnz .LBB0_1156
	v_mul_f32_e64 v112, v122, v106
	v_mul_f32_e64 v113, v123, v107
	v_mul_f32_e64 v114, v124, v104
	v_mul_f32_e64 v115, v125, v105
	v_fma_f32 v126, v118, v110, -v112
	v_fma_f32 v127, v119, v111, -v113
	v_fma_f32 v112, v120, v108, -v114
	v_fma_f32 v113, v121, v109, -v115
	v_mul_f32_e64 v110, v122, v110
	v_mul_f32_e64 v111, v123, v111
	v_mul_f32_e64 v108, v124, v108
	v_mul_f32_e64 v109, v125, v109
	v_fma_f32 v106, v118, v106, v110
	v_fma_f32 v107, v119, v107, v111
	v_fma_f32 v104, v120, v104, v108
	v_fma_f32 v105, v121, v105, v109
	v_cvt_pk_bf16_f32 v112, v112, v113
	v_cvt_pk_bf16_f32 v113, v126, v127
	s_nop 0
	v_cvt_pk_bf16_f32 v114, v104, v105
	v_cvt_pk_bf16_f32 v115, v106, v107

; __device__ __forceinline__ f32x4 sigmoid4(const f32x4& x, float s) {
;     f32x4 z = x * (s * -1.4426950408889634f), e;
; #pragma unroll
;     for (int j = 0; j < 4; ++j) e[j] = __builtin_amdgcn_exp2f(z[j]);
;     e = e + 1.0f;
; #pragma unroll
;     for (int j = 0; j < 4; ++j) e[j] = __builtin_amdgcn_rcpf(e[j]);
;     return e;
; }
;     __device__ __forceinline__ void operator()(const f32x4 (&acc)[2][2][4][2], const Unit& u, int wr, int wc, int fr, int fq, const Pre&) const {
;     ...
;                 } else if (kind == KD_A) {
;                     st_bf16x8(abuf + (size_t)row * DM + 128 * (pn - TL_A) + cw, acc[ai][0][m][0] * rs * sigmoid4(acc[ai][1][m][0], rs), acc[ai][0][m][1] * rs * sigmoid4(acc[ai][1][m][1], rs));
.LBB0_1161:
	s_waitcnt vmcnt(0)
	v_lshlrev_b64 v[88:89], 12, v[112:113]
	v_lshl_add_u64 v[88:89], s[12:13], 0, v[88:89]
	v_lshl_add_u64 v[88:89], s[88:89], 1, v[88:89]
	v_mul_f32_e32 v99, 0xbfb8aa3b, v180
	v_lshl_add_u64 v[92:93], v[172:173], 1, v[88:89]
	v_mul_f32_e32 v88, v48, v99
	v_mul_f32_e32 v89, v49, v99
	v_mul_f32_e32 v90, v50, v99
	v_mul_f32_e32 v91, v51, v99
	v_exp_f32_e32 v88, v88
	v_exp_f32_e32 v90, v90
	v_exp_f32_e32 v91, v91
	v_exp_f32_e32 v89, v89
	v_mul_f32_e32 v98, v52, v99
	v_mul_f32_e32 v102, v53, v99
	v_add_f32_e64 v90, v90, 1.0
	v_add_f32_e64 v91, v91, 1.0
	v_add_f32_e64 v88, v88, 1.0
	v_add_f32_e64 v89, v89, 1.0
	v_mul_f32_e32 v100, v54, v99
	v_mul_f32_e32 v99, v55, v99
	v_rcp_f32_e32 v88, v88
	v_rcp_f32_e32 v89, v89
	v_rcp_f32_e32 v90, v90
	v_rcp_f32_e32 v91, v91
	v_exp_f32_e32 v98, v98
	v_exp_f32_e32 v100, v100
	v_exp_f32_e32 v101, v99
	v_exp_f32_e32 v99, v102
	v_mul_f32_e64 v94, v62, v180
	v_mul_f32_e64 v95, v63, v180
	v_mul_f32_e64 v96, v60, v180
	v_mul_f32_e64 v97, v61, v180
	v_mul_f32_e64 v90, v94, v90
	v_mul_f32_e64 v91, v95, v91
	v_mul_f32_e64 v88, v96, v88
	v_mul_f32_e64 v89, v97, v89
	v_add_f32_e64 v94, v100, 1.0
	v_add_f32_e64 v95, v101, 1.0
	v_add_f32_e64 v96, v98, 1.0
	v_add_f32_e64 v97, v99, 1.0
	v_rcp_f32_e32 v94, v94
	v_rcp_f32_e32 v96, v96
	v_rcp_f32_e32 v95, v95
	v_rcp_f32_e32 v97, v97
	v_mul_f32_e64 v98, v58, v180
	v_mul_f32_e64 v99, v59, v180
	v_mul_f32_e64 v100, v56, v180
	v_mul_f32_e64 v101, v57, v180
	v_mul_f32_e64 v94, v98, v94
	v_mul_f32_e64 v95, v99, v95
	v_mul_f32_e64 v96, v100, v96
	v_mul_f32_e64 v97, v101, v97
	v_cvt_pk_bf16_f32 v88, v88, v89
	v_cvt_pk_bf16_f32 v89, v90, v91
	s_nop 0
	v_cvt_pk_bf16_f32 v90, v96, v97
	v_cvt_pk_bf16_f32 v91, v94, v95
	global_store_dwordx4 v[92:93], v[88:91], off

; __device__ __forceinline__ f32x4 sigmoid4(const f32x4& x, float s) {
;     f32x4 z = x * (s * -1.4426950408889634f), e;
; #pragma unroll
;     for (int j = 0; j < 4; ++j) e[j] = __builtin_amdgcn_exp2f(z[j]);
;     e = e + 1.0f;
; #pragma unroll
;     for (int j = 0; j < 4; ++j) e[j] = __builtin_amdgcn_rcpf(e[j]);
;     return e;
; }
;     __device__ __forceinline__ void operator()(const f32x4 (&acc)[2][2][4][2], const Unit& u, int wr, int wc, int fr, int fq, const Pre&) const {
;     ...
;                 } else if (kind == KD_G) {
; #pragma unroll
;                     for (int bj = 0; bj < 2; ++bj)
;                         st_bf16x8(gabuf + (size_t)row * DM + 256 * (pn - TL_G) + 128 * bj + cw, sigmoid4(acc[ai][bj][m][0], rs), sigmoid4(acc[ai][bj][m][1], rs));
.LBB0_1164:
	s_mov_b64 s[36:37], -1
	s_mov_b64 s[2:3], 0
	s_cmp_lt_i32 s7, 1
	s_mov_b64 s[16:17], 0
	s_cbranch_scc1 .LBB0_1266
	s_cmp_gt_i32 s7, 1
	s_cbranch_scc0 .LBB0_1169
	s_cmp_eq_u32 s7, 2
	s_mov_b64 s[16:17], -1
	s_cbranch_scc0 .LBB0_1168
	v_ashrrev_i32_e32 v111, 31, v110
	v_readlane_b32 s16, v249, 46
	v_lshlrev_b64 v[48:49], 12, v[110:111]
	v_readlane_b32 s17, v249, 47
	v_mul_f32_e32 v54, 0xbfb8aa3b, v178
	v_mul_f32_e32 v50, v38, v54
	v_lshl_add_u64 v[48:49], s[16:17], 0, v[48:49]
	v_lshl_add_u64 v[48:49], s[38:39], 1, v[48:49]
	v_mul_f32_e32 v51, v39, v54
	v_lshl_add_u64 v[52:53], v[172:173], 1, v[48:49]
	v_mul_f32_e32 v48, v36, v54
	v_mul_f32_e32 v49, v37, v54
	v_exp_f32_e32 v50, v50
	v_exp_f32_e32 v51, v51
	v_exp_f32_e32 v48, v48
	v_exp_f32_e32 v49, v49
	s_mov_b64 s[16:17], 0
	v_add_f32_e64 v50, v50, 1.0
	v_add_f32_e64 v51, v51, 1.0
	v_add_f32_e64 v48, v48, 1.0
	v_add_f32_e64 v49, v49, 1.0
	v_rcp_f32_e32 v57, v50
	v_rcp_f32_e32 v58, v51
	v_mul_f32_e32 v50, v34, v54
	v_mul_f32_e32 v51, v35, v54
	v_rcp_f32_e32 v55, v48
	v_rcp_f32_e32 v56, v49
	v_mul_f32_e32 v48, v32, v54
	v_mul_f32_e32 v49, v33, v54
	v_exp_f32_e32 v50, v50
	v_exp_f32_e32 v51, v51
	v_exp_f32_e32 v48, v48
	v_exp_f32_e32 v49, v49
	v_add_f32_e64 v50, v50, 1.0
	v_add_f32_e64 v51, v51, 1.0
	s_nop 0
	v_rcp_f32_e32 v51, v51
	v_add_f32_e64 v48, v48, 1.0
	v_add_f32_e64 v49, v49, 1.0
	v_rcp_f32_e32 v61, v50
	v_rcp_f32_e32 v59, v48
	v_rcp_f32_e32 v60, v49
	v_cvt_pk_bf16_f32 v48, v55, v56
	v_cvt_pk_bf16_f32 v49, v57, v58
	v_cvt_pk_bf16_f32 v50, v59, v60
	v_cvt_pk_bf16_f32 v51, v61, v51
	global_store_dwordx4 v[52:53], v[48:51], off
	s_nop 1
	v_mul_f32_e32 v50, v42, v54
	v_mul_f32_e32 v51, v43, v54
	v_mul_f32_e32 v48, v40, v54
	v_mul_f32_e32 v49, v41, v54
	v_exp_f32_e32 v50, v50
	v_exp_f32_e32 v51, v51
	v_exp_f32_e32 v48, v48
	v_exp_f32_e32 v49, v49
	v_add_f32_e64 v50, v50, 1.0
	v_add_f32_e64 v51, v51, 1.0
	s_nop 0
	v_rcp_f32_e32 v57, v50
	v_add_f32_e64 v48, v48, 1.0
	v_add_f32_e64 v49, v49, 1.0
	v_rcp_f32_e32 v58, v51
	v_mul_f32_e32 v50, v46, v54
	v_mul_f32_e32 v51, v47, v54
	v_rcp_f32_e32 v55, v48
	v_rcp_f32_e32 v56, v49
	v_mul_f32_e32 v48, v44, v54
	v_mul_f32_e32 v49, v45, v54
	v_exp_f32_e32 v50, v50
	v_exp_f32_e32 v51, v51
	v_exp_f32_e32 v48, v48
	v_exp_f32_e32 v49, v49
	v_add_f32_e64 v50, v50, 1.0
	v_add_f32_e64 v51, v51, 1.0
	s_nop 0
	v_rcp_f32_e32 v51, v51
	v_add_f32_e64 v48, v48, 1.0
	v_add_f32_e64 v49, v49, 1.0
	v_rcp_f32_e32 v60, v50
	v_rcp_f32_e32 v54, v48
	v_rcp_f32_e32 v59, v49
	v_cvt_pk_bf16_f32 v48, v55, v56
	v_cvt_pk_bf16_f32 v49, v57, v58
	v_cvt_pk_bf16_f32 v50, v54, v59
	v_cvt_pk_bf16_f32 v51, v60, v51
	global_store_dwordx4 v[52:53], v[48:51], off offset:256

;     __device__ __forceinline__ void operator()(const f32x4 (&acc)[2][2][4][2], const Unit& u, int wr, int wc, int fr, int fq, const Pre&) const {
;     ...
;                 } else if (kind == KD_P) {
;                     const float r2 = rs * rs;
;                     st_bf16x8(pbuf + (size_t)row * DM + 128 * (pn - TL_P) + cw, acc[ai][0][m][0] * acc[ai][1][m][0] * r2, acc[ai][0][m][1] * acc[ai][1][m][1] * r2);
.LBB0_1169:
	s_and_b64 vcc, exec, s[36:37]
	s_cbranch_vccz .LBB0_1171
	v_ashrrev_i32_e32 v111, 31, v110
	v_readlane_b32 s36, v249, 44
	v_lshlrev_b64 v[50:51], 12, v[110:111]
	v_readlane_b32 s37, v249, 45
	v_mul_f32_e32 v48, v178, v178
	v_mul_f32_e64 v54, v36, v40
	v_mul_f32_e64 v55, v37, v41
	v_lshl_add_u64 v[50:51], s[36:37], 0, v[50:51]
	v_lshl_add_u64 v[50:51], s[42:43], 1, v[50:51]
	v_lshl_add_u64 v[52:53], v[172:173], 1, v[50:51]
	v_mul_f32_e64 v50, v38, v42
	v_mul_f32_e64 v51, v39, v43
	v_mul_f32_e64 v56, v34, v46
	v_mul_f32_e64 v57, v35, v47
	v_mul_f32_e64 v50, v50, v48
	v_mul_f32_e64 v51, v51, v48
	v_mul_f32_e64 v58, v32, v44
	v_mul_f32_e64 v59, v33, v45
	v_mul_f32_e64 v54, v54, v48
	v_mul_f32_e64 v55, v55, v48
	v_mul_f32_e64 v56, v56, v48
	v_mul_f32_e64 v57, v57, v48
	v_mul_f32_e64 v58, v58, v48
	v_mul_f32_e64 v59, v59, v48
	v_cvt_pk_bf16_f32 v48, v54, v55
	v_cvt_pk_bf16_f32 v49, v50, v51
	s_nop 0
	v_cvt_pk_bf16_f32 v50, v58, v59
	v_cvt_pk_bf16_f32 v51, v56, v57
	global_store_dwordx4 v[52:53], v[48:51], off

;     __device__ __forceinline__ void operator()(const f32x4 (&acc)[2][2][4][2], const Unit& u, int wr, int wc, int fr, int fq, const Pre&) const {
;     ...
;                 } else {
;                     const f32x4 x1 = acc[ai][0][m][0] * rs, x2 = acc[ai][0][m][1] * rs;
;                     if (wc < 2) {
;                         if (roti) st_bf16x8(kib + (size_t)row * 64 + cw, x1 * cs[q] - x2 * sn[q], x2 * cs[q] + x1 * sn[q]);
;                         else st_bf16x8(kib + (size_t)row * 64 + cw, x1, x2);
;                     } else if (wc == 2 && fq < 2) {
;                         *(f32x4*)(wib + (size_t)row * 16 + 8 * fq) = x1 * 0.03125f; *(f32x4*)(wib + (size_t)row * 16 + 8 * fq + 4) = x2 * 0.03125f;
;                     }
.LBB0_1173:
	s_andn2_b64 vcc, exec, s[64:65]
	s_mov_b64 s[2:3], -1
	s_cbranch_vccnz .LBB0_1201
	s_andn2_b64 vcc, exec, s[58:59]
	s_cbranch_vccnz .LBB0_1198
	v_readlane_b32 s16, v249, 63
	v_mov_b32_e32 v179, v178
	v_readlane_b32 s17, v248, 0
	s_andn2_b64 vcc, exec, s[16:17]
	v_mul_f32_e64 v50, v36, v178
	v_mul_f32_e64 v51, v37, v179
	v_mul_f32_e64 v48, v32, v178
	v_mul_f32_e64 v49, v33, v179
	s_cbranch_vccnz .LBB0_1187
	v_readlane_b32 s2, v248, 24
	v_mov_b32_e32 v52, v178
	v_mov_b32_e32 v53, v178
	v_readlane_b32 s3, v248, 25
	v_mul_f32_e64 v54, v38, v52
	v_mul_f32_e64 v55, v39, v53
	v_mul_f32_e64 v52, v34, v52
	v_mul_f32_e64 v53, v35, v53
	s_andn2_b64 vcc, exec, s[2:3]
	s_mov_b64 s[2:3], -1
	s_cbranch_vccnz .LBB0_1180
	s_mov_b64 s[2:3], exec
	v_readlane_b32 s16, v248, 7
	v_readlane_b32 s17, v248, 8
	s_and_b64 s[16:17], s[2:3], s[16:17]
	s_mov_b64 exec, s[16:17]
	s_cbranch_execz .LBB0_1179
	v_ashrrev_i32_e32 v111, 31, v110
	v_readlane_b32 s16, v249, 56
	v_lshlrev_b64 v[60:61], 6, v[110:111]
	v_readlane_b32 s17, v249, 57
	s_mov_b32 s4, 0x3d000000
	v_mul_f32_e64 v58, v54, s4
	v_mul_f32_e64 v59, v55, s4
	v_lshl_add_u64 v[60:61], s[16:17], 0, v[60:61]
	v_mul_f32_e64 v56, v50, s4
	v_mul_f32_e64 v57, v51, s4
	v_lshl_add_u64 v[60:61], v[174:175], 2, v[60:61]
	global_store_dwordx4 v[60:61], v[56:59], off
	s_nop 1
	v_mul_f32_e64 v58, v52, s4
	v_mul_f32_e64 v59, v53, s4
	v_mul_f32_e64 v56, v48, s4
	v_mul_f32_e64 v57, v49, s4
	global_store_dwordx4 v[60:61], v[56:59], off offset:16

;     __device__ __forceinline__ void operator()(const f32x4 (&acc)[2][2][4][2], const Unit& u, int wr, int wc, int fr, int fq, const Pre&) const {
;     ...
;                     const f32x4 x1 = acc[ai][0][m][0] * rs, x2 = acc[ai][0][m][1] * rs;
;                     if (wc < 2) {
;                         if (roti) st_bf16x8(kib + (size_t)row * 64 + cw, x1 * cs[q] - x2 * sn[q], x2 * cs[q] + x1 * sn[q]);
;                         else st_bf16x8(kib + (size_t)row * 64 + cw, x1, x2);
.LBB0_1183:
	s_andn2_saveexec_b64 s[2:3], s[2:3]
	s_cbranch_execz .LBB0_1185
	s_waitcnt vmcnt(0)
	v_mul_f32_e64 v58, v52, v82
	v_mul_f32_e64 v59, v53, v83
	v_mul_f32_e64 v52, v52, v86
	v_mul_f32_e64 v53, v53, v87
	v_mul_f32_e64 v62, v48, v84
	v_mul_f32_e64 v63, v49, v85
	v_mul_f32_e64 v60, v48, v80
	v_mul_f32_e64 v61, v49, v81
	v_fma_f32 v58, v54, v86, -v58
	v_fma_f32 v59, v55, v87, -v59
	v_fma_f32 v88, v54, v82, v52
	v_fma_f32 v89, v55, v83, v53
	v_fma_f32 v54, v50, v80, v62
	v_fma_f32 v55, v51, v81, v63
	v_fma_f32 v60, v50, v84, -v60
	v_fma_f32 v61, v51, v85, -v61
	s_nop 0
	v_cvt_pk_bf16_f32 v52, v60, v61
	v_cvt_pk_bf16_f32 v53, v58, v59
	v_cvt_pk_bf16_f32 v54, v54, v55
	v_cvt_pk_bf16_f32 v55, v88, v89
	global_store_dwordx4 v[56:57], v[52:55], off

;     __device__ __forceinline__ void operator()(const f32x4 (&acc)[2][2][4][2], const Unit& u, int wr, int wc, int fr, int fq, const Pre&) const {
;     ...
;                 } else if (kind == KD_QI) {
; #pragma unroll
;                     for (int bj = 0; bj < 2; ++bj) {
;                         const f32x4 x1 = acc[ai][bj][m][0] * rs, x2 = acc[ai][bj][m][1] * rs;
;                         bf16_t* o = qib + (size_t)row * 1024 + 256 * (pn - TL_QI) + 128 * bj + cw;
;                         if (roti) st_bf16x8(o, x1 * cs[q] - x2 * sn[q], x2 * cs[q] + x1 * sn[q]); else st_bf16x8(o, x1, x2);
;                     }
.LBB0_1187:
	s_andn2_b64 vcc, exec, s[2:3]
	s_cbranch_vccnz .LBB0_1197
	v_mov_b32_e32 v52, v178
	v_mov_b32_e32 v53, v178
	v_readlane_b32 s36, v248, 9
	v_mul_f32_e64 v60, v38, v52
	v_mul_f32_e64 v61, v39, v53
	v_mul_f32_e64 v58, v34, v52
	v_mul_f32_e64 v59, v35, v53
	v_readlane_b32 s37, v248, 10
	s_and_saveexec_b64 s[2:3], s[36:37]
	s_xor_b64 s[2:3], exec, s[2:3]
	s_cbranch_execz .LBB0_1190
	v_cvt_pk_bf16_f32 v54, v50, v51
	v_cvt_pk_bf16_f32 v55, v60, v61
	v_cvt_pk_bf16_f32 v56, v48, v49
	v_cvt_pk_bf16_f32 v57, v58, v59
.LBB0_1190:
	s_andn2_saveexec_b64 s[2:3], s[2:3]
	s_cbranch_execz .LBB0_1192
	s_waitcnt vmcnt(0)
	v_mul_f32_e64 v54, v48, v80
	v_mul_f32_e64 v55, v49, v81
	v_mul_f32_e64 v52, v58, v82
	v_mul_f32_e64 v53, v59, v83
	v_fma_f32 v54, v50, v84, -v54
	v_fma_f32 v55, v51, v85, -v55
	v_mul_f32_e64 v56, v58, v86
	v_mul_f32_e64 v57, v59, v87
	v_mul_f32_e64 v48, v48, v84
	v_mul_f32_e64 v49, v49, v85
	v_fma_f32 v52, v60, v86, -v52
	v_fma_f32 v53, v61, v87, -v53
	v_fma_f32 v58, v60, v82, v56
	v_fma_f32 v59, v61, v83, v57
	v_fma_f32 v48, v50, v80, v48
	v_fma_f32 v49, v51, v81, v49
	v_cvt_pk_bf16_f32 v54, v54, v55
	v_cvt_pk_bf16_f32 v55, v52, v53
	s_nop 0
	v_cvt_pk_bf16_f32 v56, v48, v49
	v_cvt_pk_bf16_f32 v57, v58, v59
.LBB0_1192:
	s_or_b64 exec, exec, s[2:3]
	v_ashrrev_i32_e32 v111, 31, v110
	v_readlane_b32 s2, v248, 18
	v_lshlrev_b64 v[48:49], 11, v[110:111]
	v_readlane_b32 s3, v248, 19
	v_mul_f32_e64 v52, v44, v178
	v_mul_f32_e64 v53, v45, v179
	s_nop 0
	v_lshl_add_u64 v[48:49], s[2:3], 0, v[48:49]
	v_lshl_add_u64 v[48:49], s[28:29], 1, v[48:49]
	v_lshl_add_u64 v[58:59], v[172:173], 1, v[48:49]
	v_mov_b32_e32 v48, v178
	v_mov_b32_e32 v49, v178
	global_store_dwordx4 v[58:59], v[54:57], off
	v_mul_f32_e64 v62, v42, v48
	v_mul_f32_e64 v63, v43, v49
	v_mul_f32_e64 v60, v46, v48
	v_mul_f32_e64 v61, v47, v49
	v_mul_f32_e64 v54, v40, v178
	v_mul_f32_e64 v55, v41, v179
	s_and_saveexec_b64 s[2:3], s[36:37]
	s_xor_b64 s[2:3], exec, s[2:3]
	s_cbranch_execz .LBB0_1194
	v_cvt_pk_bf16_f32 v48, v54, v55
	v_cvt_pk_bf16_f32 v49, v62, v63
	v_cvt_pk_bf16_f32 v50, v52, v53
	v_cvt_pk_bf16_f32 v51, v60, v61
.LBB0_1194:
	s_andn2_saveexec_b64 s[2:3], s[2:3]
	s_cbranch_execz .LBB0_1196
	s_waitcnt vmcnt(0)
	v_mul_f32_e64 v48, v60, v82
	v_mul_f32_e64 v49, v61, v83
	v_mul_f32_e64 v50, v52, v80
	v_mul_f32_e64 v51, v53, v81
	v_fma_f32 v56, v62, v86, -v48
	v_fma_f32 v57, v63, v87, -v49
	v_fma_f32 v48, v54, v84, -v50
	v_fma_f32 v49, v55, v85, -v51
	v_mul_f32_e64 v50, v60, v86
	v_mul_f32_e64 v51, v61, v87
	v_mul_f32_e64 v52, v52, v84
	v_mul_f32_e64 v53, v53, v85
	v_fma_f32 v60, v62, v82, v50
	v_fma_f32 v61, v63, v83, v51
	v_fma_f32 v50, v54, v80, v52
	v_fma_f32 v51, v55, v81, v53
	v_cvt_pk_bf16_f32 v48, v48, v49
	v_cvt_pk_bf16_f32 v49, v56, v57
	s_nop 0
	v_cvt_pk_bf16_f32 v50, v50, v51
	v_cvt_pk_bf16_f32 v51, v60, v61

;     __device__ __forceinline__ void operator()(const f32x4 (&acc)[2][2][4][2], const Unit& u, int wr, int wc, int fr, int fq, const Pre&) const {
;     ...
;                 } else if (kind == KD_V) {
; #pragma unroll
;                     for (int bj = 0; bj < 2; ++bj) st_bf16x8(vb + (size_t)row * 512 + 256 * (pn - TL_V) + 128 * bj + cw, acc[ai][bj][m][0] * rs, acc[ai][bj][m][1] * rs);
.LBB0_1198:
	s_andn2_b64 vcc, exec, s[2:3]
	s_cbranch_vccnz .LBB0_1200
	v_ashrrev_i32_e32 v111, 31, v110
	v_readlane_b32 s2, v249, 52
	v_lshlrev_b64 v[48:49], 10, v[110:111]
	v_readlane_b32 s3, v249, 53
	v_mul_f32_e64 v50, v38, v178
	v_mul_f32_e64 v51, v39, v178
	v_mul_f32_e64 v54, v34, v178
	v_mul_f32_e64 v55, v35, v178
	v_lshl_add_u64 v[48:49], s[2:3], 0, v[48:49]
	v_lshl_add_u64 v[48:49], s[94:95], 1, v[48:49]
	v_lshl_add_u64 v[52:53], v[172:173], 1, v[48:49]
	v_mul_f32_e64 v48, v36, v178
	v_mul_f32_e64 v49, v37, v178
	v_mul_f32_e64 v56, v32, v178
	v_mul_f32_e64 v57, v33, v178
	v_cvt_pk_bf16_f32 v48, v48, v49
	v_cvt_pk_bf16_f32 v49, v50, v51
	s_nop 0
	v_cvt_pk_bf16_f32 v50, v56, v57
	v_cvt_pk_bf16_f32 v51, v54, v55
	global_store_dwordx4 v[52:53], v[48:51], off
	v_mul_f32_e64 v54, v46, v178
	v_mul_f32_e64 v55, v47, v178
	v_mul_f32_e64 v56, v44, v178
	v_mul_f32_e64 v57, v45, v178
	v_mul_f32_e64 v50, v42, v178
	v_mul_f32_e64 v51, v43, v178
	v_mul_f32_e64 v48, v40, v178
	v_mul_f32_e64 v49, v41, v178
	s_nop 0
	v_cvt_pk_bf16_f32 v48, v48, v49
	v_cvt_pk_bf16_f32 v49, v50, v51
	v_cvt_pk_bf16_f32 v50, v56, v57
	v_cvt_pk_bf16_f32 v51, v54, v55
	global_store_dwordx4 v[52:53], v[48:51], off offset:256

;     __device__ __forceinline__ void operator()(const f32x4 (&acc)[2][2][4][2], const Unit& u, int wr, int wc, int fr, int fq, const Pre&) const {
;     ...
;                 } else if (kind == KD_Q || kind == KD_K) {
;                     bf16_t* o = (kind == KD_Q) ? qb + (size_t)row * DM + 256 * (pn - TL_Q) + cw : kb + (size_t)row * 512 + 256 * (pn - TL_K) + cw;
; #pragma unroll
;                     for (int bj = 0; bj < 2; ++bj) {
;                         const f32x4 x1 = acc[ai][bj][m][0] * rs, x2 = acc[ai][bj][m][1] * rs;
;                         if (rotqk) st_bf16x8(o + 128 * bj, x1 * cs[q] - x2 * sn[q], x2 * cs[q] + x1 * sn[q]);
;                         else st_bf16x8(o + 128 * bj, x1, x2);
;                     }
.LBB0_1201:
	s_andn2_b64 vcc, exec, s[2:3]
	s_cbranch_vccnz .LBB0_1211
	v_cndmask_b32_e64 v48, 0, 1, s[92:93]
	v_mul_f32_e64 v52, v38, v178
	v_mul_f32_e64 v53, v39, v178
	v_mul_f32_e64 v54, v36, v178
	v_mul_f32_e64 v55, v37, v178
	v_mul_f32_e64 v56, v34, v178
	v_mul_f32_e64 v57, v35, v178
	v_mul_f32_e64 v58, v32, v178
	v_mul_f32_e64 v59, v33, v178
	v_cmp_ne_u32_e64 s[2:3], 1, v48
	s_andn2_b64 vcc, exec, s[92:93]
	s_mov_b64 s[16:17], -1
	s_cbranch_vccnz .LBB0_1204
	s_mov_b64 s[16:17], 0
	v_cvt_pk_bf16_f32 v48, v54, v55
	v_cvt_pk_bf16_f32 v49, v52, v53
	v_cvt_pk_bf16_f32 v50, v58, v59
	v_cvt_pk_bf16_f32 v51, v56, v57
.LBB0_1204:
	s_andn2_b64 vcc, exec, s[16:17]
	s_cbranch_vccnz .LBB0_1206
	s_waitcnt vmcnt(0)
	v_mul_f32_e64 v48, v56, v82
	v_mul_f32_e64 v49, v57, v83
	v_mul_f32_e64 v50, v58, v80
	v_mul_f32_e64 v51, v59, v81
	v_fma_f32 v60, v52, v86, -v48
	v_fma_f32 v61, v53, v87, -v49
	v_fma_f32 v48, v54, v84, -v50
	v_fma_f32 v49, v55, v85, -v51
	v_mul_f32_e64 v50, v56, v86
	v_mul_f32_e64 v51, v57, v87
	v_mul_f32_e64 v56, v58, v84
	v_mul_f32_e64 v57, v59, v85
	v_fma_f32 v52, v52, v82, v50
	v_fma_f32 v53, v53, v83, v51
	v_fma_f32 v50, v54, v80, v56
	v_fma_f32 v51, v55, v81, v57
	v_cvt_pk_bf16_f32 v48, v48, v49
	v_cvt_pk_bf16_f32 v49, v60, v61
	s_nop 0
	v_cvt_pk_bf16_f32 v50, v50, v51
	v_cvt_pk_bf16_f32 v51, v52, v53
.LBB0_1206:
	s_and_b64 s[16:17], s[90:91], exec
	v_readlane_b32 s4, v249, 49
	v_readlane_b32 s16, v249, 51
	s_cselect_b32 s17, s4, s16
	v_readlane_b32 s4, v249, 48
	v_readlane_b32 s16, v249, 50
	v_ashrrev_i32_e32 v111, 31, v110
	s_cselect_b32 s16, s4, s16
	s_cselect_b32 s4, 12, 10
	v_lshlrev_b64 v[52:53], s4, v[110:111]
	s_cselect_b32 s37, s34, s30
	s_cselect_b32 s36, s31, s81
	v_lshl_add_u64 v[52:53], s[16:17], 0, v[52:53]
	v_lshl_add_u64 v[52:53], s[36:37], 1, v[52:53]
	v_lshl_add_u64 v[52:53], v[172:173], 1, v[52:53]
	v_mov_b32_e32 v179, v178
	global_store_dwordx4 v[52:53], v[48:51], off
	v_mul_f32_e64 v56, v40, v178
	v_mul_f32_e64 v57, v41, v179
	v_mul_f32_e64 v60, v44, v178
	v_mul_f32_e64 v61, v45, v179
	v_mov_b32_e32 v48, v178
	v_mov_b32_e32 v49, v178
	v_mul_f32_e64 v54, v42, v48
	v_mul_f32_e64 v55, v43, v49
	v_mul_f32_e64 v58, v46, v48
	v_mul_f32_e64 v59, v47, v49
	s_and_b64 vcc, exec, s[2:3]
	s_mov_b64 s[2:3], -1
	s_cbranch_vccnz .LBB0_1208
	s_mov_b64 s[2:3], 0
	v_cvt_pk_bf16_f32 v48, v56, v57
	v_cvt_pk_bf16_f32 v49, v54, v55
	v_cvt_pk_bf16_f32 v50, v60, v61
	v_cvt_pk_bf16_f32 v51, v58, v59
.LBB0_1208:
	s_andn2_b64 vcc, exec, s[2:3]
	s_cbranch_vccnz .LBB0_1210
	s_waitcnt vmcnt(0)
	v_mul_f32_e64 v48, v58, v82
	v_mul_f32_e64 v49, v59, v83
	v_mul_f32_e64 v50, v60, v80
	v_mul_f32_e64 v51, v61, v81
	v_fma_f32 v62, v54, v86, -v48
	v_fma_f32 v63, v55, v87, -v49
	v_fma_f32 v48, v56, v84, -v50
	v_fma_f32 v49, v57, v85, -v51
	v_mul_f32_e64 v50, v58, v86
	v_mul_f32_e64 v51, v59, v87
	v_mul_f32_e64 v58, v60, v84
	v_mul_f32_e64 v59, v61, v85
	v_fma_f32 v54, v54, v82, v50
	v_fma_f32 v55, v55, v83, v51
	v_fma_f32 v50, v56, v80, v58
	v_fma_f32 v51, v57, v81, v59
	v_cvt_pk_bf16_f32 v48, v48, v49
	v_cvt_pk_bf16_f32 v49, v62, v63
	s_nop 0
	v_cvt_pk_bf16_f32 v50, v50, v51
	v_cvt_pk_bf16_f32 v51, v54, v55

; __device__ __forceinline__ f32x4 sigmoid4(const f32x4& x, float s) {
;     f32x4 z = x * (s * -1.4426950408889634f), e;
; #pragma unroll
;     for (int j = 0; j < 4; ++j) e[j] = __builtin_amdgcn_exp2f(z[j]);
;     e = e + 1.0f;
; #pragma unroll
;     for (int j = 0; j < 4; ++j) e[j] = __builtin_amdgcn_rcpf(e[j]);
;     return e;
; }
;     __device__ __forceinline__ void operator()(const f32x4 (&acc)[2][2][4][2], const Unit& u, int wr, int wc, int fr, int fq, const Pre&) const {
;     ...
;                 } else if (kind == KD_A) {
;                     st_bf16x8(abuf + (size_t)row * DM + 128 * (pn - TL_A) + cw, acc[ai][0][m][0] * rs * sigmoid4(acc[ai][1][m][0], rs), acc[ai][0][m][1] * rs * sigmoid4(acc[ai][1][m][1], rs));
.LBB0_1215:
	v_ashrrev_i32_e32 v193, 31, v192
	s_waitcnt vmcnt(0)
	v_lshlrev_b64 v[104:105], 12, v[192:193]
	v_lshl_add_u64 v[104:105], s[12:13], 0, v[104:105]
	v_lshl_add_u64 v[104:105], s[88:89], 1, v[104:105]
	v_mul_f32_e32 v115, 0xbfb8aa3b, v190
	v_lshl_add_u64 v[108:109], v[172:173], 1, v[104:105]
	v_mul_f32_e32 v104, v92, v115
	v_mul_f32_e32 v105, v93, v115
	v_mul_f32_e32 v106, v94, v115
	v_mul_f32_e32 v107, v95, v115
	v_exp_f32_e32 v104, v104
	v_exp_f32_e32 v106, v106
	v_exp_f32_e32 v107, v107
	v_exp_f32_e32 v105, v105
	v_mul_f32_e32 v114, v88, v115
	v_mul_f32_e32 v118, v89, v115
	v_add_f32_e64 v106, v106, 1.0
	v_add_f32_e64 v107, v107, 1.0
	v_add_f32_e64 v104, v104, 1.0
	v_add_f32_e64 v105, v105, 1.0
	v_mul_f32_e32 v116, v90, v115
	v_mul_f32_e32 v115, v91, v115
	v_rcp_f32_e32 v104, v104
	v_rcp_f32_e32 v105, v105
	v_rcp_f32_e32 v106, v106
	v_rcp_f32_e32 v107, v107
	v_exp_f32_e32 v114, v114
	v_exp_f32_e32 v116, v116
	v_exp_f32_e32 v117, v115
	v_exp_f32_e32 v115, v118
	v_mul_f32_e64 v110, v102, v190
	v_mul_f32_e64 v111, v103, v190
	v_mul_f32_e64 v112, v100, v190
	v_mul_f32_e64 v113, v101, v190
	v_mul_f32_e64 v106, v110, v106
	v_mul_f32_e64 v107, v111, v107
	v_mul_f32_e64 v104, v112, v104
	v_mul_f32_e64 v105, v113, v105
	v_add_f32_e64 v110, v116, 1.0
	v_add_f32_e64 v111, v117, 1.0
	v_add_f32_e64 v112, v114, 1.0
	v_add_f32_e64 v113, v115, 1.0
	v_rcp_f32_e32 v110, v110
	v_rcp_f32_e32 v112, v112
	v_rcp_f32_e32 v111, v111
	v_rcp_f32_e32 v113, v113
	v_mul_f32_e64 v114, v98, v190
	v_mul_f32_e64 v115, v99, v190
	v_mul_f32_e64 v116, v96, v190
	v_mul_f32_e64 v117, v97, v190
	v_mul_f32_e64 v110, v114, v110
	v_mul_f32_e64 v111, v115, v111
	v_mul_f32_e64 v112, v116, v112
	v_mul_f32_e64 v113, v117, v113
	v_cvt_pk_bf16_f32 v104, v104, v105
	v_cvt_pk_bf16_f32 v105, v106, v107
	s_nop 0
	v_cvt_pk_bf16_f32 v106, v112, v113
	v_cvt_pk_bf16_f32 v107, v110, v111
	global_store_dwordx4 v[108:109], v[104:107], off

; __device__ __forceinline__ f32x4 sigmoid4(const f32x4& x, float s) {
;     f32x4 z = x * (s * -1.4426950408889634f), e;
; #pragma unroll
;     for (int j = 0; j < 4; ++j) e[j] = __builtin_amdgcn_exp2f(z[j]);
;     e = e + 1.0f;
; #pragma unroll
;     for (int j = 0; j < 4; ++j) e[j] = __builtin_amdgcn_rcpf(e[j]);
;     return e;
; }
;     __device__ __forceinline__ void operator()(const f32x4 (&acc)[2][2][4][2], const Unit& u, int wr, int wc, int fr, int fq, const Pre&) const {
;     ...
;                 } else if (kind == KD_G) {
; #pragma unroll
;                     for (int bj = 0; bj < 2; ++bj)
;                         st_bf16x8(gabuf + (size_t)row * DM + 256 * (pn - TL_G) + 128 * bj + cw, sigmoid4(acc[ai][bj][m][0], rs), sigmoid4(acc[ai][bj][m][1], rs));
.LBB0_1218:
	s_mov_b64 vcc, -1
	s_mov_b64 s[2:3], 0
	s_cmp_lt_i32 s7, 1
	s_mov_b64 s[56:57], 0
	s_cbranch_scc1 .LBB0_1320
	s_cmp_gt_i32 s7, 1
	s_cbranch_scc0 .LBB0_1223
	s_cmp_eq_u32 s7, 2
	s_mov_b64 s[56:57], -1
	s_cbranch_scc0 .LBB0_1222
	v_ashrrev_i32_e32 v189, 31, v188
	v_readlane_b32 s56, v249, 46
	v_lshlrev_b64 v[88:89], 12, v[188:189]
	v_readlane_b32 s57, v249, 47
	s_waitcnt vmcnt(0)
	v_mul_f32_e32 v94, 0xbfb8aa3b, v186
	v_mul_f32_e32 v90, v78, v94
	v_lshl_add_u64 v[88:89], s[56:57], 0, v[88:89]
	v_lshl_add_u64 v[88:89], s[38:39], 1, v[88:89]
	v_mul_f32_e32 v91, v79, v94
	v_lshl_add_u64 v[92:93], v[172:173], 1, v[88:89]
	v_mul_f32_e32 v88, v76, v94
	v_mul_f32_e32 v89, v77, v94
	v_exp_f32_e32 v90, v90
	v_exp_f32_e32 v91, v91
	v_exp_f32_e32 v88, v88
	v_exp_f32_e32 v89, v89
	s_mov_b64 s[56:57], 0
	v_add_f32_e64 v90, v90, 1.0
	v_add_f32_e64 v91, v91, 1.0
	v_add_f32_e64 v88, v88, 1.0
	v_add_f32_e64 v89, v89, 1.0
	v_rcp_f32_e32 v97, v90
	v_rcp_f32_e32 v98, v91
	v_mul_f32_e32 v90, v74, v94
	v_mul_f32_e32 v91, v75, v94
	v_rcp_f32_e32 v95, v88
	v_rcp_f32_e32 v96, v89
	v_mul_f32_e32 v88, v72, v94
	v_mul_f32_e32 v89, v73, v94
	v_exp_f32_e32 v90, v90
	v_exp_f32_e32 v91, v91
	v_exp_f32_e32 v88, v88
	v_exp_f32_e32 v89, v89
	v_add_f32_e64 v90, v90, 1.0
	v_add_f32_e64 v91, v91, 1.0
	s_nop 0
	v_rcp_f32_e32 v91, v91
	v_add_f32_e64 v88, v88, 1.0
	v_add_f32_e64 v89, v89, 1.0
	v_rcp_f32_e32 v101, v90
	v_rcp_f32_e32 v99, v88
	v_rcp_f32_e32 v100, v89
	v_cvt_pk_bf16_f32 v88, v95, v96
	v_cvt_pk_bf16_f32 v89, v97, v98
	v_cvt_pk_bf16_f32 v90, v99, v100
	v_cvt_pk_bf16_f32 v91, v101, v91
	global_store_dwordx4 v[92:93], v[88:91], off
	s_nop 1
	v_mul_f32_e32 v90, v70, v94
	v_mul_f32_e32 v91, v71, v94
	v_mul_f32_e32 v88, v68, v94
	v_mul_f32_e32 v89, v69, v94
	v_exp_f32_e32 v90, v90
	v_exp_f32_e32 v91, v91
	v_exp_f32_e32 v88, v88
	v_exp_f32_e32 v89, v89
	v_add_f32_e64 v90, v90, 1.0
	v_add_f32_e64 v91, v91, 1.0
	s_nop 0
	v_rcp_f32_e32 v97, v90
	v_add_f32_e64 v88, v88, 1.0
	v_add_f32_e64 v89, v89, 1.0
	v_rcp_f32_e32 v98, v91
	v_mul_f32_e32 v90, v66, v94
	v_mul_f32_e32 v91, v67, v94
	v_rcp_f32_e32 v95, v88
	v_rcp_f32_e32 v96, v89
	v_mul_f32_e32 v88, v64, v94
	v_mul_f32_e32 v89, v65, v94
	v_exp_f32_e32 v90, v90
	v_exp_f32_e32 v91, v91
	v_exp_f32_e32 v88, v88
	v_exp_f32_e32 v89, v89
	v_add_f32_e64 v90, v90, 1.0
	v_add_f32_e64 v91, v91, 1.0
	s_nop 0
	v_rcp_f32_e32 v91, v91
	v_add_f32_e64 v88, v88, 1.0
	v_add_f32_e64 v89, v89, 1.0
	v_rcp_f32_e32 v100, v90
	v_rcp_f32_e32 v94, v88
	v_rcp_f32_e32 v99, v89
	v_cvt_pk_bf16_f32 v88, v95, v96
	v_cvt_pk_bf16_f32 v89, v97, v98
	v_cvt_pk_bf16_f32 v90, v94, v99
	v_cvt_pk_bf16_f32 v91, v100, v91
	global_store_dwordx4 v[92:93], v[88:91], off offset:256

;     __device__ __forceinline__ void operator()(const f32x4 (&acc)[2][2][4][2], const Unit& u, int wr, int wc, int fr, int fq, const Pre&) const {
;     ...
;                 } else if (kind == KD_P) {
;                     const float r2 = rs * rs;
;                     st_bf16x8(pbuf + (size_t)row * DM + 128 * (pn - TL_P) + cw, acc[ai][0][m][0] * acc[ai][1][m][0] * r2, acc[ai][0][m][1] * acc[ai][1][m][1] * r2);
.LBB0_1223:
	s_and_b64 vcc, exec, vcc
	s_cbranch_vccz .LBB0_1225
	v_ashrrev_i32_e32 v189, 31, v188
	v_readlane_b32 vcc_lo, v249, 44
	v_lshlrev_b64 v[90:91], 12, v[188:189]
	v_readlane_b32 vcc_hi, v249, 45
	s_waitcnt vmcnt(0)
	v_mul_f32_e32 v88, v186, v186
	v_mul_f32_e64 v94, v76, v68
	v_mul_f32_e64 v95, v77, v69
	v_lshl_add_u64 v[90:91], vcc, 0, v[90:91]
	v_lshl_add_u64 v[90:91], s[42:43], 1, v[90:91]
	v_lshl_add_u64 v[92:93], v[172:173], 1, v[90:91]
	v_mul_f32_e64 v90, v78, v70
	v_mul_f32_e64 v91, v79, v71
	v_mul_f32_e64 v96, v74, v66
	v_mul_f32_e64 v97, v75, v67
	v_mul_f32_e64 v90, v90, v88
	v_mul_f32_e64 v91, v91, v88
	v_mul_f32_e64 v98, v72, v64
	v_mul_f32_e64 v99, v73, v65
	v_mul_f32_e64 v94, v94, v88
	v_mul_f32_e64 v95, v95, v88
	v_mul_f32_e64 v96, v96, v88
	v_mul_f32_e64 v97, v97, v88
	v_mul_f32_e64 v98, v98, v88
	v_mul_f32_e64 v99, v99, v88
	v_cvt_pk_bf16_f32 v88, v94, v95
	v_cvt_pk_bf16_f32 v89, v90, v91
	s_nop 0
	v_cvt_pk_bf16_f32 v90, v98, v99
	v_cvt_pk_bf16_f32 v91, v96, v97
	global_store_dwordx4 v[92:93], v[88:91], off

;     __device__ __forceinline__ void operator()(const f32x4 (&acc)[2][2][4][2], const Unit& u, int wr, int wc, int fr, int fq, const Pre&) const {
;     ...
;                 } else {
;                     const f32x4 x1 = acc[ai][0][m][0] * rs, x2 = acc[ai][0][m][1] * rs;
;                     if (wc < 2) {
;                         if (roti) st_bf16x8(kib + (size_t)row * 64 + cw, x1 * cs[q] - x2 * sn[q], x2 * cs[q] + x1 * sn[q]);
;                         else st_bf16x8(kib + (size_t)row * 64 + cw, x1, x2);
;                     } else if (wc == 2 && fq < 2) {
;                         *(f32x4*)(wib + (size_t)row * 16 + 8 * fq) = x1 * 0.03125f; *(f32x4*)(wib + (size_t)row * 16 + 8 * fq + 4) = x2 * 0.03125f;
;                     }
.LBB0_1227:
	s_andn2_b64 vcc, exec, s[64:65]
	s_mov_b64 s[2:3], -1
	s_cbranch_vccnz .LBB0_1255
	s_andn2_b64 vcc, exec, s[58:59]
	s_cbranch_vccnz .LBB0_1252
	v_readlane_b32 s56, v249, 63
	s_waitcnt vmcnt(0)
	v_mov_b32_e32 v187, v186
	v_readlane_b32 s57, v248, 0
	s_andn2_b64 vcc, exec, s[56:57]
	v_mul_f32_e64 v90, v76, v186
	v_mul_f32_e64 v91, v77, v187
	v_mul_f32_e64 v88, v72, v186
	v_mul_f32_e64 v89, v73, v187
	s_cbranch_vccnz .LBB0_1241
	v_readlane_b32 s2, v248, 24
	v_mov_b32_e32 v92, v186
	v_mov_b32_e32 v93, v186
	v_readlane_b32 s3, v248, 25
	v_mul_f32_e64 v94, v78, v92
	v_mul_f32_e64 v95, v79, v93
	v_mul_f32_e64 v92, v74, v92
	v_mul_f32_e64 v93, v75, v93
	s_andn2_b64 vcc, exec, s[2:3]
	s_mov_b64 s[2:3], -1
	s_cbranch_vccnz .LBB0_1234
	s_mov_b64 s[2:3], exec
	v_readlane_b32 s56, v248, 7
	v_readlane_b32 s57, v248, 8
	s_and_b64 s[56:57], s[2:3], s[56:57]
	s_mov_b64 exec, s[56:57]
	s_cbranch_execz .LBB0_1233
	v_ashrrev_i32_e32 v189, 31, v188
	v_readlane_b32 s56, v249, 56
	v_lshlrev_b64 v[100:101], 6, v[188:189]
	v_readlane_b32 s57, v249, 57
	s_mov_b32 s4, 0x3d000000
	v_mul_f32_e64 v98, v94, s4
	v_mul_f32_e64 v99, v95, s4
	v_lshl_add_u64 v[100:101], s[56:57], 0, v[100:101]
	v_mul_f32_e64 v96, v90, s4
	v_mul_f32_e64 v97, v91, s4
	v_lshl_add_u64 v[100:101], v[174:175], 2, v[100:101]
	global_store_dwordx4 v[100:101], v[96:99], off
	s_nop 1
	v_mul_f32_e64 v98, v92, s4
	v_mul_f32_e64 v99, v93, s4
	v_mul_f32_e64 v96, v88, s4
	v_mul_f32_e64 v97, v89, s4
	global_store_dwordx4 v[100:101], v[96:99], off offset:16

;     __device__ __forceinline__ void operator()(const f32x4 (&acc)[2][2][4][2], const Unit& u, int wr, int wc, int fr, int fq, const Pre&) const {
;     ...
;                     const f32x4 x1 = acc[ai][0][m][0] * rs, x2 = acc[ai][0][m][1] * rs;
;                     if (wc < 2) {
;                         if (roti) st_bf16x8(kib + (size_t)row * 64 + cw, x1 * cs[q] - x2 * sn[q], x2 * cs[q] + x1 * sn[q]);
;                         else st_bf16x8(kib + (size_t)row * 64 + cw, x1, x2);
.LBB0_1237:
	s_andn2_saveexec_b64 s[2:3], s[2:3]
	s_cbranch_execz .LBB0_1239
	v_mul_f32_e64 v98, v92, v82
	v_mul_f32_e64 v99, v93, v83
	v_mul_f32_e64 v92, v92, v86
	v_mul_f32_e64 v93, v93, v87
	v_mul_f32_e64 v102, v88, v84
	v_mul_f32_e64 v103, v89, v85
	v_mul_f32_e64 v100, v88, v80
	v_mul_f32_e64 v101, v89, v81
	v_fma_f32 v98, v94, v86, -v98
	v_fma_f32 v99, v95, v87, -v99
	v_fma_f32 v104, v94, v82, v92
	v_fma_f32 v105, v95, v83, v93
	v_fma_f32 v94, v90, v80, v102
	v_fma_f32 v95, v91, v81, v103
	v_fma_f32 v100, v90, v84, -v100
	v_fma_f32 v101, v91, v85, -v101
	s_nop 0
	v_cvt_pk_bf16_f32 v92, v100, v101
	v_cvt_pk_bf16_f32 v93, v98, v99
	v_cvt_pk_bf16_f32 v94, v94, v95
	v_cvt_pk_bf16_f32 v95, v104, v105
	global_store_dwordx4 v[96:97], v[92:95], off

;     __device__ __forceinline__ void operator()(const f32x4 (&acc)[2][2][4][2], const Unit& u, int wr, int wc, int fr, int fq, const Pre&) const {
;     ...
;                 } else if (kind == KD_QI) {
; #pragma unroll
;                     for (int bj = 0; bj < 2; ++bj) {
;                         const f32x4 x1 = acc[ai][bj][m][0] * rs, x2 = acc[ai][bj][m][1] * rs;
;                         bf16_t* o = qib + (size_t)row * 1024 + 256 * (pn - TL_QI) + 128 * bj + cw;
;                         if (roti) st_bf16x8(o, x1 * cs[q] - x2 * sn[q], x2 * cs[q] + x1 * sn[q]); else st_bf16x8(o, x1, x2);
;                     }
.LBB0_1241:
	s_andn2_b64 vcc, exec, s[2:3]
	s_cbranch_vccnz .LBB0_1251
	v_mov_b32_e32 v92, v186
	v_mov_b32_e32 v93, v186
	v_readlane_b32 vcc_lo, v248, 9
	v_mul_f32_e64 v100, v78, v92
	v_mul_f32_e64 v101, v79, v93
	v_mul_f32_e64 v98, v74, v92
	v_mul_f32_e64 v99, v75, v93
	v_readlane_b32 vcc_hi, v248, 10
	s_and_saveexec_b64 s[2:3], vcc
	s_xor_b64 s[2:3], exec, s[2:3]
	s_cbranch_execz .LBB0_1244
	v_cvt_pk_bf16_f32 v94, v90, v91
	v_cvt_pk_bf16_f32 v95, v100, v101
	v_cvt_pk_bf16_f32 v96, v88, v89
	v_cvt_pk_bf16_f32 v97, v98, v99
.LBB0_1244:
	s_andn2_saveexec_b64 s[2:3], s[2:3]
	s_cbranch_execz .LBB0_1246
	v_mul_f32_e64 v94, v88, v80
	v_mul_f32_e64 v95, v89, v81
	v_mul_f32_e64 v92, v98, v82
	v_mul_f32_e64 v93, v99, v83
	v_fma_f32 v94, v90, v84, -v94
	v_fma_f32 v95, v91, v85, -v95
	v_mul_f32_e64 v96, v98, v86
	v_mul_f32_e64 v97, v99, v87
	v_mul_f32_e64 v88, v88, v84
	v_mul_f32_e64 v89, v89, v85
	v_fma_f32 v92, v100, v86, -v92
	v_fma_f32 v93, v101, v87, -v93
	v_fma_f32 v98, v100, v82, v96
	v_fma_f32 v99, v101, v83, v97
	v_fma_f32 v88, v90, v80, v88
	v_fma_f32 v89, v91, v81, v89
	v_cvt_pk_bf16_f32 v94, v94, v95
	v_cvt_pk_bf16_f32 v95, v92, v93
	s_nop 0
	v_cvt_pk_bf16_f32 v96, v88, v89
	v_cvt_pk_bf16_f32 v97, v98, v99
.LBB0_1246:
	s_or_b64 exec, exec, s[2:3]
	v_ashrrev_i32_e32 v189, 31, v188
	v_readlane_b32 s2, v248, 18
	v_lshlrev_b64 v[88:89], 11, v[188:189]
	v_readlane_b32 s3, v248, 19
	v_mul_f32_e64 v92, v64, v186
	v_mul_f32_e64 v93, v65, v187
	s_nop 0
	v_lshl_add_u64 v[88:89], s[2:3], 0, v[88:89]
	v_lshl_add_u64 v[88:89], s[28:29], 1, v[88:89]
	v_lshl_add_u64 v[98:99], v[172:173], 1, v[88:89]
	v_mov_b32_e32 v88, v186
	v_mov_b32_e32 v89, v186
	global_store_dwordx4 v[98:99], v[94:97], off
	v_mul_f32_e64 v100, v70, v88
	v_mul_f32_e64 v101, v71, v89
	v_mul_f32_e64 v102, v66, v88
	v_mul_f32_e64 v103, v67, v89
	v_mul_f32_e64 v94, v68, v186
	v_mul_f32_e64 v95, v69, v187
	s_and_saveexec_b64 s[2:3], vcc
	s_xor_b64 s[2:3], exec, s[2:3]
	s_cbranch_execz .LBB0_1248
	v_cvt_pk_bf16_f32 v88, v94, v95
	v_cvt_pk_bf16_f32 v89, v100, v101
	v_cvt_pk_bf16_f32 v90, v92, v93
	v_cvt_pk_bf16_f32 v91, v102, v103
.LBB0_1248:
	s_andn2_saveexec_b64 s[2:3], s[2:3]
	s_cbranch_execz .LBB0_1250
	v_mul_f32_e64 v88, v102, v82
	v_mul_f32_e64 v89, v103, v83
	v_mul_f32_e64 v90, v92, v80
	v_mul_f32_e64 v91, v93, v81
	v_fma_f32 v96, v100, v86, -v88
	v_fma_f32 v97, v101, v87, -v89
	v_fma_f32 v88, v94, v84, -v90
	v_fma_f32 v89, v95, v85, -v91
	v_mul_f32_e64 v90, v102, v86
	v_mul_f32_e64 v91, v103, v87
	v_mul_f32_e64 v92, v92, v84
	v_mul_f32_e64 v93, v93, v85
	v_fma_f32 v100, v100, v82, v90
	v_fma_f32 v101, v101, v83, v91
	v_fma_f32 v90, v94, v80, v92
	v_fma_f32 v91, v95, v81, v93
	v_cvt_pk_bf16_f32 v88, v88, v89
	v_cvt_pk_bf16_f32 v89, v96, v97
	s_nop 0
	v_cvt_pk_bf16_f32 v90, v90, v91
	v_cvt_pk_bf16_f32 v91, v100, v101

;     __device__ __forceinline__ void operator()(const f32x4 (&acc)[2][2][4][2], const Unit& u, int wr, int wc, int fr, int fq, const Pre&) const {
;     ...
;                 } else if (kind == KD_V) {
; #pragma unroll
;                     for (int bj = 0; bj < 2; ++bj) st_bf16x8(vb + (size_t)row * 512 + 256 * (pn - TL_V) + 128 * bj + cw, acc[ai][bj][m][0] * rs, acc[ai][bj][m][1] * rs);
.LBB0_1252:
	s_andn2_b64 vcc, exec, s[2:3]
	s_cbranch_vccnz .LBB0_1254
	v_ashrrev_i32_e32 v189, 31, v188
	v_readlane_b32 s2, v249, 52
	v_lshlrev_b64 v[88:89], 10, v[188:189]
	v_readlane_b32 s3, v249, 53
	s_waitcnt vmcnt(0)
	v_mul_f32_e64 v90, v78, v186
	v_mul_f32_e64 v91, v79, v186
	v_mul_f32_e64 v94, v74, v186
	v_mul_f32_e64 v95, v75, v186
	v_lshl_add_u64 v[88:89], s[2:3], 0, v[88:89]
	v_lshl_add_u64 v[88:89], s[94:95], 1, v[88:89]
	v_lshl_add_u64 v[92:93], v[172:173], 1, v[88:89]
	v_mul_f32_e64 v88, v76, v186
	v_mul_f32_e64 v89, v77, v186
	v_mul_f32_e64 v96, v72, v186
	v_mul_f32_e64 v97, v73, v186
	v_cvt_pk_bf16_f32 v88, v88, v89
	v_cvt_pk_bf16_f32 v89, v90, v91
	s_nop 0
	v_cvt_pk_bf16_f32 v90, v96, v97
	v_cvt_pk_bf16_f32 v91, v94, v95
	global_store_dwordx4 v[92:93], v[88:91], off
	v_mul_f32_e64 v94, v66, v186
	v_mul_f32_e64 v95, v67, v186
	v_mul_f32_e64 v96, v64, v186
	v_mul_f32_e64 v97, v65, v186
	v_mul_f32_e64 v90, v70, v186
	v_mul_f32_e64 v91, v71, v186
	v_mul_f32_e64 v88, v68, v186
	v_mul_f32_e64 v89, v69, v186
	s_nop 0
	v_cvt_pk_bf16_f32 v88, v88, v89
	v_cvt_pk_bf16_f32 v89, v90, v91
	v_cvt_pk_bf16_f32 v90, v96, v97
	v_cvt_pk_bf16_f32 v91, v94, v95
	global_store_dwordx4 v[92:93], v[88:91], off offset:256

;     __device__ __forceinline__ void operator()(const f32x4 (&acc)[2][2][4][2], const Unit& u, int wr, int wc, int fr, int fq, const Pre&) const {
;     ...
;                 } else if (kind == KD_Q || kind == KD_K) {
;                     bf16_t* o = (kind == KD_Q) ? qb + (size_t)row * DM + 256 * (pn - TL_Q) + cw : kb + (size_t)row * 512 + 256 * (pn - TL_K) + cw;
; #pragma unroll
;                     for (int bj = 0; bj < 2; ++bj) {
;                         const f32x4 x1 = acc[ai][bj][m][0] * rs, x2 = acc[ai][bj][m][1] * rs;
;                         if (rotqk) st_bf16x8(o + 128 * bj, x1 * cs[q] - x2 * sn[q], x2 * cs[q] + x1 * sn[q]);
;                         else st_bf16x8(o + 128 * bj, x1, x2);
;                     }
.LBB0_1255:
	s_andn2_b64 vcc, exec, s[2:3]
	s_cbranch_vccnz .LBB0_1265
	v_cndmask_b32_e64 v88, 0, 1, s[92:93]
	s_waitcnt vmcnt(0)
	v_mul_f32_e64 v92, v78, v186
	v_mul_f32_e64 v93, v79, v186
	v_mul_f32_e64 v94, v76, v186
	v_mul_f32_e64 v95, v77, v186
	v_mul_f32_e64 v96, v74, v186
	v_mul_f32_e64 v97, v75, v186
	v_mul_f32_e64 v98, v72, v186
	v_mul_f32_e64 v99, v73, v186
	v_cmp_ne_u32_e64 s[2:3], 1, v88
	s_andn2_b64 vcc, exec, s[92:93]
	s_mov_b64 s[56:57], -1
	s_cbranch_vccnz .LBB0_1258
	s_mov_b64 s[56:57], 0
	v_cvt_pk_bf16_f32 v88, v94, v95
	v_cvt_pk_bf16_f32 v89, v92, v93
	v_cvt_pk_bf16_f32 v90, v98, v99
	v_cvt_pk_bf16_f32 v91, v96, v97
.LBB0_1258:
	s_andn2_b64 vcc, exec, s[56:57]
	s_cbranch_vccnz .LBB0_1260
	v_mul_f32_e64 v88, v96, v82
	v_mul_f32_e64 v89, v97, v83
	v_mul_f32_e64 v90, v98, v80
	v_mul_f32_e64 v91, v99, v81
	v_fma_f32 v100, v92, v86, -v88
	v_fma_f32 v101, v93, v87, -v89
	v_fma_f32 v88, v94, v84, -v90
	v_fma_f32 v89, v95, v85, -v91
	v_mul_f32_e64 v90, v96, v86
	v_mul_f32_e64 v91, v97, v87
	v_mul_f32_e64 v96, v98, v84
	v_mul_f32_e64 v97, v99, v85
	v_fma_f32 v92, v92, v82, v90
	v_fma_f32 v93, v93, v83, v91
	v_fma_f32 v90, v94, v80, v96
	v_fma_f32 v91, v95, v81, v97
	v_cvt_pk_bf16_f32 v88, v88, v89
	v_cvt_pk_bf16_f32 v89, v100, v101
	s_nop 0
	v_cvt_pk_bf16_f32 v90, v90, v91
	v_cvt_pk_bf16_f32 v91, v92, v93
.LBB0_1260:
	s_and_b64 s[56:57], s[90:91], exec
	v_readlane_b32 s4, v249, 49
	v_readlane_b32 s56, v249, 51
	s_cselect_b32 s57, s4, s56
	v_readlane_b32 s4, v249, 48
	v_readlane_b32 s56, v249, 50
	v_ashrrev_i32_e32 v189, 31, v188
	s_cselect_b32 s56, s4, s56
	s_cselect_b32 s4, 12, 10
	v_lshlrev_b64 v[92:93], s4, v[188:189]
	s_cselect_b32 vcc_hi, s34, s30
	s_cselect_b32 vcc_lo, s31, s81
	v_lshl_add_u64 v[92:93], s[56:57], 0, v[92:93]
	v_lshl_add_u64 v[92:93], vcc, 1, v[92:93]
	v_lshl_add_u64 v[92:93], v[172:173], 1, v[92:93]
	v_mov_b32_e32 v187, v186
	global_store_dwordx4 v[92:93], v[88:91], off
	v_mul_f32_e64 v96, v68, v186
	v_mul_f32_e64 v97, v69, v187
	v_mul_f32_e64 v100, v64, v186
	v_mul_f32_e64 v101, v65, v187
	v_mov_b32_e32 v88, v186
	v_mov_b32_e32 v89, v186
	v_mul_f32_e64 v94, v70, v88
	v_mul_f32_e64 v95, v71, v89
	v_mul_f32_e64 v98, v66, v88
	v_mul_f32_e64 v99, v67, v89
	s_and_b64 vcc, exec, s[2:3]
	s_mov_b64 s[2:3], -1
	s_cbranch_vccnz .LBB0_1262
	s_mov_b64 s[2:3], 0
	v_cvt_pk_bf16_f32 v88, v96, v97
	v_cvt_pk_bf16_f32 v89, v94, v95
	v_cvt_pk_bf16_f32 v90, v100, v101
	v_cvt_pk_bf16_f32 v91, v98, v99
.LBB0_1262:
	s_andn2_b64 vcc, exec, s[2:3]
	s_cbranch_vccnz .LBB0_1264
	v_mul_f32_e64 v88, v98, v82
	v_mul_f32_e64 v89, v99, v83
	v_mul_f32_e64 v90, v100, v80
	v_mul_f32_e64 v91, v101, v81
	v_fma_f32 v102, v94, v86, -v88
	v_fma_f32 v103, v95, v87, -v89
	v_fma_f32 v88, v96, v84, -v90
	v_fma_f32 v89, v97, v85, -v91
	v_mul_f32_e64 v86, v98, v86
	v_mul_f32_e64 v87, v99, v87
	v_mul_f32_e64 v84, v100, v84
	v_mul_f32_e64 v85, v101, v85
	v_fma_f32 v82, v94, v82, v86
	v_fma_f32 v83, v95, v83, v87
	v_fma_f32 v80, v96, v80, v84
	v_fma_f32 v81, v97, v81, v85
	v_cvt_pk_bf16_f32 v88, v88, v89
	v_cvt_pk_bf16_f32 v89, v102, v103
	s_nop 0
	v_cvt_pk_bf16_f32 v90, v80, v81
	v_cvt_pk_bf16_f32 v91, v82, v83

; __device__ __forceinline__ f32x4 sigmoid4(const f32x4& x, float s) {
;     f32x4 z = x * (s * -1.4426950408889634f), e;
; #pragma unroll
;     for (int j = 0; j < 4; ++j) e[j] = __builtin_amdgcn_exp2f(z[j]);
;     e = e + 1.0f;
; #pragma unroll
;     for (int j = 0; j < 4; ++j) e[j] = __builtin_amdgcn_rcpf(e[j]);
;     return e;
; }
;     __device__ __forceinline__ void operator()(const f32x4 (&acc)[2][2][4][2], const Unit& u, int wr, int wc, int fr, int fq, const Pre&) const {
;     ...
;                 } else if (kind == KD_A) {
;                     st_bf16x8(abuf + (size_t)row * DM + 128 * (pn - TL_A) + cw, acc[ai][0][m][0] * rs * sigmoid4(acc[ai][1][m][0], rs), acc[ai][0][m][1] * rs * sigmoid4(acc[ai][1][m][1], rs));
.LBB0_1269:
	v_ashrrev_i32_e32 v111, 31, v110
	v_lshlrev_b64 v[48:49], 12, v[110:111]
	v_lshl_add_u64 v[48:49], s[12:13], 0, v[48:49]
	v_lshl_add_u64 v[48:49], s[88:89], 1, v[48:49]
	v_mul_f32_e32 v59, 0xbfb8aa3b, v178
	v_lshl_add_u64 v[52:53], v[172:173], 1, v[48:49]
	v_mul_f32_e32 v48, v40, v59
	v_mul_f32_e32 v49, v41, v59
	v_mul_f32_e32 v50, v42, v59
	v_mul_f32_e32 v51, v43, v59
	v_exp_f32_e32 v48, v48
	v_exp_f32_e32 v50, v50
	v_exp_f32_e32 v51, v51
	v_exp_f32_e32 v49, v49
	v_mul_f32_e32 v58, v44, v59
	v_mul_f32_e32 v62, v45, v59
	v_add_f32_e64 v50, v50, 1.0
	v_add_f32_e64 v51, v51, 1.0
	v_add_f32_e64 v48, v48, 1.0
	v_add_f32_e64 v49, v49, 1.0
	v_mul_f32_e32 v60, v46, v59
	v_mul_f32_e32 v59, v47, v59
	v_rcp_f32_e32 v48, v48
	v_rcp_f32_e32 v49, v49
	v_rcp_f32_e32 v50, v50
	v_rcp_f32_e32 v51, v51
	v_exp_f32_e32 v58, v58
	v_exp_f32_e32 v60, v60
	v_exp_f32_e32 v61, v59
	v_exp_f32_e32 v59, v62
	v_mul_f32_e64 v54, v38, v178
	v_mul_f32_e64 v55, v39, v178
	v_mul_f32_e64 v56, v36, v178
	v_mul_f32_e64 v57, v37, v178
	v_mul_f32_e64 v50, v54, v50
	v_mul_f32_e64 v51, v55, v51
	v_mul_f32_e64 v48, v56, v48
	v_mul_f32_e64 v49, v57, v49
	v_add_f32_e64 v54, v60, 1.0
	v_add_f32_e64 v55, v61, 1.0
	v_add_f32_e64 v56, v58, 1.0
	v_add_f32_e64 v57, v59, 1.0
	v_rcp_f32_e32 v54, v54
	v_rcp_f32_e32 v56, v56
	v_rcp_f32_e32 v55, v55
	v_rcp_f32_e32 v57, v57
	v_mul_f32_e64 v58, v34, v178
	v_mul_f32_e64 v59, v35, v178
	v_mul_f32_e64 v60, v32, v178
	v_mul_f32_e64 v61, v33, v178
	v_mul_f32_e64 v54, v58, v54
	v_mul_f32_e64 v55, v59, v55
	v_mul_f32_e64 v56, v60, v56
	v_mul_f32_e64 v57, v61, v57
	v_cvt_pk_bf16_f32 v48, v48, v49
	v_cvt_pk_bf16_f32 v49, v50, v51
	s_nop 0
	v_cvt_pk_bf16_f32 v50, v56, v57
	v_cvt_pk_bf16_f32 v51, v54, v55
	global_store_dwordx4 v[52:53], v[48:51], off

; __device__ __forceinline__ f32x4 sigmoid4(const f32x4& x, float s) {
;     f32x4 z = x * (s * -1.4426950408889634f), e;
; #pragma unroll
;     for (int j = 0; j < 4; ++j) e[j] = __builtin_amdgcn_exp2f(z[j]);
;     e = e + 1.0f;
; #pragma unroll
;     for (int j = 0; j < 4; ++j) e[j] = __builtin_amdgcn_rcpf(e[j]);
;     return e;
; }
;     __device__ __forceinline__ void operator()(const f32x4 (&acc)[2][2][4][2], const Unit& u, int wr, int wc, int fr, int fq, const Pre&) const {
;     ...
;                 } else if (kind == KD_G) {
; #pragma unroll
;                     for (int bj = 0; bj < 2; ++bj)
;                         st_bf16x8(gabuf + (size_t)row * DM + 256 * (pn - TL_G) + 128 * bj + cw, sigmoid4(acc[ai][bj][m][0], rs), sigmoid4(acc[ai][bj][m][1], rs));
.LBB0_1272:
	s_mov_b64 s[36:37], -1
	s_mov_b64 s[2:3], 0
	s_cmp_lt_i32 s7, 1
	s_mov_b64 s[16:17], 0
	s_cbranch_scc1 .LBB0_1325
	s_cmp_gt_i32 s7, 1
	s_cbranch_scc0 .LBB0_1277
	s_cmp_eq_u32 s7, 2
	s_mov_b64 s[16:17], -1
	s_cbranch_scc0 .LBB0_1276
	v_ashrrev_i32_e32 v109, 31, v108
	v_readlane_b32 s16, v249, 46
	v_lshlrev_b64 v[32:33], 12, v[108:109]
	v_readlane_b32 s17, v249, 47
	v_mul_f32_e32 v38, 0xbfb8aa3b, v176
	v_mul_f32_e32 v34, v22, v38
	v_lshl_add_u64 v[32:33], s[16:17], 0, v[32:33]
	v_lshl_add_u64 v[32:33], s[38:39], 1, v[32:33]
	v_mul_f32_e32 v35, v23, v38
	v_lshl_add_u64 v[36:37], v[172:173], 1, v[32:33]
	v_mul_f32_e32 v32, v20, v38
	v_mul_f32_e32 v33, v21, v38
	v_exp_f32_e32 v34, v34
	v_exp_f32_e32 v35, v35
	v_exp_f32_e32 v32, v32
	v_exp_f32_e32 v33, v33
	s_mov_b64 s[16:17], 0
	v_add_f32_e64 v34, v34, 1.0
	v_add_f32_e64 v35, v35, 1.0
	v_add_f32_e64 v32, v32, 1.0
	v_add_f32_e64 v33, v33, 1.0
	v_rcp_f32_e32 v41, v34
	v_rcp_f32_e32 v42, v35
	v_mul_f32_e32 v34, v18, v38
	v_mul_f32_e32 v35, v19, v38
	v_rcp_f32_e32 v39, v32
	v_rcp_f32_e32 v40, v33
	v_mul_f32_e32 v32, v16, v38
	v_mul_f32_e32 v33, v17, v38
	v_exp_f32_e32 v34, v34
	v_exp_f32_e32 v35, v35
	v_exp_f32_e32 v32, v32
	v_exp_f32_e32 v33, v33
	v_add_f32_e64 v34, v34, 1.0
	v_add_f32_e64 v35, v35, 1.0
	s_nop 0
	v_rcp_f32_e32 v35, v35
	v_add_f32_e64 v32, v32, 1.0
	v_add_f32_e64 v33, v33, 1.0
	v_rcp_f32_e32 v45, v34
	v_rcp_f32_e32 v43, v32
	v_rcp_f32_e32 v44, v33
	v_cvt_pk_bf16_f32 v32, v39, v40
	v_cvt_pk_bf16_f32 v33, v41, v42
	v_cvt_pk_bf16_f32 v34, v43, v44
	v_cvt_pk_bf16_f32 v35, v45, v35
	global_store_dwordx4 v[36:37], v[32:35], off
	s_nop 1
	v_mul_f32_e32 v34, v26, v38
	v_mul_f32_e32 v35, v27, v38
	v_mul_f32_e32 v32, v24, v38
	v_mul_f32_e32 v33, v25, v38
	v_exp_f32_e32 v34, v34
	v_exp_f32_e32 v35, v35
	v_exp_f32_e32 v32, v32
	v_exp_f32_e32 v33, v33
	v_add_f32_e64 v34, v34, 1.0
	v_add_f32_e64 v35, v35, 1.0
	s_nop 0
	v_rcp_f32_e32 v41, v34
	v_add_f32_e64 v32, v32, 1.0
	v_add_f32_e64 v33, v33, 1.0
	v_rcp_f32_e32 v42, v35
	v_mul_f32_e32 v34, v30, v38
	v_mul_f32_e32 v35, v31, v38
	v_rcp_f32_e32 v39, v32
	v_rcp_f32_e32 v40, v33
	v_mul_f32_e32 v32, v28, v38
	v_mul_f32_e32 v33, v29, v38
	v_exp_f32_e32 v34, v34
	v_exp_f32_e32 v35, v35
	v_exp_f32_e32 v32, v32
	v_exp_f32_e32 v33, v33
	v_add_f32_e64 v34, v34, 1.0
	v_add_f32_e64 v35, v35, 1.0
	s_nop 0
	v_rcp_f32_e32 v35, v35
	v_add_f32_e64 v32, v32, 1.0
	v_add_f32_e64 v33, v33, 1.0
	v_rcp_f32_e32 v44, v34
	v_rcp_f32_e32 v38, v32
	v_rcp_f32_e32 v43, v33
	v_cvt_pk_bf16_f32 v32, v39, v40
	v_cvt_pk_bf16_f32 v33, v41, v42
	v_cvt_pk_bf16_f32 v34, v38, v43
	v_cvt_pk_bf16_f32 v35, v44, v35
	global_store_dwordx4 v[36:37], v[32:35], off offset:256

;     __device__ __forceinline__ void operator()(const f32x4 (&acc)[2][2][4][2], const Unit& u, int wr, int wc, int fr, int fq, const Pre&) const {
;     ...
;                 } else if (kind == KD_P) {
;                     const float r2 = rs * rs;
;                     st_bf16x8(pbuf + (size_t)row * DM + 128 * (pn - TL_P) + cw, acc[ai][0][m][0] * acc[ai][1][m][0] * r2, acc[ai][0][m][1] * acc[ai][1][m][1] * r2);
.LBB0_1277:
	s_and_b64 vcc, exec, s[36:37]
	s_cbranch_vccz .LBB0_1279
	v_ashrrev_i32_e32 v109, 31, v108
	v_readlane_b32 s36, v249, 44
	v_lshlrev_b64 v[34:35], 12, v[108:109]
	v_readlane_b32 s37, v249, 45
	v_mul_f32_e32 v32, v176, v176
	v_mul_f32_e64 v38, v20, v24
	v_mul_f32_e64 v39, v21, v25
	v_lshl_add_u64 v[34:35], s[36:37], 0, v[34:35]
	v_lshl_add_u64 v[34:35], s[42:43], 1, v[34:35]
	v_lshl_add_u64 v[36:37], v[172:173], 1, v[34:35]
	v_mul_f32_e64 v34, v22, v26
	v_mul_f32_e64 v35, v23, v27
	v_mul_f32_e64 v40, v18, v30
	v_mul_f32_e64 v41, v19, v31
	v_mul_f32_e64 v34, v34, v32
	v_mul_f32_e64 v35, v35, v32
	v_mul_f32_e64 v42, v16, v28
	v_mul_f32_e64 v43, v17, v29
	v_mul_f32_e64 v38, v38, v32
	v_mul_f32_e64 v39, v39, v32
	v_mul_f32_e64 v40, v40, v32
	v_mul_f32_e64 v41, v41, v32
	v_mul_f32_e64 v42, v42, v32
	v_mul_f32_e64 v43, v43, v32
	v_cvt_pk_bf16_f32 v32, v38, v39
	v_cvt_pk_bf16_f32 v33, v34, v35
	s_nop 0
	v_cvt_pk_bf16_f32 v34, v42, v43
	v_cvt_pk_bf16_f32 v35, v40, v41
	global_store_dwordx4 v[36:37], v[32:35], off

;     __device__ __forceinline__ void operator()(const f32x4 (&acc)[2][2][4][2], const Unit& u, int wr, int wc, int fr, int fq, const Pre&) const {
;     ...
;                 } else {
;                     const f32x4 x1 = acc[ai][0][m][0] * rs, x2 = acc[ai][0][m][1] * rs;
;                     if (wc < 2) {
;                         if (roti) st_bf16x8(kib + (size_t)row * 64 + cw, x1 * cs[q] - x2 * sn[q], x2 * cs[q] + x1 * sn[q]);
;                         else st_bf16x8(kib + (size_t)row * 64 + cw, x1, x2);
;                     } else if (wc == 2 && fq < 2) {
;                         *(f32x4*)(wib + (size_t)row * 16 + 8 * fq) = x1 * 0.03125f; *(f32x4*)(wib + (size_t)row * 16 + 8 * fq + 4) = x2 * 0.03125f;
;                     }
.LBB0_1281:
	s_andn2_b64 vcc, exec, s[64:65]
	s_mov_b64 s[2:3], -1
	s_cbranch_vccnz .LBB0_1309
	s_andn2_b64 vcc, exec, s[58:59]
	s_cbranch_vccnz .LBB0_1306
	v_readlane_b32 s16, v249, 63
	v_mov_b32_e32 v177, v176
	v_readlane_b32 s17, v248, 0
	s_andn2_b64 vcc, exec, s[16:17]
	v_mul_f32_e64 v34, v20, v176
	v_mul_f32_e64 v35, v21, v177
	v_mul_f32_e64 v32, v16, v176
	v_mul_f32_e64 v33, v17, v177
	s_cbranch_vccnz .LBB0_1295
	v_readlane_b32 s2, v248, 24
	v_mov_b32_e32 v36, v176
	v_mov_b32_e32 v37, v176
	v_readlane_b32 s3, v248, 25
	v_mul_f32_e64 v38, v22, v36
	v_mul_f32_e64 v39, v23, v37
	v_mul_f32_e64 v36, v18, v36
	v_mul_f32_e64 v37, v19, v37
	s_andn2_b64 vcc, exec, s[2:3]
	s_mov_b64 s[2:3], -1
	s_cbranch_vccnz .LBB0_1288
	s_mov_b64 s[2:3], exec
	v_readlane_b32 s16, v248, 7
	v_readlane_b32 s17, v248, 8
	s_and_b64 s[16:17], s[2:3], s[16:17]
	s_mov_b64 exec, s[16:17]
	s_cbranch_execz .LBB0_1287
	v_ashrrev_i32_e32 v109, 31, v108
	v_readlane_b32 s16, v249, 56
	v_lshlrev_b64 v[44:45], 6, v[108:109]
	v_readlane_b32 s17, v249, 57
	s_mov_b32 s4, 0x3d000000
	v_mul_f32_e64 v42, v38, s4
	v_mul_f32_e64 v43, v39, s4
	v_lshl_add_u64 v[44:45], s[16:17], 0, v[44:45]
	v_mul_f32_e64 v40, v34, s4
	v_mul_f32_e64 v41, v35, s4
	v_lshl_add_u64 v[44:45], v[174:175], 2, v[44:45]
	global_store_dwordx4 v[44:45], v[40:43], off
	s_nop 1
	v_mul_f32_e64 v42, v36, s4
	v_mul_f32_e64 v43, v37, s4
	v_mul_f32_e64 v40, v32, s4
	v_mul_f32_e64 v41, v33, s4
	global_store_dwordx4 v[44:45], v[40:43], off offset:16

;     __device__ __forceinline__ void operator()(const f32x4 (&acc)[2][2][4][2], const Unit& u, int wr, int wc, int fr, int fq, const Pre&) const {
;     ...
;                     const f32x4 x1 = acc[ai][0][m][0] * rs, x2 = acc[ai][0][m][1] * rs;
;                     if (wc < 2) {
;                         if (roti) st_bf16x8(kib + (size_t)row * 64 + cw, x1 * cs[q] - x2 * sn[q], x2 * cs[q] + x1 * sn[q]);
;                         else st_bf16x8(kib + (size_t)row * 64 + cw, x1, x2);
.LBB0_1291:
	s_andn2_saveexec_b64 s[2:3], s[2:3]
	s_cbranch_execz .LBB0_1293
	s_waitcnt vmcnt(0)
	v_mul_f32_e64 v42, v36, v74
	v_mul_f32_e64 v43, v37, v75
	v_mul_f32_e64 v36, v36, v78
	v_mul_f32_e64 v37, v37, v79
	v_mul_f32_e64 v46, v32, v76
	v_mul_f32_e64 v47, v33, v77
	v_mul_f32_e64 v44, v32, v72
	v_mul_f32_e64 v45, v33, v73
	v_fma_f32 v42, v38, v78, -v42
	v_fma_f32 v43, v39, v79, -v43
	v_fma_f32 v48, v38, v74, v36
	v_fma_f32 v49, v39, v75, v37
	v_fma_f32 v38, v34, v72, v46
	v_fma_f32 v39, v35, v73, v47
	v_fma_f32 v44, v34, v76, -v44
	v_fma_f32 v45, v35, v77, -v45
	s_nop 0
	v_cvt_pk_bf16_f32 v36, v44, v45
	v_cvt_pk_bf16_f32 v37, v42, v43
	v_cvt_pk_bf16_f32 v38, v38, v39
	v_cvt_pk_bf16_f32 v39, v48, v49
	global_store_dwordx4 v[40:41], v[36:39], off

;     __device__ __forceinline__ void operator()(const f32x4 (&acc)[2][2][4][2], const Unit& u, int wr, int wc, int fr, int fq, const Pre&) const {
;     ...
;                 } else if (kind == KD_QI) {
; #pragma unroll
;                     for (int bj = 0; bj < 2; ++bj) {
;                         const f32x4 x1 = acc[ai][bj][m][0] * rs, x2 = acc[ai][bj][m][1] * rs;
;                         bf16_t* o = qib + (size_t)row * 1024 + 256 * (pn - TL_QI) + 128 * bj + cw;
;                         if (roti) st_bf16x8(o, x1 * cs[q] - x2 * sn[q], x2 * cs[q] + x1 * sn[q]); else st_bf16x8(o, x1, x2);
;                     }
.LBB0_1295:
	s_andn2_b64 vcc, exec, s[2:3]
	s_cbranch_vccnz .LBB0_1305
	v_mov_b32_e32 v36, v176
	v_mov_b32_e32 v37, v176
	v_readlane_b32 s36, v248, 9
	v_mul_f32_e64 v44, v22, v36
	v_mul_f32_e64 v45, v23, v37
	v_mul_f32_e64 v42, v18, v36
	v_mul_f32_e64 v43, v19, v37
	v_readlane_b32 s37, v248, 10
	s_and_saveexec_b64 s[2:3], s[36:37]
	s_xor_b64 s[2:3], exec, s[2:3]
	s_cbranch_execz .LBB0_1298
	v_cvt_pk_bf16_f32 v38, v34, v35
	v_cvt_pk_bf16_f32 v39, v44, v45
	v_cvt_pk_bf16_f32 v40, v32, v33
	v_cvt_pk_bf16_f32 v41, v42, v43
.LBB0_1298:
	s_andn2_saveexec_b64 s[2:3], s[2:3]
	s_cbranch_execz .LBB0_1300
	s_waitcnt vmcnt(0)
	v_mul_f32_e64 v38, v32, v72
	v_mul_f32_e64 v39, v33, v73
	v_mul_f32_e64 v36, v42, v74
	v_mul_f32_e64 v37, v43, v75
	v_fma_f32 v38, v34, v76, -v38
	v_fma_f32 v39, v35, v77, -v39
	v_mul_f32_e64 v40, v42, v78
	v_mul_f32_e64 v41, v43, v79
	v_mul_f32_e64 v32, v32, v76
	v_mul_f32_e64 v33, v33, v77
	v_fma_f32 v36, v44, v78, -v36
	v_fma_f32 v37, v45, v79, -v37
	v_fma_f32 v42, v44, v74, v40
	v_fma_f32 v43, v45, v75, v41
	v_fma_f32 v32, v34, v72, v32
	v_fma_f32 v33, v35, v73, v33
	v_cvt_pk_bf16_f32 v38, v38, v39
	v_cvt_pk_bf16_f32 v39, v36, v37
	s_nop 0
	v_cvt_pk_bf16_f32 v40, v32, v33
	v_cvt_pk_bf16_f32 v41, v42, v43
.LBB0_1300:
	s_or_b64 exec, exec, s[2:3]
	v_ashrrev_i32_e32 v109, 31, v108
	v_readlane_b32 s2, v248, 18
	v_lshlrev_b64 v[32:33], 11, v[108:109]
	v_readlane_b32 s3, v248, 19
	v_mul_f32_e64 v36, v28, v176
	v_mul_f32_e64 v37, v29, v177
	s_nop 0
	v_lshl_add_u64 v[32:33], s[2:3], 0, v[32:33]
	v_lshl_add_u64 v[32:33], s[28:29], 1, v[32:33]
	v_lshl_add_u64 v[42:43], v[172:173], 1, v[32:33]
	v_mov_b32_e32 v32, v176
	v_mov_b32_e32 v33, v176
	global_store_dwordx4 v[42:43], v[38:41], off
	v_mul_f32_e64 v46, v26, v32
	v_mul_f32_e64 v47, v27, v33
	v_mul_f32_e64 v44, v30, v32
	v_mul_f32_e64 v45, v31, v33
	v_mul_f32_e64 v38, v24, v176
	v_mul_f32_e64 v39, v25, v177
	s_and_saveexec_b64 s[2:3], s[36:37]
	s_xor_b64 s[2:3], exec, s[2:3]
	s_cbranch_execz .LBB0_1302
	v_cvt_pk_bf16_f32 v32, v38, v39
	v_cvt_pk_bf16_f32 v33, v46, v47
	v_cvt_pk_bf16_f32 v34, v36, v37
	v_cvt_pk_bf16_f32 v35, v44, v45
.LBB0_1302:
	s_andn2_saveexec_b64 s[2:3], s[2:3]
	s_cbranch_execz .LBB0_1304
	s_waitcnt vmcnt(0)
	v_mul_f32_e64 v32, v44, v74
	v_mul_f32_e64 v33, v45, v75
	v_mul_f32_e64 v34, v36, v72
	v_mul_f32_e64 v35, v37, v73
	v_fma_f32 v40, v46, v78, -v32
	v_fma_f32 v41, v47, v79, -v33
	v_fma_f32 v32, v38, v76, -v34
	v_fma_f32 v33, v39, v77, -v35
	v_mul_f32_e64 v34, v44, v78
	v_mul_f32_e64 v35, v45, v79
	v_mul_f32_e64 v36, v36, v76
	v_mul_f32_e64 v37, v37, v77
	v_fma_f32 v44, v46, v74, v34
	v_fma_f32 v45, v47, v75, v35
	v_fma_f32 v34, v38, v72, v36
	v_fma_f32 v35, v39, v73, v37
	v_cvt_pk_bf16_f32 v32, v32, v33
	v_cvt_pk_bf16_f32 v33, v40, v41
	s_nop 0
	v_cvt_pk_bf16_f32 v34, v34, v35
	v_cvt_pk_bf16_f32 v35, v44, v45

;     __device__ __forceinline__ void operator()(const f32x4 (&acc)[2][2][4][2], const Unit& u, int wr, int wc, int fr, int fq, const Pre&) const {
;     ...
;                 } else if (kind == KD_V) {
; #pragma unroll
;                     for (int bj = 0; bj < 2; ++bj) st_bf16x8(vb + (size_t)row * 512 + 256 * (pn - TL_V) + 128 * bj + cw, acc[ai][bj][m][0] * rs, acc[ai][bj][m][1] * rs);
.LBB0_1306:
	s_andn2_b64 vcc, exec, s[2:3]
	s_cbranch_vccnz .LBB0_1308
	v_ashrrev_i32_e32 v109, 31, v108
	v_readlane_b32 s2, v249, 52
	v_lshlrev_b64 v[32:33], 10, v[108:109]
	v_readlane_b32 s3, v249, 53
	v_mul_f32_e64 v34, v22, v176
	v_mul_f32_e64 v35, v23, v176
	v_mul_f32_e64 v38, v18, v176
	v_mul_f32_e64 v39, v19, v176
	v_lshl_add_u64 v[32:33], s[2:3], 0, v[32:33]
	v_lshl_add_u64 v[32:33], s[94:95], 1, v[32:33]
	v_lshl_add_u64 v[36:37], v[172:173], 1, v[32:33]
	v_mul_f32_e64 v32, v20, v176
	v_mul_f32_e64 v33, v21, v176
	v_mul_f32_e64 v40, v16, v176
	v_mul_f32_e64 v41, v17, v176
	v_cvt_pk_bf16_f32 v32, v32, v33
	v_cvt_pk_bf16_f32 v33, v34, v35
	s_nop 0
	v_cvt_pk_bf16_f32 v34, v40, v41
	v_cvt_pk_bf16_f32 v35, v38, v39
	global_store_dwordx4 v[36:37], v[32:35], off
	v_mul_f32_e64 v38, v30, v176
	v_mul_f32_e64 v39, v31, v176
	v_mul_f32_e64 v40, v28, v176
	v_mul_f32_e64 v41, v29, v176
	v_mul_f32_e64 v34, v26, v176
	v_mul_f32_e64 v35, v27, v176
	v_mul_f32_e64 v32, v24, v176
	v_mul_f32_e64 v33, v25, v176
	s_nop 0
	v_cvt_pk_bf16_f32 v32, v32, v33
	v_cvt_pk_bf16_f32 v33, v34, v35
	v_cvt_pk_bf16_f32 v34, v40, v41
	v_cvt_pk_bf16_f32 v35, v38, v39
	global_store_dwordx4 v[36:37], v[32:35], off offset:256

;     __device__ __forceinline__ void operator()(const f32x4 (&acc)[2][2][4][2], const Unit& u, int wr, int wc, int fr, int fq, const Pre&) const {
;     ...
;                 } else if (kind == KD_Q || kind == KD_K) {
;                     bf16_t* o = (kind == KD_Q) ? qb + (size_t)row * DM + 256 * (pn - TL_Q) + cw : kb + (size_t)row * 512 + 256 * (pn - TL_K) + cw;
; #pragma unroll
;                     for (int bj = 0; bj < 2; ++bj) {
;                         const f32x4 x1 = acc[ai][bj][m][0] * rs, x2 = acc[ai][bj][m][1] * rs;
;                         if (rotqk) st_bf16x8(o + 128 * bj, x1 * cs[q] - x2 * sn[q], x2 * cs[q] + x1 * sn[q]);
;                         else st_bf16x8(o + 128 * bj, x1, x2);
;                     }
.LBB0_1309:
	s_andn2_b64 vcc, exec, s[2:3]
	s_cbranch_vccnz .LBB0_1319
	v_cndmask_b32_e64 v32, 0, 1, s[92:93]
	v_mul_f32_e64 v36, v22, v176
	v_mul_f32_e64 v37, v23, v176
	v_mul_f32_e64 v38, v20, v176
	v_mul_f32_e64 v39, v21, v176
	v_mul_f32_e64 v40, v18, v176
	v_mul_f32_e64 v41, v19, v176
	v_mul_f32_e64 v42, v16, v176
	v_mul_f32_e64 v43, v17, v176
	v_cmp_ne_u32_e64 s[2:3], 1, v32
	s_andn2_b64 vcc, exec, s[92:93]
	s_mov_b64 s[16:17], -1
	s_cbranch_vccnz .LBB0_1312
	s_mov_b64 s[16:17], 0
	v_cvt_pk_bf16_f32 v32, v38, v39
	v_cvt_pk_bf16_f32 v33, v36, v37
	v_cvt_pk_bf16_f32 v34, v42, v43
	v_cvt_pk_bf16_f32 v35, v40, v41
.LBB0_1312:
	s_andn2_b64 vcc, exec, s[16:17]
	s_cbranch_vccnz .LBB0_1314
	s_waitcnt vmcnt(0)
	v_mul_f32_e64 v32, v40, v74
	v_mul_f32_e64 v33, v41, v75
	v_mul_f32_e64 v34, v42, v72
	v_mul_f32_e64 v35, v43, v73
	v_fma_f32 v44, v36, v78, -v32
	v_fma_f32 v45, v37, v79, -v33
	v_fma_f32 v32, v38, v76, -v34
	v_fma_f32 v33, v39, v77, -v35
	v_mul_f32_e64 v34, v40, v78
	v_mul_f32_e64 v35, v41, v79
	v_mul_f32_e64 v40, v42, v76
	v_mul_f32_e64 v41, v43, v77
	v_fma_f32 v36, v36, v74, v34
	v_fma_f32 v37, v37, v75, v35
	v_fma_f32 v34, v38, v72, v40
	v_fma_f32 v35, v39, v73, v41
	v_cvt_pk_bf16_f32 v32, v32, v33
	v_cvt_pk_bf16_f32 v33, v44, v45
	s_nop 0
	v_cvt_pk_bf16_f32 v34, v34, v35
	v_cvt_pk_bf16_f32 v35, v36, v37
.LBB0_1314:
	s_and_b64 s[16:17], s[90:91], exec
	v_readlane_b32 s4, v249, 49
	v_readlane_b32 s16, v249, 51
	s_cselect_b32 s17, s4, s16
	v_readlane_b32 s4, v249, 48
	v_readlane_b32 s16, v249, 50
	v_ashrrev_i32_e32 v109, 31, v108
	s_cselect_b32 s16, s4, s16
	s_cselect_b32 s4, 12, 10
	v_lshlrev_b64 v[36:37], s4, v[108:109]
	s_cselect_b32 s37, s34, s30
	s_cselect_b32 s36, s31, s81
	v_lshl_add_u64 v[36:37], s[16:17], 0, v[36:37]
	v_lshl_add_u64 v[36:37], s[36:37], 1, v[36:37]
	v_lshl_add_u64 v[36:37], v[172:173], 1, v[36:37]
	v_mov_b32_e32 v177, v176
	global_store_dwordx4 v[36:37], v[32:35], off
	v_mul_f32_e64 v40, v24, v176
	v_mul_f32_e64 v41, v25, v177
	v_mul_f32_e64 v44, v28, v176
	v_mul_f32_e64 v45, v29, v177
	v_mov_b32_e32 v32, v176
	v_mov_b32_e32 v33, v176
	v_mul_f32_e64 v38, v26, v32
	v_mul_f32_e64 v39, v27, v33
	v_mul_f32_e64 v42, v30, v32
	v_mul_f32_e64 v43, v31, v33
	s_and_b64 vcc, exec, s[2:3]
	s_mov_b64 s[2:3], -1
	s_cbranch_vccnz .LBB0_1316
	s_mov_b64 s[2:3], 0
	v_cvt_pk_bf16_f32 v32, v40, v41
	v_cvt_pk_bf16_f32 v33, v38, v39
	v_cvt_pk_bf16_f32 v34, v44, v45
	v_cvt_pk_bf16_f32 v35, v42, v43
.LBB0_1316:
	s_andn2_b64 vcc, exec, s[2:3]
	s_cbranch_vccnz .LBB0_1318
	s_waitcnt vmcnt(0)
	v_mul_f32_e64 v32, v42, v74
	v_mul_f32_e64 v33, v43, v75
	v_mul_f32_e64 v34, v44, v72
	v_mul_f32_e64 v35, v45, v73
	v_fma_f32 v46, v38, v78, -v32
	v_fma_f32 v47, v39, v79, -v33
	v_fma_f32 v32, v40, v76, -v34
	v_fma_f32 v33, v41, v77, -v35
	v_mul_f32_e64 v34, v42, v78
	v_mul_f32_e64 v35, v43, v79
	v_mul_f32_e64 v42, v44, v76
	v_mul_f32_e64 v43, v45, v77
	v_fma_f32 v38, v38, v74, v34
	v_fma_f32 v39, v39, v75, v35
	v_fma_f32 v34, v40, v72, v42
	v_fma_f32 v35, v41, v73, v43
	v_cvt_pk_bf16_f32 v32, v32, v33
	v_cvt_pk_bf16_f32 v33, v46, v47
	s_nop 0
	v_cvt_pk_bf16_f32 v34, v34, v35
	v_cvt_pk_bf16_f32 v35, v38, v39

; __device__ __forceinline__ f32x4 sigmoid4(const f32x4& x, float s) {
;     f32x4 z = x * (s * -1.4426950408889634f), e;
; #pragma unroll
;     for (int j = 0; j < 4; ++j) e[j] = __builtin_amdgcn_exp2f(z[j]);
;     e = e + 1.0f;
; #pragma unroll
;     for (int j = 0; j < 4; ++j) e[j] = __builtin_amdgcn_rcpf(e[j]);
;     return e;
; }
;     __device__ __forceinline__ void operator()(const f32x4 (&acc)[2][2][4][2], const Unit& u, int wr, int wc, int fr, int fq, const Pre&) const {
;     ...
;                 } else if (kind == KD_A) {
;                     st_bf16x8(abuf + (size_t)row * DM + 128 * (pn - TL_A) + cw, acc[ai][0][m][0] * rs * sigmoid4(acc[ai][1][m][0], rs), acc[ai][0][m][1] * rs * sigmoid4(acc[ai][1][m][1], rs));
.LBB0_1323:
	v_ashrrev_i32_e32 v189, 31, v188
	s_waitcnt vmcnt(0)
	v_lshlrev_b64 v[80:81], 12, v[188:189]
	v_lshl_add_u64 v[80:81], s[12:13], 0, v[80:81]
	v_lshl_add_u64 v[80:81], s[88:89], 1, v[80:81]
	v_mul_f32_e32 v91, 0xbfb8aa3b, v186
	v_lshl_add_u64 v[84:85], v[172:173], 1, v[80:81]
	v_mul_f32_e32 v80, v68, v91
	v_mul_f32_e32 v81, v69, v91
	v_mul_f32_e32 v82, v70, v91
	v_mul_f32_e32 v83, v71, v91
	v_exp_f32_e32 v80, v80
	v_exp_f32_e32 v82, v82
	v_exp_f32_e32 v83, v83
	v_exp_f32_e32 v81, v81
	v_mul_f32_e32 v90, v64, v91
	v_mul_f32_e32 v94, v65, v91
	v_add_f32_e64 v82, v82, 1.0
	v_add_f32_e64 v83, v83, 1.0
	v_add_f32_e64 v80, v80, 1.0
	v_add_f32_e64 v81, v81, 1.0
	v_mul_f32_e32 v92, v66, v91
	v_mul_f32_e32 v91, v67, v91
	v_rcp_f32_e32 v80, v80
	v_rcp_f32_e32 v81, v81
	v_rcp_f32_e32 v82, v82
	v_rcp_f32_e32 v83, v83
	v_exp_f32_e32 v90, v90
	v_exp_f32_e32 v92, v92
	v_exp_f32_e32 v93, v91
	v_exp_f32_e32 v91, v94
	v_mul_f32_e64 v86, v78, v186
	v_mul_f32_e64 v87, v79, v186
	v_mul_f32_e64 v88, v76, v186
	v_mul_f32_e64 v89, v77, v186
	v_mul_f32_e64 v82, v86, v82
	v_mul_f32_e64 v83, v87, v83
	v_mul_f32_e64 v80, v88, v80
	v_mul_f32_e64 v81, v89, v81
	v_add_f32_e64 v86, v92, 1.0
	v_add_f32_e64 v87, v93, 1.0
	v_add_f32_e64 v88, v90, 1.0
	v_add_f32_e64 v89, v91, 1.0
	v_rcp_f32_e32 v86, v86
	v_rcp_f32_e32 v88, v88
	v_rcp_f32_e32 v87, v87
	v_rcp_f32_e32 v89, v89
	v_mul_f32_e64 v90, v74, v186
	v_mul_f32_e64 v91, v75, v186
	v_mul_f32_e64 v92, v72, v186
	v_mul_f32_e64 v93, v73, v186
	v_mul_f32_e64 v86, v90, v86
	v_mul_f32_e64 v87, v91, v87
	v_mul_f32_e64 v88, v92, v88
	v_mul_f32_e64 v89, v93, v89
	v_cvt_pk_bf16_f32 v80, v80, v81
	v_cvt_pk_bf16_f32 v81, v82, v83
	s_nop 0
	v_cvt_pk_bf16_f32 v82, v88, v89
	v_cvt_pk_bf16_f32 v83, v86, v87
	global_store_dwordx4 v[84:85], v[80:83], off

; __device__ __forceinline__ f32x4 sigmoid4(const f32x4& x, float s) {
;     f32x4 z = x * (s * -1.4426950408889634f), e;
; #pragma unroll
;     for (int j = 0; j < 4; ++j) e[j] = __builtin_amdgcn_exp2f(z[j]);
;     e = e + 1.0f;
; #pragma unroll
;     for (int j = 0; j < 4; ++j) e[j] = __builtin_amdgcn_rcpf(e[j]);
;     return e;
; }
;     __device__ __forceinline__ void operator()(const f32x4 (&acc)[2][2][4][2], const Unit& u, int wr, int wc, int fr, int fq, const Pre&) const {
;     ...
;                 } else if (kind == KD_A) {
;                     st_bf16x8(abuf + (size_t)row * DM + 128 * (pn - TL_A) + cw, acc[ai][0][m][0] * rs * sigmoid4(acc[ai][1][m][0], rs), acc[ai][0][m][1] * rs * sigmoid4(acc[ai][1][m][1], rs));
.LBB0_1328:
	v_ashrrev_i32_e32 v109, 31, v108
	v_lshlrev_b64 v[32:33], 12, v[108:109]
	v_lshl_add_u64 v[32:33], s[12:13], 0, v[32:33]
	v_lshl_add_u64 v[32:33], s[88:89], 1, v[32:33]
	v_mul_f32_e32 v43, 0xbfb8aa3b, v176
	v_lshl_add_u64 v[36:37], v[172:173], 1, v[32:33]
	v_mul_f32_e32 v32, v24, v43
	v_mul_f32_e32 v33, v25, v43
	v_mul_f32_e32 v34, v26, v43
	v_mul_f32_e32 v35, v27, v43
	v_exp_f32_e32 v32, v32
	v_exp_f32_e32 v34, v34
	v_exp_f32_e32 v35, v35
	v_exp_f32_e32 v33, v33
	v_mul_f32_e32 v42, v28, v43
	v_mul_f32_e32 v46, v29, v43
	v_add_f32_e64 v34, v34, 1.0
	v_add_f32_e64 v35, v35, 1.0
	v_add_f32_e64 v32, v32, 1.0
	v_add_f32_e64 v33, v33, 1.0
	v_mul_f32_e32 v44, v30, v43
	v_mul_f32_e32 v43, v31, v43
	v_rcp_f32_e32 v32, v32
	v_rcp_f32_e32 v33, v33
	v_rcp_f32_e32 v34, v34
	v_rcp_f32_e32 v35, v35
	v_exp_f32_e32 v42, v42
	v_exp_f32_e32 v44, v44
	v_exp_f32_e32 v45, v43
	v_exp_f32_e32 v43, v46
	v_mul_f32_e64 v38, v22, v176
	v_mul_f32_e64 v39, v23, v176
	v_mul_f32_e64 v40, v20, v176
	v_mul_f32_e64 v41, v21, v176
	v_mul_f32_e64 v34, v38, v34
	v_mul_f32_e64 v35, v39, v35
	v_mul_f32_e64 v32, v40, v32
	v_mul_f32_e64 v33, v41, v33
	v_add_f32_e64 v38, v44, 1.0
	v_add_f32_e64 v39, v45, 1.0
	v_add_f32_e64 v40, v42, 1.0
	v_add_f32_e64 v41, v43, 1.0
	v_rcp_f32_e32 v38, v38
	v_rcp_f32_e32 v40, v40
	v_rcp_f32_e32 v39, v39
	v_rcp_f32_e32 v41, v41
	v_mul_f32_e64 v42, v18, v176
	v_mul_f32_e64 v43, v19, v176
	v_mul_f32_e64 v44, v16, v176
	v_mul_f32_e64 v45, v17, v176
	v_mul_f32_e64 v38, v42, v38
	v_mul_f32_e64 v39, v43, v39
	v_mul_f32_e64 v40, v44, v40
	v_mul_f32_e64 v41, v45, v41
	v_cvt_pk_bf16_f32 v32, v32, v33
	v_cvt_pk_bf16_f32 v33, v34, v35
	s_nop 0
	v_cvt_pk_bf16_f32 v34, v40, v41
	v_cvt_pk_bf16_f32 v35, v38, v39
	global_store_dwordx4 v[36:37], v[32:35], off

; __device__ __forceinline__ f32x4 sigmoid4(const f32x4& x, float s) {
;     f32x4 z = x * (s * -1.4426950408889634f), e;
; #pragma unroll
;     for (int j = 0; j < 4; ++j) e[j] = __builtin_amdgcn_exp2f(z[j]);
;     e = e + 1.0f;
; #pragma unroll
;     for (int j = 0; j < 4; ++j) e[j] = __builtin_amdgcn_rcpf(e[j]);
;     return e;
; }
;     __device__ __forceinline__ void operator()(const f32x4 (&acc)[2][2][4][2], const Unit& u, int wr, int wc, int fr, int fq, const Pre&) const {
;     ...
;                 } else if (kind == KD_G) {
; #pragma unroll
;                     for (int bj = 0; bj < 2; ++bj)
;                         st_bf16x8(gabuf + (size_t)row * DM + 256 * (pn - TL_G) + 128 * bj + cw, sigmoid4(acc[ai][bj][m][0], rs), sigmoid4(acc[ai][bj][m][1], rs));
.LBB0_1331:
	s_mov_b64 s[16:17], -1
	s_mov_b64 s[0:1], 0
	s_cmp_lt_i32 s7, 1
	s_mov_b64 s[2:3], 0
	s_cbranch_scc1 .LBB0_1379
	s_cmp_gt_i32 s7, 1
	s_cbranch_scc0 .LBB0_1336
	s_cmp_eq_u32 s7, 2
	s_mov_b64 s[2:3], -1
	s_cbranch_scc0 .LBB0_1335
	v_ashrrev_i32_e32 v107, 31, v106
	v_readlane_b32 s2, v249, 46
	v_lshlrev_b64 v[16:17], 12, v[106:107]
	v_readlane_b32 s3, v249, 47
	v_mul_f32_e32 v22, 0xbfb8aa3b, v170
	v_mul_f32_e32 v18, v6, v22
	v_lshl_add_u64 v[16:17], s[2:3], 0, v[16:17]
	v_lshl_add_u64 v[16:17], s[38:39], 1, v[16:17]
	v_mul_f32_e32 v19, v7, v22
	v_lshl_add_u64 v[20:21], v[172:173], 1, v[16:17]
	v_mul_f32_e32 v16, v4, v22
	v_mul_f32_e32 v17, v5, v22
	v_exp_f32_e32 v18, v18
	v_exp_f32_e32 v19, v19
	v_exp_f32_e32 v16, v16
	v_exp_f32_e32 v17, v17
	s_mov_b64 s[2:3], 0
	v_add_f32_e64 v18, v18, 1.0
	v_add_f32_e64 v19, v19, 1.0
	v_add_f32_e64 v16, v16, 1.0
	v_add_f32_e64 v17, v17, 1.0
	v_rcp_f32_e32 v25, v18
	v_rcp_f32_e32 v26, v19
	v_mul_f32_e32 v18, v2, v22
	v_mul_f32_e32 v19, v3, v22
	v_rcp_f32_e32 v23, v16
	v_rcp_f32_e32 v24, v17
	v_mul_f32_e32 v16, v0, v22
	v_mul_f32_e32 v17, v1, v22
	v_exp_f32_e32 v18, v18
	v_exp_f32_e32 v19, v19
	v_exp_f32_e32 v16, v16
	v_exp_f32_e32 v17, v17
	v_add_f32_e64 v18, v18, 1.0
	v_add_f32_e64 v19, v19, 1.0
	s_nop 0
	v_rcp_f32_e32 v19, v19
	v_add_f32_e64 v16, v16, 1.0
	v_add_f32_e64 v17, v17, 1.0
	v_rcp_f32_e32 v29, v18
	v_rcp_f32_e32 v27, v16
	v_rcp_f32_e32 v28, v17
	v_cvt_pk_bf16_f32 v16, v23, v24
	v_cvt_pk_bf16_f32 v17, v25, v26
	v_cvt_pk_bf16_f32 v18, v27, v28
	v_cvt_pk_bf16_f32 v19, v29, v19
	global_store_dwordx4 v[20:21], v[16:19], off
	s_nop 1
	v_mul_f32_e32 v18, v10, v22
	v_mul_f32_e32 v19, v11, v22
	v_mul_f32_e32 v16, v8, v22
	v_mul_f32_e32 v17, v9, v22
	v_exp_f32_e32 v18, v18
	v_exp_f32_e32 v19, v19
	v_exp_f32_e32 v16, v16
	v_exp_f32_e32 v17, v17
	v_add_f32_e64 v18, v18, 1.0
	v_add_f32_e64 v19, v19, 1.0
	s_nop 0
	v_rcp_f32_e32 v25, v18
	v_add_f32_e64 v16, v16, 1.0
	v_add_f32_e64 v17, v17, 1.0
	v_rcp_f32_e32 v26, v19
	v_mul_f32_e32 v18, v14, v22
	v_mul_f32_e32 v19, v15, v22
	v_rcp_f32_e32 v23, v16
	v_rcp_f32_e32 v24, v17
	v_mul_f32_e32 v16, v12, v22
	v_mul_f32_e32 v17, v13, v22
	v_exp_f32_e32 v18, v18
	v_exp_f32_e32 v19, v19
	v_exp_f32_e32 v16, v16
	v_exp_f32_e32 v17, v17
	v_add_f32_e64 v18, v18, 1.0
	v_add_f32_e64 v19, v19, 1.0
	s_nop 0
	v_rcp_f32_e32 v19, v19
	v_add_f32_e64 v16, v16, 1.0
	v_add_f32_e64 v17, v17, 1.0
	v_rcp_f32_e32 v28, v18
	v_rcp_f32_e32 v22, v16
	v_rcp_f32_e32 v27, v17
	v_cvt_pk_bf16_f32 v16, v23, v24
	v_cvt_pk_bf16_f32 v17, v25, v26
	v_cvt_pk_bf16_f32 v18, v22, v27
	v_cvt_pk_bf16_f32 v19, v28, v19
	global_store_dwordx4 v[20:21], v[16:19], off offset:256

;     __device__ __forceinline__ void operator()(const f32x4 (&acc)[2][2][4][2], const Unit& u, int wr, int wc, int fr, int fq, const Pre&) const {
;     ...
;                 } else if (kind == KD_P) {
;                     const float r2 = rs * rs;
;                     st_bf16x8(pbuf + (size_t)row * DM + 128 * (pn - TL_P) + cw, acc[ai][0][m][0] * acc[ai][1][m][0] * r2, acc[ai][0][m][1] * acc[ai][1][m][1] * r2);
.LBB0_1336:
	s_and_b64 vcc, exec, s[16:17]
	s_cbranch_vccz .LBB0_1338
	v_ashrrev_i32_e32 v107, 31, v106
	v_readlane_b32 s16, v249, 44
	v_lshlrev_b64 v[18:19], 12, v[106:107]
	v_readlane_b32 s17, v249, 45
	v_mul_f32_e32 v16, v170, v170
	v_mul_f32_e64 v22, v4, v8
	v_mul_f32_e64 v23, v5, v9
	v_lshl_add_u64 v[18:19], s[16:17], 0, v[18:19]
	v_lshl_add_u64 v[18:19], s[42:43], 1, v[18:19]
	v_lshl_add_u64 v[20:21], v[172:173], 1, v[18:19]
	v_mul_f32_e64 v18, v6, v10
	v_mul_f32_e64 v19, v7, v11
	v_mul_f32_e64 v24, v2, v14
	v_mul_f32_e64 v25, v3, v15
	v_mul_f32_e64 v18, v18, v16
	v_mul_f32_e64 v19, v19, v16
	v_mul_f32_e64 v26, v0, v12
	v_mul_f32_e64 v27, v1, v13
	v_mul_f32_e64 v22, v22, v16
	v_mul_f32_e64 v23, v23, v16
	v_mul_f32_e64 v24, v24, v16
	v_mul_f32_e64 v25, v25, v16
	v_mul_f32_e64 v26, v26, v16
	v_mul_f32_e64 v27, v27, v16
	v_cvt_pk_bf16_f32 v16, v22, v23
	v_cvt_pk_bf16_f32 v17, v18, v19
	s_nop 0
	v_cvt_pk_bf16_f32 v18, v26, v27
	v_cvt_pk_bf16_f32 v19, v24, v25
	global_store_dwordx4 v[20:21], v[16:19], off

;     __device__ __forceinline__ void operator()(const f32x4 (&acc)[2][2][4][2], const Unit& u, int wr, int wc, int fr, int fq, const Pre&) const {
;     ...
;                 } else {
;                     const f32x4 x1 = acc[ai][0][m][0] * rs, x2 = acc[ai][0][m][1] * rs;
;                     if (wc < 2) {
;                         if (roti) st_bf16x8(kib + (size_t)row * 64 + cw, x1 * cs[q] - x2 * sn[q], x2 * cs[q] + x1 * sn[q]);
;                         else st_bf16x8(kib + (size_t)row * 64 + cw, x1, x2);
;                     } else if (wc == 2 && fq < 2) {
;                         *(f32x4*)(wib + (size_t)row * 16 + 8 * fq) = x1 * 0.03125f; *(f32x4*)(wib + (size_t)row * 16 + 8 * fq + 4) = x2 * 0.03125f;
;                     }
.LBB0_1340:
	s_andn2_b64 vcc, exec, s[64:65]
	s_mov_b64 s[0:1], -1
	s_cbranch_vccnz .LBB0_1368
	s_andn2_b64 vcc, exec, s[58:59]
	s_cbranch_vccnz .LBB0_1365
	v_readlane_b32 s2, v249, 63
	v_mov_b32_e32 v171, v170
	v_readlane_b32 s3, v248, 0
	s_andn2_b64 vcc, exec, s[2:3]
	v_mul_f32_e64 v18, v4, v170
	v_mul_f32_e64 v19, v5, v171
	v_mul_f32_e64 v16, v0, v170
	v_mul_f32_e64 v17, v1, v171
	s_cbranch_vccnz .LBB0_1354
	v_readlane_b32 s0, v248, 24
	v_mov_b32_e32 v20, v170
	v_mov_b32_e32 v21, v170
	v_readlane_b32 s1, v248, 25
	v_mul_f32_e64 v22, v6, v20
	v_mul_f32_e64 v23, v7, v21
	v_mul_f32_e64 v20, v2, v20
	v_mul_f32_e64 v21, v3, v21
	s_andn2_b64 vcc, exec, s[0:1]
	s_mov_b64 s[0:1], -1
	s_cbranch_vccnz .LBB0_1347
	s_mov_b64 s[0:1], exec
	v_readlane_b32 s2, v248, 7
	v_readlane_b32 s3, v248, 8
	s_and_b64 s[2:3], s[0:1], s[2:3]
	s_mov_b64 exec, s[2:3]
	s_cbranch_execz .LBB0_1346
	v_ashrrev_i32_e32 v107, 31, v106
	v_readlane_b32 s2, v249, 56
	v_lshlrev_b64 v[28:29], 6, v[106:107]
	v_readlane_b32 s3, v249, 57
	s_mov_b32 s4, 0x3d000000
	v_mul_f32_e64 v26, v22, s4
	v_mul_f32_e64 v27, v23, s4
	v_lshl_add_u64 v[28:29], s[2:3], 0, v[28:29]
	v_mul_f32_e64 v24, v18, s4
	v_mul_f32_e64 v25, v19, s4
	v_lshl_add_u64 v[28:29], v[174:175], 2, v[28:29]
	global_store_dwordx4 v[28:29], v[24:27], off
	s_nop 1
	v_mul_f32_e64 v26, v20, s4
	v_mul_f32_e64 v27, v21, s4
	v_mul_f32_e64 v24, v16, s4
	v_mul_f32_e64 v25, v17, s4
	global_store_dwordx4 v[28:29], v[24:27], off offset:16

;     __device__ __forceinline__ void operator()(const f32x4 (&acc)[2][2][4][2], const Unit& u, int wr, int wc, int fr, int fq, const Pre&) const {
;     ...
;                     const f32x4 x1 = acc[ai][0][m][0] * rs, x2 = acc[ai][0][m][1] * rs;
;                     if (wc < 2) {
;                         if (roti) st_bf16x8(kib + (size_t)row * 64 + cw, x1 * cs[q] - x2 * sn[q], x2 * cs[q] + x1 * sn[q]);
;                         else st_bf16x8(kib + (size_t)row * 64 + cw, x1, x2);
.LBB0_1350:
	s_andn2_saveexec_b64 s[0:1], s[0:1]
	s_cbranch_execz .LBB0_1352
	s_waitcnt vmcnt(0)
	v_mul_f32_e64 v26, v20, v66
	v_mul_f32_e64 v27, v21, v67
	v_mul_f32_e64 v20, v20, v70
	v_mul_f32_e64 v21, v21, v71
	v_mul_f32_e64 v30, v16, v68
	v_mul_f32_e64 v31, v17, v69
	v_mul_f32_e64 v28, v16, v64
	v_mul_f32_e64 v29, v17, v65
	v_fma_f32 v26, v22, v70, -v26
	v_fma_f32 v27, v23, v71, -v27
	v_fma_f32 v32, v22, v66, v20
	v_fma_f32 v33, v23, v67, v21
	v_fma_f32 v22, v18, v64, v30
	v_fma_f32 v23, v19, v65, v31
	v_fma_f32 v28, v18, v68, -v28
	v_fma_f32 v29, v19, v69, -v29
	s_nop 0
	v_cvt_pk_bf16_f32 v20, v28, v29
	v_cvt_pk_bf16_f32 v21, v26, v27
	v_cvt_pk_bf16_f32 v22, v22, v23
	v_cvt_pk_bf16_f32 v23, v32, v33
	global_store_dwordx4 v[24:25], v[20:23], off

;     __device__ __forceinline__ void operator()(const f32x4 (&acc)[2][2][4][2], const Unit& u, int wr, int wc, int fr, int fq, const Pre&) const {
;     ...
;                 } else if (kind == KD_QI) {
; #pragma unroll
;                     for (int bj = 0; bj < 2; ++bj) {
;                         const f32x4 x1 = acc[ai][bj][m][0] * rs, x2 = acc[ai][bj][m][1] * rs;
;                         bf16_t* o = qib + (size_t)row * 1024 + 256 * (pn - TL_QI) + 128 * bj + cw;
;                         if (roti) st_bf16x8(o, x1 * cs[q] - x2 * sn[q], x2 * cs[q] + x1 * sn[q]); else st_bf16x8(o, x1, x2);
;                     }
.LBB0_1354:
	s_andn2_b64 vcc, exec, s[0:1]
	s_cbranch_vccnz .LBB0_1364
	v_mov_b32_e32 v20, v170
	v_mov_b32_e32 v21, v170
	v_readlane_b32 s16, v248, 9
	v_mul_f32_e64 v28, v6, v20
	v_mul_f32_e64 v29, v7, v21
	v_mul_f32_e64 v26, v2, v20
	v_mul_f32_e64 v27, v3, v21
	v_readlane_b32 s17, v248, 10
	s_and_saveexec_b64 s[0:1], s[16:17]
	s_xor_b64 s[0:1], exec, s[0:1]
	s_cbranch_execz .LBB0_1357
	v_cvt_pk_bf16_f32 v22, v18, v19
	v_cvt_pk_bf16_f32 v23, v28, v29
	v_cvt_pk_bf16_f32 v24, v16, v17
	v_cvt_pk_bf16_f32 v25, v26, v27
.LBB0_1357:
	s_andn2_saveexec_b64 s[0:1], s[0:1]
	s_cbranch_execz .LBB0_1359
	s_waitcnt vmcnt(0)
	v_mul_f32_e64 v22, v16, v64
	v_mul_f32_e64 v23, v17, v65
	v_mul_f32_e64 v20, v26, v66
	v_mul_f32_e64 v21, v27, v67
	v_fma_f32 v22, v18, v68, -v22
	v_fma_f32 v23, v19, v69, -v23
	v_mul_f32_e64 v24, v26, v70
	v_mul_f32_e64 v25, v27, v71
	v_mul_f32_e64 v16, v16, v68
	v_mul_f32_e64 v17, v17, v69
	v_fma_f32 v20, v28, v70, -v20
	v_fma_f32 v21, v29, v71, -v21
	v_fma_f32 v26, v28, v66, v24
	v_fma_f32 v27, v29, v67, v25
	v_fma_f32 v16, v18, v64, v16
	v_fma_f32 v17, v19, v65, v17
	v_cvt_pk_bf16_f32 v22, v22, v23
	v_cvt_pk_bf16_f32 v23, v20, v21
	s_nop 0
	v_cvt_pk_bf16_f32 v24, v16, v17
	v_cvt_pk_bf16_f32 v25, v26, v27
.LBB0_1359:
	s_or_b64 exec, exec, s[0:1]
	v_ashrrev_i32_e32 v107, 31, v106
	v_readlane_b32 s0, v248, 18
	v_lshlrev_b64 v[16:17], 11, v[106:107]
	v_readlane_b32 s1, v248, 19
	v_mul_f32_e64 v20, v12, v170
	v_mul_f32_e64 v21, v13, v171
	s_nop 0
	v_lshl_add_u64 v[16:17], s[0:1], 0, v[16:17]
	v_lshl_add_u64 v[16:17], s[28:29], 1, v[16:17]
	v_lshl_add_u64 v[26:27], v[172:173], 1, v[16:17]
	v_mov_b32_e32 v16, v170
	v_mov_b32_e32 v17, v170
	global_store_dwordx4 v[26:27], v[22:25], off
	v_mul_f32_e64 v28, v10, v16
	v_mul_f32_e64 v29, v11, v17
	v_mul_f32_e64 v30, v14, v16
	v_mul_f32_e64 v31, v15, v17
	v_mul_f32_e64 v22, v8, v170
	v_mul_f32_e64 v23, v9, v171
	s_and_saveexec_b64 s[0:1], s[16:17]
	s_xor_b64 s[0:1], exec, s[0:1]
	s_cbranch_execz .LBB0_1361
	v_cvt_pk_bf16_f32 v16, v22, v23
	v_cvt_pk_bf16_f32 v17, v28, v29
	v_cvt_pk_bf16_f32 v18, v20, v21
	v_cvt_pk_bf16_f32 v19, v30, v31
.LBB0_1361:
	s_andn2_saveexec_b64 s[0:1], s[0:1]
	s_cbranch_execz .LBB0_1363
	s_waitcnt vmcnt(0)
	v_mul_f32_e64 v16, v30, v66
	v_mul_f32_e64 v17, v31, v67
	v_mul_f32_e64 v18, v20, v64
	v_mul_f32_e64 v19, v21, v65
	v_fma_f32 v24, v28, v70, -v16
	v_fma_f32 v25, v29, v71, -v17
	v_fma_f32 v16, v22, v68, -v18
	v_fma_f32 v17, v23, v69, -v19
	v_mul_f32_e64 v18, v30, v70
	v_mul_f32_e64 v19, v31, v71
	v_mul_f32_e64 v20, v20, v68
	v_mul_f32_e64 v21, v21, v69
	v_fma_f32 v28, v28, v66, v18
	v_fma_f32 v29, v29, v67, v19
	v_fma_f32 v18, v22, v64, v20
	v_fma_f32 v19, v23, v65, v21
	v_cvt_pk_bf16_f32 v16, v16, v17
	v_cvt_pk_bf16_f32 v17, v24, v25
	s_nop 0
	v_cvt_pk_bf16_f32 v18, v18, v19
	v_cvt_pk_bf16_f32 v19, v28, v29

;     __device__ __forceinline__ void operator()(const f32x4 (&acc)[2][2][4][2], const Unit& u, int wr, int wc, int fr, int fq, const Pre&) const {
;     ...
;                 } else if (kind == KD_V) {
; #pragma unroll
;                     for (int bj = 0; bj < 2; ++bj) st_bf16x8(vb + (size_t)row * 512 + 256 * (pn - TL_V) + 128 * bj + cw, acc[ai][bj][m][0] * rs, acc[ai][bj][m][1] * rs);
.LBB0_1365:
	s_andn2_b64 vcc, exec, s[0:1]
	s_cbranch_vccnz .LBB0_1367
	v_ashrrev_i32_e32 v107, 31, v106
	v_readlane_b32 s0, v249, 52
	v_lshlrev_b64 v[16:17], 10, v[106:107]
	v_readlane_b32 s1, v249, 53
	v_mul_f32_e64 v18, v6, v170
	v_mul_f32_e64 v19, v7, v170
	v_mul_f32_e64 v22, v2, v170
	v_mul_f32_e64 v23, v3, v170
	v_lshl_add_u64 v[16:17], s[0:1], 0, v[16:17]
	v_lshl_add_u64 v[16:17], s[94:95], 1, v[16:17]
	v_lshl_add_u64 v[20:21], v[172:173], 1, v[16:17]
	v_mul_f32_e64 v16, v4, v170
	v_mul_f32_e64 v17, v5, v170
	v_mul_f32_e64 v24, v0, v170
	v_mul_f32_e64 v25, v1, v170
	v_cvt_pk_bf16_f32 v16, v16, v17
	v_cvt_pk_bf16_f32 v17, v18, v19
	s_nop 0
	v_cvt_pk_bf16_f32 v18, v24, v25
	v_cvt_pk_bf16_f32 v19, v22, v23
	global_store_dwordx4 v[20:21], v[16:19], off
	v_mul_f32_e64 v22, v14, v170
	v_mul_f32_e64 v23, v15, v170
	v_mul_f32_e64 v24, v12, v170
	v_mul_f32_e64 v25, v13, v170
	v_mul_f32_e64 v18, v10, v170
	v_mul_f32_e64 v19, v11, v170
	v_mul_f32_e64 v16, v8, v170
	v_mul_f32_e64 v17, v9, v170
	s_nop 0
	v_cvt_pk_bf16_f32 v16, v16, v17
	v_cvt_pk_bf16_f32 v17, v18, v19
	v_cvt_pk_bf16_f32 v18, v24, v25
	v_cvt_pk_bf16_f32 v19, v22, v23
	global_store_dwordx4 v[20:21], v[16:19], off offset:256

;     __device__ __forceinline__ void operator()(const f32x4 (&acc)[2][2][4][2], const Unit& u, int wr, int wc, int fr, int fq, const Pre&) const {
;     ...
;                 } else if (kind == KD_Q || kind == KD_K) {
;                     bf16_t* o = (kind == KD_Q) ? qb + (size_t)row * DM + 256 * (pn - TL_Q) + cw : kb + (size_t)row * 512 + 256 * (pn - TL_K) + cw;
; #pragma unroll
;                     for (int bj = 0; bj < 2; ++bj) {
;                         const f32x4 x1 = acc[ai][bj][m][0] * rs, x2 = acc[ai][bj][m][1] * rs;
;                         if (rotqk) st_bf16x8(o + 128 * bj, x1 * cs[q] - x2 * sn[q], x2 * cs[q] + x1 * sn[q]);
;                         else st_bf16x8(o + 128 * bj, x1, x2);
;                     }
.LBB0_1368:
	s_andn2_b64 vcc, exec, s[0:1]
	s_cbranch_vccnz .LBB0_1378
	v_cndmask_b32_e64 v16, 0, 1, s[92:93]
	v_mul_f32_e64 v20, v6, v170
	v_mul_f32_e64 v21, v7, v170
	v_mul_f32_e64 v22, v4, v170
	v_mul_f32_e64 v23, v5, v170
	v_mul_f32_e64 v24, v2, v170
	v_mul_f32_e64 v25, v3, v170
	v_mul_f32_e64 v26, v0, v170
	v_mul_f32_e64 v27, v1, v170
	v_cmp_ne_u32_e64 s[0:1], 1, v16
	s_andn2_b64 vcc, exec, s[92:93]
	s_mov_b64 s[2:3], -1
	s_cbranch_vccnz .LBB0_1371
	s_mov_b64 s[2:3], 0
	v_cvt_pk_bf16_f32 v16, v22, v23
	v_cvt_pk_bf16_f32 v17, v20, v21
	v_cvt_pk_bf16_f32 v18, v26, v27
	v_cvt_pk_bf16_f32 v19, v24, v25
.LBB0_1371:
	s_andn2_b64 vcc, exec, s[2:3]
	s_cbranch_vccnz .LBB0_1373
	s_waitcnt vmcnt(0)
	v_mul_f32_e64 v16, v24, v66
	v_mul_f32_e64 v17, v25, v67
	v_mul_f32_e64 v18, v26, v64
	v_mul_f32_e64 v19, v27, v65
	v_fma_f32 v28, v20, v70, -v16
	v_fma_f32 v29, v21, v71, -v17
	v_fma_f32 v16, v22, v68, -v18
	v_fma_f32 v17, v23, v69, -v19
	v_mul_f32_e64 v18, v24, v70
	v_mul_f32_e64 v19, v25, v71
	v_mul_f32_e64 v24, v26, v68
	v_mul_f32_e64 v25, v27, v69
	v_fma_f32 v20, v20, v66, v18
	v_fma_f32 v21, v21, v67, v19
	v_fma_f32 v18, v22, v64, v24
	v_fma_f32 v19, v23, v65, v25
	v_cvt_pk_bf16_f32 v16, v16, v17
	v_cvt_pk_bf16_f32 v17, v28, v29
	s_nop 0
	v_cvt_pk_bf16_f32 v18, v18, v19
	v_cvt_pk_bf16_f32 v19, v20, v21
.LBB0_1373:
	s_and_b64 s[2:3], s[90:91], exec
	v_readlane_b32 s2, v249, 49
	v_readlane_b32 s3, v249, 51
	s_cselect_b32 s3, s2, s3
	v_readlane_b32 s2, v249, 48
	v_readlane_b32 s4, v249, 50
	v_ashrrev_i32_e32 v107, 31, v106
	s_cselect_b32 s2, s2, s4
	s_cselect_b32 s4, 12, 10
	v_lshlrev_b64 v[20:21], s4, v[106:107]
	s_cselect_b32 s17, s34, s30
	s_cselect_b32 s16, s31, s81
	v_lshl_add_u64 v[20:21], s[2:3], 0, v[20:21]
	v_lshl_add_u64 v[20:21], s[16:17], 1, v[20:21]
	v_lshl_add_u64 v[20:21], v[172:173], 1, v[20:21]
	v_mov_b32_e32 v171, v170
	global_store_dwordx4 v[20:21], v[16:19], off
	v_mul_f32_e64 v24, v8, v170
	v_mul_f32_e64 v25, v9, v171
	v_mul_f32_e64 v28, v12, v170
	v_mul_f32_e64 v29, v13, v171
	v_mov_b32_e32 v16, v170
	v_mov_b32_e32 v17, v170
	v_mul_f32_e64 v22, v10, v16
	v_mul_f32_e64 v23, v11, v17
	v_mul_f32_e64 v26, v14, v16
	v_mul_f32_e64 v27, v15, v17
	s_and_b64 vcc, exec, s[0:1]
	s_mov_b64 s[0:1], -1
	s_cbranch_vccnz .LBB0_1375
	s_mov_b64 s[0:1], 0
	v_cvt_pk_bf16_f32 v16, v24, v25
	v_cvt_pk_bf16_f32 v17, v22, v23
	v_cvt_pk_bf16_f32 v18, v28, v29
	v_cvt_pk_bf16_f32 v19, v26, v27
.LBB0_1375:
	s_andn2_b64 vcc, exec, s[0:1]
	s_cbranch_vccnz .LBB0_1377
	s_waitcnt vmcnt(0)
	v_mul_f32_e64 v16, v26, v66
	v_mul_f32_e64 v17, v27, v67
	v_mul_f32_e64 v18, v28, v64
	v_mul_f32_e64 v19, v29, v65
	v_fma_f32 v30, v22, v70, -v16
	v_fma_f32 v31, v23, v71, -v17
	v_fma_f32 v16, v24, v68, -v18
	v_fma_f32 v17, v25, v69, -v19
	v_mul_f32_e64 v18, v26, v70
	v_mul_f32_e64 v19, v27, v71
	v_mul_f32_e64 v26, v28, v68
	v_mul_f32_e64 v27, v29, v69
	v_fma_f32 v22, v22, v66, v18
	v_fma_f32 v23, v23, v67, v19
	v_fma_f32 v18, v24, v64, v26
	v_fma_f32 v19, v25, v65, v27
	v_cvt_pk_bf16_f32 v16, v16, v17
	v_cvt_pk_bf16_f32 v17, v30, v31
	s_nop 0
	v_cvt_pk_bf16_f32 v18, v18, v19
	v_cvt_pk_bf16_f32 v19, v22, v23

; __device__ __forceinline__ f32x4 sigmoid4(const f32x4& x, float s) {
;     f32x4 z = x * (s * -1.4426950408889634f), e;
; #pragma unroll
;     for (int j = 0; j < 4; ++j) e[j] = __builtin_amdgcn_exp2f(z[j]);
;     e = e + 1.0f;
; #pragma unroll
;     for (int j = 0; j < 4; ++j) e[j] = __builtin_amdgcn_rcpf(e[j]);
;     return e;
; }
;     __device__ __forceinline__ void operator()(const f32x4 (&acc)[2][2][4][2], const Unit& u, int wr, int wc, int fr, int fq, const Pre&) const {
;     ...
;                 } else if (kind == KD_A) {
;                     st_bf16x8(abuf + (size_t)row * DM + 128 * (pn - TL_A) + cw, acc[ai][0][m][0] * rs * sigmoid4(acc[ai][1][m][0], rs), acc[ai][0][m][1] * rs * sigmoid4(acc[ai][1][m][1], rs));
.LBB0_1382:
	v_ashrrev_i32_e32 v107, 31, v106
	v_lshlrev_b64 v[16:17], 12, v[106:107]
	v_lshl_add_u64 v[16:17], s[12:13], 0, v[16:17]
	v_lshl_add_u64 v[16:17], s[88:89], 1, v[16:17]
	v_mul_f32_e32 v27, 0xbfb8aa3b, v170
	v_lshl_add_u64 v[20:21], v[172:173], 1, v[16:17]
	v_mul_f32_e32 v16, v8, v27
	v_mul_f32_e32 v17, v9, v27
	v_mul_f32_e32 v18, v10, v27
	v_mul_f32_e32 v19, v11, v27
	v_exp_f32_e32 v16, v16
	v_exp_f32_e32 v18, v18
	v_exp_f32_e32 v19, v19
	v_exp_f32_e32 v17, v17
	v_mul_f32_e32 v26, v12, v27
	v_mul_f32_e32 v30, v13, v27
	v_add_f32_e64 v18, v18, 1.0
	v_add_f32_e64 v19, v19, 1.0
	v_add_f32_e64 v16, v16, 1.0
	v_add_f32_e64 v17, v17, 1.0
	v_mul_f32_e32 v28, v14, v27
	v_mul_f32_e32 v27, v15, v27
	v_rcp_f32_e32 v16, v16
	v_rcp_f32_e32 v17, v17
	v_rcp_f32_e32 v18, v18
	v_rcp_f32_e32 v19, v19
	v_exp_f32_e32 v26, v26
	v_exp_f32_e32 v28, v28
	v_exp_f32_e32 v29, v27
	v_exp_f32_e32 v27, v30
	v_mul_f32_e64 v22, v6, v170
	v_mul_f32_e64 v23, v7, v170
	v_mul_f32_e64 v24, v4, v170
	v_mul_f32_e64 v25, v5, v170
	v_mul_f32_e64 v18, v22, v18
	v_mul_f32_e64 v19, v23, v19
	v_mul_f32_e64 v16, v24, v16
	v_mul_f32_e64 v17, v25, v17
	v_add_f32_e64 v22, v28, 1.0
	v_add_f32_e64 v23, v29, 1.0
	v_add_f32_e64 v24, v26, 1.0
	v_add_f32_e64 v25, v27, 1.0
	v_rcp_f32_e32 v22, v22
	v_rcp_f32_e32 v24, v24
	v_rcp_f32_e32 v23, v23
	v_rcp_f32_e32 v25, v25
	v_mul_f32_e64 v26, v2, v170
	v_mul_f32_e64 v27, v3, v170
	v_mul_f32_e64 v28, v0, v170
	v_mul_f32_e64 v29, v1, v170
	v_mul_f32_e64 v22, v26, v22
	v_mul_f32_e64 v23, v27, v23
	v_mul_f32_e64 v24, v28, v24
	v_mul_f32_e64 v25, v29, v25
	v_cvt_pk_bf16_f32 v16, v16, v17
	v_cvt_pk_bf16_f32 v17, v18, v19
	s_nop 0
	v_cvt_pk_bf16_f32 v18, v24, v25
	v_cvt_pk_bf16_f32 v19, v22, v23
	global_store_dwordx4 v[20:21], v[16:19], off

; #define LAS __attribute__((address_space(3)))
; #define IX_RELU(x) __int_as_float(max(__float_as_int(x), 0))
; __device__ __forceinline__ void indexer_phase(const Frame& F, const bf16_t* QI, const bf16_t* KI, const float* WI, unsigned* MASK, const pg8::SideConv& SD) {
;     ...
;                     for (int p2 = 0; p2 < 2; ++p2) {
;                         const int k0 = g * 4 + 2 * p2, kt0 = c * 8 + k0;
;                         f32x16 a0 = {}, a1 = {};
; #pragma unroll
;                         for (int s = 0; s < 4; ++s) {
;                             const bf16x8 b0 = *(const LAS bf16x8*)(kb + k0 * 4096 + boff[s]), b1 = *(const LAS bf16x8*)(kb + (k0 + 1) * 4096 + boff[s]);
;                             a0 = __builtin_amdgcn_mfma_f32_32x32x16_bf16(afr[s], b0, a0, 0, 0, 0); a1 = __builtin_amdgcn_mfma_f32_32x32x16_bf16(afr[s], b1, a1, 0, 0, 0); }
;     ...
;                         f32x2 q0 = {0.f, 0.f}, q1 = {0.f, 0.f};
; #pragma unroll
;                         for (int h = 0; h < 16; h += 2) {
;                             const f32x2 ww = {wv[h >> 2][h & 3], wv[h >> 2][(h & 3) + 1]};
;                             const f32x2 r0 = {IX_RELU(a0[h]), IX_RELU(a0[h + 1])};
;                             const f32x2 r1 = {IX_RELU(a1[h]), IX_RELU(a1[h + 1])};
;                             q0 = ww * r0 + q0; q1 = ww * r1 + q1; }
;                         s4[2 * p2] = (kt0 * 32 + r <= tq) ? (q0[0] + q0[1]) : NEG;
;                         s4[2 * p2 + 1] = ((kt0 + 1) * 32 + r <= tq) ? (q1[0] + q1[1]) : NEG;
;     ...
;                     }
.LBB0_1470:
	s_and_b32 s16, s14, 0x8000
	s_add_i32 s16, s16, 0
	s_add_i32 s17, s61, -4
	v_mov_b32_e32 v0, 0xff800000
	s_cmp_ge_u32 s17, s56
	v_add_u32_e32 v237, s16, v225
	v_add_u32_e32 v236, s16, v226
	v_add_u32_e32 v235, s16, v227
	v_add_u32_e32 v234, s16, v228
	v_mov_b32_e32 v1, 0xff800000
	v_mov_b32_e32 v238, 0xff800000
	v_mov_b32_e32 v239, 0xff800000
	s_cbranch_scc1 .LBB0_1472
	ds_read_b128 v[0:3], v237
	ds_read_b128 v[16:19], v237 offset:4096
	ds_read_b128 v[238:241], v236
	ds_read_b128 v[242:245], v236 offset:4096
	v_cmp_le_i32_e32 vcc, v215, v214
	s_waitcnt lgkmcnt(0)
	v_mfma_f32_32x32x16_bf16 v[0:15], v[32:35], v[0:3], 0
	v_mfma_f32_32x32x16_bf16 v[16:31], v[32:35], v[16:19], 0
	v_mfma_f32_32x32x16_bf16 v[0:15], v[36:39], v[238:241], v[0:15]
	v_mfma_f32_32x32x16_bf16 v[16:31], v[36:39], v[242:245], v[16:31]
	ds_read_b128 v[238:241], v235
	ds_read_b128 v[242:245], v235 offset:4096
	s_waitcnt lgkmcnt(0)
	v_mfma_f32_32x32x16_bf16 v[0:15], v[40:43], v[238:241], v[0:15]
	v_mfma_f32_32x32x16_bf16 v[16:31], v[40:43], v[242:245], v[16:31]
	ds_read_b128 v[238:241], v234
	ds_read_b128 v[242:245], v234 offset:4096
	s_waitcnt lgkmcnt(0)
	v_mfma_f32_32x32x16_bf16 v[0:15], v[44:47], v[238:241], v[0:15]
	v_mfma_f32_32x32x16_bf16 v[16:31], v[44:47], v[242:245], v[16:31]
	s_nop 10
	v_max_i32_e32 v0, 0, v0
	v_max_i32_e32 v1, 0, v1
	v_fma_f32 v0, v60, v0, 0
	v_fma_f32 v1, v61, v1, 0
	v_max_i32_e32 v2, 0, v2
	v_max_i32_e32 v3, 0, v3
	v_fma_f32 v0, v62, v2, v0
	v_fma_f32 v1, v63, v3, v1
	v_max_i32_e32 v4, 0, v4
	v_max_i32_e32 v16, 0, v16
	v_max_i32_e32 v17, 0, v17
	v_fma_f32 v16, v60, v16, 0
	v_fma_f32 v17, v61, v17, 0
	v_max_i32_e32 v18, 0, v18
	v_max_i32_e32 v19, 0, v19
	v_fma_f32 v2, v62, v18, v16
	v_fma_f32 v3, v63, v19, v17
	v_max_i32_e32 v5, 0, v5
	v_max_i32_e32 v16, 0, v20
	v_max_i32_e32 v17, 0, v21
	v_fma_f32 v0, v56, v4, v0
	v_fma_f32 v1, v57, v5, v1
	v_fma_f32 v2, v56, v16, v2
	v_fma_f32 v3, v57, v17, v3
	v_max_i32_e32 v4, 0, v6
	v_max_i32_e32 v5, 0, v7
	v_max_i32_e32 v6, 0, v22
	v_max_i32_e32 v7, 0, v23
	v_fma_f32 v0, v58, v4, v0
	v_fma_f32 v1, v59, v5, v1
	v_fma_f32 v2, v58, v6, v2
	v_fma_f32 v3, v59, v7, v3
	v_max_i32_e32 v4, 0, v8
	v_max_i32_e32 v5, 0, v9
	v_max_i32_e32 v6, 0, v24
	v_max_i32_e32 v7, 0, v25
	v_fma_f32 v0, v52, v4, v0
	v_fma_f32 v1, v53, v5, v1
	v_fma_f32 v2, v52, v6, v2
	v_fma_f32 v3, v53, v7, v3
	v_max_i32_e32 v4, 0, v10
	v_max_i32_e32 v5, 0, v11
	v_max_i32_e32 v6, 0, v26
	v_max_i32_e32 v7, 0, v27
	v_fma_f32 v0, v54, v4, v0
	v_fma_f32 v1, v55, v5, v1
	v_fma_f32 v2, v54, v6, v2
	v_fma_f32 v3, v55, v7, v3
	v_max_i32_e32 v4, 0, v12
	v_max_i32_e32 v5, 0, v13
	v_max_i32_e32 v6, 0, v28
	v_max_i32_e32 v7, 0, v29
	v_fma_f32 v0, v48, v4, v0
	v_fma_f32 v1, v49, v5, v1
	v_fma_f32 v2, v48, v6, v2
	v_fma_f32 v3, v49, v7, v3
	v_max_i32_e32 v4, 0, v14
	v_max_i32_e32 v5, 0, v15
	v_max_i32_e32 v6, 0, v30
	v_max_i32_e32 v7, 0, v31
	v_fma_f32 v0, v50, v4, v0
	v_fma_f32 v1, v51, v5, v1
	v_fma_f32 v2, v50, v6, v2
	v_fma_f32 v3, v51, v7, v3
	v_mov_b32_e32 v4, v0
	v_mov_b32_e32 v5, v2
	v_mov_b32_e32 v2, v1
	v_add_u32_e32 v6, 32, v215
	v_add_f32_e32 v0, v4, v2
	v_add_f32_e32 v1, v5, v3
	s_nop 0
	v_cndmask_b32_e32 v238, v229, v0, vcc
	v_cmp_le_i32_e32 vcc, v6, v65
	s_nop 1
	v_cndmask_b32_e32 v239, v229, v1, vcc
	ds_read_b128 v[0:3], v237 offset:8192
	ds_read_b128 v[16:19], v237 offset:12288
	s_waitcnt lgkmcnt(0)
	v_mfma_f32_32x32x16_bf16 v[0:15], v[32:35], v[0:3], 0
	ds_read_b128 v[240:243], v236 offset:8192
	ds_read_b128 v[244:247], v236 offset:12288
	v_mfma_f32_32x32x16_bf16 v[16:31], v[32:35], v[16:19], 0
	s_waitcnt lgkmcnt(0)
	v_mfma_f32_32x32x16_bf16 v[0:15], v[36:39], v[240:243], v[0:15]
	v_mfma_f32_32x32x16_bf16 v[16:31], v[36:39], v[244:247], v[16:31]
	ds_read_b128 v[240:243], v235 offset:8192
	ds_read_b128 v[244:247], v235 offset:12288
	s_waitcnt lgkmcnt(0)
	v_mfma_f32_32x32x16_bf16 v[0:15], v[40:43], v[240:243], v[0:15]
	v_mfma_f32_32x32x16_bf16 v[16:31], v[40:43], v[244:247], v[16:31]
	ds_read_b128 v[240:243], v234 offset:8192
	ds_read_b128 v[244:247], v234 offset:12288
	s_waitcnt lgkmcnt(0)
	v_mfma_f32_32x32x16_bf16 v[0:15], v[44:47], v[240:243], v[0:15]
	v_mfma_f32_32x32x16_bf16 v[16:31], v[44:47], v[244:247], v[16:31]
	s_nop 10
	v_max_i32_e32 v0, 0, v0
	v_max_i32_e32 v1, 0, v1
	v_fma_f32 v0, v60, v0, 0
	v_fma_f32 v1, v61, v1, 0
	v_max_i32_e32 v2, 0, v2
	v_max_i32_e32 v3, 0, v3
	v_fma_f32 v0, v62, v2, v0
	v_fma_f32 v1, v63, v3, v1
	v_max_i32_e32 v4, 0, v4
	v_max_i32_e32 v16, 0, v16
	v_max_i32_e32 v17, 0, v17
	v_fma_f32 v16, v60, v16, 0
	v_fma_f32 v17, v61, v17, 0
	v_max_i32_e32 v18, 0, v18
	v_max_i32_e32 v19, 0, v19
	v_fma_f32 v2, v62, v18, v16
	v_fma_f32 v3, v63, v19, v17
	v_max_i32_e32 v5, 0, v5
	v_max_i32_e32 v16, 0, v20
	v_max_i32_e32 v17, 0, v21
	v_fma_f32 v0, v56, v4, v0
	v_fma_f32 v1, v57, v5, v1
	v_fma_f32 v2, v56, v16, v2
	v_fma_f32 v3, v57, v17, v3
	v_max_i32_e32 v4, 0, v6
	v_max_i32_e32 v5, 0, v7
	v_max_i32_e32 v6, 0, v22
	v_max_i32_e32 v7, 0, v23
	v_fma_f32 v0, v58, v4, v0
	v_fma_f32 v1, v59, v5, v1
	v_fma_f32 v2, v58, v6, v2
	v_fma_f32 v3, v59, v7, v3
	v_max_i32_e32 v4, 0, v8
	v_max_i32_e32 v5, 0, v9
	v_max_i32_e32 v6, 0, v24
	v_max_i32_e32 v7, 0, v25
	v_fma_f32 v0, v52, v4, v0
	v_fma_f32 v1, v53, v5, v1
	v_fma_f32 v2, v52, v6, v2
	v_fma_f32 v3, v53, v7, v3
	v_max_i32_e32 v4, 0, v10
	v_max_i32_e32 v5, 0, v11
	v_max_i32_e32 v6, 0, v26
	v_max_i32_e32 v7, 0, v27
	v_fma_f32 v0, v54, v4, v0
	v_fma_f32 v1, v55, v5, v1
	v_fma_f32 v2, v54, v6, v2
	v_fma_f32 v3, v55, v7, v3
	v_max_i32_e32 v4, 0, v12
	v_max_i32_e32 v5, 0, v13
	v_max_i32_e32 v6, 0, v28
	v_max_i32_e32 v7, 0, v29
	v_fma_f32 v0, v48, v4, v0
	v_fma_f32 v1, v49, v5, v1
	v_fma_f32 v2, v48, v6, v2
	v_fma_f32 v3, v49, v7, v3
	v_max_i32_e32 v4, 0, v14
	v_max_i32_e32 v5, 0, v15
	v_max_i32_e32 v6, 0, v30
	v_max_i32_e32 v7, 0, v31
	v_fma_f32 v0, v50, v4, v0
	v_fma_f32 v1, v51, v5, v1
	v_fma_f32 v2, v50, v6, v2
	v_fma_f32 v3, v51, v7, v3
	v_or_b32_e32 v7, 64, v215
	v_mov_b32_e32 v4, v0
	v_mov_b32_e32 v5, v2
	v_mov_b32_e32 v2, v1
	v_or_b32_e32 v6, 0x60, v215
	v_add_f32_e32 v0, v4, v2
	v_add_f32_e32 v1, v5, v3
	v_cmp_le_i32_e32 vcc, v7, v214
	s_nop 1
	v_cndmask_b32_e32 v0, v229, v0, vcc
	v_cmp_le_i32_e32 vcc, v6, v65
	s_nop 1
	v_cndmask_b32_e32 v1, v229, v1, vcc

; #define LAS __attribute__((address_space(3)))
; #define IX_RELU(x) __int_as_float(max(__float_as_int(x), 0))
; __device__ __forceinline__ void indexer_phase(const Frame& F, const bf16_t* QI, const bf16_t* KI, const float* WI, unsigned* MASK, const pg8::SideConv& SD) {
;     ...
;                     for (int p2 = 0; p2 < 2; ++p2) {
;                         const int k0 = g * 4 + 2 * p2, kt0 = c * 8 + k0;
;                         f32x16 a0 = {}, a1 = {};
; #pragma unroll
;                         for (int s = 0; s < 4; ++s) {
;                             const bf16x8 b0 = *(const LAS bf16x8*)(kb + k0 * 4096 + boff[s]), b1 = *(const LAS bf16x8*)(kb + (k0 + 1) * 4096 + boff[s]);
;                             a0 = __builtin_amdgcn_mfma_f32_32x32x16_bf16(afr[s], b0, a0, 0, 0, 0); a1 = __builtin_amdgcn_mfma_f32_32x32x16_bf16(afr[s], b1, a1, 0, 0, 0); }
;     ...
;                         f32x2 q0 = {0.f, 0.f}, q1 = {0.f, 0.f};
; #pragma unroll
;                         for (int h = 0; h < 16; h += 2) {
;                             const f32x2 ww = {wv[h >> 2][h & 3], wv[h >> 2][(h & 3) + 1]};
;                             const f32x2 r0 = {IX_RELU(a0[h]), IX_RELU(a0[h + 1])};
;                             const f32x2 r1 = {IX_RELU(a1[h]), IX_RELU(a1[h + 1])};
;                             q0 = ww * r0 + q0; q1 = ww * r1 + q1; }
;                         s4[2 * p2] = (kt0 * 32 + r <= tq) ? (q0[0] + q0[1]) : NEG;
;                         s4[2 * p2 + 1] = ((kt0 + 1) * 32 + r <= tq) ? (q1[0] + q1[1]) : NEG;
;     ...
;                     }
.LBB0_1536:
	v_mov_b32_e32 v0, 0xff800000
	s_cmp_ge_u32 s61, s56
	v_mov_b32_e32 v1, 0xff800000
	v_mov_b32_e32 v238, 0xff800000
	v_mov_b32_e32 v239, 0xff800000
	s_cbranch_scc1 .LBB0_1538
	ds_read_b128 v[0:3], v237 offset:16384
	ds_read_b128 v[16:19], v237 offset:20480
	ds_read_b128 v[238:241], v236 offset:16384
	ds_read_b128 v[242:245], v236 offset:20480
	s_waitcnt lgkmcnt(0)
	v_mfma_f32_32x32x16_bf16 v[0:15], v[32:35], v[0:3], 0
	v_mfma_f32_32x32x16_bf16 v[16:31], v[32:35], v[16:19], 0
	v_mfma_f32_32x32x16_bf16 v[0:15], v[36:39], v[238:241], v[0:15]
	v_mfma_f32_32x32x16_bf16 v[16:31], v[36:39], v[242:245], v[16:31]
	ds_read_b128 v[238:241], v235 offset:16384
	ds_read_b128 v[242:245], v235 offset:20480
	s_waitcnt lgkmcnt(0)
	v_mfma_f32_32x32x16_bf16 v[0:15], v[40:43], v[238:241], v[0:15]
	v_mfma_f32_32x32x16_bf16 v[16:31], v[40:43], v[242:245], v[16:31]
	ds_read_b128 v[238:241], v234 offset:16384
	ds_read_b128 v[242:245], v234 offset:20480
	s_waitcnt lgkmcnt(0)
	v_mfma_f32_32x32x16_bf16 v[0:15], v[44:47], v[238:241], v[0:15]
	v_mfma_f32_32x32x16_bf16 v[16:31], v[44:47], v[242:245], v[16:31]
	s_nop 10
	v_max_i32_e32 v0, 0, v0
	v_max_i32_e32 v1, 0, v1
	v_fma_f32 v0, v60, v0, 0
	v_fma_f32 v1, v61, v1, 0
	v_max_i32_e32 v2, 0, v2
	v_max_i32_e32 v3, 0, v3
	v_fma_f32 v0, v62, v2, v0
	v_fma_f32 v1, v63, v3, v1
	v_max_i32_e32 v4, 0, v4
	v_max_i32_e32 v16, 0, v16
	v_max_i32_e32 v17, 0, v17
	v_fma_f32 v16, v60, v16, 0
	v_fma_f32 v17, v61, v17, 0
	v_max_i32_e32 v18, 0, v18
	v_max_i32_e32 v19, 0, v19
	v_fma_f32 v2, v62, v18, v16
	v_fma_f32 v3, v63, v19, v17
	v_max_i32_e32 v5, 0, v5
	v_max_i32_e32 v16, 0, v20
	v_max_i32_e32 v17, 0, v21
	v_fma_f32 v0, v56, v4, v0
	v_fma_f32 v1, v57, v5, v1
	v_fma_f32 v2, v56, v16, v2
	v_fma_f32 v3, v57, v17, v3
	v_max_i32_e32 v4, 0, v6
	v_max_i32_e32 v5, 0, v7
	v_max_i32_e32 v6, 0, v22
	v_max_i32_e32 v7, 0, v23
	v_fma_f32 v0, v58, v4, v0
	v_fma_f32 v1, v59, v5, v1
	v_fma_f32 v2, v58, v6, v2
	v_fma_f32 v3, v59, v7, v3
	v_max_i32_e32 v4, 0, v8
	v_max_i32_e32 v5, 0, v9
	v_max_i32_e32 v6, 0, v24
	v_max_i32_e32 v7, 0, v25
	v_fma_f32 v0, v52, v4, v0
	v_fma_f32 v1, v53, v5, v1
	v_fma_f32 v2, v52, v6, v2
	v_fma_f32 v3, v53, v7, v3
	v_max_i32_e32 v4, 0, v10
	v_max_i32_e32 v5, 0, v11
	v_max_i32_e32 v6, 0, v26
	v_max_i32_e32 v7, 0, v27
	v_fma_f32 v0, v54, v4, v0
	v_fma_f32 v1, v55, v5, v1
	v_fma_f32 v2, v54, v6, v2
	v_fma_f32 v3, v55, v7, v3
	v_max_i32_e32 v4, 0, v12
	v_max_i32_e32 v5, 0, v13
	v_max_i32_e32 v6, 0, v28
	v_max_i32_e32 v7, 0, v29
	v_fma_f32 v0, v48, v4, v0
	v_fma_f32 v1, v49, v5, v1
	v_fma_f32 v2, v48, v6, v2
	v_fma_f32 v3, v49, v7, v3
	v_max_i32_e32 v4, 0, v14
	v_max_i32_e32 v5, 0, v15
	v_max_i32_e32 v6, 0, v30
	v_max_i32_e32 v7, 0, v31
	v_fma_f32 v0, v50, v4, v0
	v_fma_f32 v1, v51, v5, v1
	v_fma_f32 v2, v50, v6, v2
	v_fma_f32 v3, v51, v7, v3
	v_or_b32_e32 v7, 0x80, v215
	v_mov_b32_e32 v4, v0
	v_mov_b32_e32 v5, v2
	v_mov_b32_e32 v2, v1
	v_or_b32_e32 v6, 0xa0, v215
	v_add_f32_e32 v0, v4, v2
	v_add_f32_e32 v1, v5, v3
	v_cmp_le_i32_e32 vcc, v7, v214
	s_nop 1
	v_cndmask_b32_e32 v238, v229, v0, vcc
	v_cmp_le_i32_e32 vcc, v6, v65
	s_nop 1
	v_cndmask_b32_e32 v239, v229, v1, vcc
	ds_read_b128 v[0:3], v237 offset:24576
	ds_read_b128 v[16:19], v237 offset:28672
	s_waitcnt lgkmcnt(0)
	v_mfma_f32_32x32x16_bf16 v[0:15], v[32:35], v[0:3], 0
	ds_read_b128 v[240:243], v236 offset:24576
	ds_read_b128 v[244:247], v236 offset:28672
	v_mfma_f32_32x32x16_bf16 v[16:31], v[32:35], v[16:19], 0
	s_waitcnt lgkmcnt(0)
	v_mfma_f32_32x32x16_bf16 v[0:15], v[36:39], v[240:243], v[0:15]
	v_mfma_f32_32x32x16_bf16 v[16:31], v[36:39], v[244:247], v[16:31]
	ds_read_b128 v[240:243], v235 offset:24576
	ds_read_b128 v[244:247], v235 offset:28672
	s_waitcnt lgkmcnt(0)
	v_mfma_f32_32x32x16_bf16 v[0:15], v[40:43], v[240:243], v[0:15]
	ds_read_b128 v[240:243], v234 offset:24576
	ds_read_b128 v[234:237], v234 offset:28672
	v_mfma_f32_32x32x16_bf16 v[16:31], v[40:43], v[244:247], v[16:31]
	s_waitcnt lgkmcnt(0)
	v_mfma_f32_32x32x16_bf16 v[0:15], v[44:47], v[240:243], v[0:15]
	v_mfma_f32_32x32x16_bf16 v[16:31], v[44:47], v[234:237], v[16:31]
	s_nop 10
	v_max_i32_e32 v0, 0, v0
	v_max_i32_e32 v1, 0, v1
	v_fma_f32 v0, v60, v0, 0
	v_fma_f32 v1, v61, v1, 0
	v_max_i32_e32 v2, 0, v2
	v_max_i32_e32 v3, 0, v3
	v_fma_f32 v0, v62, v2, v0
	v_fma_f32 v1, v63, v3, v1
	v_max_i32_e32 v4, 0, v4
	v_max_i32_e32 v16, 0, v16
	v_max_i32_e32 v17, 0, v17
	v_fma_f32 v16, v60, v16, 0
	v_fma_f32 v17, v61, v17, 0
	v_max_i32_e32 v18, 0, v18
	v_max_i32_e32 v19, 0, v19
	v_fma_f32 v2, v62, v18, v16
	v_fma_f32 v3, v63, v19, v17
	v_max_i32_e32 v5, 0, v5
	v_max_i32_e32 v16, 0, v20
	v_max_i32_e32 v17, 0, v21
	v_fma_f32 v0, v56, v4, v0
	v_fma_f32 v1, v57, v5, v1
	v_fma_f32 v2, v56, v16, v2
	v_fma_f32 v3, v57, v17, v3
	v_max_i32_e32 v4, 0, v6
	v_max_i32_e32 v5, 0, v7
	v_max_i32_e32 v6, 0, v22
	v_max_i32_e32 v7, 0, v23
	v_fma_f32 v0, v58, v4, v0
	v_fma_f32 v1, v59, v5, v1
	v_fma_f32 v2, v58, v6, v2
	v_fma_f32 v3, v59, v7, v3
	v_max_i32_e32 v4, 0, v8
	v_max_i32_e32 v5, 0, v9
	v_max_i32_e32 v6, 0, v24
	v_max_i32_e32 v7, 0, v25
	v_fma_f32 v0, v52, v4, v0
	v_fma_f32 v1, v53, v5, v1
	v_fma_f32 v2, v52, v6, v2
	v_fma_f32 v3, v53, v7, v3
	v_max_i32_e32 v4, 0, v10
	v_max_i32_e32 v5, 0, v11
	v_max_i32_e32 v6, 0, v26
	v_max_i32_e32 v7, 0, v27
	v_fma_f32 v0, v54, v4, v0
	v_fma_f32 v1, v55, v5, v1
	v_fma_f32 v2, v54, v6, v2
	v_fma_f32 v3, v55, v7, v3
	v_max_i32_e32 v4, 0, v12
	v_max_i32_e32 v5, 0, v13
	v_max_i32_e32 v6, 0, v28
	v_max_i32_e32 v7, 0, v29
	v_fma_f32 v0, v48, v4, v0
	v_fma_f32 v1, v49, v5, v1
	v_fma_f32 v2, v48, v6, v2
	v_fma_f32 v3, v49, v7, v3
	v_max_i32_e32 v4, 0, v14
	v_max_i32_e32 v5, 0, v15
	v_max_i32_e32 v6, 0, v30
	v_max_i32_e32 v7, 0, v31
	v_fma_f32 v0, v50, v4, v0
	v_fma_f32 v1, v51, v5, v1
	v_fma_f32 v2, v50, v6, v2
	v_fma_f32 v3, v51, v7, v3
	v_or_b32_e32 v7, 0xc0, v215
	v_mov_b32_e32 v4, v0
	v_mov_b32_e32 v5, v2
	v_mov_b32_e32 v2, v1
	v_or_b32_e32 v6, 0xe0, v215
	v_add_f32_e32 v0, v4, v2
	v_add_f32_e32 v1, v5, v3
	v_cmp_le_i32_e32 vcc, v7, v214
	s_nop 1
	v_cndmask_b32_e32 v0, v229, v0, vcc
	v_cmp_le_i32_e32 vcc, v6, v65
	s_nop 1
	v_cndmask_b32_e32 v1, v229, v1, vcc

; __device__ __forceinline__ void indexer_phase(const Frame& F, const bf16_t* QI, const bf16_t* KI, const float* WI, unsigned* MASK, const pg8::SideConv& SD) {
;     ...
;             for (int it = 0; it < 64 && __any(!done); ++it) {
;                 const unsigned ul = __float_as_uint(lo), uh = __float_as_uint(hiv);
;                 const unsigned kl = (ul & 0x80000000u) ? ~ul : (ul | 0x80000000u), kh = (uh & 0x80000000u) ? ~uh : (uh | 0x80000000u);
;                 const bool adj = (kh - kl) <= 1u;
;                 const unsigned km = kl + ((kh - kl) >> 1);
;                 const float kmid = __uint_as_float((km & 0x80000000u) ? (km ^ 0x80000000u) : ~km);
;                 const float fmid = 0.5f * (lo + hiv);
;                 const float mid = (it < 24 && fmid > lo && fmid < hiv) ? fmid : kmid;
;                 const float piv = adj ? hiv : mid;
;                 int lt = 0; const f32x2 pv2 = {piv, piv};
; #pragma unroll
;                 for (int gq = 0; gq < 4; ++gq) {
;                     unsigned bits = 0u;
;                     if (gq * 4 < nch) {
; #pragma unroll
;                     for (int cc = 0; cc < 4; ++cc) { const int c = gq * 4 + cc;
; #pragma unroll
;                         for (int k = 0; k < 8; k += 2) { const f32x2 d = (f32x2){sc[c * 8 + k], sc[c * 8 + k + 1]} - pv2;
;                             bits = __builtin_amdgcn_alignbit(bits, __float_as_uint(d[0]), 31); bits = __builtin_amdgcn_alignbit(bits, __float_as_uint(d[1]), 31); } }
;                     lt += 32 - __popc(bits); }
;                 }
.LBB0_1670:
	v_cmp_eq_u32_e64 s[16:17], 0, v0
	s_mov_b64 vcc, s[16:17]
	s_cbranch_vccz .LBB0_1686
	v_not_b32_e32 v0, v5
	v_or_b32_e32 v1, 0x80000000, v5
	v_cmp_gt_i32_e32 vcc, 0, v5
	v_or_b32_e32 v7, 0x80000000, v6
	s_cmp_lt_u32 s85, 24
	v_cndmask_b32_e32 v0, v1, v0, vcc
	v_not_b32_e32 v1, v6
	v_cmp_gt_i32_e32 vcc, 0, v6
	s_cselect_b64 s[64:65], -1, 0
	v_mov_b32_e32 v8, 0
	v_cndmask_b32_e32 v1, v7, v1, vcc
	v_sub_u32_e32 v1, v1, v0
	v_lshrrev_b32_e32 v7, 1, v1
	v_add_u32_e32 v0, v7, v0
	v_cmp_lt_i32_e32 vcc, -1, v0
	v_cmp_lt_u32_e64 s[14:15], 1, v1
	s_nop 0
	v_cndmask_b32_e64 v7, v232, -1, vcc
	v_xor_b32_e32 v0, v7, v0
	v_add_f32_e32 v7, v5, v6
	v_mul_f32_e32 v7, 0.5, v7
	v_cmp_gt_f32_e32 vcc, v7, v5
	s_and_b64 s[64:65], s[64:65], vcc
	v_cmp_lt_f32_e32 vcc, v7, v6
	s_and_b64 vcc, s[64:65], vcc
	s_nop 0
	v_cndmask_b32_e32 v7, v0, v7, vcc
	v_cmp_gt_u32_e32 vcc, 2, v1
	s_nop 1
	v_cndmask_b32_e32 v0, v7, v6, vcc
	s_andn2_b64 vcc, exec, s[54:55]
	v_mov_b32_e32 v1, v0
	s_cbranch_vccnz .LBB0_1675
	v_sub_f32_e32 v8, v212, v0
	v_sub_f32_e32 v9, v213, v1
	v_lshrrev_b32_e32 v8, 31, v8
	v_alignbit_b32 v10, v8, v9, 31
	v_sub_f32_e32 v8, v210, v0
	v_sub_f32_e32 v9, v211, v1
	v_alignbit_b32 v8, v10, v8, 31
	v_alignbit_b32 v10, v8, v9, 31
	v_sub_f32_e32 v8, v208, v0
	v_sub_f32_e32 v9, v209, v1
	v_alignbit_b32 v8, v10, v8, 31
	v_alignbit_b32 v10, v8, v9, 31
	v_sub_f32_e32 v8, v206, v0
	v_sub_f32_e32 v9, v207, v1
	v_alignbit_b32 v8, v10, v8, 31
	v_alignbit_b32 v10, v8, v9, 31
	v_sub_f32_e32 v8, v204, v0
	v_sub_f32_e32 v9, v205, v1
	v_alignbit_b32 v8, v10, v8, 31
	v_alignbit_b32 v10, v8, v9, 31
	v_sub_f32_e32 v8, v202, v0
	v_sub_f32_e32 v9, v203, v1
	v_alignbit_b32 v8, v10, v8, 31
	v_alignbit_b32 v10, v8, v9, 31
	v_sub_f32_e32 v8, v200, v0
	v_sub_f32_e32 v9, v201, v1
	v_alignbit_b32 v8, v10, v8, 31
	v_alignbit_b32 v10, v8, v9, 31
	v_sub_f32_e32 v8, v198, v0
	v_sub_f32_e32 v9, v199, v1
	v_alignbit_b32 v8, v10, v8, 31
	v_alignbit_b32 v10, v8, v9, 31
	v_sub_f32_e32 v8, v196, v0
	v_sub_f32_e32 v9, v197, v1
	v_alignbit_b32 v8, v10, v8, 31
	v_alignbit_b32 v10, v8, v9, 31
	v_sub_f32_e32 v8, v194, v0
	v_sub_f32_e32 v9, v195, v1
	v_alignbit_b32 v8, v10, v8, 31
	v_alignbit_b32 v10, v8, v9, 31
	v_sub_f32_e32 v8, v192, v0
	v_sub_f32_e32 v9, v193, v1
	v_alignbit_b32 v8, v10, v8, 31
	v_alignbit_b32 v10, v8, v9, 31
	v_sub_f32_e32 v8, v190, v0
	v_sub_f32_e32 v9, v191, v1
	v_alignbit_b32 v8, v10, v8, 31
	v_alignbit_b32 v10, v8, v9, 31
	v_sub_f32_e32 v8, v188, v0
	v_sub_f32_e32 v9, v189, v1
	v_alignbit_b32 v8, v10, v8, 31
	v_alignbit_b32 v10, v8, v9, 31
	v_sub_f32_e32 v8, v186, v0
	v_sub_f32_e32 v9, v187, v1
	v_alignbit_b32 v8, v10, v8, 31
	v_alignbit_b32 v10, v8, v9, 31
	v_sub_f32_e32 v8, v184, v0
	v_sub_f32_e32 v9, v185, v1
	v_alignbit_b32 v8, v10, v8, 31
	v_alignbit_b32 v10, v8, v9, 31
	v_sub_f32_e32 v8, v182, v0
	v_sub_f32_e32 v9, v183, v1
	v_alignbit_b32 v8, v10, v8, 31
	v_alignbit_b32 v8, v8, v9, 31
	v_not_b32_e32 v8, v8
	v_bcnt_u32_b32 v8, v8, 0
	s_andn2_b64 vcc, exec, s[56:57]
	s_cbranch_vccz .LBB0_1676

; __device__ __forceinline__ void indexer_phase(const Frame& F, const bf16_t* QI, const bf16_t* KI, const float* WI, unsigned* MASK, const pg8::SideConv& SD) {
;     ...
;                 for (int gq = 0; gq < 4; ++gq) {
;                     unsigned bits = 0u;
;                     if (gq * 4 < nch) {
; #pragma unroll
;                     for (int cc = 0; cc < 4; ++cc) { const int c = gq * 4 + cc;
; #pragma unroll
;                         for (int k = 0; k < 8; k += 2) { const f32x2 d = (f32x2){sc[c * 8 + k], sc[c * 8 + k + 1]} - pv2;
;                             bits = __builtin_amdgcn_alignbit(bits, __float_as_uint(d[0]), 31); bits = __builtin_amdgcn_alignbit(bits, __float_as_uint(d[1]), 31); } }
;                     lt += 32 - __popc(bits); }
;                 }
.LBB0_1674:
	v_sub_f32_e32 v10, v148, v0
	v_sub_f32_e32 v11, v149, v1
	v_lshrrev_b32_e32 v9, 31, v10
	v_alignbit_b32 v9, v9, v11, 31
	v_sub_f32_e32 v10, v146, v0
	v_sub_f32_e32 v11, v147, v1
	v_alignbit_b32 v9, v9, v10, 31
	v_alignbit_b32 v9, v9, v11, 31
	v_sub_f32_e32 v10, v144, v0
	v_sub_f32_e32 v11, v145, v1
	v_alignbit_b32 v9, v9, v10, 31
	v_alignbit_b32 v9, v9, v11, 31
	v_sub_f32_e32 v10, v142, v0
	v_sub_f32_e32 v11, v143, v1
	v_alignbit_b32 v9, v9, v10, 31
	v_alignbit_b32 v9, v9, v11, 31
	v_sub_f32_e32 v10, v140, v0
	v_sub_f32_e32 v11, v141, v1
	v_alignbit_b32 v9, v9, v10, 31
	v_alignbit_b32 v9, v9, v11, 31
	v_sub_f32_e32 v10, v138, v0
	v_sub_f32_e32 v11, v139, v1
	v_alignbit_b32 v9, v9, v10, 31
	v_alignbit_b32 v9, v9, v11, 31
	v_sub_f32_e32 v10, v136, v0
	v_sub_f32_e32 v11, v137, v1
	v_alignbit_b32 v9, v9, v10, 31
	v_alignbit_b32 v9, v9, v11, 31
	v_sub_f32_e32 v10, v134, v0
	v_sub_f32_e32 v11, v135, v1
	v_alignbit_b32 v9, v9, v10, 31
	v_alignbit_b32 v9, v9, v11, 31
	v_sub_f32_e32 v10, v132, v0
	v_sub_f32_e32 v11, v133, v1
	v_alignbit_b32 v9, v9, v10, 31
	v_alignbit_b32 v9, v9, v11, 31
	v_sub_f32_e32 v10, v130, v0
	v_sub_f32_e32 v11, v131, v1
	v_alignbit_b32 v9, v9, v10, 31
	v_alignbit_b32 v9, v9, v11, 31
	v_sub_f32_e32 v10, v128, v0
	v_sub_f32_e32 v11, v129, v1
	v_alignbit_b32 v9, v9, v10, 31
	v_alignbit_b32 v9, v9, v11, 31
	v_sub_f32_e32 v10, v126, v0
	v_sub_f32_e32 v11, v127, v1
	v_alignbit_b32 v9, v9, v10, 31
	v_alignbit_b32 v9, v9, v11, 31
	v_sub_f32_e32 v10, v124, v0
	v_sub_f32_e32 v11, v125, v1
	v_alignbit_b32 v9, v9, v10, 31
	v_alignbit_b32 v9, v9, v11, 31
	v_sub_f32_e32 v10, v122, v0
	v_sub_f32_e32 v11, v123, v1
	v_alignbit_b32 v9, v9, v10, 31
	v_alignbit_b32 v9, v9, v11, 31
	v_sub_f32_e32 v10, v120, v0
	v_sub_f32_e32 v11, v121, v1
	v_alignbit_b32 v9, v9, v10, 31
	v_alignbit_b32 v9, v9, v11, 31
	v_sub_f32_e32 v10, v118, v0
	v_sub_f32_e32 v11, v119, v1
	v_alignbit_b32 v9, v9, v10, 31
	v_alignbit_b32 v9, v9, v11, 31
	v_not_b32_e32 v9, v9
	v_bcnt_u32_b32 v8, v9, v8
	s_andn2_b64 vcc, exec, s[60:61]
	s_cbranch_vccz .LBB0_1678
	s_branch .LBB0_1679

; __device__ __forceinline__ void indexer_phase(const Frame& F, const bf16_t* QI, const bf16_t* KI, const float* WI, unsigned* MASK, const pg8::SideConv& SD) {
;     ...
;                 for (int gq = 0; gq < 4; ++gq) {
;                     unsigned bits = 0u;
;                     if (gq * 4 < nch) {
; #pragma unroll
;                     for (int cc = 0; cc < 4; ++cc) { const int c = gq * 4 + cc;
; #pragma unroll
;                         for (int k = 0; k < 8; k += 2) { const f32x2 d = (f32x2){sc[c * 8 + k], sc[c * 8 + k + 1]} - pv2;
;                             bits = __builtin_amdgcn_alignbit(bits, __float_as_uint(d[0]), 31); bits = __builtin_amdgcn_alignbit(bits, __float_as_uint(d[1]), 31); } }
;                     lt += 32 - __popc(bits); }
;                 }
.LBB0_1676:
	v_sub_f32_e32 v10, v180, v0
	v_sub_f32_e32 v11, v181, v1
	v_lshrrev_b32_e32 v9, 31, v10
	v_alignbit_b32 v9, v9, v11, 31
	v_sub_f32_e32 v10, v178, v0
	v_sub_f32_e32 v11, v179, v1
	v_alignbit_b32 v9, v9, v10, 31
	v_alignbit_b32 v9, v9, v11, 31
	v_sub_f32_e32 v10, v176, v0
	v_sub_f32_e32 v11, v177, v1
	v_alignbit_b32 v9, v9, v10, 31
	v_alignbit_b32 v9, v9, v11, 31
	v_sub_f32_e32 v10, v174, v0
	v_sub_f32_e32 v11, v175, v1
	v_alignbit_b32 v9, v9, v10, 31
	v_alignbit_b32 v9, v9, v11, 31
	v_sub_f32_e32 v10, v172, v0
	v_sub_f32_e32 v11, v173, v1
	v_alignbit_b32 v9, v9, v10, 31
	v_alignbit_b32 v9, v9, v11, 31
	v_sub_f32_e32 v10, v170, v0
	v_sub_f32_e32 v11, v171, v1
	v_alignbit_b32 v9, v9, v10, 31
	v_alignbit_b32 v9, v9, v11, 31
	v_sub_f32_e32 v10, v168, v0
	v_sub_f32_e32 v11, v169, v1
	v_alignbit_b32 v9, v9, v10, 31
	v_alignbit_b32 v9, v9, v11, 31
	v_sub_f32_e32 v10, v166, v0
	v_sub_f32_e32 v11, v167, v1
	v_alignbit_b32 v9, v9, v10, 31
	v_alignbit_b32 v9, v9, v11, 31
	v_sub_f32_e32 v10, v164, v0
	v_sub_f32_e32 v11, v165, v1
	v_alignbit_b32 v9, v9, v10, 31
	v_alignbit_b32 v9, v9, v11, 31
	v_sub_f32_e32 v10, v162, v0
	v_sub_f32_e32 v11, v163, v1
	v_alignbit_b32 v9, v9, v10, 31
	v_alignbit_b32 v9, v9, v11, 31
	v_sub_f32_e32 v10, v160, v0
	v_sub_f32_e32 v11, v161, v1
	v_alignbit_b32 v9, v9, v10, 31
	v_alignbit_b32 v9, v9, v11, 31
	v_sub_f32_e32 v10, v158, v0
	v_sub_f32_e32 v11, v159, v1
	v_alignbit_b32 v9, v9, v10, 31
	v_alignbit_b32 v9, v9, v11, 31
	v_sub_f32_e32 v10, v156, v0
	v_sub_f32_e32 v11, v157, v1
	v_alignbit_b32 v9, v9, v10, 31
	v_alignbit_b32 v9, v9, v11, 31
	v_sub_f32_e32 v10, v154, v0
	v_sub_f32_e32 v11, v155, v1
	v_alignbit_b32 v9, v9, v10, 31
	v_alignbit_b32 v9, v9, v11, 31
	v_sub_f32_e32 v10, v152, v0
	v_sub_f32_e32 v11, v153, v1
	v_alignbit_b32 v9, v9, v10, 31
	v_alignbit_b32 v9, v9, v11, 31
	v_sub_f32_e32 v10, v150, v0
	v_sub_f32_e32 v11, v151, v1
	v_alignbit_b32 v9, v9, v10, 31
	v_alignbit_b32 v9, v9, v11, 31
	v_not_b32_e32 v9, v9
	v_bcnt_u32_b32 v8, v9, v8
	s_andn2_b64 vcc, exec, s[58:59]
	s_cbranch_vccz .LBB0_1674

; __device__ __forceinline__ void indexer_phase(const Frame& F, const bf16_t* QI, const bf16_t* KI, const float* WI, unsigned* MASK, const pg8::SideConv& SD) {
;     ...
;                 for (int gq = 0; gq < 4; ++gq) {
;                     unsigned bits = 0u;
;                     if (gq * 4 < nch) {
; #pragma unroll
;                     for (int cc = 0; cc < 4; ++cc) { const int c = gq * 4 + cc;
; #pragma unroll
;                         for (int k = 0; k < 8; k += 2) { const f32x2 d = (f32x2){sc[c * 8 + k], sc[c * 8 + k + 1]} - pv2;
;                             bits = __builtin_amdgcn_alignbit(bits, __float_as_uint(d[0]), 31); bits = __builtin_amdgcn_alignbit(bits, __float_as_uint(d[1]), 31); } }
;                     lt += 32 - __popc(bits); }
;                 }
;                 const int cnt = half_sum_rl(lt, hi);
.LBB0_1678:
	v_sub_f32_e32 v10, v116, v0
	v_sub_f32_e32 v11, v117, v1
	v_lshrrev_b32_e32 v9, 31, v10
	v_alignbit_b32 v9, v9, v11, 31
	v_sub_f32_e32 v10, v114, v0
	v_sub_f32_e32 v11, v115, v1
	v_alignbit_b32 v9, v9, v10, 31
	v_alignbit_b32 v9, v9, v11, 31
	v_sub_f32_e32 v10, v112, v0
	v_sub_f32_e32 v11, v113, v1
	v_alignbit_b32 v9, v9, v10, 31
	v_alignbit_b32 v9, v9, v11, 31
	v_sub_f32_e32 v10, v110, v0
	v_sub_f32_e32 v11, v111, v1
	v_alignbit_b32 v9, v9, v10, 31
	v_alignbit_b32 v9, v9, v11, 31
	v_sub_f32_e32 v10, v108, v0
	v_sub_f32_e32 v11, v109, v1
	v_alignbit_b32 v9, v9, v10, 31
	v_alignbit_b32 v9, v9, v11, 31
	v_sub_f32_e32 v10, v106, v0
	v_sub_f32_e32 v11, v107, v1
	v_alignbit_b32 v9, v9, v10, 31
	v_alignbit_b32 v9, v9, v11, 31
	v_sub_f32_e32 v10, v104, v0
	v_sub_f32_e32 v11, v105, v1
	v_alignbit_b32 v9, v9, v10, 31
	v_alignbit_b32 v9, v9, v11, 31
	v_sub_f32_e32 v10, v102, v0
	v_sub_f32_e32 v11, v103, v1
	v_alignbit_b32 v9, v9, v10, 31
	v_alignbit_b32 v9, v9, v11, 31
	v_sub_f32_e32 v10, v98, v0
	v_sub_f32_e32 v11, v99, v1
	v_alignbit_b32 v9, v9, v10, 31
	v_alignbit_b32 v9, v9, v11, 31
	v_sub_f32_e32 v10, v92, v0
	v_sub_f32_e32 v11, v93, v1
	v_alignbit_b32 v9, v9, v10, 31
	v_alignbit_b32 v9, v9, v11, 31
	v_sub_f32_e32 v10, v90, v0
	v_sub_f32_e32 v11, v91, v1
	v_alignbit_b32 v9, v9, v10, 31
	v_alignbit_b32 v9, v9, v11, 31
	v_sub_f32_e32 v10, v86, v0
	v_sub_f32_e32 v11, v87, v1
	v_alignbit_b32 v9, v9, v10, 31
	v_alignbit_b32 v9, v9, v11, 31
	v_sub_f32_e32 v10, v100, v0
	v_sub_f32_e32 v11, v101, v1
	v_alignbit_b32 v9, v9, v10, 31
	v_alignbit_b32 v9, v9, v11, 31
	v_sub_f32_e32 v10, v96, v0
	v_sub_f32_e32 v11, v97, v1
	v_alignbit_b32 v9, v9, v10, 31
	v_alignbit_b32 v9, v9, v11, 31
	v_sub_f32_e32 v10, v94, v0
	v_sub_f32_e32 v11, v95, v1
	v_sub_f32_e32 v0, v88, v0
	v_sub_f32_e32 v1, v89, v1
	v_alignbit_b32 v9, v9, v10, 31
	v_alignbit_b32 v9, v9, v11, 31
	v_alignbit_b32 v0, v9, v0, 31
	v_alignbit_b32 v0, v0, v1, 31
	v_not_b32_e32 v0, v0
	v_bcnt_u32_b32 v8, v0, v8

; #define SBAR() __builtin_amdgcn_sched_barrier(0)
; __device__ __forceinline__ unsigned sel_bit_mask(unsigned w, int b) { unsigned m; asm("v_bfe_i32 %0, %1, %2, 1" : "=v"(m) : "v"(w), "n"(b)); return m; }
; #define VMW() asm volatile("s_waitcnt vmcnt(0)" ::: "memory")
; #define SWRITE_H(bf) do { SWRITE_HV(bf); SWRITE_HK(bf); } while (0)
; #define MASKT(P0_, P1_, t) do { } while (0)
; template <bool SEL>
; __device__ __forceinline__ void partialSM(f32x16& p0, f32x16& p1, float& m_reg, float& mn, float& alpha, unsigned selw) {
;     ...
;     constexpr float C2 = 1.4426950408889634f * SCALE;
;     if (__builtin_expect(__all((pmax - m_reg) * SCALE <= THR), 1)) { mn = m_reg; alpha = 1.f; }
;     else { mn = fmaxf(m_reg, pmax); alpha = __builtin_amdgcn_exp2f((m_reg - mn) * C2); m_reg = mn; }
;     const float mnL = -mn * C2;
; #pragma unroll
;     for (int r = 0; r < 16; ++r) p0[r] = fmaf(p0[r], C2, mnL);
; #pragma unroll
;     for (int r = 0; r < 16; ++r) p1[r] = fmaf(p1[r], C2, mnL);
; #pragma unroll
;     for (int r = 0; r < 16; ++r) p0[r] = __builtin_amdgcn_exp2f(p0[r]);
;     if (SEL) {
; #pragma unroll
;         for (int r = 0; r < 16; ++r) p0[r] = __uint_as_float(__float_as_uint(p0[r]) & sel_bit_mask(selw, r));
;     }
; }
; template <int QS, int KS, int OS, bool SEL, int QREG, bool MERGE>
; __device__ __forceinline__ void attn_block(const BlockRef& cur, const BlockRef& nxt, int skv, int W, char* lds, Seam& S, const MergeArgs& MG, const int wid) {
;     ...
;     SBAR(); qkt<0, QREG>(pA0, pA1, K_lds, r32, hi, S.qr, qlds);
;     MASKT(pA0, pA1, 0); partialSM<SEL>(pA0, pA1, m_reg, mnA, alA, mwA);
;     if (NT > 1) { VMW(); SWRITE_H(1); }
;     __syncthreads();
.LBB0_1808:
	v_max_f32_e32 v51, v51, v51
	v_max_f32_e32 v51, 0xf149f2ca, v51
	v_sub_f32_e32 v52, 0xf149f2ca, v51
	v_mul_f32_e32 v52, 0x3e0293ee, v52
	v_exp_f32_e32 v52, v52
	s_cmp_eq_u64 s[0:1], exec
	s_cselect_b64 vcc, -1, 0
	v_cndmask_b32_e32 v184, v51, v199, vcc
	v_cndmask_b32_e64 v214, v52, 1.0, vcc
	v_mul_f32_e32 v52, 0xbe0293ee, v184
	v_fmamk_f32 v20, v20, 0x3e0293ee, v52
	v_fmamk_f32 v21, v21, 0x3e0293ee, v52
	v_fmamk_f32 v22, v22, 0x3e0293ee, v52
	v_fma_f32 v180, v4, s10, v52
	v_fma_f32 v181, v5, s10, v52
	v_exp_f32_e32 v4, v20
	v_exp_f32_e32 v5, v21
	v_mov_b32_e32 v51, v52
	v_fma_f32 v178, v6, s10, v52
	v_fma_f32 v179, v7, s10, v52
	v_exp_f32_e32 v6, v22
	v_fmamk_f32 v18, v18, 0x3e0293ee, v52
	v_fmamk_f32 v19, v19, 0x3e0293ee, v52
	v_fmamk_f32 v23, v23, 0x3e0293ee, v52
	v_fmamk_f32 v24, v24, 0x3e0293ee, v52
	v_fmamk_f32 v25, v25, 0x3e0293ee, v52
	v_fmamk_f32 v26, v26, 0x3e0293ee, v52
	v_fmamk_f32 v27, v27, 0x3e0293ee, v52
	v_fmamk_f32 v28, v28, 0x3e0293ee, v52
	v_fmamk_f32 v29, v29, 0x3e0293ee, v52
	v_fmamk_f32 v30, v30, 0x3e0293ee, v52
	v_fmamk_f32 v31, v31, 0x3e0293ee, v52
	v_fmamk_f32 v32, v32, 0x3e0293ee, v52
	v_fmac_f32_e32 v51, 0x3e0293ee, v33
	v_fma_f32 v168, v16, s10, v52
	v_fma_f32 v169, v17, s10, v52
	v_fma_f32 v170, v14, s10, v52
	v_fma_f32 v171, v15, s10, v52
	v_fma_f32 v172, v12, s10, v52
	v_fma_f32 v173, v13, s10, v52
	v_fma_f32 v174, v10, s10, v52
	v_fma_f32 v175, v11, s10, v52
	v_fma_f32 v176, v8, s10, v52
	v_fma_f32 v177, v9, s10, v52
	v_fma_f32 v182, v2, s10, v52
	v_fma_f32 v183, v3, s10, v52
	v_exp_f32_e32 v2, v18
	v_exp_f32_e32 v3, v19
	v_exp_f32_e32 v7, v23
	v_exp_f32_e32 v8, v24
	v_exp_f32_e32 v9, v25
	v_exp_f32_e32 v10, v26
	v_exp_f32_e32 v11, v27
	v_exp_f32_e32 v12, v28
	v_exp_f32_e32 v13, v29
	v_exp_f32_e32 v14, v51
	v_exp_f32_e32 v15, v32
	v_exp_f32_e32 v16, v31
	v_exp_f32_e32 v17, v30
	v_and_b32_e32 v125, v38, v5
	v_and_b32_e32 v124, v37, v4
	v_and_b32_e32 v4, 0xc0, v35
	v_lshlrev_b32_e32 v5, 1, v200
	v_and_b32_e32 v122, v39, v6
	v_and_or_b32 v4, v34, 24, v4
	v_and_b32_e32 v5, 32, v5
	v_and_b32_e32 v6, 0x100, v34
	s_cmp_lg_u32 0, -1
	v_or3_b32 v4, v4, v5, v6
	s_cselect_b32 s0, 0, 0
	v_and_b32_e32 v113, v50, v14
	v_and_b32_e32 v112, v49, v15
	v_and_b32_e32 v115, v48, v16
	v_and_b32_e32 v114, v47, v17
	v_and_b32_e32 v117, v46, v13
	v_and_b32_e32 v116, v45, v12
	v_and_b32_e32 v119, v44, v11
	v_and_b32_e32 v118, v43, v10
	v_and_b32_e32 v121, v42, v9
	v_and_b32_e32 v120, v41, v8
	v_and_b32_e32 v123, v40, v7
	v_add_u32_e32 v206, s0, v4
	s_cmp_lt_i32 s87, 3
	v_cmp_gt_u32_e64 s[0:1], 32, v200
	v_lshl_add_u32 v205, v201, 2, s66
	v_and_b32_e32 v127, v36, v3
	v_and_b32_e32 v126, v0, v2
	s_waitcnt lgkmcnt(0)
	s_barrier
	s_cbranch_scc1 .LBB0_1823
	v_add_u32_e32 v0, s79, v202
	v_lshlrev_b32_e32 v2, 7, v201
	v_mov_b32_e32 v189, v1
	v_add3_u32 v194, v0, v2, s89
	v_lshl_add_u32 v0, s88, 6, v191
	v_mov_b32_e32 v215, 0
	v_lshl_add_u64 v[14:15], s[2:3], 0, v[188:189]
	v_lshl_add_u64 v[192:193], s[48:49], 0, v[188:189]
	s_mov_b32 s54, 2
	v_add_u32_e32 v196, 0x80, v0
	v_mov_b32_e32 v64, 0
	v_mov_b32_e32 v65, v215
	v_mov_b32_e32 v66, v215
	v_mov_b32_e32 v67, v215
	v_mov_b32_e32 v68, v215
	v_mov_b32_e32 v69, v215
	v_mov_b32_e32 v70, v215
	v_mov_b32_e32 v71, v215
	v_mov_b32_e32 v72, v215
	v_mov_b32_e32 v73, v215
	v_mov_b32_e32 v74, v215
	v_mov_b32_e32 v75, v215
	v_mov_b32_e32 v76, v215
	v_mov_b32_e32 v77, v215
	v_mov_b32_e32 v78, v215
	v_mov_b32_e32 v79, v215
	v_mov_b32_e32 v48, 0
	v_mov_b32_e32 v49, v215
	v_mov_b32_e32 v50, v215
	v_mov_b32_e32 v51, v215
	v_mov_b32_e32 v52, v215
	v_mov_b32_e32 v53, v215
	v_mov_b32_e32 v54, v215
	v_mov_b32_e32 v55, v215
	v_mov_b32_e32 v56, v215
	v_mov_b32_e32 v57, v215
	v_mov_b32_e32 v58, v215
	v_mov_b32_e32 v59, v215
	v_mov_b32_e32 v60, v215
	v_mov_b32_e32 v61, v215
	v_mov_b32_e32 v62, v215
	v_mov_b32_e32 v63, v215
	v_mov_b32_e32 v32, 0
	v_mov_b32_e32 v33, v215
	v_mov_b32_e32 v34, v215
	v_mov_b32_e32 v35, v215
	v_mov_b32_e32 v36, v215
	v_mov_b32_e32 v37, v215
	v_mov_b32_e32 v38, v215
	v_mov_b32_e32 v39, v215
	v_mov_b32_e32 v40, v215
	v_mov_b32_e32 v41, v215
	v_mov_b32_e32 v42, v215
	v_mov_b32_e32 v43, v215
	v_mov_b32_e32 v44, v215
	v_mov_b32_e32 v45, v215
	v_mov_b32_e32 v46, v215
	v_mov_b32_e32 v47, v215
	v_mov_b32_e32 v16, 0
	v_mov_b32_e32 v17, v215
	v_mov_b32_e32 v18, v215
	v_mov_b32_e32 v19, v215
	v_mov_b32_e32 v20, v215
	v_mov_b32_e32 v21, v215
	v_mov_b32_e32 v22, v215
	v_mov_b32_e32 v23, v215
	v_mov_b32_e32 v24, v215
	v_mov_b32_e32 v25, v215
	v_mov_b32_e32 v26, v215
	v_mov_b32_e32 v27, v215
	v_mov_b32_e32 v28, v215
	v_mov_b32_e32 v29, v215
	v_mov_b32_e32 v30, v215
	v_mov_b32_e32 v31, v215
	s_branch .LBB0_1812
; __device__ __forceinline__ unsigned sel_bit_mask(unsigned w, int b) { unsigned m; asm("v_bfe_i32 %0, %1, %2, 1" : "=v"(m) : "v"(w), "n"(b)); return m; }
; template <bool SEL>
; __device__ __forceinline__ void partialSM(f32x16& p0, f32x16& p1, float& m_reg, float& mn, float& alpha, unsigned selw) {
;     ...
;     constexpr float C2 = 1.4426950408889634f * SCALE;
;     if (__builtin_expect(__all((pmax - m_reg) * SCALE <= THR), 1)) { mn = m_reg; alpha = 1.f; }
;     else { mn = fmaxf(m_reg, pmax); alpha = __builtin_amdgcn_exp2f((m_reg - mn) * C2); m_reg = mn; }
;     const float mnL = -mn * C2;
; #pragma unroll
;     for (int r = 0; r < 16; ++r) p0[r] = fmaf(p0[r], C2, mnL);
; #pragma unroll
;     for (int r = 0; r < 16; ++r) p1[r] = fmaf(p1[r], C2, mnL);
; #pragma unroll
;     for (int r = 0; r < 16; ++r) p0[r] = __builtin_amdgcn_exp2f(p0[r]);
;     if (SEL) {
; #pragma unroll
;         for (int r = 0; r < 16; ++r) p0[r] = __uint_as_float(__float_as_uint(p0[r]) & sel_bit_mask(selw, r));
.LBB0_1810:
	s_or_b64 exec, exec, s[48:49]
	s_waitcnt lgkmcnt(0)
	v_add_u32_e32 v12, s66, v203
	ds_read_b128 v[4:7], v12 offset:224
	ds_read_b128 v[8:11], v12 offset:192
	ds_read_b128 v[168:171], v12 offset:128
	ds_read_b128 v[172:175], v12 offset:160
	s_waitcnt lgkmcnt(3)
	v_mul_f32_e64 v78, v78, v6
	v_mul_f32_e64 v79, v79, v7
	v_mul_f32_e64 v76, v76, v4
	v_mul_f32_e64 v77, v77, v5
	s_waitcnt lgkmcnt(2)
	v_mul_f32_e64 v74, v74, v10
	v_mul_f32_e64 v75, v75, v11
	v_mul_f32_e64 v72, v72, v8
	v_mul_f32_e64 v73, v73, v9
	s_waitcnt lgkmcnt(0)
	v_mul_f32_e64 v70, v70, v174
	v_mul_f32_e64 v71, v71, v175
	v_mul_f32_e64 v68, v68, v172
	v_mul_f32_e64 v69, v69, v173
	v_mul_f32_e64 v66, v66, v170
	v_mul_f32_e64 v67, v67, v171
	v_mul_f32_e64 v64, v64, v168
	v_mul_f32_e64 v65, v65, v169
	v_mul_f32_e64 v62, v62, v6
	v_mul_f32_e64 v63, v63, v7
	v_mul_f32_e64 v60, v60, v4
	v_mul_f32_e64 v61, v61, v5
	v_mul_f32_e64 v58, v58, v10
	v_mul_f32_e64 v59, v59, v11
	v_mul_f32_e64 v56, v56, v8
	v_mul_f32_e64 v57, v57, v9
	v_mul_f32_e64 v54, v54, v174
	v_mul_f32_e64 v55, v55, v175
	v_mul_f32_e64 v52, v52, v172
	v_mul_f32_e64 v53, v53, v173
	v_mul_f32_e64 v50, v50, v170
	v_mul_f32_e64 v51, v51, v171
	v_mul_f32_e64 v48, v48, v168
	v_mul_f32_e64 v49, v49, v169
	v_mul_f32_e64 v46, v46, v6
	v_mul_f32_e64 v47, v47, v7
	v_mul_f32_e64 v44, v44, v4
	v_mul_f32_e64 v45, v45, v5
	v_mul_f32_e64 v42, v42, v10
	v_mul_f32_e64 v43, v43, v11
	v_mul_f32_e64 v40, v40, v8
	v_mul_f32_e64 v41, v41, v9
	v_mul_f32_e64 v38, v38, v174
	v_mul_f32_e64 v39, v39, v175
	v_mul_f32_e64 v36, v36, v172
	v_mul_f32_e64 v37, v37, v173
	v_mul_f32_e64 v34, v34, v170
	v_mul_f32_e64 v35, v35, v171
	v_mul_f32_e64 v32, v32, v168
	v_mul_f32_e64 v33, v33, v169
	v_mul_f32_e64 v30, v30, v6
	v_mul_f32_e64 v31, v31, v7
	v_mul_f32_e64 v28, v28, v4
	v_mul_f32_e64 v29, v29, v5
	v_mul_f32_e64 v26, v26, v10
	v_mul_f32_e64 v27, v27, v11
	v_mul_f32_e64 v24, v24, v8
	v_mul_f32_e64 v25, v25, v9
	v_mul_f32_e64 v22, v22, v174
	v_mul_f32_e64 v23, v23, v175
	v_mul_f32_e64 v20, v20, v172
	v_mul_f32_e64 v21, v21, v173
	v_mul_f32_e64 v18, v18, v170
	v_mul_f32_e64 v19, v19, v171
	v_mul_f32_e64 v16, v16, v168
	v_mul_f32_e64 v17, v17, v169
.LBB0_1811:
	v_cndmask_b32_e64 v184, v3, v197, s[2:3]
	v_mul_f32_e32 v182, 0xbe0293ee, v184
	v_fmamk_f32 v5, v130, 0x3e0293ee, v182
	v_fmamk_f32 v7, v132, 0x3e0293ee, v182
	v_mov_b32_e32 v132, v182
	v_exp_f32_e32 v5, v5
	v_fmamk_f32 v3, v128, 0x3e0293ee, v182
	v_fmamk_f32 v4, v129, 0x3e0293ee, v182
	v_fmamk_f32 v6, v131, 0x3e0293ee, v182
	v_fmamk_f32 v8, v133, 0x3e0293ee, v182
	v_fmamk_f32 v9, v134, 0x3e0293ee, v182
	v_fmamk_f32 v10, v135, 0x3e0293ee, v182
	v_fmamk_f32 v11, v136, 0x3e0293ee, v182
	v_fmamk_f32 v12, v137, 0x3e0293ee, v182
	v_fmamk_f32 v13, v138, 0x3e0293ee, v182
	v_fmamk_f32 v128, v139, 0x3e0293ee, v182
	v_fmamk_f32 v129, v140, 0x3e0293ee, v182
	v_fmamk_f32 v130, v141, 0x3e0293ee, v182
	v_fmamk_f32 v131, v142, 0x3e0293ee, v182
	v_fmac_f32_e32 v132, 0x3e0293ee, v143
	v_fma_f32 v172, v122, s10, v182
	v_fma_f32 v173, v123, s10, v182
	v_fma_f32 v174, v120, s10, v182
	v_fma_f32 v175, v121, s10, v182
	v_fma_f32 v176, v118, s10, v182
	v_fma_f32 v177, v119, s10, v182
	v_exp_f32_e32 v3, v3
	v_exp_f32_e32 v4, v4
	v_exp_f32_e32 v6, v6
	v_exp_f32_e32 v7, v7
	v_exp_f32_e32 v8, v8
	v_exp_f32_e32 v9, v9
	v_exp_f32_e32 v10, v10
	v_exp_f32_e32 v11, v11
	v_exp_f32_e32 v12, v12
	v_exp_f32_e32 v13, v13
	v_exp_f32_e32 v118, v128
	v_exp_f32_e32 v119, v129
	v_exp_f32_e32 v120, v130
	v_exp_f32_e32 v121, v131
	v_exp_f32_e32 v122, v132
	v_fma_f32 v170, v124, s10, v182
	v_fma_f32 v171, v125, s10, v182
	v_and_b32_e32 v124, v187, v5
	v_add_f32_e32 v5, v189, v219
	v_fmac_f32_e32 v5, v214, v215
	v_add_f32_e32 v215, v220, v221
	s_add_i32 s54, s54, 2
	v_fma_f32 v168, v126, s10, v182
	v_fma_f32 v169, v127, s10, v182
	v_fma_f32 v178, v116, s10, v182
	v_fma_f32 v179, v117, s10, v182
	v_fma_f32 v180, v114, s10, v182
	v_fma_f32 v181, v115, s10, v182
	v_fma_f32 v183, v113, s10, v182
	v_fma_f32 v182, v112, s10, v182
	v_and_b32_e32 v113, v234, v122
	v_and_b32_e32 v112, v233, v121
	v_and_b32_e32 v115, v232, v120
	v_and_b32_e32 v114, v231, v119
	v_and_b32_e32 v117, v230, v118
	v_and_b32_e32 v116, v229, v13
	v_and_b32_e32 v119, v228, v12
	v_and_b32_e32 v118, v227, v11
	v_and_b32_e32 v121, v226, v10
	v_and_b32_e32 v120, v225, v9
	v_and_b32_e32 v123, v224, v8
	v_and_b32_e32 v122, v223, v7
	v_and_b32_e32 v125, v222, v6
	v_and_b32_e32 v127, v186, v4
	v_fmac_f32_e32 v215, v5, v0
	v_add_u32_e32 v194, 4, v194
	v_add_u32_e32 v196, 0x80, v196
	s_cmp_ge_i32 s54, s87
	v_and_b32_e32 v126, v185, v3
	v_mov_b32_e32 v214, v2
	s_waitcnt lgkmcnt(0)
	s_barrier
	s_cbranch_scc1 .LBB0_1824
; __device__ __forceinline__ unsigned sel_bit_mask(unsigned w, int b) { unsigned m; asm("v_bfe_i32 %0, %1, %2, 1" : "=v"(m) : "v"(w), "n"(b)); return m; }
; template <bool SEL>
; __device__ __forceinline__ void finishSM(f32x16& p0, f32x16& p1, float alpha, float& l_reg, bf16x8& pa0, bf16x8& pa1, bf16x8& pa2, bf16x8& pa3, unsigned selw) {
; #pragma unroll
;     for (int r = 0; r < 16; ++r) p1[r] = __builtin_amdgcn_exp2f(p1[r]);
;     if (SEL) {
; #pragma unroll
;         for (int r = 0; r < 16; ++r) p1[r] = __uint_as_float(__float_as_uint(p1[r]) & sel_bit_mask(selw, 16 + r));
;     }
;     float ps = 0;
; #pragma unroll
;     for (int r = 0; r < 16; ++r) ps += p0[r];
; #pragma unroll
;     for (int r = 0; r < 16; ++r) ps += p1[r];
;     { auto rr = __builtin_amdgcn_permlane32_swap(__float_as_uint(ps), __float_as_uint(ps), false, false);
;       ps = __uint_as_float(rr[0]) + __uint_as_float(rr[1]); }
;     l_reg = l_reg * alpha + ps;
;     ...
;     PK4(p0, 0, pa0); PK4(p0, 8, pa1); PK4(p1, 0, pa2); PK4(p1, 8, pa3);
; template <int KB, int QREG>
; __device__ __forceinline__ void qkt(f32x16& p0, f32x16& p1, const char* K_lds, int r32, int hi, const bf16x8* qr, const char* qlds) {
;     p0 = f32x16{}; p1 = f32x16{};
;     const char* kb[4];
; #pragma unroll
;     for (int dd = 0; dd < 4; ++dd) kb[dd] = K_lds + KB * SHM_K + KSWZ(r32, (dd * 16 + hi * 8) * 2);
; #pragma unroll
;     for (int d0 = 0; d0 < 8; ++d0) { const char* a = kb[d0 & 3] + (d0 >> 2) * 128;
;         bf16x8 b0 = *reinterpret_cast<const bf16x8*>(a);
;         bf16x8 b1 = *reinterpret_cast<const bf16x8*>(a + 32 * 256);
;         const bf16x8 qf = (d0 < QREG) ? qr[d0 < QREG ? d0 : 0] : *reinterpret_cast<const bf16x8*>(qlds + (d0 - QREG) * 1024);
;         p0 = __builtin_amdgcn_mfma_f32_32x32x16_bf16(b0, qf, p0, 0, 0, 0);
;         p1 = __builtin_amdgcn_mfma_f32_32x32x16_bf16(b1, qf, p1, 0, 0, 0); }
; }
.LBB0_1812:
	ds_read_b128 v[2:5], v213 offset:49152
	ds_read_b128 v[250:253], v212 offset:49152
	ds_read_b128 v[6:9], v213 offset:49280
	v_add_f32_e32 v0, 0, v126
	v_add_f32_e32 v0, v127, v0
	v_add_f32_e32 v0, v124, v0
	s_waitcnt lgkmcnt(2)
	v_mfma_f32_32x32x16_bf16 v[96:111], v[2:5], v[164:167], 0
	ds_read_b128 v[2:5], v213 offset:57344
	ds_read_b128 v[10:13], v212 offset:49280
	v_add_f32_e32 v0, v125, v0
	v_add_f32_e32 v0, v122, v0
	v_add_f32_e32 v0, v123, v0
	v_add_f32_e32 v0, v120, v0
	v_add_f32_e32 v0, v121, v0
	v_add_f32_e32 v0, v118, v0
	s_waitcnt lgkmcnt(3)
	v_mfma_f32_32x32x16_bf16 v[96:111], v[250:253], v[160:163], v[96:111]
	ds_read_b128 v[250:253], v212 offset:57344
	ds_read_b128 v[128:131], v213 offset:57472
	v_add_f32_e32 v0, v119, v0
	v_add_f32_e32 v0, v116, v0
	v_add_f32_e32 v0, v117, v0
	v_add_f32_e32 v0, v114, v0
	v_add_f32_e32 v0, v115, v0
	v_add_f32_e32 v0, v112, v0
	s_waitcnt lgkmcnt(3)
	v_mfma_f32_32x32x16_bf16 v[80:95], v[2:5], v[164:167], 0
	ds_read_b128 v[2:5], v211 offset:49152
	ds_read_b128 v[132:135], v212 offset:57472
	v_add_f32_e32 v0, v113, v0
	s_waitcnt lgkmcnt(3)
	v_mfma_f32_32x32x16_bf16 v[80:95], v[250:253], v[160:163], v[80:95]
	ds_read_b128 v[250:253], v211 offset:57344
	ds_read_b128 v[136:139], v211 offset:49280
	s_waitcnt lgkmcnt(3)
	v_mfma_f32_32x32x16_bf16 v[96:111], v[2:5], v[156:159], v[96:111]
	ds_read_b128 v[2:5], v210 offset:49152
	ds_read_b128 v[140:143], v211 offset:57472
	s_waitcnt lgkmcnt(3)
	v_mfma_f32_32x32x16_bf16 v[80:95], v[250:253], v[156:159], v[80:95]
	ds_read_b128 v[250:253], v210 offset:57344
	ds_read_b128 v[220:223], v210 offset:49280
	s_waitcnt lgkmcnt(3)
	v_mfma_f32_32x32x16_bf16 v[96:111], v[2:5], v[152:155], v[96:111]
	ds_read_b128 v[224:227], v210 offset:57472
	s_waitcnt lgkmcnt(2)
	v_mfma_f32_32x32x16_bf16 v[80:95], v[250:253], v[152:155], v[80:95]
	v_mfma_f32_32x32x16_bf16 v[96:111], v[6:9], v[148:151], v[96:111]
	ds_read_b128 v[2:5], v208
	ds_read_b128 v[6:9], v208 offset:1024
	v_cvt_pk_bf16_f32 v126, v126, v127
	v_cvt_pk_bf16_f32 v127, v124, v125
	v_exp_f32_e32 v124, v172
	v_exp_f32_e32 v125, v173
	v_mfma_f32_32x32x16_bf16 v[80:95], v[128:131], v[148:151], v[80:95]
	v_cvt_pk_bf16_f32 v128, v122, v123
	v_exp_f32_e32 v122, v174
	v_exp_f32_e32 v123, v175
	v_exp_f32_e32 v129, v170
	v_exp_f32_e32 v130, v171
	v_exp_f32_e32 v131, v168
	v_permlane32_swap_b32_e32 v126, v128
	v_mfma_f32_32x32x16_bf16 v[96:111], v[10:13], v[144:147], v[96:111]
	v_exp_f32_e32 v10, v178
	v_exp_f32_e32 v11, v179
	v_exp_f32_e32 v12, v176
	v_exp_f32_e32 v13, v177
	v_mfma_f32_32x32x16_bf16 v[80:95], v[132:135], v[144:147], v[80:95]
	v_bfe_i32 v133, v195, 16, 1
	v_exp_f32_e32 v132, v169
	s_waitcnt lgkmcnt(1)
	v_mfma_f32_32x32x16_bf16 v[96:111], v[136:139], v[2:5], v[96:111]
	v_mfma_f32_32x32x16_bf16 v[80:95], v[140:143], v[2:5], v[80:95]
	v_exp_f32_e32 v2, v182
	v_exp_f32_e32 v3, v183
	v_exp_f32_e32 v4, v180
	v_exp_f32_e32 v5, v181
	v_and_b32_e32 v2, v133, v2
	v_bfe_i32 v133, v195, 17, 1
	v_add_f32_e32 v0, v0, v2
	v_and_b32_e32 v3, v133, v3
	v_bfe_i32 v133, v195, 18, 1
	v_add_f32_e32 v0, v0, v3
	v_and_b32_e32 v4, v133, v4
	v_bfe_i32 v133, v195, 19, 1
	v_add_f32_e32 v0, v0, v4
	v_and_b32_e32 v5, v133, v5
	v_bfe_i32 v133, v195, 20, 1
	v_add_f32_e32 v0, v0, v5
	v_and_b32_e32 v10, v133, v10
	v_bfe_i32 v133, v195, 21, 1
	v_add_f32_e32 v0, v0, v10
	v_and_b32_e32 v11, v133, v11
	v_bfe_i32 v133, v195, 22, 1
	v_add_f32_e32 v0, v0, v11
	v_and_b32_e32 v12, v133, v12
	v_bfe_i32 v133, v195, 23, 1
	v_add_f32_e32 v0, v0, v12
	v_and_b32_e32 v13, v133, v13
	v_bfe_i32 v133, v195, 24, 1
	v_add_f32_e32 v0, v0, v13
	v_and_b32_e32 v122, v133, v122
	v_bfe_i32 v133, v195, 25, 1
	v_add_f32_e32 v0, v0, v122
	v_and_b32_e32 v123, v133, v123
	v_bfe_i32 v133, v195, 26, 1
	v_add_f32_e32 v0, v0, v123
	v_and_b32_e32 v124, v133, v124
	v_bfe_i32 v133, v195, 27, 1
	s_waitcnt lgkmcnt(0)
	v_mfma_f32_32x32x16_bf16 v[96:111], v[220:223], v[6:9], v[96:111]
	v_and_b32_e32 v125, v133, v125
	v_bfe_i32 v133, v195, 28, 1
	v_add_f32_e32 v0, v0, v124
	v_and_b32_e32 v133, v133, v129
	v_add_f32_e32 v0, v0, v125
	v_bfe_i32 v129, v195, 29, 1
	v_add_f32_e32 v0, v0, v133
	v_mfma_f32_32x32x16_bf16 v[80:95], v[224:227], v[6:9], v[80:95]
	v_and_b32_e32 v130, v129, v130
	v_bfe_i32 v129, v195, 30, 1
	v_add_f32_e32 v0, v0, v130
	v_and_b32_e32 v131, v129, v131
	v_bfe_i32 v129, v195, 31, 1
	v_add_f32_e32 v0, v0, v131
	v_and_b32_e32 v132, v129, v132
	v_add_f32_e32 v189, v0, v132
	v_mov_b32_e32 v219, v189
	v_cvt_pk_bf16_f32 v129, v120, v121
	v_cvt_pk_bf16_f32 v118, v118, v119
	v_cvt_pk_bf16_f32 v119, v116, v117
	v_cvt_pk_bf16_f32 v120, v114, v115
	v_cvt_pk_bf16_f32 v121, v112, v113
	v_cvt_pk_bf16_f32 v112, v2, v3
	v_cvt_pk_bf16_f32 v113, v4, v5
	v_cvt_pk_bf16_f32 v114, v10, v11
	v_cvt_pk_bf16_f32 v115, v12, v13
	v_cvt_pk_bf16_f32 v122, v122, v123
	v_cvt_pk_bf16_f32 v123, v124, v125
	v_cvt_pk_bf16_f32 v124, v133, v130
	v_cvt_pk_bf16_f32 v125, v131, v132
	s_nop 1
	v_permlane32_swap_b32_e32 v189, v219
	v_permlane32_swap_b32_e32 v127, v129
	v_permlane32_swap_b32_e32 v118, v120
	v_permlane32_swap_b32_e32 v119, v121
	v_permlane32_swap_b32_e32 v112, v114
	v_permlane32_swap_b32_e32 v113, v115
	v_permlane32_swap_b32_e32 v122, v124
	v_permlane32_swap_b32_e32 v123, v125
	v_add_u32_e32 v4, 32, v196
	v_add_u32_e32 v0, -2, v194
	v_ashrrev_i32_e32 v197, 31, v196
	v_ashrrev_i32_e32 v5, 31, v4
	v_lshl_add_u64 v[2:3], v[0:1], 2, s[44:45]
	v_lshlrev_b64 v[10:11], 10, v[196:197]
	v_lshlrev_b64 v[12:13], 10, v[4:5]
	global_load_dword v217, v[2:3], off
	v_lshl_add_u64 v[2:3], v[14:15], 0, v[10:11]
	v_lshl_add_u64 v[6:7], v[14:15], 0, v[12:13]
	v_lshl_add_u64 v[10:11], v[192:193], 0, v[10:11]
	global_load_dwordx4 v[2:5], v[2:3], off
	s_nop 0
	global_load_dwordx4 v[6:9], v[6:7], off
	v_lshl_add_u64 v[116:117], v[192:193], 0, v[12:13]
	global_load_dwordx4 v[10:13], v[10:11], off
	s_nop 0
	global_load_dwordx4 v[168:171], v[116:117], off
	ds_read_b64_tr_b16 v[130:131], v206 offset:0
	ds_read_b64_tr_b16 v[132:133], v206 offset:0x800
	ds_read_b64_tr_b16 v[134:135], v206 offset:0x1000
	ds_read_b64_tr_b16 v[136:137], v206 offset:0x1800
	ds_read_b64_tr_b16 v[138:139], v206 offset:0x2000
	ds_read_b64_tr_b16 v[140:141], v206 offset:0x2800
	ds_read_b64_tr_b16 v[172:173], v206 offset:0x3000
	ds_read_b64_tr_b16 v[174:175], v206 offset:0x3800
	s_waitcnt lgkmcnt(0)
; template <bool SEL>
; __device__ __forceinline__ void partialSM(f32x16& p0, f32x16& p1, float& m_reg, float& mn, float& alpha, unsigned selw) {
;     float pmax = p0[0];
; #pragma unroll
;     for (int r = 1; r < 16; ++r) pmax = fmaxf(pmax, p0[r]);
; #pragma unroll
;     for (int r = 0; r < 16; ++r) pmax = fmaxf(pmax, p1[r]);
;     { auto rr = __builtin_amdgcn_permlane32_swap(__float_as_uint(pmax), __float_as_uint(pmax), false, false);
;       pmax = fmaxf(__uint_as_float(rr[0]), __uint_as_float(rr[1])); }
;     constexpr float C2 = 1.4426950408889634f * SCALE;
;     if (__builtin_expect(__all((pmax - m_reg) * SCALE <= THR), 1)) { mn = m_reg; alpha = 1.f; }
;     else { mn = fmaxf(m_reg, pmax); alpha = __builtin_amdgcn_exp2f((m_reg - mn) * C2); m_reg = mn; }
; template <int VB>
; __device__ __forceinline__ void pv_tile(f32x16* o, int vb0, bf16x8 pa0, bf16x8 pa1, bf16x8 pa2, bf16x8 pa3) {
;     ...
;     PV_D0(0); PV_D0(1); PV_D0(2); PV_D0(3);
;     ...
; }
	s_nop 0
	v_mfma_f32_32x32x16_bf16 v[64:79], v[126:129], v[130:133], v[64:79]
	ds_read_b64_tr_b16 v[130:131], v206 offset:0x200
	ds_read_b64_tr_b16 v[132:133], v206 offset:0xa00
	v_mfma_f32_32x32x16_bf16 v[64:79], v[118:121], v[134:137], v[64:79]
	ds_read_b64_tr_b16 v[134:135], v206 offset:0x1200
	ds_read_b64_tr_b16 v[136:137], v206 offset:0x1a00
	v_mfma_f32_32x32x16_bf16 v[64:79], v[112:115], v[138:141], v[64:79]
	ds_read_b64_tr_b16 v[138:139], v206 offset:0x2200
	ds_read_b64_tr_b16 v[140:141], v206 offset:0x2a00
	ds_read_b64_tr_b16 v[176:177], v206 offset:0x3200
	ds_read_b64_tr_b16 v[178:179], v206 offset:0x3a00
	s_waitcnt lgkmcnt(0)
	v_mfma_f32_32x32x16_bf16 v[64:79], v[122:125], v[172:175], v[64:79]
	v_mfma_f32_32x32x16_bf16 v[48:63], v[126:129], v[130:133], v[48:63]
	ds_read_b64_tr_b16 v[130:131], v206 offset:0x400
	ds_read_b64_tr_b16 v[132:133], v206 offset:0xc00
	v_mfma_f32_32x32x16_bf16 v[48:63], v[118:121], v[134:137], v[48:63]
	ds_read_b64_tr_b16 v[134:135], v206 offset:0x1400
	ds_read_b64_tr_b16 v[136:137], v206 offset:0x1c00
	v_mfma_f32_32x32x16_bf16 v[48:63], v[112:115], v[138:141], v[48:63]
	ds_read_b64_tr_b16 v[138:139], v206 offset:0x2400
	ds_read_b64_tr_b16 v[140:141], v206 offset:0x2c00
	ds_read_b64_tr_b16 v[172:173], v206 offset:0x3400
	ds_read_b64_tr_b16 v[174:175], v206 offset:0x3c00
	s_waitcnt lgkmcnt(0)
	v_mfma_f32_32x32x16_bf16 v[48:63], v[122:125], v[176:179], v[48:63]
	v_mfma_f32_32x32x16_bf16 v[32:47], v[126:129], v[130:133], v[32:47]
	ds_read_b64_tr_b16 v[130:131], v206 offset:0x600
	ds_read_b64_tr_b16 v[132:133], v206 offset:0xe00
	v_mfma_f32_32x32x16_bf16 v[32:47], v[118:121], v[134:137], v[32:47]
	ds_read_b64_tr_b16 v[134:135], v206 offset:0x1600
	ds_read_b64_tr_b16 v[136:137], v206 offset:0x1e00
	v_mfma_f32_32x32x16_bf16 v[32:47], v[112:115], v[138:141], v[32:47]
	ds_read_b64_tr_b16 v[138:139], v206 offset:0x2600
	ds_read_b64_tr_b16 v[140:141], v206 offset:0x2e00
	ds_read_b64_tr_b16 v[176:177], v206 offset:0x3600
	ds_read_b64_tr_b16 v[178:179], v206 offset:0x3e00
	s_waitcnt lgkmcnt(0)
	v_mfma_f32_32x32x16_bf16 v[32:47], v[122:125], v[172:175], v[32:47]
	v_mfma_f32_32x32x16_bf16 v[16:31], v[126:129], v[130:133], v[16:31]
	v_max_f32_e32 v0, v97, v97
	s_barrier
	s_waitcnt vmcnt(0)
	s_waitcnt vmcnt(4)
	v_bfe_i32 v116, v217, 8, 1
	v_bfe_i32 v117, v217, 10, 1
	v_mfma_f32_32x32x16_bf16 v[16:31], v[118:121], v[134:137], v[16:31]
	v_bfe_i32 v120, v217, 1, 1
	v_bfe_i32 v121, v217, 3, 1
	v_bfe_i32 v118, v217, 12, 1
	v_bfe_i32 v126, v217, 13, 1
	v_bfe_i32 v119, v217, 14, 1
	v_bfe_i32 v127, v217, 15, 1
	s_waitcnt vmcnt(3)
	ds_write_b128 v216, v[2:5]
	s_waitcnt vmcnt(2)
	ds_write_b128 v218, v[6:9]
	s_waitcnt vmcnt(1)
	ds_write_b128 v204, v[10:13] offset:32768
	s_waitcnt vmcnt(0)
	ds_write_b128 v204, v[168:171] offset:40960
	v_mfma_f32_32x32x16_bf16 v[16:31], v[112:115], v[138:141], v[16:31]
	v_max_f32_e32 v112, v96, v96
	v_max_f32_e32 v0, v112, v0
	v_max3_f32 v0, v0, v98, v99
	v_max3_f32 v0, v0, v100, v101
	v_max3_f32 v0, v0, v102, v103
	v_max3_f32 v0, v0, v104, v105
	v_max3_f32 v0, v0, v106, v107
	v_max3_f32 v0, v0, v108, v109
	v_max3_f32 v0, v0, v110, v111
	v_max3_f32 v0, v0, v80, v81
	v_max3_f32 v0, v0, v82, v83
	v_max3_f32 v0, v0, v84, v85
	v_max3_f32 v0, v0, v86, v87
	v_max3_f32 v0, v0, v88, v89
	v_max3_f32 v0, v0, v90, v91
	v_max3_f32 v0, v0, v92, v93
	v_max3_f32 v0, v0, v94, v95
	v_mov_b32_e32 v112, v0
	s_nop 1
	v_permlane32_swap_b32_e32 v0, v112
	v_max_f32_e32 v112, v112, v112
	v_max_f32_e32 v0, v0, v0
	v_max_f32_e32 v0, v0, v112
	v_sub_f32_e32 v112, v0, v184
	v_mul_f32_e32 v112, 0x3db504f3, v112
	v_cmp_ge_f32_e32 vcc, s5, v112
	v_max_f32_e32 v112, v184, v184
	v_max_f32_e32 v128, v112, v0
	v_mfma_f32_32x32x16_bf16 v[16:31], v[122:125], v[176:179], v[16:31]
	v_sub_f32_e32 v0, v184, v128
	v_mul_f32_e32 v0, 0x3e0293ee, v0
	v_exp_f32_e32 v0, v0
	s_cmp_eq_u64 vcc, exec
	s_cselect_b64 s[2:3], -1, 0
	v_bfe_i32 v112, v217, 0, 1
	v_cndmask_b32_e64 v0, v0, 1.0, s[2:3]
	v_cmp_gt_f32_e32 vcc, 1.0, v0
	v_bfe_i32 v113, v217, 2, 1
	v_bfe_i32 v114, v217, 4, 1
	v_bfe_i32 v122, v217, 5, 1
	v_bfe_i32 v115, v217, 6, 1
	v_bfe_i32 v123, v217, 7, 1
	v_bfe_i32 v124, v217, 9, 1
	v_bfe_i32 v125, v217, 11, 1
	s_cbranch_vccz .LBB0_1816
	s_and_saveexec_b64 s[48:49], s[0:1]
	ds_write_b32 v205, v0 offset:128
	s_or_b64 exec, exec, s[48:49]
	s_waitcnt lgkmcnt(0)
	v_add_u32_e32 v129, s66, v203
	ds_read_b128 v[130:133], v129 offset:224
	ds_read_b128 v[134:137], v129 offset:192
	ds_read_b128 v[138:141], v129 offset:160
	ds_read_b128 v[172:175], v129 offset:128
	s_waitcnt lgkmcnt(3)
	v_mul_f32_e64 v76, v76, v130
	v_mul_f32_e64 v77, v77, v131
	s_waitcnt lgkmcnt(2)
	v_mul_f32_e64 v72, v72, v134
	v_mul_f32_e64 v73, v73, v135
	s_waitcnt lgkmcnt(1)
	v_mul_f32_e64 v68, v68, v138
	v_mul_f32_e64 v69, v69, v139
	v_mul_f32_e64 v78, v78, v132
	v_mul_f32_e64 v79, v79, v133
	v_mul_f32_e64 v74, v74, v136
	v_mul_f32_e64 v75, v75, v137
	v_mul_f32_e64 v70, v70, v140
	v_mul_f32_e64 v71, v71, v141
	s_waitcnt lgkmcnt(0)
	v_mul_f32_e64 v66, v66, v174
	v_mul_f32_e64 v67, v67, v175
	v_mul_f32_e64 v64, v64, v172
	v_mul_f32_e64 v65, v65, v173
	v_mul_f32_e64 v60, v60, v130
	v_mul_f32_e64 v61, v61, v131
	v_mul_f32_e64 v56, v56, v134
	v_mul_f32_e64 v57, v57, v135
	v_mul_f32_e64 v52, v52, v138
	v_mul_f32_e64 v53, v53, v139
	v_mul_f32_e64 v62, v62, v132
	v_mul_f32_e64 v63, v63, v133
	v_mul_f32_e64 v58, v58, v136
	v_mul_f32_e64 v59, v59, v137
	v_mul_f32_e64 v54, v54, v140
	v_mul_f32_e64 v55, v55, v141
	v_mul_f32_e64 v50, v50, v174
	v_mul_f32_e64 v51, v51, v175
	v_mul_f32_e64 v48, v48, v172
	v_mul_f32_e64 v49, v49, v173
	v_mul_f32_e64 v44, v44, v130
	v_mul_f32_e64 v45, v45, v131
	v_mul_f32_e64 v40, v40, v134
	v_mul_f32_e64 v41, v41, v135
	v_mul_f32_e64 v36, v36, v138
	v_mul_f32_e64 v37, v37, v139
	v_mul_f32_e64 v46, v46, v132
	v_mul_f32_e64 v47, v47, v133
	v_mul_f32_e64 v42, v42, v136
	v_mul_f32_e64 v43, v43, v137
	v_mul_f32_e64 v38, v38, v140
	v_mul_f32_e64 v39, v39, v141
	v_mul_f32_e64 v34, v34, v174
	v_mul_f32_e64 v35, v35, v175
	v_mul_f32_e64 v32, v32, v172
	v_mul_f32_e64 v33, v33, v173
	v_mul_f32_e64 v28, v28, v130
	v_mul_f32_e64 v29, v29, v131
	v_mul_f32_e64 v24, v24, v134
	v_mul_f32_e64 v25, v25, v135
	v_mul_f32_e64 v20, v20, v138
	v_mul_f32_e64 v21, v21, v139
	v_mul_f32_e64 v30, v30, v132
	v_mul_f32_e64 v31, v31, v133
	v_mul_f32_e64 v26, v26, v136
	v_mul_f32_e64 v27, v27, v137
	v_mul_f32_e64 v22, v22, v140
	v_mul_f32_e64 v23, v23, v141
	v_mul_f32_e64 v18, v18, v174
	v_mul_f32_e64 v19, v19, v175
	v_mul_f32_e64 v16, v16, v172
	v_mul_f32_e64 v17, v17, v173

; #define SBAR() __builtin_amdgcn_sched_barrier(0)
; __device__ __forceinline__ unsigned sel_bit_mask(unsigned w, int b) { unsigned m; asm("v_bfe_i32 %0, %1, %2, 1" : "=v"(m) : "v"(w), "n"(b)); return m; }
; #define SLOAD_H(Kp, Vp, k0) do { S.st_v0 = load8(ROW(Vp, k0, sr)); S.st_v1 = load8(ROW(Vp, k0, 32 + sr));              \
;                          S.st_k0 = load8(ROW(Kp, k0, sr)); S.st_k1 = load8(ROW(Kp, k0, 32 + sr)); } while (0)
; template <bool SEL>
; __device__ __forceinline__ void finishSM(f32x16& p0, f32x16& p1, float alpha, float& l_reg, bf16x8& pa0, bf16x8& pa1, bf16x8& pa2, bf16x8& pa3, unsigned selw) {
; #pragma unroll
;     for (int r = 0; r < 16; ++r) p1[r] = __builtin_amdgcn_exp2f(p1[r]);
;     if (SEL) {
; #pragma unroll
;         for (int r = 0; r < 16; ++r) p1[r] = __uint_as_float(__float_as_uint(p1[r]) & sel_bit_mask(selw, 16 + r));
;     }
;     float ps = 0;
; #pragma unroll
;     for (int r = 0; r < 16; ++r) ps += p0[r];
; #pragma unroll
;     for (int r = 0; r < 16; ++r) ps += p1[r];
;     { auto rr = __builtin_amdgcn_permlane32_swap(__float_as_uint(ps), __float_as_uint(ps), false, false);
;       ps = __uint_as_float(rr[0]) + __uint_as_float(rr[1]); }
;     l_reg = l_reg * alpha + ps;
;     ...
;     PK4(p0, 0, pa0); PK4(p0, 8, pa1); PK4(p1, 0, pa2); PK4(p1, 8, pa3);
; template <int QS, int KS, int OS, bool SEL, int QREG, bool MERGE>
; __device__ __forceinline__ void attn_block(const BlockRef& cur, const BlockRef& nxt, int skv, int W, char* lds, Seam& S, const MergeArgs& MG, const int wid) {
;     ...
;     const bool even = (NT & 1) == 0;
;     if (even) { SBAR(); mwB = MLOAD(NT - 1); qkt<1, QREG>(pB0, pB1, K_lds, r32, hi, S.qr, qlds); SBAR(); }
;     SLOAD_H(nxt.K, nxt.V, kbn); SBAR();
; #pragma unroll
;     for (int d0 = 0; d0 < 8; ++d0) S.qr[d0] = load8(nxt.Q + (size_t)(wid * QBLK + r32) * QS + d0 * 16 + hi * 8);
;     SBAR();
;     finishSM<SEL>(pA0, pA1, alA, l_reg, pa0, pa1, pa2, pa3, mwA); SBAR();
;     pv_tile<0>(o, vb0, pa0, pa1, pa2, pa3);
.LBB0_1826:
	s_add_i32 s2, s84, 0xc0000001
	s_and_b32 s2, s2, 0xffffff00
	s_cmp_gt_i32 s84, 0x3fffffff
	s_cselect_b32 s2, s2, 0
	v_add_u32_e32 v2, s2, v191
	v_ashrrev_i32_e32 v3, 31, v2
	v_add_u32_e32 v6, s2, v207
	v_lshlrev_b64 v[2:3], 10, v[2:3]
	v_ashrrev_i32_e32 v7, 31, v6
	v_lshl_add_u64 v[4:5], s[36:37], 0, v[2:3]
	v_mov_b32_e32 v189, v1
	v_lshlrev_b64 v[6:7], 10, v[6:7]
	v_lshl_add_u64 v[4:5], v[4:5], 0, v[188:189]
	v_lshl_add_u64 v[8:9], s[36:37], 0, v[6:7]
	v_lshl_add_u64 v[2:3], s[38:39], 0, v[2:3]
	v_lshl_add_u64 v[8:9], v[8:9], 0, v[188:189]
	global_load_dwordx4 v[132:135], v[4:5], off
	global_load_dwordx4 v[140:143], v[8:9], off
	v_lshl_add_u64 v[2:3], v[2:3], 0, v[188:189]
	v_lshl_add_u64 v[4:5], s[38:39], 0, v[6:7]
	v_lshl_add_u64 v[4:5], v[4:5], 0, v[188:189]
	global_load_dwordx4 v[128:131], v[2:3], off
	global_load_dwordx4 v[136:139], v[4:5], off
	v_mov_b32_e32 v191, v1
	v_lshlrev_b64 v[2:3], 12, v[190:191]
	v_lshlrev_b32_e32 v4, 3, v202
	v_ashrrev_i32_e32 v5, 31, v4
	v_lshl_add_u64 v[2:3], s[8:9], 0, v[2:3]
	v_lshl_add_u64 v[2:3], v[4:5], 1, v[2:3]
	global_load_dwordx4 v[164:167], v[2:3], off
	global_load_dwordx4 v[160:163], v[2:3], off offset:32
	global_load_dwordx4 v[156:159], v[2:3], off offset:64
	global_load_dwordx4 v[152:155], v[2:3], off offset:96
	global_load_dwordx4 v[148:151], v[2:3], off offset:128
	global_load_dwordx4 v[144:147], v[2:3], off offset:160
	global_load_dwordx4 v[4:7], v[2:3], off offset:192
	global_load_dwordx4 v[8:11], v[2:3], off offset:224
	v_add_f32_e32 v0, 0, v126
	v_add_f32_e32 v0, v127, v0
	v_add_f32_e32 v0, v124, v0
	v_add_f32_e32 v0, v125, v0
	v_add_f32_e32 v0, v122, v0
	v_add_f32_e32 v0, v123, v0
	v_add_f32_e32 v0, v120, v0
	v_add_f32_e32 v0, v121, v0
	v_add_f32_e32 v0, v118, v0
	v_add_f32_e32 v0, v119, v0
	v_add_f32_e32 v0, v116, v0
	v_exp_f32_e32 v2, v182
	v_add_f32_e32 v0, v117, v0
	v_exp_f32_e32 v3, v183
	v_add_f32_e32 v0, v114, v0
	v_exp_f32_e32 v13, v180
	v_add_f32_e32 v0, v115, v0
	v_cvt_pk_bf16_f32 v12, v126, v127
	v_exp_f32_e32 v14, v181
	v_exp_f32_e32 v127, v176
	v_exp_f32_e32 v176, v177
	v_bfe_i32 v177, v195, 16, 1
	v_add_f32_e32 v0, v112, v0
	v_exp_f32_e32 v15, v178
	v_and_b32_e32 v2, v177, v2
	v_bfe_i32 v177, v195, 17, 1
	v_add_f32_e32 v0, v113, v0
	v_exp_f32_e32 v126, v179
	v_and_b32_e32 v3, v177, v3
	v_bfe_i32 v177, v195, 18, 1
	v_add_f32_e32 v0, v0, v2
	v_and_b32_e32 v177, v177, v13
	v_add_f32_e32 v0, v0, v3
	v_bfe_i32 v13, v195, 19, 1
	v_add_f32_e32 v0, v0, v177
	v_and_b32_e32 v178, v13, v14
	v_exp_f32_e32 v174, v174
	v_bfe_i32 v13, v195, 20, 1
	v_add_f32_e32 v0, v0, v178
	v_and_b32_e32 v179, v13, v15
	v_exp_f32_e32 v175, v175
	v_bfe_i32 v13, v195, 21, 1
	v_add_f32_e32 v0, v0, v179
	v_and_b32_e32 v126, v13, v126
	v_exp_f32_e32 v172, v172
	v_bfe_i32 v13, v195, 22, 1
	v_add_f32_e32 v0, v0, v126
	v_and_b32_e32 v127, v13, v127
	v_exp_f32_e32 v173, v173
	v_bfe_i32 v13, v195, 23, 1
	v_add_f32_e32 v0, v0, v127
	v_and_b32_e32 v176, v13, v176
	v_exp_f32_e32 v170, v170
	v_bfe_i32 v13, v195, 24, 1
	v_add_f32_e32 v0, v0, v176
	v_and_b32_e32 v174, v13, v174
	v_exp_f32_e32 v171, v171
	v_bfe_i32 v13, v195, 25, 1
	v_add_f32_e32 v0, v0, v174
	v_and_b32_e32 v175, v13, v175
	v_exp_f32_e32 v168, v168
	v_bfe_i32 v13, v195, 26, 1
	v_add_f32_e32 v0, v0, v175
	v_and_b32_e32 v172, v13, v172
	v_exp_f32_e32 v169, v169
	v_bfe_i32 v13, v195, 27, 1
	v_add_f32_e32 v0, v0, v172
	v_and_b32_e32 v173, v13, v173
	v_bfe_i32 v13, v195, 28, 1
	v_add_f32_e32 v0, v0, v173
	v_and_b32_e32 v170, v13, v170
	v_bfe_i32 v13, v195, 29, 1
	v_add_f32_e32 v0, v0, v170
	v_and_b32_e32 v171, v13, v171
	v_bfe_i32 v13, v195, 30, 1
	v_add_f32_e32 v0, v0, v171
	v_and_b32_e32 v168, v13, v168
	v_bfe_i32 v13, v195, 31, 1
	v_add_f32_e32 v0, v0, v168
	v_and_b32_e32 v169, v13, v169
	v_add_f32_e32 v0, v0, v169
	v_mov_b32_e32 v13, v0
	s_nop 1
	v_permlane32_swap_b32_e32 v0, v13
	v_add_f32_e32 v0, v0, v13
	v_fmac_f32_e32 v0, v215, v214
	v_cvt_pk_bf16_f32 v13, v124, v125
	v_cvt_pk_bf16_f32 v14, v122, v123
	v_cvt_pk_bf16_f32 v15, v120, v121
	v_cvt_pk_bf16_f32 v118, v118, v119
	v_cvt_pk_bf16_f32 v119, v116, v117
	v_cvt_pk_bf16_f32 v120, v114, v115
	v_cvt_pk_bf16_f32 v121, v112, v113
	v_cvt_pk_bf16_f32 v112, v2, v3
	v_cvt_pk_bf16_f32 v113, v177, v178
	v_cvt_pk_bf16_f32 v114, v179, v126
	v_cvt_pk_bf16_f32 v115, v127, v176
	v_cvt_pk_bf16_f32 v122, v174, v175
	v_cvt_pk_bf16_f32 v123, v172, v173
	v_cvt_pk_bf16_f32 v124, v170, v171
	v_cvt_pk_bf16_f32 v125, v168, v169
	s_nop 0
	v_permlane32_swap_b32_e32 v12, v14
	v_permlane32_swap_b32_e32 v13, v15
	v_permlane32_swap_b32_e32 v118, v120
	v_permlane32_swap_b32_e32 v119, v121
	v_permlane32_swap_b32_e32 v112, v114
	v_permlane32_swap_b32_e32 v113, v115
	v_permlane32_swap_b32_e32 v122, v124
	v_permlane32_swap_b32_e32 v123, v125
	ds_read_b64_tr_b16 v[168:169], v206 offset:0
	ds_read_b64_tr_b16 v[170:171], v206 offset:0x800
	ds_read_b64_tr_b16 v[172:173], v206 offset:0x1000
	ds_read_b64_tr_b16 v[174:175], v206 offset:0x1800
	ds_read_b64_tr_b16 v[176:177], v206 offset:0x2000
	ds_read_b64_tr_b16 v[178:179], v206 offset:0x2800
	ds_read_b64_tr_b16 v[180:181], v206 offset:0x3000
	ds_read_b64_tr_b16 v[182:183], v206 offset:0x3800
	s_waitcnt lgkmcnt(0)
	s_nop 0
	v_mfma_f32_32x32x16_bf16 v[64:79], v[12:15], v[168:171], v[64:79]
	ds_read_b64_tr_b16 v[168:169], v206 offset:0x200
	ds_read_b64_tr_b16 v[170:171], v206 offset:0xa00
	v_mfma_f32_32x32x16_bf16 v[64:79], v[118:121], v[172:175], v[64:79]
	ds_read_b64_tr_b16 v[172:173], v206 offset:0x1200
	ds_read_b64_tr_b16 v[174:175], v206 offset:0x1a00
	v_mfma_f32_32x32x16_bf16 v[64:79], v[112:115], v[176:179], v[64:79]
	ds_read_b64_tr_b16 v[176:177], v206 offset:0x2200
	ds_read_b64_tr_b16 v[178:179], v206 offset:0x2a00
	ds_read_b64_tr_b16 v[186:187], v206 offset:0x3200
	ds_read_b64_tr_b16 v[188:189], v206 offset:0x3a00
	s_waitcnt lgkmcnt(0)
; #define SBAR() __builtin_amdgcn_sched_barrier(0)
; #define RESC(a) do { if (__any((a) < 1.f)) { if (hi == 0) al_l[r32] = (a); asm volatile("s_waitcnt lgkmcnt(0)" ::: "memory");              \
;                      for (int d_ = 0; d_ < 4; ++d_) for (int r = 0; r < 16; ++r) o[d_][r] *= al_l[crow(r, hi)]; } } while (0)
; #define MASKT(P0_, P1_, t) do { } while (0)
; template <bool SEL>
; __device__ __forceinline__ void partialSM(f32x16& p0, f32x16& p1, float& m_reg, float& mn, float& alpha, unsigned selw) {
;     float pmax = p0[0];
; #pragma unroll
;     for (int r = 1; r < 16; ++r) pmax = fmaxf(pmax, p0[r]);
; #pragma unroll
;     for (int r = 0; r < 16; ++r) pmax = fmaxf(pmax, p1[r]);
;     { auto rr = __builtin_amdgcn_permlane32_swap(__float_as_uint(pmax), __float_as_uint(pmax), false, false);
;       pmax = fmaxf(__uint_as_float(rr[0]), __uint_as_float(rr[1])); }
;     constexpr float C2 = 1.4426950408889634f * SCALE;
;     if (__builtin_expect(__all((pmax - m_reg) * SCALE <= THR), 1)) { mn = m_reg; alpha = 1.f; }
;     else { mn = fmaxf(m_reg, pmax); alpha = __builtin_amdgcn_exp2f((m_reg - mn) * C2); m_reg = mn; }
; template <int QS, int KS, int OS, bool SEL, int QREG, bool MERGE>
; __device__ __forceinline__ void attn_block(const BlockRef& cur, const BlockRef& nxt, int skv, int W, char* lds, Seam& S, const MergeArgs& MG, const int wid) {
;     ...
;     pv_tile<0>(o, vb0, pa0, pa1, pa2, pa3);
;     if (even) { MASKT(pB0, pB1, NT - 1); partialSM<SEL>(pB0, pB1, m_reg, mnB, alB, mwB); __syncthreads(); RESC(alB);
;         finishSM<SEL>(pB0, pB1, alB, l_reg, pa0, pa1, pa2, pa3, mwB); SBAR(); pv_tile<1>(o, vb0, pa0, pa1, pa2, pa3); }
	v_mfma_f32_32x32x16_bf16 v[64:79], v[122:125], v[180:183], v[64:79]
	v_mfma_f32_32x32x16_bf16 v[48:63], v[12:15], v[168:171], v[48:63]
	ds_read_b64_tr_b16 v[168:169], v206 offset:0x400
	ds_read_b64_tr_b16 v[170:171], v206 offset:0xc00
	v_mfma_f32_32x32x16_bf16 v[48:63], v[118:121], v[172:175], v[48:63]
	ds_read_b64_tr_b16 v[172:173], v206 offset:0x1400
	ds_read_b64_tr_b16 v[174:175], v206 offset:0x1c00
	v_mfma_f32_32x32x16_bf16 v[48:63], v[112:115], v[176:179], v[48:63]
	ds_read_b64_tr_b16 v[176:177], v206 offset:0x2400
	ds_read_b64_tr_b16 v[178:179], v206 offset:0x2c00
	ds_read_b64_tr_b16 v[180:181], v206 offset:0x3400
	ds_read_b64_tr_b16 v[182:183], v206 offset:0x3c00
	s_waitcnt lgkmcnt(0)
	v_mfma_f32_32x32x16_bf16 v[48:63], v[122:125], v[186:189], v[48:63]
	v_mfma_f32_32x32x16_bf16 v[32:47], v[12:15], v[168:171], v[32:47]
	ds_read_b64_tr_b16 v[168:169], v206 offset:0x600
	ds_read_b64_tr_b16 v[170:171], v206 offset:0xe00
	v_mfma_f32_32x32x16_bf16 v[32:47], v[118:121], v[172:175], v[32:47]
	ds_read_b64_tr_b16 v[172:173], v206 offset:0x1600
	ds_read_b64_tr_b16 v[174:175], v206 offset:0x1e00
	v_mfma_f32_32x32x16_bf16 v[32:47], v[112:115], v[176:179], v[32:47]
	ds_read_b64_tr_b16 v[176:177], v206 offset:0x2600
	ds_read_b64_tr_b16 v[178:179], v206 offset:0x2e00
	ds_read_b64_tr_b16 v[186:187], v206 offset:0x3600
	ds_read_b64_tr_b16 v[188:189], v206 offset:0x3e00
	s_waitcnt lgkmcnt(0)
	v_mfma_f32_32x32x16_bf16 v[32:47], v[122:125], v[180:183], v[32:47]
	v_mfma_f32_32x32x16_bf16 v[16:31], v[12:15], v[168:171], v[16:31]
	s_andn2_b64 vcc, exec, s[0:1]
	v_mfma_f32_32x32x16_bf16 v[16:31], v[118:121], v[172:175], v[16:31]
	v_mfma_f32_32x32x16_bf16 v[16:31], v[112:115], v[176:179], v[16:31]
	v_mfma_f32_32x32x16_bf16 v[16:31], v[122:125], v[186:189], v[16:31]
	s_cbranch_vccnz .LBB0_1832
	v_max_f32_e32 v2, v81, v81
	v_max_f32_e32 v3, v80, v80
	v_max_f32_e32 v2, v3, v2
	v_max3_f32 v2, v2, v82, v83
	v_max3_f32 v2, v2, v84, v85
	v_max3_f32 v2, v2, v86, v87
	v_max3_f32 v2, v2, v88, v89
	v_max3_f32 v2, v2, v90, v91
	v_max3_f32 v2, v2, v92, v93
	v_max3_f32 v2, v2, v94, v95
	v_max3_f32 v2, v2, v96, v97
	v_max3_f32 v2, v2, v98, v99
	v_max3_f32 v2, v2, v100, v101
	v_max3_f32 v2, v2, v102, v103
	v_max3_f32 v2, v2, v104, v105
	v_max3_f32 v2, v2, v106, v107
	v_max3_f32 v2, v2, v108, v109
	v_max3_f32 v2, v2, v110, v111
	v_mov_b32_e32 v3, v2
	s_nop 1
	v_permlane32_swap_b32_e32 v2, v3
	v_max_f32_e32 v3, v3, v3
	v_max_f32_e32 v2, v2, v2
	v_max_f32_e32 v2, v2, v3
	v_max_f32_e32 v12, v184, v184
	v_max_f32_e32 v123, v12, v2
	v_sub_f32_e32 v3, v2, v184
	v_sub_f32_e32 v2, v184, v123
	v_mul_f32_e32 v2, 0x3e0293ee, v2
	v_mul_f32_e32 v3, 0x3db504f3, v3
	v_exp_f32_e32 v2, v2
	v_cmp_ge_f32_e32 vcc, s5, v3
	s_cmp_eq_u64 vcc, exec
	s_cselect_b64 s[0:1], -1, 0
	v_cndmask_b32_e64 v2, v2, 1.0, s[0:1]
	v_cmp_gt_f32_e32 vcc, 1.0, v2
	s_waitcnt vmcnt(12)
	v_bfe_i32 v3, v217, 0, 1
	v_bfe_i32 v12, v217, 1, 1
	v_bfe_i32 v13, v217, 2, 1
	v_bfe_i32 v14, v217, 3, 1
	v_bfe_i32 v15, v217, 4, 1
	v_bfe_i32 v112, v217, 5, 1
	v_bfe_i32 v113, v217, 6, 1
	v_bfe_i32 v114, v217, 7, 1
	v_bfe_i32 v115, v217, 8, 1
	v_bfe_i32 v116, v217, 9, 1
	v_bfe_i32 v117, v217, 10, 1
	v_bfe_i32 v118, v217, 11, 1
	v_bfe_i32 v119, v217, 12, 1
	v_bfe_i32 v120, v217, 13, 1
	v_bfe_i32 v121, v217, 14, 1
	v_bfe_i32 v122, v217, 15, 1
	s_barrier
	s_cbranch_vccz .LBB0_1831
	v_cmp_gt_u32_e32 vcc, 32, v200
	s_and_saveexec_b64 s[2:3], vcc
	ds_write_b32 v205, v2 offset:128
	s_or_b64 exec, exec, s[2:3]
	s_waitcnt lgkmcnt(0)
	v_add_u32_e32 v176, s66, v203
	ds_read_b128 v[124:127], v176 offset:224
	ds_read_b128 v[168:171], v176 offset:192
	ds_read_b128 v[172:175], v176 offset:160
	ds_read_b128 v[176:179], v176 offset:128
	s_waitcnt lgkmcnt(3)
	v_mul_f32_e64 v76, v76, v124
	v_mul_f32_e64 v77, v77, v125
	s_waitcnt lgkmcnt(2)
	v_mul_f32_e64 v72, v72, v168
	v_mul_f32_e64 v73, v73, v169
	s_waitcnt lgkmcnt(1)
	v_mul_f32_e64 v68, v68, v172
	v_mul_f32_e64 v69, v69, v173
	v_mul_f32_e64 v78, v78, v126
	v_mul_f32_e64 v79, v79, v127
	v_mul_f32_e64 v74, v74, v170
	v_mul_f32_e64 v75, v75, v171
	v_mul_f32_e64 v70, v70, v174
	v_mul_f32_e64 v71, v71, v175
	s_waitcnt lgkmcnt(0)
	v_mul_f32_e64 v66, v66, v178
	v_mul_f32_e64 v67, v67, v179
	v_mul_f32_e64 v64, v64, v176
	v_mul_f32_e64 v65, v65, v177
	v_mul_f32_e64 v60, v60, v124
	v_mul_f32_e64 v61, v61, v125
	v_mul_f32_e64 v56, v56, v168
	v_mul_f32_e64 v57, v57, v169
	v_mul_f32_e64 v52, v52, v172
	v_mul_f32_e64 v53, v53, v173
	v_mul_f32_e64 v62, v62, v126
	v_mul_f32_e64 v63, v63, v127
	v_mul_f32_e64 v58, v58, v170
	v_mul_f32_e64 v59, v59, v171
	v_mul_f32_e64 v54, v54, v174
	v_mul_f32_e64 v55, v55, v175
	v_mul_f32_e64 v50, v50, v178
	v_mul_f32_e64 v51, v51, v179
	v_mul_f32_e64 v48, v48, v176
	v_mul_f32_e64 v49, v49, v177
	v_mul_f32_e64 v44, v44, v124
	v_mul_f32_e64 v45, v45, v125
	v_mul_f32_e64 v40, v40, v168
	v_mul_f32_e64 v41, v41, v169
	v_mul_f32_e64 v36, v36, v172
	v_mul_f32_e64 v37, v37, v173
	v_mul_f32_e64 v46, v46, v126
	v_mul_f32_e64 v47, v47, v127
	v_mul_f32_e64 v42, v42, v170
	v_mul_f32_e64 v43, v43, v171
	v_mul_f32_e64 v38, v38, v174
	v_mul_f32_e64 v39, v39, v175
	v_mul_f32_e64 v34, v34, v178
	v_mul_f32_e64 v35, v35, v179
	v_mul_f32_e64 v32, v32, v176
	v_mul_f32_e64 v33, v33, v177
	v_mul_f32_e64 v28, v28, v124
	v_mul_f32_e64 v29, v29, v125
	v_mul_f32_e64 v24, v24, v168
	v_mul_f32_e64 v25, v25, v169
	v_mul_f32_e64 v20, v20, v172
	v_mul_f32_e64 v21, v21, v173
	v_mul_f32_e64 v30, v30, v126
	v_mul_f32_e64 v31, v31, v127
	v_mul_f32_e64 v26, v26, v170
	v_mul_f32_e64 v27, v27, v171
	v_mul_f32_e64 v22, v22, v174
	v_mul_f32_e64 v23, v23, v175
	v_mul_f32_e64 v18, v18, v178
	v_mul_f32_e64 v19, v19, v179
	v_mul_f32_e64 v16, v16, v176
	v_mul_f32_e64 v17, v17, v177

; __device__ __forceinline__ unsigned cvt_pk_bf16(float lo, float hi) { unsigned r; asm volatile("v_cvt_pk_bf16_f32 %0, %1, %2" : "=v"(r) : "v"(lo), "v"(hi)); return r; }
; __device__ __forceinline__ float bf_lo(unsigned w) { return __uint_as_float(w << 16); }
; __device__ __forceinline__ float bf_hi(unsigned w) { return __uint_as_float(w & 0xffff0000u); }
; template <int QS, int KS, int OS, bool SEL, int QREG, bool MERGE>
; __device__ __forceinline__ void attn_block(const BlockRef& cur, const BlockRef& nxt, int skv, int W, char* lds, Seam& S, const MergeArgs& MG, const int wid) {
;     ...
;             for (int p = 0; p < 8; ++p) {
;                 const int row = 4 * p + rq;
;                 const size_t e = eoff + (size_t)row * OS;
;                 const u32x4 y = *(const u32x4*)(stg + row * 256 + ch * 16);
;                 if (p < 7) MG_LOAD(p + 1, na, nga, np2, np1, np0);
;                 float ov[8];
; #pragma unroll
;                 for (int j = 0; j < 4; ++j) {
;                     ov[2 * j] = bf_lo(ca[j]) * (w0[2 * j] * bf_lo(cp0[j]) + w1[2 * j] * bf_lo(cp1[j]) + w2[2 * j] * bf_lo(cp2[j])) + bf_lo(cga[j]) * bf_lo(y[j]);
;                     ov[2 * j + 1] = bf_hi(ca[j]) * (w0[2 * j + 1] * bf_hi(cp0[j]) + w1[2 * j + 1] * bf_hi(cp1[j]) + w2[2 * j + 1] * bf_hi(cp2[j])) + bf_hi(cga[j]) * bf_hi(y[j]);
;                 }
;                 u32x4 wv_; wv_.x = cvt_pk_bf16(ov[0], ov[1]); wv_.y = cvt_pk_bf16(ov[2], ov[3]); wv_.z = cvt_pk_bf16(ov[4], ov[5]); wv_.w = cvt_pk_bf16(ov[6], ov[7]);
;                 *(u32x4*)(MOUT + e) = wv_;
;                 ca = na; cga = nga; cp2 = np2; cp1 = np1; cp0 = np0;
.Lmg_nowait:
	v_lshlrev_b32_e32 v2, 16, v52
	v_lshlrev_b32_e32 v3, 16, v44
	v_lshlrev_b32_e32 v0, 16, v48
	v_mul_f32_e64 v2, v16, v2
	v_mul_f32_e64 v3, v17, v3
	s_waitcnt lgkmcnt(0)
	v_lshlrev_b32_e32 v87, 16, v76
	v_fma_f32 v0, v20, v0, v2
	v_add_f32_e32 v2, v0, v3
	v_lshlrev_b32_e32 v3, 16, v40
	v_lshlrev_b32_e32 v86, 16, v36
	v_mul_f32_e64 v2, v2, v86
	v_mul_f32_e64 v3, v3, v87
	v_and_b32_e32 v48, 0xffff0000, v48
	v_add_f32_e32 v0, v2, v3
	v_and_b32_e32 v3, 0xffff0000, v44
	v_and_b32_e32 v2, 0xffff0000, v52
	v_mul_f32_e64 v2, v28, v2
	v_mul_f32_e64 v3, v29, v3
	v_and_b32_e32 v87, 0xffff0000, v76
	v_fma_f32 v2, v21, v48, v2
	v_add_f32_e32 v2, v2, v3
	v_and_b32_e32 v3, 0xffff0000, v40
	v_and_b32_e32 v86, 0xffff0000, v36
	v_mul_f32_e64 v2, v2, v86
	v_mul_f32_e64 v3, v3, v87
	v_lshlrev_b32_e32 v36, 16, v49
	v_add_f32_e32 v44, v2, v3
	v_lshlrev_b32_e32 v2, 16, v53
	v_lshlrev_b32_e32 v3, 16, v45
	v_mul_f32_e64 v2, v18, v2
	v_mul_f32_e64 v3, v19, v3
	v_lshlrev_b32_e32 v87, 16, v77
	v_fma_f32 v2, v22, v36, v2
	v_add_f32_e32 v2, v2, v3
	v_lshlrev_b32_e32 v3, 16, v41
	v_lshlrev_b32_e32 v86, 16, v37
	v_mul_f32_e64 v2, v2, v86
	v_mul_f32_e64 v3, v3, v87
	v_and_b32_e32 v36, 0xffff0000, v49
	v_add_f32_e32 v48, v2, v3
	v_and_b32_e32 v3, 0xffff0000, v45
	v_and_b32_e32 v2, 0xffff0000, v53
	v_mul_f32_e64 v2, v30, v2
	v_mul_f32_e64 v3, v31, v3
	v_and_b32_e32 v40, 0xffff0000, v37
	v_fma_f32 v2, v23, v36, v2
	v_add_f32_e32 v2, v2, v3
	v_and_b32_e32 v3, 0xffff0000, v41
	v_and_b32_e32 v41, 0xffff0000, v77
	v_mul_f32_e64 v2, v2, v40
	v_mul_f32_e64 v3, v3, v41
	v_lshlrev_b32_e32 v36, 16, v50
	v_add_f32_e32 v40, v2, v3
	v_lshlrev_b32_e32 v2, 16, v54
	v_lshlrev_b32_e32 v3, 16, v46
	v_mul_f32_e64 v2, v12, v2
	v_mul_f32_e64 v3, v13, v3
	v_lshlrev_b32_e32 v37, 16, v78
	v_fma_f32 v2, v24, v36, v2
	v_add_f32_e32 v2, v2, v3
	v_lshlrev_b32_e32 v3, 16, v42
	v_lshlrev_b32_e32 v36, 16, v38
	v_mul_f32_e64 v2, v2, v36
	v_mul_f32_e64 v3, v3, v37
	v_and_b32_e32 v36, 0xffff0000, v50
	v_add_f32_e32 v41, v2, v3
	v_and_b32_e32 v3, 0xffff0000, v46
	v_and_b32_e32 v2, 0xffff0000, v54
	v_mul_f32_e64 v2, v32, v2
	v_mul_f32_e64 v3, v33, v3
	v_and_b32_e32 v37, 0xffff0000, v78
	v_fma_f32 v2, v25, v36, v2
	v_add_f32_e32 v2, v2, v3
	v_and_b32_e32 v3, 0xffff0000, v42
	v_and_b32_e32 v36, 0xffff0000, v38
	v_mul_f32_e64 v2, v2, v36
	v_mul_f32_e64 v3, v3, v37
	v_lshlrev_b32_e32 v36, 16, v51
	v_add_f32_e32 v38, v2, v3
	v_lshlrev_b32_e32 v2, 16, v55
	v_lshlrev_b32_e32 v3, 16, v47
	v_mul_f32_e64 v2, v14, v2
	v_mul_f32_e64 v3, v15, v3
	v_lshlrev_b32_e32 v37, 16, v79
	v_fma_f32 v2, v26, v36, v2
	v_add_f32_e32 v2, v2, v3
	v_lshlrev_b32_e32 v3, 16, v43
	v_lshlrev_b32_e32 v36, 16, v39
	v_mul_f32_e64 v2, v2, v36
	v_mul_f32_e64 v3, v3, v37
	v_and_b32_e32 v36, 0xffff0000, v51
	v_add_f32_e32 v42, v2, v3
	v_and_b32_e32 v3, 0xffff0000, v47
	v_and_b32_e32 v2, 0xffff0000, v55
	v_mul_f32_e64 v2, v34, v2
	v_mul_f32_e64 v3, v35, v3
	v_and_b32_e32 v37, 0xffff0000, v79
	v_fma_f32 v2, v27, v36, v2
	v_add_f32_e32 v2, v2, v3
	v_and_b32_e32 v3, 0xffff0000, v43
	v_and_b32_e32 v36, 0xffff0000, v39
	v_mul_f32_e64 v2, v2, v36
	v_mul_f32_e64 v3, v3, v37
	v_cvt_pk_bf16_f32 v36, v0, v44
	v_cvt_pk_bf16_f32 v37, v48, v40
	v_cvt_pk_bf16_f32 v38, v41, v38
	s_add_u32 s0, s0, 0x4000
	v_add_f32_e32 v2, v2, v3
	v_cvt_pk_bf16_f32 v39, v42, v2
	v_add_co_u32_e32 v2, vcc, s83, v82
	s_addc_u32 s1, s1, 0
	s_nop 0
	v_addc_co_u32_e32 v3, vcc, 0, v83, vcc
	global_store_dwordx4 v[2:3], v[36:39], off
	s_waitcnt vmcnt(1)
	v_mov_b64_e32 v[48:49], v[68:69]
	v_mov_b64_e32 v[44:45], v[64:65]
	v_mov_b64_e32 v[40:41], v[60:61]
	v_mov_b64_e32 v[36:37], v[56:57]
	v_add_u32_e32 v84, 4, v84
	v_add_u32_e32 v85, 0x400, v85
	s_cmp_lg_u32 s0, 0x20000
	v_mov_b64_e32 v[50:51], v[70:71]
	v_mov_b64_e32 v[46:47], v[66:67]
	v_mov_b64_e32 v[42:43], v[62:63]
	v_mov_b64_e32 v[38:39], v[58:59]
	v_mov_b32_e32 v52, v72
	v_mov_b32_e32 v53, v73
	v_mov_b32_e32 v54, v74
	v_mov_b32_e32 v55, v75
	s_cbranch_scc0 .LBB0_1790

; __device__ __forceinline__ float bf_lo(unsigned w) { return __uint_as_float(w << 16); }
; __device__ __forceinline__ float bf_hi(unsigned w) { return __uint_as_float(w & 0xffff0000u); }
;     __device__ __forceinline__ void operator()(const f32x4 (&acc)[2][2][4][2], const Unit& u, int wr, int wc, int fr, int fq, const Pre&) const {
;         const size_t off0 = (size_t)(u.pm * 256 + wr * 64 + fr) * DM + u.pn * 256 + 32 * wc + 8 * fq;
;         u32x4 rb[2][4][2];
;         if (!RF32) {
; #pragma unroll
;             for (int ai = 0; ai < 2; ++ai)
; #pragma unroll
;                 for (int m = 0; m < 4; ++m)
; #pragma unroll
;                     for (int bj = 0; bj < 2; ++bj) rb[ai][m][bj] = *(const u32x4*)((const bf16_t*)resid + off0 + (size_t)(ai * 128 + m * 16) * DM + 128 * bj);
;         }
; #pragma unroll
;         for (int ai = 0; ai < 2; ++ai) {
;             f32x4 r0[4][2], r1[4][2];
; #pragma unroll
;             for (int m = 0; m < 4; ++m)
; #pragma unroll
;                 for (int bj = 0; bj < 2; ++bj) {
;                     const size_t off = off0 + (size_t)(ai * 128 + m * 16) * DM + 128 * bj;
;                     if (RF32) { r0[m][bj] = *(const f32x4*)((const float*)resid + off); r1[m][bj] = *(const f32x4*)((const float*)resid + off + 4); }
;                     else { const u32x4 rbv = rb[ai][m][bj];
;                         r0[m][bj] = (f32x4){bf_lo(rbv.x), bf_hi(rbv.x), bf_lo(rbv.y), bf_hi(rbv.y)}; r1[m][bj] = (f32x4){bf_lo(rbv.z), bf_hi(rbv.z), bf_lo(rbv.w), bf_hi(rbv.w)}; }
;                 }
; #pragma unroll
;             for (int m = 0; m < 4; ++m) {
;                 const int row = u.pm * 256 + ai * 128 + wr * 64 + m * 16 + fr; float sq = 0.f;
; #pragma unroll
;                 for (int bj = 0; bj < 2; ++bj) {
;                     const size_t off = off0 + (size_t)(ai * 128 + m * 16) * DM + 128 * bj;
;                     const f32x4 v0 = acc[ai][bj][m][0] + r0[m][bj], v1 = acc[ai][bj][m][1] + r1[m][bj];
;                     st_bf16x8(hb + off, v0, v1);
;                     sq += v0[0] * v0[0] + v0[1] * v0[1] + v0[2] * v0[2] + v0[3] * v0[3] + v1[0] * v1[0] + v1[1] * v1[1] + v1[2] * v1[2] + v1[3] * v1[3];
;                 }
;                 if (ss) { sq += __shfl_xor(sq, 16); sq += __shfl_xor(sq, 32); if (fq == 0) atomicAdd(ss + row, sq); }
;             }
.LBB0_2065:
	s_lshl_b32 s0, s40, 8
	s_add_i32 s0, s0, s67
	v_mbcnt_lo_u32_b32 v182, -1, 0
	v_mbcnt_hi_u32_b32 v182, -1, v182
	v_readlane_b32 s40, v249, 3
	v_and_or_b32 v176, v182, 15, s0
	s_lshl_b32 s0, s90, 8
	v_ashrrev_i32_e32 v130, 1, v182
	s_ashr_i32 s1, s0, 31
	v_and_b32_e32 v130, -8, v130
	v_ashrrev_i32_e32 v177, 31, v176
	v_ashrrev_i32_e32 v131, 31, v130
	s_or_b64 s[0:1], s[0:1], s[4:5]
	v_lshlrev_b64 v[128:129], 11, v[176:177]
	v_lshl_add_u64 v[130:131], s[0:1], 0, v[130:131]
	v_lshl_add_u64 v[178:179], v[130:131], 0, v[128:129]
	v_readlane_b32 s41, v249, 4
	s_mov_b64 s[0:1], 0x20200
	v_and_b32_e32 v238, 64, v237
	v_lshl_add_u64 v[180:181], v[178:179], 2, s[40:41]
	global_load_dwordx4 v[184:187], v[180:181], off
	global_load_dwordx4 v[188:191], v[180:181], off offset:16
	global_load_dwordx4 v[222:225], v[180:181], off offset:512
	global_load_dwordx4 v[226:229], v[180:181], off offset:528
	v_add_co_u32_e32 v130, vcc, s81, v180
	v_lshl_add_u64 v[128:129], v[180:181], 0, s[14:15]
	s_nop 0
	v_addc_co_u32_e32 v131, vcc, 0, v181, vcc
	global_load_dwordx4 v[172:175], v[130:131], off
	global_load_dwordx4 v[168:171], v[128:129], off offset:16
	v_lshl_add_u64 v[128:129], v[180:181], 0, s[0:1]
	s_mov_b64 s[0:1], 0x40000
	global_load_dwordx4 v[164:167], v[130:131], off offset:512
	global_load_dwordx4 v[160:163], v[128:129], off offset:16
	v_lshl_add_u64 v[128:129], v[180:181], 0, s[0:1]
	s_mov_b32 s0, 0x40000
	v_add_co_u32_e32 v130, vcc, s0, v180
	s_mov_b64 s[0:1], 0x40200
	s_nop 0
	v_addc_co_u32_e32 v131, vcc, 0, v181, vcc
	global_load_dwordx4 v[156:159], v[130:131], off
	global_load_dwordx4 v[152:155], v[128:129], off offset:16
	v_lshl_add_u64 v[128:129], v[180:181], 0, s[0:1]
	s_mov_b64 s[0:1], 0x60000
	global_load_dwordx4 v[148:151], v[130:131], off offset:512
	global_load_dwordx4 v[144:147], v[128:129], off offset:16
	v_lshl_add_u64 v[128:129], v[180:181], 0, s[0:1]
	s_mov_b32 s0, 0x60000
	v_add_co_u32_e32 v130, vcc, s0, v180
	s_mov_b64 s[0:1], 0x60200
	s_nop 0
	v_addc_co_u32_e32 v131, vcc, 0, v181, vcc
	global_load_dwordx4 v[140:143], v[130:131], off
	global_load_dwordx4 v[136:139], v[128:129], off offset:16
	v_lshl_add_u64 v[128:129], v[180:181], 0, s[0:1]
	global_load_dwordx4 v[132:135], v[130:131], off offset:512
	s_nop 0
	global_load_dwordx4 v[128:131], v[128:129], off offset:16
	v_xor_b32_e32 v183, 16, v237
	v_cmp_gt_u32_e64 s[0:1], 16, v182
	v_add_u32_e32 v182, 64, v238
	v_cmp_lt_i32_e32 vcc, v183, v182
	v_xor_b32_e32 v239, 32, v237
	v_lshl_add_u64 v[178:179], v[178:179], 1, s[6:7]
	v_cndmask_b32_e32 v183, v237, v183, vcc
	v_cmp_lt_i32_e32 vcc, v239, v182
	v_lshlrev_b32_e32 v182, 2, v183
	v_readlane_b32 s42, v249, 5
	v_cndmask_b32_e32 v238, v237, v239, vcc
	v_readlane_b32 s43, v249, 6
	v_readlane_b32 s44, v249, 7
	v_readlane_b32 s45, v249, 8
	v_readlane_b32 s46, v249, 9
	v_readlane_b32 s47, v249, 10
	v_readlane_b32 s48, v249, 11
	v_readlane_b32 s49, v249, 12
	v_readlane_b32 s50, v249, 13
	v_readlane_b32 s51, v249, 14
	v_readlane_b32 s52, v249, 15
	v_readlane_b32 s53, v249, 16
	v_readlane_b32 s54, v249, 17
	v_readlane_b32 s55, v249, 18
	s_waitcnt vmcnt(0)
	v_add_f32_e64 v124, v124, v184
	v_add_f32_e64 v125, v125, v185
	v_add_f32_e64 v126, v126, v186
	v_add_f32_e64 v127, v127, v187
	v_add_f32_e64 v108, v108, v222
	v_add_f32_e64 v109, v109, v223
	v_add_f32_e64 v184, v106, v228
	v_add_f32_e64 v185, v107, v229
	v_add_f32_e64 v186, v104, v226
	v_add_f32_e64 v187, v105, v227
	v_cvt_pk_bf16_f32 v104, v124, v125
	v_mul_f32_e32 v107, v125, v125
	v_mul_f32_e32 v125, v109, v109
	v_add_f32_e64 v110, v110, v224
	v_add_f32_e64 v111, v111, v225
	v_fmac_f32_e32 v107, v124, v124
	v_fmac_f32_e32 v125, v108, v108
	v_fmac_f32_e32 v107, v126, v126
	v_fmac_f32_e32 v125, v110, v110
	v_add_f32_e64 v120, v120, v188
	v_add_f32_e64 v121, v121, v189
	v_fmac_f32_e32 v107, v127, v127
	v_fmac_f32_e32 v125, v111, v111
	v_fmac_f32_e32 v107, v120, v120
	v_fmac_f32_e32 v125, v186, v186
	v_add_f32_e64 v122, v122, v190
	v_add_f32_e64 v123, v123, v191
	v_fmac_f32_e32 v107, v121, v121
	v_fmac_f32_e32 v125, v187, v187
	v_fmac_f32_e32 v107, v122, v122
	v_fmac_f32_e32 v125, v184, v184
	v_fmac_f32_e32 v107, v123, v123
	v_fmac_f32_e32 v125, v185, v185
	v_cvt_pk_bf16_f32 v105, v126, v127
	v_cvt_pk_bf16_f32 v106, v120, v121
	v_add_f32_e32 v120, v107, v125
	ds_bpermute_b32 v121, v182, v120
	v_cvt_pk_bf16_f32 v107, v122, v123
	global_store_dwordx4 v[178:179], v[104:107], off
	v_cvt_pk_bf16_f32 v108, v108, v109
	v_cvt_pk_bf16_f32 v109, v110, v111
	v_cvt_pk_bf16_f32 v110, v186, v187
	v_cvt_pk_bf16_f32 v111, v184, v185
	global_store_dwordx4 v[178:179], v[108:111], off offset:256
	s_waitcnt lgkmcnt(0)
	v_add_f32_e32 v106, v120, v121
	v_lshlrev_b32_e32 v120, 2, v238
	ds_bpermute_b32 v107, v120, v106
	v_lshl_add_u64 v[104:105], v[176:177], 2, s[8:9]
	s_and_saveexec_b64 s[40:41], s[0:1]
	s_cbranch_execz .LBB0_2067
	s_waitcnt lgkmcnt(0)
	v_add_f32_e32 v106, v106, v107
	global_atomic_add_f32 v[104:105], v106, off
;     __device__ __forceinline__ void operator()(const f32x4 (&acc)[2][2][4][2], const Unit& u, int wr, int wc, int fr, int fq, const Pre&) const {
;     ...
; #pragma unroll
;             for (int m = 0; m < 4; ++m) {
;                 const int row = u.pm * 256 + ai * 128 + wr * 64 + m * 16 + fr; float sq = 0.f;
; #pragma unroll
;                 for (int bj = 0; bj < 2; ++bj) {
;                     const size_t off = off0 + (size_t)(ai * 128 + m * 16) * DM + 128 * bj;
;                     const f32x4 v0 = acc[ai][bj][m][0] + r0[m][bj], v1 = acc[ai][bj][m][1] + r1[m][bj];
;                     st_bf16x8(hb + off, v0, v1);
;                     sq += v0[0] * v0[0] + v0[1] * v0[1] + v0[2] * v0[2] + v0[3] * v0[3] + v1[0] * v1[0] + v1[1] * v1[1] + v1[2] * v1[2] + v1[3] * v1[3];
;                 }
;                 if (ss) { sq += __shfl_xor(sq, 16); sq += __shfl_xor(sq, 32); if (fq == 0) atomicAdd(ss + row, sq); }
;             }
.LBB0_2067:
	s_or_b64 exec, exec, s[40:41]
	v_add_f32_e64 v116, v116, v172
	v_add_f32_e64 v117, v117, v173
	v_add_f32_e64 v92, v92, v164
	v_add_f32_e64 v93, v93, v165
	v_add_f32_e64 v122, v88, v160
	v_add_f32_e64 v123, v89, v161
	v_mul_f32_e32 v88, v117, v117
	v_mul_f32_e32 v89, v93, v93
	v_add_f32_e64 v110, v118, v174
	v_add_f32_e64 v111, v119, v175
	v_add_f32_e64 v94, v94, v166
	v_add_f32_e64 v95, v95, v167
	v_fmac_f32_e32 v88, v116, v116
	v_fmac_f32_e32 v89, v92, v92
	v_fmac_f32_e32 v88, v110, v110
	v_fmac_f32_e32 v89, v94, v94
	v_add_f32_e64 v112, v112, v168
	v_add_f32_e64 v113, v113, v169
	v_fmac_f32_e32 v88, v111, v111
	v_fmac_f32_e32 v89, v95, v95
	v_fmac_f32_e32 v88, v112, v112
	v_fmac_f32_e32 v89, v122, v122
	v_add_f32_e64 v114, v114, v170
	v_add_f32_e64 v115, v115, v171
	v_add_f32_e64 v118, v90, v162
	v_add_f32_e64 v119, v91, v163
	v_fmac_f32_e32 v88, v113, v113
	v_fmac_f32_e32 v89, v123, v123
	v_fmac_f32_e32 v88, v114, v114
	v_fmac_f32_e32 v89, v118, v118
	v_fmac_f32_e32 v88, v115, v115
	v_fmac_f32_e32 v89, v119, v119
	v_add_f32_e32 v88, v88, v89
	ds_bpermute_b32 v89, v182, v88
	s_mov_b32 s29, 0x10000
	v_cvt_pk_bf16_f32 v106, v116, v117
	s_waitcnt lgkmcnt(1)
	v_cvt_pk_bf16_f32 v107, v110, v111
	v_add_co_u32_e32 v110, vcc, s29, v178
	s_waitcnt lgkmcnt(0)
	v_add_f32_e32 v88, v88, v89
	ds_bpermute_b32 v89, v120, v88
	v_addc_co_u32_e32 v111, vcc, 0, v179, vcc
	v_cvt_pk_bf16_f32 v108, v112, v113
	v_cvt_pk_bf16_f32 v109, v114, v115
	global_store_dwordx4 v[110:111], v[106:109], off
	v_cvt_pk_bf16_f32 v90, v92, v93
	v_cvt_pk_bf16_f32 v91, v94, v95
	v_cvt_pk_bf16_f32 v92, v122, v123
	v_cvt_pk_bf16_f32 v93, v118, v119
	global_store_dwordx4 v[110:111], v[90:93], off offset:256
	s_and_saveexec_b64 s[40:41], s[0:1]
	s_cbranch_execz .LBB0_2069
	s_waitcnt lgkmcnt(0)
	v_add_f32_e32 v88, v88, v89
	global_atomic_add_f32 v[104:105], v88, off offset:64
.LBB0_2069:
	s_or_b64 exec, exec, s[40:41]
	v_add_f32_e64 v94, v100, v156
	v_add_f32_e64 v95, v101, v157
	v_add_f32_e64 v76, v76, v148
	v_add_f32_e64 v77, v77, v149
	v_add_f32_e64 v92, v102, v158
	v_add_f32_e64 v93, v103, v159
	v_add_f32_e64 v102, v72, v144
	v_add_f32_e64 v103, v73, v145
	v_mul_f32_e32 v72, v95, v95
	v_mul_f32_e32 v73, v77, v77
	v_add_f32_e64 v78, v78, v150
	v_add_f32_e64 v79, v79, v151
	v_fmac_f32_e32 v72, v94, v94
	v_fmac_f32_e32 v73, v76, v76
	v_fmac_f32_e32 v72, v92, v92
	v_fmac_f32_e32 v73, v78, v78
	v_add_f32_e64 v96, v96, v152
	v_add_f32_e64 v97, v97, v153
	v_fmac_f32_e32 v72, v93, v93
	v_fmac_f32_e32 v73, v79, v79
	v_fmac_f32_e32 v72, v96, v96
	v_fmac_f32_e32 v73, v102, v102
	v_add_f32_e64 v98, v98, v154
	v_add_f32_e64 v99, v99, v155
	v_add_f32_e64 v100, v74, v146
	v_add_f32_e64 v101, v75, v147
	v_fmac_f32_e32 v72, v97, v97
	v_fmac_f32_e32 v73, v103, v103
	v_fmac_f32_e32 v72, v98, v98
	v_fmac_f32_e32 v73, v100, v100
	v_fmac_f32_e32 v72, v99, v99
	v_fmac_f32_e32 v73, v101, v101
	v_add_f32_e32 v72, v72, v73
	ds_bpermute_b32 v73, v182, v72
	v_cvt_pk_bf16_f32 v88, v94, v95
	s_waitcnt lgkmcnt(1)
	v_cvt_pk_bf16_f32 v89, v92, v93
	v_add_co_u32_e32 v92, vcc, s81, v178
	s_waitcnt lgkmcnt(0)
	v_add_f32_e32 v72, v72, v73
	ds_bpermute_b32 v73, v120, v72
	v_addc_co_u32_e32 v93, vcc, 0, v179, vcc
	v_cvt_pk_bf16_f32 v90, v96, v97
	v_cvt_pk_bf16_f32 v91, v98, v99
	global_store_dwordx4 v[92:93], v[88:91], off
	v_cvt_pk_bf16_f32 v74, v76, v77
	v_cvt_pk_bf16_f32 v75, v78, v79
	v_cvt_pk_bf16_f32 v76, v102, v103
	v_cvt_pk_bf16_f32 v77, v100, v101
	global_store_dwordx4 v[92:93], v[74:77], off offset:256
	s_and_saveexec_b64 s[40:41], s[0:1]
	s_cbranch_execz .LBB0_2071
	s_waitcnt lgkmcnt(0)
	v_add_f32_e32 v72, v72, v73
	global_atomic_add_f32 v[104:105], v72, off offset:128
.LBB0_2071:
	s_or_b64 exec, exec, s[40:41]
	v_add_f32_e64 v78, v84, v140
	v_add_f32_e64 v79, v85, v141
	v_add_f32_e64 v68, v68, v132
	v_add_f32_e64 v69, v69, v133
	v_add_f32_e64 v76, v86, v142
	v_add_f32_e64 v77, v87, v143
	v_add_f32_e64 v86, v64, v128
	v_add_f32_e64 v87, v65, v129
	v_mul_f32_e32 v64, v79, v79
	v_mul_f32_e32 v65, v69, v69
	v_add_f32_e64 v70, v70, v134
	v_add_f32_e64 v71, v71, v135
	v_fmac_f32_e32 v64, v78, v78
	v_fmac_f32_e32 v65, v68, v68
	v_fmac_f32_e32 v64, v76, v76
	v_fmac_f32_e32 v65, v70, v70
	v_add_f32_e64 v80, v80, v136
	v_add_f32_e64 v81, v81, v137
	v_fmac_f32_e32 v64, v77, v77
	v_fmac_f32_e32 v65, v71, v71
	v_fmac_f32_e32 v64, v80, v80
	v_fmac_f32_e32 v65, v86, v86
	v_add_f32_e64 v82, v82, v138
	v_add_f32_e64 v83, v83, v139
	v_add_f32_e64 v84, v66, v130
	v_add_f32_e64 v85, v67, v131
	v_fmac_f32_e32 v64, v81, v81
	v_fmac_f32_e32 v65, v87, v87
	v_fmac_f32_e32 v64, v82, v82
	v_fmac_f32_e32 v65, v84, v84
	v_fmac_f32_e32 v64, v83, v83
	v_fmac_f32_e32 v65, v85, v85
	v_add_f32_e32 v64, v64, v65
	ds_bpermute_b32 v65, v182, v64
	s_mov_b32 s29, 0x30000
	v_cvt_pk_bf16_f32 v72, v78, v79
	s_waitcnt lgkmcnt(1)
	v_cvt_pk_bf16_f32 v73, v76, v77
	v_add_co_u32_e32 v76, vcc, s29, v178
	s_waitcnt lgkmcnt(0)
	v_add_f32_e32 v64, v64, v65
	ds_bpermute_b32 v65, v120, v64
	v_addc_co_u32_e32 v77, vcc, 0, v179, vcc
	v_cvt_pk_bf16_f32 v74, v80, v81
	v_cvt_pk_bf16_f32 v75, v82, v83
	global_store_dwordx4 v[76:77], v[72:75], off
	v_cvt_pk_bf16_f32 v66, v68, v69
	v_cvt_pk_bf16_f32 v67, v70, v71
	v_cvt_pk_bf16_f32 v68, v86, v87
	v_cvt_pk_bf16_f32 v69, v84, v85
	global_store_dwordx4 v[76:77], v[66:69], off offset:256
	s_and_saveexec_b64 s[40:41], s[0:1]
	s_cbranch_execz .LBB0_2073
	s_waitcnt lgkmcnt(0)
	v_add_f32_e32 v64, v64, v65
	global_atomic_add_f32 v[104:105], v64, off offset:192
; __device__ __forceinline__ float bf_lo(unsigned w) { return __uint_as_float(w << 16); }
; __device__ __forceinline__ float bf_hi(unsigned w) { return __uint_as_float(w & 0xffff0000u); }
;     __device__ __forceinline__ void operator()(const f32x4 (&acc)[2][2][4][2], const Unit& u, int wr, int wc, int fr, int fq, const Pre&) const {
;     ...
;         for (int ai = 0; ai < 2; ++ai) {
;             f32x4 r0[4][2], r1[4][2];
; #pragma unroll
;             for (int m = 0; m < 4; ++m)
; #pragma unroll
;                 for (int bj = 0; bj < 2; ++bj) {
;                     const size_t off = off0 + (size_t)(ai * 128 + m * 16) * DM + 128 * bj;
;                     if (RF32) { r0[m][bj] = *(const f32x4*)((const float*)resid + off); r1[m][bj] = *(const f32x4*)((const float*)resid + off + 4); }
;                     else { const u32x4 rbv = rb[ai][m][bj];
;                         r0[m][bj] = (f32x4){bf_lo(rbv.x), bf_hi(rbv.x), bf_lo(rbv.y), bf_hi(rbv.y)}; r1[m][bj] = (f32x4){bf_lo(rbv.z), bf_hi(rbv.z), bf_lo(rbv.w), bf_hi(rbv.w)}; }
;                 }
; #pragma unroll
;             for (int m = 0; m < 4; ++m) {
;                 const int row = u.pm * 256 + ai * 128 + wr * 64 + m * 16 + fr; float sq = 0.f;
; #pragma unroll
;                 for (int bj = 0; bj < 2; ++bj) {
;                     const size_t off = off0 + (size_t)(ai * 128 + m * 16) * DM + 128 * bj;
;                     const f32x4 v0 = acc[ai][bj][m][0] + r0[m][bj], v1 = acc[ai][bj][m][1] + r1[m][bj];
;                     st_bf16x8(hb + off, v0, v1);
;                     sq += v0[0] * v0[0] + v0[1] * v0[1] + v0[2] * v0[2] + v0[3] * v0[3] + v1[0] * v1[0] + v1[1] * v1[1] + v1[2] * v1[2] + v1[3] * v1[3];
;                 }
;                 if (ss) { sq += __shfl_xor(sq, 16); sq += __shfl_xor(sq, 32); if (fq == 0) atomicAdd(ss + row, sq); }
;             }
.LBB0_2073:
	s_or_b64 exec, exec, s[40:41]
	v_add_co_u32_e32 v64, vcc, 0x100000, v180
	s_mov_b64 s[40:41], 0x100000
	s_waitcnt lgkmcnt(0)
	v_addc_co_u32_e32 v65, vcc, 0, v181, vcc
	v_lshl_add_u64 v[66:67], v[180:181], 0, s[40:41]
	s_mov_b64 s[40:41], 0x100200
	global_load_dwordx4 v[112:115], v[64:65], off
	global_load_dwordx4 v[116:119], v[66:67], off offset:16
	v_lshl_add_u64 v[66:67], v[180:181], 0, s[40:41]
	global_load_dwordx4 v[122:125], v[64:65], off offset:512
	global_load_dwordx4 v[126:129], v[66:67], off offset:16
	s_mov_b64 s[40:41], 0x120000
	v_add_co_u32_e32 v74, vcc, 0x120000, v180
	v_lshl_add_u64 v[64:65], v[180:181], 0, s[40:41]
	s_mov_b64 s[40:41], 0x120200
	v_addc_co_u32_e32 v75, vcc, 0, v181, vcc
	v_lshl_add_u64 v[66:67], v[180:181], 0, s[40:41]
	s_mov_b64 s[40:41], 0x140000
	v_add_co_u32_e32 v76, vcc, 0x140000, v180
	v_lshl_add_u64 v[68:69], v[180:181], 0, s[40:41]
	s_mov_b64 s[40:41], 0x140200
	v_addc_co_u32_e32 v77, vcc, 0, v181, vcc
	v_lshl_add_u64 v[70:71], v[180:181], 0, s[40:41]
	s_mov_b64 s[40:41], 0x160000
	global_load_dwordx4 v[108:111], v[74:75], off
	global_load_dwordx4 v[104:107], v[64:65], off offset:16
	global_load_dwordx4 v[100:103], v[74:75], off offset:512
	global_load_dwordx4 v[96:99], v[66:67], off offset:16
	v_add_co_u32_e32 v64, vcc, 0x160000, v180
	v_lshl_add_u64 v[72:73], v[180:181], 0, s[40:41]
	s_nop 0
	v_addc_co_u32_e32 v65, vcc, 0, v181, vcc
	v_lshl_add_u64 v[130:131], v[180:181], 0, s[16:17]
	global_load_dwordx4 v[92:95], v[76:77], off
	global_load_dwordx4 v[88:91], v[68:69], off offset:16
	global_load_dwordx4 v[84:87], v[76:77], off offset:512
	global_load_dwordx4 v[80:83], v[70:71], off offset:16
	s_nop 0
	global_load_dwordx4 v[76:79], v[64:65], off
	s_nop 0
	global_load_dwordx4 v[72:75], v[72:73], off offset:16
	s_nop 0
	global_load_dwordx4 v[68:71], v[64:65], off offset:512
	s_nop 0
	global_load_dwordx4 v[64:67], v[130:131], off offset:16
	s_waitcnt vmcnt(15)
	v_add_f32_e64 v60, v60, v112
	v_add_f32_e64 v61, v61, v113
	v_add_f32_e64 v62, v62, v114
	v_add_f32_e64 v63, v63, v115
	s_waitcnt vmcnt(13)
	v_add_f32_e64 v56, v56, v122
	v_add_f32_e64 v57, v57, v123
	v_add_f32_e64 v52, v52, v116
	v_add_f32_e64 v53, v53, v117
	s_waitcnt vmcnt(12)
	v_add_f32_e64 v114, v48, v126
	v_add_f32_e64 v115, v49, v127
	v_cvt_pk_bf16_f32 v48, v60, v61
	v_mul_f32_e32 v61, v61, v61
	v_mul_f32_e32 v116, v57, v57
	v_add_f32_e64 v58, v58, v124
	v_add_f32_e64 v59, v59, v125
	v_fmac_f32_e32 v61, v60, v60
	v_fmac_f32_e32 v116, v56, v56
	v_fmac_f32_e32 v61, v62, v62
	v_fmac_f32_e32 v116, v58, v58
	v_fmac_f32_e32 v61, v63, v63
	v_fmac_f32_e32 v116, v59, v59
	v_fmac_f32_e32 v61, v52, v52
	v_fmac_f32_e32 v116, v114, v114
	v_add_f32_e64 v54, v54, v118
	v_add_f32_e64 v55, v55, v119
	v_add_f32_e64 v112, v50, v128
	v_add_f32_e64 v113, v51, v129
	v_fmac_f32_e32 v61, v53, v53
	v_fmac_f32_e32 v116, v115, v115
	v_fmac_f32_e32 v61, v54, v54
	v_fmac_f32_e32 v116, v112, v112
	v_fmac_f32_e32 v61, v55, v55
	v_fmac_f32_e32 v116, v113, v113
	v_cvt_pk_bf16_f32 v49, v62, v63
	v_cvt_pk_bf16_f32 v50, v52, v53
	v_add_f32_e32 v52, v61, v116
	ds_bpermute_b32 v53, v182, v52
	v_cvt_pk_bf16_f32 v51, v54, v55
	v_add_co_u32_e32 v54, vcc, s84, v178
	s_nop 1
	v_addc_co_u32_e32 v55, vcc, 0, v179, vcc
	global_store_dwordx4 v[54:55], v[48:51], off
	s_waitcnt lgkmcnt(0)
	s_nop 0
	v_add_f32_e32 v48, v52, v53
	ds_bpermute_b32 v49, v120, v48
	v_cvt_pk_bf16_f32 v50, v56, v57
	v_cvt_pk_bf16_f32 v51, v58, v59
	v_cvt_pk_bf16_f32 v52, v114, v115
	v_cvt_pk_bf16_f32 v53, v112, v113
	global_store_dwordx4 v[54:55], v[50:53], off offset:256
	s_and_saveexec_b64 s[40:41], s[0:1]
	s_cbranch_execz .LBB0_2075
	v_add_u32_e32 v50, 0x80, v176
	v_ashrrev_i32_e32 v51, 31, v50
	v_lshl_add_u64 v[50:51], v[50:51], 2, s[8:9]
	s_waitcnt lgkmcnt(0)
	v_add_f32_e32 v48, v48, v49
	global_atomic_add_f32 v[50:51], v48, off
;     __device__ __forceinline__ void operator()(const f32x4 (&acc)[2][2][4][2], const Unit& u, int wr, int wc, int fr, int fq, const Pre&) const {
;     ...
; #pragma unroll
;             for (int m = 0; m < 4; ++m) {
;                 const int row = u.pm * 256 + ai * 128 + wr * 64 + m * 16 + fr; float sq = 0.f;
; #pragma unroll
;                 for (int bj = 0; bj < 2; ++bj) {
;                     const size_t off = off0 + (size_t)(ai * 128 + m * 16) * DM + 128 * bj;
;                     const f32x4 v0 = acc[ai][bj][m][0] + r0[m][bj], v1 = acc[ai][bj][m][1] + r1[m][bj];
;                     st_bf16x8(hb + off, v0, v1);
;                     sq += v0[0] * v0[0] + v0[1] * v0[1] + v0[2] * v0[2] + v0[3] * v0[3] + v1[0] * v1[0] + v1[1] * v1[1] + v1[2] * v1[2] + v1[3] * v1[3];
;                 }
;                 if (ss) { sq += __shfl_xor(sq, 16); sq += __shfl_xor(sq, 32); if (fq == 0) atomicAdd(ss + row, sq); }
;             }
.LBB0_2075:
	s_or_b64 exec, exec, s[40:41]
	s_waitcnt vmcnt(13)
	v_add_f32_e64 v44, v44, v108
	v_add_f32_e64 v45, v45, v109
	s_waitcnt vmcnt(12)
	v_add_f32_e64 v50, v32, v104
	v_add_f32_e64 v51, v33, v105
	v_cvt_pk_bf16_f32 v32, v44, v45
	s_waitcnt vmcnt(11)
	v_add_f32_e64 v40, v40, v100
	v_add_f32_e64 v41, v41, v101
	v_mul_f32_e32 v45, v45, v45
	v_fmac_f32_e32 v45, v44, v44
	v_mul_f32_e32 v44, v41, v41
	v_add_f32_e64 v46, v46, v110
	v_add_f32_e64 v47, v47, v111
	v_add_f32_e64 v42, v42, v102
	v_add_f32_e64 v43, v43, v103
	v_fmac_f32_e32 v44, v40, v40
	v_fmac_f32_e32 v45, v46, v46
	v_fmac_f32_e32 v44, v42, v42
	s_waitcnt vmcnt(10)
	v_add_f32_e64 v36, v36, v96
	v_add_f32_e64 v37, v37, v97
	v_fmac_f32_e32 v45, v47, v47
	v_fmac_f32_e32 v44, v43, v43
	v_fmac_f32_e32 v45, v50, v50
	v_fmac_f32_e32 v44, v36, v36
	s_waitcnt lgkmcnt(0)
	v_add_f32_e64 v48, v34, v106
	v_add_f32_e64 v49, v35, v107
	v_add_f32_e64 v38, v38, v98
	v_add_f32_e64 v39, v39, v99
	v_fmac_f32_e32 v45, v51, v51
	v_fmac_f32_e32 v44, v37, v37
	v_fmac_f32_e32 v45, v48, v48
	v_fmac_f32_e32 v44, v38, v38
	v_fmac_f32_e32 v45, v49, v49
	v_fmac_f32_e32 v44, v39, v39
	v_cvt_pk_bf16_f32 v33, v46, v47
	v_add_f32_e32 v46, v45, v44
	ds_bpermute_b32 v47, v182, v46
	v_add_co_u32_e32 v44, vcc, s85, v178
	v_cvt_pk_bf16_f32 v34, v50, v51
	v_cvt_pk_bf16_f32 v35, v48, v49
	s_nop 1
	v_addc_co_u32_e32 v45, vcc, 0, v179, vcc
	global_store_dwordx4 v[44:45], v[32:35], off
	s_waitcnt lgkmcnt(0)
	s_nop 0
	v_add_f32_e32 v32, v46, v47
	ds_bpermute_b32 v33, v120, v32
	v_cvt_pk_bf16_f32 v34, v40, v41
	v_cvt_pk_bf16_f32 v35, v42, v43
	v_cvt_pk_bf16_f32 v36, v36, v37
	v_cvt_pk_bf16_f32 v37, v38, v39
	global_store_dwordx4 v[44:45], v[34:37], off offset:256
	s_and_saveexec_b64 s[40:41], s[0:1]
	s_cbranch_execz .LBB0_2077
	v_add_u32_e32 v34, 0x90, v176
	v_ashrrev_i32_e32 v35, 31, v34
	v_lshl_add_u64 v[34:35], v[34:35], 2, s[8:9]
	s_waitcnt lgkmcnt(0)
	v_add_f32_e32 v32, v32, v33
	global_atomic_add_f32 v[34:35], v32, off
.LBB0_2077:
	s_or_b64 exec, exec, s[40:41]
	s_waitcnt vmcnt(11)
	v_add_f32_e64 v20, v20, v92
	v_add_f32_e64 v21, v21, v93
	s_waitcnt vmcnt(10)
	v_add_f32_e64 v34, v16, v88
	v_add_f32_e64 v35, v17, v89
	v_cvt_pk_bf16_f32 v16, v20, v21
	s_waitcnt vmcnt(9)
	v_add_f32_e64 v28, v28, v84
	v_add_f32_e64 v29, v29, v85
	v_mul_f32_e32 v21, v21, v21
	v_fmac_f32_e32 v21, v20, v20
	v_mul_f32_e32 v20, v29, v29
	v_add_f32_e64 v22, v22, v94
	v_add_f32_e64 v23, v23, v95
	v_add_f32_e64 v30, v30, v86
	v_add_f32_e64 v31, v31, v87
	v_fmac_f32_e32 v20, v28, v28
	v_fmac_f32_e32 v21, v22, v22
	v_fmac_f32_e32 v20, v30, v30
	s_waitcnt vmcnt(8)
	v_add_f32_e64 v24, v24, v80
	v_add_f32_e64 v25, v25, v81
	v_fmac_f32_e32 v21, v23, v23
	v_fmac_f32_e32 v20, v31, v31
	v_fmac_f32_e32 v21, v34, v34
	v_fmac_f32_e32 v20, v24, v24
	s_waitcnt lgkmcnt(0)
	v_add_f32_e64 v32, v18, v90
	v_add_f32_e64 v33, v19, v91
	v_add_f32_e64 v26, v26, v82
	v_add_f32_e64 v27, v27, v83
	v_fmac_f32_e32 v21, v35, v35
	v_fmac_f32_e32 v20, v25, v25
	v_fmac_f32_e32 v21, v32, v32
	v_fmac_f32_e32 v20, v26, v26
	v_fmac_f32_e32 v21, v33, v33
	v_fmac_f32_e32 v20, v27, v27
	v_add_f32_e32 v20, v21, v20
	ds_bpermute_b32 v21, v182, v20
	v_cvt_pk_bf16_f32 v17, v22, v23
	v_add_co_u32_e32 v22, vcc, s86, v178
	v_cvt_pk_bf16_f32 v18, v34, v35
	v_cvt_pk_bf16_f32 v19, v32, v33
	s_nop 1
	v_addc_co_u32_e32 v23, vcc, 0, v179, vcc
	global_store_dwordx4 v[22:23], v[16:19], off
	s_waitcnt lgkmcnt(0)
	s_nop 0
	v_add_f32_e32 v16, v20, v21
	ds_bpermute_b32 v17, v120, v16
	v_cvt_pk_bf16_f32 v18, v28, v29
	v_cvt_pk_bf16_f32 v19, v30, v31
	v_cvt_pk_bf16_f32 v20, v24, v25
	v_cvt_pk_bf16_f32 v21, v26, v27
	global_store_dwordx4 v[22:23], v[18:21], off offset:256
	s_and_saveexec_b64 s[40:41], s[0:1]
	s_cbranch_execz .LBB0_2079
	v_add_u32_e32 v18, 0xa0, v176
	v_ashrrev_i32_e32 v19, 31, v18
	v_lshl_add_u64 v[18:19], v[18:19], 2, s[8:9]
	s_waitcnt lgkmcnt(0)
	v_add_f32_e32 v16, v16, v17
	global_atomic_add_f32 v[18:19], v16, off
.LBB0_2079:
	s_or_b64 exec, exec, s[40:41]
	s_waitcnt vmcnt(9)
	v_add_f32_e64 v4, v4, v76
	v_add_f32_e64 v5, v5, v77
	s_waitcnt vmcnt(8)
	v_add_f32_e64 v18, v0, v72
	v_add_f32_e64 v19, v1, v73
	v_cvt_pk_bf16_f32 v0, v4, v5
	s_waitcnt vmcnt(7)
	v_add_f32_e64 v12, v12, v68
	v_add_f32_e64 v13, v13, v69
	v_mul_f32_e32 v5, v5, v5
	v_fmac_f32_e32 v5, v4, v4
	v_mul_f32_e32 v4, v13, v13
	v_add_f32_e64 v6, v6, v78
	v_add_f32_e64 v7, v7, v79
	v_add_f32_e64 v14, v14, v70
	v_add_f32_e64 v15, v15, v71
	v_fmac_f32_e32 v4, v12, v12
	v_fmac_f32_e32 v5, v6, v6
	v_fmac_f32_e32 v4, v14, v14
	s_waitcnt vmcnt(6)
	v_add_f32_e64 v8, v8, v64
	v_add_f32_e64 v9, v9, v65
	v_fmac_f32_e32 v5, v7, v7
	v_fmac_f32_e32 v4, v15, v15
	v_fmac_f32_e32 v5, v18, v18
	v_fmac_f32_e32 v4, v8, v8
	s_waitcnt lgkmcnt(0)
	v_add_f32_e64 v16, v2, v74
	v_add_f32_e64 v17, v3, v75
	v_add_f32_e64 v10, v10, v66
	v_add_f32_e64 v11, v11, v67
	v_fmac_f32_e32 v5, v19, v19
	v_fmac_f32_e32 v4, v9, v9
	v_fmac_f32_e32 v5, v16, v16
	v_fmac_f32_e32 v4, v10, v10
	v_fmac_f32_e32 v5, v17, v17
	v_fmac_f32_e32 v4, v11, v11
	v_add_f32_e32 v4, v5, v4
	ds_bpermute_b32 v5, v182, v4
	v_cvt_pk_bf16_f32 v1, v6, v7
	v_add_co_u32_e32 v6, vcc, s87, v178
	v_cvt_pk_bf16_f32 v2, v18, v19
	v_cvt_pk_bf16_f32 v3, v16, v17
	s_nop 1
	v_addc_co_u32_e32 v7, vcc, 0, v179, vcc
	global_store_dwordx4 v[6:7], v[0:3], off
	s_waitcnt lgkmcnt(0)
	s_nop 0
	v_add_f32_e32 v0, v4, v5
	ds_bpermute_b32 v1, v120, v0
	v_cvt_pk_bf16_f32 v2, v12, v13
	v_cvt_pk_bf16_f32 v3, v14, v15
	v_cvt_pk_bf16_f32 v4, v8, v9
	v_cvt_pk_bf16_f32 v5, v10, v11
	global_store_dwordx4 v[6:7], v[2:5], off offset:256
	s_and_saveexec_b64 s[40:41], s[0:1]
	s_cbranch_execz .LBB0_2081
	v_add_u32_e32 v2, 0xb0, v176
	v_ashrrev_i32_e32 v3, 31, v2
	v_lshl_add_u64 v[2:3], v[2:3], 2, s[8:9]
	s_waitcnt lgkmcnt(0)
	v_add_f32_e32 v0, v0, v1
	global_atomic_add_f32 v[2:3], v0, off

.LBB0_2168:
	ds_read_b128 v[156:159], v145
	ds_read_b128 v[160:163], v145 offset:1024
	ds_read_b128 v[164:167], v145 offset:2048
	ds_read_b128 v[168:171], v145 offset:3072
	s_add_u32 s28, s16, 0xfff80080
	s_addc_u32 s29, s17, -1
	s_cmp_eq_u32 s56, 28
	s_cselect_b32 s31, s13, s29
	s_cselect_b32 s30, s12, s28
	s_cselect_b32 s29, s15, s55
	s_cselect_b32 s28, s14, s54
	v_lshl_add_u64 v[142:143], s[16:17], 0, v[136:137]
	s_add_i32 m0, s38, 0xc000
	ds_read_b128 v[172:175], v146
	ds_read_b128 v[176:179], v146 offset:1024
	ds_read_b128 v[180:183], v146 offset:2048
	ds_read_b128 v[184:187], v146 offset:3072
	ds_read_b128 v[188:191], v146 offset:4096
	ds_read_b128 v[192:195], v146 offset:5120
	ds_read_b128 v[196:199], v146 offset:6144
	ds_read_b128 v[200:203], v146 offset:7168
	global_load_lds_dwordx4 v[142:143], off
	v_lshl_add_u64 v[142:143], s[16:17], 0, v[138:139]
	s_add_i32 m0, s38, 0xe000
	s_nop 0
	global_load_lds_dwordx4 v[142:143], off
	s_waitcnt lgkmcnt(8)
	s_barrier
	s_waitcnt lgkmcnt(0)
	s_setprio 1
	s_waitcnt lgkmcnt(0)
	v_mfma_f32_16x16x32_bf16 v[124:127], v[156:159], v[172:175], v[124:127]
	v_mfma_f32_16x16x32_bf16 v[120:123], v[164:167], v[172:175], v[120:123]
	v_mfma_f32_16x16x32_bf16 v[108:111], v[156:159], v[180:183], v[108:111]
	v_mfma_f32_16x16x32_bf16 v[104:107], v[164:167], v[180:183], v[104:107]
	v_mfma_f32_16x16x32_bf16 v[92:95], v[156:159], v[188:191], v[92:95]
	v_mfma_f32_16x16x32_bf16 v[88:91], v[164:167], v[188:191], v[88:91]
	v_mfma_f32_16x16x32_bf16 v[76:79], v[156:159], v[196:199], v[76:79]
	v_mfma_f32_16x16x32_bf16 v[72:75], v[164:167], v[196:199], v[72:75]
	v_mfma_f32_16x16x32_bf16 v[124:127], v[160:163], v[176:179], v[124:127]
	v_mfma_f32_16x16x32_bf16 v[120:123], v[168:171], v[176:179], v[120:123]
	v_mfma_f32_16x16x32_bf16 v[108:111], v[160:163], v[184:187], v[108:111]
	v_mfma_f32_16x16x32_bf16 v[104:107], v[168:171], v[184:187], v[104:107]
	v_mfma_f32_16x16x32_bf16 v[92:95], v[160:163], v[192:195], v[92:95]
	v_mfma_f32_16x16x32_bf16 v[88:91], v[168:171], v[192:195], v[88:91]
	v_mfma_f32_16x16x32_bf16 v[76:79], v[160:163], v[200:203], v[76:79]
	v_mfma_f32_16x16x32_bf16 v[72:75], v[168:171], v[200:203], v[72:75]
	s_setprio 0
	s_barrier
	s_add_i32 s57, s45, s37
	v_lshl_add_u64 v[142:143], s[28:29], 0, v[130:131]
	s_mov_b32 m0, s57
	ds_read_b128 v[204:207], v147
	ds_read_b128 v[208:211], v147 offset:1024
	ds_read_b128 v[212:215], v147 offset:2048
	ds_read_b128 v[216:219], v147 offset:3072
	global_load_lds_dwordx4 v[142:143], off
	v_lshl_add_u64 v[220:221], s[28:29], 0, v[134:135]
	s_add_i32 m0, s57, 0x2000
	s_nop 0
	global_load_lds_dwordx4 v[220:221], off
	s_barrier
	s_waitcnt lgkmcnt(0)
	s_setprio 1
	s_waitcnt lgkmcnt(0)
	v_mfma_f32_16x16x32_bf16 v[116:119], v[204:207], v[172:175], v[116:119]
	v_mfma_f32_16x16x32_bf16 v[112:115], v[212:215], v[172:175], v[112:115]
	v_mfma_f32_16x16x32_bf16 v[100:103], v[204:207], v[180:183], v[100:103]
	v_mfma_f32_16x16x32_bf16 v[96:99], v[212:215], v[180:183], v[96:99]
	v_mfma_f32_16x16x32_bf16 v[84:87], v[204:207], v[188:191], v[84:87]
	v_mfma_f32_16x16x32_bf16 v[80:83], v[212:215], v[188:191], v[80:83]
	v_mfma_f32_16x16x32_bf16 v[68:71], v[204:207], v[196:199], v[68:71]
	v_mfma_f32_16x16x32_bf16 v[64:67], v[212:215], v[196:199], v[64:67]
	v_mfma_f32_16x16x32_bf16 v[116:119], v[208:211], v[176:179], v[116:119]
	v_mfma_f32_16x16x32_bf16 v[112:115], v[216:219], v[176:179], v[112:115]
	v_mfma_f32_16x16x32_bf16 v[100:103], v[208:211], v[184:187], v[100:103]
	v_mfma_f32_16x16x32_bf16 v[96:99], v[216:219], v[184:187], v[96:99]
	v_mfma_f32_16x16x32_bf16 v[84:87], v[208:211], v[192:195], v[84:87]
	v_mfma_f32_16x16x32_bf16 v[80:83], v[216:219], v[192:195], v[80:83]
	v_mfma_f32_16x16x32_bf16 v[68:71], v[208:211], v[200:203], v[68:71]
	v_mfma_f32_16x16x32_bf16 v[64:67], v[216:219], v[200:203], v[64:67]
	s_setprio 0
	s_mov_b32 m0, s38
	v_lshl_add_u64 v[222:223], s[30:31], 0, v[128:129]
	s_barrier
	ds_read_b128 v[172:175], v146 offset:16384
	ds_read_b128 v[176:179], v146 offset:17408
	ds_read_b128 v[180:183], v146 offset:18432
	ds_read_b128 v[184:187], v146 offset:19456
	ds_read_b128 v[188:191], v146 offset:20480
	ds_read_b128 v[192:195], v146 offset:21504
	ds_read_b128 v[196:199], v146 offset:22528
	ds_read_b128 v[200:203], v146 offset:23552
	global_load_lds_dwordx4 v[222:223], off
	v_lshl_add_u64 v[224:225], s[30:31], 0, v[132:133]
	s_mov_b32 m0, s39
	s_nop 0
	global_load_lds_dwordx4 v[224:225], off
	s_barrier
	s_waitcnt lgkmcnt(0)
	s_setprio 1
	s_waitcnt lgkmcnt(0)
	v_mfma_f32_16x16x32_bf16 v[60:63], v[156:159], v[172:175], v[60:63]
	v_mfma_f32_16x16x32_bf16 v[56:59], v[164:167], v[172:175], v[56:59]
	v_mfma_f32_16x16x32_bf16 v[44:47], v[156:159], v[180:183], v[44:47]
	v_mfma_f32_16x16x32_bf16 v[40:43], v[164:167], v[180:183], v[40:43]
	v_mfma_f32_16x16x32_bf16 v[28:31], v[156:159], v[188:191], v[28:31]
	v_mfma_f32_16x16x32_bf16 v[24:27], v[164:167], v[188:191], v[24:27]
	v_mfma_f32_16x16x32_bf16 v[12:15], v[156:159], v[196:199], v[12:15]
	v_mfma_f32_16x16x32_bf16 v[8:11], v[164:167], v[196:199], v[8:11]
	v_mfma_f32_16x16x32_bf16 v[60:63], v[160:163], v[176:179], v[60:63]
	v_mfma_f32_16x16x32_bf16 v[56:59], v[168:171], v[176:179], v[56:59]
	v_mfma_f32_16x16x32_bf16 v[44:47], v[160:163], v[184:187], v[44:47]
	v_mfma_f32_16x16x32_bf16 v[40:43], v[168:171], v[184:187], v[40:43]
	v_mfma_f32_16x16x32_bf16 v[28:31], v[160:163], v[192:195], v[28:31]
	v_mfma_f32_16x16x32_bf16 v[24:27], v[168:171], v[192:195], v[24:27]
	v_mfma_f32_16x16x32_bf16 v[12:15], v[160:163], v[200:203], v[12:15]
	v_mfma_f32_16x16x32_bf16 v[8:11], v[168:171], v[200:203], v[8:11]
	s_setprio 0
	s_barrier
	s_add_u32 s58, s28, 0x80000
	s_addc_u32 s59, s29, 0
	s_add_i32 s57, s48, s37
	v_lshl_add_u64 v[156:157], s[58:59], 0, v[130:131]
	s_mov_b32 m0, s57
	s_nop 0
	global_load_lds_dwordx4 v[156:157], off
	v_lshl_add_u64 v[156:157], s[58:59], 0, v[134:135]
	s_add_i32 m0, s57, 0x2000
	s_nop 0
	global_load_lds_dwordx4 v[156:157], off
	s_waitcnt vmcnt(6)
	s_barrier
	s_setprio 1
	v_mfma_f32_16x16x32_bf16 v[52:55], v[204:207], v[172:175], v[52:55]
	v_mfma_f32_16x16x32_bf16 v[48:51], v[212:215], v[172:175], v[48:51]
	v_mfma_f32_16x16x32_bf16 v[36:39], v[204:207], v[180:183], v[36:39]
	v_mfma_f32_16x16x32_bf16 v[32:35], v[212:215], v[180:183], v[32:35]
	v_mfma_f32_16x16x32_bf16 v[20:23], v[204:207], v[188:191], v[20:23]
	v_mfma_f32_16x16x32_bf16 v[16:19], v[212:215], v[188:191], v[16:19]
	v_mfma_f32_16x16x32_bf16 v[4:7], v[204:207], v[196:199], v[4:7]
	v_mfma_f32_16x16x32_bf16 v[0:3], v[212:215], v[196:199], v[0:3]
	v_mfma_f32_16x16x32_bf16 v[52:55], v[208:211], v[176:179], v[52:55]
	v_mfma_f32_16x16x32_bf16 v[48:51], v[216:219], v[176:179], v[48:51]
	v_mfma_f32_16x16x32_bf16 v[36:39], v[208:211], v[184:187], v[36:39]
	v_mfma_f32_16x16x32_bf16 v[32:35], v[216:219], v[184:187], v[32:35]
	v_mfma_f32_16x16x32_bf16 v[20:23], v[208:211], v[192:195], v[20:23]
	v_mfma_f32_16x16x32_bf16 v[16:19], v[216:219], v[192:195], v[16:19]
	v_mfma_f32_16x16x32_bf16 v[4:7], v[208:211], v[200:203], v[4:7]
	v_mfma_f32_16x16x32_bf16 v[0:3], v[216:219], v[200:203], v[0:3]
	s_setprio 0
	s_add_i32 s57, 0, 0x18000
	v_add_u32_e32 v140, s57, v144
	s_barrier
	ds_read_b128 v[156:159], v140
	ds_read_b128 v[160:163], v140 offset:1024
	ds_read_b128 v[164:167], v140 offset:2048
	ds_read_b128 v[168:171], v140 offset:3072
	s_add_u32 s30, s30, 0x80000
	s_addc_u32 s31, s31, 0
	s_mov_b32 m0, s40
	v_lshl_add_u64 v[204:205], s[30:31], 0, v[128:129]
	ds_read_b128 v[172:175], v146 offset:32768
	ds_read_b128 v[176:179], v146 offset:33792
	ds_read_b128 v[180:183], v146 offset:34816
	ds_read_b128 v[184:187], v146 offset:35840
	ds_read_b128 v[188:191], v146 offset:36864
	ds_read_b128 v[192:195], v146 offset:37888
	ds_read_b128 v[196:199], v146 offset:38912
	ds_read_b128 v[200:203], v146 offset:39936
	global_load_lds_dwordx4 v[204:205], off
	v_lshl_add_u64 v[204:205], s[30:31], 0, v[132:133]
	s_mov_b32 m0, s41
	s_nop 0
	global_load_lds_dwordx4 v[204:205], off
	s_waitcnt lgkmcnt(8)
	s_barrier
	s_waitcnt lgkmcnt(0)
	s_setprio 1
	s_waitcnt lgkmcnt(0)
	v_mfma_f32_16x16x32_bf16 v[124:127], v[156:159], v[172:175], v[124:127]
	v_mfma_f32_16x16x32_bf16 v[120:123], v[164:167], v[172:175], v[120:123]
	v_mfma_f32_16x16x32_bf16 v[108:111], v[156:159], v[180:183], v[108:111]
	v_mfma_f32_16x16x32_bf16 v[104:107], v[164:167], v[180:183], v[104:107]
	v_mfma_f32_16x16x32_bf16 v[92:95], v[156:159], v[188:191], v[92:95]
	v_mfma_f32_16x16x32_bf16 v[88:91], v[164:167], v[188:191], v[88:91]
	v_mfma_f32_16x16x32_bf16 v[76:79], v[156:159], v[196:199], v[76:79]
	v_mfma_f32_16x16x32_bf16 v[72:75], v[164:167], v[196:199], v[72:75]
	v_mfma_f32_16x16x32_bf16 v[124:127], v[160:163], v[176:179], v[124:127]
	v_mfma_f32_16x16x32_bf16 v[120:123], v[168:171], v[176:179], v[120:123]
	v_mfma_f32_16x16x32_bf16 v[108:111], v[160:163], v[184:187], v[108:111]
	v_mfma_f32_16x16x32_bf16 v[104:107], v[168:171], v[184:187], v[104:107]
	v_mfma_f32_16x16x32_bf16 v[92:95], v[160:163], v[192:195], v[92:95]
	v_mfma_f32_16x16x32_bf16 v[88:91], v[168:171], v[192:195], v[88:91]
	v_mfma_f32_16x16x32_bf16 v[76:79], v[160:163], v[200:203], v[76:79]
	v_mfma_f32_16x16x32_bf16 v[72:75], v[168:171], v[200:203], v[72:75]
	s_setprio 0
	s_barrier
	s_add_i32 s30, 0, 0x1c000
	s_add_i32 s31, s57, s37
	v_add_u32_e32 v140, s30, v144
	v_lshl_add_u64 v[142:143], v[142:143], 0, s[6:7]
	s_mov_b32 m0, s31
	ds_read_b128 v[204:207], v140
	ds_read_b128 v[208:211], v140 offset:1024
	ds_read_b128 v[212:215], v140 offset:2048
	ds_read_b128 v[216:219], v140 offset:3072
	global_load_lds_dwordx4 v[142:143], off
	v_lshl_add_u64 v[142:143], v[220:221], 0, s[6:7]
	s_add_i32 m0, s31, 0x2000
	s_nop 0
	global_load_lds_dwordx4 v[142:143], off
	s_barrier
	s_waitcnt lgkmcnt(0)
	s_setprio 1
	s_waitcnt lgkmcnt(0)
	v_mfma_f32_16x16x32_bf16 v[116:119], v[204:207], v[172:175], v[116:119]
	v_mfma_f32_16x16x32_bf16 v[112:115], v[212:215], v[172:175], v[112:115]
	v_mfma_f32_16x16x32_bf16 v[100:103], v[204:207], v[180:183], v[100:103]
	v_mfma_f32_16x16x32_bf16 v[96:99], v[212:215], v[180:183], v[96:99]
	v_mfma_f32_16x16x32_bf16 v[84:87], v[204:207], v[188:191], v[84:87]
	v_mfma_f32_16x16x32_bf16 v[80:83], v[212:215], v[188:191], v[80:83]
	v_mfma_f32_16x16x32_bf16 v[68:71], v[204:207], v[196:199], v[68:71]
	v_mfma_f32_16x16x32_bf16 v[64:67], v[212:215], v[196:199], v[64:67]
	v_mfma_f32_16x16x32_bf16 v[116:119], v[208:211], v[176:179], v[116:119]
	v_mfma_f32_16x16x32_bf16 v[112:115], v[216:219], v[176:179], v[112:115]
	v_mfma_f32_16x16x32_bf16 v[100:103], v[208:211], v[184:187], v[100:103]
	v_mfma_f32_16x16x32_bf16 v[96:99], v[216:219], v[184:187], v[96:99]
	v_mfma_f32_16x16x32_bf16 v[84:87], v[208:211], v[192:195], v[84:87]
	v_mfma_f32_16x16x32_bf16 v[80:83], v[216:219], v[192:195], v[80:83]
	v_mfma_f32_16x16x32_bf16 v[68:71], v[208:211], v[200:203], v[68:71]
	v_mfma_f32_16x16x32_bf16 v[64:67], v[216:219], v[200:203], v[64:67]
	s_setprio 0
	s_mov_b32 m0, s43
	v_lshl_add_u64 v[142:143], v[222:223], 0, s[6:7]
	s_barrier
	ds_read_b128 v[172:175], v146 offset:49152
	ds_read_b128 v[176:179], v146 offset:50176
	ds_read_b128 v[180:183], v146 offset:51200
	ds_read_b128 v[184:187], v146 offset:52224
	ds_read_b128 v[188:191], v146 offset:53248
	ds_read_b128 v[192:195], v146 offset:54272
	ds_read_b128 v[196:199], v146 offset:55296
	ds_read_b128 v[200:203], v146 offset:56320
	global_load_lds_dwordx4 v[142:143], off
	v_lshl_add_u64 v[142:143], v[224:225], 0, s[6:7]
	s_mov_b32 m0, s44
	s_nop 0
	global_load_lds_dwordx4 v[142:143], off
	s_barrier
;     __device__ __forceinline__ void operator()(const f32x4 (&acc)[2][2][4][2], const Unit& u, int wr, int wc, int fr, int fq, const Pre& pr) const {
;         const float (&rsv)[8] = pr.rsv;
; #pragma unroll
;         for (int ai = 0; ai < 2; ++ai)
; #pragma unroll
;             for (int m = 0; m < 4; ++m) {
;                 const int row = u.pm * 256 + ai * 128 + wr * 64 + m * 16 + fr; const float rs = __builtin_amdgcn_rsqf(rsv[ai * 4 + m] * (1.0f / DM) + NORM_EPS);
; #pragma unroll
;                 for (int bj = 0; bj < 2; ++bj) st_bf16x8(out + (size_t)row * ldo + u.pn * 256 + 128 * bj + 32 * wc + 8 * fq, acc[ai][bj][m][0] * rs, acc[ai][bj][m][1] * rs);
;             }
	s_waitcnt lgkmcnt(0)
	s_setprio 1
	s_waitcnt lgkmcnt(0)
	v_mfma_f32_16x16x32_bf16 v[60:63], v[156:159], v[172:175], v[60:63]
	v_mfma_f32_16x16x32_bf16 v[56:59], v[164:167], v[172:175], v[56:59]
	v_mfma_f32_16x16x32_bf16 v[44:47], v[156:159], v[180:183], v[44:47]
	v_mfma_f32_16x16x32_bf16 v[40:43], v[164:167], v[180:183], v[40:43]
	v_mfma_f32_16x16x32_bf16 v[28:31], v[156:159], v[188:191], v[28:31]
	v_mfma_f32_16x16x32_bf16 v[24:27], v[164:167], v[188:191], v[24:27]
	v_mfma_f32_16x16x32_bf16 v[12:15], v[156:159], v[196:199], v[12:15]
	v_mfma_f32_16x16x32_bf16 v[8:11], v[164:167], v[196:199], v[8:11]
	v_mfma_f32_16x16x32_bf16 v[60:63], v[160:163], v[176:179], v[60:63]
	v_mfma_f32_16x16x32_bf16 v[56:59], v[168:171], v[176:179], v[56:59]
	v_mfma_f32_16x16x32_bf16 v[44:47], v[160:163], v[184:187], v[44:47]
	v_mfma_f32_16x16x32_bf16 v[40:43], v[168:171], v[184:187], v[40:43]
	v_mfma_f32_16x16x32_bf16 v[28:31], v[160:163], v[192:195], v[28:31]
	v_mfma_f32_16x16x32_bf16 v[24:27], v[168:171], v[192:195], v[24:27]
	v_mfma_f32_16x16x32_bf16 v[12:15], v[160:163], v[200:203], v[12:15]
	v_mfma_f32_16x16x32_bf16 v[8:11], v[168:171], v[200:203], v[8:11]
	s_setprio 0
	s_barrier
	s_add_u32 s28, s28, 0x80080
	s_addc_u32 s29, s29, 0
	s_add_i32 s30, s30, s37
	v_lshl_add_u64 v[142:143], s[28:29], 0, v[130:131]
	s_mov_b32 m0, s30
	s_nop 0
	global_load_lds_dwordx4 v[142:143], off
	v_lshl_add_u64 v[142:143], s[28:29], 0, v[134:135]
	s_add_i32 m0, s30, 0x2000
	s_nop 0
	global_load_lds_dwordx4 v[142:143], off
	s_waitcnt vmcnt(6)
	s_barrier
	s_setprio 1
	v_mfma_f32_16x16x32_bf16 v[52:55], v[204:207], v[172:175], v[52:55]
	v_mfma_f32_16x16x32_bf16 v[48:51], v[212:215], v[172:175], v[48:51]
	v_mfma_f32_16x16x32_bf16 v[36:39], v[204:207], v[180:183], v[36:39]
	v_mfma_f32_16x16x32_bf16 v[32:35], v[212:215], v[180:183], v[32:35]
	v_mfma_f32_16x16x32_bf16 v[20:23], v[204:207], v[188:191], v[20:23]
	v_mfma_f32_16x16x32_bf16 v[16:19], v[212:215], v[188:191], v[16:19]
	v_mfma_f32_16x16x32_bf16 v[4:7], v[204:207], v[196:199], v[4:7]
	v_mfma_f32_16x16x32_bf16 v[0:3], v[212:215], v[196:199], v[0:3]
	v_mfma_f32_16x16x32_bf16 v[52:55], v[208:211], v[176:179], v[52:55]
	v_mfma_f32_16x16x32_bf16 v[48:51], v[216:219], v[176:179], v[48:51]
	v_mfma_f32_16x16x32_bf16 v[36:39], v[208:211], v[184:187], v[36:39]
	v_mfma_f32_16x16x32_bf16 v[32:35], v[216:219], v[184:187], v[32:35]
	v_mfma_f32_16x16x32_bf16 v[20:23], v[208:211], v[192:195], v[20:23]
	v_mfma_f32_16x16x32_bf16 v[16:19], v[216:219], v[192:195], v[16:19]
	v_mfma_f32_16x16x32_bf16 v[4:7], v[208:211], v[200:203], v[4:7]
	v_mfma_f32_16x16x32_bf16 v[0:3], v[216:219], v[200:203], v[0:3]
	s_setprio 0
	s_add_i32 s56, s56, 2
	s_add_u32 s16, s16, 0x100
	s_addc_u32 s17, s17, 0
	s_add_u32 s54, s54, 0x100
	s_addc_u32 s55, s55, 0
	s_cmp_gt_u32 s56, 29
	s_barrier
	s_cbranch_scc0 .LBB0_2168
	v_mbcnt_lo_u32_b32 v142, -1, 0
	v_mbcnt_hi_u32_b32 v142, -1, v142
	s_waitcnt vmcnt(0)
	v_fmamk_f32 v141, v141, 0x3a000000, v148
	v_and_or_b32 v140, v142, 15, s11
	s_lshl_b32 s16, s53, 8
	v_rsq_f32_e32 v156, v141
	v_ashrrev_i32_e32 v141, 31, v140
	s_ashr_i32 s17, s16, 31
	v_ashrrev_i32_e32 v142, 1, v142
	v_lshlrev_b64 v[158:159], 10, v[140:141]
	v_and_b32_e32 v142, -8, v142
	v_lshl_add_u64 v[158:159], s[4:5], 0, v[158:159]
	s_lshl_b64 s[16:17], s[16:17], 1
	v_ashrrev_i32_e32 v143, 31, v142
	v_lshl_add_u64 v[158:159], v[158:159], 0, s[16:17]
	v_lshl_add_u64 v[158:159], v[158:159], 0, s[0:1]
	v_lshlrev_b64 v[142:143], 1, v[142:143]
	v_lshl_add_u64 v[158:159], v[158:159], 0, v[142:143]
	v_mul_f32_e64 v126, v156, v126
	v_mul_f32_e64 v127, v156, v127
	v_mul_f32_e64 v124, v156, v124
	v_mul_f32_e64 v125, v156, v125
	v_mul_f32_e64 v160, v156, v122
	v_mul_f32_e64 v161, v156, v123
	v_mul_f32_e64 v122, v156, v120
	v_mul_f32_e64 v123, v156, v121
	v_cvt_pk_bf16_f32 v120, v124, v125
	v_cvt_pk_bf16_f32 v121, v126, v127
	v_cvt_pk_bf16_f32 v122, v122, v123
	v_cvt_pk_bf16_f32 v123, v160, v161
	global_store_dwordx4 v[158:159], v[120:123], off
	v_mul_f32_e64 v118, v156, v118
	v_mul_f32_e64 v119, v156, v119
	v_mul_f32_e64 v116, v156, v116
	v_mul_f32_e64 v117, v156, v117
	v_mul_f32_e64 v120, v156, v114
	v_mul_f32_e64 v121, v156, v115
	v_mul_f32_e64 v114, v156, v112
	v_mul_f32_e64 v115, v156, v113
	v_cvt_pk_bf16_f32 v112, v116, v117
	v_cvt_pk_bf16_f32 v113, v118, v119
	v_cvt_pk_bf16_f32 v114, v114, v115
	v_cvt_pk_bf16_f32 v115, v120, v121
	global_store_dwordx4 v[158:159], v[112:115], off offset:256
	s_and_b64 vcc, exec, s[8:9]
	s_mov_b32 s30, s10
	v_or_b32_e32 v112, 16, v140
	v_fmamk_f32 v113, v155, 0x3a000000, v148
	v_rsq_f32_e32 v114, v113
	v_ashrrev_i32_e32 v113, 31, v112
	v_lshlrev_b64 v[112:113], 10, v[112:113]
	v_lshl_add_u64 v[112:113], s[4:5], 0, v[112:113]
	v_lshl_add_u64 v[112:113], v[112:113], 0, s[16:17]
	v_lshl_add_u64 v[112:113], v[112:113], 0, s[0:1]
	v_lshl_add_u64 v[112:113], v[112:113], 0, v[142:143]
	v_mul_f32_e64 v110, v114, v110
	v_mul_f32_e64 v111, v114, v111
	v_mul_f32_e64 v108, v114, v108
	v_mul_f32_e64 v109, v114, v109
	v_mul_f32_e64 v116, v114, v106
	v_mul_f32_e64 v117, v114, v107
	v_mul_f32_e64 v106, v114, v104
	v_mul_f32_e64 v107, v114, v105
	v_cvt_pk_bf16_f32 v104, v108, v109
	v_cvt_pk_bf16_f32 v105, v110, v111
	v_cvt_pk_bf16_f32 v106, v106, v107
	v_cvt_pk_bf16_f32 v107, v116, v117
	global_store_dwordx4 v[112:113], v[104:107], off
	v_mul_f32_e64 v102, v114, v102
	v_mul_f32_e64 v103, v114, v103
	v_mul_f32_e64 v100, v114, v100
	v_mul_f32_e64 v101, v114, v101
	v_mul_f32_e64 v104, v114, v98
	v_mul_f32_e64 v105, v114, v99
	v_mul_f32_e64 v98, v114, v96
	v_mul_f32_e64 v99, v114, v97
	v_cvt_pk_bf16_f32 v96, v100, v101
	v_cvt_pk_bf16_f32 v97, v102, v103
;     __device__ __forceinline__ void operator()(const f32x4 (&acc)[2][2][4][2], const Unit& u, int wr, int wc, int fr, int fq, const Pre& pr) const {
;     ...
;         for (int ai = 0; ai < 2; ++ai)
; #pragma unroll
;             for (int m = 0; m < 4; ++m) {
;                 const int row = u.pm * 256 + ai * 128 + wr * 64 + m * 16 + fr; const float rs = __builtin_amdgcn_rsqf(rsv[ai * 4 + m] * (1.0f / DM) + NORM_EPS);
; #pragma unroll
;                 for (int bj = 0; bj < 2; ++bj) st_bf16x8(out + (size_t)row * ldo + u.pn * 256 + 128 * bj + 32 * wc + 8 * fq, acc[ai][bj][m][0] * rs, acc[ai][bj][m][1] * rs);
;             }
	v_cvt_pk_bf16_f32 v98, v98, v99
	v_cvt_pk_bf16_f32 v99, v104, v105
	global_store_dwordx4 v[112:113], v[96:99], off offset:256
	s_mov_b32 s53, s52
	s_mov_b64 s[28:29], s[14:15]
	v_or_b32_e32 v96, 32, v140
	v_fmamk_f32 v97, v154, 0x3a000000, v148
	v_rsq_f32_e32 v98, v97
	v_ashrrev_i32_e32 v97, 31, v96
	v_lshlrev_b64 v[96:97], 10, v[96:97]
	v_lshl_add_u64 v[96:97], s[4:5], 0, v[96:97]
	v_lshl_add_u64 v[96:97], v[96:97], 0, s[16:17]
	v_lshl_add_u64 v[96:97], v[96:97], 0, s[0:1]
	v_lshl_add_u64 v[96:97], v[96:97], 0, v[142:143]
	v_mul_f32_e64 v94, v98, v94
	v_mul_f32_e64 v95, v98, v95
	v_mul_f32_e64 v92, v98, v92
	v_mul_f32_e64 v93, v98, v93
	v_mul_f32_e64 v100, v98, v90
	v_mul_f32_e64 v101, v98, v91
	v_mul_f32_e64 v90, v98, v88
	v_mul_f32_e64 v91, v98, v89
	v_cvt_pk_bf16_f32 v88, v92, v93
	v_cvt_pk_bf16_f32 v89, v94, v95
	v_cvt_pk_bf16_f32 v90, v90, v91
	v_cvt_pk_bf16_f32 v91, v100, v101
	global_store_dwordx4 v[96:97], v[88:91], off
	v_mul_f32_e64 v86, v98, v86
	v_mul_f32_e64 v87, v98, v87
	v_mul_f32_e64 v84, v98, v84
	v_mul_f32_e64 v85, v98, v85
	v_mul_f32_e64 v88, v98, v82
	v_mul_f32_e64 v89, v98, v83
	v_mul_f32_e64 v82, v98, v80
	v_mul_f32_e64 v83, v98, v81
	v_cvt_pk_bf16_f32 v80, v84, v85
	v_cvt_pk_bf16_f32 v81, v86, v87
	v_cvt_pk_bf16_f32 v82, v82, v83
	v_cvt_pk_bf16_f32 v83, v88, v89
	global_store_dwordx4 v[96:97], v[80:83], off offset:256
	s_nop 1
	v_or_b32_e32 v80, 48, v140
	v_fmamk_f32 v81, v153, 0x3a000000, v148
	v_rsq_f32_e32 v82, v81
	v_ashrrev_i32_e32 v81, 31, v80
	v_lshlrev_b64 v[80:81], 10, v[80:81]
	v_lshl_add_u64 v[80:81], s[4:5], 0, v[80:81]
	v_lshl_add_u64 v[80:81], v[80:81], 0, s[16:17]
	v_lshl_add_u64 v[80:81], v[80:81], 0, s[0:1]
	v_lshl_add_u64 v[80:81], v[80:81], 0, v[142:143]
	v_mul_f32_e64 v78, v82, v78
	v_mul_f32_e64 v79, v82, v79
	v_mul_f32_e64 v76, v82, v76
	v_mul_f32_e64 v77, v82, v77
	v_mul_f32_e64 v84, v82, v74
	v_mul_f32_e64 v85, v82, v75
	v_mul_f32_e64 v74, v82, v72
	v_mul_f32_e64 v75, v82, v73
	v_cvt_pk_bf16_f32 v72, v76, v77
	v_cvt_pk_bf16_f32 v73, v78, v79
	v_cvt_pk_bf16_f32 v74, v74, v75
	v_cvt_pk_bf16_f32 v75, v84, v85
	global_store_dwordx4 v[80:81], v[72:75], off
	v_mul_f32_e64 v70, v82, v70
	v_mul_f32_e64 v71, v82, v71
	v_mul_f32_e64 v68, v82, v68
	v_mul_f32_e64 v69, v82, v69
	v_mul_f32_e64 v72, v82, v66
	v_mul_f32_e64 v73, v82, v67
	v_mul_f32_e64 v66, v82, v64
	v_mul_f32_e64 v67, v82, v65
	v_cvt_pk_bf16_f32 v64, v68, v69
	v_cvt_pk_bf16_f32 v65, v70, v71
	v_cvt_pk_bf16_f32 v66, v66, v67
	v_cvt_pk_bf16_f32 v67, v72, v73
	global_store_dwordx4 v[80:81], v[64:67], off offset:256
	s_nop 1
	v_add_u32_e32 v64, 0x80, v140
	v_fmamk_f32 v65, v152, 0x3a000000, v148
	v_rsq_f32_e32 v66, v65
	v_ashrrev_i32_e32 v65, 31, v64
	v_lshlrev_b64 v[64:65], 10, v[64:65]
	v_lshl_add_u64 v[64:65], s[4:5], 0, v[64:65]
	v_lshl_add_u64 v[64:65], v[64:65], 0, s[16:17]
	v_lshl_add_u64 v[64:65], v[64:65], 0, s[0:1]
	v_lshl_add_u64 v[64:65], v[64:65], 0, v[142:143]
	v_mul_f32_e64 v62, v66, v62
	v_mul_f32_e64 v63, v66, v63
	v_mul_f32_e64 v60, v66, v60
	v_mul_f32_e64 v61, v66, v61
	v_mul_f32_e64 v68, v66, v58
	v_mul_f32_e64 v69, v66, v59
	v_mul_f32_e64 v58, v66, v56
	v_mul_f32_e64 v59, v66, v57
	v_cvt_pk_bf16_f32 v56, v60, v61
	v_cvt_pk_bf16_f32 v57, v62, v63
	v_cvt_pk_bf16_f32 v58, v58, v59
	v_cvt_pk_bf16_f32 v59, v68, v69
	global_store_dwordx4 v[64:65], v[56:59], off
	v_mul_f32_e64 v54, v66, v54
	v_mul_f32_e64 v55, v66, v55
	v_mul_f32_e64 v52, v66, v52
	v_mul_f32_e64 v53, v66, v53
	v_mul_f32_e64 v56, v66, v50
	v_mul_f32_e64 v57, v66, v51
	v_mul_f32_e64 v50, v66, v48
	v_mul_f32_e64 v51, v66, v49
	v_cvt_pk_bf16_f32 v48, v52, v53
	v_cvt_pk_bf16_f32 v49, v54, v55
	v_cvt_pk_bf16_f32 v50, v50, v51
	v_cvt_pk_bf16_f32 v51, v56, v57
;     __device__ __forceinline__ void operator()(const f32x4 (&acc)[2][2][4][2], const Unit& u, int wr, int wc, int fr, int fq, const Pre& pr) const {
;     ...
;         for (int ai = 0; ai < 2; ++ai)
; #pragma unroll
;             for (int m = 0; m < 4; ++m) {
;                 const int row = u.pm * 256 + ai * 128 + wr * 64 + m * 16 + fr; const float rs = __builtin_amdgcn_rsqf(rsv[ai * 4 + m] * (1.0f / DM) + NORM_EPS);
; #pragma unroll
;                 for (int bj = 0; bj < 2; ++bj) st_bf16x8(out + (size_t)row * ldo + u.pn * 256 + 128 * bj + 32 * wc + 8 * fq, acc[ai][bj][m][0] * rs, acc[ai][bj][m][1] * rs);
;             }
	global_store_dwordx4 v[64:65], v[48:51], off offset:256
	s_nop 1
	v_add_u32_e32 v48, 0x90, v140
	v_fmamk_f32 v49, v151, 0x3a000000, v148
	v_rsq_f32_e32 v50, v49
	v_ashrrev_i32_e32 v49, 31, v48
	v_lshlrev_b64 v[48:49], 10, v[48:49]
	v_lshl_add_u64 v[48:49], s[4:5], 0, v[48:49]
	v_lshl_add_u64 v[48:49], v[48:49], 0, s[16:17]
	v_lshl_add_u64 v[48:49], v[48:49], 0, s[0:1]
	v_lshl_add_u64 v[48:49], v[48:49], 0, v[142:143]
	v_mul_f32_e64 v46, v50, v46
	v_mul_f32_e64 v47, v50, v47
	v_mul_f32_e64 v44, v50, v44
	v_mul_f32_e64 v45, v50, v45
	v_mul_f32_e64 v52, v50, v42
	v_mul_f32_e64 v53, v50, v43
	v_mul_f32_e64 v42, v50, v40
	v_mul_f32_e64 v43, v50, v41
	v_cvt_pk_bf16_f32 v40, v44, v45
	v_cvt_pk_bf16_f32 v41, v46, v47
	v_cvt_pk_bf16_f32 v42, v42, v43
	v_cvt_pk_bf16_f32 v43, v52, v53
	global_store_dwordx4 v[48:49], v[40:43], off
	v_mul_f32_e64 v38, v50, v38
	v_mul_f32_e64 v39, v50, v39
	v_mul_f32_e64 v36, v50, v36
	v_mul_f32_e64 v37, v50, v37
	v_mul_f32_e64 v40, v50, v34
	v_mul_f32_e64 v41, v50, v35
	v_mul_f32_e64 v34, v50, v32
	v_mul_f32_e64 v35, v50, v33
	v_cvt_pk_bf16_f32 v32, v36, v37
	v_cvt_pk_bf16_f32 v33, v38, v39
	v_cvt_pk_bf16_f32 v34, v34, v35
	v_cvt_pk_bf16_f32 v35, v40, v41
	global_store_dwordx4 v[48:49], v[32:35], off offset:256
	s_nop 1
	v_add_u32_e32 v32, 0xa0, v140
	v_fmamk_f32 v33, v150, 0x3a000000, v148
	v_rsq_f32_e32 v34, v33
	v_ashrrev_i32_e32 v33, 31, v32
	v_lshlrev_b64 v[32:33], 10, v[32:33]
	v_lshl_add_u64 v[32:33], s[4:5], 0, v[32:33]
	v_lshl_add_u64 v[32:33], v[32:33], 0, s[16:17]
	v_lshl_add_u64 v[32:33], v[32:33], 0, s[0:1]
	v_lshl_add_u64 v[32:33], v[32:33], 0, v[142:143]
	v_mul_f32_e64 v30, v34, v30
	v_mul_f32_e64 v31, v34, v31
	v_mul_f32_e64 v28, v34, v28
	v_mul_f32_e64 v29, v34, v29
	v_mul_f32_e64 v36, v34, v26
	v_mul_f32_e64 v37, v34, v27
	v_mul_f32_e64 v26, v34, v24
	v_mul_f32_e64 v27, v34, v25
	v_cvt_pk_bf16_f32 v24, v28, v29
	v_cvt_pk_bf16_f32 v25, v30, v31
	v_cvt_pk_bf16_f32 v26, v26, v27
	v_cvt_pk_bf16_f32 v27, v36, v37
	global_store_dwordx4 v[32:33], v[24:27], off
	v_mul_f32_e64 v22, v34, v22
	v_mul_f32_e64 v23, v34, v23
	v_mul_f32_e64 v20, v34, v20
	v_mul_f32_e64 v21, v34, v21
	v_mul_f32_e64 v24, v34, v18
	v_mul_f32_e64 v25, v34, v19
	v_mul_f32_e64 v18, v34, v16
	v_mul_f32_e64 v19, v34, v17
	v_cvt_pk_bf16_f32 v16, v20, v21
	v_cvt_pk_bf16_f32 v17, v22, v23
	v_cvt_pk_bf16_f32 v18, v18, v19
	v_cvt_pk_bf16_f32 v19, v24, v25
	global_store_dwordx4 v[32:33], v[16:19], off offset:256
	s_nop 1
	v_add_u32_e32 v16, 0xb0, v140
	v_fmamk_f32 v17, v149, 0x3a000000, v148
	v_rsq_f32_e32 v18, v17
	v_ashrrev_i32_e32 v17, 31, v16
	v_lshlrev_b64 v[16:17], 10, v[16:17]
	v_lshl_add_u64 v[16:17], s[4:5], 0, v[16:17]
	v_lshl_add_u64 v[16:17], v[16:17], 0, s[16:17]
	v_lshl_add_u64 v[16:17], v[16:17], 0, s[0:1]
	v_lshl_add_u64 v[16:17], v[16:17], 0, v[142:143]
	v_mul_f32_e64 v14, v18, v14
	v_mul_f32_e64 v15, v18, v15
	v_mul_f32_e64 v12, v18, v12
	v_mul_f32_e64 v13, v18, v13
	v_mul_f32_e64 v20, v18, v10
	v_mul_f32_e64 v21, v18, v11
	v_mul_f32_e64 v10, v18, v8
	v_mul_f32_e64 v11, v18, v9
	v_cvt_pk_bf16_f32 v8, v12, v13
	v_cvt_pk_bf16_f32 v9, v14, v15
	v_cvt_pk_bf16_f32 v10, v10, v11
	v_cvt_pk_bf16_f32 v11, v20, v21
	global_store_dwordx4 v[16:17], v[8:11], off
	s_mov_b64 s[16:17], s[12:13]
	v_mul_f32_e64 v6, v18, v6
	v_mul_f32_e64 v7, v18, v7
	v_mul_f32_e64 v8, v18, v2
	v_mul_f32_e64 v9, v18, v3
	v_mul_f32_e64 v2, v18, v0
	v_mul_f32_e64 v3, v18, v1
	v_mul_f32_e64 v4, v18, v4
	v_mul_f32_e64 v5, v18, v5
	v_cvt_pk_bf16_f32 v0, v4, v5
	v_cvt_pk_bf16_f32 v1, v6, v7
	v_cvt_pk_bf16_f32 v2, v2, v3
	v_cvt_pk_bf16_f32 v3, v8, v9
	global_store_dwordx4 v[16:17], v[0:3], off offset:256
	s_cbranch_vccz .LBB0_2161
	s_waitcnt vmcnt(0)
	s_cmpk_gt_u32 s96, 0xff
	s_cbranch_scc1 .LBB0_2172
	s_barrier

; __device__ __forceinline__ unsigned sel_bit_mask(unsigned w, int b) { unsigned m; asm("v_bfe_i32 %0, %1, %2, 1" : "=v"(m) : "v"(w), "n"(b)); return m; }
; template <bool SEL>
; __device__ __forceinline__ void partialSM(f32x16& p0, f32x16& p1, float& m_reg, float& mn, float& alpha, unsigned selw) {
;     ...
;     constexpr float C2 = 1.4426950408889634f * SCALE;
;     if (__builtin_expect(__all((pmax - m_reg) * SCALE <= THR), 1)) { mn = m_reg; alpha = 1.f; }
;     else { mn = fmaxf(m_reg, pmax); alpha = __builtin_amdgcn_exp2f((m_reg - mn) * C2); m_reg = mn; }
;     const float mnL = -mn * C2;
; #pragma unroll
;     for (int r = 0; r < 16; ++r) p0[r] = fmaf(p0[r], C2, mnL);
; #pragma unroll
;     for (int r = 0; r < 16; ++r) p1[r] = fmaf(p1[r], C2, mnL);
; #pragma unroll
;     for (int r = 0; r < 16; ++r) p0[r] = __builtin_amdgcn_exp2f(p0[r]);
;     if (SEL) {
; #pragma unroll
;         for (int r = 0; r < 16; ++r) p0[r] = __uint_as_float(__float_as_uint(p0[r]) & sel_bit_mask(selw, r));
;     }
; }
.LBB0_2257:
	v_max_f32_e32 v33, 0xf149f2ca, v33
	v_cndmask_b32_e64 v168, v33, v192, s[0:1]
	v_mul_f32_e32 v34, 0xbe0293ee, v168
	v_fmamk_f32 v16, v16, 0x3e0293ee, v34
	v_exp_f32_e32 v174, v16
	v_sub_f32_e32 v16, 0xf149f2ca, v33
	v_mul_f32_e32 v16, 0x3e0293ee, v16
	v_exp_f32_e32 v16, v16
	v_fmamk_f32 v17, v17, 0x3e0293ee, v34
	v_fmamk_f32 v18, v18, 0x3e0293ee, v34
	v_fmamk_f32 v19, v19, 0x3e0293ee, v34
	v_fmamk_f32 v20, v20, 0x3e0293ee, v34
	v_fmamk_f32 v21, v21, 0x3e0293ee, v34
	v_fmamk_f32 v22, v22, 0x3e0293ee, v34
	v_fmamk_f32 v23, v23, 0x3e0293ee, v34
	v_fmamk_f32 v24, v24, 0x3e0293ee, v34
	v_fmamk_f32 v25, v25, 0x3e0293ee, v34
	v_fmamk_f32 v26, v26, 0x3e0293ee, v34
	v_fmamk_f32 v27, v27, 0x3e0293ee, v34
	v_fmamk_f32 v28, v28, 0x3e0293ee, v34
	v_fmamk_f32 v29, v29, 0x3e0293ee, v34
	v_fmamk_f32 v30, v30, 0x3e0293ee, v34
	v_fmamk_f32 v31, v31, 0x3e0293ee, v34
	v_exp_f32_e32 v176, v17
	v_exp_f32_e32 v172, v18
	v_exp_f32_e32 v175, v19
	v_exp_f32_e32 v171, v20
	v_exp_f32_e32 v173, v21
	v_exp_f32_e32 v169, v22
	v_exp_f32_e32 v170, v23
	v_exp_f32_e32 v163, v24
	v_exp_f32_e32 v166, v25
	v_exp_f32_e32 v161, v26
	v_exp_f32_e32 v164, v27
	v_exp_f32_e32 v160, v28
	v_exp_f32_e32 v167, v29
	v_exp_f32_e32 v162, v30
	v_exp_f32_e32 v165, v31
	v_fma_f32 v158, v0, s12, v34
	v_fma_f32 v159, v1, s12, v34
	v_and_b32_e32 v0, 0xc0, v195
	v_lshlrev_b32_e32 v1, 1, v194
	v_fma_f32 v156, v2, s12, v34
	v_fma_f32 v157, v3, s12, v34
	v_and_or_b32 v0, v32, 24, v0
	v_and_b32_e32 v1, 32, v1
	v_and_b32_e32 v2, 0x100, v32
	s_cmp_lg_u32 0, -1
	v_cndmask_b32_e64 v209, v16, 1.0, s[0:1]
	v_or3_b32 v0, v0, v1, v2
	s_cselect_b32 s0, 0, 0
	v_fma_f32 v120, v14, s12, v34
	v_fma_f32 v121, v15, s12, v34
	v_fma_f32 v122, v12, s12, v34
	v_fma_f32 v123, v13, s12, v34
	v_fma_f32 v124, v10, s12, v34
	v_fma_f32 v125, v11, s12, v34
	v_fma_f32 v126, v8, s12, v34
	v_fma_f32 v127, v9, s12, v34
	v_fma_f32 v152, v6, s12, v34
	v_fma_f32 v153, v7, s12, v34
	v_fma_f32 v154, v4, s12, v34
	v_fma_f32 v155, v5, s12, v34
	v_add_u32_e32 v201, s0, v0
	s_cmp_lt_i32 s57, 3
	v_cmp_gt_u32_e64 s[0:1], 32, v194
	v_lshl_add_u32 v200, v196, 2, s53
	s_waitcnt lgkmcnt(0)
	s_barrier
	s_cbranch_scc1 .LBB0_2272
	v_lshl_add_u32 v0, s58, 6, v202
	v_mov_b32_e32 v210, 0
	v_lshl_add_u64 v[186:187], s[2:3], 0, v[184:185]
	v_lshl_add_u64 v[188:189], s[36:37], 0, v[184:185]
	s_mov_b32 s38, 2
	v_add_u32_e32 v190, 0x80, v0
	v_mov_b32_e32 v48, 0
	v_mov_b32_e32 v49, v210
	v_mov_b32_e32 v50, v210
	v_mov_b32_e32 v51, v210
	v_mov_b32_e32 v52, v210
	v_mov_b32_e32 v53, v210
	v_mov_b32_e32 v54, v210
	v_mov_b32_e32 v55, v210
	v_mov_b32_e32 v56, v210
	v_mov_b32_e32 v57, v210
	v_mov_b32_e32 v58, v210
	v_mov_b32_e32 v59, v210
	v_mov_b32_e32 v60, v210
	v_mov_b32_e32 v61, v210
	v_mov_b32_e32 v62, v210
	v_mov_b32_e32 v63, v210
	v_mov_b32_e32 v32, 0
	v_mov_b32_e32 v33, v210
	v_mov_b32_e32 v34, v210
	v_mov_b32_e32 v35, v210
	v_mov_b32_e32 v36, v210
	v_mov_b32_e32 v37, v210
	v_mov_b32_e32 v38, v210
	v_mov_b32_e32 v39, v210
	v_mov_b32_e32 v40, v210
	v_mov_b32_e32 v41, v210
	v_mov_b32_e32 v42, v210
	v_mov_b32_e32 v43, v210
	v_mov_b32_e32 v44, v210
	v_mov_b32_e32 v45, v210
	v_mov_b32_e32 v46, v210
	v_mov_b32_e32 v47, v210
	v_mov_b32_e32 v16, 0
	v_mov_b32_e32 v17, v210
	v_mov_b32_e32 v18, v210
	v_mov_b32_e32 v19, v210
	v_mov_b32_e32 v20, v210
	v_mov_b32_e32 v21, v210
	v_mov_b32_e32 v22, v210
	v_mov_b32_e32 v23, v210
	v_mov_b32_e32 v24, v210
	v_mov_b32_e32 v25, v210
	v_mov_b32_e32 v26, v210
	v_mov_b32_e32 v27, v210
	v_mov_b32_e32 v28, v210
	v_mov_b32_e32 v29, v210
	v_mov_b32_e32 v30, v210
	v_mov_b32_e32 v31, v210
	v_mov_b32_e32 v0, 0
	v_mov_b32_e32 v1, v210
	v_mov_b32_e32 v2, v210
	v_mov_b32_e32 v3, v210
	v_mov_b32_e32 v4, v210
	v_mov_b32_e32 v5, v210
	v_mov_b32_e32 v6, v210
	v_mov_b32_e32 v7, v210
	v_mov_b32_e32 v8, v210
	v_mov_b32_e32 v9, v210
	v_mov_b32_e32 v10, v210
	v_mov_b32_e32 v11, v210
	v_mov_b32_e32 v12, v210
	v_mov_b32_e32 v13, v210
	v_mov_b32_e32 v14, v210
	v_mov_b32_e32 v15, v210
	s_branch .LBB0_2261
.LBB0_2259:
	s_or_b64 exec, exec, s[36:37]
	s_waitcnt lgkmcnt(0)
	v_add_u32_e32 v153, s53, v198
	s_waitcnt vmcnt(2)
	ds_read_b128 v[154:157], v153 offset:224
	s_waitcnt vmcnt(1)
	ds_read_b128 v[158:161], v153 offset:192
	s_waitcnt vmcnt(0)
	ds_read_b128 v[162:165], v153 offset:128
	ds_read_b128 v[166:169], v153 offset:160
	s_waitcnt lgkmcnt(3)
	v_mul_f32_e64 v62, v62, v156
	v_mul_f32_e64 v63, v63, v157
	v_mul_f32_e64 v60, v60, v154
	v_mul_f32_e64 v61, v61, v155
	s_waitcnt lgkmcnt(2)
	v_mul_f32_e64 v58, v58, v160
	v_mul_f32_e64 v59, v59, v161
	v_mul_f32_e64 v56, v56, v158
	v_mul_f32_e64 v57, v57, v159
	s_waitcnt lgkmcnt(0)
	v_mul_f32_e64 v54, v54, v168
	v_mul_f32_e64 v55, v55, v169
	v_mul_f32_e64 v52, v52, v166
	v_mul_f32_e64 v53, v53, v167
	v_mul_f32_e64 v50, v50, v164
	v_mul_f32_e64 v51, v51, v165
	v_mul_f32_e64 v48, v48, v162
	v_mul_f32_e64 v49, v49, v163
	v_mul_f32_e64 v46, v46, v156
	v_mul_f32_e64 v47, v47, v157
	v_mul_f32_e64 v44, v44, v154
	v_mul_f32_e64 v45, v45, v155
	v_mul_f32_e64 v42, v42, v160
	v_mul_f32_e64 v43, v43, v161
	v_mul_f32_e64 v40, v40, v158
	v_mul_f32_e64 v41, v41, v159
	v_mul_f32_e64 v38, v38, v168
	v_mul_f32_e64 v39, v39, v169
	v_mul_f32_e64 v36, v36, v166
	v_mul_f32_e64 v37, v37, v167
	v_mul_f32_e64 v34, v34, v164
	v_mul_f32_e64 v35, v35, v165
	v_mul_f32_e64 v32, v32, v162
	v_mul_f32_e64 v33, v33, v163
	v_mul_f32_e64 v30, v30, v156
	v_mul_f32_e64 v31, v31, v157
	v_mul_f32_e64 v28, v28, v154
	v_mul_f32_e64 v29, v29, v155
	v_mul_f32_e64 v26, v26, v160
	v_mul_f32_e64 v27, v27, v161
	v_mul_f32_e64 v24, v24, v158
	v_mul_f32_e64 v25, v25, v159
	v_mul_f32_e64 v22, v22, v168
	v_mul_f32_e64 v23, v23, v169
	v_mul_f32_e64 v20, v20, v166
	v_mul_f32_e64 v21, v21, v167
	v_mul_f32_e64 v18, v18, v164
	v_mul_f32_e64 v19, v19, v165
	v_mul_f32_e64 v16, v16, v162
	v_mul_f32_e64 v17, v17, v163
	v_mul_f32_e64 v14, v14, v156
	v_mul_f32_e64 v15, v15, v157
	v_mul_f32_e64 v12, v12, v154
	v_mul_f32_e64 v13, v13, v155
	v_mul_f32_e64 v10, v10, v160
	v_mul_f32_e64 v11, v11, v161
	v_mul_f32_e64 v8, v8, v158
	v_mul_f32_e64 v9, v9, v159
	v_mul_f32_e64 v6, v6, v168
	v_mul_f32_e64 v7, v7, v169
	v_mul_f32_e64 v4, v4, v166
	v_mul_f32_e64 v5, v5, v167
	v_mul_f32_e64 v2, v2, v164
	v_mul_f32_e64 v3, v3, v165
	v_mul_f32_e64 v0, v0, v162
	v_mul_f32_e64 v1, v1, v163
; template <bool SEL>
; __device__ __forceinline__ void partialSM(f32x16& p0, f32x16& p1, float& m_reg, float& mn, float& alpha, unsigned selw) {
;     ...
;     const float mnL = -mn * C2;
; #pragma unroll
;     for (int r = 0; r < 16; ++r) p0[r] = fmaf(p0[r], C2, mnL);
; #pragma unroll
;     for (int r = 0; r < 16; ++r) p1[r] = fmaf(p1[r], C2, mnL);
; #pragma unroll
;     for (int r = 0; r < 16; ++r) p0[r] = __builtin_amdgcn_exp2f(p0[r]);
;     if (SEL) {
; #pragma unroll
;         for (int r = 0; r < 16; ++r) p0[r] = __uint_as_float(__float_as_uint(p0[r]) & sel_bit_mask(selw, r));
;     }
; }
; template <bool SEL>
; __device__ __forceinline__ void finishSM(f32x16& p0, f32x16& p1, float alpha, float& l_reg, bf16x8& pa0, bf16x8& pa1, bf16x8& pa2, bf16x8& pa3, unsigned selw) {
; #pragma unroll
;     for (int r = 0; r < 16; ++r) p1[r] = __builtin_amdgcn_exp2f(p1[r]);
;     if (SEL) {
; #pragma unroll
;         for (int r = 0; r < 16; ++r) p1[r] = __uint_as_float(__float_as_uint(p1[r]) & sel_bit_mask(selw, 16 + r));
;     }
;     float ps = 0;
; #pragma unroll
;     for (int r = 0; r < 16; ++r) ps += p0[r];
; #pragma unroll
;     for (int r = 0; r < 16; ++r) ps += p1[r];
;     { auto rr = __builtin_amdgcn_permlane32_swap(__float_as_uint(ps), __float_as_uint(ps), false, false);
;       ps = __uint_as_float(rr[0]) + __uint_as_float(rr[1]); }
;     l_reg = l_reg * alpha + ps;
;     ...
;     PK4(p0, 0, pa0); PK4(p0, 8, pa1); PK4(p1, 0, pa2); PK4(p1, 8, pa3);
; template <int KB, int QREG>
; __device__ __forceinline__ void qkt(f32x16& p0, f32x16& p1, const char* K_lds, int r32, int hi, const bf16x8* qr, const char* qlds) {
;     p0 = f32x16{}; p1 = f32x16{};
;     const char* kb[4];
; #pragma unroll
;     for (int dd = 0; dd < 4; ++dd) kb[dd] = K_lds + KB * SHM_K + KSWZ(r32, (dd * 16 + hi * 8) * 2);
; #pragma unroll
;     for (int d0 = 0; d0 < 8; ++d0) { const char* a = kb[d0 & 3] + (d0 >> 2) * 128;
;         bf16x8 b0 = *reinterpret_cast<const bf16x8*>(a);
;         bf16x8 b1 = *reinterpret_cast<const bf16x8*>(a + 32 * 256);
;         const bf16x8 qf = (d0 < QREG) ? qr[d0 < QREG ? d0 : 0] : *reinterpret_cast<const bf16x8*>(qlds + (d0 - QREG) * 1024);
;         p0 = __builtin_amdgcn_mfma_f32_32x32x16_bf16(b0, qf, p0, 0, 0, 0);
;         p1 = __builtin_amdgcn_mfma_f32_32x32x16_bf16(b1, qf, p1, 0, 0, 0); }
.LBB0_2260:
	v_cndmask_b32_e64 v168, v152, v215, s[2:3]
	s_waitcnt vmcnt(2)
	v_mul_f32_e32 v158, 0xbe0293ee, v168
	v_mov_b32_e32 v178, v158
	v_fmamk_f32 v112, v112, 0x3e0293ee, v158
	v_fmamk_f32 v113, v113, 0x3e0293ee, v158
	v_fmamk_f32 v114, v114, 0x3e0293ee, v158
	v_fmamk_f32 v115, v115, 0x3e0293ee, v158
	v_fmamk_f32 v116, v116, 0x3e0293ee, v158
	v_fmamk_f32 v117, v117, 0x3e0293ee, v158
	v_fmamk_f32 v118, v118, 0x3e0293ee, v158
	v_fmamk_f32 v119, v119, 0x3e0293ee, v158
	v_fmamk_f32 v154, v120, 0x3e0293ee, v158
	v_fmamk_f32 v155, v121, 0x3e0293ee, v158
	v_fmamk_f32 v156, v122, 0x3e0293ee, v158
	v_fmamk_f32 v157, v123, 0x3e0293ee, v158
	v_fmamk_f32 v159, v124, 0x3e0293ee, v158
	s_waitcnt vmcnt(1)
	v_fmamk_f32 v162, v125, 0x3e0293ee, v158
	s_waitcnt vmcnt(0)
	v_fmamk_f32 v165, v126, 0x3e0293ee, v158
	v_fmac_f32_e32 v178, 0x3e0293ee, v127
	v_exp_f32_e32 v174, v112
	v_exp_f32_e32 v176, v113
	v_exp_f32_e32 v172, v114
	v_exp_f32_e32 v175, v115
	v_exp_f32_e32 v171, v116
	v_exp_f32_e32 v173, v117
	v_exp_f32_e32 v169, v118
	v_exp_f32_e32 v170, v119
	v_exp_f32_e32 v163, v154
	v_exp_f32_e32 v166, v155
	v_exp_f32_e32 v161, v156
	v_exp_f32_e32 v164, v157
	v_exp_f32_e32 v160, v159
	v_exp_f32_e32 v167, v162
	v_exp_f32_e32 v162, v165
	v_exp_f32_e32 v165, v178
	v_fma_f32 v120, v110, s12, v158
	v_fma_f32 v121, v111, s12, v158
	v_fma_f32 v122, v108, s12, v158
	v_fma_f32 v123, v109, s12, v158
	v_fma_f32 v124, v106, s12, v158
	v_fma_f32 v125, v107, s12, v158
	v_fma_f32 v126, v104, s12, v158
	v_fma_f32 v127, v105, s12, v158
	v_fma_f32 v152, v102, s12, v158
	v_fma_f32 v153, v103, s12, v158
	v_fma_f32 v154, v100, s12, v158
	v_fma_f32 v155, v101, s12, v158
	v_fma_f32 v156, v98, s12, v158
	v_fma_f32 v157, v99, s12, v158
	v_fma_f32 v159, v97, s12, v158
	v_fma_f32 v158, v96, s12, v158
	v_add_f32_e32 v96, v213, v214
	v_fmac_f32_e32 v96, v209, v210
	v_add_f32_e32 v210, v216, v217
	s_add_i32 s38, s38, 2
	v_fmac_f32_e32 v210, v96, v191
	s_cmp_ge_i32 s38, s57
	v_add_u32_e32 v190, 0x80, v190
	v_mov_b32_e32 v209, v177
	s_waitcnt lgkmcnt(0)
	s_barrier
	s_cbranch_scc1 .LBB0_2273
.LBB0_2261:
	ds_read_b128 v[64:67], v205 offset:49152
	s_waitcnt vmcnt(2)
	ds_read_b128 v[100:103], v205 offset:49280
	v_exp_f32_e32 v158, v158
	v_exp_f32_e32 v159, v159
	v_exp_f32_e32 v156, v156
	s_waitcnt lgkmcnt(1)
	v_mfma_f32_32x32x16_bf16 v[84:99], v[64:67], v[148:151], 0
	ds_read_b128 v[64:67], v205 offset:57344
	s_waitcnt vmcnt(1)
	ds_read_b128 v[104:107], v205 offset:57472
	v_exp_f32_e32 v157, v157
	v_exp_f32_e32 v154, v154
	v_exp_f32_e32 v155, v155
	v_exp_f32_e32 v152, v152
	v_exp_f32_e32 v153, v153
	v_exp_f32_e32 v126, v126
	s_waitcnt lgkmcnt(1)
	v_mfma_f32_32x32x16_bf16 v[68:83], v[64:67], v[148:151], 0
	ds_read_b128 v[64:67], v206 offset:49152
	s_waitcnt vmcnt(0)
	ds_read_b128 v[108:111], v206 offset:49280
	ds_read_b128 v[112:115], v206 offset:57344
	ds_read_b128 v[116:119], v206 offset:57472
	v_exp_f32_e32 v127, v127
	v_exp_f32_e32 v124, v124
	v_exp_f32_e32 v125, v125
	v_exp_f32_e32 v122, v122
	v_exp_f32_e32 v123, v123
	v_exp_f32_e32 v120, v120
	s_waitcnt lgkmcnt(3)
	v_mfma_f32_32x32x16_bf16 v[84:99], v[64:67], v[144:147], v[84:99]
	ds_read_b128 v[64:67], v207 offset:49152
	ds_read_b128 v[178:181], v207 offset:49280
	ds_read_b128 v[214:217], v207 offset:57344
	ds_read_b128 v[218:221], v207 offset:57472
	ds_read_b128 v[222:225], v208 offset:49152
	ds_read_b128 v[226:229], v208 offset:49280
	ds_read_b128 v[230:233], v208 offset:57344
	ds_read_b128 v[234:237], v208 offset:57472
	v_exp_f32_e32 v121, v121
	s_waitcnt lgkmcnt(9)
	v_mfma_f32_32x32x16_bf16 v[68:83], v[112:115], v[144:147], v[68:83]
	ds_read_b128 v[112:115], v204
	ds_read_b128 v[238:241], v204 offset:1024
	s_waitcnt lgkmcnt(9)
	v_mfma_f32_32x32x16_bf16 v[84:99], v[64:67], v[140:143], v[84:99]
	v_add_f32_e32 v64, 0, v174
	v_add_f32_e32 v64, v176, v64
	v_add_f32_e32 v64, v172, v64
	v_add_f32_e32 v64, v175, v64
	v_add_f32_e32 v64, v171, v64
	v_add_f32_e32 v64, v173, v64
	v_add_f32_e32 v64, v169, v64
	s_waitcnt lgkmcnt(7)
	v_mfma_f32_32x32x16_bf16 v[68:83], v[214:217], v[140:143], v[68:83]
	v_add_f32_e32 v64, v170, v64
	v_add_f32_e32 v64, v163, v64
	v_add_f32_e32 v64, v166, v64
	v_add_f32_e32 v64, v161, v64
	v_add_f32_e32 v64, v164, v64
	v_add_f32_e32 v64, v160, v64
	v_add_f32_e32 v64, v167, v64
	s_waitcnt lgkmcnt(5)
	v_mfma_f32_32x32x16_bf16 v[84:99], v[222:225], v[136:139], v[84:99]
	v_add_f32_e32 v64, v162, v64
	v_add_f32_e32 v64, v165, v64
	v_add_f32_e32 v64, v158, v64
	v_add_f32_e32 v64, v159, v64
	v_add_f32_e32 v64, v156, v64
	v_add_f32_e32 v64, v157, v64
	v_add_f32_e32 v64, v154, v64
	s_waitcnt lgkmcnt(3)
	v_mfma_f32_32x32x16_bf16 v[68:83], v[230:233], v[136:139], v[68:83]
	v_add_f32_e32 v64, v155, v64
	v_add_f32_e32 v64, v152, v64
	v_add_f32_e32 v64, v153, v64
	v_add_f32_e32 v64, v126, v64
	v_add_f32_e32 v64, v127, v64
	v_add_f32_e32 v64, v124, v64
	v_add_f32_e32 v64, v125, v64
	v_mfma_f32_32x32x16_bf16 v[84:99], v[100:103], v[132:135], v[84:99]
	v_add_f32_e32 v64, v122, v64
	v_add_f32_e32 v64, v123, v64
	v_add_f32_e32 v64, v120, v64
	v_add_f32_e32 v213, v121, v64
	v_mov_b32_e32 v214, v213
	v_cvt_pk_bf16_f32 v64, v174, v176
	v_cvt_pk_bf16_f32 v65, v172, v175
	v_mfma_f32_32x32x16_bf16 v[68:83], v[104:107], v[132:135], v[68:83]
	v_cvt_pk_bf16_f32 v66, v171, v173
	s_nop 0
	v_permlane32_swap_b32_e32 v213, v214
	v_cvt_pk_bf16_f32 v67, v169, v170
	v_permlane32_swap_b32_e32 v64, v66
	v_cvt_pk_bf16_f32 v100, v163, v166
	v_mfma_f32_32x32x16_bf16 v[84:99], v[108:111], v[128:131], v[84:99]
	v_cvt_pk_bf16_f32 v101, v161, v164
	v_cvt_pk_bf16_f32 v102, v160, v167
	v_cvt_pk_bf16_f32 v103, v162, v165
	v_cvt_pk_bf16_f32 v104, v158, v159
	v_cvt_pk_bf16_f32 v105, v156, v157
	v_cvt_pk_bf16_f32 v106, v154, v155
	v_cvt_pk_bf16_f32 v107, v152, v153
	v_mfma_f32_32x32x16_bf16 v[68:83], v[116:119], v[128:131], v[68:83]
	v_cvt_pk_bf16_f32 v108, v126, v127
	v_cvt_pk_bf16_f32 v109, v124, v125
	v_cvt_pk_bf16_f32 v110, v122, v123
	v_cvt_pk_bf16_f32 v111, v120, v121
	v_permlane32_swap_b32_e32 v65, v67
	v_permlane32_swap_b32_e32 v100, v102
	s_waitcnt lgkmcnt(1)
; template <bool SEL>
; __device__ __forceinline__ void partialSM(f32x16& p0, f32x16& p1, float& m_reg, float& mn, float& alpha, unsigned selw) {
;     float pmax = p0[0];
; #pragma unroll
;     for (int r = 1; r < 16; ++r) pmax = fmaxf(pmax, p0[r]);
; #pragma unroll
;     for (int r = 0; r < 16; ++r) pmax = fmaxf(pmax, p1[r]);
;     { auto rr = __builtin_amdgcn_permlane32_swap(__float_as_uint(pmax), __float_as_uint(pmax), false, false);
;       pmax = fmaxf(__uint_as_float(rr[0]), __uint_as_float(rr[1])); }
;     constexpr float C2 = 1.4426950408889634f * SCALE;
;     if (__builtin_expect(__all((pmax - m_reg) * SCALE <= THR), 1)) { mn = m_reg; alpha = 1.f; }
;     else { mn = fmaxf(m_reg, pmax); alpha = __builtin_amdgcn_exp2f((m_reg - mn) * C2); m_reg = mn; }
; template <int VB>
; __device__ __forceinline__ void pv_tile(f32x16* o, int vb0, bf16x8 pa0, bf16x8 pa1, bf16x8 pa2, bf16x8 pa3) {
;     ...
;     PV_D0(0); PV_D0(1); PV_D0(2); PV_D0(3);
	v_mfma_f32_32x32x16_bf16 v[84:99], v[178:181], v[112:115], v[84:99]
	v_permlane32_swap_b32_e32 v101, v103
	v_permlane32_swap_b32_e32 v104, v106
	v_permlane32_swap_b32_e32 v105, v107
	v_permlane32_swap_b32_e32 v108, v110
	v_mfma_f32_32x32x16_bf16 v[68:83], v[218:221], v[112:115], v[68:83]
	v_permlane32_swap_b32_e32 v109, v111
	s_waitcnt lgkmcnt(0)
	v_mfma_f32_32x32x16_bf16 v[84:99], v[226:229], v[238:241], v[84:99]
	v_mfma_f32_32x32x16_bf16 v[68:83], v[234:237], v[238:241], v[68:83]
	v_ashrrev_i32_e32 v191, 31, v190
	v_add_u32_e32 v116, 32, v190
	v_lshlrev_b64 v[112:113], 10, v[190:191]
	v_ashrrev_i32_e32 v117, 31, v116
	v_lshl_add_u64 v[114:115], v[186:187], 0, v[112:113]
	v_lshlrev_b64 v[116:117], 10, v[116:117]
	v_lshl_add_u64 v[112:113], v[188:189], 0, v[112:113]
	v_lshl_add_u64 v[118:119], v[186:187], 0, v[116:117]
	global_load_dwordx4 v[152:155], v[114:115], off
	global_load_dwordx4 v[156:159], v[118:119], off
	v_lshl_add_u64 v[114:115], v[188:189], 0, v[116:117]
	global_load_dwordx4 v[160:163], v[112:113], off
	global_load_dwordx4 v[164:167], v[114:115], off
	ds_read_b64_tr_b16 v[112:113], v201 offset:0
	ds_read_b64_tr_b16 v[114:115], v201 offset:0x800
	ds_read_b64_tr_b16 v[116:117], v201 offset:0x1000
	ds_read_b64_tr_b16 v[118:119], v201 offset:0x1800
	ds_read_b64_tr_b16 v[120:121], v201 offset:0x2000
	ds_read_b64_tr_b16 v[122:123], v201 offset:0x2800
	ds_read_b64_tr_b16 v[124:125], v201 offset:0x3000
	ds_read_b64_tr_b16 v[126:127], v201 offset:0x3800
	s_waitcnt lgkmcnt(0)
	s_nop 0
	v_mfma_f32_32x32x16_bf16 v[48:63], v[64:67], v[112:115], v[48:63]
	ds_read_b64_tr_b16 v[112:113], v201 offset:0x200
	ds_read_b64_tr_b16 v[114:115], v201 offset:0xa00
	v_mfma_f32_32x32x16_bf16 v[48:63], v[100:103], v[116:119], v[48:63]
	ds_read_b64_tr_b16 v[116:117], v201 offset:0x1200
	ds_read_b64_tr_b16 v[118:119], v201 offset:0x1a00
	v_mfma_f32_32x32x16_bf16 v[48:63], v[104:107], v[120:123], v[48:63]
	ds_read_b64_tr_b16 v[120:121], v201 offset:0x2200
	ds_read_b64_tr_b16 v[122:123], v201 offset:0x2a00
	ds_read_b64_tr_b16 v[170:171], v201 offset:0x3200
	ds_read_b64_tr_b16 v[172:173], v201 offset:0x3a00
	s_waitcnt lgkmcnt(0)
	v_mfma_f32_32x32x16_bf16 v[48:63], v[108:111], v[124:127], v[48:63]
	v_mfma_f32_32x32x16_bf16 v[32:47], v[64:67], v[112:115], v[32:47]
	ds_read_b64_tr_b16 v[112:113], v201 offset:0x400
	ds_read_b64_tr_b16 v[114:115], v201 offset:0xc00
	v_mfma_f32_32x32x16_bf16 v[32:47], v[100:103], v[116:119], v[32:47]
	ds_read_b64_tr_b16 v[116:117], v201 offset:0x1400
	ds_read_b64_tr_b16 v[118:119], v201 offset:0x1c00
	v_mfma_f32_32x32x16_bf16 v[32:47], v[104:107], v[120:123], v[32:47]
	ds_read_b64_tr_b16 v[120:121], v201 offset:0x2400
	ds_read_b64_tr_b16 v[122:123], v201 offset:0x2c00
	ds_read_b64_tr_b16 v[124:125], v201 offset:0x3400
	ds_read_b64_tr_b16 v[126:127], v201 offset:0x3c00
	s_waitcnt lgkmcnt(0)
	v_mfma_f32_32x32x16_bf16 v[32:47], v[108:111], v[170:173], v[32:47]
	v_mfma_f32_32x32x16_bf16 v[16:31], v[64:67], v[112:115], v[16:31]
	ds_read_b64_tr_b16 v[112:113], v201 offset:0x600
	ds_read_b64_tr_b16 v[114:115], v201 offset:0xe00
	v_mfma_f32_32x32x16_bf16 v[16:31], v[100:103], v[116:119], v[16:31]
	ds_read_b64_tr_b16 v[116:117], v201 offset:0x1600
	ds_read_b64_tr_b16 v[118:119], v201 offset:0x1e00
	v_mfma_f32_32x32x16_bf16 v[16:31], v[104:107], v[120:123], v[16:31]
	ds_read_b64_tr_b16 v[120:121], v201 offset:0x2600
	ds_read_b64_tr_b16 v[122:123], v201 offset:0x2e00
	ds_read_b64_tr_b16 v[170:171], v201 offset:0x3600
	ds_read_b64_tr_b16 v[172:173], v201 offset:0x3e00
	s_waitcnt lgkmcnt(0)
	v_mfma_f32_32x32x16_bf16 v[16:31], v[108:111], v[124:127], v[16:31]
	v_mfma_f32_32x32x16_bf16 v[0:15], v[64:67], v[112:115], v[0:15]
	v_max_f32_e32 v124, v85, v85
	v_max_f32_e32 v125, v84, v84
	v_max_f32_e32 v124, v125, v124
	v_max3_f32 v124, v124, v86, v87
	v_max3_f32 v124, v124, v88, v89
	v_max3_f32 v64, v124, v90, v91
	v_max3_f32 v64, v64, v92, v93
	v_max3_f32 v64, v64, v94, v95
	v_mfma_f32_32x32x16_bf16 v[0:15], v[100:103], v[116:119], v[0:15]
	v_max3_f32 v64, v64, v96, v97
	v_max3_f32 v64, v64, v98, v99
	v_max3_f32 v64, v64, v68, v69
	v_max3_f32 v64, v64, v70, v71
	v_max3_f32 v64, v64, v72, v73
	v_max3_f32 v64, v64, v74, v75
	v_max3_f32 v64, v64, v76, v77
	v_max3_f32 v64, v64, v78, v79
	v_mfma_f32_32x32x16_bf16 v[0:15], v[104:107], v[120:123], v[0:15]
	v_max3_f32 v64, v64, v80, v81
	v_max3_f32 v64, v64, v82, v83
	v_mov_b32_e32 v65, v64
	s_nop 1
	v_permlane32_swap_b32_e32 v64, v65
	v_max_f32_e32 v65, v65, v65
	v_max_f32_e32 v64, v64, v64
	v_max_f32_e32 v64, v64, v65
	v_max_f32_e32 v66, v168, v168
	v_sub_f32_e32 v65, v64, v168
	v_max_f32_e32 v64, v66, v64
	v_mfma_f32_32x32x16_bf16 v[0:15], v[108:111], v[170:173], v[0:15]
	v_sub_f32_e32 v66, v168, v64
	v_mul_f32_e32 v66, 0x3e0293ee, v66
	v_mul_f32_e32 v65, 0x3db504f3, v65
	v_exp_f32_e32 v66, v66
	v_cmp_ge_f32_e32 vcc, s5, v65
	s_cmp_eq_u64 vcc, exec
	s_cselect_b64 s[2:3], -1, 0
	s_barrier
	s_waitcnt vmcnt(0)
	v_cndmask_b32_e64 v191, v66, 1.0, s[2:3]
	v_cmp_gt_f32_e32 vcc, 1.0, v191
	s_waitcnt vmcnt(3)
	ds_write_b128 v211, v[152:155]
	s_waitcnt vmcnt(2)
	ds_write_b128 v212, v[156:159]
	s_waitcnt vmcnt(1)
	ds_write_b128 v199, v[160:163] offset:32768
	s_waitcnt vmcnt(0)
	ds_write_b128 v199, v[164:167] offset:40960
	s_cbranch_vccz .LBB0_2265
	s_and_saveexec_b64 s[36:37], s[0:1]
	ds_write_b32 v200, v191 offset:128
	s_or_b64 exec, exec, s[36:37]
	s_waitcnt lgkmcnt(0)
	v_add_u32_e32 v65, s53, v198
	ds_read_b128 v[100:103], v65 offset:224
	ds_read_b128 v[104:107], v65 offset:192
	ds_read_b128 v[108:111], v65 offset:160
	ds_read_b128 v[112:115], v65 offset:128
	s_waitcnt lgkmcnt(3)
	v_mul_f32_e64 v60, v60, v100
	v_mul_f32_e64 v61, v61, v101
	s_waitcnt lgkmcnt(2)
	v_mul_f32_e64 v56, v56, v104
	v_mul_f32_e64 v57, v57, v105
	s_waitcnt lgkmcnt(1)
	v_mul_f32_e64 v52, v52, v108
	v_mul_f32_e64 v53, v53, v109
	v_mul_f32_e64 v62, v62, v102
	v_mul_f32_e64 v63, v63, v103
	v_mul_f32_e64 v58, v58, v106
	v_mul_f32_e64 v59, v59, v107
	v_mul_f32_e64 v54, v54, v110
	v_mul_f32_e64 v55, v55, v111
	s_waitcnt lgkmcnt(0)
	v_mul_f32_e64 v50, v50, v114
	v_mul_f32_e64 v51, v51, v115
	v_mul_f32_e64 v48, v48, v112
	v_mul_f32_e64 v49, v49, v113
	v_mul_f32_e64 v44, v44, v100
	v_mul_f32_e64 v45, v45, v101
	v_mul_f32_e64 v40, v40, v104
	v_mul_f32_e64 v41, v41, v105
	v_mul_f32_e64 v36, v36, v108
	v_mul_f32_e64 v37, v37, v109
	v_mul_f32_e64 v46, v46, v102
	v_mul_f32_e64 v47, v47, v103
	v_mul_f32_e64 v42, v42, v106
	v_mul_f32_e64 v43, v43, v107
	v_mul_f32_e64 v38, v38, v110
	v_mul_f32_e64 v39, v39, v111
	v_mul_f32_e64 v34, v34, v114
	v_mul_f32_e64 v35, v35, v115
	v_mul_f32_e64 v32, v32, v112
	v_mul_f32_e64 v33, v33, v113
	v_mul_f32_e64 v28, v28, v100
	v_mul_f32_e64 v29, v29, v101
	v_mul_f32_e64 v24, v24, v104
	v_mul_f32_e64 v25, v25, v105
	v_mul_f32_e64 v20, v20, v108
	v_mul_f32_e64 v21, v21, v109
	v_mul_f32_e64 v30, v30, v102
	v_mul_f32_e64 v31, v31, v103
	v_mul_f32_e64 v26, v26, v106
	v_mul_f32_e64 v27, v27, v107
	v_mul_f32_e64 v22, v22, v110
	v_mul_f32_e64 v23, v23, v111
	v_mul_f32_e64 v18, v18, v114
	v_mul_f32_e64 v19, v19, v115
	v_mul_f32_e64 v16, v16, v112
	v_mul_f32_e64 v17, v17, v113
	v_mul_f32_e64 v12, v12, v100
	v_mul_f32_e64 v13, v13, v101
	v_mul_f32_e64 v8, v8, v104
	v_mul_f32_e64 v9, v9, v105
	v_mul_f32_e64 v4, v4, v108
	v_mul_f32_e64 v5, v5, v109
	v_mul_f32_e64 v14, v14, v102
	v_mul_f32_e64 v15, v15, v103
	v_mul_f32_e64 v10, v10, v106
	v_mul_f32_e64 v11, v11, v107
	v_mul_f32_e64 v6, v6, v110
	v_mul_f32_e64 v7, v7, v111
	v_mul_f32_e64 v2, v2, v114
	v_mul_f32_e64 v3, v3, v115
	v_mul_f32_e64 v0, v0, v112
	v_mul_f32_e64 v1, v1, v113

; #define SBAR() __builtin_amdgcn_sched_barrier(0)
; __device__ __forceinline__ unsigned sel_bit_mask(unsigned w, int b) { unsigned m; asm("v_bfe_i32 %0, %1, %2, 1" : "=v"(m) : "v"(w), "n"(b)); return m; }
; #define SLOAD_H(Kp, Vp, k0) do { S.st_v0 = load8(ROW(Vp, k0, sr)); S.st_v1 = load8(ROW(Vp, k0, 32 + sr));              \
;                          S.st_k0 = load8(ROW(Kp, k0, sr)); S.st_k1 = load8(ROW(Kp, k0, 32 + sr)); } while (0)
; template <bool SEL>
; __device__ __forceinline__ void finishSM(f32x16& p0, f32x16& p1, float alpha, float& l_reg, bf16x8& pa0, bf16x8& pa1, bf16x8& pa2, bf16x8& pa3, unsigned selw) {
; #pragma unroll
;     for (int r = 0; r < 16; ++r) p1[r] = __builtin_amdgcn_exp2f(p1[r]);
;     if (SEL) {
; #pragma unroll
;         for (int r = 0; r < 16; ++r) p1[r] = __uint_as_float(__float_as_uint(p1[r]) & sel_bit_mask(selw, 16 + r));
;     }
;     float ps = 0;
; #pragma unroll
;     for (int r = 0; r < 16; ++r) ps += p0[r];
; #pragma unroll
;     for (int r = 0; r < 16; ++r) ps += p1[r];
;     { auto rr = __builtin_amdgcn_permlane32_swap(__float_as_uint(ps), __float_as_uint(ps), false, false);
;       ps = __uint_as_float(rr[0]) + __uint_as_float(rr[1]); }
;     l_reg = l_reg * alpha + ps;
;     ...
;     PK4(p0, 0, pa0); PK4(p0, 8, pa1); PK4(p1, 0, pa2); PK4(p1, 8, pa3);
; template <int QS, int KS, int OS, bool SEL, int QREG, bool MERGE>
; __device__ __forceinline__ void attn_block(const BlockRef& cur, const BlockRef& nxt, int skv, int W, char* lds, Seam& S, const MergeArgs& MG, const int wid) {
;     ...
;     const bool even = (NT & 1) == 0;
;     if (even) { SBAR(); mwB = MLOAD(NT - 1); qkt<1, QREG>(pB0, pB1, K_lds, r32, hi, S.qr, qlds); SBAR(); }
;     SLOAD_H(nxt.K, nxt.V, kbn); SBAR();
; #pragma unroll
;     for (int d0 = 0; d0 < 8; ++d0) S.qr[d0] = load8(nxt.Q + (size_t)(wid * QBLK + r32) * QS + d0 * 16 + hi * 8);
;     SBAR();
;     finishSM<SEL>(pA0, pA1, alA, l_reg, pa0, pa1, pa2, pa3, mwA); SBAR();
;     pv_tile<0>(o, vb0, pa0, pa1, pa2, pa3);
.LBB0_2275:
	s_add_i32 s2, s56, 0xc0000001
	s_andn2_b32 s2, s2, 63
	s_cmp_gt_i32 s56, 0x3fffffff
	s_cselect_b32 s2, s2, 0
	s_waitcnt vmcnt(3)
	v_add_u32_e32 v96, s2, v202
	v_add_u32_e32 v98, s2, v203
	v_ashrrev_i32_e32 v97, 31, v96
	v_ashrrev_i32_e32 v99, 31, v98
	s_waitcnt vmcnt(1)
	v_lshlrev_b64 v[104:105], 10, v[96:97]
	v_lshlrev_b64 v[106:107], 10, v[98:99]
	v_lshl_add_u64 v[96:97], s[28:29], 0, v[104:105]
	v_lshl_add_u64 v[98:99], s[28:29], 0, v[106:107]
	v_lshl_add_u64 v[104:105], s[30:31], 0, v[104:105]
	v_lshl_add_u64 v[106:107], s[30:31], 0, v[106:107]
	v_lshl_add_u64 v[96:97], v[96:97], 0, v[184:185]
	v_lshl_add_u64 v[100:101], v[98:99], 0, v[184:185]
	v_lshl_add_u64 v[104:105], v[104:105], 0, v[184:185]
	s_waitcnt vmcnt(0)
	v_lshl_add_u64 v[108:109], v[106:107], 0, v[184:185]
	global_load_dwordx4 v[96:99], v[96:97], off
	s_nop 0
	global_load_dwordx4 v[100:103], v[100:101], off
	s_nop 0
	global_load_dwordx4 v[104:107], v[104:105], off
	s_nop 0
	global_load_dwordx4 v[108:111], v[108:109], off
	v_or_b32_e32 v112, s6, v196
	v_mov_b32_e32 v113, v185
	v_lshlrev_b64 v[112:113], 10, v[112:113]
	v_lshlrev_b32_e32 v114, 3, v197
	v_ashrrev_i32_e32 v115, 31, v114
	v_lshl_add_u64 v[112:113], s[8:9], 0, v[112:113]
	v_lshl_add_u64 v[116:117], v[114:115], 1, v[112:113]
	global_load_dwordx4 v[148:151], v[116:117], off
	global_load_dwordx4 v[144:147], v[116:117], off offset:32
	global_load_dwordx4 v[140:143], v[116:117], off offset:64
	global_load_dwordx4 v[136:139], v[116:117], off offset:96
	global_load_dwordx4 v[132:135], v[116:117], off offset:128
	global_load_dwordx4 v[128:131], v[116:117], off offset:160
	global_load_dwordx4 v[112:115], v[116:117], off offset:192
	s_nop 0
	global_load_dwordx4 v[116:119], v[116:117], off offset:224
	v_exp_f32_e32 v187, v120
	v_add_f32_e32 v120, 0, v174
	v_add_f32_e32 v120, v176, v120
	v_add_f32_e32 v120, v172, v120
	v_add_f32_e32 v120, v175, v120
	v_add_f32_e32 v120, v171, v120
	v_add_f32_e32 v120, v173, v120
	v_add_f32_e32 v120, v169, v120
	v_add_f32_e32 v120, v170, v120
	v_add_f32_e32 v120, v163, v120
	v_add_f32_e32 v120, v166, v120
	v_add_f32_e32 v120, v161, v120
	v_add_f32_e32 v120, v164, v120
	v_exp_f32_e32 v158, v158
	v_add_f32_e32 v120, v160, v120
	v_exp_f32_e32 v159, v159
	v_add_f32_e32 v120, v167, v120
	v_exp_f32_e32 v177, v156
	v_add_f32_e32 v120, v162, v120
	v_exp_f32_e32 v157, v157
	v_add_f32_e32 v120, v165, v120
	v_exp_f32_e32 v178, v154
	v_add_f32_e32 v120, v158, v120
	v_exp_f32_e32 v179, v155
	v_add_f32_e32 v120, v159, v120
	v_exp_f32_e32 v180, v152
	v_add_f32_e32 v120, v177, v120
	v_exp_f32_e32 v181, v153
	v_add_f32_e32 v120, v157, v120
	v_exp_f32_e32 v126, v126
	v_add_f32_e32 v120, v178, v120
	v_exp_f32_e32 v127, v127
	v_add_f32_e32 v120, v179, v120
	v_exp_f32_e32 v182, v124
	v_add_f32_e32 v120, v180, v120
	v_exp_f32_e32 v183, v125
	v_add_f32_e32 v120, v181, v120
	v_exp_f32_e32 v184, v122
	v_add_f32_e32 v120, v126, v120
	v_exp_f32_e32 v186, v123
	v_add_f32_e32 v120, v127, v120
	v_add_f32_e32 v120, v182, v120
	v_exp_f32_e32 v121, v121
	v_add_f32_e32 v120, v183, v120
	v_add_f32_e32 v120, v184, v120
	v_add_f32_e32 v120, v186, v120
	v_add_f32_e32 v120, v187, v120
	v_add_f32_e32 v120, v121, v120
	v_mov_b32_e32 v122, v120
	s_nop 1
	v_permlane32_swap_b32_e32 v120, v122
	v_add_f32_e32 v120, v120, v122
	v_fmac_f32_e32 v120, v210, v209
	v_cvt_pk_bf16_f32 v122, v174, v176
	v_cvt_pk_bf16_f32 v123, v172, v175
	v_cvt_pk_bf16_f32 v124, v171, v173
	v_cvt_pk_bf16_f32 v125, v169, v170
	v_cvt_pk_bf16_f32 v152, v163, v166
	v_cvt_pk_bf16_f32 v153, v161, v164
	v_cvt_pk_bf16_f32 v154, v160, v167
	v_cvt_pk_bf16_f32 v155, v162, v165
	v_cvt_pk_bf16_f32 v156, v158, v159
	v_cvt_pk_bf16_f32 v157, v177, v157
	v_cvt_pk_bf16_f32 v158, v178, v179
	v_cvt_pk_bf16_f32 v159, v180, v181
	v_cvt_pk_bf16_f32 v160, v126, v127
	v_cvt_pk_bf16_f32 v161, v182, v183
	v_cvt_pk_bf16_f32 v162, v184, v186
	v_cvt_pk_bf16_f32 v163, v187, v121
	s_nop 0
	v_permlane32_swap_b32_e32 v122, v124
	v_permlane32_swap_b32_e32 v123, v125
	v_permlane32_swap_b32_e32 v152, v154
	v_permlane32_swap_b32_e32 v153, v155
	v_permlane32_swap_b32_e32 v156, v158
	v_permlane32_swap_b32_e32 v157, v159
	v_permlane32_swap_b32_e32 v160, v162
	v_permlane32_swap_b32_e32 v161, v163
	ds_read_b64_tr_b16 v[164:165], v201 offset:0
	ds_read_b64_tr_b16 v[166:167], v201 offset:0x800
	ds_read_b64_tr_b16 v[170:171], v201 offset:0x1000
	ds_read_b64_tr_b16 v[172:173], v201 offset:0x1800
	ds_read_b64_tr_b16 v[174:175], v201 offset:0x2000
	ds_read_b64_tr_b16 v[176:177], v201 offset:0x2800
	ds_read_b64_tr_b16 v[178:179], v201 offset:0x3000
	ds_read_b64_tr_b16 v[180:181], v201 offset:0x3800
	s_waitcnt lgkmcnt(0)
	s_nop 0
	v_mfma_f32_32x32x16_bf16 v[48:63], v[122:125], v[164:167], v[48:63]
	ds_read_b64_tr_b16 v[164:165], v201 offset:0x200
	ds_read_b64_tr_b16 v[166:167], v201 offset:0xa00
	v_mfma_f32_32x32x16_bf16 v[48:63], v[152:155], v[170:173], v[48:63]
	ds_read_b64_tr_b16 v[170:171], v201 offset:0x1200
	ds_read_b64_tr_b16 v[172:173], v201 offset:0x1a00
	v_mfma_f32_32x32x16_bf16 v[48:63], v[156:159], v[174:177], v[48:63]
	ds_read_b64_tr_b16 v[174:175], v201 offset:0x2200
	ds_read_b64_tr_b16 v[176:177], v201 offset:0x2a00
	ds_read_b64_tr_b16 v[186:187], v201 offset:0x3200
	ds_read_b64_tr_b16 v[188:189], v201 offset:0x3a00
	s_waitcnt lgkmcnt(0)
; template <bool SEL>
; __device__ __forceinline__ void partialSM(f32x16& p0, f32x16& p1, float& m_reg, float& mn, float& alpha, unsigned selw) {
;     float pmax = p0[0];
; #pragma unroll
;     for (int r = 1; r < 16; ++r) pmax = fmaxf(pmax, p0[r]);
; #pragma unroll
;     for (int r = 0; r < 16; ++r) pmax = fmaxf(pmax, p1[r]);
;     { auto rr = __builtin_amdgcn_permlane32_swap(__float_as_uint(pmax), __float_as_uint(pmax), false, false);
;       pmax = fmaxf(__uint_as_float(rr[0]), __uint_as_float(rr[1])); }
;     constexpr float C2 = 1.4426950408889634f * SCALE;
;     if (__builtin_expect(__all((pmax - m_reg) * SCALE <= THR), 1)) { mn = m_reg; alpha = 1.f; }
;     else { mn = fmaxf(m_reg, pmax); alpha = __builtin_amdgcn_exp2f((m_reg - mn) * C2); m_reg = mn; }
	v_mfma_f32_32x32x16_bf16 v[48:63], v[160:163], v[178:181], v[48:63]
	v_mfma_f32_32x32x16_bf16 v[32:47], v[122:125], v[164:167], v[32:47]
	ds_read_b64_tr_b16 v[164:165], v201 offset:0x400
	ds_read_b64_tr_b16 v[166:167], v201 offset:0xc00
	v_mfma_f32_32x32x16_bf16 v[32:47], v[152:155], v[170:173], v[32:47]
	ds_read_b64_tr_b16 v[170:171], v201 offset:0x1400
	ds_read_b64_tr_b16 v[172:173], v201 offset:0x1c00
	v_mfma_f32_32x32x16_bf16 v[32:47], v[156:159], v[174:177], v[32:47]
	ds_read_b64_tr_b16 v[174:175], v201 offset:0x2400
	ds_read_b64_tr_b16 v[176:177], v201 offset:0x2c00
	ds_read_b64_tr_b16 v[178:179], v201 offset:0x3400
	ds_read_b64_tr_b16 v[180:181], v201 offset:0x3c00
	s_waitcnt lgkmcnt(0)
	v_mfma_f32_32x32x16_bf16 v[32:47], v[160:163], v[186:189], v[32:47]
	v_mfma_f32_32x32x16_bf16 v[16:31], v[122:125], v[164:167], v[16:31]
	ds_read_b64_tr_b16 v[164:165], v201 offset:0x600
	ds_read_b64_tr_b16 v[166:167], v201 offset:0xe00
	v_mfma_f32_32x32x16_bf16 v[16:31], v[152:155], v[170:173], v[16:31]
	ds_read_b64_tr_b16 v[170:171], v201 offset:0x1600
	ds_read_b64_tr_b16 v[172:173], v201 offset:0x1e00
	v_mfma_f32_32x32x16_bf16 v[16:31], v[156:159], v[174:177], v[16:31]
	ds_read_b64_tr_b16 v[174:175], v201 offset:0x2600
	ds_read_b64_tr_b16 v[176:177], v201 offset:0x2e00
	ds_read_b64_tr_b16 v[186:187], v201 offset:0x3600
	ds_read_b64_tr_b16 v[188:189], v201 offset:0x3e00
	s_waitcnt lgkmcnt(0)
	v_mfma_f32_32x32x16_bf16 v[16:31], v[160:163], v[178:181], v[16:31]
	v_mfma_f32_32x32x16_bf16 v[0:15], v[122:125], v[164:167], v[0:15]
	s_andn2_b64 vcc, exec, s[0:1]
	v_mfma_f32_32x32x16_bf16 v[0:15], v[152:155], v[170:173], v[0:15]
	v_mfma_f32_32x32x16_bf16 v[0:15], v[156:159], v[174:177], v[0:15]
	v_mfma_f32_32x32x16_bf16 v[0:15], v[160:163], v[186:189], v[0:15]
	s_cbranch_vccnz .LBB0_2281
	v_max_f32_e32 v121, v65, v65
	v_max_f32_e32 v122, v64, v64
	v_max_f32_e32 v121, v122, v121
	v_max3_f32 v121, v121, v66, v67
	v_max3_f32 v121, v121, v68, v69
	v_max3_f32 v121, v121, v70, v71
	v_max3_f32 v121, v121, v72, v73
	v_max3_f32 v121, v121, v74, v75
	v_max3_f32 v121, v121, v76, v77
	v_max3_f32 v121, v121, v78, v79
	v_max3_f32 v121, v121, v80, v81
	v_max3_f32 v121, v121, v82, v83
	v_max3_f32 v121, v121, v84, v85
	v_max3_f32 v121, v121, v86, v87
	v_max3_f32 v121, v121, v88, v89
	v_max3_f32 v121, v121, v90, v91
	v_max3_f32 v121, v121, v92, v93
	v_max3_f32 v121, v121, v94, v95
	v_mov_b32_e32 v122, v121
	s_nop 1
	v_permlane32_swap_b32_e32 v121, v122
	v_max_f32_e32 v122, v122, v122
	v_max_f32_e32 v121, v121, v121
	v_max_f32_e32 v121, v121, v122
	v_sub_f32_e32 v122, v121, v168
	v_mul_f32_e32 v123, 0x3db504f3, v122
	v_max_f32_e32 v122, v168, v168
	v_max_f32_e32 v122, v122, v121
	v_sub_f32_e32 v121, v168, v122
	v_mul_f32_e32 v121, 0x3e0293ee, v121
	v_exp_f32_e32 v121, v121
	v_cmp_ge_f32_e32 vcc, s5, v123
	s_cmp_eq_u64 vcc, exec
	s_cselect_b64 s[0:1], -1, 0
	v_cndmask_b32_e64 v121, v121, 1.0, s[0:1]
	v_cmp_gt_f32_e32 vcc, 1.0, v121
	s_barrier
	s_cbranch_vccz .LBB0_2280
	v_cmp_gt_u32_e32 vcc, 32, v194
	s_and_saveexec_b64 s[2:3], vcc
	ds_write_b32 v200, v121 offset:128
	s_or_b64 exec, exec, s[2:3]
	s_waitcnt lgkmcnt(0)
	v_add_u32_e32 v123, s53, v198
	ds_read_b128 v[124:127], v123 offset:224
	ds_read_b128 v[152:155], v123 offset:192
	ds_read_b128 v[156:159], v123 offset:160
	ds_read_b128 v[160:163], v123 offset:128
	s_waitcnt lgkmcnt(3)
	v_mul_f32_e64 v60, v60, v124
	v_mul_f32_e64 v61, v61, v125
	s_waitcnt lgkmcnt(2)
	v_mul_f32_e64 v56, v56, v152
	v_mul_f32_e64 v57, v57, v153
	s_waitcnt lgkmcnt(1)
	v_mul_f32_e64 v52, v52, v156
	v_mul_f32_e64 v53, v53, v157
	v_mul_f32_e64 v62, v62, v126
	v_mul_f32_e64 v63, v63, v127
	v_mul_f32_e64 v58, v58, v154
	v_mul_f32_e64 v59, v59, v155
	v_mul_f32_e64 v54, v54, v158
	v_mul_f32_e64 v55, v55, v159
	s_waitcnt lgkmcnt(0)
	v_mul_f32_e64 v50, v50, v162
	v_mul_f32_e64 v51, v51, v163
	v_mul_f32_e64 v48, v48, v160
	v_mul_f32_e64 v49, v49, v161
	v_mul_f32_e64 v44, v44, v124
	v_mul_f32_e64 v45, v45, v125
	v_mul_f32_e64 v40, v40, v152
	v_mul_f32_e64 v41, v41, v153
	v_mul_f32_e64 v36, v36, v156
	v_mul_f32_e64 v37, v37, v157
	v_mul_f32_e64 v46, v46, v126
	v_mul_f32_e64 v47, v47, v127
	v_mul_f32_e64 v42, v42, v154
	v_mul_f32_e64 v43, v43, v155
	v_mul_f32_e64 v38, v38, v158
	v_mul_f32_e64 v39, v39, v159
	v_mul_f32_e64 v34, v34, v162
	v_mul_f32_e64 v35, v35, v163
	v_mul_f32_e64 v32, v32, v160
	v_mul_f32_e64 v33, v33, v161
	v_mul_f32_e64 v28, v28, v124
	v_mul_f32_e64 v29, v29, v125
	v_mul_f32_e64 v24, v24, v152
	v_mul_f32_e64 v25, v25, v153
	v_mul_f32_e64 v20, v20, v156
	v_mul_f32_e64 v21, v21, v157
	v_mul_f32_e64 v30, v30, v126
	v_mul_f32_e64 v31, v31, v127
	v_mul_f32_e64 v26, v26, v154
	v_mul_f32_e64 v27, v27, v155
	v_mul_f32_e64 v22, v22, v158
	v_mul_f32_e64 v23, v23, v159
	v_mul_f32_e64 v18, v18, v162
	v_mul_f32_e64 v19, v19, v163
	v_mul_f32_e64 v16, v16, v160
	v_mul_f32_e64 v17, v17, v161
	v_mul_f32_e64 v12, v12, v124
	v_mul_f32_e64 v13, v13, v125
	v_mul_f32_e64 v8, v8, v152
	v_mul_f32_e64 v9, v9, v153
	v_mul_f32_e64 v4, v4, v156
	v_mul_f32_e64 v5, v5, v157
	v_mul_f32_e64 v14, v14, v126
	v_mul_f32_e64 v15, v15, v127
	v_mul_f32_e64 v10, v10, v154
	v_mul_f32_e64 v11, v11, v155
	v_mul_f32_e64 v6, v6, v158
	v_mul_f32_e64 v7, v7, v159
	v_mul_f32_e64 v2, v2, v162
	v_mul_f32_e64 v3, v3, v163
	v_mul_f32_e64 v0, v0, v160
	v_mul_f32_e64 v1, v1, v161

.LBB0_2485:
	ds_read_b128 v[128:131], v179
	ds_read_b128 v[132:135], v179 offset:1024
	ds_read_b128 v[136:139], v179 offset:2048
	ds_read_b128 v[140:143], v179 offset:3072
	s_add_u32 s30, s28, 0xfffe0080
	s_addc_u32 s31, s29, -1
	s_cmp_eq_u32 s63, 4
	s_cselect_b32 s35, s13, s31
	s_cselect_b32 s34, s12, s30
	s_cselect_b32 s31, s15, s62
	s_cselect_b32 s30, s14, s11
	v_lshl_add_u64 v[176:177], s[28:29], 0, v[168:169]
	s_add_i32 m0, s17, 0xc000
	ds_read_b128 v[144:147], v180
	ds_read_b128 v[148:151], v180 offset:1024
	ds_read_b128 v[152:155], v180 offset:2048
	ds_read_b128 v[156:159], v180 offset:3072
	ds_read_b128 v[172:175], v180 offset:4096
	ds_read_b128 v[182:185], v180 offset:5120
	ds_read_b128 v[186:189], v180 offset:6144
	ds_read_b128 v[190:193], v180 offset:7168
	global_load_lds_dwordx4 v[176:177], off
	v_lshl_add_u64 v[176:177], s[28:29], 0, v[170:171]
	s_add_i32 m0, s17, 0xe000
	s_nop 0
	global_load_lds_dwordx4 v[176:177], off
	s_waitcnt lgkmcnt(8)
	s_barrier
	s_waitcnt lgkmcnt(0)
	s_setprio 1
	s_waitcnt lgkmcnt(0)
	v_mfma_f32_16x16x32_bf16 v[124:127], v[128:131], v[144:147], v[124:127]
	v_mfma_f32_16x16x32_bf16 v[120:123], v[136:139], v[144:147], v[120:123]
	v_mfma_f32_16x16x32_bf16 v[112:115], v[128:131], v[152:155], v[112:115]
	v_mfma_f32_16x16x32_bf16 v[104:107], v[136:139], v[152:155], v[104:107]
	v_mfma_f32_16x16x32_bf16 v[96:99], v[128:131], v[172:175], v[96:99]
	v_mfma_f32_16x16x32_bf16 v[88:91], v[136:139], v[172:175], v[88:91]
	v_mfma_f32_16x16x32_bf16 v[80:83], v[128:131], v[186:189], v[80:83]
	v_mfma_f32_16x16x32_bf16 v[72:75], v[136:139], v[186:189], v[72:75]
	v_mfma_f32_16x16x32_bf16 v[124:127], v[132:135], v[148:151], v[124:127]
	v_mfma_f32_16x16x32_bf16 v[120:123], v[140:143], v[148:151], v[120:123]
	v_mfma_f32_16x16x32_bf16 v[112:115], v[132:135], v[156:159], v[112:115]
	v_mfma_f32_16x16x32_bf16 v[104:107], v[140:143], v[156:159], v[104:107]
	v_mfma_f32_16x16x32_bf16 v[96:99], v[132:135], v[182:185], v[96:99]
	v_mfma_f32_16x16x32_bf16 v[88:91], v[140:143], v[182:185], v[88:91]
	v_mfma_f32_16x16x32_bf16 v[80:83], v[132:135], v[190:193], v[80:83]
	v_mfma_f32_16x16x32_bf16 v[72:75], v[140:143], v[190:193], v[72:75]
	s_setprio 0
	s_barrier
	s_add_i32 s64, s49, s39
	v_lshl_add_u64 v[176:177], s[30:31], 0, v[162:163]
	s_mov_b32 m0, s64
	ds_read_b128 v[194:197], v181
	ds_read_b128 v[198:201], v181 offset:1024
	ds_read_b128 v[202:205], v181 offset:2048
	ds_read_b128 v[206:209], v181 offset:3072
	global_load_lds_dwordx4 v[176:177], off
	v_lshl_add_u64 v[210:211], s[30:31], 0, v[166:167]
	s_add_i32 m0, s64, 0x2000
	s_nop 0
	global_load_lds_dwordx4 v[210:211], off
	s_barrier
	s_waitcnt lgkmcnt(0)
	s_setprio 1
	s_waitcnt lgkmcnt(0)
	v_mfma_f32_16x16x32_bf16 v[116:119], v[194:197], v[144:147], v[116:119]
	v_mfma_f32_16x16x32_bf16 v[108:111], v[202:205], v[144:147], v[108:111]
	v_mfma_f32_16x16x32_bf16 v[100:103], v[194:197], v[152:155], v[100:103]
	v_mfma_f32_16x16x32_bf16 v[92:95], v[202:205], v[152:155], v[92:95]
	v_mfma_f32_16x16x32_bf16 v[84:87], v[194:197], v[172:175], v[84:87]
	v_mfma_f32_16x16x32_bf16 v[76:79], v[202:205], v[172:175], v[76:79]
	v_mfma_f32_16x16x32_bf16 v[68:71], v[194:197], v[186:189], v[68:71]
	v_mfma_f32_16x16x32_bf16 v[64:67], v[202:205], v[186:189], v[64:67]
	v_mfma_f32_16x16x32_bf16 v[116:119], v[198:201], v[148:151], v[116:119]
	v_mfma_f32_16x16x32_bf16 v[108:111], v[206:209], v[148:151], v[108:111]
	v_mfma_f32_16x16x32_bf16 v[100:103], v[198:201], v[156:159], v[100:103]
	v_mfma_f32_16x16x32_bf16 v[92:95], v[206:209], v[156:159], v[92:95]
	v_mfma_f32_16x16x32_bf16 v[84:87], v[198:201], v[182:185], v[84:87]
	v_mfma_f32_16x16x32_bf16 v[76:79], v[206:209], v[182:185], v[76:79]
	v_mfma_f32_16x16x32_bf16 v[68:71], v[198:201], v[190:193], v[68:71]
	v_mfma_f32_16x16x32_bf16 v[64:67], v[206:209], v[190:193], v[64:67]
	s_setprio 0
	s_mov_b32 m0, s17
	v_lshl_add_u64 v[212:213], s[34:35], 0, v[160:161]
	s_barrier
	ds_read_b128 v[144:147], v180 offset:16384
	ds_read_b128 v[148:151], v180 offset:17408
	ds_read_b128 v[152:155], v180 offset:18432
	ds_read_b128 v[156:159], v180 offset:19456
	ds_read_b128 v[172:175], v180 offset:20480
	ds_read_b128 v[182:185], v180 offset:21504
	ds_read_b128 v[186:189], v180 offset:22528
	ds_read_b128 v[190:193], v180 offset:23552
	global_load_lds_dwordx4 v[212:213], off
	v_lshl_add_u64 v[214:215], s[34:35], 0, v[164:165]
	s_mov_b32 m0, s40
	s_nop 0
	global_load_lds_dwordx4 v[214:215], off
	s_barrier
	s_waitcnt lgkmcnt(0)
	s_setprio 1
	s_waitcnt lgkmcnt(0)
	v_mfma_f32_16x16x32_bf16 v[60:63], v[128:131], v[144:147], v[60:63]
	v_mfma_f32_16x16x32_bf16 v[56:59], v[136:139], v[144:147], v[56:59]
	v_mfma_f32_16x16x32_bf16 v[48:51], v[128:131], v[152:155], v[48:51]
	v_mfma_f32_16x16x32_bf16 v[40:43], v[136:139], v[152:155], v[40:43]
	v_mfma_f32_16x16x32_bf16 v[32:35], v[128:131], v[172:175], v[32:35]
	v_mfma_f32_16x16x32_bf16 v[24:27], v[136:139], v[172:175], v[24:27]
	v_mfma_f32_16x16x32_bf16 v[16:19], v[128:131], v[186:189], v[16:19]
	v_mfma_f32_16x16x32_bf16 v[8:11], v[136:139], v[186:189], v[8:11]
	v_mfma_f32_16x16x32_bf16 v[60:63], v[132:135], v[148:151], v[60:63]
	v_mfma_f32_16x16x32_bf16 v[56:59], v[140:143], v[148:151], v[56:59]
	v_mfma_f32_16x16x32_bf16 v[48:51], v[132:135], v[156:159], v[48:51]
	v_mfma_f32_16x16x32_bf16 v[40:43], v[140:143], v[156:159], v[40:43]
	v_mfma_f32_16x16x32_bf16 v[32:35], v[132:135], v[182:185], v[32:35]
	v_mfma_f32_16x16x32_bf16 v[24:27], v[140:143], v[182:185], v[24:27]
	v_mfma_f32_16x16x32_bf16 v[16:19], v[132:135], v[190:193], v[16:19]
	v_mfma_f32_16x16x32_bf16 v[8:11], v[140:143], v[190:193], v[8:11]
	s_setprio 0
	s_barrier
	s_add_u32 s64, s30, 0x20000
	s_addc_u32 s65, s31, 0
	s_add_i32 s66, s52, s39
	v_lshl_add_u64 v[128:129], s[64:65], 0, v[162:163]
	s_mov_b32 m0, s66
	s_nop 0
	global_load_lds_dwordx4 v[128:129], off
	v_lshl_add_u64 v[128:129], s[64:65], 0, v[166:167]
	s_add_i32 m0, s66, 0x2000
	s_nop 0
	global_load_lds_dwordx4 v[128:129], off
	s_waitcnt vmcnt(6)
	s_barrier
	s_setprio 1
	v_mfma_f32_16x16x32_bf16 v[52:55], v[194:197], v[144:147], v[52:55]
	v_mfma_f32_16x16x32_bf16 v[44:47], v[202:205], v[144:147], v[44:47]
	v_mfma_f32_16x16x32_bf16 v[36:39], v[194:197], v[152:155], v[36:39]
	v_mfma_f32_16x16x32_bf16 v[28:31], v[202:205], v[152:155], v[28:31]
	v_mfma_f32_16x16x32_bf16 v[20:23], v[194:197], v[172:175], v[20:23]
	v_mfma_f32_16x16x32_bf16 v[12:15], v[202:205], v[172:175], v[12:15]
	v_mfma_f32_16x16x32_bf16 v[4:7], v[194:197], v[186:189], v[4:7]
	v_mfma_f32_16x16x32_bf16 v[0:3], v[202:205], v[186:189], v[0:3]
	v_mfma_f32_16x16x32_bf16 v[52:55], v[198:201], v[148:151], v[52:55]
	v_mfma_f32_16x16x32_bf16 v[44:47], v[206:209], v[148:151], v[44:47]
	v_mfma_f32_16x16x32_bf16 v[36:39], v[198:201], v[156:159], v[36:39]
	v_mfma_f32_16x16x32_bf16 v[28:31], v[206:209], v[156:159], v[28:31]
	v_mfma_f32_16x16x32_bf16 v[20:23], v[198:201], v[182:185], v[20:23]
	v_mfma_f32_16x16x32_bf16 v[12:15], v[206:209], v[182:185], v[12:15]
	v_mfma_f32_16x16x32_bf16 v[4:7], v[198:201], v[190:193], v[4:7]
	v_mfma_f32_16x16x32_bf16 v[0:3], v[206:209], v[190:193], v[0:3]
	s_setprio 0
	s_add_i32 s64, 0, 0x18000
	v_add_u32_e32 v140, s64, v178
	s_barrier
	ds_read_b128 v[128:131], v140
	ds_read_b128 v[132:135], v140 offset:1024
	ds_read_b128 v[136:139], v140 offset:2048
	ds_read_b128 v[140:143], v140 offset:3072
	s_add_u32 s34, s34, 0x20000
	s_addc_u32 s35, s35, 0
	s_mov_b32 m0, s41
	v_lshl_add_u64 v[194:195], s[34:35], 0, v[160:161]
	ds_read_b128 v[144:147], v180 offset:32768
	ds_read_b128 v[148:151], v180 offset:33792
	ds_read_b128 v[152:155], v180 offset:34816
	ds_read_b128 v[156:159], v180 offset:35840
	ds_read_b128 v[172:175], v180 offset:36864
	ds_read_b128 v[182:185], v180 offset:37888
	ds_read_b128 v[186:189], v180 offset:38912
	ds_read_b128 v[190:193], v180 offset:39936
	global_load_lds_dwordx4 v[194:195], off
	v_lshl_add_u64 v[194:195], s[34:35], 0, v[164:165]
	s_mov_b32 m0, s42
	s_nop 0
	global_load_lds_dwordx4 v[194:195], off
	s_waitcnt lgkmcnt(8)
	s_barrier
	s_waitcnt lgkmcnt(0)
	s_setprio 1
	s_waitcnt lgkmcnt(0)
	v_mfma_f32_16x16x32_bf16 v[124:127], v[128:131], v[144:147], v[124:127]
	v_mfma_f32_16x16x32_bf16 v[120:123], v[136:139], v[144:147], v[120:123]
	v_mfma_f32_16x16x32_bf16 v[112:115], v[128:131], v[152:155], v[112:115]
	v_mfma_f32_16x16x32_bf16 v[104:107], v[136:139], v[152:155], v[104:107]
	v_mfma_f32_16x16x32_bf16 v[96:99], v[128:131], v[172:175], v[96:99]
	v_mfma_f32_16x16x32_bf16 v[88:91], v[136:139], v[172:175], v[88:91]
	v_mfma_f32_16x16x32_bf16 v[80:83], v[128:131], v[186:189], v[80:83]
	v_mfma_f32_16x16x32_bf16 v[72:75], v[136:139], v[186:189], v[72:75]
	v_mfma_f32_16x16x32_bf16 v[124:127], v[132:135], v[148:151], v[124:127]
	v_mfma_f32_16x16x32_bf16 v[120:123], v[140:143], v[148:151], v[120:123]
	v_mfma_f32_16x16x32_bf16 v[112:115], v[132:135], v[156:159], v[112:115]
	v_mfma_f32_16x16x32_bf16 v[104:107], v[140:143], v[156:159], v[104:107]
	v_mfma_f32_16x16x32_bf16 v[96:99], v[132:135], v[182:185], v[96:99]
	v_mfma_f32_16x16x32_bf16 v[88:91], v[140:143], v[182:185], v[88:91]
	v_mfma_f32_16x16x32_bf16 v[80:83], v[132:135], v[190:193], v[80:83]
	v_mfma_f32_16x16x32_bf16 v[72:75], v[140:143], v[190:193], v[72:75]
	s_setprio 0
	s_barrier
	s_add_i32 s34, 0, 0x1c000
	s_add_i32 s35, s64, s39
	v_add_u32_e32 v206, s34, v178
	v_lshl_add_u64 v[176:177], v[176:177], 0, s[6:7]
	s_mov_b32 m0, s35
	ds_read_b128 v[194:197], v206
	ds_read_b128 v[198:201], v206 offset:1024
	ds_read_b128 v[202:205], v206 offset:2048
	ds_read_b128 v[206:209], v206 offset:3072
	global_load_lds_dwordx4 v[176:177], off
	v_lshl_add_u64 v[176:177], v[210:211], 0, s[6:7]
	s_add_i32 m0, s35, 0x2000
	s_nop 0
	global_load_lds_dwordx4 v[176:177], off
	s_barrier
	s_waitcnt lgkmcnt(0)
	s_setprio 1
	s_waitcnt lgkmcnt(0)
	v_mfma_f32_16x16x32_bf16 v[116:119], v[194:197], v[144:147], v[116:119]
	v_mfma_f32_16x16x32_bf16 v[108:111], v[202:205], v[144:147], v[108:111]
	v_mfma_f32_16x16x32_bf16 v[100:103], v[194:197], v[152:155], v[100:103]
	v_mfma_f32_16x16x32_bf16 v[92:95], v[202:205], v[152:155], v[92:95]
	v_mfma_f32_16x16x32_bf16 v[84:87], v[194:197], v[172:175], v[84:87]
	v_mfma_f32_16x16x32_bf16 v[76:79], v[202:205], v[172:175], v[76:79]
	v_mfma_f32_16x16x32_bf16 v[68:71], v[194:197], v[186:189], v[68:71]
	v_mfma_f32_16x16x32_bf16 v[64:67], v[202:205], v[186:189], v[64:67]
	v_mfma_f32_16x16x32_bf16 v[116:119], v[198:201], v[148:151], v[116:119]
	v_mfma_f32_16x16x32_bf16 v[108:111], v[206:209], v[148:151], v[108:111]
	v_mfma_f32_16x16x32_bf16 v[100:103], v[198:201], v[156:159], v[100:103]
	v_mfma_f32_16x16x32_bf16 v[92:95], v[206:209], v[156:159], v[92:95]
	v_mfma_f32_16x16x32_bf16 v[84:87], v[198:201], v[182:185], v[84:87]
	v_mfma_f32_16x16x32_bf16 v[76:79], v[206:209], v[182:185], v[76:79]
	v_mfma_f32_16x16x32_bf16 v[68:71], v[198:201], v[190:193], v[68:71]
	v_mfma_f32_16x16x32_bf16 v[64:67], v[206:209], v[190:193], v[64:67]
	s_setprio 0
	s_mov_b32 m0, s45
	v_lshl_add_u64 v[176:177], v[212:213], 0, s[6:7]
	s_barrier
	ds_read_b128 v[144:147], v180 offset:49152
	ds_read_b128 v[148:151], v180 offset:50176
	ds_read_b128 v[152:155], v180 offset:51200
	ds_read_b128 v[156:159], v180 offset:52224
	ds_read_b128 v[172:175], v180 offset:53248
	ds_read_b128 v[182:185], v180 offset:54272
	ds_read_b128 v[186:189], v180 offset:55296
	ds_read_b128 v[190:193], v180 offset:56320
	global_load_lds_dwordx4 v[176:177], off
	v_lshl_add_u64 v[176:177], v[214:215], 0, s[6:7]
	s_mov_b32 m0, s48
	s_nop 0
	global_load_lds_dwordx4 v[176:177], off
	s_barrier
;     __device__ __forceinline__ void operator()(const f32x4 (&acc)[2][2][4][2], const Unit& u, int wr, int wc, int fr, int fq, const Pre&) const {
;         const size_t off0 = (size_t)(u.pm * 256 + wr * 64 + fr) * DM + u.pn * 256 + 32 * wc + 8 * fq;
;         u32x4 rb[2][4][2];
;         if (!RF32) {
; #pragma unroll
;             for (int ai = 0; ai < 2; ++ai)
; #pragma unroll
;                 for (int m = 0; m < 4; ++m)
; #pragma unroll
;                     for (int bj = 0; bj < 2; ++bj) rb[ai][m][bj] = *(const u32x4*)((const bf16_t*)resid + off0 + (size_t)(ai * 128 + m * 16) * DM + 128 * bj);
;         }
	s_waitcnt lgkmcnt(0)
	s_setprio 1
	s_waitcnt lgkmcnt(0)
	v_mfma_f32_16x16x32_bf16 v[60:63], v[128:131], v[144:147], v[60:63]
	v_mfma_f32_16x16x32_bf16 v[56:59], v[136:139], v[144:147], v[56:59]
	v_mfma_f32_16x16x32_bf16 v[48:51], v[128:131], v[152:155], v[48:51]
	v_mfma_f32_16x16x32_bf16 v[40:43], v[136:139], v[152:155], v[40:43]
	v_mfma_f32_16x16x32_bf16 v[32:35], v[128:131], v[172:175], v[32:35]
	v_mfma_f32_16x16x32_bf16 v[24:27], v[136:139], v[172:175], v[24:27]
	v_mfma_f32_16x16x32_bf16 v[16:19], v[128:131], v[186:189], v[16:19]
	v_mfma_f32_16x16x32_bf16 v[8:11], v[136:139], v[186:189], v[8:11]
	v_mfma_f32_16x16x32_bf16 v[60:63], v[132:135], v[148:151], v[60:63]
	v_mfma_f32_16x16x32_bf16 v[56:59], v[140:143], v[148:151], v[56:59]
	v_mfma_f32_16x16x32_bf16 v[48:51], v[132:135], v[156:159], v[48:51]
	v_mfma_f32_16x16x32_bf16 v[40:43], v[140:143], v[156:159], v[40:43]
	v_mfma_f32_16x16x32_bf16 v[32:35], v[132:135], v[182:185], v[32:35]
	v_mfma_f32_16x16x32_bf16 v[24:27], v[140:143], v[182:185], v[24:27]
	v_mfma_f32_16x16x32_bf16 v[16:19], v[132:135], v[190:193], v[16:19]
	v_mfma_f32_16x16x32_bf16 v[8:11], v[140:143], v[190:193], v[8:11]
	s_setprio 0
	s_barrier
	s_add_u32 s30, s30, 0x20080
	s_addc_u32 s31, s31, 0
	s_add_i32 s34, s34, s39
	v_lshl_add_u64 v[128:129], s[30:31], 0, v[162:163]
	s_mov_b32 m0, s34
	s_nop 0
	global_load_lds_dwordx4 v[128:129], off
	v_lshl_add_u64 v[128:129], s[30:31], 0, v[166:167]
	s_add_i32 m0, s34, 0x2000
	s_nop 0
	global_load_lds_dwordx4 v[128:129], off
	s_waitcnt vmcnt(6)
	s_barrier
	s_setprio 1
	v_mfma_f32_16x16x32_bf16 v[52:55], v[194:197], v[144:147], v[52:55]
	v_mfma_f32_16x16x32_bf16 v[44:47], v[202:205], v[144:147], v[44:47]
	v_mfma_f32_16x16x32_bf16 v[36:39], v[194:197], v[152:155], v[36:39]
	v_mfma_f32_16x16x32_bf16 v[28:31], v[202:205], v[152:155], v[28:31]
	v_mfma_f32_16x16x32_bf16 v[20:23], v[194:197], v[172:175], v[20:23]
	v_mfma_f32_16x16x32_bf16 v[12:15], v[202:205], v[172:175], v[12:15]
	v_mfma_f32_16x16x32_bf16 v[4:7], v[194:197], v[186:189], v[4:7]
	v_mfma_f32_16x16x32_bf16 v[0:3], v[202:205], v[186:189], v[0:3]
	v_mfma_f32_16x16x32_bf16 v[52:55], v[198:201], v[148:151], v[52:55]
	v_mfma_f32_16x16x32_bf16 v[44:47], v[206:209], v[148:151], v[44:47]
	v_mfma_f32_16x16x32_bf16 v[36:39], v[198:201], v[156:159], v[36:39]
	v_mfma_f32_16x16x32_bf16 v[28:31], v[206:209], v[156:159], v[28:31]
	v_mfma_f32_16x16x32_bf16 v[20:23], v[198:201], v[182:185], v[20:23]
	v_mfma_f32_16x16x32_bf16 v[12:15], v[206:209], v[182:185], v[12:15]
	v_mfma_f32_16x16x32_bf16 v[4:7], v[198:201], v[190:193], v[4:7]
	v_mfma_f32_16x16x32_bf16 v[0:3], v[206:209], v[190:193], v[0:3]
	s_setprio 0
	s_add_i32 s63, s63, 2
	s_add_u32 s28, s28, 0x100
	s_addc_u32 s29, s29, 0
	s_add_u32 s11, s11, 0x100
	s_addc_u32 s62, s62, 0
	s_cmp_gt_u32 s63, 5
	s_barrier
	s_cbranch_scc0 .LBB0_2485
	s_lshl_b32 s11, s16, 8
	v_mbcnt_lo_u32_b32 v130, -1, 0
	v_mbcnt_hi_u32_b32 v130, -1, v130
	s_add_i32 s11, s11, s44
	v_and_or_b32 v128, v130, 15, s11
	s_lshl_b32 s28, s61, 8
	v_ashrrev_i32_e32 v130, 1, v130
	s_ashr_i32 s29, s28, 31
	v_and_b32_e32 v130, -8, v130
	v_ashrrev_i32_e32 v129, 31, v128
	v_ashrrev_i32_e32 v131, 31, v130
	s_or_b64 s[28:29], s[28:29], s[0:1]
	v_lshlrev_b64 v[128:129], 11, v[128:129]
	v_lshl_add_u64 v[130:131], s[28:29], 0, v[130:131]
	v_lshl_add_u64 v[128:129], v[130:131], 0, v[128:129]
	v_lshlrev_b64 v[210:211], 1, v[128:129]
	v_lshl_add_u64 v[128:129], s[2:3], 0, v[210:211]
	v_add_co_u32_e32 v130, vcc, s43, v128
	global_load_dwordx4 v[172:175], v[128:129], off
	global_load_dwordx4 v[182:185], v[128:129], off offset:256
	v_addc_co_u32_e32 v131, vcc, 0, v129, vcc
	global_load_dwordx4 v[186:189], v[130:131], off
	global_load_dwordx4 v[190:193], v[130:131], off offset:256
	v_add_co_u32_e32 v130, vcc, s53, v128
	s_mov_b32 s16, s10
	s_nop 0
	v_addc_co_u32_e32 v131, vcc, 0, v129, vcc
	global_load_dwordx4 v[194:197], v[130:131], off
	global_load_dwordx4 v[198:201], v[130:131], off offset:256
	v_add_co_u32_e32 v130, vcc, s54, v128
	s_mov_b32 s61, s60
	s_nop 0
	v_addc_co_u32_e32 v131, vcc, 0, v129, vcc
	global_load_dwordx4 v[202:205], v[130:131], off
	global_load_dwordx4 v[206:209], v[130:131], off offset:256
	v_add_co_u32_e32 v130, vcc, s55, v128
	s_mov_b64 s[30:31], s[14:15]
	s_nop 0
	v_addc_co_u32_e32 v131, vcc, 0, v129, vcc
	v_add_co_u32_e32 v132, vcc, s56, v128
	s_mov_b64 s[28:29], s[12:13]
	s_nop 0
	v_addc_co_u32_e32 v133, vcc, 0, v129, vcc
	v_add_co_u32_e32 v134, vcc, s57, v128
	s_waitcnt vmcnt(0)
; __device__ __forceinline__ float bf_lo(unsigned w) { return __uint_as_float(w << 16); }
; __device__ __forceinline__ float bf_hi(unsigned w) { return __uint_as_float(w & 0xffff0000u); }
;     __device__ __forceinline__ void operator()(const f32x4 (&acc)[2][2][4][2], const Unit& u, int wr, int wc, int fr, int fq, const Pre&) const {
;     ...
;         for (int ai = 0; ai < 2; ++ai) {
;             f32x4 r0[4][2], r1[4][2];
; #pragma unroll
;             for (int m = 0; m < 4; ++m)
; #pragma unroll
;                 for (int bj = 0; bj < 2; ++bj) {
;                     const size_t off = off0 + (size_t)(ai * 128 + m * 16) * DM + 128 * bj;
;                     if (RF32) { r0[m][bj] = *(const f32x4*)((const float*)resid + off); r1[m][bj] = *(const f32x4*)((const float*)resid + off + 4); }
;                     else { const u32x4 rbv = rb[ai][m][bj];
;                         r0[m][bj] = (f32x4){bf_lo(rbv.x), bf_hi(rbv.x), bf_lo(rbv.y), bf_hi(rbv.y)}; r1[m][bj] = (f32x4){bf_lo(rbv.z), bf_hi(rbv.z), bf_lo(rbv.w), bf_hi(rbv.w)}; }
;                 }
; #pragma unroll
;             for (int m = 0; m < 4; ++m) {
;                 const int row = u.pm * 256 + ai * 128 + wr * 64 + m * 16 + fr; float sq = 0.f;
; #pragma unroll
;                 for (int bj = 0; bj < 2; ++bj) {
;                     const size_t off = off0 + (size_t)(ai * 128 + m * 16) * DM + 128 * bj;
;                     const f32x4 v0 = acc[ai][bj][m][0] + r0[m][bj], v1 = acc[ai][bj][m][1] + r1[m][bj];
;                     st_bf16x8(hb + off, v0, v1);
;                     sq += v0[0] * v0[0] + v0[1] * v0[1] + v0[2] * v0[2] + v0[3] * v0[3] + v1[0] * v1[0] + v1[1] * v1[1] + v1[2] * v1[2] + v1[3] * v1[3];
;                 }
	v_lshlrev_b32_e32 v212, 16, v172
	v_addc_co_u32_e32 v135, vcc, 0, v129, vcc
	v_add_co_u32_e32 v128, vcc, s58, v128
	v_and_b32_e32 v213, 0xffff0000, v172
	s_nop 0
	v_addc_co_u32_e32 v129, vcc, 0, v129, vcc
	global_load_dwordx4 v[156:159], v[130:131], off
	global_load_dwordx4 v[152:155], v[130:131], off offset:256
	global_load_dwordx4 v[148:151], v[132:133], off
	global_load_dwordx4 v[144:147], v[132:133], off offset:256
	global_load_dwordx4 v[140:143], v[134:135], off
	global_load_dwordx4 v[136:139], v[134:135], off offset:256
	s_nop 0
	global_load_dwordx4 v[132:135], v[128:129], off
	s_nop 0
	global_load_dwordx4 v[128:131], v[128:129], off offset:256
	v_lshlrev_b32_e32 v214, 16, v173
	v_and_b32_e32 v215, 0xffff0000, v173
	v_lshlrev_b32_e32 v216, 16, v174
	v_and_b32_e32 v217, 0xffff0000, v174
	v_lshlrev_b32_e32 v218, 16, v175
	v_and_b32_e32 v219, 0xffff0000, v175
	v_lshlrev_b32_e32 v220, 16, v182
	v_and_b32_e32 v221, 0xffff0000, v182
	v_lshlrev_b32_e32 v182, 16, v183
	v_and_b32_e32 v183, 0xffff0000, v183
	v_lshlrev_b32_e32 v222, 16, v184
	v_and_b32_e32 v223, 0xffff0000, v184
	v_lshlrev_b32_e32 v184, 16, v185
	v_and_b32_e32 v185, 0xffff0000, v185
	v_lshlrev_b32_e32 v172, 16, v208
	v_and_b32_e32 v173, 0xffff0000, v208
	v_lshlrev_b32_e32 v176, 16, v209
	v_and_b32_e32 v177, 0xffff0000, v209
	v_add_f32_e64 v126, v126, v214
	v_add_f32_e64 v127, v127, v215
	v_add_f32_e64 v124, v124, v212
	v_add_f32_e64 v125, v125, v213
	v_add_f32_e64 v208, v122, v218
	v_add_f32_e64 v209, v123, v219
	v_add_f32_e64 v212, v120, v216
	v_add_f32_e64 v213, v121, v217
	v_lshl_add_u64 v[120:121], s[4:5], 0, v[210:211]
	v_cvt_pk_bf16_f32 v122, v124, v125
	v_cvt_pk_bf16_f32 v123, v126, v127
	v_lshlrev_b32_e32 v224, 16, v186
	v_and_b32_e32 v225, 0xffff0000, v186
	v_lshlrev_b32_e32 v186, 16, v187
	v_and_b32_e32 v187, 0xffff0000, v187
	v_cvt_pk_bf16_f32 v124, v212, v213
	v_cvt_pk_bf16_f32 v125, v208, v209
	global_store_dwordx4 v[120:121], v[122:125], off
	v_add_f32_e64 v118, v118, v182
	v_add_f32_e64 v119, v119, v183
	v_add_f32_e64 v116, v116, v220
	v_add_f32_e64 v117, v117, v221
	v_add_f32_e64 v122, v110, v184
	v_add_f32_e64 v123, v111, v185
	v_add_f32_e64 v110, v108, v222
	v_add_f32_e64 v111, v109, v223
	v_cvt_pk_bf16_f32 v108, v116, v117
	v_cvt_pk_bf16_f32 v109, v118, v119
	v_lshlrev_b32_e32 v226, 16, v188
	v_and_b32_e32 v227, 0xffff0000, v188
	v_lshlrev_b32_e32 v188, 16, v189
	v_and_b32_e32 v189, 0xffff0000, v189
	v_cvt_pk_bf16_f32 v110, v110, v111
	v_cvt_pk_bf16_f32 v111, v122, v123
	global_store_dwordx4 v[120:121], v[108:111], off offset:256
	v_lshlrev_b32_e32 v228, 16, v190
	v_and_b32_e32 v229, 0xffff0000, v190
	v_add_f32_e64 v108, v114, v186
	v_add_f32_e64 v109, v115, v187
	v_add_f32_e64 v110, v112, v224
	v_add_f32_e64 v111, v113, v225
	v_add_f32_e64 v112, v106, v188
	v_add_f32_e64 v113, v107, v189
	v_add_f32_e64 v106, v104, v226
	v_add_f32_e64 v107, v105, v227
	v_cvt_pk_bf16_f32 v104, v110, v111
	v_cvt_pk_bf16_f32 v105, v108, v109
	v_add_co_u32_e32 v108, vcc, s43, v120
	v_lshlrev_b32_e32 v190, 16, v191
	v_and_b32_e32 v191, 0xffff0000, v191
	v_lshlrev_b32_e32 v230, 16, v192
	v_and_b32_e32 v231, 0xffff0000, v192
	v_lshlrev_b32_e32 v192, 16, v193
	v_and_b32_e32 v193, 0xffff0000, v193
	v_addc_co_u32_e32 v109, vcc, 0, v121, vcc
	v_lshlrev_b32_e32 v232, 16, v194
	v_and_b32_e32 v233, 0xffff0000, v194
	v_lshlrev_b32_e32 v194, 16, v195
	v_and_b32_e32 v195, 0xffff0000, v195
	v_cvt_pk_bf16_f32 v106, v106, v107
	v_cvt_pk_bf16_f32 v107, v112, v113
	global_store_dwordx4 v[108:109], v[104:107], off
	v_add_f32_e64 v102, v102, v190
	v_add_f32_e64 v103, v103, v191
	v_add_f32_e64 v100, v100, v228
	v_add_f32_e64 v101, v101, v229
	v_add_f32_e64 v104, v94, v192
	v_add_f32_e64 v105, v95, v193
	v_add_f32_e64 v94, v92, v230
	v_add_f32_e64 v95, v93, v231
	v_cvt_pk_bf16_f32 v92, v100, v101
	v_cvt_pk_bf16_f32 v93, v102, v103
	v_lshlrev_b32_e32 v234, 16, v196
	v_and_b32_e32 v235, 0xffff0000, v196
	v_lshlrev_b32_e32 v196, 16, v197
	v_and_b32_e32 v197, 0xffff0000, v197
	v_cvt_pk_bf16_f32 v94, v94, v95
	v_cvt_pk_bf16_f32 v95, v104, v105
	global_store_dwordx4 v[108:109], v[92:95], off offset:256
	v_lshlrev_b32_e32 v236, 16, v198
	v_and_b32_e32 v237, 0xffff0000, v198
	v_add_f32_e64 v92, v98, v194
	v_add_f32_e64 v93, v99, v195
	v_add_f32_e64 v94, v96, v232
	v_add_f32_e64 v95, v97, v233
	v_add_f32_e64 v96, v90, v196
	v_add_f32_e64 v97, v91, v197
	v_add_f32_e64 v90, v88, v234
	v_add_f32_e64 v91, v89, v235
	v_cvt_pk_bf16_f32 v88, v94, v95
	v_cvt_pk_bf16_f32 v89, v92, v93
	v_add_co_u32_e32 v92, vcc, s53, v120
	v_lshlrev_b32_e32 v198, 16, v199
	v_and_b32_e32 v199, 0xffff0000, v199
	v_lshlrev_b32_e32 v238, 16, v200
	v_and_b32_e32 v239, 0xffff0000, v200
	v_lshlrev_b32_e32 v200, 16, v201
	v_and_b32_e32 v201, 0xffff0000, v201
	v_addc_co_u32_e32 v93, vcc, 0, v121, vcc
	v_lshlrev_b32_e32 v240, 16, v202
	v_and_b32_e32 v241, 0xffff0000, v202
	v_lshlrev_b32_e32 v202, 16, v203
	v_and_b32_e32 v203, 0xffff0000, v203
	v_cvt_pk_bf16_f32 v90, v90, v91
	v_cvt_pk_bf16_f32 v91, v96, v97
	global_store_dwordx4 v[92:93], v[88:91], off
	v_add_f32_e64 v86, v86, v198
	v_add_f32_e64 v87, v87, v199
	v_add_f32_e64 v84, v84, v236
	v_add_f32_e64 v85, v85, v237
	v_add_f32_e64 v88, v78, v200
	v_add_f32_e64 v89, v79, v201
	v_add_f32_e64 v78, v76, v238
	v_add_f32_e64 v79, v77, v239
	v_cvt_pk_bf16_f32 v76, v84, v85
	v_cvt_pk_bf16_f32 v77, v86, v87
	v_lshlrev_b32_e32 v242, 16, v204
	v_and_b32_e32 v243, 0xffff0000, v204
	v_lshlrev_b32_e32 v204, 16, v205
	v_and_b32_e32 v205, 0xffff0000, v205
	v_cvt_pk_bf16_f32 v78, v78, v79
	v_cvt_pk_bf16_f32 v79, v88, v89
	global_store_dwordx4 v[92:93], v[76:79], off offset:256
	v_lshlrev_b32_e32 v174, 16, v206
	v_and_b32_e32 v175, 0xffff0000, v206
	v_add_f32_e64 v76, v82, v202
	v_add_f32_e64 v77, v83, v203
	v_add_f32_e64 v78, v80, v240
	v_add_f32_e64 v79, v81, v241
	v_add_f32_e64 v80, v74, v204
	v_add_f32_e64 v81, v75, v205
	v_add_f32_e64 v74, v72, v242
	v_add_f32_e64 v75, v73, v243
	v_cvt_pk_bf16_f32 v72, v78, v79
	v_cvt_pk_bf16_f32 v73, v76, v77
	v_add_co_u32_e32 v76, vcc, s54, v120
	v_lshlrev_b32_e32 v206, 16, v207
	s_nop 0
	v_addc_co_u32_e32 v77, vcc, 0, v121, vcc
	v_and_b32_e32 v207, 0xffff0000, v207
	v_cvt_pk_bf16_f32 v74, v74, v75
	v_cvt_pk_bf16_f32 v75, v80, v81
	global_store_dwordx4 v[76:77], v[72:75], off
	v_add_f32_e64 v70, v70, v206
	v_add_f32_e64 v71, v71, v207
	v_add_f32_e64 v68, v68, v174
	v_add_f32_e64 v69, v69, v175
	v_add_f32_e64 v72, v66, v176
	v_add_f32_e64 v73, v67, v177
	v_add_f32_e64 v66, v64, v172
	v_add_f32_e64 v67, v65, v173
	v_cvt_pk_bf16_f32 v64, v68, v69
	v_cvt_pk_bf16_f32 v65, v70, v71
	s_waitcnt vmcnt(0)
; __device__ __forceinline__ float bf_lo(unsigned w) { return __uint_as_float(w << 16); }
; __device__ __forceinline__ float bf_hi(unsigned w) { return __uint_as_float(w & 0xffff0000u); }
;     __device__ __forceinline__ void operator()(const f32x4 (&acc)[2][2][4][2], const Unit& u, int wr, int wc, int fr, int fq, const Pre&) const {
;     ...
;         for (int ai = 0; ai < 2; ++ai) {
;             f32x4 r0[4][2], r1[4][2];
; #pragma unroll
;             for (int m = 0; m < 4; ++m)
; #pragma unroll
;                 for (int bj = 0; bj < 2; ++bj) {
;                     const size_t off = off0 + (size_t)(ai * 128 + m * 16) * DM + 128 * bj;
;                     if (RF32) { r0[m][bj] = *(const f32x4*)((const float*)resid + off); r1[m][bj] = *(const f32x4*)((const float*)resid + off + 4); }
;                     else { const u32x4 rbv = rb[ai][m][bj];
;                         r0[m][bj] = (f32x4){bf_lo(rbv.x), bf_hi(rbv.x), bf_lo(rbv.y), bf_hi(rbv.y)}; r1[m][bj] = (f32x4){bf_lo(rbv.z), bf_hi(rbv.z), bf_lo(rbv.w), bf_hi(rbv.w)}; }
;                 }
; #pragma unroll
;             for (int m = 0; m < 4; ++m) {
;                 const int row = u.pm * 256 + ai * 128 + wr * 64 + m * 16 + fr; float sq = 0.f;
; #pragma unroll
;                 for (int bj = 0; bj < 2; ++bj) {
;                     const size_t off = off0 + (size_t)(ai * 128 + m * 16) * DM + 128 * bj;
;                     const f32x4 v0 = acc[ai][bj][m][0] + r0[m][bj], v1 = acc[ai][bj][m][1] + r1[m][bj];
;                     st_bf16x8(hb + off, v0, v1);
;                     sq += v0[0] * v0[0] + v0[1] * v0[1] + v0[2] * v0[2] + v0[3] * v0[3] + v1[0] * v1[0] + v1[1] * v1[1] + v1[2] * v1[2] + v1[3] * v1[3];
;                 }
	v_lshlrev_b32_e32 v78, 16, v159
	v_cvt_pk_bf16_f32 v66, v66, v67
	v_cvt_pk_bf16_f32 v67, v72, v73
	v_lshlrev_b32_e32 v72, 16, v156
	v_and_b32_e32 v73, 0xffff0000, v156
	global_store_dwordx4 v[76:77], v[64:67], off offset:256
	v_lshlrev_b32_e32 v76, 16, v158
	v_and_b32_e32 v77, 0xffff0000, v158
	v_and_b32_e32 v79, 0xffff0000, v159
	v_add_f32_e64 v60, v60, v72
	v_add_f32_e64 v61, v61, v73
	v_lshlrev_b32_e32 v74, 16, v157
	v_and_b32_e32 v75, 0xffff0000, v157
	v_add_f32_e64 v72, v58, v78
	v_add_f32_e64 v73, v59, v79
	v_add_f32_e64 v58, v56, v76
	v_add_f32_e64 v59, v57, v77
	v_cvt_pk_bf16_f32 v56, v60, v61
	v_add_co_u32_e32 v60, vcc, s55, v120
	v_lshlrev_b32_e32 v80, 16, v152
	v_and_b32_e32 v81, 0xffff0000, v152
	v_lshlrev_b32_e32 v82, 16, v153
	v_and_b32_e32 v83, 0xffff0000, v153
	v_lshlrev_b32_e32 v84, 16, v154
	v_and_b32_e32 v85, 0xffff0000, v154
	v_lshlrev_b32_e32 v86, 16, v155
	v_and_b32_e32 v87, 0xffff0000, v155
	v_add_f32_e64 v62, v62, v74
	v_add_f32_e64 v63, v63, v75
	v_addc_co_u32_e32 v61, vcc, 0, v121, vcc
	v_cvt_pk_bf16_f32 v57, v62, v63
	v_lshlrev_b32_e32 v90, 16, v149
	v_and_b32_e32 v91, 0xffff0000, v149
	v_cvt_pk_bf16_f32 v58, v58, v59
	v_cvt_pk_bf16_f32 v59, v72, v73
	global_store_dwordx4 v[60:61], v[56:59], off
	v_add_f32_e64 v54, v54, v82
	v_add_f32_e64 v55, v55, v83
	v_add_f32_e64 v52, v52, v80
	v_add_f32_e64 v53, v53, v81
	v_add_f32_e64 v56, v46, v86
	v_add_f32_e64 v57, v47, v87
	v_add_f32_e64 v46, v44, v84
	v_add_f32_e64 v47, v45, v85
	v_cvt_pk_bf16_f32 v44, v52, v53
	v_cvt_pk_bf16_f32 v45, v54, v55
	v_lshlrev_b32_e32 v88, 16, v148
	v_and_b32_e32 v89, 0xffff0000, v148
	v_lshlrev_b32_e32 v92, 16, v150
	v_and_b32_e32 v93, 0xffff0000, v150
	v_lshlrev_b32_e32 v94, 16, v151
	v_and_b32_e32 v95, 0xffff0000, v151
	v_cvt_pk_bf16_f32 v46, v46, v47
	v_cvt_pk_bf16_f32 v47, v56, v57
	global_store_dwordx4 v[60:61], v[44:47], off offset:256
	v_lshlrev_b32_e32 v96, 16, v144
	v_and_b32_e32 v97, 0xffff0000, v144
	v_add_f32_e64 v44, v50, v90
	v_add_f32_e64 v45, v51, v91
	v_add_f32_e64 v46, v48, v88
	v_add_f32_e64 v47, v49, v89
	v_add_f32_e64 v48, v42, v94
	v_add_f32_e64 v49, v43, v95
	v_add_f32_e64 v42, v40, v92
	v_add_f32_e64 v43, v41, v93
	v_cvt_pk_bf16_f32 v40, v46, v47
	v_cvt_pk_bf16_f32 v41, v44, v45
	v_add_co_u32_e32 v44, vcc, s56, v120
	v_lshlrev_b32_e32 v98, 16, v145
	v_and_b32_e32 v99, 0xffff0000, v145
	v_lshlrev_b32_e32 v100, 16, v146
	v_and_b32_e32 v101, 0xffff0000, v146
	v_lshlrev_b32_e32 v102, 16, v147
	v_and_b32_e32 v103, 0xffff0000, v147
	v_addc_co_u32_e32 v45, vcc, 0, v121, vcc
	v_lshlrev_b32_e32 v106, 16, v141
	v_and_b32_e32 v107, 0xffff0000, v141
	v_cvt_pk_bf16_f32 v42, v42, v43
	v_cvt_pk_bf16_f32 v43, v48, v49
	global_store_dwordx4 v[44:45], v[40:43], off
	v_add_f32_e64 v38, v38, v98
	v_add_f32_e64 v39, v39, v99
	v_add_f32_e64 v36, v36, v96
	v_add_f32_e64 v37, v37, v97
	v_add_f32_e64 v40, v30, v102
	v_add_f32_e64 v41, v31, v103
	v_add_f32_e64 v30, v28, v100
	v_add_f32_e64 v31, v29, v101
	v_cvt_pk_bf16_f32 v28, v36, v37
	v_cvt_pk_bf16_f32 v29, v38, v39
	v_lshlrev_b32_e32 v104, 16, v140
	v_and_b32_e32 v105, 0xffff0000, v140
	v_lshlrev_b32_e32 v108, 16, v142
	v_and_b32_e32 v109, 0xffff0000, v142
	v_lshlrev_b32_e32 v110, 16, v143
	v_and_b32_e32 v111, 0xffff0000, v143
	v_cvt_pk_bf16_f32 v30, v30, v31
	v_cvt_pk_bf16_f32 v31, v40, v41
	global_store_dwordx4 v[44:45], v[28:31], off offset:256
	v_lshlrev_b32_e32 v112, 16, v136
	v_and_b32_e32 v113, 0xffff0000, v136
	v_add_f32_e64 v28, v34, v106
	v_add_f32_e64 v29, v35, v107
	v_add_f32_e64 v30, v32, v104
	v_add_f32_e64 v31, v33, v105
	v_add_f32_e64 v32, v26, v110
	v_add_f32_e64 v33, v27, v111
	v_add_f32_e64 v26, v24, v108
	v_add_f32_e64 v27, v25, v109
	v_cvt_pk_bf16_f32 v24, v30, v31
	v_cvt_pk_bf16_f32 v25, v28, v29
	v_add_co_u32_e32 v28, vcc, s57, v120
	v_lshlrev_b32_e32 v114, 16, v137
	v_and_b32_e32 v115, 0xffff0000, v137
	v_lshlrev_b32_e32 v116, 16, v138
	v_and_b32_e32 v117, 0xffff0000, v138
	v_lshlrev_b32_e32 v118, 16, v139
	v_and_b32_e32 v119, 0xffff0000, v139
	v_addc_co_u32_e32 v29, vcc, 0, v121, vcc
	v_lshlrev_b32_e32 v124, 16, v133
	v_and_b32_e32 v125, 0xffff0000, v133
	v_cvt_pk_bf16_f32 v26, v26, v27
	v_cvt_pk_bf16_f32 v27, v32, v33
	global_store_dwordx4 v[28:29], v[24:27], off
	v_add_f32_e64 v22, v22, v114
	v_add_f32_e64 v23, v23, v115
	v_add_f32_e64 v20, v20, v112
	v_add_f32_e64 v21, v21, v113
	v_add_f32_e64 v24, v14, v118
	v_add_f32_e64 v25, v15, v119
	v_add_f32_e64 v14, v12, v116
	v_add_f32_e64 v15, v13, v117
	v_cvt_pk_bf16_f32 v12, v20, v21
	v_cvt_pk_bf16_f32 v13, v22, v23
	v_lshlrev_b32_e32 v122, 16, v132
	v_and_b32_e32 v123, 0xffff0000, v132
	v_lshlrev_b32_e32 v126, 16, v134
	v_and_b32_e32 v127, 0xffff0000, v134
	v_lshlrev_b32_e32 v132, 16, v135
	v_and_b32_e32 v133, 0xffff0000, v135
	v_cvt_pk_bf16_f32 v14, v14, v15
	v_cvt_pk_bf16_f32 v15, v24, v25
	global_store_dwordx4 v[28:29], v[12:15], off offset:256
	v_lshlrev_b32_e32 v64, 16, v130
	v_and_b32_e32 v65, 0xffff0000, v130
	v_add_f32_e64 v12, v18, v124
	v_add_f32_e64 v13, v19, v125
	v_add_f32_e64 v14, v16, v122
	v_add_f32_e64 v15, v17, v123
	v_add_f32_e64 v16, v10, v132
	v_add_f32_e64 v17, v11, v133
	v_add_f32_e64 v10, v8, v126
	v_add_f32_e64 v11, v9, v127
	v_cvt_pk_bf16_f32 v8, v14, v15
	v_cvt_pk_bf16_f32 v9, v12, v13
	v_add_co_u32_e32 v12, vcc, s58, v120
	v_lshlrev_b32_e32 v68, 16, v131
	v_and_b32_e32 v69, 0xffff0000, v131
	v_addc_co_u32_e32 v13, vcc, 0, v121, vcc
	v_lshlrev_b32_e32 v66, 16, v128
	v_and_b32_e32 v67, 0xffff0000, v128
	v_lshlrev_b32_e32 v70, 16, v129
	v_and_b32_e32 v71, 0xffff0000, v129
	v_cvt_pk_bf16_f32 v10, v10, v11
	v_cvt_pk_bf16_f32 v11, v16, v17
	global_store_dwordx4 v[12:13], v[8:11], off
	s_and_b64 vcc, exec, s[8:9]
	v_add_f32_e64 v6, v6, v70
	v_add_f32_e64 v7, v7, v71
	v_add_f32_e64 v8, v2, v68
	v_add_f32_e64 v9, v3, v69
	v_add_f32_e64 v2, v0, v64
	v_add_f32_e64 v3, v1, v65
	v_add_f32_e64 v4, v4, v66
	v_add_f32_e64 v5, v5, v67
	s_nop 0
	v_cvt_pk_bf16_f32 v0, v4, v5
	v_cvt_pk_bf16_f32 v1, v6, v7
	v_cvt_pk_bf16_f32 v2, v2, v3
	v_cvt_pk_bf16_f32 v3, v8, v9
	global_store_dwordx4 v[12:13], v[0:3], off offset:256
	s_cbranch_vccz .LBB0_2478
	s_waitcnt vmcnt(0)
	s_cmpk_gt_u32 s96, 0xff
	s_cbranch_scc1 .LBB0_2489
	s_barrier

; __device__ __forceinline__ float bf_lo(unsigned w) { return __uint_as_float(w << 16); }
; __device__ __forceinline__ float bf_hi(unsigned w) { return __uint_as_float(w & 0xffff0000u); }
; __device__ __forceinline__ void p9_route(const Frame& F, const bf16_t* h) {
;     ...
;         f32x4 acc0 = (f32x4){0.f, 0.f, 0.f, 0.f}, acc1 = (f32x4){0.f, 0.f, 0.f, 0.f}; float ss = 0.f;
; #pragma unroll 4
;         for (int s = 0; s < 64; ++s) {
;             const u32x2 ab = *(const u32x2*)(hp + 16 * s); const f32x4 a = (f32x4){bf_lo(ab.x), bf_hi(ab.x), bf_lo(ab.y), bf_hi(ab.y)};
;             const f32x4 b0 = *(const f32x4*)(w0 + 16 * s), b1 = *(const f32x4*)(w1 + 16 * s);
;             ss += a[0] * a[0] + a[1] * a[1] + a[2] * a[2] + a[3] * a[3];
; #pragma unroll
;             for (int j = 0; j < 4; ++j) { acc0 = __builtin_amdgcn_mfma_f32_16x16x4f32(a[j], b0[j], acc0, 0, 0, 0); acc1 = __builtin_amdgcn_mfma_f32_16x16x4f32(a[j], b1[j], acc1, 0, 0, 0); }
;         }
;         ss += __shfl_xor(ss, 16); ss += __shfl_xor(ss, 32);
;         if (kq == 0) ssp[kh * 64 + tg * 16 + tok] = ss;
.LBB0_2551:
	v_lshl_add_u64 v[28:29], s[24:25], 0, v[16:17]
	global_load_dwordx2 v[44:45], v[28:29], off offset:-64
	v_lshl_add_u64 v[30:31], s[24:25], 0, v[18:19]
	v_add_co_u32_e32 v46, vcc, s36, v30
	s_add_i32 s2, s2, -4
	s_nop 0
	v_addc_co_u32_e32 v47, vcc, 0, v31, vcc
	v_add_co_u32_e32 v48, vcc, s37, v30
	v_lshl_add_u64 v[18:19], v[18:19], 0, s[16:17]
	s_nop 0
	v_addc_co_u32_e32 v49, vcc, 0, v31, vcc
	global_load_dwordx2 v[50:51], v[28:29], off offset:-32
	global_load_dwordx2 v[52:53], v[28:29], off
	global_load_dwordx2 v[54:55], v[28:29], off offset:32
	s_nop 0
	global_load_dwordx4 v[28:31], v[46:47], off
	global_load_dwordx4 v[32:35], v[48:49], off
	global_load_dwordx4 v[36:39], v[46:47], off offset:64
	global_load_dwordx4 v[40:43], v[48:49], off offset:64
	v_lshl_add_u64 v[16:17], v[16:17], 0, s[28:29]
	s_cmp_eq_u32 s2, 0
	s_waitcnt vmcnt(0)
	v_lshlrev_b32_e32 v56, 16, v44
	v_and_b32_e32 v57, 0xffff0000, v44
	v_lshlrev_b32_e32 v59, 16, v45
	v_and_b32_e32 v58, 0xffff0000, v45
	v_mfma_f32_16x16x4_f32 v[0:3], v56, v28, v[0:3]
	v_lshlrev_b32_e32 v44, 16, v50
	v_and_b32_e32 v45, 0xffff0000, v50
	v_lshlrev_b32_e32 v61, 16, v51
	v_and_b32_e32 v60, 0xffff0000, v51
	v_mfma_f32_16x16x4_f32 v[4:7], v56, v32, v[4:7]
	v_mfma_f32_16x16x4_f32 v[0:3], v57, v29, v[0:3]
	v_mfma_f32_16x16x4_f32 v[4:7], v57, v33, v[4:7]
	v_mfma_f32_16x16x4_f32 v[0:3], v59, v30, v[0:3]
	v_mfma_f32_16x16x4_f32 v[4:7], v59, v34, v[4:7]
	v_mfma_f32_16x16x4_f32 v[0:3], v58, v31, v[0:3]
	global_load_dwordx4 v[28:31], v[46:47], off offset:128
	v_mfma_f32_16x16x4_f32 v[4:7], v58, v35, v[4:7]
	global_load_dwordx4 v[32:35], v[48:49], off offset:128
	v_mfma_f32_16x16x4_f32 v[0:3], v44, v36, v[0:3]
	v_mfma_f32_16x16x4_f32 v[4:7], v44, v40, v[4:7]
	v_mfma_f32_16x16x4_f32 v[0:3], v45, v37, v[0:3]
	v_mfma_f32_16x16x4_f32 v[4:7], v45, v41, v[4:7]
	v_mfma_f32_16x16x4_f32 v[0:3], v61, v38, v[0:3]
	v_mfma_f32_16x16x4_f32 v[4:7], v61, v42, v[4:7]
	v_mfma_f32_16x16x4_f32 v[0:3], v60, v39, v[0:3]
	global_load_dwordx4 v[36:39], v[46:47], off offset:192
	v_lshlrev_b32_e32 v46, 16, v52
	v_and_b32_e32 v47, 0xffff0000, v52
	v_mfma_f32_16x16x4_f32 v[4:7], v60, v43, v[4:7]
	global_load_dwordx4 v[40:43], v[48:49], off offset:192
	s_waitcnt vmcnt(0)
	v_mfma_f32_16x16x4_f32 v[0:3], v46, v28, v[0:3]
	v_and_b32_e32 v28, 0xffff0000, v53
	v_mfma_f32_16x16x4_f32 v[4:7], v46, v32, v[4:7]
	v_and_b32_e32 v32, 0xffff0000, v55
	v_mfma_f32_16x16x4_f32 v[0:3], v47, v29, v[0:3]
	v_lshlrev_b32_e32 v29, 16, v53
	v_mfma_f32_16x16x4_f32 v[4:7], v47, v33, v[4:7]
	v_lshlrev_b32_e32 v33, 16, v55
	v_mul_f32_e64 v46, v46, v46
	v_mul_f32_e64 v47, v47, v47
	v_mul_f32_e64 v48, v32, v32
	v_mul_f32_e64 v49, v33, v33
	v_mfma_f32_16x16x4_f32 v[0:3], v29, v30, v[0:3]
	v_lshlrev_b32_e32 v30, 16, v54
	v_mfma_f32_16x16x4_f32 v[4:7], v29, v34, v[4:7]
	v_mfma_f32_16x16x4_f32 v[0:3], v28, v31, v[0:3]
	v_and_b32_e32 v31, 0xffff0000, v54
	v_mfma_f32_16x16x4_f32 v[4:7], v28, v35, v[4:7]
	v_mul_f32_e64 v34, v56, v56
	v_mul_f32_e64 v35, v57, v57
	v_mul_f32_e64 v28, v28, v28
	v_mul_f32_e64 v29, v29, v29
	v_add_f32_e32 v15, v34, v35
	v_mfma_f32_16x16x4_f32 v[0:3], v30, v36, v[0:3]
	v_mfma_f32_16x16x4_f32 v[4:7], v30, v40, v[4:7]
	v_mfma_f32_16x16x4_f32 v[0:3], v31, v37, v[0:3]
	v_mul_f32_e64 v36, v58, v58
	v_mul_f32_e64 v37, v59, v59
	v_add_f32_e32 v15, v37, v15
	v_add_f32_e32 v15, v36, v15
	v_add_f32_e32 v8, v8, v15
	v_mfma_f32_16x16x4_f32 v[4:7], v31, v41, v[4:7]
	v_mul_f32_e64 v40, v44, v44
	v_mul_f32_e64 v41, v45, v45
	v_mul_f32_e64 v44, v60, v60
	v_mul_f32_e64 v45, v61, v61
	v_add_f32_e32 v27, v40, v41
	v_mul_f32_e64 v30, v30, v30
	v_mul_f32_e64 v31, v31, v31
	v_add_f32_e32 v27, v45, v27
	v_add_f32_e32 v30, v30, v31
	v_add_f32_e32 v27, v44, v27
	v_mfma_f32_16x16x4_f32 v[0:3], v33, v38, v[0:3]
	v_add_f32_e32 v30, v49, v30
	v_add_f32_e32 v8, v8, v27
	v_mfma_f32_16x16x4_f32 v[4:7], v33, v42, v[4:7]
	v_add_f32_e32 v33, v46, v47
	v_add_f32_e32 v29, v29, v33
	v_add_f32_e32 v28, v28, v29
	v_add_f32_e32 v29, v48, v30
	v_add_f32_e32 v8, v8, v28
	v_add_f32_e32 v8, v8, v29
	v_mfma_f32_16x16x4_f32 v[0:3], v32, v39, v[0:3]
	v_mfma_f32_16x16x4_f32 v[4:7], v32, v43, v[4:7]
	s_cbranch_scc0 .LBB0_2551
	ds_bpermute_b32 v15, v20, v8
	s_waitcnt lgkmcnt(0)
	v_add_f32_e32 v8, v8, v15
	ds_bpermute_b32 v15, v21, v8
	s_and_saveexec_b64 s[2:3], s[0:1]
	s_cbranch_execz .LBB0_2554
	s_waitcnt lgkmcnt(0)
	v_add_f32_e32 v8, v8, v15
	ds_write_b32 v22, v8 offset:16384

;     __device__ __forceinline__ void operator()(const f32x4 (&acc)[2][2][4][2], const Unit& u, int wr, int wc, int fr, int fq, const Pre&) const {
;         const int cw = 128 * u.pn + 32 * wc + 8 * fq; const float* bg = bgu + (size_t)u.aux * 4096 + cw;
;         const f32x4 bg0 = *(const f32x4*)bg, bg1 = *(const f32x4*)(bg + 4), bu0 = *(const f32x4*)(bg + 2048), bu1 = *(const f32x4*)(bg + 2052);
;         float rsv[8];
; #pragma unroll
;         for (int q = 0; q < 8; ++q) rsv[q] = rss[u.pm * 256 + (q >> 2) * 128 + wr * 64 + (q & 3) * 16 + fr];
; #pragma unroll
;         for (int ai = 0; ai < 2; ++ai)
; #pragma unroll
;             for (int m = 0; m < 4; ++m) {
;                 const int row = u.pm * 256 + ai * 128 + wr * 64 + m * 16 + fr; const float rs = rsv[ai * 4 + m] * (1.0f / W8_SCALE);
;                 f32x4 o[2];
; #pragma unroll
;                 for (int n = 0; n < 2; ++n) {
;                     f32x4 g = acc[ai][0][m][n] * rs + (n ? bg1 : bg0), up = acc[ai][1][m][n] * rs + (n ? bu1 : bu0);
; #pragma unroll
;                     for (int j = 0; j < 4; ++j) { g[j] = fminf(g[j], 7.0f); up[j] = __builtin_amdgcn_fmed3f(up[j], -7.0f, 7.0f); }
;                     f32x4 z = g * (-1.702f * 1.4426950408889634f), e;
; #pragma unroll
;                     for (int j = 0; j < 4; ++j) e[j] = __builtin_amdgcn_exp2f(z[j]);
;                     e = e + 1.0f;
; #pragma unroll
;                     for (int j = 0; j < 4; ++j) e[j] = __builtin_amdgcn_rcpf(e[j]);
;                     o[n] = (up + 1.0f) * g * e;
;                 }
;                 *(u32x2*)(hdn + (size_t)row * DFF + cw) = pack_fp8x8(o[0][0], o[0][1], o[0][2], o[0][3], o[1][0], o[1][1], o[1][2], o[1][3]);
;             }
.LBB0_2717:
	s_nop 15
 s_nop 7
	v_mbcnt_lo_u32_b32 v6, -1, 0
	v_mbcnt_hi_u32_b32 v6, -1, v6
	s_lshl_b32 s0, s50, 7
	v_ashrrev_i32_e32 v0, 1, v6
	v_and_b32_e32 v0, -8, v0
	s_or_b32 s0, s0, s82
	v_ashrrev_i32_e32 v229, 31, v228
	v_and_or_b32 v6, v6, 15, s81
	v_add_u32_e32 v16, s0, v0
	v_lshlrev_b64 v[0:1], 14, v[228:229]
	v_lshl_add_u32 v36, s48, 8, v6
	v_lshl_add_u64 v[0:1], s[70:71], 0, v[0:1]
	v_ashrrev_i32_e32 v17, 31, v16
	v_ashrrev_i32_e32 v37, 31, v36
	v_lshl_add_u64 v[4:5], v[16:17], 2, v[0:1]
	v_lshl_add_u64 v[6:7], v[36:37], 2, s[10:11]
	global_load_dwordx4 v[0:3], v[4:5], off offset:16
	global_load_dwordx4 v[8:11], v[4:5], off
	global_load_dword v48, v[6:7], off
	v_add_co_u32_e32 v6, vcc, s69, v4
	v_or_b32_e32 v30, 16, v36
	s_nop 0
	v_addc_co_u32_e32 v7, vcc, 0, v5, vcc
	global_load_dwordx4 v[12:15], v[6:7], off
	v_lshl_add_u64 v[4:5], v[4:5], 0, s[36:37]
	global_load_dwordx4 v[4:7], v[4:5], off offset:16
	v_or_b32_e32 v28, 32, v36
	v_or_b32_e32 v26, 48, v36
	v_add_u32_e32 v24, 0x80, v36
	v_add_u32_e32 v22, 0x90, v36
	v_add_u32_e32 v20, 0xa0, v36
	v_add_u32_e32 v18, 0xb0, v36
	v_ashrrev_i32_e32 v31, 31, v30
	v_ashrrev_i32_e32 v29, 31, v28
	v_ashrrev_i32_e32 v27, 31, v26
	v_ashrrev_i32_e32 v25, 31, v24
	v_ashrrev_i32_e32 v23, 31, v22
	v_ashrrev_i32_e32 v21, 31, v20
	v_ashrrev_i32_e32 v19, 31, v18
	v_lshl_add_u64 v[32:33], v[30:31], 2, s[10:11]
	v_lshl_add_u64 v[34:35], v[28:29], 2, s[10:11]
	v_lshl_add_u64 v[38:39], v[26:27], 2, s[10:11]
	v_lshl_add_u64 v[40:41], v[24:25], 2, s[10:11]
	v_lshl_add_u64 v[42:43], v[22:23], 2, s[10:11]
	v_lshl_add_u64 v[44:45], v[20:21], 2, s[10:11]
	v_lshl_add_u64 v[46:47], v[18:19], 2, s[10:11]
	global_load_dword v60, v[32:33], off
	global_load_dword v61, v[34:35], off
	global_load_dword v62, v[38:39], off
	s_nop 0
	global_load_dword v35, v[40:41], off
	global_load_dword v34, v[42:43], off
	global_load_dword v33, v[44:45], off
	global_load_dword v32, v[46:47], off
	v_lshlrev_b64 v[36:37], 11, v[36:37]
	v_lshl_add_u64 v[36:37], s[12:13], 0, v[36:37]
	v_lshl_add_u64 v[36:37], v[36:37], 0, v[16:17]
	v_lshlrev_b64 v[30:31], 11, v[30:31]
	v_lshl_add_u64 v[30:31], s[12:13], 0, v[30:31]
	v_lshl_add_u64 v[30:31], v[30:31], 0, v[16:17]
	v_lshlrev_b64 v[28:29], 11, v[28:29]
	v_lshl_add_u64 v[28:29], s[12:13], 0, v[28:29]
	v_lshl_add_u64 v[28:29], v[28:29], 0, v[16:17]
	v_lshlrev_b64 v[26:27], 11, v[26:27]
	v_lshl_add_u64 v[26:27], s[12:13], 0, v[26:27]
	v_lshl_add_u64 v[26:27], v[26:27], 0, v[16:17]
	v_lshlrev_b64 v[24:25], 11, v[24:25]
	v_lshl_add_u64 v[24:25], s[12:13], 0, v[24:25]
	v_lshl_add_u64 v[24:25], v[24:25], 0, v[16:17]
	v_lshlrev_b64 v[22:23], 11, v[22:23]
	v_lshl_add_u64 v[22:23], s[12:13], 0, v[22:23]
	v_lshl_add_u64 v[22:23], v[22:23], 0, v[16:17]
	v_lshlrev_b64 v[20:21], 11, v[20:21]
	v_lshl_add_u64 v[20:21], s[12:13], 0, v[20:21]
	v_lshl_add_u64 v[20:21], v[20:21], 0, v[16:17]
	s_and_b64 vcc, exec, s[42:43]
	s_waitcnt vmcnt(0)
	v_mul_f32_e32 v38, 0x3c800000, v48
	v_fma_f32 v42, v188, v38, v8
	v_fma_f32 v43, v189, v38, v9
	v_fma_f32 v46, v184, v38, v0
	v_fma_f32 v47, v185, v38, v1
	v_min_f32_e32 v42, 0x40e00000, v42
	v_min_f32_e32 v43, 0x40e00000, v43
	v_min_f32_e32 v46, 0x40e00000, v46
	v_fma_f32 v50, v180, v38, v12
	v_fma_f32 v51, v181, v38, v13
	v_min_f32_e32 v47, 0x40e00000, v47
	v_med3_f32 v50, v50, s85, v247
	v_med3_f32 v51, v51, s85, v247
	v_add_f32_e64 v50, v50, 1.0
	v_add_f32_e64 v51, v51, 1.0
	v_mul_f32_e32 v54, 0xc01d265f, v42
	v_mul_f32_e32 v55, 0xc01d265f, v43
	v_mul_f32_e32 v58, 0xc01d265f, v46
	v_mul_f32_e64 v42, v42, v50
	v_mul_f32_e64 v43, v43, v51
	v_mul_f32_e32 v50, 0xc01d265f, v47
	v_fma_f32 v48, v182, v38, v14
	v_fma_f32 v49, v183, v38, v15
	v_exp_f32_e32 v54, v54
	v_exp_f32_e32 v55, v55
	v_exp_f32_e32 v58, v58
	v_exp_f32_e32 v59, v50
	v_fma_f32 v40, v190, v38, v10
	v_fma_f32 v41, v191, v38, v11
	v_fma_f32 v44, v186, v38, v2
	v_fma_f32 v45, v187, v38, v3
	v_med3_f32 v48, v48, s85, v247
	v_med3_f32 v49, v49, s85, v247
	v_min_f32_e32 v40, 0x40e00000, v40
	v_min_f32_e32 v41, 0x40e00000, v41
	v_min_f32_e32 v44, 0x40e00000, v44
	v_min_f32_e32 v45, 0x40e00000, v45
	v_add_f32_e64 v48, v48, 1.0
	v_add_f32_e64 v49, v49, 1.0
	v_fma_f32 v52, v178, v38, v6
	v_fma_f32 v53, v179, v38, v7
	v_mul_f32_e32 v56, 0xc01d265f, v40
	v_mul_f32_e32 v57, 0xc01d265f, v41
	v_mul_f32_e64 v40, v40, v48
	v_mul_f32_e64 v41, v41, v49
	v_mul_f32_e32 v48, 0xc01d265f, v44
	v_mul_f32_e32 v49, 0xc01d265f, v45
	v_exp_f32_e32 v56, v56
	v_exp_f32_e32 v57, v57
	v_add_f32_e64 v54, v54, 1.0
	v_add_f32_e64 v55, v55, 1.0
	v_exp_f32_e32 v48, v48
	v_exp_f32_e32 v49, v49
	v_med3_f32 v50, v52, s85, v247
	v_med3_f32 v51, v53, s85, v247
	v_add_f32_e64 v52, v58, 1.0
	v_add_f32_e64 v53, v59, 1.0
	v_fma_f32 v39, v177, v38, v5
	v_fma_f32 v38, v176, v38, v4
	v_rcp_f32_e32 v54, v54
	v_rcp_f32_e32 v55, v55
	v_rcp_f32_e32 v52, v52
	v_rcp_f32_e32 v53, v53
	v_med3_f32 v38, v38, s85, v247
	v_med3_f32 v39, v39, s85, v247
	v_add_f32_e64 v38, v38, 1.0
	v_add_f32_e64 v39, v39, 1.0
	v_add_f32_e64 v56, v56, 1.0
	v_add_f32_e64 v57, v57, 1.0
	v_add_f32_e64 v48, v48, 1.0
	v_add_f32_e64 v49, v49, 1.0
	v_mul_f32_e64 v38, v46, v38
	v_mul_f32_e64 v39, v47, v39
	v_rcp_f32_e32 v56, v56
	v_rcp_f32_e32 v57, v57
	v_mul_f32_e64 v42, v42, v54
	v_mul_f32_e64 v43, v43, v55
	v_rcp_f32_e32 v48, v48
	v_rcp_f32_e32 v49, v49
	v_mul_f32_e64 v38, v38, v52
	v_mul_f32_e64 v39, v39, v53
	v_mov_b32_e32 v46, v201
	v_mov_b32_e32 v47, v201
	v_cvt_pk_fp8_f32 v46, v42, v43
	v_cvt_pk_fp8_f32 v47, v38, v39
	v_add_f32_e64 v50, v50, 1.0
	v_add_f32_e64 v51, v51, 1.0
	v_mul_f32_e64 v40, v40, v56
	v_mul_f32_e64 v41, v41, v57
	v_mul_f32_e64 v38, v44, v50
	v_mul_f32_e64 v39, v45, v51
;     __device__ __forceinline__ void operator()(const f32x4 (&acc)[2][2][4][2], const Unit& u, int wr, int wc, int fr, int fq, const Pre&) const {
;     ...
;         for (int ai = 0; ai < 2; ++ai)
; #pragma unroll
;             for (int m = 0; m < 4; ++m) {
;                 const int row = u.pm * 256 + ai * 128 + wr * 64 + m * 16 + fr; const float rs = rsv[ai * 4 + m] * (1.0f / W8_SCALE);
;                 f32x4 o[2];
; #pragma unroll
;                 for (int n = 0; n < 2; ++n) {
;                     f32x4 g = acc[ai][0][m][n] * rs + (n ? bg1 : bg0), up = acc[ai][1][m][n] * rs + (n ? bu1 : bu0);
; #pragma unroll
;                     for (int j = 0; j < 4; ++j) { g[j] = fminf(g[j], 7.0f); up[j] = __builtin_amdgcn_fmed3f(up[j], -7.0f, 7.0f); }
;                     f32x4 z = g * (-1.702f * 1.4426950408889634f), e;
; #pragma unroll
;                     for (int j = 0; j < 4; ++j) e[j] = __builtin_amdgcn_exp2f(z[j]);
;                     e = e + 1.0f;
; #pragma unroll
;                     for (int j = 0; j < 4; ++j) e[j] = __builtin_amdgcn_rcpf(e[j]);
;                     o[n] = (up + 1.0f) * g * e;
;                 }
;                 *(u32x2*)(hdn + (size_t)row * DFF + cw) = pack_fp8x8(o[0][0], o[0][1], o[0][2], o[0][3], o[1][0], o[1][1], o[1][2], o[1][3]);
;             }
	v_cvt_pk_fp8_f32 v46, v40, v41 op_sel:[0,0,1]
	v_mul_f32_e64 v38, v38, v48
	v_mul_f32_e64 v39, v39, v49
	s_nop 0
	v_cvt_pk_fp8_f32 v47, v38, v39 op_sel:[0,0,1]
	global_store_dwordx2 v[36:37], v[46:47], off
	v_mul_f32_e32 v36, 0x3c800000, v60
	v_fma_f32 v38, v174, v36, v10
	v_fma_f32 v39, v175, v36, v11
	v_fma_f32 v40, v172, v36, v8
	v_fma_f32 v41, v173, v36, v9
	v_min_f32_e32 v38, 0x40e00000, v38
	v_min_f32_e32 v39, 0x40e00000, v39
	v_mul_f32_e32 v47, 0xc01d265f, v38
	v_exp_f32_e32 v48, v47
	v_mul_f32_e32 v47, 0xc01d265f, v39
	v_exp_f32_e32 v49, v47
	v_min_f32_e32 v40, 0x40e00000, v40
	v_fma_f32 v42, v170, v36, v14
	v_fma_f32 v43, v171, v36, v15
	v_fma_f32 v44, v168, v36, v12
	v_fma_f32 v45, v169, v36, v13
	v_min_f32_e32 v41, 0x40e00000, v41
	v_mul_f32_e32 v37, 0xc01d265f, v40
	v_add_f32_e64 v48, v48, 1.0
	v_add_f32_e64 v49, v49, 1.0
	v_med3_f32 v44, v44, s85, v247
	v_med3_f32 v45, v45, s85, v247
	v_exp_f32_e32 v46, v37
	v_mul_f32_e32 v37, 0xc01d265f, v41
	v_rcp_f32_e32 v48, v48
	v_rcp_f32_e32 v49, v49
	v_exp_f32_e32 v47, v37
	v_med3_f32 v42, v42, s85, v247
	v_med3_f32 v43, v43, s85, v247
	v_add_f32_e64 v44, v44, 1.0
	v_add_f32_e64 v45, v45, 1.0
	v_add_f32_e64 v42, v42, 1.0
	v_add_f32_e64 v43, v43, 1.0
	v_mul_f32_e64 v40, v40, v44
	v_mul_f32_e64 v41, v41, v45
	v_fma_f32 v44, v164, v36, v0
	v_fma_f32 v45, v165, v36, v1
	v_mul_f32_e64 v38, v38, v42
	v_mul_f32_e64 v39, v39, v43
	v_min_f32_e32 v44, 0x40e00000, v44
	v_min_f32_e32 v45, 0x40e00000, v45
	v_mul_f32_e64 v38, v38, v48
	v_mul_f32_e64 v39, v39, v49
	v_mul_f32_e32 v48, 0xc01d265f, v44
	v_mul_f32_e32 v49, 0xc01d265f, v45
	v_add_f32_e64 v46, v46, 1.0
	v_add_f32_e64 v47, v47, 1.0
	v_exp_f32_e32 v48, v48
	v_exp_f32_e32 v49, v49
	v_rcp_f32_e32 v46, v46
	v_rcp_f32_e32 v47, v47
	v_fma_f32 v42, v166, v36, v2
	v_fma_f32 v43, v167, v36, v3
	v_add_f32_e64 v48, v48, 1.0
	v_add_f32_e64 v49, v49, 1.0
	v_min_f32_e32 v42, 0x40e00000, v42
	v_min_f32_e32 v43, 0x40e00000, v43
	v_mul_f32_e32 v50, 0xc01d265f, v42
	v_mul_f32_e32 v51, 0xc01d265f, v43
	v_exp_f32_e32 v50, v50
	v_exp_f32_e32 v51, v51
	v_mul_f32_e64 v40, v40, v46
	v_mul_f32_e64 v41, v41, v47
	v_fma_f32 v46, v162, v36, v6
	v_fma_f32 v47, v163, v36, v7
	v_fma_f32 v37, v161, v36, v5
	v_fma_f32 v36, v160, v36, v4
	v_rcp_f32_e32 v48, v48
	v_rcp_f32_e32 v49, v49
	v_med3_f32 v36, v36, s85, v247
	v_med3_f32 v37, v37, s85, v247
	v_add_f32_e64 v36, v36, 1.0
	v_add_f32_e64 v37, v37, 1.0
	v_add_f32_e64 v50, v50, 1.0
	v_add_f32_e64 v51, v51, 1.0
	v_mul_f32_e64 v36, v44, v36
	v_mul_f32_e64 v37, v45, v37
	v_rcp_f32_e32 v50, v50
	v_rcp_f32_e32 v51, v51
	v_mul_f32_e64 v36, v36, v48
	v_mul_f32_e64 v37, v37, v49
	v_mov_b32_e32 v44, v201
	v_mov_b32_e32 v45, v201
	v_med3_f32 v46, v46, s85, v247
	v_med3_f32 v47, v47, s85, v247
	v_cvt_pk_fp8_f32 v44, v40, v41
	v_cvt_pk_fp8_f32 v45, v36, v37
	v_add_f32_e64 v46, v46, 1.0
	v_add_f32_e64 v47, v47, 1.0
	v_cvt_pk_fp8_f32 v44, v38, v39 op_sel:[0,0,1]
	v_mul_f32_e64 v36, v42, v46
	v_mul_f32_e64 v37, v43, v47
	s_nop 0
	v_mul_f32_e64 v36, v36, v50
	v_mul_f32_e64 v37, v37, v51
	s_nop 0
	v_cvt_pk_fp8_f32 v45, v36, v37 op_sel:[0,0,1]
	global_store_dwordx2 v[30:31], v[44:45], off
	v_mul_f32_e32 v30, 0x3c800000, v61
	v_fma_f32 v36, v158, v30, v10
	v_fma_f32 v37, v159, v30, v11
	v_fma_f32 v38, v156, v30, v8
	v_fma_f32 v39, v157, v30, v9
	v_min_f32_e32 v36, 0x40e00000, v36
	v_min_f32_e32 v37, 0x40e00000, v37
	v_mul_f32_e32 v45, 0xc01d265f, v36
	v_exp_f32_e32 v46, v45
	v_mul_f32_e32 v45, 0xc01d265f, v37
	v_exp_f32_e32 v47, v45
	v_min_f32_e32 v38, 0x40e00000, v38
	v_fma_f32 v40, v154, v30, v14
	v_fma_f32 v41, v155, v30, v15
	v_fma_f32 v42, v152, v30, v12
	v_fma_f32 v43, v153, v30, v13
	v_min_f32_e32 v39, 0x40e00000, v39
	v_mul_f32_e32 v31, 0xc01d265f, v38
	v_add_f32_e64 v46, v46, 1.0
	v_add_f32_e64 v47, v47, 1.0
	v_med3_f32 v42, v42, s85, v247
	v_med3_f32 v43, v43, s85, v247
	v_exp_f32_e32 v44, v31
	v_mul_f32_e32 v31, 0xc01d265f, v39
	v_rcp_f32_e32 v46, v46
	v_rcp_f32_e32 v47, v47
	v_exp_f32_e32 v45, v31
	v_med3_f32 v40, v40, s85, v247
	v_med3_f32 v41, v41, s85, v247
	v_add_f32_e64 v42, v42, 1.0
	v_add_f32_e64 v43, v43, 1.0
	v_add_f32_e64 v40, v40, 1.0
	v_add_f32_e64 v41, v41, 1.0
	v_mul_f32_e64 v38, v38, v42
	v_mul_f32_e64 v39, v39, v43
	v_fma_f32 v42, v148, v30, v0
	v_fma_f32 v43, v149, v30, v1
	v_mul_f32_e64 v36, v36, v40
	v_mul_f32_e64 v37, v37, v41
	v_min_f32_e32 v42, 0x40e00000, v42
	v_min_f32_e32 v43, 0x40e00000, v43
	v_mul_f32_e64 v36, v36, v46
	v_mul_f32_e64 v37, v37, v47
	v_mul_f32_e32 v46, 0xc01d265f, v42
	v_mul_f32_e32 v47, 0xc01d265f, v43
	v_add_f32_e64 v44, v44, 1.0
	v_add_f32_e64 v45, v45, 1.0
	v_exp_f32_e32 v46, v46
	v_exp_f32_e32 v47, v47
	v_rcp_f32_e32 v44, v44
	v_rcp_f32_e32 v45, v45
	v_fma_f32 v40, v150, v30, v2
	v_fma_f32 v41, v151, v30, v3
	v_add_f32_e64 v46, v46, 1.0
	v_add_f32_e64 v47, v47, 1.0
	v_min_f32_e32 v40, 0x40e00000, v40
	v_min_f32_e32 v41, 0x40e00000, v41
	v_mul_f32_e32 v48, 0xc01d265f, v40
	v_mul_f32_e32 v49, 0xc01d265f, v41
	v_exp_f32_e32 v48, v48
	v_exp_f32_e32 v49, v49
	v_mul_f32_e64 v38, v38, v44
	v_mul_f32_e64 v39, v39, v45
	v_fma_f32 v44, v146, v30, v6
	v_fma_f32 v45, v147, v30, v7
	v_fma_f32 v31, v145, v30, v5
	v_fma_f32 v30, v144, v30, v4
	v_rcp_f32_e32 v46, v46
	v_rcp_f32_e32 v47, v47
	v_med3_f32 v30, v30, s85, v247
	v_med3_f32 v31, v31, s85, v247
	v_add_f32_e64 v30, v30, 1.0
	v_add_f32_e64 v31, v31, 1.0
	v_add_f32_e64 v48, v48, 1.0
	v_add_f32_e64 v49, v49, 1.0
	v_mul_f32_e64 v30, v42, v30
	v_mul_f32_e64 v31, v43, v31
	v_rcp_f32_e32 v48, v48
	v_rcp_f32_e32 v49, v49
	v_mul_f32_e64 v30, v30, v46
	v_mul_f32_e64 v31, v31, v47
	v_mov_b32_e32 v42, v201
	v_mov_b32_e32 v43, v201
	v_med3_f32 v44, v44, s85, v247
;     __device__ __forceinline__ void operator()(const f32x4 (&acc)[2][2][4][2], const Unit& u, int wr, int wc, int fr, int fq, const Pre&) const {
;     ...
;         for (int ai = 0; ai < 2; ++ai)
; #pragma unroll
;             for (int m = 0; m < 4; ++m) {
;                 const int row = u.pm * 256 + ai * 128 + wr * 64 + m * 16 + fr; const float rs = rsv[ai * 4 + m] * (1.0f / W8_SCALE);
;                 f32x4 o[2];
; #pragma unroll
;                 for (int n = 0; n < 2; ++n) {
;                     f32x4 g = acc[ai][0][m][n] * rs + (n ? bg1 : bg0), up = acc[ai][1][m][n] * rs + (n ? bu1 : bu0);
; #pragma unroll
;                     for (int j = 0; j < 4; ++j) { g[j] = fminf(g[j], 7.0f); up[j] = __builtin_amdgcn_fmed3f(up[j], -7.0f, 7.0f); }
;                     f32x4 z = g * (-1.702f * 1.4426950408889634f), e;
; #pragma unroll
;                     for (int j = 0; j < 4; ++j) e[j] = __builtin_amdgcn_exp2f(z[j]);
;                     e = e + 1.0f;
; #pragma unroll
;                     for (int j = 0; j < 4; ++j) e[j] = __builtin_amdgcn_rcpf(e[j]);
;                     o[n] = (up + 1.0f) * g * e;
;                 }
;                 *(u32x2*)(hdn + (size_t)row * DFF + cw) = pack_fp8x8(o[0][0], o[0][1], o[0][2], o[0][3], o[1][0], o[1][1], o[1][2], o[1][3]);
;             }
	v_med3_f32 v45, v45, s85, v247
	v_cvt_pk_fp8_f32 v42, v38, v39
	v_cvt_pk_fp8_f32 v43, v30, v31
	v_add_f32_e64 v44, v44, 1.0
	v_add_f32_e64 v45, v45, 1.0
	v_cvt_pk_fp8_f32 v42, v36, v37 op_sel:[0,0,1]
	v_mul_f32_e64 v30, v40, v44
	v_mul_f32_e64 v31, v41, v45
	s_nop 0
	v_mul_f32_e64 v30, v30, v48
	v_mul_f32_e64 v31, v31, v49
	s_nop 0
	v_cvt_pk_fp8_f32 v43, v30, v31 op_sel:[0,0,1]
	global_store_dwordx2 v[28:29], v[42:43], off
	v_mul_f32_e32 v28, 0x3c800000, v62
	v_fma_f32 v30, v142, v28, v10
	v_fma_f32 v31, v143, v28, v11
	v_fma_f32 v36, v140, v28, v8
	v_fma_f32 v37, v141, v28, v9
	v_min_f32_e32 v30, 0x40e00000, v30
	v_min_f32_e32 v31, 0x40e00000, v31
	v_mul_f32_e32 v43, 0xc01d265f, v30
	v_exp_f32_e32 v44, v43
	v_mul_f32_e32 v43, 0xc01d265f, v31
	v_exp_f32_e32 v45, v43
	v_min_f32_e32 v36, 0x40e00000, v36
	v_fma_f32 v38, v138, v28, v14
	v_fma_f32 v39, v139, v28, v15
	v_fma_f32 v40, v136, v28, v12
	v_fma_f32 v41, v137, v28, v13
	v_min_f32_e32 v37, 0x40e00000, v37
	v_mul_f32_e32 v29, 0xc01d265f, v36
	v_add_f32_e64 v44, v44, 1.0
	v_add_f32_e64 v45, v45, 1.0
	v_med3_f32 v40, v40, s85, v247
	v_med3_f32 v41, v41, s85, v247
	v_exp_f32_e32 v42, v29
	v_mul_f32_e32 v29, 0xc01d265f, v37
	v_rcp_f32_e32 v44, v44
	v_rcp_f32_e32 v45, v45
	v_exp_f32_e32 v43, v29
	v_med3_f32 v38, v38, s85, v247
	v_med3_f32 v39, v39, s85, v247
	v_add_f32_e64 v40, v40, 1.0
	v_add_f32_e64 v41, v41, 1.0
	v_add_f32_e64 v38, v38, 1.0
	v_add_f32_e64 v39, v39, 1.0
	v_mul_f32_e64 v36, v36, v40
	v_mul_f32_e64 v37, v37, v41
	v_fma_f32 v40, v132, v28, v0
	v_fma_f32 v41, v133, v28, v1
	v_mul_f32_e64 v30, v30, v38
	v_mul_f32_e64 v31, v31, v39
	v_min_f32_e32 v40, 0x40e00000, v40
	v_min_f32_e32 v41, 0x40e00000, v41
	v_mul_f32_e64 v30, v30, v44
	v_mul_f32_e64 v31, v31, v45
	v_mul_f32_e32 v44, 0xc01d265f, v40
	v_mul_f32_e32 v45, 0xc01d265f, v41
	v_add_f32_e64 v42, v42, 1.0
	v_add_f32_e64 v43, v43, 1.0
	v_exp_f32_e32 v44, v44
	v_exp_f32_e32 v45, v45
	v_rcp_f32_e32 v42, v42
	v_rcp_f32_e32 v43, v43
	v_fma_f32 v38, v134, v28, v2
	v_fma_f32 v39, v135, v28, v3
	v_add_f32_e64 v44, v44, 1.0
	v_add_f32_e64 v45, v45, 1.0
	v_min_f32_e32 v38, 0x40e00000, v38
	v_min_f32_e32 v39, 0x40e00000, v39
	v_mul_f32_e32 v46, 0xc01d265f, v38
	v_mul_f32_e32 v47, 0xc01d265f, v39
	v_exp_f32_e32 v46, v46
	v_exp_f32_e32 v47, v47
	v_mul_f32_e64 v36, v36, v42
	v_mul_f32_e64 v37, v37, v43
	v_fma_f32 v42, v130, v28, v6
	v_fma_f32 v43, v131, v28, v7
	v_fma_f32 v29, v129, v28, v5
	v_fma_f32 v28, v128, v28, v4
	v_rcp_f32_e32 v44, v44
	v_rcp_f32_e32 v45, v45
	v_med3_f32 v28, v28, s85, v247
	v_med3_f32 v29, v29, s85, v247
	v_add_f32_e64 v28, v28, 1.0
	v_add_f32_e64 v29, v29, 1.0
	v_add_f32_e64 v46, v46, 1.0
	v_add_f32_e64 v47, v47, 1.0
	v_mul_f32_e64 v28, v40, v28
	v_mul_f32_e64 v29, v41, v29
	v_rcp_f32_e32 v46, v46
	v_rcp_f32_e32 v47, v47
	v_mul_f32_e64 v28, v28, v44
	v_mul_f32_e64 v29, v29, v45
	v_mov_b32_e32 v40, v201
	v_mov_b32_e32 v41, v201
	v_med3_f32 v42, v42, s85, v247
	v_med3_f32 v43, v43, s85, v247
	v_cvt_pk_fp8_f32 v40, v36, v37
	v_cvt_pk_fp8_f32 v41, v28, v29
	v_add_f32_e64 v42, v42, 1.0
	v_add_f32_e64 v43, v43, 1.0
	v_cvt_pk_fp8_f32 v40, v30, v31 op_sel:[0,0,1]
	v_mul_f32_e64 v28, v38, v42
	v_mul_f32_e64 v29, v39, v43
	s_nop 0
	v_mul_f32_e64 v28, v28, v46
	v_mul_f32_e64 v29, v29, v47
	s_nop 0
	v_cvt_pk_fp8_f32 v41, v28, v29 op_sel:[0,0,1]
	global_store_dwordx2 v[26:27], v[40:41], off
	v_mul_f32_e32 v26, 0x3c800000, v35
	v_fma_f32 v28, v118, v26, v10
	v_fma_f32 v29, v119, v26, v11
	v_fma_f32 v30, v116, v26, v8
	v_fma_f32 v31, v117, v26, v9
	v_min_f32_e32 v28, 0x40e00000, v28
	v_min_f32_e32 v29, 0x40e00000, v29
	v_mul_f32_e32 v35, 0xc01d265f, v28
	v_exp_f32_e32 v42, v35
	v_mul_f32_e32 v35, 0xc01d265f, v29
	v_exp_f32_e32 v43, v35
	v_fma_f32 v36, v126, v26, v14
	v_fma_f32 v37, v127, v26, v15
	v_fma_f32 v38, v124, v26, v12
	v_fma_f32 v39, v125, v26, v13
	v_min_f32_e32 v30, 0x40e00000, v30
	v_add_f32_e64 v42, v42, 1.0
	v_add_f32_e64 v43, v43, 1.0
	v_med3_f32 v38, v38, s85, v247
	v_min_f32_e32 v31, 0x40e00000, v31
	v_med3_f32 v39, v39, s85, v247
	v_mul_f32_e32 v27, 0xc01d265f, v30
	v_med3_f32 v36, v36, s85, v247
	v_med3_f32 v37, v37, s85, v247
	v_rcp_f32_e32 v42, v42
	v_rcp_f32_e32 v43, v43
	v_exp_f32_e32 v40, v27
	v_mul_f32_e32 v27, 0xc01d265f, v31
	v_add_f32_e64 v36, v36, 1.0
	v_add_f32_e64 v37, v37, 1.0
	v_add_f32_e64 v38, v38, 1.0
	v_add_f32_e64 v39, v39, 1.0
	v_exp_f32_e32 v41, v27
	v_mul_f32_e64 v30, v30, v38
	v_mul_f32_e64 v31, v31, v39
	v_mul_f32_e64 v28, v28, v36
	v_mul_f32_e64 v29, v29, v37
	v_fma_f32 v36, v110, v26, v2
	v_fma_f32 v37, v111, v26, v3
	v_fma_f32 v38, v108, v26, v0
	v_fma_f32 v39, v109, v26, v1
	v_min_f32_e32 v36, 0x40e00000, v36
	v_min_f32_e32 v38, 0x40e00000, v38
	v_mul_f32_e64 v28, v28, v42
	v_mul_f32_e64 v29, v29, v43
	v_min_f32_e32 v39, 0x40e00000, v39
	v_min_f32_e32 v37, 0x40e00000, v37
	v_mul_f32_e32 v35, 0xc01d265f, v38
	v_mul_f32_e32 v43, 0xc01d265f, v36
	v_exp_f32_e32 v42, v35
	v_mul_f32_e32 v35, 0xc01d265f, v39
	v_exp_f32_e32 v44, v43
	v_mul_f32_e32 v43, 0xc01d265f, v37
	v_add_f32_e64 v40, v40, 1.0
	v_add_f32_e64 v41, v41, 1.0
	v_exp_f32_e32 v45, v43
	v_exp_f32_e32 v43, v35
	v_rcp_f32_e32 v40, v40
	v_rcp_f32_e32 v41, v41
	v_add_f32_e64 v44, v44, 1.0
	v_add_f32_e64 v45, v45, 1.0
	v_add_f32_e64 v42, v42, 1.0
	v_add_f32_e64 v43, v43, 1.0
	v_rcp_f32_e32 v44, v44
	v_mul_f32_e64 v30, v30, v40
	v_mul_f32_e64 v31, v31, v41
	v_fma_f32 v40, v122, v26, v6
	v_fma_f32 v41, v123, v26, v7
	v_fma_f32 v27, v121, v26, v5
	v_fma_f32 v26, v120, v26, v4
	v_rcp_f32_e32 v42, v42
	v_rcp_f32_e32 v43, v43
	v_med3_f32 v26, v26, s85, v247
	v_med3_f32 v27, v27, s85, v247
	v_add_f32_e64 v26, v26, 1.0
	v_add_f32_e64 v27, v27, 1.0
;     __device__ __forceinline__ void operator()(const f32x4 (&acc)[2][2][4][2], const Unit& u, int wr, int wc, int fr, int fq, const Pre&) const {
;     ...
;         for (int ai = 0; ai < 2; ++ai)
; #pragma unroll
;             for (int m = 0; m < 4; ++m) {
;                 const int row = u.pm * 256 + ai * 128 + wr * 64 + m * 16 + fr; const float rs = rsv[ai * 4 + m] * (1.0f / W8_SCALE);
;                 f32x4 o[2];
; #pragma unroll
;                 for (int n = 0; n < 2; ++n) {
;                     f32x4 g = acc[ai][0][m][n] * rs + (n ? bg1 : bg0), up = acc[ai][1][m][n] * rs + (n ? bu1 : bu0);
; #pragma unroll
;                     for (int j = 0; j < 4; ++j) { g[j] = fminf(g[j], 7.0f); up[j] = __builtin_amdgcn_fmed3f(up[j], -7.0f, 7.0f); }
;                     f32x4 z = g * (-1.702f * 1.4426950408889634f), e;
; #pragma unroll
;                     for (int j = 0; j < 4; ++j) e[j] = __builtin_amdgcn_exp2f(z[j]);
;                     e = e + 1.0f;
; #pragma unroll
;                     for (int j = 0; j < 4; ++j) e[j] = __builtin_amdgcn_rcpf(e[j]);
;                     o[n] = (up + 1.0f) * g * e;
;                 }
;                 *(u32x2*)(hdn + (size_t)row * DFF + cw) = pack_fp8x8(o[0][0], o[0][1], o[0][2], o[0][3], o[1][0], o[1][1], o[1][2], o[1][3]);
;             }
	v_rcp_f32_e32 v45, v45
	v_mul_f32_e64 v26, v38, v26
	v_mul_f32_e64 v27, v39, v27
	v_mov_b32_e32 v38, v201
	v_mul_f32_e64 v26, v26, v42
	v_mul_f32_e64 v27, v27, v43
	v_mov_b32_e32 v39, v201
	v_med3_f32 v40, v40, s85, v247
	v_med3_f32 v41, v41, s85, v247
	v_cvt_pk_fp8_f32 v38, v30, v31
	v_cvt_pk_fp8_f32 v39, v26, v27
	v_add_f32_e64 v40, v40, 1.0
	v_add_f32_e64 v41, v41, 1.0
	v_cvt_pk_fp8_f32 v38, v28, v29 op_sel:[0,0,1]
	v_mul_f32_e64 v26, v36, v40
	v_mul_f32_e64 v27, v37, v41
	s_nop 0
	v_mul_f32_e64 v26, v26, v44
	v_mul_f32_e64 v27, v27, v45
	s_nop 0
	v_cvt_pk_fp8_f32 v39, v26, v27 op_sel:[0,0,1]
	global_store_dwordx2 v[24:25], v[38:39], off
	v_mul_f32_e32 v24, 0x3c800000, v34
	v_fma_f32 v26, v102, v24, v10
	v_fma_f32 v27, v103, v24, v11
	v_fma_f32 v28, v100, v24, v8
	v_fma_f32 v29, v101, v24, v9
	v_min_f32_e32 v26, 0x40e00000, v26
	v_min_f32_e32 v27, 0x40e00000, v27
	v_mul_f32_e32 v37, 0xc01d265f, v26
	v_exp_f32_e32 v38, v37
	v_mul_f32_e32 v37, 0xc01d265f, v27
	v_exp_f32_e32 v39, v37
	v_min_f32_e32 v28, 0x40e00000, v28
	v_fma_f32 v30, v114, v24, v14
	v_fma_f32 v31, v115, v24, v15
	v_fma_f32 v34, v112, v24, v12
	v_fma_f32 v35, v113, v24, v13
	v_min_f32_e32 v29, 0x40e00000, v29
	v_mul_f32_e32 v25, 0xc01d265f, v28
	v_add_f32_e64 v38, v38, 1.0
	v_add_f32_e64 v39, v39, 1.0
	v_med3_f32 v34, v34, s85, v247
	v_med3_f32 v35, v35, s85, v247
	v_exp_f32_e32 v36, v25
	v_mul_f32_e32 v25, 0xc01d265f, v29
	v_rcp_f32_e32 v38, v38
	v_rcp_f32_e32 v39, v39
	v_exp_f32_e32 v37, v25
	v_med3_f32 v30, v30, s85, v247
	v_med3_f32 v31, v31, s85, v247
	v_add_f32_e64 v34, v34, 1.0
	v_add_f32_e64 v35, v35, 1.0
	v_add_f32_e64 v30, v30, 1.0
	v_add_f32_e64 v31, v31, 1.0
	v_mul_f32_e64 v28, v28, v34
	v_mul_f32_e64 v29, v29, v35
	v_fma_f32 v34, v92, v24, v0
	v_fma_f32 v35, v93, v24, v1
	v_mul_f32_e64 v26, v26, v30
	v_mul_f32_e64 v27, v27, v31
	v_min_f32_e32 v34, 0x40e00000, v34
	v_min_f32_e32 v35, 0x40e00000, v35
	v_mul_f32_e64 v26, v26, v38
	v_mul_f32_e64 v27, v27, v39
	v_mul_f32_e32 v38, 0xc01d265f, v34
	v_mul_f32_e32 v39, 0xc01d265f, v35
	v_add_f32_e64 v36, v36, 1.0
	v_add_f32_e64 v37, v37, 1.0
	v_exp_f32_e32 v38, v38
	v_exp_f32_e32 v39, v39
	v_rcp_f32_e32 v36, v36
	v_rcp_f32_e32 v37, v37
	v_fma_f32 v30, v94, v24, v2
	v_fma_f32 v31, v95, v24, v3
	v_add_f32_e64 v38, v38, 1.0
	v_add_f32_e64 v39, v39, 1.0
	v_min_f32_e32 v30, 0x40e00000, v30
	v_min_f32_e32 v31, 0x40e00000, v31
	v_mul_f32_e32 v40, 0xc01d265f, v30
	v_mul_f32_e32 v41, 0xc01d265f, v31
	v_exp_f32_e32 v40, v40
	v_exp_f32_e32 v41, v41
	v_mul_f32_e64 v28, v28, v36
	v_mul_f32_e64 v29, v29, v37
	v_fma_f32 v36, v106, v24, v6
	v_fma_f32 v37, v107, v24, v7
	v_fma_f32 v25, v105, v24, v5
	v_fma_f32 v24, v104, v24, v4
	v_rcp_f32_e32 v38, v38
	v_rcp_f32_e32 v39, v39
	v_med3_f32 v24, v24, s85, v247
	v_med3_f32 v25, v25, s85, v247
	v_add_f32_e64 v24, v24, 1.0
	v_add_f32_e64 v25, v25, 1.0
	v_add_f32_e64 v40, v40, 1.0
	v_add_f32_e64 v41, v41, 1.0
	v_mul_f32_e64 v24, v34, v24
	v_mul_f32_e64 v25, v35, v25
	v_rcp_f32_e32 v40, v40
	v_rcp_f32_e32 v41, v41
	v_mul_f32_e64 v24, v24, v38
	v_mul_f32_e64 v25, v25, v39
	v_mov_b32_e32 v34, v201
	v_mov_b32_e32 v35, v201
	v_med3_f32 v36, v36, s85, v247
	v_med3_f32 v37, v37, s85, v247
	v_cvt_pk_fp8_f32 v34, v28, v29
	v_cvt_pk_fp8_f32 v35, v24, v25
	v_add_f32_e64 v36, v36, 1.0
	v_add_f32_e64 v37, v37, 1.0
	v_cvt_pk_fp8_f32 v34, v26, v27 op_sel:[0,0,1]
	v_mul_f32_e64 v24, v30, v36
	v_mul_f32_e64 v25, v31, v37
	s_nop 0
	v_mul_f32_e64 v24, v24, v40
	v_mul_f32_e64 v25, v25, v41
	s_nop 0
	v_cvt_pk_fp8_f32 v35, v24, v25 op_sel:[0,0,1]
	global_store_dwordx2 v[22:23], v[34:35], off
	v_mul_f32_e32 v22, 0x3c800000, v33
	v_fma_f32 v24, v86, v22, v10
	v_fma_f32 v25, v87, v22, v11
	v_fma_f32 v26, v84, v22, v8
	v_fma_f32 v27, v85, v22, v9
	v_min_f32_e32 v24, 0x40e00000, v24
	v_min_f32_e32 v25, 0x40e00000, v25
	v_mul_f32_e32 v33, 0xc01d265f, v24
	v_exp_f32_e32 v36, v33
	v_mul_f32_e32 v33, 0xc01d265f, v25
	v_exp_f32_e32 v37, v33
	v_fma_f32 v28, v98, v22, v14
	v_fma_f32 v29, v99, v22, v15
	v_fma_f32 v30, v96, v22, v12
	v_fma_f32 v31, v97, v22, v13
	v_min_f32_e32 v26, 0x40e00000, v26
	v_add_f32_e64 v36, v36, 1.0
	v_add_f32_e64 v37, v37, 1.0
	v_med3_f32 v30, v30, s85, v247
	v_min_f32_e32 v27, 0x40e00000, v27
	v_med3_f32 v31, v31, s85, v247
	v_mul_f32_e32 v23, 0xc01d265f, v26
	v_med3_f32 v28, v28, s85, v247
	v_med3_f32 v29, v29, s85, v247
	v_rcp_f32_e32 v36, v36
	v_rcp_f32_e32 v37, v37
	v_exp_f32_e32 v34, v23
	v_mul_f32_e32 v23, 0xc01d265f, v27
	v_add_f32_e64 v28, v28, 1.0
	v_add_f32_e64 v29, v29, 1.0
	v_add_f32_e64 v30, v30, 1.0
	v_add_f32_e64 v31, v31, 1.0
	v_exp_f32_e32 v35, v23
	v_mul_f32_e64 v26, v26, v30
	v_mul_f32_e64 v27, v27, v31
	v_mul_f32_e64 v24, v24, v28
	v_mul_f32_e64 v25, v25, v29
	v_fma_f32 v28, v78, v22, v2
	v_fma_f32 v29, v79, v22, v3
	v_fma_f32 v30, v76, v22, v0
	v_fma_f32 v31, v77, v22, v1
;     __device__ __forceinline__ void operator()(const f32x4 (&acc)[2][2][4][2], const Unit& u, int wr, int wc, int fr, int fq, const Pre&) const {
;     ...
;         for (int ai = 0; ai < 2; ++ai)
; #pragma unroll
;             for (int m = 0; m < 4; ++m) {
;                 const int row = u.pm * 256 + ai * 128 + wr * 64 + m * 16 + fr; const float rs = rsv[ai * 4 + m] * (1.0f / W8_SCALE);
;                 f32x4 o[2];
; #pragma unroll
;                 for (int n = 0; n < 2; ++n) {
;                     f32x4 g = acc[ai][0][m][n] * rs + (n ? bg1 : bg0), up = acc[ai][1][m][n] * rs + (n ? bu1 : bu0);
; #pragma unroll
;                     for (int j = 0; j < 4; ++j) { g[j] = fminf(g[j], 7.0f); up[j] = __builtin_amdgcn_fmed3f(up[j], -7.0f, 7.0f); }
;                     f32x4 z = g * (-1.702f * 1.4426950408889634f), e;
; #pragma unroll
;                     for (int j = 0; j < 4; ++j) e[j] = __builtin_amdgcn_exp2f(z[j]);
;                     e = e + 1.0f;
; #pragma unroll
;                     for (int j = 0; j < 4; ++j) e[j] = __builtin_amdgcn_rcpf(e[j]);
;                     o[n] = (up + 1.0f) * g * e;
;                 }
;                 *(u32x2*)(hdn + (size_t)row * DFF + cw) = pack_fp8x8(o[0][0], o[0][1], o[0][2], o[0][3], o[1][0], o[1][1], o[1][2], o[1][3]);
;             }
	v_min_f32_e32 v28, 0x40e00000, v28
	v_min_f32_e32 v30, 0x40e00000, v30
	v_mul_f32_e64 v24, v24, v36
	v_mul_f32_e64 v25, v25, v37
	v_min_f32_e32 v31, 0x40e00000, v31
	v_min_f32_e32 v29, 0x40e00000, v29
	v_mul_f32_e32 v33, 0xc01d265f, v30
	v_mul_f32_e32 v37, 0xc01d265f, v28
	v_exp_f32_e32 v36, v33
	v_mul_f32_e32 v33, 0xc01d265f, v31
	v_exp_f32_e32 v38, v37
	v_mul_f32_e32 v37, 0xc01d265f, v29
	v_add_f32_e64 v34, v34, 1.0
	v_add_f32_e64 v35, v35, 1.0
	v_exp_f32_e32 v39, v37
	v_exp_f32_e32 v37, v33
	v_rcp_f32_e32 v34, v34
	v_rcp_f32_e32 v35, v35
	v_add_f32_e64 v38, v38, 1.0
	v_add_f32_e64 v39, v39, 1.0
	v_add_f32_e64 v36, v36, 1.0
	v_add_f32_e64 v37, v37, 1.0
	v_rcp_f32_e32 v38, v38
	v_mul_f32_e64 v26, v26, v34
	v_mul_f32_e64 v27, v27, v35
	v_fma_f32 v34, v90, v22, v6
	v_fma_f32 v35, v91, v22, v7
	v_fma_f32 v23, v89, v22, v5
	v_fma_f32 v22, v88, v22, v4
	v_rcp_f32_e32 v36, v36
	v_rcp_f32_e32 v37, v37
	v_med3_f32 v22, v22, s85, v247
	v_med3_f32 v23, v23, s85, v247
	v_add_f32_e64 v22, v22, 1.0
	v_add_f32_e64 v23, v23, 1.0
	v_rcp_f32_e32 v39, v39
	v_mul_f32_e64 v22, v30, v22
	v_mul_f32_e64 v23, v31, v23
	v_mov_b32_e32 v30, v201
	v_mul_f32_e64 v22, v22, v36
	v_mul_f32_e64 v23, v23, v37
	v_mov_b32_e32 v31, v201
	v_med3_f32 v34, v34, s85, v247
	v_med3_f32 v35, v35, s85, v247
	v_cvt_pk_fp8_f32 v30, v26, v27
	v_cvt_pk_fp8_f32 v31, v22, v23
	v_add_f32_e64 v34, v34, 1.0
	v_add_f32_e64 v35, v35, 1.0
	v_cvt_pk_fp8_f32 v30, v24, v25 op_sel:[0,0,1]
	v_mul_f32_e64 v22, v28, v34
	v_mul_f32_e64 v23, v29, v35
	s_nop 0
	v_mul_f32_e64 v22, v22, v38
	v_mul_f32_e64 v23, v23, v39
	s_nop 0
	v_cvt_pk_fp8_f32 v31, v22, v23 op_sel:[0,0,1]
	global_store_dwordx2 v[20:21], v[30:31], off
	v_mul_f32_e32 v20, 0x3c800000, v32
	v_fma_f32 v8, v68, v20, v8
	v_fma_f32 v9, v69, v20, v9
	v_fma_f32 v10, v70, v20, v10
	v_fma_f32 v11, v71, v20, v11
	v_min_f32_e32 v8, 0x40e00000, v8
	v_fma_f32 v14, v82, v20, v14
	v_fma_f32 v15, v83, v20, v15
	v_fma_f32 v12, v80, v20, v12
	v_fma_f32 v13, v81, v20, v13
	v_min_f32_e32 v9, 0x40e00000, v9
	v_mul_f32_e32 v21, 0xc01d265f, v8
	v_exp_f32_e32 v22, v21
	v_mul_f32_e32 v21, 0xc01d265f, v9
	v_med3_f32 v12, v12, s85, v247
	v_med3_f32 v13, v13, s85, v247
	v_min_f32_e32 v10, 0x40e00000, v10
	v_fma_f32 v0, v64, v20, v0
	v_fma_f32 v1, v65, v20, v1
	v_min_f32_e32 v11, 0x40e00000, v11
	v_mul_f32_e32 v23, 0xc01d265f, v10
	v_add_f32_e64 v12, v12, 1.0
	v_add_f32_e64 v13, v13, 1.0
	v_min_f32_e32 v0, 0x40e00000, v0
	v_min_f32_e32 v1, 0x40e00000, v1
	v_exp_f32_e32 v24, v23
	v_mul_f32_e32 v23, 0xc01d265f, v11
	v_mul_f32_e64 v8, v8, v12
	v_mul_f32_e64 v9, v9, v13
	v_mul_f32_e32 v12, 0xc01d265f, v0
	v_mul_f32_e32 v13, 0xc01d265f, v1
	v_exp_f32_e32 v25, v23
	v_exp_f32_e32 v23, v21
	v_exp_f32_e32 v12, v12
	v_exp_f32_e32 v13, v13
	v_med3_f32 v14, v14, s85, v247
	v_med3_f32 v15, v15, s85, v247
	v_fma_f32 v2, v66, v20, v2
	v_fma_f32 v3, v67, v20, v3
	v_add_f32_e64 v14, v14, 1.0
	v_add_f32_e64 v15, v15, 1.0
	v_min_f32_e32 v2, 0x40e00000, v2
	v_min_f32_e32 v3, 0x40e00000, v3
	v_mul_f32_e64 v10, v10, v14
	v_mul_f32_e64 v11, v11, v15
	v_mul_f32_e32 v14, 0xc01d265f, v2
	v_mul_f32_e32 v15, 0xc01d265f, v3
	v_add_f32_e64 v22, v22, 1.0
	v_add_f32_e64 v23, v23, 1.0
	v_exp_f32_e32 v14, v14
	v_exp_f32_e32 v15, v15
	v_add_f32_e64 v12, v12, 1.0
	v_add_f32_e64 v13, v13, 1.0
	v_rcp_f32_e32 v22, v22
	v_rcp_f32_e32 v23, v23
	v_fma_f32 v4, v72, v20, v4
	v_fma_f32 v5, v73, v20, v5
	v_rcp_f32_e32 v12, v12
	v_rcp_f32_e32 v13, v13
	v_med3_f32 v4, v4, s85, v247
	v_med3_f32 v5, v5, s85, v247
	v_add_f32_e64 v4, v4, 1.0
	v_add_f32_e64 v5, v5, 1.0
	v_add_f32_e64 v24, v24, 1.0
	v_add_f32_e64 v25, v25, 1.0
	v_add_f32_e64 v14, v14, 1.0
	v_add_f32_e64 v15, v15, 1.0
	v_mul_f32_e64 v0, v0, v4
	v_mul_f32_e64 v1, v1, v5
	v_rcp_f32_e32 v24, v24
	v_rcp_f32_e32 v25, v25
	v_mul_f32_e64 v8, v8, v22
	v_mul_f32_e64 v9, v9, v23
	v_fma_f32 v6, v74, v20, v6
	v_fma_f32 v7, v75, v20, v7
	v_rcp_f32_e32 v14, v14
	v_rcp_f32_e32 v15, v15
	v_mul_f32_e64 v0, v0, v12
	v_mul_f32_e64 v1, v1, v13
	v_mov_b32_e32 v4, v201
	v_mov_b32_e32 v5, v201
	v_med3_f32 v6, v6, s85, v247
	v_med3_f32 v7, v7, s85, v247
	v_cvt_pk_fp8_f32 v4, v8, v9
	v_cvt_pk_fp8_f32 v5, v0, v1
	v_add_f32_e64 v6, v6, 1.0
	v_add_f32_e64 v7, v7, 1.0
	v_mul_f32_e64 v10, v10, v24
	v_mul_f32_e64 v11, v11, v25
	v_mul_f32_e64 v0, v2, v6
	v_mul_f32_e64 v1, v3, v7
	v_cvt_pk_fp8_f32 v4, v10, v11 op_sel:[0,0,1]
	v_mul_f32_e64 v0, v0, v14
	v_mul_f32_e64 v1, v1, v15
	s_nop 0
	v_cvt_pk_fp8_f32 v5, v0, v1 op_sel:[0,0,1]
	v_lshlrev_b64 v[0:1], 11, v[18:19]
	v_lshl_add_u64 v[0:1], s[12:13], 0, v[0:1]
	v_lshl_add_u64 v[0:1], v[0:1], 0, v[16:17]
	global_store_dwordx2 v[0:1], v[4:5], off
	s_cbranch_vccnz .LBB0_2719
	s_mov_b32 s50, s38
	s_mov_b32 s48, s40
	v_mov_b32_e32 v228, v224
	v_mov_b64_e32 v[0:1], v[226:227]
	s_mov_b64 s[0:1], s[44:45]
	s_branch .LBB0_2701

.LBB0_2796:
	ds_read_b128 v[0:3], v175
	ds_read_b128 v[4:7], v175 offset:1024
	ds_read_b128 v[8:11], v175 offset:2048
	ds_read_b128 v[12:15], v175 offset:3072
	s_add_u32 s34, s30, 0xfffc0080
	s_addc_u32 s35, s31, -1
	s_cmp_eq_u32 s57, 12
	s_cselect_b32 s37, s15, s35
	s_cselect_b32 s36, s14, s34
	s_cselect_b32 s35, s17, s55
	s_cselect_b32 s34, s16, s13
	v_lshl_add_u64 v[16:17], s[30:31], 0, v[160:161]
	s_add_i32 m0, s29, 0xc000
	ds_read_b128 v[188:191], v176
	ds_read_b128 v[192:195], v176 offset:1024
	ds_read_b128 v[196:199], v176 offset:2048
	ds_read_b128 v[200:203], v176 offset:3072
	ds_read_b128 v[204:207], v176 offset:4096
	ds_read_b128 v[208:211], v176 offset:5120
	ds_read_b128 v[212:215], v176 offset:6144
	ds_read_b128 v[216:219], v176 offset:7168
	global_load_lds_dwordx4 v[16:17], off
	v_lshl_add_u64 v[16:17], s[30:31], 0, v[162:163]
	s_add_i32 m0, s29, 0xe000
	s_nop 0
	global_load_lds_dwordx4 v[16:17], off
	s_waitcnt lgkmcnt(8)
	s_barrier
	s_waitcnt lgkmcnt(0)
	s_setprio 1
	s_waitcnt lgkmcnt(0)
	v_mfma_f32_16x16x128_f8f6f4 v[148:151], v[0:7], v[188:195], v[148:151]
	v_mfma_f32_16x16x128_f8f6f4 v[144:147], v[8:15], v[188:195], v[144:147]
	v_mfma_f32_16x16x128_f8f6f4 v[140:143], v[0:7], v[196:203], v[140:143]
	v_mfma_f32_16x16x128_f8f6f4 v[136:139], v[8:15], v[196:203], v[136:139]
	v_mfma_f32_16x16x128_f8f6f4 v[132:135], v[0:7], v[204:211], v[132:135]
	v_mfma_f32_16x16x128_f8f6f4 v[120:123], v[8:15], v[204:211], v[120:123]
	v_mfma_f32_16x16x128_f8f6f4 v[100:103], v[0:7], v[212:219], v[100:103]
	v_mfma_f32_16x16x128_f8f6f4 v[96:99], v[8:15], v[212:219], v[96:99]
	s_setprio 0
	s_barrier
	s_add_i32 s58, s53, s43
	v_lshl_add_u64 v[166:167], s[34:35], 0, v[156:157]
	s_mov_b32 m0, s58
	ds_read_b128 v[16:19], v178
	ds_read_b128 v[20:23], v178 offset:1024
	ds_read_b128 v[220:223], v178 offset:2048
	ds_read_b128 v[224:227], v178 offset:3072
	global_load_lds_dwordx4 v[166:167], off
	v_lshl_add_u64 v[168:169], s[34:35], 0, v[152:153]
	s_add_i32 m0, s58, 0x2000
	s_nop 0
	global_load_lds_dwordx4 v[168:169], off
	s_barrier
	s_waitcnt lgkmcnt(0)
	s_setprio 1
	s_waitcnt lgkmcnt(0)
	v_mfma_f32_16x16x128_f8f6f4 v[128:131], v[16:23], v[188:195], v[128:131]
	v_mfma_f32_16x16x128_f8f6f4 v[124:127], v[220:227], v[188:195], v[124:127]
	v_mfma_f32_16x16x128_f8f6f4 v[116:119], v[16:23], v[196:203], v[116:119]
	v_mfma_f32_16x16x128_f8f6f4 v[112:115], v[220:227], v[196:203], v[112:115]
	v_mfma_f32_16x16x128_f8f6f4 v[108:111], v[16:23], v[204:211], v[108:111]
	v_mfma_f32_16x16x128_f8f6f4 v[104:107], v[220:227], v[204:211], v[104:107]
	v_mfma_f32_16x16x128_f8f6f4 v[92:95], v[16:23], v[212:219], v[92:95]
	v_mfma_f32_16x16x128_f8f6f4 v[88:91], v[220:227], v[212:219], v[88:91]
	s_setprio 0
	s_mov_b32 m0, s29
	v_lshl_add_u64 v[170:171], s[36:37], 0, v[158:159]
	s_barrier
	ds_read_b128 v[188:191], v176 offset:16384
	ds_read_b128 v[192:195], v176 offset:17408
	ds_read_b128 v[196:199], v176 offset:18432
	ds_read_b128 v[200:203], v176 offset:19456
	ds_read_b128 v[204:207], v176 offset:20480
	ds_read_b128 v[208:211], v176 offset:21504
	ds_read_b128 v[212:215], v176 offset:22528
	ds_read_b128 v[216:219], v176 offset:23552
	global_load_lds_dwordx4 v[170:171], off
	v_lshl_add_u64 v[172:173], s[36:37], 0, v[154:155]
	s_mov_b32 m0, s45
	s_nop 0
	global_load_lds_dwordx4 v[172:173], off
	s_barrier
	s_waitcnt lgkmcnt(0)
	s_setprio 1
	s_waitcnt lgkmcnt(0)
	v_mfma_f32_16x16x128_f8f6f4 v[84:87], v[0:7], v[188:195], v[84:87]
	v_mfma_f32_16x16x128_f8f6f4 v[80:83], v[8:15], v[188:195], v[80:83]
	v_mfma_f32_16x16x128_f8f6f4 v[68:71], v[0:7], v[196:203], v[68:71]
	v_mfma_f32_16x16x128_f8f6f4 v[64:67], v[8:15], v[196:203], v[64:67]
	v_mfma_f32_16x16x128_f8f6f4 v[52:55], v[0:7], v[204:211], v[52:55]
	v_mfma_f32_16x16x128_f8f6f4 v[48:51], v[8:15], v[204:211], v[48:51]
	v_mfma_f32_16x16x128_f8f6f4 v[36:39], v[0:7], v[212:219], v[36:39]
	v_mfma_f32_16x16x128_f8f6f4 v[32:35], v[8:15], v[212:219], v[32:35]
	s_setprio 0
	s_barrier
	s_add_u32 s58, s34, 0x40000
	s_addc_u32 s59, s35, 0
	s_add_i32 s60, s54, s43
	v_lshl_add_u64 v[0:1], s[58:59], 0, v[156:157]
	s_mov_b32 m0, s60
	s_nop 0
	global_load_lds_dwordx4 v[0:1], off
	v_lshl_add_u64 v[0:1], s[58:59], 0, v[152:153]
	s_add_i32 m0, s60, 0x2000
	s_nop 0
	global_load_lds_dwordx4 v[0:1], off
	s_waitcnt vmcnt(6)
	s_barrier
	s_setprio 1
	v_mfma_f32_16x16x128_f8f6f4 v[76:79], v[16:23], v[188:195], v[76:79]
	v_mfma_f32_16x16x128_f8f6f4 v[72:75], v[220:227], v[188:195], v[72:75]
	v_mfma_f32_16x16x128_f8f6f4 v[60:63], v[16:23], v[196:203], v[60:63]
	v_mfma_f32_16x16x128_f8f6f4 v[56:59], v[220:227], v[196:203], v[56:59]
	v_mfma_f32_16x16x128_f8f6f4 v[44:47], v[16:23], v[204:211], v[44:47]
	v_mfma_f32_16x16x128_f8f6f4 v[40:43], v[220:227], v[204:211], v[40:43]
	v_mfma_f32_16x16x128_f8f6f4 v[28:31], v[16:23], v[212:219], v[28:31]
	v_mfma_f32_16x16x128_f8f6f4 v[24:27], v[220:227], v[212:219], v[24:27]
	s_setprio 0
	s_add_i32 s58, 0, 0x18000
	v_add_u32_e32 v12, s58, v174
	s_barrier
	ds_read_b128 v[0:3], v12
	ds_read_b128 v[4:7], v12 offset:1024
	ds_read_b128 v[8:11], v12 offset:2048
	ds_read_b128 v[12:15], v12 offset:3072
	s_add_u32 s36, s36, 0x40000
	s_addc_u32 s37, s37, 0
	s_mov_b32 m0, s46
	v_lshl_add_u64 v[212:213], s[36:37], 0, v[158:159]
	ds_read_b128 v[16:19], v176 offset:32768
	ds_read_b128 v[20:23], v176 offset:33792
	ds_read_b128 v[188:191], v176 offset:34816
	ds_read_b128 v[192:195], v176 offset:35840
	ds_read_b128 v[196:199], v176 offset:36864
	ds_read_b128 v[200:203], v176 offset:37888
	ds_read_b128 v[204:207], v176 offset:38912
	ds_read_b128 v[208:211], v176 offset:39936
	global_load_lds_dwordx4 v[212:213], off
	v_lshl_add_u64 v[212:213], s[36:37], 0, v[154:155]
	s_mov_b32 m0, s47
	s_nop 0
	global_load_lds_dwordx4 v[212:213], off
	s_waitcnt lgkmcnt(8)
	s_barrier
;     __device__ __forceinline__ void operator()(const f32x4 (&acc)[2][2][4][2], const Unit& u, int wr, int wc, int fr, int fq, const Pre& pr) const {
;         const int c0 = 256 * u.pn + 32 * wc + 8 * fq; const float* bp = bdn + (size_t)u.aux * DM + c0;
;         const f32x4 b00 = *(const f32x4*)bp, b01 = *(const f32x4*)(bp + 4), b10 = *(const f32x4*)(bp + 128), b11 = *(const f32x4*)(bp + 132); const float (&gwv)[8] = pr.gwv;
	s_waitcnt lgkmcnt(0)
	s_setprio 1
	s_waitcnt lgkmcnt(0)
	v_mfma_f32_16x16x128_f8f6f4 v[148:151], v[0:7], v[16:23], v[148:151]
	v_mfma_f32_16x16x128_f8f6f4 v[144:147], v[8:15], v[16:23], v[144:147]
	v_mfma_f32_16x16x128_f8f6f4 v[140:143], v[0:7], v[188:195], v[140:143]
	v_mfma_f32_16x16x128_f8f6f4 v[136:139], v[8:15], v[188:195], v[136:139]
	v_mfma_f32_16x16x128_f8f6f4 v[132:135], v[0:7], v[196:203], v[132:135]
	v_mfma_f32_16x16x128_f8f6f4 v[120:123], v[8:15], v[196:203], v[120:123]
	v_mfma_f32_16x16x128_f8f6f4 v[100:103], v[0:7], v[204:211], v[100:103]
	v_mfma_f32_16x16x128_f8f6f4 v[96:99], v[8:15], v[204:211], v[96:99]
	s_setprio 0
	s_barrier
	s_add_i32 s36, 0, 0x1c000
	s_add_i32 s37, s58, s43
	v_add_u32_e32 v165, s36, v174
	v_lshl_add_u64 v[166:167], v[166:167], 0, s[4:5]
	s_mov_b32 m0, s37
	ds_read_b128 v[212:215], v165
	ds_read_b128 v[216:219], v165 offset:1024
	ds_read_b128 v[220:223], v165 offset:2048
	ds_read_b128 v[224:227], v165 offset:3072
	global_load_lds_dwordx4 v[166:167], off
	v_lshl_add_u64 v[166:167], v[168:169], 0, s[4:5]
	s_add_i32 m0, s37, 0x2000
	s_nop 0
	global_load_lds_dwordx4 v[166:167], off
	s_barrier
	s_waitcnt lgkmcnt(0)
	s_setprio 1
	s_waitcnt lgkmcnt(0)
	v_mfma_f32_16x16x128_f8f6f4 v[128:131], v[212:219], v[16:23], v[128:131]
	v_mfma_f32_16x16x128_f8f6f4 v[124:127], v[220:227], v[16:23], v[124:127]
	v_mfma_f32_16x16x128_f8f6f4 v[116:119], v[212:219], v[188:195], v[116:119]
	v_mfma_f32_16x16x128_f8f6f4 v[112:115], v[220:227], v[188:195], v[112:115]
	v_mfma_f32_16x16x128_f8f6f4 v[108:111], v[212:219], v[196:203], v[108:111]
	v_mfma_f32_16x16x128_f8f6f4 v[104:107], v[220:227], v[196:203], v[104:107]
	v_mfma_f32_16x16x128_f8f6f4 v[92:95], v[212:219], v[204:211], v[92:95]
	v_mfma_f32_16x16x128_f8f6f4 v[88:91], v[220:227], v[204:211], v[88:91]
	s_setprio 0
	s_mov_b32 m0, s50
	v_lshl_add_u64 v[166:167], v[170:171], 0, s[4:5]
	s_barrier
	ds_read_b128 v[16:19], v176 offset:49152
	ds_read_b128 v[20:23], v176 offset:50176
	ds_read_b128 v[188:191], v176 offset:51200
	ds_read_b128 v[192:195], v176 offset:52224
	ds_read_b128 v[196:199], v176 offset:53248
	ds_read_b128 v[200:203], v176 offset:54272
	ds_read_b128 v[204:207], v176 offset:55296
	ds_read_b128 v[208:211], v176 offset:56320
	global_load_lds_dwordx4 v[166:167], off
	v_lshl_add_u64 v[166:167], v[172:173], 0, s[4:5]
	s_mov_b32 m0, s51
	s_nop 0
	global_load_lds_dwordx4 v[166:167], off
	s_barrier
	s_waitcnt lgkmcnt(0)
	s_setprio 1
	s_waitcnt lgkmcnt(0)
	v_mfma_f32_16x16x128_f8f6f4 v[84:87], v[0:7], v[16:23], v[84:87]
	v_mfma_f32_16x16x128_f8f6f4 v[80:83], v[8:15], v[16:23], v[80:83]
	v_mfma_f32_16x16x128_f8f6f4 v[68:71], v[0:7], v[188:195], v[68:71]
	v_mfma_f32_16x16x128_f8f6f4 v[64:67], v[8:15], v[188:195], v[64:67]
	v_mfma_f32_16x16x128_f8f6f4 v[52:55], v[0:7], v[196:203], v[52:55]
	v_mfma_f32_16x16x128_f8f6f4 v[48:51], v[8:15], v[196:203], v[48:51]
	v_mfma_f32_16x16x128_f8f6f4 v[36:39], v[0:7], v[204:211], v[36:39]
	v_mfma_f32_16x16x128_f8f6f4 v[32:35], v[8:15], v[204:211], v[32:35]
	s_setprio 0
	s_barrier
	s_add_u32 s34, s34, 0x40080
	s_addc_u32 s35, s35, 0
	s_add_i32 s36, s36, s43
	v_lshl_add_u64 v[0:1], s[34:35], 0, v[156:157]
	s_mov_b32 m0, s36
	s_nop 0
	global_load_lds_dwordx4 v[0:1], off
	v_lshl_add_u64 v[0:1], s[34:35], 0, v[152:153]
	s_add_i32 m0, s36, 0x2000
	s_nop 0
	global_load_lds_dwordx4 v[0:1], off
	s_waitcnt vmcnt(6)
	s_barrier
	s_setprio 1
	v_mfma_f32_16x16x128_f8f6f4 v[76:79], v[212:219], v[16:23], v[76:79]
	v_mfma_f32_16x16x128_f8f6f4 v[72:75], v[220:227], v[16:23], v[72:75]
	v_mfma_f32_16x16x128_f8f6f4 v[60:63], v[212:219], v[188:195], v[60:63]
	v_mfma_f32_16x16x128_f8f6f4 v[56:59], v[220:227], v[188:195], v[56:59]
	v_mfma_f32_16x16x128_f8f6f4 v[44:47], v[212:219], v[196:203], v[44:47]
	v_mfma_f32_16x16x128_f8f6f4 v[40:43], v[220:227], v[196:203], v[40:43]
	v_mfma_f32_16x16x128_f8f6f4 v[28:31], v[212:219], v[204:211], v[28:31]
	v_mfma_f32_16x16x128_f8f6f4 v[24:27], v[220:227], v[204:211], v[24:27]
	s_setprio 0
	s_add_i32 s57, s57, 2
	s_add_u32 s30, s30, 0x100
	s_addc_u32 s31, s31, 0
	s_add_u32 s13, s13, 0x100
	s_addc_u32 s55, s55, 0
	s_cmp_gt_u32 s57, 13
	s_barrier
	s_cbranch_scc0 .LBB0_2796
	s_nop 15
 s_nop 7
	v_mbcnt_lo_u32_b32 v18, -1, 0
	v_mbcnt_hi_u32_b32 v18, -1, v18
	s_lshl_b32 s13, s28, 8
	v_ashrrev_i32_e32 v0, 1, v18
	v_and_b32_e32 v0, -8, v0
	s_or_b32 s13, s13, s49
	v_ashrrev_i32_e32 v165, 31, v164
	v_add_u32_e32 v16, s13, v0
	v_lshlrev_b64 v[0:1], 13, v[164:165]
	v_lshl_add_u64 v[0:1], s[74:75], 0, v[0:1]
	v_ashrrev_i32_e32 v17, 31, v16
	v_lshl_add_u64 v[0:1], v[16:17], 2, v[0:1]
	global_load_dwordx4 v[12:15], v[0:1], off
	global_load_dwordx4 v[8:11], v[0:1], off offset:16
	global_load_dwordx4 v[4:7], v[0:1], off offset:512
	s_nop 0
	global_load_dwordx4 v[0:3], v[0:1], off offset:528
	s_waitcnt vmcnt(0)
;     __device__ __forceinline__ void operator()(const f32x4 (&acc)[2][2][4][2], const Unit& u, int wr, int wc, int fr, int fq, const Pre& pr) const {
;     ...
; #pragma unroll
;         for (int ai = 0; ai < 2; ++ai)
; #pragma unroll
;             for (int m = 0; m < 4; ++m) {
;                 const int row = u.pm * 256 + ai * 128 + wr * 64 + m * 16 + fr; const float gw = gwv[ai * 4 + m] * YS_SCALE;
;                 constexpr float iw = 1.0f / W8_SCALE;
;                 const f32x4 o0 = (acc[ai][0][m][0] * iw + b00) * gw, o1 = (acc[ai][0][m][1] * iw + b01) * gw, o2 = (acc[ai][1][m][0] * iw + b10) * gw, o3 = (acc[ai][1][m][1] * iw + b11) * gw;
;                 *(u32x2*)(ys + (size_t)row * DM + c0) = pack_fp8x8(o0[0], o0[1], o0[2], o0[3], o1[0], o1[1], o1[2], o1[3]);
;                 *(u32x2*)(ys + (size_t)row * DM + c0 + 128) = pack_fp8x8(o2[0], o2[1], o2[2], o2[3], o3[0], o3[1], o3[2], o3[3]);
;             }
	v_mul_f32_e32 v20, 0x41800000, v187
	v_mov_b32_e32 v22, 0
	v_mov_b32_e32 v23, 0
	v_mov_b32_e32 v164, 0
	v_mov_b32_e32 v165, 0
	v_mul_f32_e32 v166, 0x41800000, v186
	v_mov_b32_e32 v168, 0
	v_mov_b32_e32 v169, 0
	v_mov_b32_e32 v170, 0
	v_mov_b32_e32 v171, 0
	v_and_or_b32 v18, v18, 15, s48
	v_add_u32_e32 v18, s11, v18
	v_ashrrev_i32_e32 v19, 31, v18
	v_add_u32_e32 v186, 16, v18
	v_lshlrev_b64 v[190:191], 11, v[18:19]
	v_ashrrev_i32_e32 v187, 31, v186
	v_lshl_add_u64 v[190:191], s[2:3], 0, v[190:191]
	v_lshlrev_b64 v[186:187], 11, v[186:187]
	v_mul_f32_e32 v172, 0x41800000, v185
	v_lshl_add_u64 v[190:191], v[190:191], 0, v[16:17]
	v_lshl_add_u64 v[186:187], s[2:3], 0, v[186:187]
	v_lshl_add_u64 v[186:187], v[186:187], 0, v[16:17]
	v_add_u32_e32 v188, 32, v18
	v_ashrrev_i32_e32 v189, 31, v188
	s_and_b64 vcc, exec, s[8:9]
	s_mov_b32 s34, s12
	s_mov_b32 s28, s10
	s_mov_b64 s[36:37], s[16:17]
	s_mov_b64 s[30:31], s[14:15]
	v_fma_f32 v148, v148, s6, v12
	v_fma_f32 v149, v149, s6, v13
	v_fma_f32 v144, v144, s6, v8
	v_fma_f32 v145, v145, s6, v9
	v_fma_f32 v150, v150, s6, v14
	v_fma_f32 v151, v151, s6, v15
	v_fma_f32 v146, v146, s6, v10
	v_fma_f32 v147, v147, s6, v11
	v_fma_f32 v130, v130, s6, v6
	v_fma_f32 v131, v131, s6, v7
	v_fma_f32 v128, v128, s6, v4
	v_fma_f32 v129, v129, s6, v5
	v_fma_f32 v126, v126, s6, v2
	v_fma_f32 v127, v127, s6, v3
	v_fma_f32 v124, v124, s6, v0
	v_fma_f32 v125, v125, s6, v1
	v_mul_f32_e64 v148, v20, v148
	v_mul_f32_e64 v149, v20, v149
	v_mul_f32_e64 v144, v20, v144
	v_mul_f32_e64 v145, v20, v145
	v_fma_f32 v140, v140, s6, v12
	v_fma_f32 v141, v141, s6, v13
	v_fma_f32 v136, v136, s6, v8
	v_fma_f32 v137, v137, s6, v9
	v_mul_f32_e64 v150, v20, v150
	v_mul_f32_e64 v151, v20, v151
	v_mul_f32_e64 v146, v20, v146
	v_mul_f32_e64 v147, v20, v147
	v_mul_f32_e64 v130, v20, v130
	v_mul_f32_e64 v131, v20, v131
	v_mul_f32_e64 v128, v20, v128
	v_mul_f32_e64 v129, v20, v129
	v_mul_f32_e64 v126, v20, v126
	v_mul_f32_e64 v127, v20, v127
	v_mul_f32_e64 v21, v20, v125
	v_mul_f32_e64 v20, v20, v124
	v_cvt_pk_fp8_f32 v22, v148, v149
	v_cvt_pk_fp8_f32 v23, v144, v145
	v_fma_f32 v116, v116, s6, v4
	v_fma_f32 v117, v117, s6, v5
	v_fma_f32 v112, v112, s6, v0
	v_fma_f32 v113, v113, s6, v1
	v_mul_f32_e64 v140, v166, v140
	v_mul_f32_e64 v141, v166, v141
	v_mul_f32_e64 v136, v166, v136
	v_mul_f32_e64 v137, v166, v137
	v_cvt_pk_fp8_f32 v164, v128, v129
	v_cvt_pk_fp8_f32 v165, v20, v21
	v_mul_f32_e64 v116, v166, v116
	v_mul_f32_e64 v117, v166, v117
	v_mul_f32_e64 v112, v166, v112
	v_mul_f32_e64 v113, v166, v113
	v_cvt_pk_fp8_f32 v168, v140, v141
	v_cvt_pk_fp8_f32 v169, v136, v137
	v_cvt_pk_fp8_f32 v170, v116, v117
	v_cvt_pk_fp8_f32 v171, v112, v113
	v_fma_f32 v142, v142, s6, v14
	v_fma_f32 v143, v143, s6, v15
	v_fma_f32 v138, v138, s6, v10
	v_fma_f32 v139, v139, s6, v11
	v_cvt_pk_fp8_f32 v22, v150, v151 op_sel:[0,0,1]
	v_cvt_pk_fp8_f32 v23, v146, v147 op_sel:[0,0,1]
	v_fma_f32 v118, v118, s6, v6
	v_fma_f32 v119, v119, s6, v7
	v_fma_f32 v114, v114, s6, v2
	v_fma_f32 v115, v115, s6, v3
	v_mul_f32_e64 v124, v166, v142
	v_mul_f32_e64 v125, v166, v143
	v_mul_f32_e64 v138, v166, v138
	v_mul_f32_e64 v139, v166, v139
	v_cvt_pk_fp8_f32 v164, v130, v131 op_sel:[0,0,1]
	v_cvt_pk_fp8_f32 v165, v126, v127 op_sel:[0,0,1]
	v_mul_f32_e64 v118, v166, v118
	v_mul_f32_e64 v119, v166, v119
	v_mul_f32_e64 v114, v166, v114
	v_mul_f32_e64 v115, v166, v115
	v_cvt_pk_fp8_f32 v168, v124, v125 op_sel:[0,0,1]
	v_cvt_pk_fp8_f32 v169, v138, v139 op_sel:[0,0,1]
	v_fma_f32 v120, v120, s6, v8
	v_fma_f32 v121, v121, s6, v9
	v_cvt_pk_fp8_f32 v170, v118, v119 op_sel:[0,0,1]
	v_cvt_pk_fp8_f32 v171, v114, v115 op_sel:[0,0,1]
	global_store_dwordx2 v[190:191], v[22:23], off
	global_store_dwordx2 v[190:191], v[164:165], off offset:128
	global_store_dwordx2 v[186:187], v[168:169], off
	global_store_dwordx2 v[186:187], v[170:171], off offset:128
	v_mul_f32_e64 v22, v172, v120
	v_mul_f32_e64 v23, v172, v121
	v_mov_b32_e32 v113, 0
	v_cvt_pk_fp8_f32 v113, v22, v23
	v_fma_f32 v132, v132, s6, v12
	v_fma_f32 v133, v133, s6, v13
	v_fma_f32 v122, v122, s6, v10
	v_fma_f32 v123, v123, s6, v11
	v_mul_f32_e64 v132, v172, v132
	v_mul_f32_e64 v133, v172, v133
	v_mul_f32_e64 v20, v172, v122
	v_mul_f32_e64 v21, v172, v123
	v_fma_f32 v108, v108, s6, v4
	v_fma_f32 v109, v109, s6, v5
	v_fma_f32 v104, v104, s6, v0
	v_fma_f32 v105, v105, s6, v1
	v_mov_b32_e32 v112, 0
	v_mul_f32_e64 v108, v172, v108
	v_mul_f32_e64 v109, v172, v109
	v_cvt_pk_fp8_f32 v112, v132, v133
	v_mul_f32_e64 v104, v172, v104
	v_mul_f32_e64 v105, v172, v105
	v_cvt_pk_fp8_f32 v113, v20, v21 op_sel:[0,0,1]
	v_mov_b32_e32 v20, 0
	v_mov_b32_e32 v21, 0
	v_cvt_pk_fp8_f32 v20, v108, v109
	v_cvt_pk_fp8_f32 v21, v104, v105
	v_fma_f32 v134, v134, s6, v14
	v_fma_f32 v135, v135, s6, v15
	v_fma_f32 v110, v110, s6, v6
	v_fma_f32 v111, v111, s6, v7
	v_mul_f32_e64 v134, v172, v134
	v_mul_f32_e64 v135, v172, v135
	v_fma_f32 v106, v106, s6, v2
	v_fma_f32 v107, v107, s6, v3
	v_mul_f32_e64 v110, v172, v110
	v_mul_f32_e64 v111, v172, v111
	v_mul_f32_e64 v22, v172, v106
	v_mul_f32_e64 v23, v172, v107
	v_cvt_pk_fp8_f32 v112, v134, v135 op_sel:[0,0,1]
	v_lshlrev_b64 v[104:105], 11, v[188:189]
	v_cvt_pk_fp8_f32 v20, v110, v111 op_sel:[0,0,1]
	v_cvt_pk_fp8_f32 v21, v22, v23 op_sel:[0,0,1]
	v_lshl_add_u64 v[22:23], s[2:3], 0, v[104:105]
	v_lshl_add_u64 v[22:23], v[22:23], 0, v[16:17]
	global_store_dwordx2 v[22:23], v[112:113], off
	global_store_dwordx2 v[22:23], v[20:21], off offset:128
	v_mul_f32_e32 v22, 0x41800000, v184
	v_fma_f32 v100, v100, s6, v12
	v_fma_f32 v101, v101, s6, v13
	v_fma_f32 v96, v96, s6, v8
	v_fma_f32 v97, v97, s6, v9
	v_fma_f32 v102, v102, s6, v14
;     __device__ __forceinline__ void operator()(const f32x4 (&acc)[2][2][4][2], const Unit& u, int wr, int wc, int fr, int fq, const Pre& pr) const {
;         const int c0 = 256 * u.pn + 32 * wc + 8 * fq; const float* bp = bdn + (size_t)u.aux * DM + c0;
;         const f32x4 b00 = *(const f32x4*)bp, b01 = *(const f32x4*)(bp + 4), b10 = *(const f32x4*)(bp + 128), b11 = *(const f32x4*)(bp + 132); const float (&gwv)[8] = pr.gwv;
; #pragma unroll
;         for (int ai = 0; ai < 2; ++ai)
; #pragma unroll
;             for (int m = 0; m < 4; ++m) {
;                 const int row = u.pm * 256 + ai * 128 + wr * 64 + m * 16 + fr; const float gw = gwv[ai * 4 + m] * YS_SCALE;
;                 constexpr float iw = 1.0f / W8_SCALE;
;                 const f32x4 o0 = (acc[ai][0][m][0] * iw + b00) * gw, o1 = (acc[ai][0][m][1] * iw + b01) * gw, o2 = (acc[ai][1][m][0] * iw + b10) * gw, o3 = (acc[ai][1][m][1] * iw + b11) * gw;
;                 *(u32x2*)(ys + (size_t)row * DM + c0) = pack_fp8x8(o0[0], o0[1], o0[2], o0[3], o1[0], o1[1], o1[2], o1[3]);
;                 *(u32x2*)(ys + (size_t)row * DM + c0 + 128) = pack_fp8x8(o2[0], o2[1], o2[2], o2[3], o3[0], o3[1], o3[2], o3[3]);
;             }
;     }
	v_fma_f32 v103, v103, s6, v15
	v_mul_f32_e64 v100, v22, v100
	v_mul_f32_e64 v101, v22, v101
	v_fma_f32 v98, v98, s6, v10
	v_fma_f32 v99, v99, s6, v11
	v_mul_f32_e64 v96, v22, v96
	v_mul_f32_e64 v97, v22, v97
	v_fma_f32 v94, v94, s6, v6
	v_fma_f32 v95, v95, s6, v7
	v_fma_f32 v92, v92, s6, v4
	v_fma_f32 v93, v93, s6, v5
	v_fma_f32 v90, v90, s6, v2
	v_fma_f32 v91, v91, s6, v3
	v_fma_f32 v88, v88, s6, v0
	v_fma_f32 v89, v89, s6, v1
	v_mov_b32_e32 v104, 0
	v_mov_b32_e32 v105, 0
	v_mul_f32_e64 v102, v22, v102
	v_mul_f32_e64 v103, v22, v103
	v_mul_f32_e64 v98, v22, v98
	v_mul_f32_e64 v99, v22, v99
	v_mul_f32_e64 v94, v22, v94
	v_mul_f32_e64 v95, v22, v95
	v_mul_f32_e64 v92, v22, v92
	v_mul_f32_e64 v93, v22, v93
	v_cvt_pk_fp8_f32 v104, v100, v101
	v_cvt_pk_fp8_f32 v105, v96, v97
	v_mul_f32_e64 v90, v22, v90
	v_mul_f32_e64 v91, v22, v91
	v_mul_f32_e64 v23, v22, v89
	v_mul_f32_e64 v22, v22, v88
	v_mov_b32_e32 v88, 0
	v_mov_b32_e32 v89, 0
	v_cvt_pk_fp8_f32 v88, v92, v93
	v_cvt_pk_fp8_f32 v89, v22, v23
	v_add_u32_e32 v20, 48, v18
	v_cvt_pk_fp8_f32 v104, v102, v103 op_sel:[0,0,1]
	v_cvt_pk_fp8_f32 v105, v98, v99 op_sel:[0,0,1]
	v_ashrrev_i32_e32 v21, 31, v20
	v_lshlrev_b64 v[20:21], 11, v[20:21]
	v_cvt_pk_fp8_f32 v88, v94, v95 op_sel:[0,0,1]
	v_cvt_pk_fp8_f32 v89, v90, v91 op_sel:[0,0,1]
	v_lshl_add_u64 v[20:21], s[2:3], 0, v[20:21]
	v_lshl_add_u64 v[20:21], v[20:21], 0, v[16:17]
	v_mul_f32_e32 v22, 0x41800000, v183
	v_fma_f32 v84, v84, s6, v12
	v_fma_f32 v85, v85, s6, v13
	v_fma_f32 v80, v80, s6, v8
	v_fma_f32 v81, v81, s6, v9
	global_store_dwordx2 v[20:21], v[104:105], off
	global_store_dwordx2 v[20:21], v[88:89], off offset:128
	v_fma_f32 v86, v86, s6, v14
	v_fma_f32 v87, v87, s6, v15
	v_mul_f32_e64 v84, v22, v84
	v_mul_f32_e64 v85, v22, v85
	v_fma_f32 v82, v82, s6, v10
	v_fma_f32 v83, v83, s6, v11
	v_mul_f32_e64 v80, v22, v80
	v_mul_f32_e64 v81, v22, v81
	v_fma_f32 v78, v78, s6, v6
	v_fma_f32 v79, v79, s6, v7
	v_fma_f32 v76, v76, s6, v4
	v_fma_f32 v77, v77, s6, v5
	v_fma_f32 v74, v74, s6, v2
	v_fma_f32 v75, v75, s6, v3
	v_fma_f32 v72, v72, s6, v0
	v_fma_f32 v73, v73, s6, v1
	v_mov_b32_e32 v88, 0
	v_mov_b32_e32 v89, 0
	v_mul_f32_e64 v86, v22, v86
	v_mul_f32_e64 v87, v22, v87
	v_mul_f32_e64 v82, v22, v82
	v_mul_f32_e64 v83, v22, v83
	v_mul_f32_e64 v78, v22, v78
	v_mul_f32_e64 v79, v22, v79
	v_mul_f32_e64 v76, v22, v76
	v_mul_f32_e64 v77, v22, v77
	v_cvt_pk_fp8_f32 v88, v84, v85
	v_cvt_pk_fp8_f32 v89, v80, v81
	v_mul_f32_e64 v74, v22, v74
	v_mul_f32_e64 v75, v22, v75
	v_mul_f32_e64 v23, v22, v73
	v_mul_f32_e64 v22, v22, v72
	v_mov_b32_e32 v72, 0
	v_mov_b32_e32 v73, 0
	v_cvt_pk_fp8_f32 v72, v76, v77
	v_cvt_pk_fp8_f32 v73, v22, v23
	v_add_u32_e32 v20, 0x80, v18
	v_cvt_pk_fp8_f32 v88, v86, v87 op_sel:[0,0,1]
	v_cvt_pk_fp8_f32 v89, v82, v83 op_sel:[0,0,1]
	v_ashrrev_i32_e32 v21, 31, v20
	v_lshlrev_b64 v[20:21], 11, v[20:21]
	v_cvt_pk_fp8_f32 v72, v78, v79 op_sel:[0,0,1]
	v_cvt_pk_fp8_f32 v73, v74, v75 op_sel:[0,0,1]
	v_lshl_add_u64 v[20:21], s[2:3], 0, v[20:21]
	v_lshl_add_u64 v[20:21], v[20:21], 0, v[16:17]
	v_mul_f32_e32 v22, 0x41800000, v182
	v_fma_f32 v68, v68, s6, v12
	v_fma_f32 v69, v69, s6, v13
	v_fma_f32 v64, v64, s6, v8
	v_fma_f32 v65, v65, s6, v9
	global_store_dwordx2 v[20:21], v[88:89], off
	global_store_dwordx2 v[20:21], v[72:73], off offset:128
	v_fma_f32 v70, v70, s6, v14
	v_fma_f32 v71, v71, s6, v15
	v_mul_f32_e64 v68, v22, v68
	v_mul_f32_e64 v69, v22, v69
	v_fma_f32 v66, v66, s6, v10
	v_fma_f32 v67, v67, s6, v11
	v_mul_f32_e64 v64, v22, v64
	v_mul_f32_e64 v65, v22, v65
	v_fma_f32 v62, v62, s6, v6
	v_fma_f32 v63, v63, s6, v7
	v_fma_f32 v60, v60, s6, v4
	v_fma_f32 v61, v61, s6, v5
	v_fma_f32 v58, v58, s6, v2
	v_fma_f32 v59, v59, s6, v3
	v_fma_f32 v56, v56, s6, v0
	v_fma_f32 v57, v57, s6, v1
	v_mov_b32_e32 v72, 0
	v_mov_b32_e32 v73, 0
	v_mul_f32_e64 v70, v22, v70
	v_mul_f32_e64 v71, v22, v71
	v_mul_f32_e64 v66, v22, v66
	v_mul_f32_e64 v67, v22, v67
	v_mul_f32_e64 v62, v22, v62
	v_mul_f32_e64 v63, v22, v63
	v_mul_f32_e64 v60, v22, v60
	v_mul_f32_e64 v61, v22, v61
	v_cvt_pk_fp8_f32 v72, v68, v69
	v_cvt_pk_fp8_f32 v73, v64, v65
;     __device__ __forceinline__ void operator()(const f32x4 (&acc)[2][2][4][2], const Unit& u, int wr, int wc, int fr, int fq, const Pre& pr) const {
;         const int c0 = 256 * u.pn + 32 * wc + 8 * fq; const float* bp = bdn + (size_t)u.aux * DM + c0;
;         const f32x4 b00 = *(const f32x4*)bp, b01 = *(const f32x4*)(bp + 4), b10 = *(const f32x4*)(bp + 128), b11 = *(const f32x4*)(bp + 132); const float (&gwv)[8] = pr.gwv;
; #pragma unroll
;         for (int ai = 0; ai < 2; ++ai)
; #pragma unroll
;             for (int m = 0; m < 4; ++m) {
;                 const int row = u.pm * 256 + ai * 128 + wr * 64 + m * 16 + fr; const float gw = gwv[ai * 4 + m] * YS_SCALE;
;                 constexpr float iw = 1.0f / W8_SCALE;
;                 const f32x4 o0 = (acc[ai][0][m][0] * iw + b00) * gw, o1 = (acc[ai][0][m][1] * iw + b01) * gw, o2 = (acc[ai][1][m][0] * iw + b10) * gw, o3 = (acc[ai][1][m][1] * iw + b11) * gw;
;                 *(u32x2*)(ys + (size_t)row * DM + c0) = pack_fp8x8(o0[0], o0[1], o0[2], o0[3], o1[0], o1[1], o1[2], o1[3]);
;                 *(u32x2*)(ys + (size_t)row * DM + c0 + 128) = pack_fp8x8(o2[0], o2[1], o2[2], o2[3], o3[0], o3[1], o3[2], o3[3]);
;             }
;     }
	v_mul_f32_e64 v58, v22, v58
	v_mul_f32_e64 v59, v22, v59
	v_mul_f32_e64 v23, v22, v57
	v_mul_f32_e64 v22, v22, v56
	v_mov_b32_e32 v56, 0
	v_mov_b32_e32 v57, 0
	v_cvt_pk_fp8_f32 v56, v60, v61
	v_cvt_pk_fp8_f32 v57, v22, v23
	v_add_u32_e32 v20, 0x90, v18
	v_cvt_pk_fp8_f32 v72, v70, v71 op_sel:[0,0,1]
	v_cvt_pk_fp8_f32 v73, v66, v67 op_sel:[0,0,1]
	v_ashrrev_i32_e32 v21, 31, v20
	v_lshlrev_b64 v[20:21], 11, v[20:21]
	v_cvt_pk_fp8_f32 v56, v62, v63 op_sel:[0,0,1]
	v_cvt_pk_fp8_f32 v57, v58, v59 op_sel:[0,0,1]
	v_lshl_add_u64 v[20:21], s[2:3], 0, v[20:21]
	v_lshl_add_u64 v[20:21], v[20:21], 0, v[16:17]
	v_mul_f32_e32 v22, 0x41800000, v181
	v_fma_f32 v52, v52, s6, v12
	v_fma_f32 v53, v53, s6, v13
	v_fma_f32 v48, v48, s6, v8
	v_fma_f32 v49, v49, s6, v9
	global_store_dwordx2 v[20:21], v[72:73], off
	global_store_dwordx2 v[20:21], v[56:57], off offset:128
	v_fma_f32 v54, v54, s6, v14
	v_fma_f32 v55, v55, s6, v15
	v_mul_f32_e64 v52, v22, v52
	v_mul_f32_e64 v53, v22, v53
	v_fma_f32 v50, v50, s6, v10
	v_fma_f32 v51, v51, s6, v11
	v_mul_f32_e64 v48, v22, v48
	v_mul_f32_e64 v49, v22, v49
	v_fma_f32 v46, v46, s6, v6
	v_fma_f32 v47, v47, s6, v7
	v_fma_f32 v44, v44, s6, v4
	v_fma_f32 v45, v45, s6, v5
	v_fma_f32 v42, v42, s6, v2
	v_fma_f32 v43, v43, s6, v3
	v_fma_f32 v40, v40, s6, v0
	v_fma_f32 v41, v41, s6, v1
	v_mov_b32_e32 v56, 0
	v_mov_b32_e32 v57, 0
	v_mul_f32_e64 v54, v22, v54
	v_mul_f32_e64 v55, v22, v55
	v_mul_f32_e64 v50, v22, v50
	v_mul_f32_e64 v51, v22, v51
	v_mul_f32_e64 v46, v22, v46
	v_mul_f32_e64 v47, v22, v47
	v_mul_f32_e64 v44, v22, v44
	v_mul_f32_e64 v45, v22, v45
	v_cvt_pk_fp8_f32 v56, v52, v53
	v_cvt_pk_fp8_f32 v57, v48, v49
	v_mul_f32_e64 v42, v22, v42
	v_mul_f32_e64 v43, v22, v43
	v_mul_f32_e64 v23, v22, v41
	v_mul_f32_e64 v22, v22, v40
	v_mov_b32_e32 v40, 0
	v_mov_b32_e32 v41, 0
	v_cvt_pk_fp8_f32 v40, v44, v45
	v_cvt_pk_fp8_f32 v41, v22, v23
	v_add_u32_e32 v20, 0xa0, v18
	v_cvt_pk_fp8_f32 v56, v54, v55 op_sel:[0,0,1]
	v_cvt_pk_fp8_f32 v57, v50, v51 op_sel:[0,0,1]
	v_ashrrev_i32_e32 v21, 31, v20
	v_lshlrev_b64 v[20:21], 11, v[20:21]
	v_cvt_pk_fp8_f32 v40, v46, v47 op_sel:[0,0,1]
	v_cvt_pk_fp8_f32 v41, v42, v43 op_sel:[0,0,1]
	v_lshl_add_u64 v[20:21], s[2:3], 0, v[20:21]
	v_lshl_add_u64 v[20:21], v[20:21], 0, v[16:17]
	global_store_dwordx2 v[20:21], v[56:57], off
	global_store_dwordx2 v[20:21], v[40:41], off offset:128
	v_mul_f32_e32 v20, 0x41800000, v180
	v_fma_f32 v12, v36, s6, v12
	v_fma_f32 v13, v37, s6, v13
	v_fma_f32 v8, v32, s6, v8
	v_fma_f32 v9, v33, s6, v9
	v_mul_f32_e64 v12, v20, v12
	v_mul_f32_e64 v13, v20, v13
	v_mul_f32_e64 v8, v20, v8
	v_mul_f32_e64 v9, v20, v9
	v_fma_f32 v4, v28, s6, v4
	v_fma_f32 v5, v29, s6, v5
	v_fma_f32 v0, v24, s6, v0
	v_fma_f32 v1, v25, s6, v1
	v_mov_b32_e32 v22, 0
	v_mov_b32_e32 v23, 0
	v_mul_f32_e64 v4, v20, v4
	v_mul_f32_e64 v5, v20, v5
	v_cvt_pk_fp8_f32 v22, v12, v13
	v_cvt_pk_fp8_f32 v23, v8, v9
	v_mul_f32_e64 v0, v20, v0
	v_mul_f32_e64 v1, v20, v1
	v_mov_b32_e32 v8, 0
	v_mov_b32_e32 v9, 0
	v_cvt_pk_fp8_f32 v8, v4, v5
	v_cvt_pk_fp8_f32 v9, v0, v1
	v_fma_f32 v14, v38, s6, v14
	v_fma_f32 v15, v39, s6, v15
	v_fma_f32 v10, v34, s6, v10
	v_fma_f32 v11, v35, s6, v11
	v_add_u32_e32 v18, 0xb0, v18
	v_mul_f32_e64 v14, v20, v14
	v_mul_f32_e64 v15, v20, v15
	v_mul_f32_e64 v10, v20, v10
	v_mul_f32_e64 v11, v20, v11
	v_fma_f32 v6, v30, s6, v6
	v_fma_f32 v7, v31, s6, v7
	v_fma_f32 v2, v26, s6, v2
	v_fma_f32 v3, v27, s6, v3
	v_mul_f32_e64 v6, v20, v6
	v_mul_f32_e64 v7, v20, v7
	v_mul_f32_e64 v2, v20, v2
	v_mul_f32_e64 v3, v20, v3
	v_cvt_pk_fp8_f32 v22, v14, v15 op_sel:[0,0,1]
	v_cvt_pk_fp8_f32 v23, v10, v11 op_sel:[0,0,1]
	v_ashrrev_i32_e32 v19, 31, v18
	v_lshlrev_b64 v[0:1], 11, v[18:19]
	v_cvt_pk_fp8_f32 v8, v6, v7 op_sel:[0,0,1]
	v_cvt_pk_fp8_f32 v9, v2, v3 op_sel:[0,0,1]
	v_lshl_add_u64 v[0:1], s[2:3], 0, v[0:1]
	v_lshl_add_u64 v[0:1], v[0:1], 0, v[16:17]
	v_mov_b32_e32 v164, v179
	global_store_dwordx2 v[0:1], v[22:23], off
	global_store_dwordx2 v[0:1], v[8:9], off offset:128
	s_cbranch_vccz .LBB0_2793
	s_waitcnt vmcnt(0)
	s_cmpk_gt_u32 s96, 0xff
	s_cbranch_scc1 .LBB0_2800
	s_barrier

; __device__ __forceinline__ float bf_lo(unsigned w) { return __uint_as_float(w << 16); }
; __device__ __forceinline__ float bf_hi(unsigned w) { return __uint_as_float(w & 0xffff0000u); }
; #define FIN_Y(W, HI) ((__builtin_amdgcn_cvt_pk_f32_fp8((int)y0.W, HI) + __builtin_amdgcn_cvt_pk_f32_fp8((int)y1.W, HI)) + (__builtin_amdgcn_cvt_pk_f32_fp8((int)y2.W, HI) + __builtin_amdgcn_cvt_pk_f32_fp8((int)y3.W, HI)))
; __device__ __forceinline__ void p_final(const Frame& F, const bf16_t* h) {
;     ...
;     for (; r < T; r += stride) {
;         const int rn = r + stride, rnn = rn + stride;
;         u32x4 pnn = (u32x4){0u, 0u, 0u, 0u};
;         if (rn < T) FIN_LOAD(hhn, yyn, rn, pnx);
;         if (rnn < T) pnn = *(const u32x4*)(pos + rnn * 4);
;         f32x4 v[8]; float ss = 0.f;
; #pragma unroll
;         for (int i = 0; i < 4; ++i) {
;             const u32x4 hv = hh[i]; const u32x2 y0 = yy[0][i], y1 = yy[1][i], y2 = yy[2][i], y3 = yy[3][i];
;             f32x4 a, b;
;             constexpr float iy = 1.0f / YS_SCALE;
;     ...
;             { const f32x2 s0 = FIN_Y(x, false), s1 = FIN_Y(x, true), s2 = FIN_Y(y, false), s3 = FIN_Y(y, true);
;               a[0] = bf_lo(hv.x) + s0[0] * iy; a[1] = bf_hi(hv.x) + s0[1] * iy; a[2] = bf_lo(hv.y) + s1[0] * iy; a[3] = bf_hi(hv.y) + s1[1] * iy;
;               b[0] = bf_lo(hv.z) + s2[0] * iy; b[1] = bf_hi(hv.z) + s2[1] * iy; b[2] = bf_lo(hv.w) + s3[0] * iy; b[3] = bf_hi(hv.w) + s3[1] * iy; }
;     ...
;             v[2 * i] = a; v[2 * i + 1] = b;
;             ss += a[0] * a[0] + a[1] * a[1] + a[2] * a[2] + a[3] * a[3] + b[0] * b[0] + b[1] * b[1] + b[2] * b[2] + b[3] * b[3];
;         }
.LBB0_2863:
	s_waitcnt vmcnt(15)
	v_cvt_pk_f32_fp8_e32 v[154:155], v138
	s_waitcnt vmcnt(11)
	v_cvt_pk_f32_fp8_e32 v[156:157], v140
	s_waitcnt vmcnt(7)
	v_cvt_pk_f32_fp8_e32 v[158:159], v142
	s_waitcnt vmcnt(3)
	v_cvt_pk_f32_fp8_e32 v[160:161], v144
	v_cvt_pk_f32_fp8_sdwa v[162:163], v144 src0_sel:WORD_1
	v_add_f32_e64 v154, v154, v156
	v_add_f32_e64 v155, v155, v157
	v_cvt_pk_f32_fp8_e32 v[164:165], v139
	v_add_f32_e64 v156, v158, v160
	v_add_f32_e64 v157, v159, v161
	v_cvt_pk_f32_fp8_sdwa v[158:159], v140 src0_sel:WORD_1
	v_add_f32_e64 v154, v154, v156
	v_add_f32_e64 v155, v155, v157
	v_cvt_pk_f32_fp8_sdwa v[156:157], v138 src0_sel:WORD_1
	v_cvt_pk_f32_fp8_sdwa v[160:161], v142 src0_sel:WORD_1
	v_cvt_pk_f32_fp8_e32 v[166:167], v141
	v_cvt_pk_f32_fp8_sdwa v[138:139], v139 src0_sel:WORD_1
	v_add_f32_e64 v156, v156, v158
	v_add_f32_e64 v157, v157, v159
	v_add_f32_e64 v158, v160, v162
	v_add_f32_e64 v159, v161, v163
	v_cvt_pk_f32_fp8_e32 v[160:161], v143
	v_cvt_pk_f32_fp8_e32 v[162:163], v145
	v_cvt_pk_f32_fp8_sdwa v[140:141], v141 src0_sel:WORD_1
	v_cvt_pk_f32_fp8_sdwa v[142:143], v143 src0_sel:WORD_1
	v_cvt_pk_f32_fp8_sdwa v[144:145], v145 src0_sel:WORD_1
	v_add_f32_e64 v156, v156, v158
	v_add_f32_e64 v157, v157, v159
	v_add_f32_e64 v138, v138, v140
	v_add_f32_e64 v139, v139, v141
	v_add_f32_e64 v158, v164, v166
	v_add_f32_e64 v159, v165, v167
	v_add_f32_e64 v140, v142, v144
	v_add_f32_e64 v141, v143, v145
	v_add_f32_e64 v160, v160, v162
	v_add_f32_e64 v161, v161, v163
	v_add_f32_e64 v142, v138, v140
	v_add_f32_e64 v143, v139, v141
	v_lshlrev_b32_e32 v138, 16, v64
	v_and_b32_e32 v139, 0xffff0000, v64
	v_lshlrev_b32_e32 v64, 16, v65
	v_and_b32_e32 v65, 0xffff0000, v65
	v_add_f32_e64 v158, v158, v160
	v_add_f32_e64 v159, v159, v161
	v_fma_f32 v140, v156, s10, v64
	v_fma_f32 v141, v157, s10, v65
	v_lshlrev_b32_e32 v64, 16, v66
	v_and_b32_e32 v65, 0xffff0000, v66
	v_fma_f32 v138, v154, s10, v138
	v_fma_f32 v139, v155, s10, v139
	v_fma_f32 v64, v158, s10, v64
	v_fma_f32 v65, v159, s10, v65
	v_cvt_pk_f32_fp8_e32 v[154:155], v130
	v_cvt_pk_f32_fp8_e32 v[156:157], v132
	v_cvt_pk_f32_fp8_e32 v[158:159], v134
	s_waitcnt vmcnt(2)
	v_cvt_pk_f32_fp8_e32 v[160:161], v136
	v_cvt_pk_f32_fp8_sdwa v[166:167], v136 src0_sel:WORD_1
	v_add_f32_e64 v154, v154, v156
	v_add_f32_e64 v155, v155, v157
	v_cvt_pk_f32_fp8_e32 v[168:169], v131
	v_add_f32_e64 v156, v158, v160
	v_add_f32_e64 v157, v159, v161
	v_cvt_pk_f32_fp8_sdwa v[158:159], v132 src0_sel:WORD_1
	v_add_f32_e64 v154, v154, v156
	v_add_f32_e64 v155, v155, v157
	v_cvt_pk_f32_fp8_sdwa v[156:157], v130 src0_sel:WORD_1
	v_cvt_pk_f32_fp8_sdwa v[160:161], v134 src0_sel:WORD_1
	v_cvt_pk_f32_fp8_e32 v[170:171], v133
	v_cvt_pk_f32_fp8_sdwa v[130:131], v131 src0_sel:WORD_1
	v_add_f32_e64 v156, v156, v158
	v_add_f32_e64 v157, v157, v159
	v_add_f32_e64 v158, v160, v166
	v_add_f32_e64 v159, v161, v167
	v_cvt_pk_f32_fp8_e32 v[160:161], v135
	v_cvt_pk_f32_fp8_e32 v[166:167], v137
	v_cvt_pk_f32_fp8_sdwa v[132:133], v133 src0_sel:WORD_1
	v_cvt_pk_f32_fp8_sdwa v[134:135], v135 src0_sel:WORD_1
	v_cvt_pk_f32_fp8_sdwa v[136:137], v137 src0_sel:WORD_1
	v_add_f32_e64 v156, v156, v158
	v_add_f32_e64 v157, v157, v159
	v_add_f32_e64 v158, v168, v170
	v_add_f32_e64 v159, v169, v171
	v_add_f32_e64 v160, v160, v166
	v_add_f32_e64 v161, v161, v167
	v_add_f32_e64 v130, v130, v132
	v_add_f32_e64 v131, v131, v133
	v_add_f32_e64 v132, v134, v136
	v_add_f32_e64 v133, v135, v137
	v_add_f32_e64 v158, v158, v160
	v_add_f32_e64 v159, v159, v161
	v_add_f32_e64 v130, v130, v132
	v_add_f32_e64 v131, v131, v133
	v_lshlrev_b32_e32 v132, 16, v60
	v_and_b32_e32 v133, 0xffff0000, v60
	v_lshlrev_b32_e32 v60, 16, v61
	v_and_b32_e32 v61, 0xffff0000, v61
	v_lshlrev_b32_e32 v134, 16, v62
	v_and_b32_e32 v135, 0xffff0000, v62
	v_fma_f32 v132, v154, s10, v132
	v_fma_f32 v133, v155, s10, v133
	v_fma_f32 v60, v156, s10, v60
	v_fma_f32 v61, v157, s10, v61
	v_fma_f32 v134, v158, s10, v134
	v_fma_f32 v135, v159, s10, v135
	v_cvt_pk_f32_fp8_e32 v[154:155], v122
	v_cvt_pk_f32_fp8_e32 v[156:157], v124
	v_cvt_pk_f32_fp8_e32 v[158:159], v126
	s_waitcnt vmcnt(1)
	v_cvt_pk_f32_fp8_e32 v[160:161], v128
	v_cvt_pk_f32_fp8_sdwa v[170:171], v128 src0_sel:WORD_1
	v_add_f32_e64 v154, v154, v156
	v_add_f32_e64 v155, v155, v157
	v_cvt_pk_f32_fp8_e32 v[172:173], v123
	v_add_f32_e64 v156, v158, v160
	v_add_f32_e64 v157, v159, v161
	v_cvt_pk_f32_fp8_sdwa v[158:159], v124 src0_sel:WORD_1
	v_add_f32_e64 v154, v154, v156
	v_add_f32_e64 v155, v155, v157
	v_cvt_pk_f32_fp8_sdwa v[156:157], v122 src0_sel:WORD_1
	v_cvt_pk_f32_fp8_sdwa v[160:161], v126 src0_sel:WORD_1
	v_cvt_pk_f32_fp8_e32 v[174:175], v125
	v_cvt_pk_f32_fp8_sdwa v[122:123], v123 src0_sel:WORD_1
	v_add_f32_e64 v156, v156, v158
	v_add_f32_e64 v157, v157, v159
	v_add_f32_e64 v158, v160, v170
	v_add_f32_e64 v159, v161, v171
	v_cvt_pk_f32_fp8_e32 v[160:161], v127
	v_cvt_pk_f32_fp8_e32 v[170:171], v129
	v_cvt_pk_f32_fp8_sdwa v[124:125], v125 src0_sel:WORD_1
	v_cvt_pk_f32_fp8_sdwa v[126:127], v127 src0_sel:WORD_1
	v_cvt_pk_f32_fp8_sdwa v[128:129], v129 src0_sel:WORD_1
	v_add_f32_e64 v156, v156, v158
	v_add_f32_e64 v157, v157, v159
	v_add_f32_e64 v158, v172, v174
	v_add_f32_e64 v159, v173, v175
	v_add_f32_e64 v160, v160, v170
	v_add_f32_e64 v161, v161, v171
	v_add_f32_e64 v122, v122, v124
	v_add_f32_e64 v123, v123, v125
	v_add_f32_e64 v124, v126, v128
	v_add_f32_e64 v125, v127, v129
	v_add_f32_e64 v158, v158, v160
	v_add_f32_e64 v159, v159, v161
	v_add_f32_e64 v122, v122, v124
	v_add_f32_e64 v123, v123, v125
	v_lshlrev_b32_e32 v124, 16, v56
	v_and_b32_e32 v125, 0xffff0000, v56
	v_lshlrev_b32_e32 v56, 16, v57
	v_and_b32_e32 v57, 0xffff0000, v57
	v_lshlrev_b32_e32 v126, 16, v58
	v_and_b32_e32 v127, 0xffff0000, v58
	v_fma_f32 v124, v154, s10, v124
	v_fma_f32 v125, v155, s10, v125
	v_fma_f32 v56, v156, s10, v56
	v_fma_f32 v57, v157, s10, v57
	v_fma_f32 v126, v158, s10, v126
	v_fma_f32 v127, v159, s10, v127
	v_cvt_pk_f32_fp8_e32 v[128:129], v114
	v_cvt_pk_f32_fp8_e32 v[154:155], v116
	v_cvt_pk_f32_fp8_e32 v[156:157], v118
	s_waitcnt vmcnt(0)
; __device__ __forceinline__ float bf_lo(unsigned w) { return __uint_as_float(w << 16); }
; __device__ __forceinline__ float bf_hi(unsigned w) { return __uint_as_float(w & 0xffff0000u); }
; #define FIN_Y(W, HI) ((__builtin_amdgcn_cvt_pk_f32_fp8((int)y0.W, HI) + __builtin_amdgcn_cvt_pk_f32_fp8((int)y1.W, HI)) + (__builtin_amdgcn_cvt_pk_f32_fp8((int)y2.W, HI) + __builtin_amdgcn_cvt_pk_f32_fp8((int)y3.W, HI)))
; __device__ __forceinline__ void p_final(const Frame& F, const bf16_t* h) {
;     ...
;         f32x4 v[8]; float ss = 0.f;
; #pragma unroll
;         for (int i = 0; i < 4; ++i) {
;             const u32x4 hv = hh[i]; const u32x2 y0 = yy[0][i], y1 = yy[1][i], y2 = yy[2][i], y3 = yy[3][i];
;             f32x4 a, b;
;             constexpr float iy = 1.0f / YS_SCALE;
;     ...
;             { const f32x2 s0 = FIN_Y(x, false), s1 = FIN_Y(x, true), s2 = FIN_Y(y, false), s3 = FIN_Y(y, true);
;               a[0] = bf_lo(hv.x) + s0[0] * iy; a[1] = bf_hi(hv.x) + s0[1] * iy; a[2] = bf_lo(hv.y) + s1[0] * iy; a[3] = bf_hi(hv.y) + s1[1] * iy;
;               b[0] = bf_lo(hv.z) + s2[0] * iy; b[1] = bf_hi(hv.z) + s2[1] * iy; b[2] = bf_lo(hv.w) + s3[0] * iy; b[3] = bf_hi(hv.w) + s3[1] * iy; }
;     ...
;             v[2 * i] = a; v[2 * i + 1] = b;
;             ss += a[0] * a[0] + a[1] * a[1] + a[2] * a[2] + a[3] * a[3] + b[0] * b[0] + b[1] * b[1] + b[2] * b[2] + b[3] * b[3];
;         }
;         ss = wave_sum(ss);
	v_cvt_pk_f32_fp8_e32 v[158:159], v120
	v_lshlrev_b32_e32 v58, 16, v59
	v_and_b32_e32 v59, 0xffff0000, v59
	v_fma_f32 v58, v122, s10, v58
	v_fma_f32 v59, v123, s10, v59
	v_add_f32_e64 v122, v128, v154
	v_add_f32_e64 v123, v129, v155
	v_add_f32_e64 v128, v156, v158
	v_add_f32_e64 v129, v157, v159
	v_cvt_pk_f32_fp8_sdwa v[154:155], v116 src0_sel:WORD_1
	v_add_f32_e64 v122, v122, v128
	v_add_f32_e64 v123, v123, v129
	v_cvt_pk_f32_fp8_sdwa v[128:129], v114 src0_sel:WORD_1
	v_cvt_pk_f32_fp8_sdwa v[156:157], v118 src0_sel:WORD_1
	v_cvt_pk_f32_fp8_sdwa v[158:159], v120 src0_sel:WORD_1
	v_cvt_pk_f32_fp8_e32 v[160:161], v115
	v_cvt_pk_f32_fp8_e32 v[170:171], v117
	v_add_f32_e64 v128, v128, v154
	v_add_f32_e64 v129, v129, v155
	v_add_f32_e64 v154, v156, v158
	v_add_f32_e64 v155, v157, v159
	v_cvt_pk_f32_fp8_e32 v[156:157], v119
	v_cvt_pk_f32_fp8_e32 v[158:159], v121
	v_cvt_pk_f32_fp8_sdwa v[114:115], v115 src0_sel:WORD_1
	v_cvt_pk_f32_fp8_sdwa v[116:117], v117 src0_sel:WORD_1
	v_cvt_pk_f32_fp8_sdwa v[118:119], v119 src0_sel:WORD_1
	v_cvt_pk_f32_fp8_sdwa v[120:121], v121 src0_sel:WORD_1
	v_add_f32_e64 v128, v128, v154
	v_add_f32_e64 v129, v129, v155
	v_add_f32_e64 v114, v114, v116
	v_add_f32_e64 v115, v115, v117
	v_add_f32_e64 v154, v160, v170
	v_add_f32_e64 v155, v161, v171
	v_add_f32_e64 v116, v118, v120
	v_add_f32_e64 v117, v119, v121
	v_add_f32_e64 v156, v156, v158
	v_add_f32_e64 v157, v157, v159
	v_add_f32_e64 v114, v114, v116
	v_add_f32_e64 v115, v115, v117
	v_lshlrev_b32_e32 v116, 16, v36
	v_and_b32_e32 v117, 0xffff0000, v36
	v_lshlrev_b32_e32 v36, 16, v37
	v_and_b32_e32 v37, 0xffff0000, v37
	v_lshlrev_b32_e32 v66, 16, v67
	v_and_b32_e32 v67, 0xffff0000, v67
	v_lshlrev_b32_e32 v62, 16, v63
	v_and_b32_e32 v63, 0xffff0000, v63
	v_add_f32_e64 v154, v154, v156
	v_add_f32_e64 v155, v155, v157
	v_fma_f32 v116, v122, s10, v116
	v_fma_f32 v117, v123, s10, v117
	v_fma_f32 v118, v128, s10, v36
	v_fma_f32 v119, v129, s10, v37
	v_lshlrev_b32_e32 v36, 16, v38
	v_and_b32_e32 v37, 0xffff0000, v38
	v_fma_f32 v66, v142, s10, v66
	v_fma_f32 v67, v143, s10, v67
	v_mul_f32_e64 v142, v138, v138
	v_mul_f32_e64 v143, v139, v139
	v_fma_f32 v62, v130, s10, v62
	v_fma_f32 v63, v131, s10, v63
	v_mul_f32_e64 v130, v132, v132
	v_mul_f32_e64 v131, v133, v133
	v_fma_f32 v120, v154, s10, v36
	v_fma_f32 v121, v155, s10, v37
	v_lshlrev_b32_e32 v36, 16, v39
	v_and_b32_e32 v37, 0xffff0000, v39
	v_mov_b32_e32 v38, v125
	v_mov_b32_e32 v39, v117
	v_mul_f32_e64 v144, v140, v140
	v_mul_f32_e64 v145, v141, v141
	v_mul_f32_e64 v136, v60, v60
	v_mul_f32_e64 v137, v61, v61
	v_fma_f32 v114, v114, s10, v36
	v_fma_f32 v115, v115, s10, v37
	v_mov_b32_e32 v36, v124
	v_mov_b32_e32 v37, v116
	v_mul_f32_e64 v38, v38, v38
	v_mul_f32_e64 v39, v39, v39
	v_add_f32_e32 v33, v130, v131
	v_add_f32_e32 v35, v142, v143
	v_fma_f32 v36, v36, v36, v38
	v_fma_f32 v37, v37, v37, v39
	v_mov_b32_e32 v38, v56
	v_mov_b32_e32 v39, v118
	v_add_f32_e32 v33, v33, v136
	v_add_f32_e32 v35, v35, v144
	v_mul_f32_e64 v162, v64, v64
	v_mul_f32_e64 v163, v65, v65
	v_mul_f32_e64 v166, v134, v134
	v_mul_f32_e64 v167, v135, v135
	v_fma_f32 v36, v38, v38, v36
	v_fma_f32 v37, v39, v39, v37
	v_mov_b32_e32 v38, v57
	v_mov_b32_e32 v39, v119
	v_add_f32_e32 v33, v137, v33
	v_add_f32_e32 v35, v145, v35
	v_fma_f32 v36, v38, v38, v36
	v_fma_f32 v37, v39, v39, v37
	v_mov_b32_e32 v38, v126
	v_mov_b32_e32 v39, v120
	v_add_f32_e32 v33, v33, v166
	v_add_f32_e32 v35, v35, v162
	v_mul_f32_e64 v164, v66, v66
	v_mul_f32_e64 v165, v67, v67
	v_mul_f32_e64 v168, v62, v62
	v_mul_f32_e64 v169, v63, v63
	v_fma_f32 v36, v38, v38, v36
	v_fma_f32 v37, v39, v39, v37
	v_mov_b32_e32 v38, v127
	v_mov_b32_e32 v39, v121
	v_add_f32_e32 v33, v167, v33
	v_add_f32_e32 v35, v163, v35
	v_fma_f32 v36, v38, v38, v36
	v_fma_f32 v37, v39, v39, v37
	v_mov_b32_e32 v38, v58
	v_mov_b32_e32 v39, v114
	v_add_f32_e32 v33, v33, v168
	v_add_f32_e32 v35, v35, v164
	v_fma_f32 v36, v38, v38, v36
	v_fma_f32 v37, v39, v39, v37
	v_mov_b32_e32 v38, v59
	v_mov_b32_e32 v39, v115
	v_add_f32_e32 v33, v169, v33
	v_add_f32_e32 v35, v165, v35
	v_fma_f32 v36, v38, v38, v36
	v_fma_f32 v37, v39, v39, v37
	v_add_f32_e32 v33, v35, v33
	v_add_f32_e32 v33, v33, v36
	v_add_f32_e32 v33, v33, v37
	ds_bpermute_b32 v35, v146, v33
	v_lshl_add_u64 v[128:129], s[2:3], 0, v[74:75]
	v_lshl_add_u64 v[78:79], v[78:79], 0, s[8:9]
	s_mov_b32 s12, s1
	v_mov_b32_e32 v130, v110
	s_waitcnt lgkmcnt(0)
;     template <class Tp> __device__ __forceinline__ Tp* W(size_t off) const { return (Tp*)(ws + off); }
; __device__ __forceinline__ void p_final(const Frame& F, const bf16_t* h) {
;     ...
;         ss = wave_sum(ss);
;         float rs = __builtin_amdgcn_rsqf(ss * (1.0f / DM) + NORM_EPS);
;     ...
;         if (F.W<unsigned>(WS_CTL + CTL_CNT + 1024)[0] != 0u) rs = __builtin_nanf("");
;     ...
; #pragma unroll
;         for (int i = 0; i < 4; ++i) {
;             const int c = (i * 64 + ln) * 8;
;             *(f32x4*)(F.a->out + (size_t)r * DM + c) = v[2 * i] * rs * gg[2 * i]; *(f32x4*)(F.a->out + (size_t)r * DM + c + 4) = v[2 * i + 1] * rs * gg[2 * i + 1];
;         }
; #pragma unroll
;         for (int i = 0; i < 4; ++i) { hh[i] = hhn[i]; yy[0][i] = yyn[0][i]; yy[1][i] = yyn[1][i]; yy[2][i] = yyn[2][i]; yy[3][i] = yyn[3][i]; }
;         pnx = pnn;
	v_add_f32_e32 v33, v33, v35
	ds_bpermute_b32 v35, v147, v33
	v_mov_b32_e32 v131, v111
	v_mov_b32_e32 v142, v96
	v_mov_b32_e32 v143, v97
	v_mov_b32_e32 v144, v88
	s_waitcnt lgkmcnt(0)
	v_add_f32_e32 v33, v33, v35
	ds_bpermute_b32 v35, v148, v33
	v_mov_b32_e32 v145, v89
	v_mov_b32_e32 v136, v86
	v_mov_b32_e32 v137, v87
	s_waitcnt lgkmcnt(0)
	v_add_f32_e32 v33, v33, v35
	ds_bpermute_b32 v35, v149, v33
	s_waitcnt lgkmcnt(0)
	v_add_f32_e32 v33, v33, v35
	ds_bpermute_b32 v35, v150, v33
	s_waitcnt lgkmcnt(0)
	v_add_f32_e32 v33, v33, v35
	ds_bpermute_b32 v35, v151, v33
	s_waitcnt lgkmcnt(0)
	v_add_f32_e32 v33, v33, v35
	v_fmamk_f32 v33, v33, 0x3a000000, v152
	v_rsq_f32_e32 v122, v33
	s_nop 0
	v_mul_f32_e64 v36, v138, v122
	v_mul_f32_e64 v37, v139, v122
	v_mul_f32_e64 v38, v140, v122
	v_mul_f32_e64 v39, v141, v122
	v_mul_f32_e64 v36, v4, v36
	v_mul_f32_e64 v37, v5, v37
	v_mul_f32_e64 v38, v6, v38
	v_mul_f32_e64 v39, v7, v39
	global_store_dwordx4 v[128:129], v[36:39], off
	v_mov_b32_e32 v138, v112
	v_mov_b32_e32 v139, v113
	v_mul_f32_e64 v36, v64, v122
	v_mul_f32_e64 v37, v65, v122
	v_mul_f32_e64 v38, v66, v122
	v_mul_f32_e64 v39, v67, v122
	v_mul_f32_e64 v36, v0, v36
	v_mul_f32_e64 v37, v1, v37
	v_mul_f32_e64 v38, v2, v38
	v_mul_f32_e64 v39, v3, v39
	global_store_dwordx4 v[128:129], v[36:39], off offset:16
	v_mov_b64_e32 v[66:67], v[42:43]
	v_mov_b64_e32 v[64:65], v[40:41]
	v_mul_f32_e64 v36, v132, v122
	v_mul_f32_e64 v37, v133, v122
	v_mul_f32_e64 v38, v60, v122
	v_mul_f32_e64 v39, v61, v122
	v_mul_f32_e64 v36, v12, v36
	v_mul_f32_e64 v37, v13, v37
	v_mul_f32_e64 v38, v14, v38
	v_mul_f32_e64 v39, v15, v39
	global_store_dwordx4 v[128:129], v[36:39], off offset:2048
	v_mov_b32_e32 v140, v104
	v_mov_b32_e32 v141, v105
	v_mul_f32_e64 v36, v134, v122
	v_mul_f32_e64 v37, v135, v122
	v_mul_f32_e64 v38, v62, v122
	v_mul_f32_e64 v39, v63, v122
	v_mul_f32_e64 v36, v8, v36
	v_mul_f32_e64 v37, v9, v37
	v_mul_f32_e64 v38, v10, v38
	v_mul_f32_e64 v39, v11, v39
	global_store_dwordx4 v[128:129], v[36:39], off offset:2064
	v_mov_b64_e32 v[62:63], v[46:47]
	v_mov_b64_e32 v[60:61], v[44:45]
	v_mul_f32_e64 v36, v124, v122
	v_mul_f32_e64 v37, v125, v122
	v_mul_f32_e64 v38, v56, v122
	v_mul_f32_e64 v39, v57, v122
	v_mul_f32_e64 v36, v20, v36
	v_mul_f32_e64 v37, v21, v37
	v_mul_f32_e64 v38, v22, v38
	v_mul_f32_e64 v39, v23, v39
	v_lshl_add_u64 v[56:57], s[2:3], 0, v[76:77]
	global_store_dwordx4 v[56:57], v[36:39], off offset:-16
	v_mov_b32_e32 v132, v102
	v_mov_b32_e32 v133, v103
	v_mul_f32_e64 v36, v126, v122
	v_mul_f32_e64 v37, v127, v122
	v_mul_f32_e64 v38, v58, v122
	v_mul_f32_e64 v39, v59, v122
	v_mul_f32_e64 v36, v16, v36
	v_mul_f32_e64 v37, v17, v37
	v_mul_f32_e64 v38, v18, v38
	v_mul_f32_e64 v39, v19, v39
	global_store_dwordx4 v[56:57], v[36:39], off
	v_lshl_add_u64 v[56:57], s[2:3], 0, v[80:81]
	s_add_u32 s2, s2, s4
	v_mul_f32_e64 v36, v116, v122
	v_mul_f32_e64 v37, v117, v122
	v_mul_f32_e64 v38, v118, v122
	v_mul_f32_e64 v39, v119, v122
	v_mul_f32_e64 v36, v28, v36
	v_mul_f32_e64 v37, v29, v37
	v_mul_f32_e64 v38, v30, v38
	v_mul_f32_e64 v39, v31, v39
	global_store_dwordx4 v[56:57], v[36:39], off offset:-16
	s_addc_u32 s3, s3, s5
	s_add_i32 s6, s6, s13
	v_mul_f32_e64 v36, v120, v122
	v_mul_f32_e64 v37, v121, v122
	v_mul_f32_e64 v38, v114, v122
	v_mul_f32_e64 v39, v115, v122
	v_mul_f32_e64 v36, v24, v36
	v_mul_f32_e64 v37, v25, v37
	v_mul_f32_e64 v38, v26, v38
	v_mul_f32_e64 v39, v27, v39
	global_store_dwordx4 v[56:57], v[36:39], off
	v_mov_b64_e32 v[58:59], v[50:51]
	s_andn2_b64 vcc, exec, s[14:15]
	v_mov_b64_e32 v[36:37], v[52:53]
	v_mov_b64_e32 v[56:57], v[48:49]
	v_mov_b64_e32 v[38:39], v[54:55]
	v_mov_b32_e32 v122, v108
	v_mov_b32_e32 v123, v109
	v_mov_b32_e32 v114, v106
	v_mov_b32_e32 v115, v107
	v_mov_b32_e32 v124, v100
	v_mov_b32_e32 v125, v101
	v_mov_b32_e32 v116, v98
	v_mov_b32_e32 v117, v99
	v_mov_b32_e32 v134, v94
	v_mov_b32_e32 v135, v95
	v_mov_b32_e32 v126, v92
	v_mov_b32_e32 v127, v93
	v_mov_b32_e32 v118, v90
	v_mov_b32_e32 v119, v91
	v_mov_b32_e32 v128, v84
	v_mov_b32_e32 v129, v85
	v_mov_b32_e32 v120, v82
	v_mov_b32_e32 v121, v83
	s_cbranch_vccz .LBB0_2868
